# cache-policy lever: nt hint also on the once-read Q-row loads of the attention unit prologues (K/V tiles, rope and gain tables keep the default policy)
# speedup vs baseline: 1.0009x; 1.0009x over previous
; template <int DQK, int DV, bool LEAD> ...
;     ...
;     const int krow_l = wid * 8 + (lane >> 3);
;     const int kc_l = (lane & 7) ^ (((krow_l >> 1) & 1) | (((krow_l >> 3) & 1) << 1) | (((krow_l >> 4) & 1) << 2));
;     const int vc_l = (lane & 7) ^ ((krow_l >> 1) & 7);
;     const bf16_t* ksrc = K + (size_t)(krow0 + krow_l) * kpitch + kc_l * 8;
;     const int rrow_l = (wid & 3) * 16 + (lane >> 2), rc_l = (lane & 3) ^ (((rrow_l >> 4) & 1) << 1);
;     const bf16_t* krsrc = (DQK == 96) ? KR + (size_t)(krow0 + rrow_l) * 32 + rc_l * 8 : nullptr;
;     const bf16_t* vsrc = Vt + (size_t)krow_l * NR + krow0 + vc_l * 8;
;     const unsigned kdst = lds0 + KOFF + wid * 1024, krdst = lds0 + KOFF + 8192 + (wid & 3) * 1024, vdst = lds0 + VOFF + wid * 1024;
;     ...
;     ATT_DMA_K(0, 0); ATT_DMA_V(0, 0); ATT_DMA_K(1, 1); ATT_DMA_K(2, 2);
;     bf16x8 qf[NQB * NDS];
;     {
;       const float c2 = (DQK == 64) ? C2_EVEN : C2_ODD; const bool lat = tq0 >= 0;
; #pragma unroll
;       for (int qb = 0; qb < NQB; ++qb) {
;           const bf16_t* qp = Q + (size_t)(qrow0 + qoff + qb * 16 + q16) * qpitch + g4 * 8;
;           bf16x8 raw[NDS];
; #pragma unroll
;           for (int ds = 0; ds < NDS; ++ds) raw[ds] = *(const bf16x8*)(qp + ds * 32);
;           float x[NDS][8];
; #pragma unroll
;           for (int ds = 0; ds < NDS; ++ds)
; #pragma unroll
;               for (int j = 0; j < 8; ++j) x[ds][j] = __uint_as_float(((unsigned)(unsigned short)raw[ds][j]) << 16);
;           const int tq = tq0 + qoff + qb * 16 + q16, prow = (tq >> 6) & 127, pcol = tq & 63;
;           float sn = 0.f;
; #pragma unroll
;           for (int ds = 0; ds < 2; ++ds)
; #pragma unroll
;               for (int j = 0; j < 8; ++j) sn += x[ds][j] * x[ds][j];
;           sn = lanes4_sum(sn);
;           const float rn = rsqrtf(sn * (1.f / 64.f) + EPS);
; #pragma unroll
;           for (int ds = 0; ds < 2; ++ds)
; #pragma unroll
;               for (int j = 0; j < 8; ++j) x[ds][j] *= rn * qgain[32 * ds + 8 * g4 + j];
;           if constexpr (DQK == 64) {
; #pragma unroll
;               for (int ds = 0; ds < 2; ++ds)
; #pragma unroll
;                   for (int j = 0; j < 8; ++j) {
;                       auto rr = __builtin_amdgcn_permlane32_swap(__float_as_uint(x[ds][j]), __float_as_uint(x[ds][j]), false, false);
;                       const float other = hi ? __uint_as_float(rr[0]) : __uint_as_float(rr[1]);
.LBB0_641:
	s_bfe_u32 s24, s4, 0x40005
	s_ashr_i32 s5, s4, 9
	s_mul_i32 s6, s24, 0xc0
	s_add_u32 s46, s8, s6
	s_addc_u32 s47, s9, 0
	s_lshl_b32 s6, s24, 7
	s_add_u32 s50, s10, s6
	s_addc_u32 s51, s11, 0
	s_mul_i32 s6, s24, 0x840000
	s_add_u32 s52, s22, s6
	s_mov_b64 s[6:7], s[0:1]
	s_load_dwordx2 s[6:7], s[6:7], 0x98
	s_addc_u32 s53, s23, 0
	s_lshl_b32 s4, s4, 8
	s_mul_i32 s40, s5, 0x2100
	s_and_b32 s31, s4, 0x1f00
	s_add_i32 s25, s40, s31
	s_lshl_b64 s[4:5], s[20:21], 2
	s_waitcnt lgkmcnt(0)
	s_add_u32 s44, s6, s4
	s_addc_u32 s45, s7, s5
	v_readfirstlane_b32 s4, v0
	s_cmpk_gt_u32 s4, 0xff
	s_mov_b64 s[4:5], -1
	s_cbranch_scc0 .LBB0_648
	v_mov_b32_e32 v236, v0
	v_mov_b64_e32 v[6:7], s[52:53]
	v_readfirstlane_b32 s38, v236
	s_ashr_i32 s4, s38, 6
	v_bfe_u32 v2, v236, 3, 3
	v_lshl_or_b32 v8, s4, 3, v2
	v_ashrrev_i32_e32 v3, 1, v8
	v_and_b32_e32 v4, 1, v3
	s_lshl_b32 s5, s4, 1
	s_lshr_b32 s7, s38, 5
	v_and_b32_e32 v2, 7, v236
	s_and_b32 s6, s5, 2
	v_and_or_b32 v4, s7, 4, v4
	s_and_b32 s30, s4, 3
	v_bitop3_b32 v9, v4, v2, s6 bitop3:0x36
	v_bfe_u32 v4, v236, 2, 4
	v_add_u32_e32 v2, s40, v8
	v_lshl_or_b32 v4, s30, 4, v4
	v_xor_b32_e32 v10, v3, v236
	v_ashrrev_i32_e32 v3, 31, v2
	v_or_b32_e32 v4, s40, v4
	v_lshlrev_b64 v[2:3], 11, v[2:3]
	v_and_b32_e32 v12, 3, v236
	v_ashrrev_i32_e32 v5, 31, v4
	v_bitop3_b32 v11, s5, v12, 2 bitop3:0x6c
	v_lshlrev_b64 v[4:5], 6, v[4:5]
	s_lshl_b32 s42, s4, 10
	s_lshl_b32 s6, s30, 10
	v_lshl_add_u64 v[2:3], s[50:51], 0, v[2:3]
	v_lshlrev_b32_e32 v194, 4, v9
	s_ashr_i32 s41, s40, 31
	s_add_i32 s42, s42, 0
	v_lshl_add_u64 v[4:5], s[28:29], 0, v[4:5]
	v_mad_i64_i32 v[6:7], s[4:5], v8, s91, v[6:7]
	v_lshl_add_u64 v[192:193], v[2:3], 0, v[194:195]
	v_lshlrev_b32_e32 v194, 4, v11
	v_lshlrev_b32_e32 v2, 4, v10
	s_add_i32 s43, s6, 0
	s_mov_b32 s4, m0
	s_mov_b32 m0, s42
	s_nop 0
	global_load_lds_dwordx4 v[192:193], off
	s_mov_b32 m0, s4
	v_lshl_add_u64 v[6:7], s[40:41], 1, v[6:7]
	v_lshl_add_u64 v[204:205], v[4:5], 0, v[194:195]
	v_and_b32_e32 v194, 0x70, v2
	s_addk_i32 s43, 0x2000
	s_mov_b32 s4, m0
	s_mov_b32 m0, s43
	s_nop 0
	global_load_lds_dwordx4 v[204:205], off
	s_mov_b32 m0, s4
	s_add_i32 s41, s42, 0x9000
	v_lshl_add_u64 v[206:207], v[6:7], 0, v[194:195]
	s_mov_b32 s4, m0
	s_mov_b32 m0, s41
	s_nop 0
	global_load_lds_dwordx4 v[206:207], off
	s_mov_b32 m0, s4
	s_mov_b64 s[4:5], 0x20000
	v_lshl_add_u64 v[2:3], v[192:193], 0, s[4:5]
	s_add_i32 s4, s42, 0x3000
	s_mov_b32 s5, m0
	s_mov_b32 m0, s4
	s_nop 0
	global_load_lds_dwordx4 v[2:3], off
	s_mov_b32 m0, s5
	v_lshl_add_u64 v[2:3], v[204:205], 0, s[60:61]
	s_add_i32 s4, s43, 0x3000
	s_mov_b32 s5, m0
	s_mov_b32 m0, s4
	s_nop 0
	global_load_lds_dwordx4 v[2:3], off
	s_mov_b32 m0, s5
	s_mov_b64 s[4:5], 0x40000
	v_lshl_add_u64 v[2:3], v[192:193], 0, s[4:5]
	s_add_i32 s4, s42, 0x6000
	s_mov_b32 s5, m0
	s_mov_b32 m0, s4
	s_nop 0
	global_load_lds_dwordx4 v[2:3], off
	s_mov_b32 m0, s5
	s_mov_b64 s[4:5], 0x2000
	v_and_b32_e32 v237, 15, v236
	v_lshl_add_u64 v[2:3], v[204:205], 0, s[4:5]
	s_add_i32 s4, s43, 0x6000
	s_mov_b32 s5, m0
	s_mov_b32 m0, s4
	s_nop 0
	global_load_lds_dwordx4 v[2:3], off
	s_mov_b32 m0, s5
	v_lshl_or_b32 v2, s30, 6, v237
	v_and_b32_e32 v8, 48, v236
	v_or_b32_e32 v6, s25, v2
	v_mov_b32_e32 v9, v195
	v_lshl_add_u64 v[2:3], s[46:47], 0, v[8:9]
	v_or_b32_e32 v7, 16, v6
	v_mad_i64_i32 v[4:5], s[4:5], v6, s90, v[2:3]
	v_mad_i64_i32 v[10:11], s[4:5], v7, s90, v[2:3]
	v_or_b32_e32 v7, 32, v6
	v_or_b32_e32 v6, 48, v6
	v_mad_i64_i32 v[14:15], s[4:5], v7, s90, v[2:3]
	v_mad_i64_i32 v[16:17], s[4:5], v6, s90, v[2:3]
	global_load_dwordx4 v[54:57], v[4:5], off offset:64 nt
	global_load_dwordx4 v[62:65], v[10:11], off offset:64 nt
	global_load_dwordx4 v[84:87], v[14:15], off offset:64 nt
	global_load_dwordx4 v[122:125], v[16:17], off offset:64 nt
	global_load_dwordx4 v[138:141], v[4:5], off nt
	global_load_dwordx4 v[144:147], v[10:11], off nt
	global_load_dwordx4 v[80:83], v[14:15], off nt
	global_load_dwordx4 v[6:9], v[16:17], off nt
	s_lshr_b32 s4, s31, 6
	v_and_b32_e32 v194, 63, v236
	v_lshlrev_b32_e32 v2, 1, v236
	s_or_b32 s4, s4, s30
	v_and_or_b32 v239, v2, 24, v12
	v_bfe_u32 v241, v236, 3, 1
	v_mov_b32_e32 v18, s4
	v_cmp_gt_u32_e32 vcc, 32, v194
	v_or_b32_e32 v19, 16, v237
	v_bfe_u32 v238, v236, 4, 2
	s_ashr_i32 s16, s38, 8
	v_bfe_u32 v242, v236, 1, 2
	v_lshlrev_b32_e32 v243, 2, v241
	v_lshl_add_u32 v240, v239, 7, 0
	v_cndmask_b32_e32 v12, v237, v18, vcc
	v_cndmask_b32_e32 v19, v19, v18, vcc
	v_lshl_add_u32 v244, s16, 12, v240
	v_bitop3_b32 v2, v243, v238, v242 bitop3:0x36
	v_lshlrev_b32_e32 v12, 6, v12
	v_lshlrev_b32_e32 v19, 6, v19
	v_lshl_add_u32 v203, v2, 4, v244
	global_load_dwordx4 v[2:5], v[4:5], off offset:128 nt
	s_nop 0
	global_load_dwordx4 v[112:115], v12, s[36:37] offset:48
	global_load_dwordx4 v[108:111], v12, s[36:37] offset:32
	global_load_dwordx4 v[104:107], v12, s[36:37] offset:16
	global_load_dwordx4 v[100:103], v12, s[36:37]
	s_nop 0
	global_load_dwordx4 v[10:13], v[10:11], off offset:128 nt
	s_nop 0
	global_load_dwordx4 v[96:99], v19, s[36:37] offset:48
	global_load_dwordx4 v[92:95], v19, s[36:37] offset:32
	global_load_dwordx4 v[88:91], v19, s[36:37] offset:16
	global_load_dwordx4 v[58:61], v19, s[36:37]
	global_load_dwordx4 v[34:37], v[14:15], off offset:128 nt
	v_or_b32_e32 v14, 32, v237
	v_cndmask_b32_e32 v14, v14, v18, vcc
	v_lshlrev_b32_e32 v14, 6, v14
	global_load_dwordx4 v[76:79], v14, s[36:37] offset:48
	global_load_dwordx4 v[70:73], v14, s[36:37] offset:32
	global_load_dwordx4 v[66:69], v14, s[36:37] offset:16
	global_load_dwordx4 v[50:53], v14, s[36:37]
	global_load_dwordx4 v[46:49], v[16:17], off offset:128 nt
	v_or_b32_e32 v14, 48, v237
	v_cndmask_b32_e32 v14, v14, v18, vcc
	v_lshlrev_b32_e32 v18, 6, v14
	v_lshlrev_b32_e32 v162, 5, v238
	global_load_dwordx4 v[14:17], v18, s[36:37] offset:48
	global_load_dwordx4 v[20:23], v18, s[36:37] offset:32
	global_load_dwordx4 v[24:27], v18, s[36:37] offset:16
	global_load_dwordx4 v[30:33], v18, s[36:37]
	global_load_dwordx4 v[38:41], v162, s[44:45] offset:144
	global_load_dwordx4 v[42:45], v162, s[44:45] offset:128
	v_and_b32_e32 v160, 16, v236
	v_cmp_eq_u32_e32 vcc, 0, v160
	s_mov_b32 s6, 0x3d000000
	s_brev_b32 s7, 60
	s_mov_b32 s4, 0x358637bd
	s_mov_b32 s7, 0x3c800000
	v_mov_b64_e32 v[170:171], s[4:5]
	s_mov_b32 s48, 2
	s_waitcnt vmcnt(26)
; template <int DQK, int DV, bool LEAD> ...
;     ...
;           float x[NDS][8];
; #pragma unroll
;           for (int ds = 0; ds < NDS; ++ds)
; #pragma unroll
;               for (int j = 0; j < 8; ++j) x[ds][j] = __uint_as_float(((unsigned)(unsigned short)raw[ds][j]) << 16);
;           const int tq = tq0 + qoff + qb * 16 + q16, prow = (tq >> 6) & 127, pcol = tq & 63;
;           float sn = 0.f;
; #pragma unroll
;           for (int ds = 0; ds < 2; ++ds)
; #pragma unroll
;               for (int j = 0; j < 8; ++j) sn += x[ds][j] * x[ds][j];
;           sn = lanes4_sum(sn);
;           const float rn = rsqrtf(sn * (1.f / 64.f) + EPS);
	v_and_b32_e32 v117, 0xffff0000, v125
	s_waitcnt vmcnt(25)
	v_and_b32_e32 v191, 0xffff0000, v138
	v_lshlrev_b32_e32 v190, 16, v138
	v_lshlrev_b32_e32 v116, 16, v125
	s_waitcnt vmcnt(22)
	v_and_b32_e32 v127, 0xffff0000, v8
	v_lshlrev_b32_e32 v126, 16, v8
	v_mul_f32_e32 v8, v191, v191
	v_and_b32_e32 v119, 0xffff0000, v124
	v_lshlrev_b32_e32 v118, 16, v124
	v_and_b32_e32 v125, 0xffff0000, v9
	v_lshlrev_b32_e32 v124, 16, v9
	v_and_b32_e32 v211, 0xffff0000, v139
	v_lshlrev_b32_e32 v210, 16, v139
	v_pk_fma_f32 v[8:9], v[190:191], v[190:191], v[8:9] op_sel_hi:[1,1,0]
	v_and_b32_e32 v187, 0xffff0000, v141
	v_lshlrev_b32_e32 v186, 16, v141
	v_and_b32_e32 v189, 0xffff0000, v140
	v_lshlrev_b32_e32 v188, 16, v140
	v_and_b32_e32 v141, 0xffff0000, v82
	v_lshlrev_b32_e32 v140, 16, v82
	v_pk_fma_f32 v[8:9], v[210:211], v[210:211], v[8:9]
	v_mul_f32_e32 v82, v211, v211
	v_pk_add_f32 v[8:9], v[82:83], v[8:9] op_sel_hi:[0,1]
	v_pk_fma_f32 v[8:9], v[188:189], v[188:189], v[8:9]
	v_mul_f32_e32 v82, v189, v189
	v_pk_add_f32 v[8:9], v[82:83], v[8:9] op_sel_hi:[0,1]
	v_pk_fma_f32 v[8:9], v[186:187], v[186:187], v[8:9]
	v_mul_f32_e32 v82, v187, v187
	v_and_b32_e32 v185, 0xffff0000, v54
	v_lshlrev_b32_e32 v184, 16, v54
	v_pk_add_f32 v[8:9], v[82:83], v[8:9] op_sel_hi:[0,1]
	v_pk_fma_f32 v[8:9], v[184:185], v[184:185], v[8:9]
	v_mul_f32_e32 v82, v185, v185
	v_and_b32_e32 v179, 0xffff0000, v55
	v_lshlrev_b32_e32 v178, 16, v55
	v_pk_add_f32 v[8:9], v[82:83], v[8:9] op_sel_hi:[0,1]
	v_pk_fma_f32 v[8:9], v[178:179], v[178:179], v[8:9]
	v_mul_f32_e32 v82, v179, v179
	v_and_b32_e32 v177, 0xffff0000, v56
	v_lshlrev_b32_e32 v176, 16, v56
	v_pk_add_f32 v[8:9], v[82:83], v[8:9] op_sel_hi:[0,1]
	v_pk_fma_f32 v[8:9], v[176:177], v[176:177], v[8:9]
	v_mul_f32_e32 v82, v177, v177
	v_and_b32_e32 v175, 0xffff0000, v57
	v_lshlrev_b32_e32 v174, 16, v57
	v_pk_add_f32 v[8:9], v[82:83], v[8:9] op_sel_hi:[0,1]
	v_pk_fma_f32 v[8:9], v[174:175], v[174:175], v[8:9]
	v_mul_f32_e32 v82, v175, v175
	v_pk_add_f32 v[8:9], v[82:83], v[8:9] op_sel_hi:[0,1]
	v_and_b32_e32 v129, 0xffff0000, v7
	v_lshlrev_b32_e32 v128, 16, v7
	v_mov_b32_e32 v7, v8
	s_nop 1
	v_permlane16_swap_b32_e32 v8, v7
	v_add_f32_e32 v7, v8, v7
	v_mov_b32_e32 v9, v7
	v_and_b32_e32 v167, 0xffff0000, v144
	s_nop 0
	v_permlane32_swap_b32_e32 v7, v9
	v_lshlrev_b32_e32 v166, 16, v144
	v_mul_f32_e32 v8, v167, v167
	v_and_b32_e32 v137, 0xffff0000, v83
	v_lshlrev_b32_e32 v136, 16, v83
	v_and_b32_e32 v159, 0xffff0000, v145
	v_lshlrev_b32_e32 v158, 16, v145
	v_pk_fma_f32 v[82:83], v[166:167], v[166:167], v[8:9] op_sel_hi:[1,1,0]
	v_mul_f32_e32 v8, v159, v159
	v_pk_fma_f32 v[82:83], v[158:159], v[158:159], v[82:83]
	v_and_b32_e32 v157, 0xffff0000, v146
	v_lshlrev_b32_e32 v156, 16, v146
	v_pk_add_f32 v[82:83], v[8:9], v[82:83] op_sel_hi:[0,1]
	v_pk_fma_f32 v[82:83], v[156:157], v[156:157], v[82:83]
	v_mul_f32_e32 v8, v157, v157
	v_and_b32_e32 v155, 0xffff0000, v147
	v_lshlrev_b32_e32 v154, 16, v147
	v_pk_add_f32 v[82:83], v[8:9], v[82:83] op_sel_hi:[0,1]
	v_pk_fma_f32 v[82:83], v[154:155], v[154:155], v[82:83]
	v_mul_f32_e32 v8, v155, v155
	v_and_b32_e32 v153, 0xffff0000, v62
	v_lshlrev_b32_e32 v152, 16, v62
	v_pk_add_f32 v[82:83], v[8:9], v[82:83] op_sel_hi:[0,1]
	v_pk_fma_f32 v[82:83], v[152:153], v[152:153], v[82:83]
	v_mul_f32_e32 v8, v153, v153
	v_and_b32_e32 v151, 0xffff0000, v63
	v_lshlrev_b32_e32 v150, 16, v63
	v_pk_add_f32 v[82:83], v[8:9], v[82:83] op_sel_hi:[0,1]
	v_pk_fma_f32 v[82:83], v[150:151], v[150:151], v[82:83]
	v_mul_f32_e32 v8, v151, v151
	v_and_b32_e32 v29, 0xffff0000, v64
	v_lshlrev_b32_e32 v28, 16, v64
	v_pk_add_f32 v[82:83], v[8:9], v[82:83] op_sel_hi:[0,1]
	v_pk_fma_f32 v[82:83], v[28:29], v[28:29], v[82:83]
	v_mul_f32_e32 v8, v29, v29
	v_and_b32_e32 v19, 0xffff0000, v65
	v_lshlrev_b32_e32 v18, 16, v65
	v_pk_add_f32 v[82:83], v[8:9], v[82:83] op_sel_hi:[0,1]
	v_pk_fma_f32 v[82:83], v[18:19], v[18:19], v[82:83]
	v_mul_f32_e32 v8, v19, v19
	v_pk_add_f32 v[82:83], v[8:9], v[82:83] op_sel_hi:[0,1]
	v_mov_b32_e32 v8, v82
	s_nop 1
	v_permlane16_swap_b32_e32 v82, v8
	v_and_b32_e32 v149, 0xffff0000, v80
	v_add_f32_e32 v181, v82, v8
	v_lshlrev_b32_e32 v148, 16, v80
	v_mul_f32_e32 v8, v149, v149
	v_and_b32_e32 v143, 0xffff0000, v81
	v_lshlrev_b32_e32 v142, 16, v81
	v_pk_fma_f32 v[80:81], v[148:149], v[148:149], v[8:9] op_sel_hi:[1,1,0]
	v_mul_f32_e32 v8, v143, v143
	v_pk_fma_f32 v[80:81], v[142:143], v[142:143], v[80:81]
	v_and_b32_e32 v135, 0xffff0000, v84
	v_pk_add_f32 v[80:81], v[8:9], v[80:81] op_sel_hi:[0,1]
	v_pk_fma_f32 v[80:81], v[140:141], v[140:141], v[80:81]
	v_mul_f32_e32 v8, v141, v141
	v_pk_add_f32 v[80:81], v[8:9], v[80:81] op_sel_hi:[0,1]
	v_pk_fma_f32 v[80:81], v[136:137], v[136:137], v[80:81]
	v_mul_f32_e32 v8, v137, v137
	v_lshlrev_b32_e32 v134, 16, v84
	v_pk_add_f32 v[80:81], v[8:9], v[80:81] op_sel_hi:[0,1]
	v_pk_fma_f32 v[80:81], v[134:135], v[134:135], v[80:81]
	v_mul_f32_e32 v8, v135, v135
	v_and_b32_e32 v133, 0xffff0000, v85
	v_lshlrev_b32_e32 v132, 16, v85
	v_pk_add_f32 v[80:81], v[8:9], v[80:81] op_sel_hi:[0,1]
	v_pk_fma_f32 v[80:81], v[132:133], v[132:133], v[80:81]
	v_mul_f32_e32 v8, v133, v133
	v_and_b32_e32 v131, 0xffff0000, v86
	v_lshlrev_b32_e32 v130, 16, v86
	v_pk_add_f32 v[80:81], v[8:9], v[80:81] op_sel_hi:[0,1]
	v_pk_fma_f32 v[80:81], v[130:131], v[130:131], v[80:81]
	v_mul_f32_e32 v8, v131, v131
	v_and_b32_e32 v75, 0xffff0000, v87
	v_lshlrev_b32_e32 v74, 16, v87
	v_pk_add_f32 v[80:81], v[8:9], v[80:81] op_sel_hi:[0,1]
	v_pk_fma_f32 v[80:81], v[74:75], v[74:75], v[80:81]
	v_mul_f32_e32 v8, v75, v75
	v_pk_add_f32 v[80:81], v[8:9], v[80:81] op_sel_hi:[0,1]
	v_mov_b32_e32 v8, v80
; template <int DQK, int DV, bool LEAD> ...
;     ...
;           float sn = 0.f;
; #pragma unroll
;           for (int ds = 0; ds < 2; ++ds)
; #pragma unroll
;               for (int j = 0; j < 8; ++j) sn += x[ds][j] * x[ds][j];
;           sn = lanes4_sum(sn);
;           const float rn = rsqrtf(sn * (1.f / 64.f) + EPS);
; #pragma unroll
;           for (int ds = 0; ds < 2; ++ds)
; #pragma unroll
;               for (int j = 0; j < 8; ++j) x[ds][j] *= rn * qgain[32 * ds + 8 * g4 + j];
;           if constexpr (DQK == 64) {
; #pragma unroll
;               for (int ds = 0; ds < 2; ++ds)
; #pragma unroll
;                   for (int j = 0; j < 8; ++j) {
;                       auto rr = __builtin_amdgcn_permlane32_swap(__float_as_uint(x[ds][j]), __float_as_uint(x[ds][j]), false, false);
;                       const float other = hi ? __uint_as_float(rr[0]) : __uint_as_float(rr[1]);
;                       float cc = 1.f, sg = 0.f;
;                       if (lat) { const f32x2 cs = rope[(ds ? pcol : prow) * 16 + 8 * (g4 & 1) + j]; cc = cs.x; sg = hi ? cs.y : -cs.y; }
;                       x[ds][j] = x[ds][j] * cc + other * sg; }
;           } else {
;               float sr = 0.f;
; #pragma unroll
;               for (int j = 0; j < 8; ++j) sr += x[2][j] * x[2][j];
;               sr = lanes4_sum(sr);
;               const float rq = rsqrtf(sr * (1.f / 32.f) + EPS);
; #pragma unroll
;               for (int j = 0; j < 8; ++j) { const float av = x[2][j] * rq * qgain[64 + 8 * g4 + j];
;                   auto rr = __builtin_amdgcn_permlane16_swap(__float_as_uint(av), __float_as_uint(av), false, false);
;                   const float other = (g4 & 1) ? __uint_as_float(rr[0]) : __uint_as_float(rr[1]);
;                   float cc = 1.f, sg = 0.f;
;                   if (lat) { const f32x2 cs = rope[((g4 & 2) ? pcol : prow) * 8 + j]; cc = cs.x; sg = (g4 & 1) ? cs.y : -cs.y; }
;                   x[2][j] = av * cc + other * sg; }
;           }
; #pragma unroll
;           for (int ds = 0; ds < NDS; ++ds) { u32x4 w;
; #pragma unroll
;               for (int i = 0; i < 4; ++i) w[i] = cvtpk(x[ds][2 * i] * c2, x[ds][2 * i + 1] * c2);
;               qf[qb * NDS + ds] = __builtin_bit_cast(bf16x8, w); }
	v_and_b32_e32 v139, 0xffff0000, v6
	s_nop 0
	v_permlane16_swap_b32_e32 v80, v8
	v_lshlrev_b32_e32 v138, 16, v6
	v_mul_f32_e32 v6, v139, v139
	v_add_f32_e32 v161, v80, v8
	v_pk_fma_f32 v[80:81], v[138:139], v[138:139], v[6:7] op_sel_hi:[1,1,0]
	v_mul_f32_e32 v6, v129, v129
	v_pk_fma_f32 v[80:81], v[128:129], v[128:129], v[80:81]
	global_load_dwordx4 v[54:57], v162, s[44:45] offset:16
	global_load_dwordx4 v[62:65], v162, s[44:45]
	v_pk_add_f32 v[80:81], v[6:7], v[80:81] op_sel_hi:[0,1]
	v_pk_fma_f32 v[80:81], v[126:127], v[126:127], v[80:81]
	v_mul_f32_e32 v6, v127, v127
	v_pk_add_f32 v[80:81], v[6:7], v[80:81] op_sel_hi:[0,1]
	v_pk_fma_f32 v[80:81], v[124:125], v[124:125], v[80:81]
	v_mul_f32_e32 v6, v125, v125
	v_and_b32_e32 v121, 0xffff0000, v123
	v_lshlrev_b32_e32 v120, 16, v123
	v_and_b32_e32 v123, 0xffff0000, v122
	v_lshlrev_b32_e32 v122, 16, v122
	v_pk_add_f32 v[80:81], v[6:7], v[80:81] op_sel_hi:[0,1]
	v_pk_fma_f32 v[80:81], v[122:123], v[122:123], v[80:81]
	v_mul_f32_e32 v6, v123, v123
	v_pk_add_f32 v[80:81], v[6:7], v[80:81] op_sel_hi:[0,1]
	v_pk_fma_f32 v[80:81], v[120:121], v[120:121], v[80:81]
	v_mul_f32_e32 v6, v121, v121
	v_pk_add_f32 v[80:81], v[6:7], v[80:81] op_sel_hi:[0,1]
	v_pk_fma_f32 v[80:81], v[118:119], v[118:119], v[80:81]
	v_mul_f32_e32 v6, v119, v119
	v_pk_add_f32 v[80:81], v[6:7], v[80:81] op_sel_hi:[0,1]
	v_pk_fma_f32 v[80:81], v[116:117], v[116:117], v[80:81]
	v_mul_f32_e32 v6, v117, v117
	v_pk_add_f32 v[80:81], v[6:7], v[80:81] op_sel_hi:[0,1]
	v_mov_b32_e32 v6, v80
	s_nop 1
	v_permlane16_swap_b32_e32 v80, v6
	v_add_f32_e32 v145, v80, v6
	global_load_dwordx4 v[80:83], v162, s[44:45] offset:272
	global_load_dwordx4 v[84:87], v162, s[44:45] offset:256
	s_waitcnt vmcnt(25)
	v_and_b32_e32 v201, 0xffff0000, v2
	v_lshlrev_b32_e32 v200, 16, v2
	v_mul_f32_e32 v2, v201, v201
	s_waitcnt vmcnt(20)
	v_and_b32_e32 v213, 0xffff0000, v13
	v_lshlrev_b32_e32 v212, 16, v13
	v_and_b32_e32 v217, 0xffff0000, v12
	v_lshlrev_b32_e32 v216, 16, v12
	v_and_b32_e32 v13, 0xffff0000, v3
	v_lshlrev_b32_e32 v12, 16, v3
	v_pk_fma_f32 v[2:3], v[200:201], v[200:201], v[2:3] op_sel_hi:[1,1,0]
	v_cndmask_b32_e64 v219, v115, -v115, vcc
	v_cndmask_b32_e64 v218, v113, -v113, vcc
	v_mov_b32_e32 v113, v114
	s_waitcnt vmcnt(14)
	v_cndmask_b32_e64 v115, v79, -v79, vcc
	v_cndmask_b32_e64 v114, v77, -v77, vcc
	v_mov_b32_e32 v77, v78
	s_waitcnt vmcnt(9)
	v_cndmask_b32_e64 v79, v17, -v17, vcc
	v_cndmask_b32_e64 v78, v15, -v15, vcc
	v_mov_b32_e32 v15, v16
	v_and_b32_e32 v17, 0xffff0000, v4
	v_lshlrev_b32_e32 v16, 16, v4
	v_pk_fma_f32 v[2:3], v[12:13], v[12:13], v[2:3]
	v_mul_f32_e32 v4, v13, v13
	v_pk_add_f32 v[2:3], v[4:5], v[2:3] op_sel_hi:[0,1]
	v_pk_fma_f32 v[2:3], v[16:17], v[16:17], v[2:3]
	v_mul_f32_e32 v4, v17, v17
	v_and_b32_e32 v221, 0xffff0000, v5
	v_lshlrev_b32_e32 v220, 16, v5
	v_pk_add_f32 v[2:3], v[4:5], v[2:3] op_sel_hi:[0,1]
	v_pk_fma_f32 v[2:3], v[220:221], v[220:221], v[2:3]
	v_mul_f32_e32 v4, v221, v221
	v_pk_add_f32 v[2:3], v[4:5], v[2:3] op_sel_hi:[0,1]
	v_mov_b32_e32 v3, v2
	s_nop 1
	v_permlane16_swap_b32_e32 v2, v3
	v_add_f32_e32 v6, v2, v3
	v_mov_b32_e32 v8, v6
	s_nop 1
	v_permlane32_swap_b32_e32 v6, v8
	v_pk_add_f32 v[2:3], v[6:7], v[8:9]
	v_mov_b32_e32 v147, v145
	v_pk_fma_f32 v[6:7], v[2:3], s[6:7], v[170:171] op_sel_hi:[1,1,0]
	s_nop 0
	v_permlane32_swap_b32_e32 v145, v147
	v_mul_f32_e32 v2, 0x4b800000, v7
	v_cmp_gt_f32_e64 s[4:5], s95, v7
	v_cndmask_b32_e64 v215, v95, -v95, vcc
	v_cndmask_b32_e64 v214, v93, -v93, vcc
	v_cndmask_b32_e64 v2, v7, v2, s[4:5]
	v_rsq_f32_e32 v2, v2
	v_mov_b32_e32 v93, v94
	s_waitcnt vmcnt(8)
	v_cndmask_b32_e64 v95, v23, -v23, vcc
	v_cndmask_b32_e64 v94, v21, -v21, vcc
	v_mul_f32_e32 v3, 0x45800000, v2
	v_cndmask_b32_e64 v144, v2, v3, s[4:5]
	s_waitcnt vmcnt(5)
	v_pk_mul_f32 v[2:3], v[144:145], v[40:41] op_sel_hi:[0,1]
	v_pk_mul_f32 v[2:3], v[2:3], v[174:175]
	v_pk_mul_f32 v[4:5], v[144:145], v[38:39] op_sel_hi:[0,1]
	v_pk_mul_f32 v[2:3], v[2:3], s[82:83] op_sel_hi:[1,0]
	v_pk_mul_f32 v[8:9], v[4:5], v[176:177]
	v_cvt_pk_bf16_f32 v5, v2, v3
	v_pk_mul_f32 v[2:3], v[8:9], s[82:83] op_sel_hi:[1,0]
	s_waitcnt vmcnt(4)
	v_pk_mul_f32 v[8:9], v[42:43], v[144:145] op_sel_hi:[1,0]
	v_cvt_pk_bf16_f32 v4, v2, v3
	v_pk_mul_f32 v[2:3], v[144:145], v[44:45] op_sel_hi:[0,1]
	v_pk_mul_f32 v[2:3], v[2:3], v[178:179]
	v_pk_mul_f32 v[8:9], v[8:9], v[184:185]
	v_pk_mul_f32 v[2:3], v[2:3], s[82:83] op_sel_hi:[1,0]
	v_pk_mul_f32 v[8:9], v[8:9], s[82:83] op_sel_hi:[1,0]
	v_mov_b32_e32 v21, v22
	v_cvt_pk_bf16_f32 v3, v2, v3
	v_cvt_pk_bf16_f32 v2, v8, v9
	s_waitcnt vmcnt(3)
	v_pk_mul_f32 v[8:9], v[56:57], v[144:145] op_sel_hi:[1,0]
	v_pk_mul_f32 v[22:23], v[54:55], v[144:145] op_sel_hi:[1,0]
	v_pk_mul_f32 v[8:9], v[8:9], v[186:187]
	v_pk_mul_f32 v[22:23], v[22:23], v[188:189]
	v_pk_mul_f32 v[8:9], v[8:9], s[82:83] op_sel_hi:[1,0]
	v_pk_mul_f32 v[22:23], v[22:23], s[82:83] op_sel_hi:[1,0]
	v_and_b32_e32 v165, 0xffff0000, v37
	v_lshlrev_b32_e32 v164, 16, v37
	v_and_b32_e32 v173, 0xffff0000, v36
	v_lshlrev_b32_e32 v172, 16, v36
	v_cndmask_b32_e64 v37, v107, -v107, vcc
	v_cndmask_b32_e64 v36, v105, -v105, vcc
	v_mov_b32_e32 v105, v106
	v_and_b32_e32 v107, 0xffff0000, v11
	v_lshlrev_b32_e32 v106, 16, v11
	v_cvt_pk_bf16_f32 v9, v8, v9
	v_cvt_pk_bf16_f32 v8, v22, v23
	s_waitcnt vmcnt(2)
; __device__ __forceinline__ unsigned cvtpk(float lo, float hi) { f32x2 v = {lo, hi}; bf16x2_t b = __builtin_convertvector(v, bf16x2_t); return __builtin_bit_cast(unsigned, b); }
; template <int DQK, int DV, bool LEAD> ...
;     ...
;           } else {
;               float sr = 0.f;
; #pragma unroll
;               for (int j = 0; j < 8; ++j) sr += x[2][j] * x[2][j];
;               sr = lanes4_sum(sr);
;               const float rq = rsqrtf(sr * (1.f / 32.f) + EPS);
; #pragma unroll
;               for (int j = 0; j < 8; ++j) { const float av = x[2][j] * rq * qgain[64 + 8 * g4 + j];
;                   auto rr = __builtin_amdgcn_permlane16_swap(__float_as_uint(av), __float_as_uint(av), false, false);
;                   const float other = (g4 & 1) ? __uint_as_float(rr[0]) : __uint_as_float(rr[1]);
;                   float cc = 1.f, sg = 0.f;
;                   if (lat) { const f32x2 cs = rope[((g4 & 2) ? pcol : prow) * 8 + j]; cc = cs.x; sg = (g4 & 1) ? cs.y : -cs.y; }
;                   x[2][j] = av * cc + other * sg; }
;           }
; #pragma unroll
;           for (int ds = 0; ds < NDS; ++ds) { u32x4 w;
; #pragma unroll
;               for (int i = 0; i < 4; ++i) w[i] = cvtpk(x[ds][2 * i] * c2, x[ds][2 * i + 1] * c2);
;               qf[qb * NDS + ds] = __builtin_bit_cast(bf16x8, w); }
	v_pk_mul_f32 v[22:23], v[64:65], v[144:145] op_sel_hi:[1,0]
	v_mul_f32_e32 v11, 0x4b800000, v6
	v_cmp_gt_f32_e64 s[4:5], s95, v6
	v_pk_mul_f32 v[22:23], v[22:23], v[210:211]
	v_cndmask_b32_e64 v209, v99, -v99, vcc
	v_cndmask_b32_e64 v6, v6, v11, s[4:5]
	v_pk_mul_f32 v[22:23], v[22:23], s[82:83] op_sel_hi:[1,0]
	v_rsq_f32_e32 v11, v6
	v_cvt_pk_bf16_f32 v7, v22, v23
	v_cndmask_b32_e64 v23, v27, -v27, vcc
	v_cndmask_b32_e64 v22, v25, -v25, vcc
	v_mov_b32_e32 v25, v26
	v_pk_mul_f32 v[26:27], v[62:63], v[144:145] op_sel_hi:[1,0]
	v_cndmask_b32_e64 v208, v97, -v97, vcc
	v_pk_mul_f32 v[26:27], v[26:27], v[190:191]
	v_mov_b32_e32 v97, v98
	v_pk_mul_f32 v[26:27], v[26:27], s[82:83] op_sel_hi:[1,0]
	v_and_b32_e32 v99, 0xffff0000, v49
	v_cvt_pk_bf16_f32 v6, v26, v27
	v_mul_f32_e32 v26, 0x45800000, v11
	v_cndmask_b32_e64 v26, v11, v26, s[4:5]
	v_pk_mul_f32 v[176:177], v[26:27], v[12:13] op_sel_hi:[0,1]
	v_pk_mul_f32 v[12:13], v[26:27], v[220:221] op_sel_hi:[0,1]
	s_waitcnt vmcnt(1)
	v_pk_mul_f32 v[12:13], v[12:13], v[82:83]
	v_lshlrev_b32_e32 v98, 16, v49
	v_cndmask_b32_e64 v199, v111, -v111, vcc
	v_cndmask_b32_e64 v198, v109, -v109, vcc
	v_mov_b32_e32 v109, v110
	v_and_b32_e32 v111, 0xffff0000, v48
	v_lshlrev_b32_e32 v110, 16, v48
	v_and_b32_e32 v49, 0xffff0000, v35
	v_lshlrev_b32_e32 v48, 16, v35
	v_pk_mul_f32 v[174:175], v[26:27], v[200:201] op_sel_hi:[0,1]
	v_pk_mul_f32 v[16:17], v[26:27], v[16:17] op_sel_hi:[0,1]
	v_mov_b32_e32 v11, v12
	v_mov_b32_e32 v26, v12
	v_mov_b32_e32 v27, v13
	v_mov_b32_e32 v35, v13
	v_permlane16_swap_b32_e32 v11, v26
	s_nop 0
	v_permlane16_swap_b32_e32 v27, v35
	v_cndmask_b32_e32 v27, v27, v35, vcc
	v_cndmask_b32_e32 v26, v11, v26, vcc
	v_pk_mul_f32 v[26:27], v[218:219], v[26:27]
	v_pk_mul_f32 v[16:17], v[16:17], v[80:81]
	v_pk_fma_f32 v[12:13], v[12:13], v[112:113], v[26:27]
	v_mov_b32_e32 v11, v16
	v_pk_mul_f32 v[12:13], v[12:13], s[82:83] op_sel_hi:[1,0]
	v_mov_b32_e32 v26, v17
	v_cvt_pk_bf16_f32 v13, v12, v13
	v_mov_b32_e32 v12, v16
	v_mov_b32_e32 v27, v17
	s_nop 0
	v_permlane16_swap_b32_e32 v11, v12
	v_permlane16_swap_b32_e32 v26, v27
	v_cndmask_b32_e32 v27, v26, v27, vcc
	v_cndmask_b32_e32 v26, v11, v12, vcc
	v_pk_mul_f32 v[26:27], v[198:199], v[26:27]
	v_cndmask_b32_e64 v178, v101, -v101, vcc
	v_pk_fma_f32 v[16:17], v[16:17], v[108:109], v[26:27]
	v_mov_b32_e32 v101, v102
	v_pk_mul_f32 v[16:17], v[16:17], s[82:83] op_sel_hi:[1,0]
	v_cndmask_b32_e64 v179, v103, -v103, vcc
	v_cvt_pk_bf16_f32 v12, v16, v17
	s_waitcnt vmcnt(0)
	v_pk_mul_f32 v[16:17], v[86:87], v[176:177]
	v_mov_b32_e32 v183, v181
	v_mov_b32_e32 v11, v16
	v_mov_b32_e32 v26, v16
	v_mov_b32_e32 v27, v17
	v_mov_b32_e32 v35, v17
	v_permlane16_swap_b32_e32 v11, v26
	s_nop 0
	v_permlane16_swap_b32_e32 v27, v35
	v_cndmask_b32_e32 v27, v27, v35, vcc
	v_cndmask_b32_e32 v26, v11, v26, vcc
	v_pk_mul_f32 v[26:27], v[36:37], v[26:27]
	v_and_b32_e32 v37, 0xffff0000, v10
	v_pk_fma_f32 v[16:17], v[104:105], v[16:17], v[26:27]
	v_permlane32_swap_b32_e32 v181, v183
	v_pk_mul_f32 v[16:17], v[16:17], s[82:83] op_sel_hi:[1,0]
	v_cndmask_b32_e64 v169, v73, -v73, vcc
	v_cvt_pk_bf16_f32 v11, v16, v17
	v_pk_mul_f32 v[16:17], v[84:85], v[174:175]
	v_cndmask_b32_e64 v168, v71, -v71, vcc
	v_mov_b32_e32 v26, v16
	v_mov_b32_e32 v35, v16
	v_mov_b32_e32 v27, v17
	v_mov_b32_e32 v36, v17
	v_permlane16_swap_b32_e32 v26, v35
	s_nop 0
	v_permlane16_swap_b32_e32 v27, v36
	v_cndmask_b32_e32 v27, v27, v36, vcc
	v_cndmask_b32_e32 v26, v26, v35, vcc
	v_pk_mul_f32 v[16:17], v[100:101], v[16:17]
	v_lshlrev_b32_e32 v36, 16, v10
	v_mul_f32_e32 v10, v37, v37
	v_pk_fma_f32 v[16:17], v[178:179], v[26:27], v[16:17]
	v_pk_fma_f32 v[26:27], v[36:37], v[36:37], v[10:11] op_sel_hi:[1,1,0]
	v_mul_f32_e32 v10, v107, v107
	v_pk_fma_f32 v[26:27], v[106:107], v[106:107], v[26:27]
	v_pk_mul_f32 v[16:17], v[16:17], s[82:83] op_sel_hi:[1,0]
	v_pk_add_f32 v[26:27], v[10:11], v[26:27] op_sel_hi:[0,1]
	v_pk_fma_f32 v[26:27], v[216:217], v[216:217], v[26:27]
	v_mul_f32_e32 v10, v217, v217
	v_pk_add_f32 v[26:27], v[10:11], v[26:27] op_sel_hi:[0,1]
	v_pk_fma_f32 v[26:27], v[212:213], v[212:213], v[26:27]
	v_mul_f32_e32 v10, v213, v213
	v_pk_add_f32 v[26:27], v[10:11], v[26:27] op_sel_hi:[0,1]
	v_mov_b32_e32 v10, v26
	s_nop 1
	v_permlane16_swap_b32_e32 v26, v10
	v_add_f32_e32 v180, v26, v10
	v_mov_b32_e32 v182, v180
	s_nop 1
	v_permlane32_swap_b32_e32 v180, v182
	v_pk_add_f32 v[26:27], v[180:181], v[182:183]
	v_mov_b32_e32 v71, v72
	v_pk_fma_f32 v[26:27], v[26:27], s[6:7], v[170:171] op_sel_hi:[1,1,0]
	v_cndmask_b32_e64 v73, v91, -v91, vcc
	v_mul_f32_e32 v10, 0x4b800000, v27
	v_cmp_gt_f32_e64 s[4:5], s95, v27
	v_mul_f32_e32 v35, 0x4b800000, v26
	v_cndmask_b32_e64 v72, v89, -v89, vcc
	v_cndmask_b32_e64 v10, v27, v10, s[4:5]
	v_rsq_f32_e32 v27, v10
	v_cvt_pk_bf16_f32 v10, v16, v17
	v_mov_b32_e32 v89, v90
	v_cndmask_b32_e64 v91, v69, -v69, vcc
	v_mul_f32_e32 v16, 0x45800000, v27
	v_cndmask_b32_e64 v102, v27, v16, s[4:5]
	v_pk_mul_f32 v[16:17], v[40:41], v[102:103] op_sel_hi:[1,0]
	v_cmp_gt_f32_e64 s[4:5], s95, v26
	v_pk_mul_f32 v[16:17], v[16:17], v[18:19]
	v_pk_mul_f32 v[104:105], v[54:55], v[102:103] op_sel_hi:[1,0]
	v_pk_mul_f32 v[16:17], v[16:17], s[82:83] op_sel_hi:[1,0]
	v_cndmask_b32_e64 v26, v26, v35, s[4:5]
	v_cvt_pk_bf16_f32 v19, v16, v17
	v_pk_mul_f32 v[16:17], v[38:39], v[102:103] op_sel_hi:[1,0]
	v_pk_mul_f32 v[104:105], v[104:105], v[156:157]
	v_pk_mul_f32 v[16:17], v[16:17], v[28:29]
	v_pk_mul_f32 v[28:29], v[42:43], v[102:103] op_sel_hi:[1,0]
	v_pk_mul_f32 v[16:17], v[16:17], s[82:83] op_sel_hi:[1,0]
	v_pk_mul_f32 v[28:29], v[28:29], v[152:153]
	v_cvt_pk_bf16_f32 v18, v16, v17
; template <int DQK, int DV, bool LEAD> ...
;     ...
;           float sn = 0.f;
; #pragma unroll
;           for (int ds = 0; ds < 2; ++ds)
; #pragma unroll
;               for (int j = 0; j < 8; ++j) sn += x[ds][j] * x[ds][j];
;           sn = lanes4_sum(sn);
;           const float rn = rsqrtf(sn * (1.f / 64.f) + EPS);
; #pragma unroll
;           for (int ds = 0; ds < 2; ++ds)
; #pragma unroll
;               for (int j = 0; j < 8; ++j) x[ds][j] *= rn * qgain[32 * ds + 8 * g4 + j];
;           if constexpr (DQK == 64) {
; #pragma unroll
;               for (int ds = 0; ds < 2; ++ds)
; #pragma unroll
;                   for (int j = 0; j < 8; ++j) {
;                       auto rr = __builtin_amdgcn_permlane32_swap(__float_as_uint(x[ds][j]), __float_as_uint(x[ds][j]), false, false);
;                       const float other = hi ? __uint_as_float(rr[0]) : __uint_as_float(rr[1]);
;                       float cc = 1.f, sg = 0.f;
;                       if (lat) { const f32x2 cs = rope[(ds ? pcol : prow) * 16 + 8 * (g4 & 1) + j]; cc = cs.x; sg = hi ? cs.y : -cs.y; }
;                       x[ds][j] = x[ds][j] * cc + other * sg; }
;           } else {
;               float sr = 0.f;
; #pragma unroll
;               for (int j = 0; j < 8; ++j) sr += x[2][j] * x[2][j];
;               sr = lanes4_sum(sr);
;               const float rq = rsqrtf(sr * (1.f / 32.f) + EPS);
; #pragma unroll
;               for (int j = 0; j < 8; ++j) { const float av = x[2][j] * rq * qgain[64 + 8 * g4 + j];
;                   auto rr = __builtin_amdgcn_permlane16_swap(__float_as_uint(av), __float_as_uint(av), false, false);
;                   const float other = (g4 & 1) ? __uint_as_float(rr[0]) : __uint_as_float(rr[1]);
;                   float cc = 1.f, sg = 0.f;
;                   if (lat) { const f32x2 cs = rope[((g4 & 2) ? pcol : prow) * 8 + j]; cc = cs.x; sg = (g4 & 1) ? cs.y : -cs.y; }
;                   x[2][j] = av * cc + other * sg; }
;           }
; #pragma unroll
;           for (int ds = 0; ds < NDS; ++ds) { u32x4 w;
; #pragma unroll
;               for (int i = 0; i < 4; ++i) w[i] = cvtpk(x[ds][2 * i] * c2, x[ds][2 * i + 1] * c2);
;               qf[qb * NDS + ds] = __builtin_bit_cast(bf16x8, w); }
	v_pk_mul_f32 v[16:17], v[44:45], v[102:103] op_sel_hi:[1,0]
	v_pk_mul_f32 v[28:29], v[28:29], s[82:83] op_sel_hi:[1,0]
	v_pk_mul_f32 v[16:17], v[16:17], v[150:151]
	v_rsq_f32_e32 v35, v26
	v_pk_mul_f32 v[16:17], v[16:17], s[82:83] op_sel_hi:[1,0]
	v_pk_mul_f32 v[104:105], v[104:105], s[82:83] op_sel_hi:[1,0]
	v_cvt_pk_bf16_f32 v17, v16, v17
	v_cvt_pk_bf16_f32 v16, v28, v29
	v_pk_mul_f32 v[28:29], v[56:57], v[102:103] op_sel_hi:[1,0]
	v_cndmask_b32_e64 v90, v67, -v67, vcc
	v_pk_mul_f32 v[28:29], v[28:29], v[154:155]
	v_mov_b32_e32 v67, v68
	v_pk_mul_f32 v[28:29], v[28:29], s[82:83] op_sel_hi:[1,0]
	v_and_b32_e32 v69, 0xffff0000, v47
	v_cvt_pk_bf16_f32 v29, v28, v29
	v_cvt_pk_bf16_f32 v28, v104, v105
	v_pk_mul_f32 v[104:105], v[64:65], v[102:103] op_sel_hi:[1,0]
	v_pk_mul_f32 v[102:103], v[62:63], v[102:103] op_sel_hi:[1,0]
	v_lshlrev_b32_e32 v68, 16, v47
	v_pk_mul_f32 v[102:103], v[102:103], v[166:167]
	v_pk_mul_f32 v[104:105], v[104:105], v[158:159]
	v_pk_mul_f32 v[102:103], v[102:103], s[82:83] op_sel_hi:[1,0]
	v_mul_f32_e32 v47, 0x45800000, v35
	v_pk_mul_f32 v[104:105], v[104:105], s[82:83] op_sel_hi:[1,0]
	v_cvt_pk_bf16_f32 v26, v102, v103
	v_cndmask_b32_e64 v102, v35, v47, s[4:5]
	v_cvt_pk_bf16_f32 v27, v104, v105
	v_pk_mul_f32 v[104:105], v[102:103], v[36:37] op_sel_hi:[0,1]
	v_pk_mul_f32 v[36:37], v[102:103], v[212:213] op_sel_hi:[0,1]
	v_pk_mul_f32 v[36:37], v[82:83], v[36:37]
	v_cndmask_b32_e64 v101, v61, -v61, vcc
	v_cndmask_b32_e64 v100, v59, -v59, vcc
	v_mov_b32_e32 v35, v36
	v_mov_b32_e32 v47, v36
	v_mov_b32_e32 v59, v37
	v_mov_b32_e32 v61, v37
	v_permlane16_swap_b32_e32 v35, v47
	s_nop 0
	v_permlane16_swap_b32_e32 v59, v61
	v_pk_mul_f32 v[106:107], v[102:103], v[106:107] op_sel_hi:[0,1]
	v_pk_mul_f32 v[108:109], v[102:103], v[216:217] op_sel_hi:[0,1]
	v_cndmask_b32_e32 v103, v59, v61, vcc
	v_cndmask_b32_e32 v102, v35, v47, vcc
	v_pk_mul_f32 v[102:103], v[208:209], v[102:103]
	v_mov_b32_e32 v163, v161
	v_pk_fma_f32 v[36:37], v[36:37], v[96:97], v[102:103]
	v_pk_mul_f32 v[96:97], v[80:81], v[108:109]
	v_pk_mul_f32 v[36:37], v[36:37], s[82:83] op_sel_hi:[1,0]
	v_mov_b32_e32 v35, v96
	v_cvt_pk_bf16_f32 v37, v36, v37
	v_mov_b32_e32 v36, v96
	v_mov_b32_e32 v47, v97
	v_mov_b32_e32 v59, v97
	v_permlane16_swap_b32_e32 v35, v36
	s_nop 0
	v_permlane16_swap_b32_e32 v47, v59
	v_cndmask_b32_e32 v103, v47, v59, vcc
	v_cndmask_b32_e32 v102, v35, v36, vcc
	v_pk_mul_f32 v[102:103], v[214:215], v[102:103]
	v_permlane32_swap_b32_e32 v161, v163
	v_pk_fma_f32 v[92:93], v[92:93], v[96:97], v[102:103]
	s_nop 0
	v_pk_mul_f32 v[92:93], v[92:93], s[82:83] op_sel_hi:[1,0]
	s_nop 0
	v_cvt_pk_bf16_f32 v36, v92, v93
	v_pk_mul_f32 v[92:93], v[86:87], v[106:107]
	s_nop 0
	v_mov_b32_e32 v35, v92
	v_mov_b32_e32 v47, v92
	v_mov_b32_e32 v59, v93
	v_mov_b32_e32 v61, v93
	v_permlane16_swap_b32_e32 v35, v47
	s_nop 0
	v_permlane16_swap_b32_e32 v59, v61
	v_cndmask_b32_e32 v97, v59, v61, vcc
	v_cndmask_b32_e32 v96, v35, v47, vcc
	v_pk_mul_f32 v[88:89], v[88:89], v[92:93]
	v_cndmask_b32_e64 v92, v51, -v51, vcc
	v_pk_fma_f32 v[72:73], v[72:73], v[96:97], v[88:89]
	v_cndmask_b32_e64 v93, v53, -v53, vcc
	v_pk_mul_f32 v[72:73], v[72:73], s[82:83] op_sel_hi:[1,0]
	s_nop 0
	v_cvt_pk_bf16_f32 v35, v72, v73
	v_pk_mul_f32 v[72:73], v[84:85], v[104:105]
	s_nop 0
	v_mov_b32_e32 v47, v72
	v_mov_b32_e32 v59, v72
	v_mov_b32_e32 v61, v73
	v_mov_b32_e32 v88, v73
	v_permlane16_swap_b32_e32 v47, v59
	s_nop 0
	v_permlane16_swap_b32_e32 v61, v88
	v_cndmask_b32_e32 v89, v61, v88, vcc
	v_cndmask_b32_e32 v88, v47, v59, vcc
	v_mov_b32_e32 v59, v60
	v_pk_mul_f32 v[58:59], v[58:59], v[72:73]
	s_nop 0
	v_pk_fma_f32 v[58:59], v[100:101], v[88:89], v[58:59]
	v_and_b32_e32 v89, 0xffff0000, v34
	v_lshlrev_b32_e32 v88, 16, v34
	v_mul_f32_e32 v34, v89, v89
	v_pk_fma_f32 v[60:61], v[88:89], v[88:89], v[34:35] op_sel_hi:[1,1,0]
	v_mul_f32_e32 v34, v49, v49
	v_pk_fma_f32 v[60:61], v[48:49], v[48:49], v[60:61]
	v_pk_mul_f32 v[58:59], v[58:59], s[82:83] op_sel_hi:[1,0]
	v_pk_add_f32 v[60:61], v[34:35], v[60:61] op_sel_hi:[0,1]
	v_pk_fma_f32 v[60:61], v[172:173], v[172:173], v[60:61]
	v_mul_f32_e32 v34, v173, v173
	v_pk_add_f32 v[60:61], v[34:35], v[60:61] op_sel_hi:[0,1]
	v_pk_fma_f32 v[60:61], v[164:165], v[164:165], v[60:61]
	v_mul_f32_e32 v34, v165, v165
	v_pk_add_f32 v[60:61], v[34:35], v[60:61] op_sel_hi:[0,1]
	v_mov_b32_e32 v34, v60
	s_nop 1
	v_permlane16_swap_b32_e32 v60, v34
	v_add_f32_e32 v160, v60, v34
	v_mov_b32_e32 v162, v160
	s_nop 1
	v_permlane32_swap_b32_e32 v160, v162
	v_pk_add_f32 v[60:61], v[160:161], v[162:163]
	s_nop 0
	v_pk_fma_f32 v[72:73], v[60:61], s[6:7], v[170:171] op_sel_hi:[1,1,0]
	s_nop 0
	v_mul_f32_e32 v34, 0x4b800000, v73
	v_cmp_gt_f32_e64 s[4:5], s95, v73
	s_nop 1
	v_cndmask_b32_e64 v34, v73, v34, s[4:5]
	v_rsq_f32_e32 v47, v34
	v_cvt_pk_bf16_f32 v34, v58, v59
	v_mul_f32_e32 v51, 0x45800000, v47
	v_cndmask_b32_e64 v96, v47, v51, s[4:5]
	v_pk_mul_f32 v[58:59], v[40:41], v[96:97] op_sel_hi:[1,0]
	v_mul_f32_e32 v47, 0x4b800000, v72
	v_pk_mul_f32 v[58:59], v[58:59], v[74:75]
	v_pk_mul_f32 v[74:75], v[42:43], v[96:97] op_sel_hi:[1,0]
	v_pk_mul_f32 v[58:59], v[58:59], s[82:83] op_sel_hi:[1,0]
	v_pk_mul_f32 v[74:75], v[74:75], v[134:135]
	v_cvt_pk_bf16_f32 v61, v58, v59
	v_pk_mul_f32 v[58:59], v[38:39], v[96:97] op_sel_hi:[1,0]
	v_pk_mul_f32 v[74:75], v[74:75], s[82:83] op_sel_hi:[1,0]
	v_pk_mul_f32 v[58:59], v[58:59], v[130:131]
	v_cmp_gt_f32_e64 s[4:5], s95, v72
	v_pk_mul_f32 v[58:59], v[58:59], s[82:83] op_sel_hi:[1,0]
	v_pk_mul_f32 v[100:101], v[54:55], v[96:97] op_sel_hi:[1,0]
	v_cvt_pk_bf16_f32 v60, v58, v59
	v_pk_mul_f32 v[58:59], v[44:45], v[96:97] op_sel_hi:[1,0]
; template <int DQK, int DV, bool LEAD> ...
;     ...
;           float sn = 0.f;
; #pragma unroll
;           for (int ds = 0; ds < 2; ++ds)
; #pragma unroll
;               for (int j = 0; j < 8; ++j) sn += x[ds][j] * x[ds][j];
;           sn = lanes4_sum(sn);
;           const float rn = rsqrtf(sn * (1.f / 64.f) + EPS);
; #pragma unroll
;           for (int ds = 0; ds < 2; ++ds)
; #pragma unroll
;               for (int j = 0; j < 8; ++j) x[ds][j] *= rn * qgain[32 * ds + 8 * g4 + j];
;           if constexpr (DQK == 64) {
; #pragma unroll
;               for (int ds = 0; ds < 2; ++ds)
; #pragma unroll
;                   for (int j = 0; j < 8; ++j) {
;                       auto rr = __builtin_amdgcn_permlane32_swap(__float_as_uint(x[ds][j]), __float_as_uint(x[ds][j]), false, false);
;                       const float other = hi ? __uint_as_float(rr[0]) : __uint_as_float(rr[1]);
;                       float cc = 1.f, sg = 0.f;
;                       if (lat) { const f32x2 cs = rope[(ds ? pcol : prow) * 16 + 8 * (g4 & 1) + j]; cc = cs.x; sg = hi ? cs.y : -cs.y; }
;                       x[ds][j] = x[ds][j] * cc + other * sg; }
;           } else {
;               float sr = 0.f;
; #pragma unroll
;               for (int j = 0; j < 8; ++j) sr += x[2][j] * x[2][j];
;               sr = lanes4_sum(sr);
;               const float rq = rsqrtf(sr * (1.f / 32.f) + EPS);
; #pragma unroll
;               for (int j = 0; j < 8; ++j) { const float av = x[2][j] * rq * qgain[64 + 8 * g4 + j];
;                   auto rr = __builtin_amdgcn_permlane16_swap(__float_as_uint(av), __float_as_uint(av), false, false);
;                   const float other = (g4 & 1) ? __uint_as_float(rr[0]) : __uint_as_float(rr[1]);
;                   float cc = 1.f, sg = 0.f;
;                   if (lat) { const f32x2 cs = rope[((g4 & 2) ? pcol : prow) * 8 + j]; cc = cs.x; sg = (g4 & 1) ? cs.y : -cs.y; }
;                   x[2][j] = av * cc + other * sg; }
;           }
; #pragma unroll
;           for (int ds = 0; ds < NDS; ++ds) { u32x4 w;
; #pragma unroll
;               for (int i = 0; i < 4; ++i) w[i] = cvtpk(x[ds][2 * i] * c2, x[ds][2 * i + 1] * c2);
;               qf[qb * NDS + ds] = __builtin_bit_cast(bf16x8, w); }
	v_cndmask_b32_e64 v47, v72, v47, s[4:5]
	v_pk_mul_f32 v[58:59], v[58:59], v[132:133]
	v_pk_mul_f32 v[100:101], v[100:101], v[140:141]
	v_pk_mul_f32 v[58:59], v[58:59], s[82:83] op_sel_hi:[1,0]
	v_rsq_f32_e32 v47, v47
	v_cvt_pk_bf16_f32 v59, v58, v59
	v_cvt_pk_bf16_f32 v58, v74, v75
	v_pk_mul_f32 v[74:75], v[56:57], v[96:97] op_sel_hi:[1,0]
	v_pk_mul_f32 v[100:101], v[100:101], s[82:83] op_sel_hi:[1,0]
	v_pk_mul_f32 v[74:75], v[74:75], v[136:137]
	v_mul_f32_e32 v51, 0x45800000, v47
	v_pk_mul_f32 v[74:75], v[74:75], s[82:83] op_sel_hi:[1,0]
	s_nop 0
	v_cvt_pk_bf16_f32 v75, v74, v75
	v_cvt_pk_bf16_f32 v74, v100, v101
	v_pk_mul_f32 v[100:101], v[64:65], v[96:97] op_sel_hi:[1,0]
	v_pk_mul_f32 v[96:97], v[62:63], v[96:97] op_sel_hi:[1,0]
	v_pk_mul_f32 v[100:101], v[100:101], v[142:143]
	v_pk_mul_f32 v[96:97], v[96:97], v[148:149]
	v_pk_mul_f32 v[100:101], v[100:101], s[82:83] op_sel_hi:[1,0]
	v_pk_mul_f32 v[96:97], v[96:97], s[82:83] op_sel_hi:[1,0]
	v_cvt_pk_bf16_f32 v73, v100, v101
	v_cvt_pk_bf16_f32 v72, v96, v97
	v_cndmask_b32_e64 v96, v47, v51, s[4:5]
	v_pk_mul_f32 v[100:101], v[96:97], v[48:49] op_sel_hi:[0,1]
	v_pk_mul_f32 v[48:49], v[96:97], v[164:165] op_sel_hi:[0,1]
	v_pk_mul_f32 v[48:49], v[82:83], v[48:49]
	v_pk_mul_f32 v[88:89], v[96:97], v[88:89] op_sel_hi:[0,1]
	v_pk_mul_f32 v[102:103], v[96:97], v[172:173] op_sel_hi:[0,1]
	v_mov_b32_e32 v47, v48
	v_mov_b32_e32 v51, v48
	v_mov_b32_e32 v53, v49
	v_mov_b32_e32 v96, v49
	v_permlane16_swap_b32_e32 v47, v51
	s_nop 0
	v_permlane16_swap_b32_e32 v53, v96
	v_cndmask_b32_e32 v97, v53, v96, vcc
	v_cndmask_b32_e32 v96, v47, v51, vcc
	v_pk_mul_f32 v[96:97], v[114:115], v[96:97]
	s_nop 0
	v_pk_fma_f32 v[48:49], v[48:49], v[76:77], v[96:97]
	v_pk_mul_f32 v[76:77], v[80:81], v[102:103]
	v_pk_mul_f32 v[48:49], v[48:49], s[82:83] op_sel_hi:[1,0]
	v_mov_b32_e32 v47, v76
	v_cvt_pk_bf16_f32 v49, v48, v49
	v_mov_b32_e32 v48, v76
	v_mov_b32_e32 v51, v77
	v_mov_b32_e32 v53, v77
	v_permlane16_swap_b32_e32 v47, v48
	s_nop 0
	v_permlane16_swap_b32_e32 v51, v53
	v_cndmask_b32_e32 v97, v51, v53, vcc
	v_cndmask_b32_e32 v96, v47, v48, vcc
	v_pk_mul_f32 v[96:97], v[168:169], v[96:97]
	s_nop 0
	v_pk_fma_f32 v[70:71], v[70:71], v[76:77], v[96:97]
	s_nop 0
	v_pk_mul_f32 v[70:71], v[70:71], s[82:83] op_sel_hi:[1,0]
	s_nop 0
	v_cvt_pk_bf16_f32 v48, v70, v71
	v_pk_mul_f32 v[70:71], v[86:87], v[100:101]
	s_nop 0
	v_mov_b32_e32 v47, v70
	v_mov_b32_e32 v51, v70
	v_mov_b32_e32 v53, v71
	v_mov_b32_e32 v76, v71
	v_permlane16_swap_b32_e32 v47, v51
	s_nop 0
	v_permlane16_swap_b32_e32 v53, v76
	v_cndmask_b32_e32 v77, v53, v76, vcc
	v_cndmask_b32_e32 v76, v47, v51, vcc
	v_pk_mul_f32 v[66:67], v[66:67], v[70:71]
	s_nop 0
	v_pk_fma_f32 v[66:67], v[90:91], v[76:77], v[66:67]
	s_nop 0
	v_pk_mul_f32 v[66:67], v[66:67], s[82:83] op_sel_hi:[1,0]
	s_nop 0
	v_cvt_pk_bf16_f32 v47, v66, v67
	v_pk_mul_f32 v[66:67], v[84:85], v[88:89]
	s_nop 0
	v_mov_b32_e32 v51, v66
	v_mov_b32_e32 v53, v66
	v_mov_b32_e32 v70, v67
	v_mov_b32_e32 v71, v67
	v_permlane16_swap_b32_e32 v51, v53
	s_nop 0
	v_permlane16_swap_b32_e32 v70, v71
	v_cndmask_b32_e32 v71, v70, v71, vcc
	v_cndmask_b32_e32 v70, v51, v53, vcc
	v_and_b32_e32 v53, 0xffff0000, v46
	v_mov_b32_e32 v51, v52
	v_lshlrev_b32_e32 v52, 16, v46
	v_mul_f32_e32 v46, v53, v53
	v_pk_mul_f32 v[50:51], v[50:51], v[66:67]
	v_pk_fma_f32 v[66:67], v[52:53], v[52:53], v[46:47] op_sel_hi:[1,1,0]
	v_mul_f32_e32 v46, v69, v69
	v_pk_fma_f32 v[66:67], v[68:69], v[68:69], v[66:67]
	v_pk_fma_f32 v[50:51], v[92:93], v[70:71], v[50:51]
	v_pk_add_f32 v[66:67], v[46:47], v[66:67] op_sel_hi:[0,1]
	v_pk_fma_f32 v[66:67], v[110:111], v[110:111], v[66:67]
	v_mul_f32_e32 v46, v111, v111
	v_pk_add_f32 v[66:67], v[46:47], v[66:67] op_sel_hi:[0,1]
	v_pk_fma_f32 v[66:67], v[98:99], v[98:99], v[66:67]
	v_mul_f32_e32 v46, v99, v99
	v_pk_add_f32 v[66:67], v[46:47], v[66:67] op_sel_hi:[0,1]
	v_mov_b32_e32 v46, v66
	s_nop 1
	v_permlane16_swap_b32_e32 v66, v46
	v_add_f32_e32 v144, v66, v46
	v_mov_b32_e32 v146, v144
	s_nop 1
	v_permlane32_swap_b32_e32 v144, v146
	v_pk_add_f32 v[66:67], v[144:145], v[146:147]
	v_pk_mul_f32 v[50:51], v[50:51], s[82:83] op_sel_hi:[1,0]
	v_pk_fma_f32 v[66:67], v[66:67], s[6:7], v[170:171] op_sel_hi:[1,1,0]
	s_mov_b64 s[6:7], 0x60000
	v_mul_f32_e32 v46, 0x4b800000, v67
	v_cmp_gt_f32_e64 s[4:5], s95, v67
	s_nop 1
	v_cndmask_b32_e64 v46, v67, v46, s[4:5]
	v_rsq_f32_e32 v67, v46
	v_cvt_pk_bf16_f32 v46, v50, v51
	v_cndmask_b32_e64 v50, v31, -v31, vcc
	v_cndmask_b32_e64 v51, v33, -v33, vcc
	v_mul_f32_e32 v31, 0x45800000, v67
	v_cndmask_b32_e64 v70, v67, v31, s[4:5]
	v_mul_f32_e32 v31, 0x4b800000, v66
	v_cmp_gt_f32_e64 s[4:5], s95, v66
	v_pk_mul_f32 v[62:63], v[62:63], v[70:71] op_sel_hi:[1,0]
	v_pk_mul_f32 v[64:65], v[64:65], v[70:71] op_sel_hi:[1,0]
	v_cndmask_b32_e64 v31, v66, v31, s[4:5]
	v_pk_mul_f32 v[38:39], v[38:39], v[70:71] op_sel_hi:[1,0]
	v_rsq_f32_e32 v31, v31
	v_pk_mul_f32 v[62:63], v[62:63], v[138:139]
	v_pk_mul_f32 v[64:65], v[64:65], v[128:129]
	v_pk_mul_f32 v[54:55], v[54:55], v[70:71] op_sel_hi:[1,0]
	v_pk_mul_f32 v[56:57], v[56:57], v[70:71] op_sel_hi:[1,0]
	v_pk_mul_f32 v[42:43], v[42:43], v[70:71] op_sel_hi:[1,0]
	v_pk_mul_f32 v[44:45], v[44:45], v[70:71] op_sel_hi:[1,0]
	v_pk_mul_f32 v[76:77], v[38:39], v[118:119]
	v_pk_mul_f32 v[38:39], v[40:41], v[70:71] op_sel_hi:[1,0]
	v_pk_mul_f32 v[54:55], v[54:55], v[126:127]
	v_pk_mul_f32 v[56:57], v[56:57], v[124:125]
	v_pk_mul_f32 v[42:43], v[42:43], v[122:123]
	v_pk_mul_f32 v[44:45], v[44:45], v[120:121]
	v_pk_mul_f32 v[70:71], v[38:39], v[116:117]
	v_pk_mul_f32 v[38:39], v[62:63], s[82:83] op_sel_hi:[1,0]
	v_pk_mul_f32 v[40:41], v[64:65], s[82:83] op_sel_hi:[1,0]
; __device__ __forceinline__ unsigned cvtpk(float lo, float hi) { f32x2 v = {lo, hi}; bf16x2_t b = __builtin_convertvector(v, bf16x2_t); return __builtin_bit_cast(unsigned, b); }
; #define ATT_SB() __builtin_amdgcn_sched_barrier(0)
; #define ATT_DMA_K(t, sl) do { glds16(ksrc + (size_t)(t) * 64 * kpitch, (unsigned)__builtin_amdgcn_readfirstlane(kdst + (sl) * KSLOT)); \
;         if constexpr (DQK == 96) glds16(krsrc + (size_t)(t) * 64 * 32, (unsigned)__builtin_amdgcn_readfirstlane(krdst + (sl) * KSLOT)); } while (0)
; #define ATT_DMA_V(t, sl) do { glds16(vsrc + (size_t)(t) * 64, (unsigned)__builtin_amdgcn_readfirstlane(vdst + (sl) * VSLOT)); \
;         if constexpr (DV == 128) glds16(vsrc + (size_t)64 * NR + (size_t)(t) * 64, (unsigned)__builtin_amdgcn_readfirstlane(vdst + (sl) * VSLOT + 8192)); } while (0)
; #define ATT_KLOAD(sl) do { _Pragma("unroll") for (int kb_ = 0; kb_ < NKW; ++kb_) _Pragma("unroll") for (int ds_ = 0; ds_ < NDS; ++ds_) { \
;         if (ds_ < 2) kf[kb_ * NDS + ds_] = *(const LAS bf16x8*)(kp[ds_ & 1] + (sl) * KSLOT + (kb_ & 1) * 512 + (kb_ >> 1) * 4096); \
;         else kf[kb_ * NDS + ds_] = *(const LAS bf16x8*)(krp + (sl) * KSLOT + (kb_ & 1) * 256 + (kb_ >> 1) * 2048); } } while (0)
; template <int DQK, int DV, bool LEAD> ...
;     ...
;           for (int ds = 0; ds < NDS; ++ds) { u32x4 w;
; #pragma unroll
;               for (int i = 0; i < 4; ++i) w[i] = cvtpk(x[ds][2 * i] * c2, x[ds][2 * i + 1] * c2);
;               qf[qb * NDS + ds] = __builtin_bit_cast(bf16x8, w); }
;       }
; #pragma unroll
;       for (int d0 = 0; d0 < NQB * NDS; ++d0) asm volatile("" : "+v"(qf[d0])); }
;     wait_bar<0>();
;     bf16x8 kf[NKW * NDS], vf[NVF];
;     ATT_KLOAD(0);
;     asm volatile("s_waitcnt lgkmcnt(0)\n\ts_barrier" ::: "memory");
;     float lsum[NQB];
; #pragma unroll
;     for (int qb = 0; qb < NQB; ++qb) lsum[qb] = 0.f;
;     const f32x4 zero4 = {0.f, 0.f, 0.f, 0.f};
;     f32x4 o[NDB][NQB], c[NKW][NQB]; u32x4 pw[4];
; #pragma unroll
;     for (int i = 0; i < NDB; ++i)
; #pragma unroll
;         for (int qb = 0; qb < NQB; ++qb) o[i][qb] = zero4;
;     ATT_DMA_K(3, 0); ATT_DMA_V(1, 1);
;     ATT_QK(); ATT_SB();
;     ATT_KLOAD(1); ATT_SB();
	v_cvt_pk_bf16_f32 v38, v38, v39
	v_cvt_pk_bf16_f32 v39, v40, v41
	v_pk_mul_f32 v[40:41], v[54:55], s[82:83] op_sel_hi:[1,0]
	v_pk_mul_f32 v[54:55], v[56:57], s[82:83] op_sel_hi:[1,0]
	v_pk_mul_f32 v[42:43], v[42:43], s[82:83] op_sel_hi:[1,0]
	v_pk_mul_f32 v[44:45], v[44:45], s[82:83] op_sel_hi:[1,0]
	v_cvt_pk_bf16_f32 v40, v40, v41
	v_cvt_pk_bf16_f32 v41, v54, v55
	v_cvt_pk_bf16_f32 v42, v42, v43
	v_cvt_pk_bf16_f32 v43, v44, v45
	v_pk_mul_f32 v[44:45], v[76:77], s[82:83] op_sel_hi:[1,0]
	v_pk_mul_f32 v[54:55], v[70:71], s[82:83] op_sel_hi:[1,0]
	v_mul_f32_e32 v33, 0x45800000, v31
	v_cvt_pk_bf16_f32 v44, v44, v45
	v_cvt_pk_bf16_f32 v45, v54, v55
	v_cndmask_b32_e64 v54, v31, v33, s[4:5]
	v_pk_mul_f32 v[52:53], v[54:55], v[52:53] op_sel_hi:[0,1]
	v_pk_mul_f32 v[52:53], v[84:85], v[52:53]
	s_lshl_b32 s4, s16, 11
	v_mov_b32_e32 v31, v52
	v_mov_b32_e32 v33, v52
	v_mov_b32_e32 v55, v53
	v_mov_b32_e32 v56, v53
	v_permlane16_swap_b32_e32 v31, v33
	s_nop 0
	v_permlane16_swap_b32_e32 v55, v56
	v_cndmask_b32_e32 v57, v55, v56, vcc
	v_cndmask_b32_e32 v56, v31, v33, vcc
	v_mov_b32_e32 v31, v32
	v_pk_mul_f32 v[32:33], v[54:55], v[68:69] op_sel_hi:[0,1]
	v_pk_mul_f32 v[30:31], v[30:31], v[52:53]
	v_pk_mul_f32 v[32:33], v[86:87], v[32:33]
	v_pk_fma_f32 v[30:31], v[50:51], v[56:57], v[30:31]
	v_mov_b32_e32 v50, v32
	v_mov_b32_e32 v52, v32
	v_mov_b32_e32 v51, v33
	v_mov_b32_e32 v53, v33
	v_permlane16_swap_b32_e32 v50, v52
	s_nop 0
	v_permlane16_swap_b32_e32 v51, v53
	v_cndmask_b32_e32 v51, v51, v53, vcc
	v_cndmask_b32_e32 v50, v50, v52, vcc
	v_pk_mul_f32 v[24:25], v[24:25], v[32:33]
	s_cmpk_lt_u32 s38, 0x100
	v_pk_fma_f32 v[22:23], v[22:23], v[50:51], v[24:25]
	v_pk_mul_f32 v[24:25], v[54:55], v[110:111] op_sel_hi:[0,1]
	v_pk_mul_f32 v[24:25], v[80:81], v[24:25]
	v_pk_mul_f32 v[22:23], v[22:23], s[82:83] op_sel_hi:[1,0]
	v_mov_b32_e32 v32, v24
	v_mov_b32_e32 v50, v24
	v_mov_b32_e32 v33, v25
	v_mov_b32_e32 v51, v25
	v_permlane16_swap_b32_e32 v32, v50
	s_nop 0
	v_permlane16_swap_b32_e32 v33, v51
	v_cndmask_b32_e32 v33, v33, v51, vcc
	v_cndmask_b32_e32 v32, v32, v50, vcc
	v_pk_mul_f32 v[32:33], v[94:95], v[32:33]
	s_mov_b32 s16, 1
	v_pk_fma_f32 v[20:21], v[20:21], v[24:25], v[32:33]
	v_pk_mul_f32 v[24:25], v[54:55], v[98:99] op_sel_hi:[0,1]
	v_pk_mul_f32 v[24:25], v[82:83], v[24:25]
	v_pk_mul_f32 v[20:21], v[20:21], s[82:83] op_sel_hi:[1,0]
	v_mov_b32_e32 v32, v24
	v_mov_b32_e32 v50, v24
	v_mov_b32_e32 v33, v25
	v_mov_b32_e32 v51, v25
	v_permlane16_swap_b32_e32 v32, v50
	s_nop 0
	v_permlane16_swap_b32_e32 v33, v51
	v_cndmask_b32_e32 v33, v33, v51, vcc
	v_cndmask_b32_e32 v32, v32, v50, vcc
	v_pk_mul_f32 v[32:33], v[78:79], v[32:33]
	v_cvt_pk_bf16_f32 v55, v22, v23
	v_pk_fma_f32 v[14:15], v[24:25], v[14:15], v[32:33]
	v_pk_mul_f32 v[24:25], v[30:31], s[82:83] op_sel_hi:[1,0]
	v_pk_mul_f32 v[14:15], v[14:15], s[82:83] op_sel_hi:[1,0]
	v_cvt_pk_bf16_f32 v54, v24, v25
	v_cvt_pk_bf16_f32 v56, v20, v21
	v_cvt_pk_bf16_f32 v57, v14, v15
	s_waitcnt vmcnt(0) lgkmcnt(0)
	s_barrier
	ds_read_b128 v[20:23], v203
	ds_read_b128 v[30:33], v203 offset:512
	v_or_b32_e32 v24, 4, v238
	v_bitop3_b32 v14, v243, v24, v242 bitop3:0x36
	v_lshl_add_u32 v211, v14, 4, v244
	s_waitcnt lgkmcnt(1)
	v_mfma_f32_16x16x32_bf16 v[50:53], v[20:23], v[6:9], 0
	ds_read_b128 v[76:79], v211
	ds_read_b128 v[80:83], v211 offset:512
	v_lshlrev_b32_e32 v14, 5, v241
	v_lshlrev_b32_e32 v15, 6, v239
	v_mfma_f32_16x16x32_bf16 v[62:65], v[20:23], v[26:29], 0
	v_bitop3_b32 v14, v14, v236, 48 bitop3:0x78
	v_sub_u32_e32 v15, v240, v15
	v_add3_u32 v212, v15, v14, s4
	v_mfma_f32_16x16x32_bf16 v[66:69], v[20:23], v[72:75], 0
	v_lshl_add_u64 v[14:15], v[192:193], 0, s[6:7]
	s_mov_b64 s[6:7], 0x3000
	s_mov_b32 s4, 0
	v_mfma_f32_16x16x32_bf16 v[20:23], v[20:23], v[38:41], 0
	s_cselect_b64 vcc, -1, 0
	v_lshrrev_b32_e32 v25, 1, v236
	s_waitcnt lgkmcnt(1)
	v_mfma_f32_16x16x32_bf16 v[50:53], v[76:79], v[2:5], v[50:53]
	v_mfma_f32_16x16x32_bf16 v[62:65], v[76:79], v[16:19], v[62:65]
	v_mfma_f32_16x16x32_bf16 v[66:69], v[76:79], v[58:61], v[66:69]
	v_mfma_f32_16x16x32_bf16 v[20:23], v[76:79], v[42:45], v[20:23]
	ds_read_b128 v[76:79], v212 offset:8192
	ds_read_b128 v[84:87], v212 offset:8448
	s_waitcnt lgkmcnt(0)
	s_barrier
; #define ATT_SB() __builtin_amdgcn_sched_barrier(0)
; #define ATT_DMA_K(t, sl) do { glds16(ksrc + (size_t)(t) * 64 * kpitch, (unsigned)__builtin_amdgcn_readfirstlane(kdst + (sl) * KSLOT)); \
;         if constexpr (DQK == 96) glds16(krsrc + (size_t)(t) * 64 * 32, (unsigned)__builtin_amdgcn_readfirstlane(krdst + (sl) * KSLOT)); } while (0)
; #define ATT_DMA_V(t, sl) do { glds16(vsrc + (size_t)(t) * 64, (unsigned)__builtin_amdgcn_readfirstlane(vdst + (sl) * VSLOT)); \
;         if constexpr (DV == 128) glds16(vsrc + (size_t)64 * NR + (size_t)(t) * 64, (unsigned)__builtin_amdgcn_readfirstlane(vdst + (sl) * VSLOT + 8192)); } while (0)
; #define ATT_KLOAD(sl) do { _Pragma("unroll") for (int kb_ = 0; kb_ < NKW; ++kb_) _Pragma("unroll") for (int ds_ = 0; ds_ < NDS; ++ds_) { \
;         if (ds_ < 2) kf[kb_ * NDS + ds_] = *(const LAS bf16x8*)(kp[ds_ & 1] + (sl) * KSLOT + (kb_ & 1) * 512 + (kb_ >> 1) * 4096); \
;         else kf[kb_ * NDS + ds_] = *(const LAS bf16x8*)(krp + (sl) * KSLOT + (kb_ & 1) * 256 + (kb_ >> 1) * 2048); } } while (0)
; #define ATT_QK() do { _Pragma("unroll") for (int kb_ = 0; kb_ < NKW; ++kb_) _Pragma("unroll") for (int ds_ = 0; ds_ < NDS; ++ds_) _Pragma("unroll") for (int qb_ = 0; qb_ < NQB; ++qb_) \
;         c[kb_][qb_] = __builtin_amdgcn_mfma_f32_16x16x32_bf16(kf[kb_ * NDS + ds_], qf[qb_ * NDS + ds_], ds_ == 0 ? zero4 : c[kb_][qb_], 0, 0, 0); } while (0)
; template <int DQK, int DV, bool LEAD> ...
;     ...
;     bf16x8 kf[NKW * NDS], vf[NVF];
;     ATT_KLOAD(0);
;     asm volatile("s_waitcnt lgkmcnt(0)\n\ts_barrier" ::: "memory");
;     float lsum[NQB];
; #pragma unroll
;     for (int qb = 0; qb < NQB; ++qb) lsum[qb] = 0.f;
;     const f32x4 zero4 = {0.f, 0.f, 0.f, 0.f};
;     f32x4 o[NDB][NQB], c[NKW][NQB]; u32x4 pw[4];
; #pragma unroll
;     for (int i = 0; i < NDB; ++i)
; #pragma unroll
;         for (int qb = 0; qb < NQB; ++qb) o[i][qb] = zero4;
;     ATT_DMA_K(3, 0); ATT_DMA_V(1, 1);
;     ATT_QK(); ATT_SB();
;     ATT_KLOAD(1); ATT_SB();
;     if constexpr (LEAD) { ATT_EXP(); ATT_SUMPACK(); }
;     wait_bar<NDMA>();
;     int s_prev = 0, s_cur = 1, s_next = 2;
;     int one_ = 1; asm volatile("" : "+s"(one_));
	s_mov_b32 s5, m0
	s_mov_b32 m0, s42
	s_nop 0
	global_load_lds_dwordx4 v[14:15], off
	s_mov_b32 m0, s5
	s_waitcnt lgkmcnt(1)
	v_mfma_f32_16x16x32_bf16 v[164:167], v[76:79], v[10:13], v[50:53]
	v_lshl_add_u64 v[14:15], v[204:205], 0, s[6:7]
	s_mov_b32 s5, m0
	s_mov_b32 m0, s43
	s_nop 0
	global_load_lds_dwordx4 v[14:15], off
	s_mov_b32 m0, s5
	v_lshl_add_u64 v[14:15], v[206:207], 0, s[66:67]
	v_mfma_f32_16x16x32_bf16 v[152:155], v[76:79], v[34:37], v[62:65]
	s_add_i32 s5, s41, 0x2000
	s_mov_b32 s6, m0
	s_mov_b32 m0, s5
	s_nop 0
	global_load_lds_dwordx4 v[14:15], off
	s_mov_b32 m0, s6
	s_mov_b32 s6, s4
	v_mfma_f32_16x16x32_bf16 v[136:139], v[76:79], v[54:57], v[20:23]
	s_mov_b32 s7, s4
	s_mov_b32 s5, s4
	v_mfma_f32_16x16x32_bf16 v[20:23], v[30:33], v[6:9], 0
	v_mfma_f32_16x16x32_bf16 v[50:53], v[30:33], v[26:29], 0
	v_mfma_f32_16x16x32_bf16 v[62:65], v[30:33], v[72:75], 0
	v_mfma_f32_16x16x32_bf16 v[30:33], v[30:33], v[38:41], 0
	v_mfma_f32_16x16x32_bf16 v[20:23], v[80:83], v[2:5], v[20:23]
	v_mfma_f32_16x16x32_bf16 v[50:53], v[80:83], v[16:19], v[50:53]
	v_mfma_f32_16x16x32_bf16 v[62:65], v[80:83], v[58:61], v[62:65]
	v_mfma_f32_16x16x32_bf16 v[30:33], v[80:83], v[42:45], v[30:33]
	v_mfma_f32_16x16x32_bf16 v[144:147], v[76:79], v[46:49], v[66:69]
	s_waitcnt lgkmcnt(0)
	v_mfma_f32_16x16x32_bf16 v[172:175], v[84:87], v[10:13], v[20:23]
	s_nop 0
	v_lshlrev_b32_e32 v66, 7, v237
	v_mfma_f32_16x16x32_bf16 v[168:171], v[84:87], v[34:37], v[50:53]
	v_mov_b64_e32 v[22:23], s[6:7]
	v_mov_b64_e32 v[20:21], s[4:5]
	v_mfma_f32_16x16x32_bf16 v[160:163], v[84:87], v[46:49], v[62:65]
	v_mfma_f32_16x16x32_bf16 v[156:159], v[84:87], v[54:57], v[30:33]
	ds_read_b128 v[120:123], v203 offset:12288
	ds_read_b128 v[132:135], v203 offset:12800
	ds_read_b128 v[124:127], v211 offset:12288
	ds_read_b128 v[140:143], v211 offset:12800
	ds_read_b128 v[128:131], v212 offset:20480
	ds_read_b128 v[148:151], v212 offset:20736
	v_cndmask_b32_e32 v14, v24, v238, vcc
	v_bitop3_b32 v14, v14, v25, 7 bitop3:0x78
	v_lshlrev_b32_e32 v14, 4, v14
	v_add3_u32 v210, 0, v66, v14
	s_waitcnt vmcnt(3) lgkmcnt(0)
	s_barrier
	s_mov_b32 s5, 1
	v_mov_b32_e32 v14, 0
	s_cmp_lg_u32 s5, 0
	v_mov_b64_e32 v[32:33], v[22:23]
	v_mov_b64_e32 v[52:53], v[22:23]
	v_mov_b64_e32 v[64:65], v[22:23]
	v_mov_b64_e32 v[68:69], v[22:23]
	v_mov_b64_e32 v[78:79], v[22:23]
	v_mov_b64_e32 v[82:83], v[22:23]
	v_mov_b64_e32 v[86:87], v[22:23]
	v_mov_b64_e32 v[90:91], v[22:23]
	v_mov_b64_e32 v[94:95], v[22:23]
	v_mov_b64_e32 v[98:99], v[22:23]
	v_mov_b64_e32 v[102:103], v[22:23]
	v_mov_b64_e32 v[106:107], v[22:23]
	v_mov_b64_e32 v[110:111], v[22:23]
	v_mov_b64_e32 v[114:115], v[22:23]
	v_mov_b64_e32 v[118:119], v[22:23]
	s_cselect_b64 s[6:7], -1, 0
	v_mov_b64_e32 v[30:31], v[20:21]
	v_mov_b64_e32 v[50:51], v[20:21]
	v_mov_b64_e32 v[62:63], v[20:21]
	v_mov_b64_e32 v[66:67], v[20:21]
	v_mov_b64_e32 v[76:77], v[20:21]
	v_mov_b64_e32 v[80:81], v[20:21]
	v_mov_b64_e32 v[84:85], v[20:21]
	v_mov_b64_e32 v[88:89], v[20:21]
	v_mov_b64_e32 v[92:93], v[20:21]
	v_mov_b64_e32 v[96:97], v[20:21]
	v_mov_b64_e32 v[100:101], v[20:21]
	v_mov_b64_e32 v[104:105], v[20:21]
	v_mov_b64_e32 v[108:109], v[20:21]
	v_mov_b64_e32 v[112:113], v[20:21]
	v_mov_b64_e32 v[116:117], v[20:21]
	s_mov_b32 s38, 2
	v_mov_b32_e32 v15, v14
	v_mov_b32_e32 v24, v14
	v_mov_b32_e32 v25, v14

; template <int DQK, int DV, bool LEAD> ...
;     ...
;     const int krow_l = wid * 8 + (lane >> 3);
;     const int kc_l = (lane & 7) ^ (((krow_l >> 1) & 1) | (((krow_l >> 3) & 1) << 1) | (((krow_l >> 4) & 1) << 2));
;     const int vc_l = (lane & 7) ^ ((krow_l >> 1) & 7);
;     const bf16_t* ksrc = K + (size_t)(krow0 + krow_l) * kpitch + kc_l * 8;
;     const int rrow_l = (wid & 3) * 16 + (lane >> 2), rc_l = (lane & 3) ^ (((rrow_l >> 4) & 1) << 1);
;     const bf16_t* krsrc = (DQK == 96) ? KR + (size_t)(krow0 + rrow_l) * 32 + rc_l * 8 : nullptr;
;     const bf16_t* vsrc = Vt + (size_t)krow_l * NR + krow0 + vc_l * 8;
;     const unsigned kdst = lds0 + KOFF + wid * 1024, krdst = lds0 + KOFF + 8192 + (wid & 3) * 1024, vdst = lds0 + VOFF + wid * 1024;
;     ...
;     ATT_DMA_K(0, 0); ATT_DMA_V(0, 0); ATT_DMA_K(1, 1); ATT_DMA_K(2, 2);
;     bf16x8 qf[NQB * NDS];
;     {
;       const float c2 = (DQK == 64) ? C2_EVEN : C2_ODD; const bool lat = tq0 >= 0;
; #pragma unroll
;       for (int qb = 0; qb < NQB; ++qb) {
;           const bf16_t* qp = Q + (size_t)(qrow0 + qoff + qb * 16 + q16) * qpitch + g4 * 8;
;           bf16x8 raw[NDS];
; #pragma unroll
;           for (int ds = 0; ds < NDS; ++ds) raw[ds] = *(const bf16x8*)(qp + ds * 32);
;           float x[NDS][8];
; #pragma unroll
;           for (int ds = 0; ds < NDS; ++ds)
; #pragma unroll
;               for (int j = 0; j < 8; ++j) x[ds][j] = __uint_as_float(((unsigned)(unsigned short)raw[ds][j]) << 16);
;           const int tq = tq0 + qoff + qb * 16 + q16, prow = (tq >> 6) & 127, pcol = tq & 63;
;           float sn = 0.f;
; #pragma unroll
;           for (int ds = 0; ds < 2; ++ds)
; #pragma unroll
;               for (int j = 0; j < 8; ++j) sn += x[ds][j] * x[ds][j];
;           sn = lanes4_sum(sn);
;           const float rn = rsqrtf(sn * (1.f / 64.f) + EPS);
; #pragma unroll
;           for (int ds = 0; ds < 2; ++ds)
; #pragma unroll
;               for (int j = 0; j < 8; ++j) x[ds][j] *= rn * qgain[32 * ds + 8 * g4 + j];
;           if constexpr (DQK == 64) {
; #pragma unroll
;               for (int ds = 0; ds < 2; ++ds)
; #pragma unroll
;                   for (int j = 0; j < 8; ++j) {
;                       auto rr = __builtin_amdgcn_permlane32_swap(__float_as_uint(x[ds][j]), __float_as_uint(x[ds][j]), false, false);
;                       const float other = hi ? __uint_as_float(rr[0]) : __uint_as_float(rr[1]);
.LBB0_648:
	s_and_b64 vcc, exec, s[4:5]
	s_cbranch_vccz .LBB0_640
	v_mov_b32_e32 v220, v0
	v_mov_b64_e32 v[6:7], s[52:53]
	v_readfirstlane_b32 s38, v220
	s_ashr_i32 s4, s38, 6
	v_bfe_u32 v203, v220, 3, 3
	v_lshl_or_b32 v8, s4, 3, v203
	v_ashrrev_i32_e32 v2, 1, v8
	s_and_b32 s30, s4, 3
	v_and_b32_e32 v3, 1, v2
	s_lshl_b32 s5, s4, 1
	s_lshr_b32 s7, s38, 5
	v_bfe_u32 v4, v220, 2, 4
	v_and_b32_e32 v216, 7, v220
	s_and_b32 s6, s5, 2
	v_and_or_b32 v3, s7, 4, v3
	v_xor_b32_e32 v10, v2, v220
	v_add_u32_e32 v2, s40, v8
	v_lshl_or_b32 v4, s30, 4, v4
	v_bitop3_b32 v9, v3, v216, s6 bitop3:0x36
	v_ashrrev_i32_e32 v3, 31, v2
	v_and_b32_e32 v12, 3, v220
	v_or_b32_e32 v4, s40, v4
	s_lshl_b32 s4, s4, 10
	v_lshlrev_b64 v[2:3], 11, v[2:3]
	v_bitop3_b32 v11, s5, v12, 2 bitop3:0x6c
	v_ashrrev_i32_e32 v5, 31, v4
	s_add_i32 s42, s4, 0
	s_lshl_b32 s6, s30, 10
	v_mad_i64_i32 v[6:7], s[4:5], v8, s91, v[6:7]
	v_lshlrev_b64 v[4:5], 6, v[4:5]
	s_ashr_i32 s41, s40, 31
	v_lshl_add_u64 v[2:3], s[50:51], 0, v[2:3]
	v_lshlrev_b32_e32 v194, 4, v9
	s_add_i32 s5, s6, 0
	v_lshl_add_u64 v[4:5], s[28:29], 0, v[4:5]
	v_lshl_add_u64 v[6:7], s[40:41], 1, v[6:7]
	v_lshl_add_u64 v[186:187], v[2:3], 0, v[194:195]
	v_lshlrev_b32_e32 v194, 4, v11
	v_lshlrev_b32_e32 v2, 4, v10
	s_add_i32 s41, s5, 0x2000
	s_mov_b32 s5, m0
	s_mov_b32 m0, s42
	s_nop 0
	global_load_lds_dwordx4 v[186:187], off
	s_mov_b32 m0, s5
	v_lshl_add_u64 v[188:189], v[4:5], 0, v[194:195]
	v_and_b32_e32 v194, 0x70, v2
	s_mov_b32 s5, m0
	s_mov_b32 m0, s41
	s_nop 0
	global_load_lds_dwordx4 v[188:189], off
	s_mov_b32 m0, s5
	s_add_i32 s40, s42, 0x9000
	v_lshl_add_u64 v[190:191], v[6:7], 0, v[194:195]
	s_mov_b32 s5, m0
	s_mov_b32 m0, s40
	s_nop 0
	global_load_lds_dwordx4 v[190:191], off
	s_mov_b32 m0, s5
	s_mov_b64 s[6:7], 0x20000
	v_lshl_add_u64 v[2:3], v[186:187], 0, s[6:7]
	s_add_i32 s5, s42, 0x3000
	s_mov_b32 s6, m0
	s_mov_b32 m0, s5
	s_nop 0
	global_load_lds_dwordx4 v[2:3], off
	s_mov_b32 m0, s6
	v_lshl_add_u64 v[2:3], v[188:189], 0, s[60:61]
	s_add_i32 s5, s41, 0x3000
	s_mov_b32 s6, m0
	s_mov_b32 m0, s5
	s_nop 0
	global_load_lds_dwordx4 v[2:3], off
	s_mov_b32 m0, s6
	s_mov_b64 s[6:7], 0x40000
	s_lshl_b32 s4, s30, 6
	v_lshl_add_u64 v[2:3], v[186:187], 0, s[6:7]
	s_add_i32 s5, s42, 0x6000
	s_mov_b32 s6, m0
	s_mov_b32 m0, s5
	s_nop 0
	global_load_lds_dwordx4 v[2:3], off
	s_mov_b32 m0, s6
	v_and_b32_e32 v221, 15, v220
	s_mov_b64 s[6:7], 0x2000
	s_or_b32 s25, s4, s25
	v_and_b32_e32 v8, 48, v220
	v_lshl_add_u64 v[2:3], v[188:189], 0, s[6:7]
	v_or_b32_e32 v6, s25, v221
	v_mov_b32_e32 v9, v195
	s_add_i32 s5, s41, 0x6000
	s_mov_b32 s6, m0
	s_mov_b32 m0, s5
	s_nop 0
	global_load_lds_dwordx4 v[2:3], off
	s_mov_b32 m0, s6
	v_lshl_add_u64 v[2:3], s[46:47], 0, v[8:9]
	v_or_b32_e32 v7, 16, v6
	v_mad_i64_i32 v[4:5], s[4:5], v6, s90, v[2:3]
	v_mad_i64_i32 v[10:11], s[4:5], v7, s90, v[2:3]
	v_or_b32_e32 v7, 32, v6
	v_or_b32_e32 v6, 48, v6
	v_mad_i64_i32 v[22:23], s[4:5], v7, s90, v[2:3]
	v_mad_i64_i32 v[34:35], s[4:5], v6, s90, v[2:3]
	global_load_dwordx4 v[66:69], v[4:5], off offset:64 nt
	global_load_dwordx4 v[70:73], v[10:11], off offset:64 nt
	global_load_dwordx4 v[90:93], v[22:23], off offset:64 nt
	global_load_dwordx4 v[116:119], v[34:35], off offset:64 nt
	global_load_dwordx4 v[134:137], v[4:5], off nt
	global_load_dwordx4 v[140:143], v[10:11], off nt
	global_load_dwordx4 v[86:89], v[22:23], off nt
	global_load_dwordx4 v[6:9], v[34:35], off nt
	s_lshr_b32 s4, s31, 6
	v_and_b32_e32 v218, 63, v220
	v_lshlrev_b32_e32 v217, 1, v220
	s_or_b32 s4, s4, s30
	v_and_or_b32 v236, v217, 24, v12
	v_bfe_u32 v238, v220, 3, 1
	v_mov_b32_e32 v38, s4
	v_cmp_gt_u32_e32 vcc, 32, v218
	v_or_b32_e32 v24, 16, v221
	v_bfe_u32 v194, v220, 4, 2
	s_ashr_i32 s16, s38, 8
	v_bfe_u32 v239, v220, 1, 2
	v_lshlrev_b32_e32 v240, 2, v238
	v_lshl_add_u32 v237, v236, 7, 0
	v_cndmask_b32_e32 v12, v221, v38, vcc
	v_cndmask_b32_e32 v24, v24, v38, vcc
	v_lshl_add_u32 v241, s16, 12, v237
	v_bitop3_b32 v2, v240, v194, v239 bitop3:0x36
	v_lshlrev_b32_e32 v12, 6, v12
	v_lshlrev_b32_e32 v24, 6, v24
	v_lshl_add_u32 v219, v2, 4, v241
	global_load_dwordx4 v[2:5], v[4:5], off offset:128 nt
	s_nop 0
	global_load_dwordx4 v[106:109], v12, s[36:37] offset:48
	global_load_dwordx4 v[102:105], v12, s[36:37] offset:32
	global_load_dwordx4 v[18:21], v12, s[36:37] offset:16
	global_load_dwordx4 v[14:17], v12, s[36:37]
	s_nop 0
	global_load_dwordx4 v[10:13], v[10:11], off offset:128 nt
	s_nop 0
	global_load_dwordx4 v[98:101], v24, s[36:37] offset:48
	global_load_dwordx4 v[94:97], v24, s[36:37] offset:32
	global_load_dwordx4 v[30:33], v24, s[36:37] offset:16
	global_load_dwordx4 v[26:29], v24, s[36:37]
	s_nop 0
	global_load_dwordx4 v[22:25], v[22:23], off offset:128 nt
	v_or_b32_e32 v36, 32, v221
	v_or_b32_e32 v39, 48, v221
	v_cndmask_b32_e32 v36, v36, v38, vcc
	v_cndmask_b32_e32 v38, v39, v38, vcc
	v_lshlrev_b32_e32 v36, 6, v36
	v_lshlrev_b32_e32 v50, 6, v38
	v_lshlrev_b32_e32 v162, 5, v194
	global_load_dwordx4 v[82:85], v36, s[36:37] offset:48
	global_load_dwordx4 v[78:81], v36, s[36:37] offset:32
	global_load_dwordx4 v[74:77], v36, s[36:37] offset:16
	global_load_dwordx4 v[62:65], v36, s[36:37]
	s_nop 0
	global_load_dwordx4 v[34:37], v[34:35], off offset:128 nt
	s_nop 0
	global_load_dwordx4 v[38:41], v50, s[36:37] offset:48
	global_load_dwordx4 v[42:45], v50, s[36:37] offset:32
	global_load_dwordx4 v[46:49], v50, s[36:37] offset:16
	s_nop 0
	global_load_dwordx4 v[50:53], v50, s[36:37]
	s_nop 0
	global_load_dwordx4 v[54:57], v162, s[44:45] offset:144
	global_load_dwordx4 v[58:61], v162, s[44:45] offset:128
	v_and_b32_e32 v160, 16, v220
	v_cmp_eq_u32_e32 vcc, 0, v160
	s_mov_b32 s6, 0x3d000000
	s_brev_b32 s7, 60
	s_mov_b32 s4, 0x358637bd
	s_mov_b32 s7, 0x3c800000
	s_waitcnt vmcnt(26)
; template <int DQK, int DV, bool LEAD> ...
;     ...
;           float x[NDS][8];
; #pragma unroll
;           for (int ds = 0; ds < NDS; ++ds)
; #pragma unroll
;               for (int j = 0; j < 8; ++j) x[ds][j] = __uint_as_float(((unsigned)(unsigned short)raw[ds][j]) << 16);
;           const int tq = tq0 + qoff + qb * 16 + q16, prow = (tq >> 6) & 127, pcol = tq & 63;
;           float sn = 0.f;
; #pragma unroll
;           for (int ds = 0; ds < 2; ++ds)
; #pragma unroll
;               for (int j = 0; j < 8; ++j) sn += x[ds][j] * x[ds][j];
;           sn = lanes4_sum(sn);
;           const float rn = rsqrtf(sn * (1.f / 64.f) + EPS);
	v_and_b32_e32 v111, 0xffff0000, v119
	s_waitcnt vmcnt(25)
	v_and_b32_e32 v193, 0xffff0000, v134
	v_lshlrev_b32_e32 v192, 16, v134
	v_lshlrev_b32_e32 v110, 16, v119
	s_waitcnt vmcnt(22)
	v_and_b32_e32 v121, 0xffff0000, v8
	v_lshlrev_b32_e32 v120, 16, v8
	v_mul_f32_e32 v8, v193, v193
	v_and_b32_e32 v113, 0xffff0000, v118
	v_lshlrev_b32_e32 v112, 16, v118
	v_and_b32_e32 v119, 0xffff0000, v9
	v_lshlrev_b32_e32 v118, 16, v9
	v_and_b32_e32 v207, 0xffff0000, v135
	v_lshlrev_b32_e32 v206, 16, v135
	v_pk_fma_f32 v[8:9], v[192:193], v[192:193], v[8:9] op_sel_hi:[1,1,0]
	v_and_b32_e32 v181, 0xffff0000, v137
	v_lshlrev_b32_e32 v180, 16, v137
	v_and_b32_e32 v185, 0xffff0000, v136
	v_lshlrev_b32_e32 v184, 16, v136
	v_and_b32_e32 v137, 0xffff0000, v88
	v_lshlrev_b32_e32 v136, 16, v88
	v_pk_fma_f32 v[8:9], v[206:207], v[206:207], v[8:9]
	v_mul_f32_e32 v88, v207, v207
	v_pk_add_f32 v[8:9], v[88:89], v[8:9] op_sel_hi:[0,1]
	v_pk_fma_f32 v[8:9], v[184:185], v[184:185], v[8:9]
	v_mul_f32_e32 v88, v185, v185
	v_pk_add_f32 v[8:9], v[88:89], v[8:9] op_sel_hi:[0,1]
	v_pk_fma_f32 v[8:9], v[180:181], v[180:181], v[8:9]
	v_mul_f32_e32 v88, v181, v181
	v_and_b32_e32 v179, 0xffff0000, v66
	v_lshlrev_b32_e32 v178, 16, v66
	v_pk_add_f32 v[8:9], v[88:89], v[8:9] op_sel_hi:[0,1]
	v_pk_fma_f32 v[8:9], v[178:179], v[178:179], v[8:9]
	v_mul_f32_e32 v88, v179, v179
	v_and_b32_e32 v177, 0xffff0000, v67
	v_lshlrev_b32_e32 v176, 16, v67
	v_pk_add_f32 v[8:9], v[88:89], v[8:9] op_sel_hi:[0,1]
	v_pk_fma_f32 v[8:9], v[176:177], v[176:177], v[8:9]
	v_mul_f32_e32 v88, v177, v177
	v_and_b32_e32 v171, 0xffff0000, v68
	v_lshlrev_b32_e32 v170, 16, v68
	v_pk_add_f32 v[8:9], v[88:89], v[8:9] op_sel_hi:[0,1]
	v_pk_fma_f32 v[8:9], v[170:171], v[170:171], v[8:9]
	v_mul_f32_e32 v88, v171, v171
	v_and_b32_e32 v169, 0xffff0000, v69
	v_lshlrev_b32_e32 v168, 16, v69
	v_pk_add_f32 v[8:9], v[88:89], v[8:9] op_sel_hi:[0,1]
	v_pk_fma_f32 v[8:9], v[168:169], v[168:169], v[8:9]
	v_mul_f32_e32 v88, v169, v169
	v_pk_add_f32 v[8:9], v[88:89], v[8:9] op_sel_hi:[0,1]
	v_and_b32_e32 v123, 0xffff0000, v7
	v_lshlrev_b32_e32 v122, 16, v7
	v_mov_b32_e32 v7, v8
	s_nop 1
	v_permlane16_swap_b32_e32 v8, v7
	v_add_f32_e32 v7, v8, v7
	v_mov_b32_e32 v9, v7
	v_and_b32_e32 v167, 0xffff0000, v140
	s_nop 0
	v_permlane32_swap_b32_e32 v7, v9
	v_lshlrev_b32_e32 v166, 16, v140
	v_mul_f32_e32 v8, v167, v167
	v_and_b32_e32 v133, 0xffff0000, v89
	v_lshlrev_b32_e32 v132, 16, v89
	v_and_b32_e32 v159, 0xffff0000, v141
	v_lshlrev_b32_e32 v158, 16, v141
	v_pk_fma_f32 v[88:89], v[166:167], v[166:167], v[8:9] op_sel_hi:[1,1,0]
	v_mul_f32_e32 v8, v159, v159
	v_pk_fma_f32 v[88:89], v[158:159], v[158:159], v[88:89]
	v_and_b32_e32 v157, 0xffff0000, v142
	v_lshlrev_b32_e32 v156, 16, v142
	v_pk_add_f32 v[88:89], v[8:9], v[88:89] op_sel_hi:[0,1]
	v_pk_fma_f32 v[88:89], v[156:157], v[156:157], v[88:89]
	v_mul_f32_e32 v8, v157, v157
	v_and_b32_e32 v155, 0xffff0000, v143
	v_lshlrev_b32_e32 v154, 16, v143
	v_pk_add_f32 v[88:89], v[8:9], v[88:89] op_sel_hi:[0,1]
	v_pk_fma_f32 v[88:89], v[154:155], v[154:155], v[88:89]
	v_mul_f32_e32 v8, v155, v155
	v_and_b32_e32 v153, 0xffff0000, v70
	v_lshlrev_b32_e32 v152, 16, v70
	v_pk_add_f32 v[88:89], v[8:9], v[88:89] op_sel_hi:[0,1]
	v_pk_fma_f32 v[88:89], v[152:153], v[152:153], v[88:89]
	v_mul_f32_e32 v8, v153, v153
	v_and_b32_e32 v151, 0xffff0000, v71
	v_lshlrev_b32_e32 v150, 16, v71
	v_pk_add_f32 v[88:89], v[8:9], v[88:89] op_sel_hi:[0,1]
	v_pk_fma_f32 v[88:89], v[150:151], v[150:151], v[88:89]
	v_mul_f32_e32 v8, v151, v151
	v_and_b32_e32 v149, 0xffff0000, v72
	v_lshlrev_b32_e32 v148, 16, v72
	v_pk_add_f32 v[88:89], v[8:9], v[88:89] op_sel_hi:[0,1]
	v_pk_fma_f32 v[88:89], v[148:149], v[148:149], v[88:89]
	v_mul_f32_e32 v8, v149, v149
	v_and_b32_e32 v147, 0xffff0000, v73
	v_lshlrev_b32_e32 v146, 16, v73
	v_pk_add_f32 v[88:89], v[8:9], v[88:89] op_sel_hi:[0,1]
	v_pk_fma_f32 v[88:89], v[146:147], v[146:147], v[88:89]
	v_mul_f32_e32 v8, v147, v147
	v_pk_add_f32 v[88:89], v[8:9], v[88:89] op_sel_hi:[0,1]
	v_mov_b32_e32 v8, v88
	s_nop 1
	v_permlane16_swap_b32_e32 v88, v8
	v_and_b32_e32 v145, 0xffff0000, v86
	v_add_f32_e32 v173, v88, v8
	v_lshlrev_b32_e32 v144, 16, v86
	v_mul_f32_e32 v8, v145, v145
	v_and_b32_e32 v139, 0xffff0000, v87
	v_lshlrev_b32_e32 v138, 16, v87
	v_pk_fma_f32 v[86:87], v[144:145], v[144:145], v[8:9] op_sel_hi:[1,1,0]
	v_mul_f32_e32 v8, v139, v139
	v_pk_fma_f32 v[86:87], v[138:139], v[138:139], v[86:87]
	v_and_b32_e32 v131, 0xffff0000, v90
	v_pk_add_f32 v[86:87], v[8:9], v[86:87] op_sel_hi:[0,1]
	v_pk_fma_f32 v[86:87], v[136:137], v[136:137], v[86:87]
	v_mul_f32_e32 v8, v137, v137
	v_pk_add_f32 v[86:87], v[8:9], v[86:87] op_sel_hi:[0,1]
	v_pk_fma_f32 v[86:87], v[132:133], v[132:133], v[86:87]
	v_mul_f32_e32 v8, v133, v133
	v_lshlrev_b32_e32 v130, 16, v90
	v_pk_add_f32 v[86:87], v[8:9], v[86:87] op_sel_hi:[0,1]
	v_pk_fma_f32 v[86:87], v[130:131], v[130:131], v[86:87]
	v_mul_f32_e32 v8, v131, v131
	v_and_b32_e32 v129, 0xffff0000, v91
	v_lshlrev_b32_e32 v128, 16, v91
	v_pk_add_f32 v[86:87], v[8:9], v[86:87] op_sel_hi:[0,1]
	v_pk_fma_f32 v[86:87], v[128:129], v[128:129], v[86:87]
	v_mul_f32_e32 v8, v129, v129
	v_and_b32_e32 v127, 0xffff0000, v92
	v_lshlrev_b32_e32 v126, 16, v92
	v_pk_add_f32 v[86:87], v[8:9], v[86:87] op_sel_hi:[0,1]
	v_pk_fma_f32 v[86:87], v[126:127], v[126:127], v[86:87]
	v_mul_f32_e32 v8, v127, v127
	v_and_b32_e32 v125, 0xffff0000, v93
	v_lshlrev_b32_e32 v124, 16, v93
	v_pk_add_f32 v[86:87], v[8:9], v[86:87] op_sel_hi:[0,1]
	v_pk_fma_f32 v[86:87], v[124:125], v[124:125], v[86:87]
	v_mul_f32_e32 v8, v125, v125
	v_pk_add_f32 v[86:87], v[8:9], v[86:87] op_sel_hi:[0,1]
; template <int DQK, int DV, bool LEAD> ...
;     ...
;           float sn = 0.f;
; #pragma unroll
;           for (int ds = 0; ds < 2; ++ds)
; #pragma unroll
;               for (int j = 0; j < 8; ++j) sn += x[ds][j] * x[ds][j];
;           sn = lanes4_sum(sn);
;           const float rn = rsqrtf(sn * (1.f / 64.f) + EPS);
; #pragma unroll
;           for (int ds = 0; ds < 2; ++ds)
; #pragma unroll
;               for (int j = 0; j < 8; ++j) x[ds][j] *= rn * qgain[32 * ds + 8 * g4 + j];
;           if constexpr (DQK == 64) {
; #pragma unroll
;               for (int ds = 0; ds < 2; ++ds)
; #pragma unroll
;                   for (int j = 0; j < 8; ++j) {
;                       auto rr = __builtin_amdgcn_permlane32_swap(__float_as_uint(x[ds][j]), __float_as_uint(x[ds][j]), false, false);
;                       const float other = hi ? __uint_as_float(rr[0]) : __uint_as_float(rr[1]);
;                       float cc = 1.f, sg = 0.f;
;                       if (lat) { const f32x2 cs = rope[(ds ? pcol : prow) * 16 + 8 * (g4 & 1) + j]; cc = cs.x; sg = hi ? cs.y : -cs.y; }
;                       x[ds][j] = x[ds][j] * cc + other * sg; }
;           } else {
;               float sr = 0.f;
; #pragma unroll
;               for (int j = 0; j < 8; ++j) sr += x[2][j] * x[2][j];
;               sr = lanes4_sum(sr);
;               const float rq = rsqrtf(sr * (1.f / 32.f) + EPS);
; #pragma unroll
;               for (int j = 0; j < 8; ++j) { const float av = x[2][j] * rq * qgain[64 + 8 * g4 + j];
;                   auto rr = __builtin_amdgcn_permlane16_swap(__float_as_uint(av), __float_as_uint(av), false, false);
;                   const float other = (g4 & 1) ? __uint_as_float(rr[0]) : __uint_as_float(rr[1]);
;                   float cc = 1.f, sg = 0.f;
;                   if (lat) { const f32x2 cs = rope[((g4 & 2) ? pcol : prow) * 8 + j]; cc = cs.x; sg = (g4 & 1) ? cs.y : -cs.y; }
;                   x[2][j] = av * cc + other * sg; }
;           }
; #pragma unroll
;           for (int ds = 0; ds < NDS; ++ds) { u32x4 w;
; #pragma unroll
;               for (int i = 0; i < 4; ++i) w[i] = cvtpk(x[ds][2 * i] * c2, x[ds][2 * i + 1] * c2);
;               qf[qb * NDS + ds] = __builtin_bit_cast(bf16x8, w); }
	v_mov_b32_e32 v8, v86
	v_and_b32_e32 v135, 0xffff0000, v6
	s_nop 0
	v_permlane16_swap_b32_e32 v86, v8
	v_lshlrev_b32_e32 v134, 16, v6
	v_mul_f32_e32 v6, v135, v135
	v_add_f32_e32 v161, v86, v8
	v_pk_fma_f32 v[86:87], v[134:135], v[134:135], v[6:7] op_sel_hi:[1,1,0]
	v_mul_f32_e32 v6, v123, v123
	v_pk_fma_f32 v[86:87], v[122:123], v[122:123], v[86:87]
	v_and_b32_e32 v115, 0xffff0000, v117
	v_pk_add_f32 v[86:87], v[6:7], v[86:87] op_sel_hi:[0,1]
	v_pk_fma_f32 v[86:87], v[120:121], v[120:121], v[86:87]
	v_mul_f32_e32 v6, v121, v121
	v_pk_add_f32 v[86:87], v[6:7], v[86:87] op_sel_hi:[0,1]
	v_pk_fma_f32 v[86:87], v[118:119], v[118:119], v[86:87]
	v_mul_f32_e32 v6, v119, v119
	v_lshlrev_b32_e32 v114, 16, v117
	v_and_b32_e32 v117, 0xffff0000, v116
	v_lshlrev_b32_e32 v116, 16, v116
	v_pk_add_f32 v[86:87], v[6:7], v[86:87] op_sel_hi:[0,1]
	v_pk_fma_f32 v[86:87], v[116:117], v[116:117], v[86:87]
	v_mul_f32_e32 v6, v117, v117
	global_load_dwordx4 v[66:69], v162, s[44:45] offset:16
	global_load_dwordx4 v[70:73], v162, s[44:45]
	v_pk_add_f32 v[86:87], v[6:7], v[86:87] op_sel_hi:[0,1]
	v_pk_fma_f32 v[86:87], v[114:115], v[114:115], v[86:87]
	v_mul_f32_e32 v6, v115, v115
	v_pk_add_f32 v[86:87], v[6:7], v[86:87] op_sel_hi:[0,1]
	v_pk_fma_f32 v[86:87], v[112:113], v[112:113], v[86:87]
	v_mul_f32_e32 v6, v113, v113
	v_pk_add_f32 v[86:87], v[6:7], v[86:87] op_sel_hi:[0,1]
	v_pk_fma_f32 v[86:87], v[110:111], v[110:111], v[86:87]
	v_mul_f32_e32 v6, v111, v111
	v_pk_add_f32 v[86:87], v[6:7], v[86:87] op_sel_hi:[0,1]
	v_mov_b32_e32 v6, v86
	s_nop 1
	v_permlane16_swap_b32_e32 v86, v6
	v_add_f32_e32 v141, v86, v6
	global_load_dwordx4 v[86:89], v162, s[44:45] offset:272
	global_load_dwordx4 v[90:93], v162, s[44:45] offset:256
	s_waitcnt vmcnt(15)
	v_and_b32_e32 v165, 0xffff0000, v25
	v_lshlrev_b32_e32 v164, 16, v25
	v_and_b32_e32 v25, 0xffff0000, v2
	v_cndmask_b32_e64 v201, v105, -v105, vcc
	v_cndmask_b32_e64 v200, v103, -v103, vcc
	v_mov_b32_e32 v103, v104
	v_and_b32_e32 v105, 0xffff0000, v24
	v_lshlrev_b32_e32 v104, 16, v24
	v_lshlrev_b32_e32 v24, 16, v2
	v_mul_f32_e32 v2, v25, v25
	v_and_b32_e32 v205, 0xffff0000, v13
	v_lshlrev_b32_e32 v204, 16, v13
	v_and_b32_e32 v211, 0xffff0000, v12
	v_lshlrev_b32_e32 v210, 16, v12
	v_and_b32_e32 v13, 0xffff0000, v3
	v_lshlrev_b32_e32 v12, 16, v3
	v_pk_fma_f32 v[2:3], v[24:25], v[24:25], v[2:3] op_sel_hi:[1,1,0]
	v_and_b32_e32 v199, 0xffff0000, v4
	v_lshlrev_b32_e32 v198, 16, v4
	v_pk_fma_f32 v[2:3], v[12:13], v[12:13], v[2:3]
	v_mul_f32_e32 v4, v13, v13
	v_pk_add_f32 v[2:3], v[4:5], v[2:3] op_sel_hi:[0,1]
	v_pk_fma_f32 v[2:3], v[198:199], v[198:199], v[2:3]
	v_mul_f32_e32 v4, v199, v199
	v_and_b32_e32 v215, 0xffff0000, v5
	v_lshlrev_b32_e32 v214, 16, v5
	v_pk_add_f32 v[2:3], v[4:5], v[2:3] op_sel_hi:[0,1]
	v_pk_fma_f32 v[2:3], v[214:215], v[214:215], v[2:3]
	v_mul_f32_e32 v4, v215, v215
	v_pk_add_f32 v[2:3], v[4:5], v[2:3] op_sel_hi:[0,1]
	v_mov_b32_e32 v3, v2
	s_nop 1
	v_permlane16_swap_b32_e32 v2, v3
	v_add_f32_e32 v6, v2, v3
	v_mov_b32_e32 v8, v6
	s_nop 1
	v_permlane32_swap_b32_e32 v6, v8
	v_cndmask_b32_e64 v213, v109, -v109, vcc
	v_cndmask_b32_e64 v212, v107, -v107, vcc
	v_mov_b32_e32 v107, v108
	s_waitcnt vmcnt(14)
	v_cndmask_b32_e64 v109, v85, -v85, vcc
	v_cndmask_b32_e64 v108, v83, -v83, vcc
	v_mov_b32_e32 v83, v84
	s_waitcnt vmcnt(9)
	v_cndmask_b32_e64 v85, v41, -v41, vcc
	v_cndmask_b32_e64 v84, v39, -v39, vcc
	v_mov_b32_e32 v39, v40
	s_waitcnt vmcnt(8)
	v_cndmask_b32_e64 v41, v45, -v45, vcc
	v_cndmask_b32_e64 v40, v43, -v43, vcc
	v_mov_b32_e32 v43, v44
	v_pk_add_f32 v[2:3], v[6:7], v[8:9]
	v_mov_b64_e32 v[44:45], s[4:5]
	v_pk_fma_f32 v[6:7], v[2:3], s[6:7], v[44:45] op_sel_hi:[1,1,0]
	v_cndmask_b32_e64 v222, v19, -v19, vcc
	v_mul_f32_e32 v2, 0x4b800000, v7
	v_cmp_gt_f32_e64 s[4:5], s95, v7
	v_mov_b32_e32 v19, v20
	v_and_b32_e32 v229, 0xffff0000, v11
	v_cndmask_b32_e64 v2, v7, v2, s[4:5]
	v_rsq_f32_e32 v2, v2
	v_lshlrev_b32_e32 v228, 16, v11
	v_mul_f32_e32 v11, 0x4b800000, v6
	v_cndmask_b32_e64 v223, v21, -v21, vcc
	v_mul_f32_e32 v3, 0x45800000, v2
	v_cndmask_b32_e64 v20, v2, v3, s[4:5]
	s_waitcnt vmcnt(5)
	v_pk_mul_f32 v[2:3], v[20:21], v[56:57] op_sel_hi:[0,1]
	v_pk_mul_f32 v[2:3], v[2:3], v[168:169]
	v_pk_mul_f32 v[4:5], v[20:21], v[54:55] op_sel_hi:[0,1]
	v_pk_mul_f32 v[2:3], v[2:3], s[82:83] op_sel_hi:[1,0]
	v_pk_mul_f32 v[8:9], v[4:5], v[170:171]
	v_cvt_pk_bf16_f32 v5, v2, v3
	v_pk_mul_f32 v[2:3], v[8:9], s[82:83] op_sel_hi:[1,0]
	s_waitcnt vmcnt(4)
	v_pk_mul_f32 v[8:9], v[58:59], v[20:21] op_sel_hi:[1,0]
	v_cvt_pk_bf16_f32 v4, v2, v3
	v_pk_mul_f32 v[2:3], v[20:21], v[60:61] op_sel_hi:[0,1]
	v_pk_mul_f32 v[2:3], v[2:3], v[176:177]
	v_pk_mul_f32 v[8:9], v[8:9], v[178:179]
	v_pk_mul_f32 v[2:3], v[2:3], s[82:83] op_sel_hi:[1,0]
	v_pk_mul_f32 v[8:9], v[8:9], s[82:83] op_sel_hi:[1,0]
	v_cvt_pk_bf16_f32 v3, v2, v3
	v_cndmask_b32_e64 v177, v33, -v33, vcc
	v_cndmask_b32_e64 v176, v31, -v31, vcc
	v_mov_b32_e32 v31, v32
	v_cvt_pk_bf16_f32 v2, v8, v9
	s_waitcnt vmcnt(3)
	v_pk_mul_f32 v[8:9], v[68:69], v[20:21] op_sel_hi:[1,0]
	v_pk_mul_f32 v[32:33], v[66:67], v[20:21] op_sel_hi:[1,0]
	v_cmp_gt_f32_e64 s[4:5], s95, v6
	v_pk_mul_f32 v[8:9], v[8:9], v[180:181]
	v_pk_mul_f32 v[32:33], v[32:33], v[184:185]
	v_cndmask_b32_e64 v6, v6, v11, s[4:5]
	v_pk_mul_f32 v[8:9], v[8:9], s[82:83] op_sel_hi:[1,0]
	v_pk_mul_f32 v[32:33], v[32:33], s[82:83] op_sel_hi:[1,0]
	v_rsq_f32_e32 v11, v6
	v_cvt_pk_bf16_f32 v9, v8, v9
	v_cvt_pk_bf16_f32 v8, v32, v33
	s_waitcnt vmcnt(2)
; template <int DQK, int DV, bool LEAD> ...
;     ...
;           float sn = 0.f;
; #pragma unroll
;           for (int ds = 0; ds < 2; ++ds)
; #pragma unroll
;               for (int j = 0; j < 8; ++j) sn += x[ds][j] * x[ds][j];
;           sn = lanes4_sum(sn);
;           const float rn = rsqrtf(sn * (1.f / 64.f) + EPS);
; #pragma unroll
;           for (int ds = 0; ds < 2; ++ds)
; #pragma unroll
;               for (int j = 0; j < 8; ++j) x[ds][j] *= rn * qgain[32 * ds + 8 * g4 + j];
;           if constexpr (DQK == 64) {
; #pragma unroll
;               for (int ds = 0; ds < 2; ++ds)
; #pragma unroll
;                   for (int j = 0; j < 8; ++j) {
;                       auto rr = __builtin_amdgcn_permlane32_swap(__float_as_uint(x[ds][j]), __float_as_uint(x[ds][j]), false, false);
;                       const float other = hi ? __uint_as_float(rr[0]) : __uint_as_float(rr[1]);
;                       float cc = 1.f, sg = 0.f;
;                       if (lat) { const f32x2 cs = rope[(ds ? pcol : prow) * 16 + 8 * (g4 & 1) + j]; cc = cs.x; sg = hi ? cs.y : -cs.y; }
;                       x[ds][j] = x[ds][j] * cc + other * sg; }
;           } else {
;               float sr = 0.f;
; #pragma unroll
;               for (int j = 0; j < 8; ++j) sr += x[2][j] * x[2][j];
;               sr = lanes4_sum(sr);
;               const float rq = rsqrtf(sr * (1.f / 32.f) + EPS);
; #pragma unroll
;               for (int j = 0; j < 8; ++j) { const float av = x[2][j] * rq * qgain[64 + 8 * g4 + j];
;                   auto rr = __builtin_amdgcn_permlane16_swap(__float_as_uint(av), __float_as_uint(av), false, false);
;                   const float other = (g4 & 1) ? __uint_as_float(rr[0]) : __uint_as_float(rr[1]);
;                   float cc = 1.f, sg = 0.f;
;                   if (lat) { const f32x2 cs = rope[((g4 & 2) ? pcol : prow) * 8 + j]; cc = cs.x; sg = (g4 & 1) ? cs.y : -cs.y; }
;                   x[2][j] = av * cc + other * sg; }
;           }
; #pragma unroll
;           for (int ds = 0; ds < NDS; ++ds) { u32x4 w;
; #pragma unroll
;               for (int i = 0; i < 4; ++i) w[i] = cvtpk(x[ds][2 * i] * c2, x[ds][2 * i + 1] * c2);
;               qf[qb * NDS + ds] = __builtin_bit_cast(bf16x8, w); }
	v_pk_mul_f32 v[32:33], v[72:73], v[20:21] op_sel_hi:[1,0]
	v_pk_mul_f32 v[20:21], v[70:71], v[20:21] op_sel_hi:[1,0]
	v_pk_mul_f32 v[32:33], v[32:33], v[206:207]
	v_pk_mul_f32 v[20:21], v[20:21], v[192:193]
	v_pk_mul_f32 v[32:33], v[32:33], s[82:83] op_sel_hi:[1,0]
	v_pk_mul_f32 v[20:21], v[20:21], s[82:83] op_sel_hi:[1,0]
	v_cvt_pk_bf16_f32 v7, v32, v33
	v_cvt_pk_bf16_f32 v6, v20, v21
	v_mul_f32_e32 v20, 0x45800000, v11
	v_cndmask_b32_e64 v20, v11, v20, s[4:5]
	v_pk_mul_f32 v[32:33], v[20:21], v[12:13] op_sel_hi:[0,1]
	v_pk_mul_f32 v[12:13], v[20:21], v[214:215] op_sel_hi:[0,1]
	s_waitcnt vmcnt(1)
	v_pk_mul_f32 v[12:13], v[12:13], v[88:89]
	v_cndmask_b32_e64 v183, v101, -v101, vcc
	v_cndmask_b32_e64 v182, v99, -v99, vcc
	v_mov_b32_e32 v99, v100
	v_and_b32_e32 v101, 0xffff0000, v37
	v_lshlrev_b32_e32 v100, 16, v37
	v_cndmask_b32_e64 v209, v97, -v97, vcc
	v_cndmask_b32_e64 v208, v95, -v95, vcc
	v_mov_b32_e32 v95, v96
	v_cndmask_b32_e64 v97, v81, -v81, vcc
	v_cndmask_b32_e64 v96, v79, -v79, vcc
	v_mov_b32_e32 v79, v80
	v_and_b32_e32 v81, 0xffff0000, v36
	v_lshlrev_b32_e32 v80, 16, v36
	v_and_b32_e32 v37, 0xffff0000, v23
	v_lshlrev_b32_e32 v36, 16, v23
	v_pk_mul_f32 v[24:25], v[20:21], v[24:25] op_sel_hi:[0,1]
	v_pk_mul_f32 v[178:179], v[20:21], v[198:199] op_sel_hi:[0,1]
	v_mov_b32_e32 v11, v12
	v_mov_b32_e32 v20, v12
	v_mov_b32_e32 v21, v13
	v_mov_b32_e32 v23, v13
	v_permlane16_swap_b32_e32 v11, v20
	s_nop 0
	v_permlane16_swap_b32_e32 v21, v23
	v_cndmask_b32_e32 v21, v21, v23, vcc
	v_cndmask_b32_e32 v20, v11, v20, vcc
	v_pk_mul_f32 v[20:21], v[212:213], v[20:21]
	v_cndmask_b32_e64 v169, v49, -v49, vcc
	v_pk_fma_f32 v[12:13], v[12:13], v[106:107], v[20:21]
	v_pk_mul_f32 v[20:21], v[178:179], v[86:87]
	v_pk_mul_f32 v[12:13], v[12:13], s[82:83] op_sel_hi:[1,0]
	v_cndmask_b32_e64 v168, v47, -v47, vcc
	v_mov_b32_e32 v47, v48
	v_cndmask_b32_e64 v49, v17, -v17, vcc
	v_cndmask_b32_e64 v48, v15, -v15, vcc
	v_cvt_pk_bf16_f32 v13, v12, v13
	v_mov_b32_e32 v11, v20
	v_mov_b32_e32 v12, v20
	v_mov_b32_e32 v15, v21
	v_mov_b32_e32 v17, v21
	v_permlane16_swap_b32_e32 v11, v12
	s_nop 0
	v_permlane16_swap_b32_e32 v15, v17
	v_cndmask_b32_e32 v107, v15, v17, vcc
	v_cndmask_b32_e32 v106, v11, v12, vcc
	v_pk_mul_f32 v[106:107], v[200:201], v[106:107]
	v_mov_b32_e32 v175, v173
	v_pk_fma_f32 v[20:21], v[20:21], v[102:103], v[106:107]
	s_nop 0
	v_permlane32_swap_b32_e32 v173, v175
	v_pk_mul_f32 v[20:21], v[20:21], s[82:83] op_sel_hi:[1,0]
	v_cndmask_b32_e64 v171, v77, -v77, vcc
	v_cvt_pk_bf16_f32 v12, v20, v21
	s_waitcnt vmcnt(0)
	v_pk_mul_f32 v[20:21], v[92:93], v[32:33]
	v_cndmask_b32_e64 v170, v75, -v75, vcc
	v_mov_b32_e32 v11, v20
	v_mov_b32_e32 v15, v20
	v_mov_b32_e32 v17, v21
	v_mov_b32_e32 v23, v21
	v_permlane16_swap_b32_e32 v11, v15
	s_nop 0
	v_permlane16_swap_b32_e32 v17, v23
	v_cndmask_b32_e32 v33, v17, v23, vcc
	v_cndmask_b32_e32 v32, v11, v15, vcc
	v_pk_mul_f32 v[32:33], v[222:223], v[32:33]
	v_mov_b32_e32 v75, v76
	v_pk_fma_f32 v[18:19], v[18:19], v[20:21], v[32:33]
	v_cndmask_b32_e64 v32, v27, -v27, vcc
	v_pk_mul_f32 v[18:19], v[18:19], s[82:83] op_sel_hi:[1,0]
	v_and_b32_e32 v77, 0xffff0000, v35
	v_cvt_pk_bf16_f32 v11, v18, v19
	v_pk_mul_f32 v[18:19], v[90:91], v[24:25]
	v_and_b32_e32 v25, 0xffff0000, v10
	v_mov_b32_e32 v15, v18
	v_mov_b32_e32 v17, v18
	v_mov_b32_e32 v20, v19
	v_mov_b32_e32 v21, v19
	v_permlane16_swap_b32_e32 v15, v17
	s_nop 0
	v_permlane16_swap_b32_e32 v20, v21
	v_lshlrev_b32_e32 v24, 16, v10
	v_mul_f32_e32 v10, v25, v25
	v_cndmask_b32_e32 v21, v20, v21, vcc
	v_cndmask_b32_e32 v20, v15, v17, vcc
	v_mov_b32_e32 v15, v16
	v_pk_fma_f32 v[16:17], v[24:25], v[24:25], v[10:11] op_sel_hi:[1,1,0]
	v_mul_f32_e32 v10, v229, v229
	v_pk_fma_f32 v[16:17], v[228:229], v[228:229], v[16:17]
	v_pk_mul_f32 v[14:15], v[14:15], v[18:19]
	v_pk_add_f32 v[16:17], v[10:11], v[16:17] op_sel_hi:[0,1]
	v_pk_fma_f32 v[16:17], v[210:211], v[210:211], v[16:17]
	v_mul_f32_e32 v10, v211, v211
	v_pk_add_f32 v[16:17], v[10:11], v[16:17] op_sel_hi:[0,1]
	v_pk_fma_f32 v[16:17], v[204:205], v[204:205], v[16:17]
	v_mul_f32_e32 v10, v205, v205
	v_pk_add_f32 v[16:17], v[10:11], v[16:17] op_sel_hi:[0,1]
	v_mov_b32_e32 v10, v16
	s_nop 1
	v_permlane16_swap_b32_e32 v16, v10
	v_add_f32_e32 v172, v16, v10
	v_mov_b32_e32 v174, v172
	s_nop 1
	v_permlane32_swap_b32_e32 v172, v174
	v_pk_add_f32 v[16:17], v[172:173], v[174:175]
	v_pk_fma_f32 v[14:15], v[48:49], v[20:21], v[14:15]
	v_pk_fma_f32 v[18:19], v[16:17], s[6:7], v[44:45] op_sel_hi:[1,1,0]
	v_pk_mul_f32 v[14:15], v[14:15], s[82:83] op_sel_hi:[1,0]
	v_mul_f32_e32 v10, 0x4b800000, v19
	v_cmp_gt_f32_e64 s[4:5], s95, v19
	v_mul_f32_e32 v23, 0x4b800000, v18
	v_lshlrev_b32_e32 v76, 16, v35
	v_cndmask_b32_e64 v10, v19, v10, s[4:5]
	v_rsq_f32_e32 v16, v10
	v_cvt_pk_bf16_f32 v10, v14, v15
	v_cndmask_b32_e64 v33, v29, -v29, vcc
	v_mov_b32_e32 v163, v161
	v_mul_f32_e32 v14, 0x45800000, v16
	v_cndmask_b32_e64 v48, v16, v14, s[4:5]
	v_pk_mul_f32 v[14:15], v[56:57], v[48:49] op_sel_hi:[1,0]
	v_pk_mul_f32 v[20:21], v[58:59], v[48:49] op_sel_hi:[1,0]
	v_pk_mul_f32 v[14:15], v[14:15], v[146:147]
	v_pk_mul_f32 v[20:21], v[20:21], v[152:153]
	v_pk_mul_f32 v[14:15], v[14:15], s[82:83] op_sel_hi:[1,0]
	v_pk_mul_f32 v[20:21], v[20:21], s[82:83] op_sel_hi:[1,0]
	v_cvt_pk_bf16_f32 v17, v14, v15
	v_pk_mul_f32 v[14:15], v[54:55], v[48:49] op_sel_hi:[1,0]
	v_cmp_gt_f32_e64 s[4:5], s95, v18
	v_pk_mul_f32 v[14:15], v[14:15], v[148:149]
	v_pk_mul_f32 v[102:103], v[66:67], v[48:49] op_sel_hi:[1,0]
	v_pk_mul_f32 v[14:15], v[14:15], s[82:83] op_sel_hi:[1,0]
	v_cndmask_b32_e64 v18, v18, v23, s[4:5]
	v_cvt_pk_bf16_f32 v16, v14, v15
; template <int DQK, int DV, bool LEAD> ...
;     ...
;           float sn = 0.f;
; #pragma unroll
;           for (int ds = 0; ds < 2; ++ds)
; #pragma unroll
;               for (int j = 0; j < 8; ++j) sn += x[ds][j] * x[ds][j];
;           sn = lanes4_sum(sn);
;           const float rn = rsqrtf(sn * (1.f / 64.f) + EPS);
; #pragma unroll
;           for (int ds = 0; ds < 2; ++ds)
; #pragma unroll
;               for (int j = 0; j < 8; ++j) x[ds][j] *= rn * qgain[32 * ds + 8 * g4 + j];
;           if constexpr (DQK == 64) {
; #pragma unroll
;               for (int ds = 0; ds < 2; ++ds)
; #pragma unroll
;                   for (int j = 0; j < 8; ++j) {
;                       auto rr = __builtin_amdgcn_permlane32_swap(__float_as_uint(x[ds][j]), __float_as_uint(x[ds][j]), false, false);
;                       const float other = hi ? __uint_as_float(rr[0]) : __uint_as_float(rr[1]);
;                       float cc = 1.f, sg = 0.f;
;                       if (lat) { const f32x2 cs = rope[(ds ? pcol : prow) * 16 + 8 * (g4 & 1) + j]; cc = cs.x; sg = hi ? cs.y : -cs.y; }
;                       x[ds][j] = x[ds][j] * cc + other * sg; }
;           } else {
;               float sr = 0.f;
; #pragma unroll
;               for (int j = 0; j < 8; ++j) sr += x[2][j] * x[2][j];
;               sr = lanes4_sum(sr);
;               const float rq = rsqrtf(sr * (1.f / 32.f) + EPS);
; #pragma unroll
;               for (int j = 0; j < 8; ++j) { const float av = x[2][j] * rq * qgain[64 + 8 * g4 + j];
;                   auto rr = __builtin_amdgcn_permlane16_swap(__float_as_uint(av), __float_as_uint(av), false, false);
;                   const float other = (g4 & 1) ? __uint_as_float(rr[0]) : __uint_as_float(rr[1]);
;                   float cc = 1.f, sg = 0.f;
;                   if (lat) { const f32x2 cs = rope[((g4 & 2) ? pcol : prow) * 8 + j]; cc = cs.x; sg = (g4 & 1) ? cs.y : -cs.y; }
;                   x[2][j] = av * cc + other * sg; }
;           }
; #pragma unroll
;           for (int ds = 0; ds < NDS; ++ds) { u32x4 w;
; #pragma unroll
;               for (int i = 0; i < 4; ++i) w[i] = cvtpk(x[ds][2 * i] * c2, x[ds][2 * i + 1] * c2);
;               qf[qb * NDS + ds] = __builtin_bit_cast(bf16x8, w); }
	v_pk_mul_f32 v[14:15], v[60:61], v[48:49] op_sel_hi:[1,0]
	v_pk_mul_f32 v[102:103], v[102:103], v[156:157]
	v_pk_mul_f32 v[14:15], v[14:15], v[150:151]
	v_rsq_f32_e32 v23, v18
	v_pk_mul_f32 v[14:15], v[14:15], s[82:83] op_sel_hi:[1,0]
	v_pk_mul_f32 v[102:103], v[102:103], s[82:83] op_sel_hi:[1,0]
	v_cvt_pk_bf16_f32 v15, v14, v15
	v_cvt_pk_bf16_f32 v14, v20, v21
	v_pk_mul_f32 v[20:21], v[68:69], v[48:49] op_sel_hi:[1,0]
	v_mul_f32_e32 v27, 0x45800000, v23
	v_pk_mul_f32 v[20:21], v[20:21], v[154:155]
	v_permlane32_swap_b32_e32 v161, v163
	v_pk_mul_f32 v[20:21], v[20:21], s[82:83] op_sel_hi:[1,0]
	v_mov_b32_e32 v143, v141
	v_cvt_pk_bf16_f32 v21, v20, v21
	v_cvt_pk_bf16_f32 v20, v102, v103
	v_pk_mul_f32 v[102:103], v[72:73], v[48:49] op_sel_hi:[1,0]
	v_pk_mul_f32 v[48:49], v[70:71], v[48:49] op_sel_hi:[1,0]
	v_pk_mul_f32 v[102:103], v[102:103], v[158:159]
	v_pk_mul_f32 v[48:49], v[48:49], v[166:167]
	v_pk_mul_f32 v[102:103], v[102:103], s[82:83] op_sel_hi:[1,0]
	v_pk_mul_f32 v[48:49], v[48:49], s[82:83] op_sel_hi:[1,0]
	v_cvt_pk_bf16_f32 v19, v102, v103
	v_cvt_pk_bf16_f32 v18, v48, v49
	v_cndmask_b32_e64 v48, v23, v27, s[4:5]
	v_pk_mul_f32 v[102:103], v[48:49], v[24:25] op_sel_hi:[0,1]
	v_pk_mul_f32 v[24:25], v[48:49], v[204:205] op_sel_hi:[0,1]
	v_pk_mul_f32 v[24:25], v[88:89], v[24:25]
	v_pk_mul_f32 v[106:107], v[48:49], v[228:229] op_sel_hi:[0,1]
	v_mov_b32_e32 v23, v24
	v_mov_b32_e32 v27, v24
	v_mov_b32_e32 v29, v25
	v_mov_b32_e32 v35, v25
	v_permlane16_swap_b32_e32 v23, v27
	s_nop 0
	v_permlane16_swap_b32_e32 v29, v35
	v_pk_mul_f32 v[146:147], v[48:49], v[210:211] op_sel_hi:[0,1]
	v_cndmask_b32_e32 v49, v29, v35, vcc
	v_cndmask_b32_e32 v48, v23, v27, vcc
	v_pk_mul_f32 v[48:49], v[182:183], v[48:49]
	v_permlane32_swap_b32_e32 v141, v143
	v_pk_fma_f32 v[24:25], v[24:25], v[98:99], v[48:49]
	v_pk_mul_f32 v[48:49], v[86:87], v[146:147]
	v_pk_mul_f32 v[24:25], v[24:25], s[82:83] op_sel_hi:[1,0]
	v_mov_b32_e32 v23, v48
	v_cvt_pk_bf16_f32 v25, v24, v25
	v_mov_b32_e32 v24, v48
	v_mov_b32_e32 v27, v49
	v_mov_b32_e32 v29, v49
	v_permlane16_swap_b32_e32 v23, v24
	s_nop 0
	v_permlane16_swap_b32_e32 v27, v29
	v_cndmask_b32_e32 v99, v27, v29, vcc
	v_cndmask_b32_e32 v98, v23, v24, vcc
	v_pk_mul_f32 v[98:99], v[208:209], v[98:99]
	s_nop 0
	v_pk_fma_f32 v[48:49], v[94:95], v[48:49], v[98:99]
	v_or_b32_e32 v206, 4, v194
	v_pk_mul_f32 v[48:49], v[48:49], s[82:83] op_sel_hi:[1,0]
	v_lshlrev_b32_e32 v207, 7, v221
	v_cvt_pk_bf16_f32 v24, v48, v49
	v_pk_mul_f32 v[48:49], v[92:93], v[106:107]
	v_lshrrev_b32_e32 v106, 1, v220
	v_mov_b32_e32 v23, v48
	v_mov_b32_e32 v27, v48
	v_mov_b32_e32 v29, v49
	v_mov_b32_e32 v35, v49
	v_permlane16_swap_b32_e32 v23, v27
	s_nop 0
	v_permlane16_swap_b32_e32 v29, v35
	v_cndmask_b32_e32 v95, v29, v35, vcc
	v_cndmask_b32_e32 v94, v23, v27, vcc
	v_pk_mul_f32 v[30:31], v[30:31], v[48:49]
	s_nop 0
	v_pk_fma_f32 v[30:31], v[176:177], v[94:95], v[30:31]
	v_cndmask_b32_e64 v94, v63, -v63, vcc
	v_pk_mul_f32 v[30:31], v[30:31], s[82:83] op_sel_hi:[1,0]
	v_cndmask_b32_e64 v95, v65, -v65, vcc
	v_cvt_pk_bf16_f32 v23, v30, v31
	v_pk_mul_f32 v[30:31], v[90:91], v[102:103]
	s_nop 0
	v_mov_b32_e32 v27, v30
	v_mov_b32_e32 v29, v30
	v_mov_b32_e32 v35, v31
	v_mov_b32_e32 v48, v31
	v_permlane16_swap_b32_e32 v27, v29
	s_nop 0
	v_permlane16_swap_b32_e32 v35, v48
	v_cndmask_b32_e32 v49, v35, v48, vcc
	v_cndmask_b32_e32 v48, v27, v29, vcc
	v_mov_b32_e32 v27, v28
	v_pk_mul_f32 v[26:27], v[26:27], v[30:31]
	s_nop 0
	v_pk_fma_f32 v[26:27], v[32:33], v[48:49], v[26:27]
	v_and_b32_e32 v49, 0xffff0000, v22
	v_lshlrev_b32_e32 v48, 16, v22
	v_mul_f32_e32 v22, v49, v49
	v_pk_fma_f32 v[28:29], v[48:49], v[48:49], v[22:23] op_sel_hi:[1,1,0]
	v_mul_f32_e32 v22, v37, v37
	v_pk_fma_f32 v[28:29], v[36:37], v[36:37], v[28:29]
	v_pk_mul_f32 v[26:27], v[26:27], s[82:83] op_sel_hi:[1,0]
	v_pk_add_f32 v[28:29], v[22:23], v[28:29] op_sel_hi:[0,1]
	v_pk_fma_f32 v[28:29], v[104:105], v[104:105], v[28:29]
	v_mul_f32_e32 v22, v105, v105
	v_pk_add_f32 v[28:29], v[22:23], v[28:29] op_sel_hi:[0,1]
	v_pk_fma_f32 v[28:29], v[164:165], v[164:165], v[28:29]
	v_mul_f32_e32 v22, v165, v165
	v_pk_add_f32 v[28:29], v[22:23], v[28:29] op_sel_hi:[0,1]
	v_mov_b32_e32 v22, v28
	s_nop 1
	v_permlane16_swap_b32_e32 v28, v22
	v_add_f32_e32 v160, v28, v22
	v_mov_b32_e32 v162, v160
	s_nop 1
	v_permlane32_swap_b32_e32 v160, v162
	v_pk_add_f32 v[28:29], v[160:161], v[162:163]
	s_nop 0
	v_pk_fma_f32 v[30:31], v[28:29], s[6:7], v[44:45] op_sel_hi:[1,1,0]
	s_nop 0
	v_mul_f32_e32 v22, 0x4b800000, v31
	v_cmp_gt_f32_e64 s[4:5], s95, v31
	v_mul_f32_e32 v35, 0x4b800000, v30
	s_nop 0
	v_cndmask_b32_e64 v22, v31, v22, s[4:5]
	v_rsq_f32_e32 v28, v22
	v_cvt_pk_bf16_f32 v22, v26, v27
	v_mul_f32_e32 v26, 0x45800000, v28
	v_cndmask_b32_e64 v98, v28, v26, s[4:5]
	v_pk_mul_f32 v[26:27], v[56:57], v[98:99] op_sel_hi:[1,0]
	v_pk_mul_f32 v[32:33], v[58:59], v[98:99] op_sel_hi:[1,0]
	v_pk_mul_f32 v[26:27], v[26:27], v[124:125]
	v_pk_mul_f32 v[32:33], v[32:33], v[130:131]
	v_pk_mul_f32 v[26:27], v[26:27], s[82:83] op_sel_hi:[1,0]
	v_pk_mul_f32 v[32:33], v[32:33], s[82:83] op_sel_hi:[1,0]
	v_cvt_pk_bf16_f32 v29, v26, v27
	v_pk_mul_f32 v[26:27], v[54:55], v[98:99] op_sel_hi:[1,0]
	v_cmp_gt_f32_e64 s[4:5], s95, v30
	v_pk_mul_f32 v[26:27], v[26:27], v[126:127]
	v_pk_mul_f32 v[102:103], v[66:67], v[98:99] op_sel_hi:[1,0]
	v_pk_mul_f32 v[26:27], v[26:27], s[82:83] op_sel_hi:[1,0]
	v_cndmask_b32_e64 v30, v30, v35, s[4:5]
	v_cvt_pk_bf16_f32 v28, v26, v27
	v_pk_mul_f32 v[26:27], v[60:61], v[98:99] op_sel_hi:[1,0]
	v_pk_mul_f32 v[102:103], v[102:103], v[136:137]
	v_pk_mul_f32 v[26:27], v[26:27], v[128:129]
	v_rsq_f32_e32 v35, v30
; template <int DQK, int DV, bool LEAD> ...
;     ...
;           float sn = 0.f;
; #pragma unroll
;           for (int ds = 0; ds < 2; ++ds)
; #pragma unroll
;               for (int j = 0; j < 8; ++j) sn += x[ds][j] * x[ds][j];
;           sn = lanes4_sum(sn);
;           const float rn = rsqrtf(sn * (1.f / 64.f) + EPS);
; #pragma unroll
;           for (int ds = 0; ds < 2; ++ds)
; #pragma unroll
;               for (int j = 0; j < 8; ++j) x[ds][j] *= rn * qgain[32 * ds + 8 * g4 + j];
;           if constexpr (DQK == 64) {
; #pragma unroll
;               for (int ds = 0; ds < 2; ++ds)
; #pragma unroll
;                   for (int j = 0; j < 8; ++j) {
;                       auto rr = __builtin_amdgcn_permlane32_swap(__float_as_uint(x[ds][j]), __float_as_uint(x[ds][j]), false, false);
;                       const float other = hi ? __uint_as_float(rr[0]) : __uint_as_float(rr[1]);
;                       float cc = 1.f, sg = 0.f;
;                       if (lat) { const f32x2 cs = rope[(ds ? pcol : prow) * 16 + 8 * (g4 & 1) + j]; cc = cs.x; sg = hi ? cs.y : -cs.y; }
;                       x[ds][j] = x[ds][j] * cc + other * sg; }
;           } else {
;               float sr = 0.f;
; #pragma unroll
;               for (int j = 0; j < 8; ++j) sr += x[2][j] * x[2][j];
;               sr = lanes4_sum(sr);
;               const float rq = rsqrtf(sr * (1.f / 32.f) + EPS);
; #pragma unroll
;               for (int j = 0; j < 8; ++j) { const float av = x[2][j] * rq * qgain[64 + 8 * g4 + j];
;                   auto rr = __builtin_amdgcn_permlane16_swap(__float_as_uint(av), __float_as_uint(av), false, false);
;                   const float other = (g4 & 1) ? __uint_as_float(rr[0]) : __uint_as_float(rr[1]);
;                   float cc = 1.f, sg = 0.f;
;                   if (lat) { const f32x2 cs = rope[((g4 & 2) ? pcol : prow) * 8 + j]; cc = cs.x; sg = (g4 & 1) ? cs.y : -cs.y; }
;                   x[2][j] = av * cc + other * sg; }
;           }
; #pragma unroll
;           for (int ds = 0; ds < NDS; ++ds) { u32x4 w;
; #pragma unroll
;               for (int i = 0; i < 4; ++i) w[i] = cvtpk(x[ds][2 * i] * c2, x[ds][2 * i + 1] * c2);
;               qf[qb * NDS + ds] = __builtin_bit_cast(bf16x8, w); }
	v_pk_mul_f32 v[26:27], v[26:27], s[82:83] op_sel_hi:[1,0]
	v_pk_mul_f32 v[102:103], v[102:103], s[82:83] op_sel_hi:[1,0]
	v_cvt_pk_bf16_f32 v27, v26, v27
	v_cvt_pk_bf16_f32 v26, v32, v33
	v_pk_mul_f32 v[32:33], v[68:69], v[98:99] op_sel_hi:[1,0]
	v_mul_f32_e32 v63, 0x45800000, v35
	v_pk_mul_f32 v[32:33], v[32:33], v[132:133]
	s_nop 0
	v_pk_mul_f32 v[32:33], v[32:33], s[82:83] op_sel_hi:[1,0]
	s_nop 0
	v_cvt_pk_bf16_f32 v33, v32, v33
	v_cvt_pk_bf16_f32 v32, v102, v103
	v_pk_mul_f32 v[102:103], v[72:73], v[98:99] op_sel_hi:[1,0]
	v_pk_mul_f32 v[98:99], v[70:71], v[98:99] op_sel_hi:[1,0]
	v_pk_mul_f32 v[102:103], v[102:103], v[138:139]
	v_pk_mul_f32 v[98:99], v[98:99], v[144:145]
	v_pk_mul_f32 v[102:103], v[102:103], s[82:83] op_sel_hi:[1,0]
	v_pk_mul_f32 v[98:99], v[98:99], s[82:83] op_sel_hi:[1,0]
	v_cvt_pk_bf16_f32 v31, v102, v103
	v_cvt_pk_bf16_f32 v30, v98, v99
	v_cndmask_b32_e64 v98, v35, v63, s[4:5]
	v_pk_mul_f32 v[102:103], v[98:99], v[36:37] op_sel_hi:[0,1]
	v_pk_mul_f32 v[36:37], v[98:99], v[164:165] op_sel_hi:[0,1]
	v_pk_mul_f32 v[36:37], v[88:89], v[36:37]
	v_pk_mul_f32 v[48:49], v[98:99], v[48:49] op_sel_hi:[0,1]
	v_pk_mul_f32 v[104:105], v[98:99], v[104:105] op_sel_hi:[0,1]
	v_mov_b32_e32 v35, v36
	v_mov_b32_e32 v63, v36
	v_mov_b32_e32 v65, v37
	v_mov_b32_e32 v98, v37
	v_permlane16_swap_b32_e32 v35, v63
	s_nop 0
	v_permlane16_swap_b32_e32 v65, v98
	v_cndmask_b32_e32 v99, v65, v98, vcc
	v_cndmask_b32_e32 v98, v35, v63, vcc
	v_pk_mul_f32 v[98:99], v[108:109], v[98:99]
	v_pk_mul_f32 v[48:49], v[90:91], v[48:49]
	v_pk_fma_f32 v[36:37], v[36:37], v[82:83], v[98:99]
	v_pk_mul_f32 v[82:83], v[86:87], v[104:105]
	v_pk_mul_f32 v[36:37], v[36:37], s[82:83] op_sel_hi:[1,0]
	v_mov_b32_e32 v35, v82
	v_cvt_pk_bf16_f32 v37, v36, v37
	v_mov_b32_e32 v36, v82
	v_mov_b32_e32 v63, v83
	v_mov_b32_e32 v65, v83
	v_permlane16_swap_b32_e32 v35, v36
	s_nop 0
	v_permlane16_swap_b32_e32 v63, v65
	v_cndmask_b32_e32 v99, v63, v65, vcc
	v_cndmask_b32_e32 v98, v35, v36, vcc
	v_pk_mul_f32 v[96:97], v[96:97], v[98:99]
	s_nop 0
	v_pk_fma_f32 v[78:79], v[78:79], v[82:83], v[96:97]
	s_nop 0
	v_pk_mul_f32 v[78:79], v[78:79], s[82:83] op_sel_hi:[1,0]
	s_nop 0
	v_cvt_pk_bf16_f32 v36, v78, v79
	v_pk_mul_f32 v[78:79], v[92:93], v[102:103]
	s_nop 0
	v_mov_b32_e32 v35, v78
	v_mov_b32_e32 v63, v78
	v_mov_b32_e32 v65, v79
	v_mov_b32_e32 v82, v79
	v_permlane16_swap_b32_e32 v35, v63
	s_nop 0
	v_permlane16_swap_b32_e32 v65, v82
	v_cndmask_b32_e32 v83, v65, v82, vcc
	v_cndmask_b32_e32 v82, v35, v63, vcc
	v_pk_mul_f32 v[74:75], v[74:75], v[78:79]
	v_mov_b32_e32 v63, v48
	v_pk_fma_f32 v[74:75], v[170:171], v[82:83], v[74:75]
	v_mov_b32_e32 v65, v48
	v_pk_mul_f32 v[74:75], v[74:75], s[82:83] op_sel_hi:[1,0]
	s_nop 0
	v_permlane16_swap_b32_e32 v63, v65
	v_cvt_pk_bf16_f32 v35, v74, v75
	v_mov_b32_e32 v74, v49
	v_mov_b32_e32 v75, v49
	s_nop 1
	v_permlane16_swap_b32_e32 v74, v75
	v_cndmask_b32_e32 v75, v74, v75, vcc
	v_cndmask_b32_e32 v74, v63, v65, vcc
	v_mov_b32_e32 v63, v64
	v_pk_mul_f32 v[48:49], v[62:63], v[48:49]
	v_and_b32_e32 v63, 0xffff0000, v34
	v_lshlrev_b32_e32 v62, 16, v34
	v_mul_f32_e32 v34, v63, v63
	v_pk_fma_f32 v[64:65], v[62:63], v[62:63], v[34:35] op_sel_hi:[1,1,0]
	v_mul_f32_e32 v34, v77, v77
	v_pk_fma_f32 v[64:65], v[76:77], v[76:77], v[64:65]
	v_pk_fma_f32 v[48:49], v[94:95], v[74:75], v[48:49]
	v_pk_add_f32 v[64:65], v[34:35], v[64:65] op_sel_hi:[0,1]
	v_pk_fma_f32 v[64:65], v[80:81], v[80:81], v[64:65]
	v_mul_f32_e32 v34, v81, v81
	v_pk_add_f32 v[64:65], v[34:35], v[64:65] op_sel_hi:[0,1]
	v_pk_fma_f32 v[64:65], v[100:101], v[100:101], v[64:65]
	v_mul_f32_e32 v34, v101, v101
	v_pk_add_f32 v[64:65], v[34:35], v[64:65] op_sel_hi:[0,1]
	v_mov_b32_e32 v34, v64
	s_nop 1
	v_permlane16_swap_b32_e32 v64, v34
	v_add_f32_e32 v140, v64, v34
	v_mov_b32_e32 v142, v140
	s_nop 1
	v_permlane32_swap_b32_e32 v140, v142
	v_pk_add_f32 v[64:65], v[140:141], v[142:143]
	v_pk_mul_f32 v[48:49], v[48:49], s[82:83] op_sel_hi:[1,0]
	v_pk_fma_f32 v[44:45], v[64:65], s[6:7], v[44:45] op_sel_hi:[1,1,0]
	v_lshlrev_b32_e32 v78, 5, v238
	v_mul_f32_e32 v34, 0x4b800000, v45
	v_cmp_gt_f32_e64 s[4:5], s95, v45
	v_lshlrev_b32_e32 v79, 6, v236
	v_bitop3_b32 v78, v78, v220, 48 bitop3:0x78
	v_cndmask_b32_e64 v34, v45, v34, s[4:5]
	v_rsq_f32_e32 v45, v34
	v_cvt_pk_bf16_f32 v34, v48, v49
	v_cndmask_b32_e64 v48, v51, -v51, vcc
	v_cndmask_b32_e64 v49, v53, -v53, vcc
	v_mul_f32_e32 v51, 0x45800000, v45
	v_cndmask_b32_e64 v64, v45, v51, s[4:5]
	v_mul_f32_e32 v45, 0x4b800000, v44
	v_cmp_gt_f32_e64 s[4:5], s95, v44
	v_pk_mul_f32 v[58:59], v[58:59], v[64:65] op_sel_hi:[1,0]
	v_pk_mul_f32 v[60:61], v[60:61], v[64:65] op_sel_hi:[1,0]
	v_cndmask_b32_e64 v44, v44, v45, s[4:5]
	v_pk_mul_f32 v[54:55], v[54:55], v[64:65] op_sel_hi:[1,0]
	v_rsq_f32_e32 v51, v44
	v_pk_mul_f32 v[58:59], v[58:59], v[116:117]
	v_pk_mul_f32 v[60:61], v[60:61], v[114:115]
	v_pk_mul_f32 v[74:75], v[54:55], v[112:113]
	v_pk_mul_f32 v[54:55], v[56:57], v[64:65] op_sel_hi:[1,0]
	v_pk_mul_f32 v[70:71], v[70:71], v[64:65] op_sel_hi:[1,0]
	v_pk_mul_f32 v[72:73], v[72:73], v[64:65] op_sel_hi:[1,0]
	v_pk_mul_f32 v[66:67], v[66:67], v[64:65] op_sel_hi:[1,0]
	v_pk_mul_f32 v[68:69], v[68:69], v[64:65] op_sel_hi:[1,0]
	v_pk_mul_f32 v[64:65], v[54:55], v[110:111]
	v_pk_mul_f32 v[58:59], v[58:59], s[82:83] op_sel_hi:[1,0]
	v_pk_mul_f32 v[60:61], v[60:61], s[82:83] op_sel_hi:[1,0]
	v_cvt_pk_bf16_f32 v58, v58, v59
	v_cvt_pk_bf16_f32 v59, v60, v61
	v_pk_mul_f32 v[60:61], v[74:75], s[82:83] op_sel_hi:[1,0]
	v_pk_mul_f32 v[44:45], v[64:65], s[82:83] op_sel_hi:[1,0]
	v_cvt_pk_bf16_f32 v60, v60, v61
	v_cvt_pk_bf16_f32 v61, v44, v45
	v_mul_f32_e32 v44, 0x45800000, v51
; __device__ __forceinline__ unsigned cvtpk(float lo, float hi) { f32x2 v = {lo, hi}; bf16x2_t b = __builtin_convertvector(v, bf16x2_t); return __builtin_bit_cast(unsigned, b); }
; #define ATT_SB() __builtin_amdgcn_sched_barrier(0)
; #define ATT_DMA_K(t, sl) do { glds16(ksrc + (size_t)(t) * 64 * kpitch, (unsigned)__builtin_amdgcn_readfirstlane(kdst + (sl) * KSLOT)); \
;         if constexpr (DQK == 96) glds16(krsrc + (size_t)(t) * 64 * 32, (unsigned)__builtin_amdgcn_readfirstlane(krdst + (sl) * KSLOT)); } while (0)
; #define ATT_DMA_V(t, sl) do { glds16(vsrc + (size_t)(t) * 64, (unsigned)__builtin_amdgcn_readfirstlane(vdst + (sl) * VSLOT)); \
;         if constexpr (DV == 128) glds16(vsrc + (size_t)64 * NR + (size_t)(t) * 64, (unsigned)__builtin_amdgcn_readfirstlane(vdst + (sl) * VSLOT + 8192)); } while (0)
; #define ATT_KLOAD(sl) do { _Pragma("unroll") for (int kb_ = 0; kb_ < NKW; ++kb_) _Pragma("unroll") for (int ds_ = 0; ds_ < NDS; ++ds_) { \
;         if (ds_ < 2) kf[kb_ * NDS + ds_] = *(const LAS bf16x8*)(kp[ds_ & 1] + (sl) * KSLOT + (kb_ & 1) * 512 + (kb_ >> 1) * 4096); \
;         else kf[kb_ * NDS + ds_] = *(const LAS bf16x8*)(krp + (sl) * KSLOT + (kb_ & 1) * 256 + (kb_ >> 1) * 2048); } } while (0)
; template <int DQK, int DV, bool LEAD> ...
;     ...
;           for (int ds = 0; ds < NDS; ++ds) { u32x4 w;
; #pragma unroll
;               for (int i = 0; i < 4; ++i) w[i] = cvtpk(x[ds][2 * i] * c2, x[ds][2 * i + 1] * c2);
;               qf[qb * NDS + ds] = __builtin_bit_cast(bf16x8, w); }
;       }
; #pragma unroll
;       for (int d0 = 0; d0 < NQB * NDS; ++d0) asm volatile("" : "+v"(qf[d0])); }
;     wait_bar<0>();
;     bf16x8 kf[NKW * NDS], vf[NVF];
;     ATT_KLOAD(0);
;     asm volatile("s_waitcnt lgkmcnt(0)\n\ts_barrier" ::: "memory");
;     float lsum[NQB];
; #pragma unroll
;     for (int qb = 0; qb < NQB; ++qb) lsum[qb] = 0.f;
;     const f32x4 zero4 = {0.f, 0.f, 0.f, 0.f};
;     f32x4 o[NDB][NQB], c[NKW][NQB]; u32x4 pw[4];
; #pragma unroll
;     for (int i = 0; i < NDB; ++i)
; #pragma unroll
;         for (int qb = 0; qb < NQB; ++qb) o[i][qb] = zero4;
;     ATT_DMA_K(3, 0); ATT_DMA_V(1, 1);
;     ATT_QK(); ATT_SB();
;     ATT_KLOAD(1); ATT_SB();
	v_cndmask_b32_e64 v44, v51, v44, s[4:5]
	v_pk_mul_f32 v[62:63], v[44:45], v[62:63] op_sel_hi:[0,1]
	v_pk_mul_f32 v[62:63], v[90:91], v[62:63]
	v_pk_mul_f32 v[70:71], v[70:71], v[134:135]
	v_mov_b32_e32 v45, v62
	v_mov_b32_e32 v51, v62
	v_mov_b32_e32 v53, v63
	v_mov_b32_e32 v64, v63
	v_permlane16_swap_b32_e32 v45, v51
	s_nop 0
	v_permlane16_swap_b32_e32 v53, v64
	v_cndmask_b32_e32 v65, v53, v64, vcc
	v_cndmask_b32_e32 v64, v45, v51, vcc
	v_mov_b32_e32 v51, v52
	v_pk_mul_f32 v[50:51], v[50:51], v[62:63]
	v_pk_mul_f32 v[72:73], v[72:73], v[122:123]
	v_pk_fma_f32 v[48:49], v[48:49], v[64:65], v[50:51]
	v_pk_mul_f32 v[50:51], v[44:45], v[76:77] op_sel_hi:[0,1]
	v_pk_mul_f32 v[50:51], v[92:93], v[50:51]
	v_pk_mul_f32 v[66:67], v[66:67], v[120:121]
	v_mov_b32_e32 v45, v50
	v_mov_b32_e32 v52, v50
	s_nop 1
	v_permlane16_swap_b32_e32 v45, v52
	v_mov_b32_e32 v53, v51
	v_mov_b32_e32 v62, v51
	s_nop 1
	v_permlane16_swap_b32_e32 v53, v62
	v_pk_mul_f32 v[46:47], v[46:47], v[50:51]
	v_pk_mul_f32 v[50:51], v[44:45], v[80:81] op_sel_hi:[0,1]
	v_cndmask_b32_e32 v53, v53, v62, vcc
	v_cndmask_b32_e32 v52, v45, v52, vcc
	v_pk_mul_f32 v[50:51], v[86:87], v[50:51]
	v_pk_fma_f32 v[46:47], v[168:169], v[52:53], v[46:47]
	v_mov_b32_e32 v45, v50
	v_mov_b32_e32 v52, v50
	v_mov_b32_e32 v53, v51
	v_mov_b32_e32 v62, v51
	v_permlane16_swap_b32_e32 v45, v52
	s_nop 0
	v_permlane16_swap_b32_e32 v53, v62
	v_cndmask_b32_e32 v53, v53, v62, vcc
	v_cndmask_b32_e32 v52, v45, v52, vcc
	v_pk_mul_f32 v[40:41], v[40:41], v[52:53]
	v_pk_mul_f32 v[68:69], v[68:69], v[118:119]
	v_pk_fma_f32 v[40:41], v[42:43], v[50:51], v[40:41]
	v_pk_mul_f32 v[42:43], v[44:45], v[100:101] op_sel_hi:[0,1]
	v_pk_mul_f32 v[42:43], v[88:89], v[42:43]
	v_pk_mul_f32 v[54:55], v[70:71], s[82:83] op_sel_hi:[1,0]
	v_mov_b32_e32 v44, v42
	v_mov_b32_e32 v50, v42
	v_mov_b32_e32 v45, v43
	v_mov_b32_e32 v51, v43
	v_permlane16_swap_b32_e32 v44, v50
	s_nop 0
	v_permlane16_swap_b32_e32 v45, v51
	v_cndmask_b32_e32 v45, v45, v51, vcc
	v_cndmask_b32_e32 v44, v44, v50, vcc
	v_pk_mul_f32 v[44:45], v[84:85], v[44:45]
	v_pk_mul_f32 v[56:57], v[72:73], s[82:83] op_sel_hi:[1,0]
	v_pk_fma_f32 v[42:43], v[42:43], v[38:39], v[44:45]
	v_cvt_pk_bf16_f32 v54, v54, v55
	v_cvt_pk_bf16_f32 v55, v56, v57
	v_pk_mul_f32 v[56:57], v[66:67], s[82:83] op_sel_hi:[1,0]
	v_pk_mul_f32 v[66:67], v[68:69], s[82:83] op_sel_hi:[1,0]
	v_pk_mul_f32 v[38:39], v[48:49], s[82:83] op_sel_hi:[1,0]
	v_pk_mul_f32 v[44:45], v[46:47], s[82:83] op_sel_hi:[1,0]
	v_pk_mul_f32 v[40:41], v[40:41], s[82:83] op_sel_hi:[1,0]
	v_pk_mul_f32 v[42:43], v[42:43], s[82:83] op_sel_hi:[1,0]
	v_cvt_pk_bf16_f32 v56, v56, v57
	v_cvt_pk_bf16_f32 v57, v66, v67
	v_cvt_pk_bf16_f32 v38, v38, v39
	v_cvt_pk_bf16_f32 v39, v44, v45
	v_cvt_pk_bf16_f32 v40, v40, v41
	v_cvt_pk_bf16_f32 v41, v42, v43
	s_waitcnt vmcnt(0) lgkmcnt(0)
	s_barrier
	ds_read_b128 v[42:45], v219
	ds_read_b128 v[46:49], v219 offset:512
	v_bitop3_b32 v70, v240, v206, v239 bitop3:0x36
	v_lshl_add_u32 v208, v70, 4, v241
	s_waitcnt lgkmcnt(1)
	v_mfma_f32_16x16x32_bf16 v[50:53], v[42:45], v[6:9], 0
	ds_read_b128 v[70:73], v208
	ds_read_b128 v[74:77], v208 offset:512
	s_lshl_b32 s4, s16, 11
	v_sub_u32_e32 v79, v237, v79
	v_mfma_f32_16x16x32_bf16 v[62:65], v[42:45], v[18:21], 0
	v_add3_u32 v209, v79, v78, s4
	s_mov_b64 s[4:5], 0x60000
	s_lshl_b32 s6, s24, 6
	v_mfma_f32_16x16x32_bf16 v[66:69], v[42:45], v[30:33], 0
	s_cmpk_lt_u32 s38, 0x100
	s_cselect_b64 vcc, -1, 0
	s_mov_b32 s16, 1
	v_mfma_f32_16x16x32_bf16 v[42:45], v[42:45], v[54:57], 0
	s_mov_b32 s7, 2
	s_mov_b32 s24, 0
	s_waitcnt lgkmcnt(1)
	v_mfma_f32_16x16x32_bf16 v[50:53], v[70:73], v[2:5], v[50:53]
	v_mfma_f32_16x16x32_bf16 v[62:65], v[70:73], v[14:17], v[62:65]
	v_mfma_f32_16x16x32_bf16 v[66:69], v[70:73], v[26:29], v[66:69]
	v_mfma_f32_16x16x32_bf16 v[42:45], v[70:73], v[58:61], v[42:45]
	ds_read_b128 v[70:73], v209 offset:8192
	ds_read_b128 v[78:81], v209 offset:8448
	s_waitcnt lgkmcnt(0)
	s_barrier
; #define ATT_SB() __builtin_amdgcn_sched_barrier(0)
; #define ATT_DMA_K(t, sl) do { glds16(ksrc + (size_t)(t) * 64 * kpitch, (unsigned)__builtin_amdgcn_readfirstlane(kdst + (sl) * KSLOT)); \
;         if constexpr (DQK == 96) glds16(krsrc + (size_t)(t) * 64 * 32, (unsigned)__builtin_amdgcn_readfirstlane(krdst + (sl) * KSLOT)); } while (0)
; #define ATT_DMA_V(t, sl) do { glds16(vsrc + (size_t)(t) * 64, (unsigned)__builtin_amdgcn_readfirstlane(vdst + (sl) * VSLOT)); \
;         if constexpr (DV == 128) glds16(vsrc + (size_t)64 * NR + (size_t)(t) * 64, (unsigned)__builtin_amdgcn_readfirstlane(vdst + (sl) * VSLOT + 8192)); } while (0)
; #define ATT_KLOAD(sl) do { _Pragma("unroll") for (int kb_ = 0; kb_ < NKW; ++kb_) _Pragma("unroll") for (int ds_ = 0; ds_ < NDS; ++ds_) { \
;         if (ds_ < 2) kf[kb_ * NDS + ds_] = *(const LAS bf16x8*)(kp[ds_ & 1] + (sl) * KSLOT + (kb_ & 1) * 512 + (kb_ >> 1) * 4096); \
;         else kf[kb_ * NDS + ds_] = *(const LAS bf16x8*)(krp + (sl) * KSLOT + (kb_ & 1) * 256 + (kb_ >> 1) * 2048); } } while (0)
; #define ATT_QK() do { _Pragma("unroll") for (int kb_ = 0; kb_ < NKW; ++kb_) _Pragma("unroll") for (int ds_ = 0; ds_ < NDS; ++ds_) _Pragma("unroll") for (int qb_ = 0; qb_ < NQB; ++qb_) \
;         c[kb_][qb_] = __builtin_amdgcn_mfma_f32_16x16x32_bf16(kf[kb_ * NDS + ds_], qf[qb_ * NDS + ds_], ds_ == 0 ? zero4 : c[kb_][qb_], 0, 0, 0); } while (0)
; #define ATT_EXP() do { _Pragma("unroll") for (int kb_ = 0; kb_ < NKW; ++kb_) _Pragma("unroll") for (int qb_ = 0; qb_ < NQB; ++qb_) _Pragma("unroll") for (int i_ = 0; i_ < 4; ++i_) \
;         c[kb_][qb_][i_] = __builtin_amdgcn_exp2f(c[kb_][qb_][i_]); } while (0)
; template <int DQK, int DV, bool LEAD> ...
;     ...
;     ATT_DMA_K(3, 0); ATT_DMA_V(1, 1);
;     ATT_QK(); ATT_SB();
;     ATT_KLOAD(1); ATT_SB();
;     if constexpr (LEAD) { ATT_EXP(); ATT_SUMPACK(); }
;     wait_bar<NDMA>();
;     int s_prev = 0, s_cur = 1, s_next = 2;
;     int one_ = 1; asm volatile("" : "+s"(one_));
	s_waitcnt lgkmcnt(1)
	v_mfma_f32_16x16x32_bf16 v[94:97], v[70:73], v[38:41], v[42:45]
	v_mfma_f32_16x16x32_bf16 v[42:45], v[46:49], v[6:9], 0
	v_mfma_f32_16x16x32_bf16 v[82:85], v[70:73], v[10:13], v[50:53]
	v_mfma_f32_16x16x32_bf16 v[86:89], v[70:73], v[22:25], v[62:65]
	v_mfma_f32_16x16x32_bf16 v[50:53], v[46:49], v[18:21], 0
	v_mfma_f32_16x16x32_bf16 v[62:65], v[46:49], v[30:33], 0
	v_mfma_f32_16x16x32_bf16 v[46:49], v[46:49], v[54:57], 0
	v_mfma_f32_16x16x32_bf16 v[42:45], v[74:77], v[2:5], v[42:45]
	v_mfma_f32_16x16x32_bf16 v[50:53], v[74:77], v[14:17], v[50:53]
	v_mfma_f32_16x16x32_bf16 v[62:65], v[74:77], v[26:29], v[62:65]
	v_mfma_f32_16x16x32_bf16 v[46:49], v[74:77], v[58:61], v[46:49]
	s_waitcnt lgkmcnt(0)
	v_mfma_f32_16x16x32_bf16 v[74:77], v[78:81], v[10:13], v[42:45]
	s_nop 2
	v_lshl_add_u64 v[42:43], v[186:187], 0, s[4:5]
	s_mov_b32 s4, m0
	s_mov_b32 m0, s42
	s_nop 0
	global_load_lds_dwordx4 v[42:43], off
	s_mov_b32 m0, s4
	s_mov_b64 s[4:5], 0x3000
	v_mfma_f32_16x16x32_bf16 v[90:93], v[70:73], v[34:37], v[66:69]
	v_lshl_add_u64 v[42:43], v[188:189], 0, s[4:5]
	s_mov_b32 s4, m0
	s_mov_b32 m0, s41
	s_nop 0
	global_load_lds_dwordx4 v[42:43], off
	s_mov_b32 m0, s4
	v_lshl_add_u64 v[42:43], v[190:191], 0, s[66:67]
	v_mfma_f32_16x16x32_bf16 v[98:101], v[78:81], v[22:25], v[50:53]
	s_add_i32 s4, s40, 0x2000
	s_mov_b32 s5, m0
	s_mov_b32 m0, s4
	s_nop 0
	global_load_lds_dwordx4 v[42:43], off
	s_mov_b32 m0, s5
	v_mfma_f32_16x16x32_bf16 v[102:105], v[78:81], v[34:37], v[62:65]
	v_mfma_f32_16x16x32_bf16 v[78:81], v[78:81], v[38:41], v[46:49]
	ds_read_b128 v[42:45], v219 offset:12288
	s_nop 1
	ds_read_b128 v[46:49], v219 offset:12800
	ds_read_b128 v[50:53], v208 offset:12288
	ds_read_b128 v[62:65], v208 offset:12800
	ds_read_b128 v[66:69], v209 offset:20480
	ds_read_b128 v[70:73], v209 offset:20736
	v_exp_f32_e32 v82, v82
	v_exp_f32_e32 v83, v83
	v_exp_f32_e32 v84, v84
	v_exp_f32_e32 v85, v85
	v_exp_f32_e32 v86, v86
	v_exp_f32_e32 v87, v87
	v_exp_f32_e32 v88, v88
	v_exp_f32_e32 v89, v89
	v_exp_f32_e32 v90, v90
	v_exp_f32_e32 v91, v91
	v_exp_f32_e32 v92, v92
	v_exp_f32_e32 v93, v93
	v_exp_f32_e32 v94, v94
	v_exp_f32_e32 v95, v95
	v_exp_f32_e32 v96, v96
	v_exp_f32_e32 v97, v97
	v_exp_f32_e32 v107, v74
	v_exp_f32_e32 v108, v75
	v_add_f32_e32 v74, v82, v83
	v_add_f32_e32 v75, v84, v85
	v_exp_f32_e32 v109, v76
	v_exp_f32_e32 v98, v98
	v_exp_f32_e32 v102, v102
	v_exp_f32_e32 v78, v78
	v_add_f32_e32 v74, v74, v75
	v_add_f32_e32 v75, v86, v87
	v_add_f32_e32 v76, v88, v89
	v_exp_f32_e32 v110, v77
	v_add_f32_e32 v75, v75, v76
	v_add_f32_e32 v76, v90, v91
	v_add_f32_e32 v77, v92, v93
	v_exp_f32_e32 v99, v99
	v_exp_f32_e32 v103, v103
	v_exp_f32_e32 v79, v79
	v_add_f32_e32 v76, v76, v77
	v_add_f32_e32 v77, v94, v95
	v_add_f32_e32 v111, v96, v97
	v_add_f32_e32 v77, v77, v111
	v_exp_f32_e32 v100, v100
	v_exp_f32_e32 v104, v104
	v_exp_f32_e32 v80, v80
	v_add_f32_e32 v74, v74, v107
	v_add_f32_e32 v75, v75, v98
	v_add_f32_e32 v76, v76, v102
	v_add_f32_e32 v77, v77, v78
	v_exp_f32_e32 v101, v101
	v_exp_f32_e32 v105, v105
	v_exp_f32_e32 v81, v81
	v_add_f32_e32 v74, v108, v74
	v_add_f32_e32 v75, v99, v75
	v_add_f32_e32 v76, v103, v76
	v_add_f32_e32 v77, v79, v77
	s_mov_b32 s4, 1
	v_add_f32_e32 v74, v109, v74
	v_add_f32_e32 v111, v100, v75
	v_add_f32_e32 v76, v104, v76
	v_add_f32_e32 v112, v80, v77
	v_cvt_pk_bf16_f32 v138, v82, v83
	v_add_f32_e32 v75, v110, v74
	v_add_f32_e32 v74, v101, v111
	v_add_f32_e32 v77, v105, v76
	v_add_f32_e32 v76, v81, v112
	s_waitcnt vmcnt(3) lgkmcnt(0)
	s_barrier
	s_cmp_lg_u32 s4, 0
	v_pk_add_f32 v[204:205], v[74:75], 0 op_sel_hi:[1,0]
	v_cndmask_b32_e32 v74, v206, v194, vcc
	v_bitop3_b32 v74, v74, v106, 7 bitop3:0x78
	v_lshlrev_b32_e32 v74, 4, v74
	v_add3_u32 v210, 0, v207, v74
	v_mov_b32_e32 v74, 0
	v_pk_add_f32 v[192:193], v[76:77], 0 op_sel_hi:[1,0]
	v_cvt_pk_bf16_f32 v139, v84, v85
	v_cvt_pk_bf16_f32 v140, v107, v108
	v_cvt_pk_bf16_f32 v141, v109, v110
	v_cvt_pk_bf16_f32 v142, v86, v87
	v_cvt_pk_bf16_f32 v143, v88, v89
	v_cvt_pk_bf16_f32 v144, v98, v99
	v_cvt_pk_bf16_f32 v145, v100, v101
	v_cvt_pk_bf16_f32 v146, v90, v91
	v_cvt_pk_bf16_f32 v147, v92, v93
	v_cvt_pk_bf16_f32 v148, v102, v103
	v_cvt_pk_bf16_f32 v149, v104, v105
	v_cvt_pk_bf16_f32 v150, v94, v95
	v_cvt_pk_bf16_f32 v151, v96, v97
	v_cvt_pk_bf16_f32 v152, v78, v79
	v_cvt_pk_bf16_f32 v153, v80, v81
	s_cselect_b64 s[4:5], -1, 0
	s_mov_b32 s38, 2
	v_mov_b32_e32 v75, v74
	v_mov_b32_e32 v76, v74
	v_mov_b32_e32 v77, v74
	v_mov_b32_e32 v78, v74
	v_mov_b32_e32 v79, v74
	v_mov_b32_e32 v80, v74
	v_mov_b32_e32 v81, v74
	v_mov_b32_e32 v82, v74
	v_mov_b32_e32 v83, v74
	v_mov_b32_e32 v84, v74
	v_mov_b32_e32 v85, v74
	v_mov_b32_e32 v86, v74
	v_mov_b32_e32 v87, v74
	v_mov_b32_e32 v88, v74
	v_mov_b32_e32 v89, v74
	v_mov_b32_e32 v90, v74
	v_mov_b32_e32 v91, v74
	v_mov_b32_e32 v92, v74
	v_mov_b32_e32 v93, v74
	v_mov_b32_e32 v94, v74
	v_mov_b32_e32 v95, v74
	v_mov_b32_e32 v96, v74
	v_mov_b32_e32 v97, v74
	v_mov_b32_e32 v98, v74
	v_mov_b32_e32 v99, v74
	v_mov_b32_e32 v100, v74
	v_mov_b32_e32 v101, v74
	v_mov_b32_e32 v102, v74
	v_mov_b32_e32 v103, v74
	v_mov_b32_e32 v104, v74
	v_mov_b32_e32 v105, v74
	v_mov_b32_e32 v106, v74
	v_mov_b32_e32 v107, v74
	v_mov_b32_e32 v108, v74
	v_mov_b32_e32 v109, v74
	v_mov_b32_e32 v110, v74
	v_mov_b32_e32 v111, v74
	v_mov_b32_e32 v112, v74
	v_mov_b32_e32 v113, v74
	v_mov_b32_e32 v114, v74
	v_mov_b32_e32 v115, v74
	v_mov_b32_e32 v116, v74
	v_mov_b32_e32 v117, v74
	v_mov_b32_e32 v118, v74
	v_mov_b32_e32 v119, v74
	v_mov_b32_e32 v120, v74
	v_mov_b32_e32 v121, v74
	v_mov_b32_e32 v122, v74
	v_mov_b32_e32 v123, v74
	v_mov_b32_e32 v124, v74
	v_mov_b32_e32 v125, v74
	v_mov_b32_e32 v126, v74
	v_mov_b32_e32 v127, v74
	v_mov_b32_e32 v128, v74
	v_mov_b32_e32 v129, v74
	v_mov_b32_e32 v130, v74
	v_mov_b32_e32 v131, v74
	v_mov_b32_e32 v132, v74
	v_mov_b32_e32 v133, v74
	v_mov_b32_e32 v134, v74
	v_mov_b32_e32 v135, v74
	v_mov_b32_e32 v136, v74
	v_mov_b32_e32 v137, v74

; template <int DQK, int DV, bool LEAD> ...
;     ...
;     const int krow_l = wid * 8 + (lane >> 3);
;     const int kc_l = (lane & 7) ^ (((krow_l >> 1) & 1) | (((krow_l >> 3) & 1) << 1) | (((krow_l >> 4) & 1) << 2));
;     const int vc_l = (lane & 7) ^ ((krow_l >> 1) & 7);
;     const bf16_t* ksrc = K + (size_t)(krow0 + krow_l) * kpitch + kc_l * 8;
;     const int rrow_l = (wid & 3) * 16 + (lane >> 2), rc_l = (lane & 3) ^ (((rrow_l >> 4) & 1) << 1);
;     const bf16_t* krsrc = (DQK == 96) ? KR + (size_t)(krow0 + rrow_l) * 32 + rc_l * 8 : nullptr;
;     const bf16_t* vsrc = Vt + (size_t)krow_l * NR + krow0 + vc_l * 8;
;     const unsigned kdst = lds0 + KOFF + wid * 1024, krdst = lds0 + KOFF + 8192 + (wid & 3) * 1024, vdst = lds0 + VOFF + wid * 1024;
;     ...
;     ATT_DMA_K(0, 0); ATT_DMA_V(0, 0); ATT_DMA_K(1, 1); ATT_DMA_K(2, 2);
;     bf16x8 qf[NQB * NDS];
;     {
;       const float c2 = (DQK == 64) ? C2_EVEN : C2_ODD; const bool lat = tq0 >= 0;
; #pragma unroll
;       for (int qb = 0; qb < NQB; ++qb) {
;           const bf16_t* qp = Q + (size_t)(qrow0 + qoff + qb * 16 + q16) * qpitch + g4 * 8;
;           bf16x8 raw[NDS];
; #pragma unroll
;           for (int ds = 0; ds < NDS; ++ds) raw[ds] = *(const bf16x8*)(qp + ds * 32);
;           float x[NDS][8];
; #pragma unroll
;           for (int ds = 0; ds < NDS; ++ds)
; #pragma unroll
;               for (int j = 0; j < 8; ++j) x[ds][j] = __uint_as_float(((unsigned)(unsigned short)raw[ds][j]) << 16);
;           const int tq = tq0 + qoff + qb * 16 + q16, prow = (tq >> 6) & 127, pcol = tq & 63;
;           float sn = 0.f;
; #pragma unroll
;           for (int ds = 0; ds < 2; ++ds)
; #pragma unroll
;               for (int j = 0; j < 8; ++j) sn += x[ds][j] * x[ds][j];
;           sn = lanes4_sum(sn);
;           const float rn = rsqrtf(sn * (1.f / 64.f) + EPS);
; #pragma unroll
;           for (int ds = 0; ds < 2; ++ds)
; #pragma unroll
;               for (int j = 0; j < 8; ++j) x[ds][j] *= rn * qgain[32 * ds + 8 * g4 + j];
;           if constexpr (DQK == 64) {
; #pragma unroll
;               for (int ds = 0; ds < 2; ++ds)
; #pragma unroll
;                   for (int j = 0; j < 8; ++j) {
;                       auto rr = __builtin_amdgcn_permlane32_swap(__float_as_uint(x[ds][j]), __float_as_uint(x[ds][j]), false, false);
;                       const float other = hi ? __uint_as_float(rr[0]) : __uint_as_float(rr[1]);
.LBB0_661:
	v_mov_b32_e32 v142, v0
	v_mov_b64_e32 v[6:7], s[46:47]
	v_readfirstlane_b32 s16, v142
	s_ashr_i32 s4, s16, 6
	v_bfe_u32 v2, v142, 3, 3
	v_lshl_or_b32 v8, s4, 3, v2
	v_ashrrev_i32_e32 v3, 1, v8
	v_and_b32_e32 v4, 1, v3
	s_lshl_b32 s5, s4, 1
	s_lshr_b32 s7, s16, 5
	v_and_b32_e32 v2, 7, v142
	s_and_b32 s6, s5, 2
	v_and_or_b32 v4, s7, 4, v4
	s_and_b32 s24, s4, 3
	v_bitop3_b32 v9, v4, v2, s6 bitop3:0x36
	v_bfe_u32 v4, v142, 2, 4
	v_add_u32_e32 v2, s40, v8
	v_lshl_or_b32 v4, s24, 4, v4
	v_xor_b32_e32 v10, v3, v142
	v_ashrrev_i32_e32 v3, 31, v2
	v_or_b32_e32 v4, s40, v4
	v_lshlrev_b64 v[2:3], 11, v[2:3]
	v_and_b32_e32 v18, 3, v142
	v_ashrrev_i32_e32 v5, 31, v4
	v_bitop3_b32 v11, s5, v18, 2 bitop3:0x6c
	v_lshlrev_b64 v[4:5], 6, v[4:5]
	s_ashr_i32 s41, s40, 31
	s_lshl_b32 s30, s4, 10
	s_lshl_b32 s6, s24, 10
	v_lshl_add_u64 v[2:3], s[44:45], 0, v[2:3]
	v_mad_i64_i32 v[6:7], s[4:5], v8, s91, v[6:7]
	v_lshlrev_b32_e32 v194, 4, v9
	s_add_i32 s30, s30, 0
	v_lshl_add_u64 v[4:5], s[28:29], 0, v[4:5]
	v_lshl_add_u64 v[6:7], s[40:41], 1, v[6:7]
	v_lshl_add_u64 v[62:63], v[2:3], 0, v[194:195]
	v_lshlrev_b32_e32 v194, 4, v11
	v_lshlrev_b32_e32 v2, 4, v10
	s_add_i32 s41, s6, 0
	s_mov_b32 s4, m0
	s_mov_b32 m0, s30
	s_nop 0
	global_load_lds_dwordx4 v[62:63], off
	s_mov_b32 m0, s4
	v_lshl_add_u64 v[64:65], v[4:5], 0, v[194:195]
	v_and_b32_e32 v194, 0x70, v2
	s_addk_i32 s41, 0x2000
	s_mov_b32 s4, m0
	s_mov_b32 m0, s41
	s_nop 0
	global_load_lds_dwordx4 v[64:65], off
	s_mov_b32 m0, s4
	s_add_i32 s31, s30, 0x9000
	v_lshl_add_u64 v[186:187], v[6:7], 0, v[194:195]
	s_mov_b32 s4, m0
	s_mov_b32 m0, s31
	s_nop 0
	global_load_lds_dwordx4 v[186:187], off
	s_mov_b32 m0, s4
	s_mov_b64 s[4:5], 0x20000
	v_lshl_add_u64 v[2:3], v[62:63], 0, s[4:5]
	s_add_i32 s4, s30, 0x3000
	s_mov_b32 s5, m0
	s_mov_b32 m0, s4
	s_nop 0
	global_load_lds_dwordx4 v[2:3], off
	s_mov_b32 m0, s5
	v_lshl_add_u64 v[2:3], v[64:65], 0, s[60:61]
	s_add_i32 s4, s41, 0x3000
	s_mov_b32 s5, m0
	s_mov_b32 m0, s4
	s_nop 0
	global_load_lds_dwordx4 v[2:3], off
	s_mov_b32 m0, s5
	s_mov_b64 s[4:5], 0x40000
	v_lshl_add_u64 v[2:3], v[62:63], 0, s[4:5]
	s_add_i32 s4, s30, 0x6000
	s_mov_b32 s5, m0
	s_mov_b32 m0, s4
	s_nop 0
	global_load_lds_dwordx4 v[2:3], off
	s_mov_b32 m0, s5
	s_mov_b64 s[4:5], 0x2000
	v_and_b32_e32 v143, 15, v142
	v_lshl_add_u64 v[2:3], v[64:65], 0, s[4:5]
	s_add_i32 s4, s41, 0x6000
	s_mov_b32 s5, m0
	s_mov_b32 m0, s4
	s_nop 0
	global_load_lds_dwordx4 v[2:3], off
	s_mov_b32 m0, s5
	v_lshl_or_b32 v2, s24, 6, v143
	v_and_b32_e32 v8, 48, v142
	v_or_b32_e32 v6, s40, v2
	v_mov_b32_e32 v9, v195
	v_lshl_add_u64 v[2:3], s[36:37], 0, v[8:9]
	v_or_b32_e32 v7, 16, v6
	v_mad_i64_i32 v[4:5], s[4:5], v6, s90, v[2:3]
	v_mad_i64_i32 v[10:11], s[4:5], v7, s90, v[2:3]
	v_or_b32_e32 v7, 32, v6
	v_or_b32_e32 v6, 48, v6
	v_mad_i64_i32 v[14:15], s[4:5], v7, s90, v[2:3]
	v_mad_i64_i32 v[16:17], s[4:5], v6, s90, v[2:3]
	global_load_dwordx4 v[46:49], v[4:5], off offset:64 nt
	global_load_dwordx4 v[50:53], v[10:11], off offset:64 nt
	global_load_dwordx4 v[54:57], v[14:15], off offset:64 nt
	global_load_dwordx4 v[58:61], v[16:17], off offset:64 nt
	global_load_dwordx4 v[88:91], v[4:5], off nt
	global_load_dwordx4 v[94:97], v[10:11], off nt
	global_load_dwordx4 v[98:101], v[14:15], off nt
	global_load_dwordx4 v[6:9], v[16:17], off nt
	s_nop 0
	global_load_dwordx4 v[10:13], v[10:11], off offset:128 nt
	v_lshlrev_b32_e32 v2, 1, v142
	v_and_or_b32 v144, v2, 24, v18
	v_bfe_u32 v146, v142, 3, 1
	v_bfe_u32 v170, v142, 4, 2
	s_ashr_i32 s38, s16, 8
	v_bfe_u32 v147, v142, 1, 2
	v_lshlrev_b32_e32 v148, 2, v146
	v_lshl_add_u32 v145, v144, 7, 0
	v_lshl_add_u32 v149, s38, 12, v145
	v_bitop3_b32 v2, v148, v170, v147 bitop3:0x36
	v_lshl_add_u32 v194, v2, 4, v149
	global_load_dwordx4 v[2:5], v[4:5], off offset:128 nt
	v_lshlrev_b32_e32 v82, 5, v170
	global_load_dwordx4 v[22:25], v[14:15], off offset:128 nt
	global_load_dwordx4 v[42:45], v[16:17], off offset:128 nt
	global_load_dwordx4 v[30:33], v82, s[26:27] offset:144
	global_load_dwordx4 v[38:41], v82, s[26:27] offset:128
	s_mov_b32 s6, 0x3d000000
	s_brev_b32 s7, 60
	s_mov_b32 s4, 0x358637bd
	s_mov_b32 s7, 0x3c800000
	v_mov_b64_e32 v[106:107], s[4:5]
	v_and_b32_e32 v112, 16, v142
	v_and_b32_e32 v203, 63, v142
	s_mov_b32 s42, 1
	s_mov_b32 s43, 2
	s_waitcnt vmcnt(10)
	v_and_b32_e32 v73, 0xffff0000, v58
	s_waitcnt vmcnt(9)
	v_and_b32_e32 v137, 0xffff0000, v88
	v_lshlrev_b32_e32 v136, 16, v88
	v_and_b32_e32 v135, 0xffff0000, v89
	s_waitcnt vmcnt(6)
; template <int DQK, int DV, bool LEAD> ...
;     ...
;           float x[NDS][8];
; #pragma unroll
;           for (int ds = 0; ds < NDS; ++ds)
; #pragma unroll
;               for (int j = 0; j < 8; ++j) x[ds][j] = __uint_as_float(((unsigned)(unsigned short)raw[ds][j]) << 16);
;           const int tq = tq0 + qoff + qb * 16 + q16, prow = (tq >> 6) & 127, pcol = tq & 63;
;           float sn = 0.f;
; #pragma unroll
;           for (int ds = 0; ds < 2; ++ds)
; #pragma unroll
;               for (int j = 0; j < 8; ++j) sn += x[ds][j] * x[ds][j];
;           sn = lanes4_sum(sn);
;           const float rn = rsqrtf(sn * (1.f / 64.f) + EPS);
; #pragma unroll
;           for (int ds = 0; ds < 2; ++ds)
; #pragma unroll
;               for (int j = 0; j < 8; ++j) x[ds][j] *= rn * qgain[32 * ds + 8 * g4 + j];
	v_and_b32_e32 v77, 0xffff0000, v8
	v_lshlrev_b32_e32 v76, 16, v8
	v_mul_f32_e32 v8, v137, v137
	v_and_b32_e32 v75, 0xffff0000, v9
	v_lshlrev_b32_e32 v74, 16, v9
	v_lshlrev_b32_e32 v134, 16, v89
	v_pk_fma_f32 v[8:9], v[136:137], v[136:137], v[8:9] op_sel_hi:[1,1,0]
	v_and_b32_e32 v81, 0xffff0000, v54
	v_lshlrev_b32_e32 v80, 16, v54
	v_pk_fma_f32 v[8:9], v[134:135], v[134:135], v[8:9]
	v_mul_f32_e32 v54, v135, v135
	v_and_b32_e32 v133, 0xffff0000, v90
	v_lshlrev_b32_e32 v132, 16, v90
	v_pk_add_f32 v[8:9], v[54:55], v[8:9] op_sel_hi:[0,1]
	v_pk_fma_f32 v[8:9], v[132:133], v[132:133], v[8:9]
	v_mul_f32_e32 v54, v133, v133
	v_and_b32_e32 v127, 0xffff0000, v91
	v_lshlrev_b32_e32 v126, 16, v91
	v_pk_add_f32 v[8:9], v[54:55], v[8:9] op_sel_hi:[0,1]
	v_pk_fma_f32 v[8:9], v[126:127], v[126:127], v[8:9]
	v_mul_f32_e32 v54, v127, v127
	v_and_b32_e32 v125, 0xffff0000, v46
	v_lshlrev_b32_e32 v124, 16, v46
	v_pk_add_f32 v[8:9], v[54:55], v[8:9] op_sel_hi:[0,1]
	v_pk_fma_f32 v[8:9], v[124:125], v[124:125], v[8:9]
	v_mul_f32_e32 v54, v125, v125
	v_and_b32_e32 v123, 0xffff0000, v47
	v_lshlrev_b32_e32 v122, 16, v47
	v_pk_add_f32 v[8:9], v[54:55], v[8:9] op_sel_hi:[0,1]
	v_pk_fma_f32 v[8:9], v[122:123], v[122:123], v[8:9]
	v_mul_f32_e32 v54, v123, v123
	v_and_b32_e32 v121, 0xffff0000, v48
	v_lshlrev_b32_e32 v120, 16, v48
	v_pk_add_f32 v[8:9], v[54:55], v[8:9] op_sel_hi:[0,1]
	v_pk_fma_f32 v[8:9], v[120:121], v[120:121], v[8:9]
	v_mul_f32_e32 v54, v121, v121
	v_and_b32_e32 v17, 0xffff0000, v49
	v_lshlrev_b32_e32 v16, 16, v49
	v_pk_add_f32 v[8:9], v[54:55], v[8:9] op_sel_hi:[0,1]
	v_pk_fma_f32 v[8:9], v[16:17], v[16:17], v[8:9]
	v_mul_f32_e32 v54, v17, v17
	v_pk_add_f32 v[8:9], v[54:55], v[8:9] op_sel_hi:[0,1]
	v_and_b32_e32 v79, 0xffff0000, v7
	v_lshlrev_b32_e32 v78, 16, v7
	v_mov_b32_e32 v7, v8
	s_nop 1
	v_permlane16_swap_b32_e32 v8, v7
	v_add_f32_e32 v7, v8, v7
	v_mov_b32_e32 v9, v7
	v_and_b32_e32 v119, 0xffff0000, v94
	s_nop 0
	v_permlane32_swap_b32_e32 v7, v9
	v_lshlrev_b32_e32 v118, 16, v94
	v_mul_f32_e32 v8, v119, v119
	v_and_b32_e32 v37, 0xffff0000, v55
	v_lshlrev_b32_e32 v36, 16, v55
	v_and_b32_e32 v109, 0xffff0000, v95
	v_lshlrev_b32_e32 v108, 16, v95
	v_pk_fma_f32 v[54:55], v[118:119], v[118:119], v[8:9] op_sel_hi:[1,1,0]
	v_mul_f32_e32 v8, v109, v109
	v_pk_fma_f32 v[54:55], v[108:109], v[108:109], v[54:55]
	v_and_b32_e32 v105, 0xffff0000, v96
	v_lshlrev_b32_e32 v104, 16, v96
	v_pk_add_f32 v[54:55], v[8:9], v[54:55] op_sel_hi:[0,1]
	v_pk_fma_f32 v[54:55], v[104:105], v[104:105], v[54:55]
	v_mul_f32_e32 v8, v105, v105
	v_and_b32_e32 v103, 0xffff0000, v97
	v_lshlrev_b32_e32 v102, 16, v97
	v_pk_add_f32 v[54:55], v[8:9], v[54:55] op_sel_hi:[0,1]
	v_pk_fma_f32 v[54:55], v[102:103], v[102:103], v[54:55]
	v_mul_f32_e32 v8, v103, v103
	v_and_b32_e32 v29, 0xffff0000, v50
	v_lshlrev_b32_e32 v28, 16, v50
	v_pk_add_f32 v[54:55], v[8:9], v[54:55] op_sel_hi:[0,1]
	v_pk_fma_f32 v[54:55], v[28:29], v[28:29], v[54:55]
	v_mul_f32_e32 v8, v29, v29
	v_and_b32_e32 v21, 0xffff0000, v51
	v_lshlrev_b32_e32 v20, 16, v51
	v_pk_add_f32 v[54:55], v[8:9], v[54:55] op_sel_hi:[0,1]
	v_pk_fma_f32 v[54:55], v[20:21], v[20:21], v[54:55]
	v_mul_f32_e32 v8, v21, v21
	v_and_b32_e32 v19, 0xffff0000, v52
	v_lshlrev_b32_e32 v18, 16, v52
	v_pk_add_f32 v[54:55], v[8:9], v[54:55] op_sel_hi:[0,1]
	v_pk_fma_f32 v[54:55], v[18:19], v[18:19], v[54:55]
	v_mul_f32_e32 v8, v19, v19
	v_and_b32_e32 v15, 0xffff0000, v53
	v_lshlrev_b32_e32 v14, 16, v53
	v_pk_add_f32 v[54:55], v[8:9], v[54:55] op_sel_hi:[0,1]
	v_pk_fma_f32 v[54:55], v[14:15], v[14:15], v[54:55]
	v_mul_f32_e32 v8, v15, v15
	v_pk_add_f32 v[54:55], v[8:9], v[54:55] op_sel_hi:[0,1]
	v_mov_b32_e32 v8, v54
	v_and_b32_e32 v85, 0xffff0000, v101
	v_lshlrev_b32_e32 v84, 16, v101
	v_permlane16_swap_b32_e32 v54, v8
	v_and_b32_e32 v101, 0xffff0000, v98
	v_and_b32_e32 v87, 0xffff0000, v100
	v_lshlrev_b32_e32 v86, 16, v100
	v_add_f32_e32 v129, v54, v8
	v_lshlrev_b32_e32 v100, 16, v98
	v_mul_f32_e32 v8, v101, v101
	v_and_b32_e32 v93, 0xffff0000, v99
	v_lshlrev_b32_e32 v92, 16, v99
	v_pk_fma_f32 v[54:55], v[100:101], v[100:101], v[8:9] op_sel_hi:[1,1,0]
	v_mul_f32_e32 v8, v93, v93
	v_pk_fma_f32 v[54:55], v[92:93], v[92:93], v[54:55]
	v_and_b32_e32 v35, 0xffff0000, v56
	v_pk_add_f32 v[54:55], v[8:9], v[54:55] op_sel_hi:[0,1]
	v_pk_fma_f32 v[54:55], v[86:87], v[86:87], v[54:55]
	v_mul_f32_e32 v8, v87, v87
	v_pk_add_f32 v[54:55], v[8:9], v[54:55] op_sel_hi:[0,1]
	v_pk_fma_f32 v[54:55], v[84:85], v[84:85], v[54:55]
	v_mul_f32_e32 v8, v85, v85
	v_pk_add_f32 v[54:55], v[8:9], v[54:55] op_sel_hi:[0,1]
	v_pk_fma_f32 v[54:55], v[80:81], v[80:81], v[54:55]
	v_mul_f32_e32 v8, v81, v81
	v_pk_add_f32 v[54:55], v[8:9], v[54:55] op_sel_hi:[0,1]
	v_pk_fma_f32 v[54:55], v[36:37], v[36:37], v[54:55]
	v_mul_f32_e32 v8, v37, v37
	v_lshlrev_b32_e32 v34, 16, v56
	v_pk_add_f32 v[54:55], v[8:9], v[54:55] op_sel_hi:[0,1]
	v_pk_fma_f32 v[54:55], v[34:35], v[34:35], v[54:55]
	v_mul_f32_e32 v8, v35, v35
	v_and_b32_e32 v27, 0xffff0000, v57
	v_lshlrev_b32_e32 v26, 16, v57
	v_pk_add_f32 v[54:55], v[8:9], v[54:55] op_sel_hi:[0,1]
	v_pk_fma_f32 v[54:55], v[26:27], v[26:27], v[54:55]
	v_mul_f32_e32 v8, v27, v27
	v_pk_add_f32 v[54:55], v[8:9], v[54:55] op_sel_hi:[0,1]
	v_mov_b32_e32 v8, v54
	v_and_b32_e32 v89, 0xffff0000, v6
	s_nop 0
	v_permlane16_swap_b32_e32 v54, v8
	v_lshlrev_b32_e32 v88, 16, v6
	v_mul_f32_e32 v6, v89, v89
	v_add_f32_e32 v113, v54, v8
	v_pk_fma_f32 v[54:55], v[88:89], v[88:89], v[6:7] op_sel_hi:[1,1,0]
	v_mul_f32_e32 v6, v79, v79
	v_pk_fma_f32 v[54:55], v[78:79], v[78:79], v[54:55]
	global_load_dwordx4 v[46:49], v82, s[26:27] offset:16
	global_load_dwordx4 v[50:53], v82, s[26:27]
	v_pk_add_f32 v[54:55], v[6:7], v[54:55] op_sel_hi:[0,1]
	v_pk_fma_f32 v[54:55], v[76:77], v[76:77], v[54:55]
	v_mul_f32_e32 v6, v77, v77
	v_pk_add_f32 v[54:55], v[6:7], v[54:55] op_sel_hi:[0,1]
	v_pk_fma_f32 v[54:55], v[74:75], v[74:75], v[54:55]
	v_mul_f32_e32 v6, v75, v75
	v_lshlrev_b32_e32 v72, 16, v58
	v_pk_add_f32 v[54:55], v[6:7], v[54:55] op_sel_hi:[0,1]
	v_pk_fma_f32 v[54:55], v[72:73], v[72:73], v[54:55]
	v_mul_f32_e32 v6, v73, v73
	v_and_b32_e32 v71, 0xffff0000, v59
	v_lshlrev_b32_e32 v70, 16, v59
	v_pk_add_f32 v[54:55], v[6:7], v[54:55] op_sel_hi:[0,1]
	v_pk_fma_f32 v[54:55], v[70:71], v[70:71], v[54:55]
	v_mul_f32_e32 v6, v71, v71
	v_and_b32_e32 v69, 0xffff0000, v60
	v_lshlrev_b32_e32 v68, 16, v60
	v_pk_add_f32 v[54:55], v[6:7], v[54:55] op_sel_hi:[0,1]
	v_pk_fma_f32 v[54:55], v[68:69], v[68:69], v[54:55]
	v_mul_f32_e32 v6, v69, v69
	v_and_b32_e32 v67, 0xffff0000, v61
	v_lshlrev_b32_e32 v66, 16, v61
	v_pk_add_f32 v[54:55], v[6:7], v[54:55] op_sel_hi:[0,1]
	v_pk_fma_f32 v[54:55], v[66:67], v[66:67], v[54:55]
	v_mul_f32_e32 v6, v67, v67
	v_pk_add_f32 v[54:55], v[6:7], v[54:55] op_sel_hi:[0,1]
	v_mov_b32_e32 v6, v54
	s_nop 1
	v_permlane16_swap_b32_e32 v54, v6
	v_add_f32_e32 v95, v54, v6
	global_load_dwordx4 v[54:57], v82, s[26:27] offset:272
	global_load_dwordx4 v[58:61], v82, s[26:27] offset:256
	s_waitcnt vmcnt(8)
; template <int DQK, int DV, bool LEAD> ...
;     ...
;           float sn = 0.f;
; #pragma unroll
;           for (int ds = 0; ds < 2; ++ds)
; #pragma unroll
;               for (int j = 0; j < 8; ++j) sn += x[ds][j] * x[ds][j];
;           sn = lanes4_sum(sn);
;           const float rn = rsqrtf(sn * (1.f / 64.f) + EPS);
; #pragma unroll
;           for (int ds = 0; ds < 2; ++ds)
; #pragma unroll
;               for (int j = 0; j < 8; ++j) x[ds][j] *= rn * qgain[32 * ds + 8 * g4 + j];
;           if constexpr (DQK == 64) {
; #pragma unroll
;               for (int ds = 0; ds < 2; ++ds)
; #pragma unroll
;                   for (int j = 0; j < 8; ++j) {
;                       auto rr = __builtin_amdgcn_permlane32_swap(__float_as_uint(x[ds][j]), __float_as_uint(x[ds][j]), false, false);
;                       const float other = hi ? __uint_as_float(rr[0]) : __uint_as_float(rr[1]);
;                       float cc = 1.f, sg = 0.f;
;                       if (lat) { const f32x2 cs = rope[(ds ? pcol : prow) * 16 + 8 * (g4 & 1) + j]; cc = cs.x; sg = hi ? cs.y : -cs.y; }
;                       x[ds][j] = x[ds][j] * cc + other * sg; }
;           } else {
;               float sr = 0.f;
; #pragma unroll
;               for (int j = 0; j < 8; ++j) sr += x[2][j] * x[2][j];
;               sr = lanes4_sum(sr);
;               const float rq = rsqrtf(sr * (1.f / 32.f) + EPS);
; #pragma unroll
;               for (int j = 0; j < 8; ++j) { const float av = x[2][j] * rq * qgain[64 + 8 * g4 + j];
;                   auto rr = __builtin_amdgcn_permlane16_swap(__float_as_uint(av), __float_as_uint(av), false, false);
;                   const float other = (g4 & 1) ? __uint_as_float(rr[0]) : __uint_as_float(rr[1]);
;                   float cc = 1.f, sg = 0.f;
;                   if (lat) { const f32x2 cs = rope[((g4 & 2) ? pcol : prow) * 8 + j]; cc = cs.x; sg = (g4 & 1) ? cs.y : -cs.y; }
;                   x[2][j] = av * cc + other * sg; }
;           }
; #pragma unroll
;           for (int ds = 0; ds < NDS; ++ds) { u32x4 w;
; #pragma unroll
;               for (int i = 0; i < 4; ++i) w[i] = cvtpk(x[ds][2 * i] * c2, x[ds][2 * i + 1] * c2);
;               qf[qb * NDS + ds] = __builtin_bit_cast(bf16x8, w); }
	v_and_b32_e32 v155, 0xffff0000, v2
	v_lshlrev_b32_e32 v154, 16, v2
	v_mul_f32_e32 v2, v155, v155
	v_and_b32_e32 v139, 0xffff0000, v13
	v_lshlrev_b32_e32 v138, 16, v13
	v_and_b32_e32 v141, 0xffff0000, v12
	v_lshlrev_b32_e32 v140, 16, v12
	v_and_b32_e32 v13, 0xffff0000, v3
	v_lshlrev_b32_e32 v12, 16, v3
	v_pk_fma_f32 v[2:3], v[154:155], v[154:155], v[2:3] op_sel_hi:[1,1,0]
	v_and_b32_e32 v153, 0xffff0000, v4
	v_lshlrev_b32_e32 v152, 16, v4
	v_pk_fma_f32 v[2:3], v[12:13], v[12:13], v[2:3]
	v_mul_f32_e32 v4, v13, v13
	v_pk_add_f32 v[2:3], v[4:5], v[2:3] op_sel_hi:[0,1]
	v_pk_fma_f32 v[2:3], v[152:153], v[152:153], v[2:3]
	v_mul_f32_e32 v4, v153, v153
	v_and_b32_e32 v151, 0xffff0000, v5
	v_lshlrev_b32_e32 v150, 16, v5
	v_pk_add_f32 v[2:3], v[4:5], v[2:3] op_sel_hi:[0,1]
	v_pk_fma_f32 v[2:3], v[150:151], v[150:151], v[2:3]
	v_mul_f32_e32 v4, v151, v151
	v_pk_add_f32 v[2:3], v[4:5], v[2:3] op_sel_hi:[0,1]
	v_mov_b32_e32 v3, v2
	s_nop 1
	v_permlane16_swap_b32_e32 v2, v3
	v_add_f32_e32 v6, v2, v3
	v_mov_b32_e32 v8, v6
	s_nop 1
	v_permlane32_swap_b32_e32 v6, v8
	v_pk_add_f32 v[2:3], v[6:7], v[8:9]
	v_mov_b32_e32 v97, v95
	v_pk_fma_f32 v[6:7], v[2:3], s[6:7], v[106:107] op_sel_hi:[1,1,0]
	s_nop 0
	v_permlane32_swap_b32_e32 v95, v97
	v_mul_f32_e32 v2, 0x4b800000, v7
	v_cmp_gt_f32_e32 vcc, s95, v7
	s_waitcnt vmcnt(7)
	v_and_b32_e32 v111, 0xffff0000, v25
	v_lshlrev_b32_e32 v110, 16, v25
	v_cndmask_b32_e32 v2, v7, v2, vcc
	v_rsq_f32_e32 v2, v2
	v_and_b32_e32 v117, 0xffff0000, v24
	v_lshlrev_b32_e32 v116, 16, v24
	v_and_b32_e32 v25, 0xffff0000, v11
	v_mul_f32_e32 v3, 0x45800000, v2
	v_cndmask_b32_e32 v94, v2, v3, vcc
	s_waitcnt vmcnt(5)
	v_pk_mul_f32 v[2:3], v[94:95], v[32:33] op_sel_hi:[0,1]
	v_pk_mul_f32 v[2:3], v[2:3], v[16:17]
	s_waitcnt vmcnt(4)
	v_pk_mul_f32 v[8:9], v[38:39], v[94:95] op_sel_hi:[1,0]
	v_pk_mul_f32 v[2:3], v[2:3], s[82:83] op_sel_hi:[1,0]
	v_pk_mul_f32 v[8:9], v[8:9], v[124:125]
	v_cvt_pk_bf16_f32 v5, v2, v3
	v_pk_mul_f32 v[2:3], v[94:95], v[30:31] op_sel_hi:[0,1]
	v_pk_mul_f32 v[2:3], v[2:3], v[120:121]
	v_pk_mul_f32 v[8:9], v[8:9], s[82:83] op_sel_hi:[1,0]
	v_pk_mul_f32 v[2:3], v[2:3], s[82:83] op_sel_hi:[1,0]
	s_waitcnt vmcnt(3)
	v_pk_mul_f32 v[16:17], v[46:47], v[94:95] op_sel_hi:[1,0]
	v_cvt_pk_bf16_f32 v4, v2, v3
	v_pk_mul_f32 v[2:3], v[94:95], v[40:41] op_sel_hi:[0,1]
	v_pk_mul_f32 v[2:3], v[2:3], v[122:123]
	v_pk_mul_f32 v[16:17], v[16:17], v[132:133]
	v_pk_mul_f32 v[2:3], v[2:3], s[82:83] op_sel_hi:[1,0]
	v_pk_mul_f32 v[16:17], v[16:17], s[82:83] op_sel_hi:[1,0]
	v_cvt_pk_bf16_f32 v3, v2, v3
	v_cvt_pk_bf16_f32 v2, v8, v9
	v_pk_mul_f32 v[8:9], v[48:49], v[94:95] op_sel_hi:[1,0]
	v_lshlrev_b32_e32 v24, 16, v11
	v_pk_mul_f32 v[8:9], v[8:9], v[126:127]
	v_mul_f32_e32 v11, 0x4b800000, v6
	v_pk_mul_f32 v[8:9], v[8:9], s[82:83] op_sel_hi:[1,0]
	v_cmp_gt_f32_e32 vcc, s95, v6
	v_cvt_pk_bf16_f32 v9, v8, v9
	v_cvt_pk_bf16_f32 v8, v16, v17
	s_waitcnt vmcnt(2)
	v_pk_mul_f32 v[16:17], v[52:53], v[94:95] op_sel_hi:[1,0]
	v_cndmask_b32_e32 v6, v6, v11, vcc
	v_pk_mul_f32 v[16:17], v[16:17], v[134:135]
	v_rsq_f32_e32 v11, v6
	v_pk_mul_f32 v[16:17], v[16:17], s[82:83] op_sel_hi:[1,0]
	v_and_b32_e32 v83, 0xffff0000, v45
	v_cvt_pk_bf16_f32 v7, v16, v17
	v_pk_mul_f32 v[16:17], v[50:51], v[94:95] op_sel_hi:[1,0]
	v_lshlrev_b32_e32 v82, 16, v45
	v_pk_mul_f32 v[16:17], v[16:17], v[136:137]
	v_and_b32_e32 v91, 0xffff0000, v44
	v_pk_mul_f32 v[16:17], v[16:17], s[82:83] op_sel_hi:[1,0]
	v_lshlrev_b32_e32 v90, 16, v44
	v_cvt_pk_bf16_f32 v6, v16, v17
	v_mul_f32_e32 v16, 0x45800000, v11
	v_cndmask_b32_e32 v16, v11, v16, vcc
	v_pk_mul_f32 v[122:123], v[16:17], v[12:13] op_sel_hi:[0,1]
	v_pk_mul_f32 v[12:13], v[16:17], v[150:151] op_sel_hi:[0,1]
	s_waitcnt vmcnt(1)
	v_pk_mul_f32 v[12:13], v[12:13], v[56:57]
	v_and_b32_e32 v45, 0xffff0000, v23
	v_lshlrev_b32_e32 v44, 16, v23
	v_pk_mul_f32 v[120:121], v[16:17], v[154:155] op_sel_hi:[0,1]
	v_pk_mul_f32 v[124:125], v[16:17], v[152:153] op_sel_hi:[0,1]
	v_mov_b32_e32 v11, v12
	v_mov_b32_e32 v16, v12
	v_mov_b32_e32 v17, v13
	v_mov_b32_e32 v23, v13
	v_permlane16_swap_b32_e32 v11, v16
	s_nop 0
	v_permlane16_swap_b32_e32 v17, v23
	v_cmp_eq_u32_e32 vcc, 0, v112
	v_and_b32_e32 v99, 0xffff0000, v43
	v_lshlrev_b32_e32 v98, 16, v43
	v_cndmask_b32_e32 v17, v17, v23, vcc
	v_cndmask_b32_e32 v16, v11, v16, vcc
	v_pk_fma_f32 v[12:13], v[16:17], 0, v[12:13] op_sel_hi:[1,0,1]
	v_pk_mul_f32 v[16:17], v[54:55], v[124:125]
	v_pk_mul_f32 v[12:13], v[12:13], s[82:83] op_sel_hi:[1,0]
	v_mov_b32_e32 v11, v16
	v_cvt_pk_bf16_f32 v13, v12, v13
	v_mov_b32_e32 v12, v16
	v_mov_b32_e32 v23, v17
	v_mov_b32_e32 v43, v17
	v_permlane16_swap_b32_e32 v11, v12
	s_nop 0
	v_permlane16_swap_b32_e32 v23, v43
	v_cndmask_b32_e32 v125, v23, v43, vcc
	v_cndmask_b32_e32 v124, v11, v12, vcc
	v_pk_fma_f32 v[16:17], v[124:125], 0, v[16:17] op_sel_hi:[1,0,1]
	v_mov_b32_e32 v131, v129
	v_pk_mul_f32 v[16:17], v[16:17], s[82:83] op_sel_hi:[1,0]
	s_nop 0
	v_permlane32_swap_b32_e32 v129, v131
	v_cvt_pk_bf16_f32 v12, v16, v17
	s_waitcnt vmcnt(0)
; __device__ __forceinline__ unsigned cvtpk(float lo, float hi) { f32x2 v = {lo, hi}; bf16x2_t b = __builtin_convertvector(v, bf16x2_t); return __builtin_bit_cast(unsigned, b); }
; template <int DQK, int DV, bool LEAD> ...
;     ...
;           } else {
;               float sr = 0.f;
; #pragma unroll
;               for (int j = 0; j < 8; ++j) sr += x[2][j] * x[2][j];
;               sr = lanes4_sum(sr);
;               const float rq = rsqrtf(sr * (1.f / 32.f) + EPS);
; #pragma unroll
;               for (int j = 0; j < 8; ++j) { const float av = x[2][j] * rq * qgain[64 + 8 * g4 + j];
;                   auto rr = __builtin_amdgcn_permlane16_swap(__float_as_uint(av), __float_as_uint(av), false, false);
;                   const float other = (g4 & 1) ? __uint_as_float(rr[0]) : __uint_as_float(rr[1]);
;                   float cc = 1.f, sg = 0.f;
;                   if (lat) { const f32x2 cs = rope[((g4 & 2) ? pcol : prow) * 8 + j]; cc = cs.x; sg = (g4 & 1) ? cs.y : -cs.y; }
;                   x[2][j] = av * cc + other * sg; }
;           }
; #pragma unroll
;           for (int ds = 0; ds < NDS; ++ds) { u32x4 w;
; #pragma unroll
;               for (int i = 0; i < 4; ++i) w[i] = cvtpk(x[ds][2 * i] * c2, x[ds][2 * i + 1] * c2);
;               qf[qb * NDS + ds] = __builtin_bit_cast(bf16x8, w); }
	v_pk_mul_f32 v[16:17], v[60:61], v[122:123]
	v_mov_b32_e32 v115, v113
	v_mov_b32_e32 v11, v16
	v_mov_b32_e32 v23, v16
	v_mov_b32_e32 v43, v17
	v_mov_b32_e32 v94, v17
	v_permlane16_swap_b32_e32 v11, v23
	s_nop 0
	v_permlane16_swap_b32_e32 v43, v94
	v_cndmask_b32_e32 v123, v43, v94, vcc
	v_cndmask_b32_e32 v122, v11, v23, vcc
	v_pk_fma_f32 v[16:17], v[122:123], 0, v[16:17] op_sel_hi:[1,0,1]
	v_and_b32_e32 v123, 0xffff0000, v10
	v_pk_mul_f32 v[16:17], v[16:17], s[82:83] op_sel_hi:[1,0]
	v_lshlrev_b32_e32 v122, 16, v10
	v_cvt_pk_bf16_f32 v11, v16, v17
	v_mul_f32_e32 v10, v123, v123
	v_pk_fma_f32 v[124:125], v[122:123], v[122:123], v[10:11] op_sel_hi:[1,1,0]
	v_mul_f32_e32 v10, v25, v25
	v_pk_fma_f32 v[124:125], v[24:25], v[24:25], v[124:125]
	v_pk_mul_f32 v[16:17], v[58:59], v[120:121]
	v_pk_add_f32 v[124:125], v[10:11], v[124:125] op_sel_hi:[0,1]
	v_pk_fma_f32 v[124:125], v[140:141], v[140:141], v[124:125]
	v_mul_f32_e32 v10, v141, v141
	v_pk_add_f32 v[124:125], v[10:11], v[124:125] op_sel_hi:[0,1]
	v_pk_fma_f32 v[124:125], v[138:139], v[138:139], v[124:125]
	v_mul_f32_e32 v10, v139, v139
	v_pk_add_f32 v[124:125], v[10:11], v[124:125] op_sel_hi:[0,1]
	v_mov_b32_e32 v10, v124
	s_nop 1
	v_permlane16_swap_b32_e32 v124, v10
	v_add_f32_e32 v128, v124, v10
	v_mov_b32_e32 v130, v128
	s_nop 1
	v_permlane32_swap_b32_e32 v128, v130
	v_pk_add_f32 v[124:125], v[128:129], v[130:131]
	v_mov_b32_e32 v23, v16
	v_pk_fma_f32 v[124:125], v[124:125], s[6:7], v[106:107] op_sel_hi:[1,1,0]
	v_mov_b32_e32 v43, v16
	v_mul_f32_e32 v10, 0x4b800000, v125
	v_cmp_gt_f32_e64 s[4:5], s95, v125
	v_permlane16_swap_b32_e32 v23, v43
	v_mov_b32_e32 v94, v17
	v_mov_b32_e32 v96, v17
	v_cndmask_b32_e64 v10, v125, v10, s[4:5]
	s_nop 0
	v_permlane16_swap_b32_e32 v94, v96
	v_cndmask_b32_e32 v120, v23, v43, vcc
	v_rsq_f32_e32 v23, v10
	v_cndmask_b32_e32 v121, v94, v96, vcc
	v_pk_fma_f32 v[16:17], v[120:121], 0, v[16:17] op_sel_hi:[1,0,1]
	v_permlane32_swap_b32_e32 v113, v115
	v_pk_mul_f32 v[16:17], v[16:17], s[82:83] op_sel_hi:[1,0]
	s_nop 0
	v_cvt_pk_bf16_f32 v10, v16, v17
	v_mul_f32_e32 v16, 0x45800000, v23
	v_cndmask_b32_e64 v94, v23, v16, s[4:5]
	v_pk_mul_f32 v[16:17], v[32:33], v[94:95] op_sel_hi:[1,0]
	v_cmp_gt_f32_e64 s[4:5], s95, v124
	v_pk_mul_f32 v[14:15], v[16:17], v[14:15]
	s_nop 0
	v_pk_mul_f32 v[14:15], v[14:15], s[82:83] op_sel_hi:[1,0]
	s_nop 0
	v_cvt_pk_bf16_f32 v17, v14, v15
	v_pk_mul_f32 v[14:15], v[30:31], v[94:95] op_sel_hi:[1,0]
	s_nop 0
	v_pk_mul_f32 v[14:15], v[14:15], v[18:19]
	v_pk_mul_f32 v[18:19], v[38:39], v[94:95] op_sel_hi:[1,0]
	v_pk_mul_f32 v[14:15], v[14:15], s[82:83] op_sel_hi:[1,0]
	v_pk_mul_f32 v[18:19], v[18:19], v[28:29]
	v_cvt_pk_bf16_f32 v16, v14, v15
	v_pk_mul_f32 v[14:15], v[40:41], v[94:95] op_sel_hi:[1,0]
	v_pk_mul_f32 v[18:19], v[18:19], s[82:83] op_sel_hi:[1,0]
	v_pk_mul_f32 v[14:15], v[14:15], v[20:21]
	v_pk_mul_f32 v[28:29], v[50:51], v[94:95] op_sel_hi:[1,0]
	v_pk_mul_f32 v[14:15], v[14:15], s[82:83] op_sel_hi:[1,0]
	v_pk_mul_f32 v[28:29], v[28:29], v[118:119]
	v_cvt_pk_bf16_f32 v15, v14, v15
	v_cvt_pk_bf16_f32 v14, v18, v19
	v_pk_mul_f32 v[18:19], v[48:49], v[94:95] op_sel_hi:[1,0]
	v_pk_mul_f32 v[28:29], v[28:29], s[82:83] op_sel_hi:[1,0]
	v_pk_mul_f32 v[18:19], v[18:19], v[102:103]
	s_nop 0
	v_pk_mul_f32 v[18:19], v[18:19], s[82:83] op_sel_hi:[1,0]
	s_nop 0
	v_cvt_pk_bf16_f32 v21, v18, v19
	v_pk_mul_f32 v[18:19], v[46:47], v[94:95] op_sel_hi:[1,0]
	s_nop 0
	v_pk_mul_f32 v[18:19], v[18:19], v[104:105]
	s_nop 0
	v_pk_mul_f32 v[18:19], v[18:19], s[82:83] op_sel_hi:[1,0]
	s_nop 0
	v_cvt_pk_bf16_f32 v20, v18, v19
	v_pk_mul_f32 v[18:19], v[52:53], v[94:95] op_sel_hi:[1,0]
	s_nop 0
	v_pk_mul_f32 v[18:19], v[18:19], v[108:109]
	s_nop 0
	v_pk_mul_f32 v[18:19], v[18:19], s[82:83] op_sel_hi:[1,0]
	s_nop 0
	v_cvt_pk_bf16_f32 v19, v18, v19
	v_mul_f32_e32 v18, 0x4b800000, v124
	v_cndmask_b32_e64 v18, v124, v18, s[4:5]
	v_rsq_f32_e32 v23, v18
	v_cvt_pk_bf16_f32 v18, v28, v29
	v_mul_f32_e32 v28, 0x45800000, v23
	v_cndmask_b32_e64 v28, v23, v28, s[4:5]
	v_pk_mul_f32 v[104:105], v[28:29], v[24:25] op_sel_hi:[0,1]
	v_pk_mul_f32 v[24:25], v[28:29], v[138:139] op_sel_hi:[0,1]
	v_pk_mul_f32 v[24:25], v[56:57], v[24:25]
	v_pk_mul_f32 v[102:103], v[28:29], v[122:123] op_sel_hi:[0,1]
	v_pk_mul_f32 v[108:109], v[28:29], v[140:141] op_sel_hi:[0,1]
	v_mov_b32_e32 v23, v24
	v_mov_b32_e32 v28, v24
	v_mov_b32_e32 v29, v25
	v_mov_b32_e32 v43, v25
	v_permlane16_swap_b32_e32 v23, v28
	s_nop 0
	v_permlane16_swap_b32_e32 v29, v43
	v_cndmask_b32_e32 v29, v29, v43, vcc
	v_cndmask_b32_e32 v28, v23, v28, vcc
	v_pk_fma_f32 v[24:25], v[28:29], 0, v[24:25] op_sel_hi:[1,0,1]
	v_pk_mul_f32 v[28:29], v[54:55], v[108:109]
	v_pk_mul_f32 v[24:25], v[24:25], s[82:83] op_sel_hi:[1,0]
	v_mov_b32_e32 v23, v28
	v_cvt_pk_bf16_f32 v25, v24, v25
	v_mov_b32_e32 v24, v28
	v_mov_b32_e32 v43, v29
	v_mov_b32_e32 v94, v29
	v_permlane16_swap_b32_e32 v23, v24
	s_nop 0
	v_permlane16_swap_b32_e32 v43, v94
	v_cndmask_b32_e32 v109, v43, v94, vcc
	v_cndmask_b32_e32 v108, v23, v24, vcc
	v_pk_fma_f32 v[28:29], v[108:109], 0, v[28:29] op_sel_hi:[1,0,1]
	s_nop 0
	v_pk_mul_f32 v[28:29], v[28:29], s[82:83] op_sel_hi:[1,0]
	s_nop 0
	v_cvt_pk_bf16_f32 v24, v28, v29
	v_pk_mul_f32 v[28:29], v[60:61], v[104:105]
	s_nop 0
	v_mov_b32_e32 v23, v28
	v_mov_b32_e32 v43, v28
	v_mov_b32_e32 v94, v29
	v_mov_b32_e32 v96, v29
	v_permlane16_swap_b32_e32 v23, v43
	s_nop 0
	v_permlane16_swap_b32_e32 v94, v96
	v_cndmask_b32_e32 v105, v94, v96, vcc
	v_cndmask_b32_e32 v104, v23, v43, vcc
	v_pk_fma_f32 v[28:29], v[104:105], 0, v[28:29] op_sel_hi:[1,0,1]
	v_and_b32_e32 v105, 0xffff0000, v22
	v_pk_mul_f32 v[28:29], v[28:29], s[82:83] op_sel_hi:[1,0]
; template <int DQK, int DV, bool LEAD> ...
;     ...
;           float sn = 0.f;
; #pragma unroll
;           for (int ds = 0; ds < 2; ++ds)
; #pragma unroll
;               for (int j = 0; j < 8; ++j) sn += x[ds][j] * x[ds][j];
;           sn = lanes4_sum(sn);
;           const float rn = rsqrtf(sn * (1.f / 64.f) + EPS);
; #pragma unroll
;           for (int ds = 0; ds < 2; ++ds)
; #pragma unroll
;               for (int j = 0; j < 8; ++j) x[ds][j] *= rn * qgain[32 * ds + 8 * g4 + j];
;           if constexpr (DQK == 64) {
; #pragma unroll
;               for (int ds = 0; ds < 2; ++ds)
; #pragma unroll
;                   for (int j = 0; j < 8; ++j) {
;                       auto rr = __builtin_amdgcn_permlane32_swap(__float_as_uint(x[ds][j]), __float_as_uint(x[ds][j]), false, false);
;                       const float other = hi ? __uint_as_float(rr[0]) : __uint_as_float(rr[1]);
;                       float cc = 1.f, sg = 0.f;
;                       if (lat) { const f32x2 cs = rope[(ds ? pcol : prow) * 16 + 8 * (g4 & 1) + j]; cc = cs.x; sg = hi ? cs.y : -cs.y; }
;                       x[ds][j] = x[ds][j] * cc + other * sg; }
;           } else {
;               float sr = 0.f;
; #pragma unroll
;               for (int j = 0; j < 8; ++j) sr += x[2][j] * x[2][j];
;               sr = lanes4_sum(sr);
;               const float rq = rsqrtf(sr * (1.f / 32.f) + EPS);
; #pragma unroll
;               for (int j = 0; j < 8; ++j) { const float av = x[2][j] * rq * qgain[64 + 8 * g4 + j];
;                   auto rr = __builtin_amdgcn_permlane16_swap(__float_as_uint(av), __float_as_uint(av), false, false);
;                   const float other = (g4 & 1) ? __uint_as_float(rr[0]) : __uint_as_float(rr[1]);
;                   float cc = 1.f, sg = 0.f;
;                   if (lat) { const f32x2 cs = rope[((g4 & 2) ? pcol : prow) * 8 + j]; cc = cs.x; sg = (g4 & 1) ? cs.y : -cs.y; }
;                   x[2][j] = av * cc + other * sg; }
;           }
; #pragma unroll
;           for (int ds = 0; ds < NDS; ++ds) { u32x4 w;
; #pragma unroll
;               for (int i = 0; i < 4; ++i) w[i] = cvtpk(x[ds][2 * i] * c2, x[ds][2 * i + 1] * c2);
;               qf[qb * NDS + ds] = __builtin_bit_cast(bf16x8, w); }
	v_lshlrev_b32_e32 v104, 16, v22
	v_cvt_pk_bf16_f32 v23, v28, v29
	v_mul_f32_e32 v22, v105, v105
	v_pk_fma_f32 v[108:109], v[104:105], v[104:105], v[22:23] op_sel_hi:[1,1,0]
	v_mul_f32_e32 v22, v45, v45
	v_pk_fma_f32 v[108:109], v[44:45], v[44:45], v[108:109]
	v_pk_mul_f32 v[28:29], v[58:59], v[102:103]
	v_pk_add_f32 v[108:109], v[22:23], v[108:109] op_sel_hi:[0,1]
	v_pk_fma_f32 v[108:109], v[116:117], v[116:117], v[108:109]
	v_mul_f32_e32 v22, v117, v117
	v_pk_add_f32 v[108:109], v[22:23], v[108:109] op_sel_hi:[0,1]
	v_pk_fma_f32 v[108:109], v[110:111], v[110:111], v[108:109]
	v_mul_f32_e32 v22, v111, v111
	v_pk_add_f32 v[108:109], v[22:23], v[108:109] op_sel_hi:[0,1]
	v_mov_b32_e32 v22, v108
	s_nop 1
	v_permlane16_swap_b32_e32 v108, v22
	v_add_f32_e32 v112, v108, v22
	v_mov_b32_e32 v114, v112
	s_nop 1
	v_permlane32_swap_b32_e32 v112, v114
	v_pk_add_f32 v[108:109], v[112:113], v[114:115]
	v_mov_b32_e32 v43, v28
	v_pk_fma_f32 v[108:109], v[108:109], s[6:7], v[106:107] op_sel_hi:[1,1,0]
	v_mov_b32_e32 v94, v28
	v_mov_b32_e32 v96, v29
	v_mov_b32_e32 v102, v29
	v_mul_f32_e32 v22, 0x4b800000, v109
	v_cmp_gt_f32_e64 s[4:5], s95, v109
	v_permlane16_swap_b32_e32 v43, v94
	v_permlane16_swap_b32_e32 v96, v102
	v_cndmask_b32_e64 v22, v109, v22, s[4:5]
	v_cndmask_b32_e32 v103, v96, v102, vcc
	v_cndmask_b32_e32 v102, v43, v94, vcc
	v_rsq_f32_e32 v43, v22
	v_pk_fma_f32 v[28:29], v[102:103], 0, v[28:29] op_sel_hi:[1,0,1]
	s_nop 0
	v_pk_mul_f32 v[28:29], v[28:29], s[82:83] op_sel_hi:[1,0]
	s_nop 0
	v_cvt_pk_bf16_f32 v22, v28, v29
	v_mul_f32_e32 v28, 0x45800000, v43
	v_cndmask_b32_e64 v94, v43, v28, s[4:5]
	v_pk_mul_f32 v[28:29], v[32:33], v[94:95] op_sel_hi:[1,0]
	v_cmp_gt_f32_e64 s[4:5], s95, v108
	v_pk_mul_f32 v[26:27], v[28:29], v[26:27]
	s_nop 0
	v_pk_mul_f32 v[26:27], v[26:27], s[82:83] op_sel_hi:[1,0]
	s_nop 0
	v_cvt_pk_bf16_f32 v29, v26, v27
	v_pk_mul_f32 v[26:27], v[30:31], v[94:95] op_sel_hi:[1,0]
	s_nop 0
	v_pk_mul_f32 v[26:27], v[26:27], v[34:35]
	v_pk_mul_f32 v[34:35], v[38:39], v[94:95] op_sel_hi:[1,0]
	v_pk_mul_f32 v[26:27], v[26:27], s[82:83] op_sel_hi:[1,0]
	v_pk_mul_f32 v[34:35], v[34:35], v[80:81]
	v_cvt_pk_bf16_f32 v28, v26, v27
	v_pk_mul_f32 v[26:27], v[40:41], v[94:95] op_sel_hi:[1,0]
	v_pk_mul_f32 v[34:35], v[34:35], s[82:83] op_sel_hi:[1,0]
	v_pk_mul_f32 v[26:27], v[26:27], v[36:37]
	v_pk_mul_f32 v[80:81], v[50:51], v[94:95] op_sel_hi:[1,0]
	v_pk_mul_f32 v[26:27], v[26:27], s[82:83] op_sel_hi:[1,0]
	v_pk_mul_f32 v[80:81], v[80:81], v[100:101]
	v_cvt_pk_bf16_f32 v27, v26, v27
	v_cvt_pk_bf16_f32 v26, v34, v35
	v_pk_mul_f32 v[34:35], v[48:49], v[94:95] op_sel_hi:[1,0]
	v_pk_mul_f32 v[80:81], v[80:81], s[82:83] op_sel_hi:[1,0]
	v_pk_mul_f32 v[34:35], v[34:35], v[84:85]
	s_nop 0
	v_pk_mul_f32 v[34:35], v[34:35], s[82:83] op_sel_hi:[1,0]
	s_nop 0
	v_cvt_pk_bf16_f32 v37, v34, v35
	v_pk_mul_f32 v[34:35], v[46:47], v[94:95] op_sel_hi:[1,0]
	s_nop 0
	v_pk_mul_f32 v[34:35], v[34:35], v[86:87]
	s_nop 0
	v_pk_mul_f32 v[34:35], v[34:35], s[82:83] op_sel_hi:[1,0]
	s_nop 0
	v_cvt_pk_bf16_f32 v36, v34, v35
	v_pk_mul_f32 v[34:35], v[52:53], v[94:95] op_sel_hi:[1,0]
	s_nop 0
	v_pk_mul_f32 v[34:35], v[34:35], v[92:93]
	s_nop 0
	v_pk_mul_f32 v[34:35], v[34:35], s[82:83] op_sel_hi:[1,0]
	s_nop 0
	v_cvt_pk_bf16_f32 v35, v34, v35
	v_mul_f32_e32 v34, 0x4b800000, v108
	v_cndmask_b32_e64 v34, v108, v34, s[4:5]
	v_rsq_f32_e32 v43, v34
	v_cvt_pk_bf16_f32 v34, v80, v81
	v_mul_f32_e32 v80, 0x45800000, v43
	v_cndmask_b32_e64 v80, v43, v80, s[4:5]
	v_pk_mul_f32 v[86:87], v[80:81], v[44:45] op_sel_hi:[0,1]
	v_pk_mul_f32 v[44:45], v[80:81], v[110:111] op_sel_hi:[0,1]
	v_pk_mul_f32 v[44:45], v[56:57], v[44:45]
	v_pk_mul_f32 v[84:85], v[80:81], v[104:105] op_sel_hi:[0,1]
	v_pk_mul_f32 v[92:93], v[80:81], v[116:117] op_sel_hi:[0,1]
	v_mov_b32_e32 v43, v44
	v_mov_b32_e32 v80, v44
	v_mov_b32_e32 v81, v45
	v_mov_b32_e32 v94, v45
	v_permlane16_swap_b32_e32 v43, v80
	s_nop 0
	v_permlane16_swap_b32_e32 v81, v94
	v_cndmask_b32_e32 v81, v81, v94, vcc
	v_cndmask_b32_e32 v80, v43, v80, vcc
	v_pk_fma_f32 v[44:45], v[80:81], 0, v[44:45] op_sel_hi:[1,0,1]
	v_pk_mul_f32 v[80:81], v[54:55], v[92:93]
	v_pk_mul_f32 v[44:45], v[44:45], s[82:83] op_sel_hi:[1,0]
	v_mov_b32_e32 v43, v80
	v_cvt_pk_bf16_f32 v45, v44, v45
	v_mov_b32_e32 v44, v80
	v_mov_b32_e32 v92, v81
	v_mov_b32_e32 v93, v81
	v_permlane16_swap_b32_e32 v43, v44
	s_nop 0
	v_permlane16_swap_b32_e32 v92, v93
	v_cndmask_b32_e32 v93, v92, v93, vcc
	v_cndmask_b32_e32 v92, v43, v44, vcc
	v_pk_fma_f32 v[80:81], v[92:93], 0, v[80:81] op_sel_hi:[1,0,1]
	s_nop 0
	v_pk_mul_f32 v[80:81], v[80:81], s[82:83] op_sel_hi:[1,0]
	s_nop 0
	v_cvt_pk_bf16_f32 v44, v80, v81
	v_pk_mul_f32 v[80:81], v[60:61], v[86:87]
	s_nop 0
	v_mov_b32_e32 v43, v80
	v_mov_b32_e32 v86, v80
	v_mov_b32_e32 v87, v81
	v_mov_b32_e32 v92, v81
	v_permlane16_swap_b32_e32 v43, v86
	s_nop 0
	v_permlane16_swap_b32_e32 v87, v92
	v_cndmask_b32_e32 v87, v87, v92, vcc
	v_cndmask_b32_e32 v86, v43, v86, vcc
	v_pk_fma_f32 v[80:81], v[86:87], 0, v[80:81] op_sel_hi:[1,0,1]
	s_nop 0
	v_pk_mul_f32 v[80:81], v[80:81], s[82:83] op_sel_hi:[1,0]
	s_nop 0
	v_cvt_pk_bf16_f32 v43, v80, v81
	v_pk_mul_f32 v[80:81], v[58:59], v[84:85]
	s_nop 0
	v_mov_b32_e32 v85, v81
	v_mov_b32_e32 v87, v81
	v_mov_b32_e32 v84, v80
	v_mov_b32_e32 v86, v80
	v_permlane16_swap_b32_e32 v85, v87
	s_nop 0
	v_permlane16_swap_b32_e32 v84, v86
	v_cndmask_b32_e32 v85, v85, v87, vcc
	v_and_b32_e32 v87, 0xffff0000, v42
	v_cndmask_b32_e32 v84, v84, v86, vcc
	v_lshlrev_b32_e32 v86, 16, v42
	v_mul_f32_e32 v42, v87, v87
	v_pk_fma_f32 v[92:93], v[86:87], v[86:87], v[42:43] op_sel_hi:[1,1,0]
	v_mul_f32_e32 v42, v99, v99
; template <int DQK, int DV, bool LEAD> ...
;     ...
;           float sn = 0.f;
; #pragma unroll
;           for (int ds = 0; ds < 2; ++ds)
; #pragma unroll
;               for (int j = 0; j < 8; ++j) sn += x[ds][j] * x[ds][j];
;           sn = lanes4_sum(sn);
;           const float rn = rsqrtf(sn * (1.f / 64.f) + EPS);
; #pragma unroll
;           for (int ds = 0; ds < 2; ++ds)
; #pragma unroll
;               for (int j = 0; j < 8; ++j) x[ds][j] *= rn * qgain[32 * ds + 8 * g4 + j];
;           if constexpr (DQK == 64) {
; #pragma unroll
;               for (int ds = 0; ds < 2; ++ds)
; #pragma unroll
;                   for (int j = 0; j < 8; ++j) {
;                       auto rr = __builtin_amdgcn_permlane32_swap(__float_as_uint(x[ds][j]), __float_as_uint(x[ds][j]), false, false);
;                       const float other = hi ? __uint_as_float(rr[0]) : __uint_as_float(rr[1]);
;                       float cc = 1.f, sg = 0.f;
;                       if (lat) { const f32x2 cs = rope[(ds ? pcol : prow) * 16 + 8 * (g4 & 1) + j]; cc = cs.x; sg = hi ? cs.y : -cs.y; }
;                       x[ds][j] = x[ds][j] * cc + other * sg; }
;           } else {
;               float sr = 0.f;
; #pragma unroll
;               for (int j = 0; j < 8; ++j) sr += x[2][j] * x[2][j];
;               sr = lanes4_sum(sr);
;               const float rq = rsqrtf(sr * (1.f / 32.f) + EPS);
; #pragma unroll
;               for (int j = 0; j < 8; ++j) { const float av = x[2][j] * rq * qgain[64 + 8 * g4 + j];
;                   auto rr = __builtin_amdgcn_permlane16_swap(__float_as_uint(av), __float_as_uint(av), false, false);
;                   const float other = (g4 & 1) ? __uint_as_float(rr[0]) : __uint_as_float(rr[1]);
;                   float cc = 1.f, sg = 0.f;
;                   if (lat) { const f32x2 cs = rope[((g4 & 2) ? pcol : prow) * 8 + j]; cc = cs.x; sg = (g4 & 1) ? cs.y : -cs.y; }
;                   x[2][j] = av * cc + other * sg; }
;           }
; #pragma unroll
;           for (int ds = 0; ds < NDS; ++ds) { u32x4 w;
; #pragma unroll
;               for (int i = 0; i < 4; ++i) w[i] = cvtpk(x[ds][2 * i] * c2, x[ds][2 * i + 1] * c2);
;               qf[qb * NDS + ds] = __builtin_bit_cast(bf16x8, w); }
;       }
; #pragma unroll
;       for (int d0 = 0; d0 < NQB * NDS; ++d0) asm volatile("" : "+v"(qf[d0])); }
;     wait_bar<0>();
	v_pk_fma_f32 v[92:93], v[98:99], v[98:99], v[92:93]
	v_pk_fma_f32 v[80:81], v[84:85], 0, v[80:81] op_sel_hi:[1,0,1]
	v_pk_add_f32 v[92:93], v[42:43], v[92:93] op_sel_hi:[0,1]
	v_pk_fma_f32 v[92:93], v[90:91], v[90:91], v[92:93]
	v_mul_f32_e32 v42, v91, v91
	v_pk_add_f32 v[92:93], v[42:43], v[92:93] op_sel_hi:[0,1]
	v_pk_fma_f32 v[92:93], v[82:83], v[82:83], v[92:93]
	v_mul_f32_e32 v42, v83, v83
	v_pk_add_f32 v[92:93], v[42:43], v[92:93] op_sel_hi:[0,1]
	v_mov_b32_e32 v42, v92
	s_nop 1
	v_permlane16_swap_b32_e32 v92, v42
	v_add_f32_e32 v94, v92, v42
	v_mov_b32_e32 v96, v94
	s_nop 1
	v_permlane32_swap_b32_e32 v94, v96
	v_pk_add_f32 v[92:93], v[94:95], v[96:97]
	v_pk_mul_f32 v[80:81], v[80:81], s[82:83] op_sel_hi:[1,0]
	v_pk_fma_f32 v[92:93], v[92:93], s[6:7], v[106:107] op_sel_hi:[1,1,0]
	s_mov_b64 s[6:7], 0x60000
	v_mul_f32_e32 v42, 0x4b800000, v93
	v_cmp_gt_f32_e64 s[4:5], s95, v93
	v_lshl_add_u64 v[192:193], v[62:63], 0, s[6:7]
	s_mov_b64 s[6:7], 0x3000
	v_cndmask_b32_e64 v42, v93, v42, s[4:5]
	v_rsq_f32_e32 v93, v42
	v_cvt_pk_bf16_f32 v42, v80, v81
	v_lshl_add_u64 v[204:205], v[64:65], 0, s[6:7]
	v_mul_f32_e32 v80, 0x45800000, v93
	v_cndmask_b32_e64 v80, v93, v80, s[4:5]
	v_pk_mul_f32 v[50:51], v[50:51], v[80:81] op_sel_hi:[1,0]
	v_pk_mul_f32 v[52:53], v[52:53], v[80:81] op_sel_hi:[1,0]
	v_pk_mul_f32 v[30:31], v[30:31], v[80:81] op_sel_hi:[1,0]
	v_pk_mul_f32 v[50:51], v[50:51], v[88:89]
	v_pk_mul_f32 v[52:53], v[52:53], v[78:79]
	v_pk_mul_f32 v[46:47], v[46:47], v[80:81] op_sel_hi:[1,0]
	v_pk_mul_f32 v[48:49], v[48:49], v[80:81] op_sel_hi:[1,0]
	v_pk_mul_f32 v[68:69], v[30:31], v[68:69]
	v_pk_mul_f32 v[30:31], v[32:33], v[80:81] op_sel_hi:[1,0]
	v_pk_mul_f32 v[46:47], v[46:47], v[76:77]
	v_pk_mul_f32 v[48:49], v[48:49], v[74:75]
	v_pk_mul_f32 v[66:67], v[30:31], v[66:67]
	v_pk_mul_f32 v[30:31], v[50:51], s[82:83] op_sel_hi:[1,0]
	v_pk_mul_f32 v[32:33], v[52:53], s[82:83] op_sel_hi:[1,0]
	v_cvt_pk_bf16_f32 v30, v30, v31
	v_cvt_pk_bf16_f32 v31, v32, v33
	v_pk_mul_f32 v[32:33], v[46:47], s[82:83] op_sel_hi:[1,0]
	v_pk_mul_f32 v[46:47], v[48:49], s[82:83] op_sel_hi:[1,0]
	v_cvt_pk_bf16_f32 v32, v32, v33
	v_cvt_pk_bf16_f32 v33, v46, v47
	v_mul_f32_e32 v46, 0x4b800000, v92
	v_cmp_gt_f32_e64 s[4:5], s95, v92
	v_pk_mul_f32 v[38:39], v[38:39], v[80:81] op_sel_hi:[1,0]
	v_pk_mul_f32 v[40:41], v[40:41], v[80:81] op_sel_hi:[1,0]
	v_cndmask_b32_e64 v46, v92, v46, s[4:5]
	v_rsq_f32_e32 v48, v46
	v_pk_mul_f32 v[38:39], v[38:39], v[72:73]
	v_pk_mul_f32 v[40:41], v[40:41], v[70:71]
	v_pk_mul_f32 v[38:39], v[38:39], s[82:83] op_sel_hi:[1,0]
	v_pk_mul_f32 v[40:41], v[40:41], s[82:83] op_sel_hi:[1,0]
	v_cvt_pk_bf16_f32 v38, v38, v39
	v_cvt_pk_bf16_f32 v39, v40, v41
	v_pk_mul_f32 v[40:41], v[68:69], s[82:83] op_sel_hi:[1,0]
	v_pk_mul_f32 v[46:47], v[66:67], s[82:83] op_sel_hi:[1,0]
	v_cvt_pk_bf16_f32 v40, v40, v41
	v_cvt_pk_bf16_f32 v41, v46, v47
	v_mul_f32_e32 v46, 0x45800000, v48
	v_cndmask_b32_e64 v46, v48, v46, s[4:5]
	v_pk_mul_f32 v[48:49], v[46:47], v[86:87] op_sel_hi:[0,1]
	v_pk_mul_f32 v[48:49], v[58:59], v[48:49]
	v_or_b32_e32 v86, 4, v170
	v_mov_b32_e32 v47, v48
	v_mov_b32_e32 v50, v48
	v_mov_b32_e32 v51, v49
	v_mov_b32_e32 v52, v49
	v_permlane16_swap_b32_e32 v47, v50
	s_nop 0
	v_permlane16_swap_b32_e32 v51, v52
	v_cndmask_b32_e32 v51, v51, v52, vcc
	v_cndmask_b32_e32 v50, v47, v50, vcc
	v_pk_fma_f32 v[48:49], v[50:51], 0, v[48:49] op_sel_hi:[1,0,1]
	v_pk_mul_f32 v[50:51], v[46:47], v[98:99] op_sel_hi:[0,1]
	v_pk_mul_f32 v[50:51], v[60:61], v[50:51]
	v_pk_mul_f32 v[48:49], v[48:49], s[82:83] op_sel_hi:[1,0]
	v_mov_b32_e32 v47, v50
	v_mov_b32_e32 v52, v50
	v_mov_b32_e32 v53, v51
	v_mov_b32_e32 v58, v51
	v_permlane16_swap_b32_e32 v47, v52
	s_nop 0
	v_permlane16_swap_b32_e32 v53, v58
	v_cndmask_b32_e32 v53, v53, v58, vcc
	v_cndmask_b32_e32 v52, v47, v52, vcc
	v_pk_fma_f32 v[52:53], v[52:53], 0, v[50:51] op_sel_hi:[1,0,1]
	v_pk_mul_f32 v[50:51], v[46:47], v[90:91] op_sel_hi:[0,1]
	v_pk_mul_f32 v[50:51], v[54:55], v[50:51]
	v_bitop3_b32 v74, v148, v86, v147 bitop3:0x36
	v_mov_b32_e32 v47, v50
	v_mov_b32_e32 v54, v50
	s_nop 1
	v_permlane16_swap_b32_e32 v47, v54
	v_mov_b32_e32 v55, v51
	v_mov_b32_e32 v58, v51
	s_nop 1
	v_permlane16_swap_b32_e32 v55, v58
	v_cndmask_b32_e32 v54, v47, v54, vcc
	v_pk_mul_f32 v[46:47], v[46:47], v[82:83] op_sel_hi:[0,1]
	v_cndmask_b32_e32 v55, v55, v58, vcc
	v_pk_mul_f32 v[46:47], v[56:57], v[46:47]
	v_pk_fma_f32 v[54:55], v[54:55], 0, v[50:51] op_sel_hi:[1,0,1]
	v_mov_b32_e32 v50, v46
	v_mov_b32_e32 v56, v46
	v_mov_b32_e32 v51, v47
	v_mov_b32_e32 v57, v47
	v_permlane16_swap_b32_e32 v50, v56
	s_nop 0
	v_permlane16_swap_b32_e32 v51, v57
	v_cndmask_b32_e32 v51, v51, v57, vcc
	v_cndmask_b32_e32 v50, v50, v56, vcc
	v_pk_fma_f32 v[46:47], v[50:51], 0, v[46:47] op_sel_hi:[1,0,1]
	v_cvt_pk_bf16_f32 v50, v48, v49
	v_pk_mul_f32 v[48:49], v[52:53], s[82:83] op_sel_hi:[1,0]
	v_pk_mul_f32 v[46:47], v[46:47], s[82:83] op_sel_hi:[1,0]
	v_cvt_pk_bf16_f32 v51, v48, v49
	v_pk_mul_f32 v[48:49], v[54:55], s[82:83] op_sel_hi:[1,0]
	v_cvt_pk_bf16_f32 v53, v46, v47
	v_cvt_pk_bf16_f32 v52, v48, v49
	s_waitcnt vmcnt(0) lgkmcnt(0)
	s_barrier
; #define ATT_SB() __builtin_amdgcn_sched_barrier(0)
; #define ATT_DMA_K(t, sl) do { glds16(ksrc + (size_t)(t) * 64 * kpitch, (unsigned)__builtin_amdgcn_readfirstlane(kdst + (sl) * KSLOT)); \
;         if constexpr (DQK == 96) glds16(krsrc + (size_t)(t) * 64 * 32, (unsigned)__builtin_amdgcn_readfirstlane(krdst + (sl) * KSLOT)); } while (0)
; #define ATT_DMA_V(t, sl) do { glds16(vsrc + (size_t)(t) * 64, (unsigned)__builtin_amdgcn_readfirstlane(vdst + (sl) * VSLOT)); \
;         if constexpr (DV == 128) glds16(vsrc + (size_t)64 * NR + (size_t)(t) * 64, (unsigned)__builtin_amdgcn_readfirstlane(vdst + (sl) * VSLOT + 8192)); } while (0)
; #define ATT_KLOAD(sl) do { _Pragma("unroll") for (int kb_ = 0; kb_ < NKW; ++kb_) _Pragma("unroll") for (int ds_ = 0; ds_ < NDS; ++ds_) { \
;         if (ds_ < 2) kf[kb_ * NDS + ds_] = *(const LAS bf16x8*)(kp[ds_ & 1] + (sl) * KSLOT + (kb_ & 1) * 512 + (kb_ >> 1) * 4096); \
;         else kf[kb_ * NDS + ds_] = *(const LAS bf16x8*)(krp + (sl) * KSLOT + (kb_ & 1) * 256 + (kb_ >> 1) * 2048); } } while (0)
; #define ATT_QK() do { _Pragma("unroll") for (int kb_ = 0; kb_ < NKW; ++kb_) _Pragma("unroll") for (int ds_ = 0; ds_ < NDS; ++ds_) _Pragma("unroll") for (int qb_ = 0; qb_ < NQB; ++qb_) \
;         c[kb_][qb_] = __builtin_amdgcn_mfma_f32_16x16x32_bf16(kf[kb_ * NDS + ds_], qf[qb_ * NDS + ds_], ds_ == 0 ? zero4 : c[kb_][qb_], 0, 0, 0); } while (0)
; #define ATT_EXP() do { _Pragma("unroll") for (int kb_ = 0; kb_ < NKW; ++kb_) _Pragma("unroll") for (int qb_ = 0; qb_ < NQB; ++qb_) _Pragma("unroll") for (int i_ = 0; i_ < 4; ++i_) \
;         c[kb_][qb_][i_] = __builtin_amdgcn_exp2f(c[kb_][qb_][i_]); } while (0)
; template <int DQK, int DV, bool LEAD> ...
;     ...
;     bf16x8 kf[NKW * NDS], vf[NVF];
;     ATT_KLOAD(0);
;     asm volatile("s_waitcnt lgkmcnt(0)\n\ts_barrier" ::: "memory");
;     float lsum[NQB];
; #pragma unroll
;     for (int qb = 0; qb < NQB; ++qb) lsum[qb] = 0.f;
;     const f32x4 zero4 = {0.f, 0.f, 0.f, 0.f};
;     f32x4 o[NDB][NQB], c[NKW][NQB]; u32x4 pw[4];
; #pragma unroll
;     for (int i = 0; i < NDB; ++i)
; #pragma unroll
;         for (int qb = 0; qb < NQB; ++qb) o[i][qb] = zero4;
;     ATT_DMA_K(3, 0); ATT_DMA_V(1, 1);
;     ATT_QK(); ATT_SB();
;     ATT_KLOAD(1); ATT_SB();
;     if constexpr (LEAD) { ATT_EXP(); ATT_SUMPACK(); }
;     wait_bar<NDMA>();
;     int s_prev = 0, s_cur = 1, s_next = 2;
	ds_read_b128 v[46:49], v194
	ds_read_b128 v[54:57], v194 offset:512
	v_lshl_add_u32 v211, v74, 4, v149
	s_waitcnt lgkmcnt(1)
	v_mfma_f32_16x16x32_bf16 v[58:61], v[46:49], v[6:9], 0
	ds_read_b128 v[74:77], v211
	ds_read_b128 v[78:81], v211 offset:512
	v_lshlrev_b32_e32 v82, 5, v146
	v_lshlrev_b32_e32 v83, 6, v144
	v_mfma_f32_16x16x32_bf16 v[66:69], v[46:49], v[18:21], 0
	v_bitop3_b32 v82, v82, v142, 48 bitop3:0x78
	s_lshl_b32 s4, s38, 11
	v_sub_u32_e32 v83, v145, v83
	v_mfma_f32_16x16x32_bf16 v[70:73], v[46:49], v[34:37], 0
	v_add3_u32 v212, v83, v82, s4
	s_cmpk_lt_u32 s16, 0x100
	s_mov_b32 s4, 0
	v_mfma_f32_16x16x32_bf16 v[46:49], v[46:49], v[30:33], 0
	s_cselect_b64 vcc, -1, 0
	s_mov_b32 s7, s4
	s_waitcnt lgkmcnt(1)
	v_mfma_f32_16x16x32_bf16 v[58:61], v[74:77], v[2:5], v[58:61]
	v_mfma_f32_16x16x32_bf16 v[66:69], v[74:77], v[14:17], v[66:69]
	v_mfma_f32_16x16x32_bf16 v[70:73], v[74:77], v[26:29], v[70:73]
	v_mfma_f32_16x16x32_bf16 v[46:49], v[74:77], v[38:41], v[46:49]
	ds_read_b128 v[74:77], v212 offset:8192
	ds_read_b128 v[82:85], v212 offset:8448
	s_waitcnt lgkmcnt(0)
	s_barrier
	s_mov_b32 s5, m0
	s_mov_b32 m0, s30
	s_nop 0
	global_load_lds_dwordx4 v[192:193], off
	s_mov_b32 m0, s5
	s_waitcnt lgkmcnt(1)
	v_mfma_f32_16x16x32_bf16 v[150:153], v[74:77], v[10:13], v[58:61]
	s_mov_b32 s5, m0
	s_mov_b32 m0, s41
	s_nop 0
	global_load_lds_dwordx4 v[204:205], off
	s_mov_b32 m0, s5
	s_add_i32 s5, s31, 0x2000
	v_mfma_f32_16x16x32_bf16 v[138:141], v[74:77], v[22:25], v[66:69]
	v_mfma_f32_16x16x32_bf16 v[122:125], v[74:77], v[50:53], v[46:49]
	v_mfma_f32_16x16x32_bf16 v[46:49], v[54:57], v[6:9], 0
	v_mfma_f32_16x16x32_bf16 v[58:61], v[54:57], v[18:21], 0
	v_mfma_f32_16x16x32_bf16 v[66:69], v[54:57], v[34:37], 0
	v_mfma_f32_16x16x32_bf16 v[54:57], v[54:57], v[30:33], 0
	v_mfma_f32_16x16x32_bf16 v[46:49], v[78:81], v[2:5], v[46:49]
	v_mfma_f32_16x16x32_bf16 v[58:61], v[78:81], v[14:17], v[58:61]
	v_mfma_f32_16x16x32_bf16 v[66:69], v[78:81], v[26:29], v[66:69]
	v_mfma_f32_16x16x32_bf16 v[54:57], v[78:81], v[38:41], v[54:57]
	v_mfma_f32_16x16x32_bf16 v[130:133], v[74:77], v[42:45], v[70:73]
	s_waitcnt lgkmcnt(0)
	v_mfma_f32_16x16x32_bf16 v[166:169], v[82:85], v[10:13], v[46:49]
	s_nop 0
	v_lshrrev_b32_e32 v70, 1, v142
	v_lshlrev_b32_e32 v71, 7, v143
	v_lshl_add_u64 v[46:47], v[186:187], 0, s[66:67]
	v_mfma_f32_16x16x32_bf16 v[162:165], v[82:85], v[22:25], v[58:61]
	s_mov_b32 s6, m0
	s_mov_b32 m0, s5
	s_nop 0
	global_load_lds_dwordx4 v[46:47], off
	s_mov_b32 m0, s6
	s_mov_b32 s6, s4
	s_mov_b32 s5, s4
	v_mfma_f32_16x16x32_bf16 v[154:157], v[82:85], v[42:45], v[66:69]
	v_mov_b64_e32 v[48:49], s[6:7]
	v_mov_b64_e32 v[46:47], s[4:5]
	v_mfma_f32_16x16x32_bf16 v[146:149], v[82:85], v[50:53], v[54:57]
	ds_read_b128 v[114:117], v194 offset:12288
	ds_read_b128 v[134:137], v194 offset:12800
	ds_read_b128 v[118:121], v211 offset:12288
	ds_read_b128 v[142:145], v211 offset:12800
	ds_read_b128 v[126:129], v212 offset:20480
	ds_read_b128 v[158:161], v212 offset:20736
	v_cndmask_b32_e32 v54, v86, v170, vcc
	v_bitop3_b32 v54, v54, v70, 7 bitop3:0x78
	v_lshlrev_b32_e32 v54, 4, v54
	v_add3_u32 v210, 0, v71, v54
	s_waitcnt vmcnt(3) lgkmcnt(0)
	s_barrier
	s_mov_b32 s5, 1
	v_mov_b32_e32 v188, 0
	s_cmp_lg_u32 s5, 0
	v_mov_b64_e32 v[56:57], v[48:49]
	v_mov_b64_e32 v[60:61], v[48:49]
	v_mov_b64_e32 v[64:65], v[48:49]
	v_mov_b64_e32 v[68:69], v[48:49]
	v_mov_b64_e32 v[72:73], v[48:49]
	v_mov_b64_e32 v[76:77], v[48:49]
	v_mov_b64_e32 v[80:81], v[48:49]
	v_mov_b64_e32 v[84:85], v[48:49]
	v_mov_b64_e32 v[88:89], v[48:49]
	v_mov_b64_e32 v[92:93], v[48:49]
	v_mov_b64_e32 v[96:97], v[48:49]
	v_mov_b64_e32 v[100:101], v[48:49]
	v_mov_b64_e32 v[104:105], v[48:49]
	v_mov_b64_e32 v[108:109], v[48:49]
	v_mov_b64_e32 v[112:113], v[48:49]
	s_cselect_b64 s[6:7], -1, 0
	v_mov_b64_e32 v[54:55], v[46:47]
	v_mov_b64_e32 v[58:59], v[46:47]
	v_mov_b64_e32 v[62:63], v[46:47]
	v_mov_b64_e32 v[66:67], v[46:47]
	v_mov_b64_e32 v[70:71], v[46:47]
	v_mov_b64_e32 v[74:75], v[46:47]
	v_mov_b64_e32 v[78:79], v[46:47]
	v_mov_b64_e32 v[82:83], v[46:47]
	v_mov_b64_e32 v[86:87], v[46:47]
	v_mov_b64_e32 v[90:91], v[46:47]
	v_mov_b64_e32 v[94:95], v[46:47]
	v_mov_b64_e32 v[98:99], v[46:47]
	v_mov_b64_e32 v[102:103], v[46:47]
	v_mov_b64_e32 v[106:107], v[46:47]
	v_mov_b64_e32 v[110:111], v[46:47]
	s_mov_b32 s16, 2
	v_mov_b32_e32 v189, v188
	v_mov_b32_e32 v190, v188
	v_mov_b32_e32 v191, v188

; #define LAS __attribute__((address_space(3)))
; template <int DQK, int DV, bool LEAD> ...
;     ...
;     const int tid = tid_, lane = tid & 63, q16 = lane & 15, g4 = lane >> 4, hi = lane >> 5; const int wid = __builtin_amdgcn_readfirstlane(tid >> 6);
;     const int kg = KS ? (wid >> 2) : 0, qoff = KS ? (wid & 3) * 64 : wid * 32;
;     const unsigned lds0 = (unsigned)(uintptr_t)shm;
;     const int krow_l = wid * 8 + (lane >> 3);
;     const int kc_l = (lane & 7) ^ (((krow_l >> 1) & 1) | (((krow_l >> 3) & 1) << 1) | (((krow_l >> 4) & 1) << 2));
;     const int vc_l = (lane & 7) ^ ((krow_l >> 1) & 7);
;     const bf16_t* ksrc = K + (size_t)(krow0 + krow_l) * kpitch + kc_l * 8;
;     const int rrow_l = (wid & 3) * 16 + (lane >> 2), rc_l = (lane & 3) ^ (((rrow_l >> 4) & 1) << 1);
;     const bf16_t* krsrc = (DQK == 96) ? KR + (size_t)(krow0 + rrow_l) * 32 + rc_l * 8 : nullptr;
;     const bf16_t* vsrc = Vt + (size_t)krow_l * NR + krow0 + vc_l * 8;
;     const unsigned kdst = lds0 + KOFF + wid * 1024, krdst = lds0 + KOFF + 8192 + (wid & 3) * 1024, vdst = lds0 + VOFF + wid * 1024;
;     ...
;     const int kr0 = 8 * (q16 >> 2) + (q16 & 3);
;     const int fk = ((kr0 >> 1) & 1) | (((kr0 >> 3) & 1) << 1) | (((kr0 >> 4) & 1) << 2);
;     const LAS unsigned char* kp[2]; const LAS unsigned char* vp[2];
; #pragma unroll
;     for (int ds = 0; ds < 2; ++ds) kp[ds] = shm + KOFF + kr0 * 128 + ((((ds << 2) | g4) ^ fk) << 4) + kg * 4096;
;     const LAS unsigned char* krp = shm + KOFF + 8192 + kr0 * 64 + ((g4 ^ (((kr0 >> 4) & 1) << 1)) << 4) + kg * 2048;
; #pragma unroll
;     for (int s_ = 0; s_ < 2; ++s_) vp[s_] = shm + VOFF + q16 * 128 + ((((s_ << 2) | g4) ^ ((q16 >> 1) & 7)) << 4);
;     const LAS unsigned char* vpk = kg ? vp[1] : vp[0];
;     ...
;     ATT_DMA_K(0, 0); ATT_DMA_V(0, 0); ATT_DMA_K(1, 1); ATT_DMA_K(2, 2);
;     bf16x8 qf[NQB * NDS];
;     {
;       const float c2 = (DQK == 64) ? C2_EVEN : C2_ODD; const bool lat = tq0 >= 0;
; #pragma unroll
;       for (int qb = 0; qb < NQB; ++qb) {
;           const bf16_t* qp = Q + (size_t)(qrow0 + qoff + qb * 16 + q16) * qpitch + g4 * 8;
;           bf16x8 raw[NDS];
; #pragma unroll
;           for (int ds = 0; ds < NDS; ++ds) raw[ds] = *(const bf16x8*)(qp + ds * 32);
.LBB0_667:
	v_mov_b32_e32 v142, v0
	v_mov_b64_e32 v[6:7], s[46:47]
	v_readfirstlane_b32 s16, v142
	s_ashr_i32 s4, s16, 6
	v_bfe_u32 v203, v142, 3, 3
	v_lshl_or_b32 v8, s4, 3, v203
	v_ashrrev_i32_e32 v2, 1, v8
	s_and_b32 s30, s4, 3
	v_and_b32_e32 v3, 1, v2
	s_lshl_b32 s5, s4, 1
	s_lshr_b32 s7, s16, 5
	v_bfe_u32 v4, v142, 2, 4
	v_and_b32_e32 v206, 7, v142
	s_and_b32 s6, s5, 2
	v_and_or_b32 v3, s7, 4, v3
	v_xor_b32_e32 v10, v2, v142
	v_add_u32_e32 v2, s40, v8
	v_lshl_or_b32 v4, s30, 4, v4
	v_bitop3_b32 v9, v3, v206, s6 bitop3:0x36
	v_ashrrev_i32_e32 v3, 31, v2
	v_and_b32_e32 v18, 3, v142
	v_or_b32_e32 v4, s40, v4
	s_lshl_b32 s4, s4, 10
	v_lshlrev_b64 v[2:3], 11, v[2:3]
	v_bitop3_b32 v11, s5, v18, 2 bitop3:0x6c
	v_ashrrev_i32_e32 v5, 31, v4
	s_add_i32 s31, s4, 0
	s_lshl_b32 s6, s30, 10
	v_mad_i64_i32 v[6:7], s[4:5], v8, s91, v[6:7]
	v_lshlrev_b64 v[4:5], 6, v[4:5]
	v_lshl_add_u64 v[2:3], s[44:45], 0, v[2:3]
	v_lshlrev_b32_e32 v194, 4, v9
	s_add_i32 s5, s6, 0
	s_ashr_i32 s41, s40, 31
	v_lshl_add_u64 v[4:5], s[28:29], 0, v[4:5]
	v_lshl_add_u64 v[62:63], v[2:3], 0, v[194:195]
	v_lshlrev_b32_e32 v194, 4, v11
	v_lshlrev_b32_e32 v2, 4, v10
	s_add_i32 s42, s5, 0x2000
	s_mov_b32 s5, m0
	s_mov_b32 m0, s31
	s_nop 0
	global_load_lds_dwordx4 v[62:63], off
	s_mov_b32 m0, s5
	v_lshl_add_u64 v[6:7], s[40:41], 1, v[6:7]
	v_lshl_add_u64 v[64:65], v[4:5], 0, v[194:195]
	v_and_b32_e32 v194, 0x70, v2
	s_mov_b32 s5, m0
	s_mov_b32 m0, s42
	s_nop 0
	global_load_lds_dwordx4 v[64:65], off
	s_mov_b32 m0, s5
	s_add_i32 s41, s31, 0x9000
	v_lshl_add_u64 v[186:187], v[6:7], 0, v[194:195]
	s_mov_b32 s5, m0
	s_mov_b32 m0, s41
	s_nop 0
	global_load_lds_dwordx4 v[186:187], off
	s_mov_b32 m0, s5
	s_mov_b64 s[6:7], 0x20000
	v_lshl_add_u64 v[2:3], v[62:63], 0, s[6:7]
	s_add_i32 s5, s31, 0x3000
	s_mov_b32 s6, m0
	s_mov_b32 m0, s5
	s_nop 0
	global_load_lds_dwordx4 v[2:3], off
	s_mov_b32 m0, s6
	v_lshl_add_u64 v[2:3], v[64:65], 0, s[60:61]
	s_add_i32 s5, s42, 0x3000
	s_mov_b32 s6, m0
	s_mov_b32 m0, s5
	s_nop 0
	global_load_lds_dwordx4 v[2:3], off
	s_mov_b32 m0, s6
	s_mov_b64 s[6:7], 0x40000
	s_lshl_b32 s4, s30, 6
	v_lshl_add_u64 v[2:3], v[62:63], 0, s[6:7]
	s_add_i32 s5, s31, 0x6000
	s_mov_b32 s6, m0
	s_mov_b32 m0, s5
	s_nop 0
	global_load_lds_dwordx4 v[2:3], off
	s_mov_b32 m0, s6
	v_and_b32_e32 v143, 15, v142
	s_mov_b64 s[6:7], 0x2000
	s_or_b32 s24, s4, s40
	v_and_b32_e32 v8, 48, v142
	v_lshl_add_u64 v[2:3], v[64:65], 0, s[6:7]
	v_or_b32_e32 v6, s24, v143
	v_mov_b32_e32 v9, v195
	s_add_i32 s5, s42, 0x6000
	s_mov_b32 s6, m0
	s_mov_b32 m0, s5
	s_nop 0
	global_load_lds_dwordx4 v[2:3], off
	s_mov_b32 m0, s6
	v_lshl_add_u64 v[2:3], s[36:37], 0, v[8:9]
	v_or_b32_e32 v7, 16, v6
	v_mad_i64_i32 v[4:5], s[4:5], v6, s90, v[2:3]
	v_mad_i64_i32 v[10:11], s[4:5], v7, s90, v[2:3]
	v_or_b32_e32 v7, 32, v6
	v_or_b32_e32 v6, 48, v6
	v_mad_i64_i32 v[14:15], s[4:5], v7, s90, v[2:3]
	v_mad_i64_i32 v[16:17], s[4:5], v6, s90, v[2:3]
	global_load_dwordx4 v[28:31], v[4:5], off offset:64 nt
	global_load_dwordx4 v[46:49], v[10:11], off offset:64 nt
	global_load_dwordx4 v[50:53], v[14:15], off offset:64 nt
	global_load_dwordx4 v[54:57], v[16:17], off offset:64 nt
	global_load_dwordx4 v[58:61], v[4:5], off nt
	global_load_dwordx4 v[88:91], v[10:11], off nt
	global_load_dwordx4 v[94:97], v[14:15], off nt
	global_load_dwordx4 v[6:9], v[16:17], off nt
	s_nop 0
	global_load_dwordx4 v[10:13], v[10:11], off offset:128 nt
	v_lshlrev_b32_e32 v207, 1, v142
	v_and_or_b32 v144, v207, 24, v18
	v_bfe_u32 v146, v142, 3, 1
	v_bfe_u32 v194, v142, 4, 2
	s_ashr_i32 s36, s16, 8
	v_bfe_u32 v147, v142, 1, 2
	v_lshlrev_b32_e32 v148, 2, v146
	v_lshl_add_u32 v145, v144, 7, 0
	v_lshl_add_u32 v149, s36, 12, v145
	v_bitop3_b32 v2, v148, v194, v147 bitop3:0x36
	v_lshl_add_u32 v208, v2, 4, v149
	global_load_dwordx4 v[2:5], v[4:5], off offset:128 nt
	v_lshlrev_b32_e32 v82, 5, v194
	global_load_dwordx4 v[22:25], v[14:15], off offset:128 nt
	global_load_dwordx4 v[34:37], v[16:17], off offset:128 nt
	global_load_dwordx4 v[38:41], v82, s[26:27] offset:144
	global_load_dwordx4 v[42:45], v82, s[26:27] offset:128
	s_mov_b32 s6, 0x3d000000
	s_brev_b32 s7, 60
	s_mov_b32 s4, 0x358637bd
	s_mov_b32 s7, 0x3c800000
	v_mov_b64_e32 v[106:107], s[4:5]
	v_and_b32_e32 v112, 16, v142
	v_or_b32_e32 v209, 4, v194
	v_and_b32_e32 v210, 63, v142
	v_lshlrev_b32_e32 v211, 7, v143
	s_waitcnt vmcnt(10)
	v_and_b32_e32 v73, 0xffff0000, v54
	s_waitcnt vmcnt(9)
	v_and_b32_e32 v137, 0xffff0000, v58
	v_lshlrev_b32_e32 v136, 16, v58
	v_and_b32_e32 v135, 0xffff0000, v59
	s_waitcnt vmcnt(6)
; template <int DQK, int DV, bool LEAD> ...
;     ...
;           float x[NDS][8];
; #pragma unroll
;           for (int ds = 0; ds < NDS; ++ds)
; #pragma unroll
;               for (int j = 0; j < 8; ++j) x[ds][j] = __uint_as_float(((unsigned)(unsigned short)raw[ds][j]) << 16);
;           const int tq = tq0 + qoff + qb * 16 + q16, prow = (tq >> 6) & 127, pcol = tq & 63;
;           float sn = 0.f;
; #pragma unroll
;           for (int ds = 0; ds < 2; ++ds)
; #pragma unroll
;               for (int j = 0; j < 8; ++j) sn += x[ds][j] * x[ds][j];
;           sn = lanes4_sum(sn);
	v_and_b32_e32 v77, 0xffff0000, v8
	v_lshlrev_b32_e32 v76, 16, v8
	v_mul_f32_e32 v8, v137, v137
	v_and_b32_e32 v75, 0xffff0000, v9
	v_lshlrev_b32_e32 v74, 16, v9
	v_lshlrev_b32_e32 v134, 16, v59
	v_pk_fma_f32 v[8:9], v[136:137], v[136:137], v[8:9] op_sel_hi:[1,1,0]
	v_lshlrev_b32_e32 v72, 16, v54
	v_pk_fma_f32 v[8:9], v[134:135], v[134:135], v[8:9]
	v_mul_f32_e32 v54, v135, v135
	v_and_b32_e32 v133, 0xffff0000, v60
	v_lshlrev_b32_e32 v132, 16, v60
	v_pk_add_f32 v[8:9], v[54:55], v[8:9] op_sel_hi:[0,1]
	v_pk_fma_f32 v[8:9], v[132:133], v[132:133], v[8:9]
	v_mul_f32_e32 v54, v133, v133
	v_and_b32_e32 v127, 0xffff0000, v61
	v_lshlrev_b32_e32 v126, 16, v61
	v_pk_add_f32 v[8:9], v[54:55], v[8:9] op_sel_hi:[0,1]
	v_pk_fma_f32 v[8:9], v[126:127], v[126:127], v[8:9]
	v_mul_f32_e32 v54, v127, v127
	v_and_b32_e32 v125, 0xffff0000, v28
	v_lshlrev_b32_e32 v124, 16, v28
	v_pk_add_f32 v[8:9], v[54:55], v[8:9] op_sel_hi:[0,1]
	v_pk_fma_f32 v[8:9], v[124:125], v[124:125], v[8:9]
	v_mul_f32_e32 v54, v125, v125
	v_and_b32_e32 v123, 0xffff0000, v29
	v_lshlrev_b32_e32 v122, 16, v29
	v_pk_add_f32 v[8:9], v[54:55], v[8:9] op_sel_hi:[0,1]
	v_pk_fma_f32 v[8:9], v[122:123], v[122:123], v[8:9]
	v_mul_f32_e32 v54, v123, v123
	v_and_b32_e32 v121, 0xffff0000, v30
	v_lshlrev_b32_e32 v120, 16, v30
	v_pk_add_f32 v[8:9], v[54:55], v[8:9] op_sel_hi:[0,1]
	v_pk_fma_f32 v[8:9], v[120:121], v[120:121], v[8:9]
	v_mul_f32_e32 v54, v121, v121
	v_and_b32_e32 v17, 0xffff0000, v31
	v_lshlrev_b32_e32 v16, 16, v31
	v_pk_add_f32 v[8:9], v[54:55], v[8:9] op_sel_hi:[0,1]
	v_pk_fma_f32 v[8:9], v[16:17], v[16:17], v[8:9]
	v_mul_f32_e32 v54, v17, v17
	v_pk_add_f32 v[8:9], v[54:55], v[8:9] op_sel_hi:[0,1]
	v_and_b32_e32 v79, 0xffff0000, v7
	v_lshlrev_b32_e32 v78, 16, v7
	v_mov_b32_e32 v7, v8
	s_nop 1
	v_permlane16_swap_b32_e32 v8, v7
	v_add_f32_e32 v7, v8, v7
	v_mov_b32_e32 v9, v7
	v_and_b32_e32 v119, 0xffff0000, v88
	s_nop 0
	v_permlane32_swap_b32_e32 v7, v9
	v_lshlrev_b32_e32 v118, 16, v88
	v_mul_f32_e32 v8, v119, v119
	v_and_b32_e32 v71, 0xffff0000, v55
	v_lshlrev_b32_e32 v70, 16, v55
	v_and_b32_e32 v109, 0xffff0000, v89
	v_lshlrev_b32_e32 v108, 16, v89
	v_pk_fma_f32 v[54:55], v[118:119], v[118:119], v[8:9] op_sel_hi:[1,1,0]
	v_mul_f32_e32 v8, v109, v109
	v_pk_fma_f32 v[54:55], v[108:109], v[108:109], v[54:55]
	v_and_b32_e32 v105, 0xffff0000, v90
	v_lshlrev_b32_e32 v104, 16, v90
	v_pk_add_f32 v[54:55], v[8:9], v[54:55] op_sel_hi:[0,1]
	v_pk_fma_f32 v[54:55], v[104:105], v[104:105], v[54:55]
	v_mul_f32_e32 v8, v105, v105
	v_and_b32_e32 v103, 0xffff0000, v91
	v_lshlrev_b32_e32 v102, 16, v91
	v_pk_add_f32 v[54:55], v[8:9], v[54:55] op_sel_hi:[0,1]
	v_pk_fma_f32 v[54:55], v[102:103], v[102:103], v[54:55]
	v_mul_f32_e32 v8, v103, v103
	v_and_b32_e32 v29, 0xffff0000, v46
	v_lshlrev_b32_e32 v28, 16, v46
	v_pk_add_f32 v[54:55], v[8:9], v[54:55] op_sel_hi:[0,1]
	v_pk_fma_f32 v[54:55], v[28:29], v[28:29], v[54:55]
	v_mul_f32_e32 v8, v29, v29
	v_and_b32_e32 v21, 0xffff0000, v47
	v_lshlrev_b32_e32 v20, 16, v47
	v_pk_add_f32 v[54:55], v[8:9], v[54:55] op_sel_hi:[0,1]
	v_pk_fma_f32 v[54:55], v[20:21], v[20:21], v[54:55]
	v_mul_f32_e32 v8, v21, v21
	v_and_b32_e32 v19, 0xffff0000, v48
	v_lshlrev_b32_e32 v18, 16, v48
	v_pk_add_f32 v[54:55], v[8:9], v[54:55] op_sel_hi:[0,1]
	v_pk_fma_f32 v[54:55], v[18:19], v[18:19], v[54:55]
	v_mul_f32_e32 v8, v19, v19
	v_and_b32_e32 v15, 0xffff0000, v49
	v_lshlrev_b32_e32 v14, 16, v49
	v_pk_add_f32 v[54:55], v[8:9], v[54:55] op_sel_hi:[0,1]
	v_pk_fma_f32 v[54:55], v[14:15], v[14:15], v[54:55]
	v_mul_f32_e32 v8, v15, v15
	v_pk_add_f32 v[54:55], v[8:9], v[54:55] op_sel_hi:[0,1]
	v_mov_b32_e32 v8, v54
	s_nop 1
	v_permlane16_swap_b32_e32 v54, v8
	v_and_b32_e32 v101, 0xffff0000, v94
	v_add_f32_e32 v129, v54, v8
	v_lshlrev_b32_e32 v100, 16, v94
	v_mul_f32_e32 v8, v101, v101
	v_and_b32_e32 v93, 0xffff0000, v95
	v_lshlrev_b32_e32 v92, 16, v95
	v_pk_fma_f32 v[54:55], v[100:101], v[100:101], v[8:9] op_sel_hi:[1,1,0]
	v_mul_f32_e32 v8, v93, v93
	v_pk_fma_f32 v[54:55], v[92:93], v[92:93], v[54:55]
	v_and_b32_e32 v87, 0xffff0000, v96
	v_lshlrev_b32_e32 v86, 16, v96
	v_pk_add_f32 v[54:55], v[8:9], v[54:55] op_sel_hi:[0,1]
	v_pk_fma_f32 v[54:55], v[86:87], v[86:87], v[54:55]
	v_mul_f32_e32 v8, v87, v87
	v_and_b32_e32 v85, 0xffff0000, v97
	v_lshlrev_b32_e32 v84, 16, v97
	v_pk_add_f32 v[54:55], v[8:9], v[54:55] op_sel_hi:[0,1]
	v_pk_fma_f32 v[54:55], v[84:85], v[84:85], v[54:55]
	v_mul_f32_e32 v8, v85, v85
	v_and_b32_e32 v81, 0xffff0000, v50
	v_lshlrev_b32_e32 v80, 16, v50
	v_pk_add_f32 v[54:55], v[8:9], v[54:55] op_sel_hi:[0,1]
	v_pk_fma_f32 v[54:55], v[80:81], v[80:81], v[54:55]
	v_mul_f32_e32 v8, v81, v81
	v_and_b32_e32 v33, 0xffff0000, v51
	v_lshlrev_b32_e32 v32, 16, v51
	v_pk_add_f32 v[54:55], v[8:9], v[54:55] op_sel_hi:[0,1]
	v_pk_fma_f32 v[54:55], v[32:33], v[32:33], v[54:55]
	v_mul_f32_e32 v8, v33, v33
	v_and_b32_e32 v31, 0xffff0000, v52
	v_lshlrev_b32_e32 v30, 16, v52
	v_pk_add_f32 v[54:55], v[8:9], v[54:55] op_sel_hi:[0,1]
	v_pk_fma_f32 v[54:55], v[30:31], v[30:31], v[54:55]
	v_mul_f32_e32 v8, v31, v31
	v_and_b32_e32 v27, 0xffff0000, v53
	v_lshlrev_b32_e32 v26, 16, v53
	v_pk_add_f32 v[54:55], v[8:9], v[54:55] op_sel_hi:[0,1]
	v_pk_fma_f32 v[54:55], v[26:27], v[26:27], v[54:55]
	v_mul_f32_e32 v8, v27, v27
	v_pk_add_f32 v[54:55], v[8:9], v[54:55] op_sel_hi:[0,1]
	v_mov_b32_e32 v8, v54
	v_and_b32_e32 v89, 0xffff0000, v6
	s_nop 0
	v_permlane16_swap_b32_e32 v54, v8
	v_lshlrev_b32_e32 v88, 16, v6
	v_mul_f32_e32 v6, v89, v89
	v_add_f32_e32 v113, v54, v8
	v_pk_fma_f32 v[54:55], v[88:89], v[88:89], v[6:7] op_sel_hi:[1,1,0]
	v_mul_f32_e32 v6, v79, v79
	v_pk_fma_f32 v[54:55], v[78:79], v[78:79], v[54:55]
	global_load_dwordx4 v[46:49], v82, s[26:27] offset:16
	global_load_dwordx4 v[50:53], v82, s[26:27]
	v_pk_add_f32 v[54:55], v[6:7], v[54:55] op_sel_hi:[0,1]
	v_pk_fma_f32 v[54:55], v[76:77], v[76:77], v[54:55]
	v_mul_f32_e32 v6, v77, v77
	v_pk_add_f32 v[54:55], v[6:7], v[54:55] op_sel_hi:[0,1]
	v_pk_fma_f32 v[54:55], v[74:75], v[74:75], v[54:55]
	v_mul_f32_e32 v6, v75, v75
	v_pk_add_f32 v[54:55], v[6:7], v[54:55] op_sel_hi:[0,1]
	v_pk_fma_f32 v[54:55], v[72:73], v[72:73], v[54:55]
	v_mul_f32_e32 v6, v73, v73
	v_pk_add_f32 v[54:55], v[6:7], v[54:55] op_sel_hi:[0,1]
	v_pk_fma_f32 v[54:55], v[70:71], v[70:71], v[54:55]
	v_mul_f32_e32 v6, v71, v71
	v_and_b32_e32 v69, 0xffff0000, v56
	v_lshlrev_b32_e32 v68, 16, v56
	v_pk_add_f32 v[54:55], v[6:7], v[54:55] op_sel_hi:[0,1]
	v_pk_fma_f32 v[54:55], v[68:69], v[68:69], v[54:55]
	v_mul_f32_e32 v6, v69, v69
	v_and_b32_e32 v67, 0xffff0000, v57
	v_lshlrev_b32_e32 v66, 16, v57
	v_pk_add_f32 v[54:55], v[6:7], v[54:55] op_sel_hi:[0,1]
	v_pk_fma_f32 v[54:55], v[66:67], v[66:67], v[54:55]
	v_mul_f32_e32 v6, v67, v67
	v_pk_add_f32 v[54:55], v[6:7], v[54:55] op_sel_hi:[0,1]
	v_mov_b32_e32 v6, v54
	s_nop 1
	v_permlane16_swap_b32_e32 v54, v6
	v_add_f32_e32 v95, v54, v6
	global_load_dwordx4 v[54:57], v82, s[26:27] offset:272
	global_load_dwordx4 v[58:61], v82, s[26:27] offset:256
	s_waitcnt vmcnt(8)
; template <int DQK, int DV, bool LEAD> ...
;     ...
;           sn = lanes4_sum(sn);
;           const float rn = rsqrtf(sn * (1.f / 64.f) + EPS);
; #pragma unroll
;           for (int ds = 0; ds < 2; ++ds)
; #pragma unroll
;               for (int j = 0; j < 8; ++j) x[ds][j] *= rn * qgain[32 * ds + 8 * g4 + j];
;           if constexpr (DQK == 64) {
; #pragma unroll
;               for (int ds = 0; ds < 2; ++ds)
; #pragma unroll
;                   for (int j = 0; j < 8; ++j) {
;                       auto rr = __builtin_amdgcn_permlane32_swap(__float_as_uint(x[ds][j]), __float_as_uint(x[ds][j]), false, false);
;                       const float other = hi ? __uint_as_float(rr[0]) : __uint_as_float(rr[1]);
;                       float cc = 1.f, sg = 0.f;
;                       if (lat) { const f32x2 cs = rope[(ds ? pcol : prow) * 16 + 8 * (g4 & 1) + j]; cc = cs.x; sg = hi ? cs.y : -cs.y; }
;                       x[ds][j] = x[ds][j] * cc + other * sg; }
;           } else {
;               float sr = 0.f;
; #pragma unroll
;               for (int j = 0; j < 8; ++j) sr += x[2][j] * x[2][j];
;               sr = lanes4_sum(sr);
;               const float rq = rsqrtf(sr * (1.f / 32.f) + EPS);
; #pragma unroll
;               for (int j = 0; j < 8; ++j) { const float av = x[2][j] * rq * qgain[64 + 8 * g4 + j];
;                   auto rr = __builtin_amdgcn_permlane16_swap(__float_as_uint(av), __float_as_uint(av), false, false);
;                   const float other = (g4 & 1) ? __uint_as_float(rr[0]) : __uint_as_float(rr[1]);
;                   float cc = 1.f, sg = 0.f;
;                   if (lat) { const f32x2 cs = rope[((g4 & 2) ? pcol : prow) * 8 + j]; cc = cs.x; sg = (g4 & 1) ? cs.y : -cs.y; }
;                   x[2][j] = av * cc + other * sg; }
;           }
	v_and_b32_e32 v155, 0xffff0000, v2
	v_lshlrev_b32_e32 v154, 16, v2
	v_mul_f32_e32 v2, v155, v155
	v_and_b32_e32 v139, 0xffff0000, v13
	v_lshlrev_b32_e32 v138, 16, v13
	v_and_b32_e32 v141, 0xffff0000, v12
	v_lshlrev_b32_e32 v140, 16, v12
	v_and_b32_e32 v13, 0xffff0000, v3
	v_lshlrev_b32_e32 v12, 16, v3
	v_pk_fma_f32 v[2:3], v[154:155], v[154:155], v[2:3] op_sel_hi:[1,1,0]
	v_and_b32_e32 v153, 0xffff0000, v4
	v_lshlrev_b32_e32 v152, 16, v4
	v_pk_fma_f32 v[2:3], v[12:13], v[12:13], v[2:3]
	v_mul_f32_e32 v4, v13, v13
	v_pk_add_f32 v[2:3], v[4:5], v[2:3] op_sel_hi:[0,1]
	v_pk_fma_f32 v[2:3], v[152:153], v[152:153], v[2:3]
	v_mul_f32_e32 v4, v153, v153
	v_and_b32_e32 v151, 0xffff0000, v5
	v_lshlrev_b32_e32 v150, 16, v5
	v_pk_add_f32 v[2:3], v[4:5], v[2:3] op_sel_hi:[0,1]
	v_pk_fma_f32 v[2:3], v[150:151], v[150:151], v[2:3]
	v_mul_f32_e32 v4, v151, v151
	v_pk_add_f32 v[2:3], v[4:5], v[2:3] op_sel_hi:[0,1]
	v_mov_b32_e32 v3, v2
	s_nop 1
	v_permlane16_swap_b32_e32 v2, v3
	v_add_f32_e32 v6, v2, v3
	v_mov_b32_e32 v8, v6
	s_nop 1
	v_permlane32_swap_b32_e32 v6, v8
	v_pk_add_f32 v[2:3], v[6:7], v[8:9]
	v_mov_b32_e32 v97, v95
	v_pk_fma_f32 v[6:7], v[2:3], s[6:7], v[106:107] op_sel_hi:[1,1,0]
	s_nop 0
	v_permlane32_swap_b32_e32 v95, v97
	v_mul_f32_e32 v2, 0x4b800000, v7
	v_cmp_gt_f32_e32 vcc, s95, v7
	s_waitcnt vmcnt(7)
	v_and_b32_e32 v111, 0xffff0000, v25
	v_lshlrev_b32_e32 v110, 16, v25
	v_cndmask_b32_e32 v2, v7, v2, vcc
	v_rsq_f32_e32 v2, v2
	v_and_b32_e32 v117, 0xffff0000, v24
	v_lshlrev_b32_e32 v116, 16, v24
	v_and_b32_e32 v25, 0xffff0000, v11
	v_mul_f32_e32 v3, 0x45800000, v2
	v_cndmask_b32_e32 v94, v2, v3, vcc
	s_waitcnt vmcnt(5)
	v_pk_mul_f32 v[2:3], v[94:95], v[40:41] op_sel_hi:[0,1]
	v_pk_mul_f32 v[2:3], v[2:3], v[16:17]
	s_waitcnt vmcnt(4)
	v_pk_mul_f32 v[8:9], v[42:43], v[94:95] op_sel_hi:[1,0]
	v_pk_mul_f32 v[2:3], v[2:3], s[82:83] op_sel_hi:[1,0]
	v_pk_mul_f32 v[8:9], v[8:9], v[124:125]
	v_cvt_pk_bf16_f32 v5, v2, v3
	v_pk_mul_f32 v[2:3], v[94:95], v[38:39] op_sel_hi:[0,1]
	v_pk_mul_f32 v[2:3], v[2:3], v[120:121]
	v_pk_mul_f32 v[8:9], v[8:9], s[82:83] op_sel_hi:[1,0]
	v_pk_mul_f32 v[2:3], v[2:3], s[82:83] op_sel_hi:[1,0]
	s_waitcnt vmcnt(3)
	v_pk_mul_f32 v[16:17], v[46:47], v[94:95] op_sel_hi:[1,0]
	v_cvt_pk_bf16_f32 v4, v2, v3
	v_pk_mul_f32 v[2:3], v[94:95], v[44:45] op_sel_hi:[0,1]
	v_pk_mul_f32 v[2:3], v[2:3], v[122:123]
	v_pk_mul_f32 v[16:17], v[16:17], v[132:133]
	v_pk_mul_f32 v[2:3], v[2:3], s[82:83] op_sel_hi:[1,0]
	v_pk_mul_f32 v[16:17], v[16:17], s[82:83] op_sel_hi:[1,0]
	v_cvt_pk_bf16_f32 v3, v2, v3
	v_cvt_pk_bf16_f32 v2, v8, v9
	v_pk_mul_f32 v[8:9], v[48:49], v[94:95] op_sel_hi:[1,0]
	v_lshlrev_b32_e32 v24, 16, v11
	v_pk_mul_f32 v[8:9], v[8:9], v[126:127]
	v_mul_f32_e32 v11, 0x4b800000, v6
	v_pk_mul_f32 v[8:9], v[8:9], s[82:83] op_sel_hi:[1,0]
	v_cmp_gt_f32_e32 vcc, s95, v6
	v_cvt_pk_bf16_f32 v9, v8, v9
	v_cvt_pk_bf16_f32 v8, v16, v17
	s_waitcnt vmcnt(2)
	v_pk_mul_f32 v[16:17], v[52:53], v[94:95] op_sel_hi:[1,0]
	v_cndmask_b32_e32 v6, v6, v11, vcc
	v_pk_mul_f32 v[16:17], v[16:17], v[134:135]
	v_rsq_f32_e32 v11, v6
	v_pk_mul_f32 v[16:17], v[16:17], s[82:83] op_sel_hi:[1,0]
	v_and_b32_e32 v83, 0xffff0000, v37
	v_cvt_pk_bf16_f32 v7, v16, v17
	v_pk_mul_f32 v[16:17], v[50:51], v[94:95] op_sel_hi:[1,0]
	v_lshlrev_b32_e32 v82, 16, v37
	v_pk_mul_f32 v[16:17], v[16:17], v[136:137]
	v_and_b32_e32 v91, 0xffff0000, v36
	v_pk_mul_f32 v[16:17], v[16:17], s[82:83] op_sel_hi:[1,0]
	v_lshlrev_b32_e32 v90, 16, v36
	v_cvt_pk_bf16_f32 v6, v16, v17
	v_mul_f32_e32 v16, 0x45800000, v11
	v_cndmask_b32_e32 v16, v11, v16, vcc
	v_pk_mul_f32 v[122:123], v[16:17], v[12:13] op_sel_hi:[0,1]
	v_pk_mul_f32 v[12:13], v[16:17], v[150:151] op_sel_hi:[0,1]
	s_waitcnt vmcnt(1)
	v_pk_mul_f32 v[12:13], v[12:13], v[56:57]
	v_and_b32_e32 v37, 0xffff0000, v23
	v_lshlrev_b32_e32 v36, 16, v23
	v_pk_mul_f32 v[120:121], v[16:17], v[154:155] op_sel_hi:[0,1]
	v_pk_mul_f32 v[124:125], v[16:17], v[152:153] op_sel_hi:[0,1]
	v_mov_b32_e32 v11, v12
	v_mov_b32_e32 v16, v12
	v_mov_b32_e32 v17, v13
	v_mov_b32_e32 v23, v13
	v_permlane16_swap_b32_e32 v11, v16
	s_nop 0
	v_permlane16_swap_b32_e32 v17, v23
	v_cmp_eq_u32_e32 vcc, 0, v112
	v_and_b32_e32 v99, 0xffff0000, v35
	v_lshlrev_b32_e32 v98, 16, v35
	v_cndmask_b32_e32 v17, v17, v23, vcc
	v_cndmask_b32_e32 v16, v11, v16, vcc
	v_pk_fma_f32 v[12:13], v[16:17], 0, v[12:13] op_sel_hi:[1,0,1]
	v_pk_mul_f32 v[16:17], v[54:55], v[124:125]
	v_pk_mul_f32 v[12:13], v[12:13], s[82:83] op_sel_hi:[1,0]
	v_mov_b32_e32 v11, v16
	v_cvt_pk_bf16_f32 v13, v12, v13
	v_mov_b32_e32 v12, v16
	v_mov_b32_e32 v23, v17
	v_mov_b32_e32 v35, v17
	v_permlane16_swap_b32_e32 v11, v12
	s_nop 0
	v_permlane16_swap_b32_e32 v23, v35
	v_cndmask_b32_e32 v125, v23, v35, vcc
	v_cndmask_b32_e32 v124, v11, v12, vcc
	v_pk_fma_f32 v[16:17], v[124:125], 0, v[16:17] op_sel_hi:[1,0,1]
	v_mov_b32_e32 v131, v129
	v_pk_mul_f32 v[16:17], v[16:17], s[82:83] op_sel_hi:[1,0]
	s_nop 0
	v_permlane32_swap_b32_e32 v129, v131
	v_cvt_pk_bf16_f32 v12, v16, v17
	s_waitcnt vmcnt(0)
; __device__ __forceinline__ unsigned cvtpk(float lo, float hi) { f32x2 v = {lo, hi}; bf16x2_t b = __builtin_convertvector(v, bf16x2_t); return __builtin_bit_cast(unsigned, b); }
; template <int DQK, int DV, bool LEAD> ...
;     ...
;           const float rn = rsqrtf(sn * (1.f / 64.f) + EPS);
; #pragma unroll
;           for (int ds = 0; ds < 2; ++ds)
; #pragma unroll
;               for (int j = 0; j < 8; ++j) x[ds][j] *= rn * qgain[32 * ds + 8 * g4 + j];
;           if constexpr (DQK == 64) {
; #pragma unroll
;               for (int ds = 0; ds < 2; ++ds)
; #pragma unroll
;                   for (int j = 0; j < 8; ++j) {
;                       auto rr = __builtin_amdgcn_permlane32_swap(__float_as_uint(x[ds][j]), __float_as_uint(x[ds][j]), false, false);
;                       const float other = hi ? __uint_as_float(rr[0]) : __uint_as_float(rr[1]);
;                       float cc = 1.f, sg = 0.f;
;                       if (lat) { const f32x2 cs = rope[(ds ? pcol : prow) * 16 + 8 * (g4 & 1) + j]; cc = cs.x; sg = hi ? cs.y : -cs.y; }
;                       x[ds][j] = x[ds][j] * cc + other * sg; }
;           } else {
;               float sr = 0.f;
; #pragma unroll
;               for (int j = 0; j < 8; ++j) sr += x[2][j] * x[2][j];
;               sr = lanes4_sum(sr);
;               const float rq = rsqrtf(sr * (1.f / 32.f) + EPS);
; #pragma unroll
;               for (int j = 0; j < 8; ++j) { const float av = x[2][j] * rq * qgain[64 + 8 * g4 + j];
;                   auto rr = __builtin_amdgcn_permlane16_swap(__float_as_uint(av), __float_as_uint(av), false, false);
;                   const float other = (g4 & 1) ? __uint_as_float(rr[0]) : __uint_as_float(rr[1]);
;                   float cc = 1.f, sg = 0.f;
;                   if (lat) { const f32x2 cs = rope[((g4 & 2) ? pcol : prow) * 8 + j]; cc = cs.x; sg = (g4 & 1) ? cs.y : -cs.y; }
;                   x[2][j] = av * cc + other * sg; }
;           }
; #pragma unroll
;           for (int ds = 0; ds < NDS; ++ds) { u32x4 w;
; #pragma unroll
;               for (int i = 0; i < 4; ++i) w[i] = cvtpk(x[ds][2 * i] * c2, x[ds][2 * i + 1] * c2);
;               qf[qb * NDS + ds] = __builtin_bit_cast(bf16x8, w); }
	v_pk_mul_f32 v[16:17], v[60:61], v[122:123]
	v_mov_b32_e32 v115, v113
	v_mov_b32_e32 v11, v16
	v_mov_b32_e32 v23, v16
	v_mov_b32_e32 v35, v17
	v_mov_b32_e32 v94, v17
	v_permlane16_swap_b32_e32 v11, v23
	s_nop 0
	v_permlane16_swap_b32_e32 v35, v94
	v_cndmask_b32_e32 v123, v35, v94, vcc
	v_cndmask_b32_e32 v122, v11, v23, vcc
	v_pk_fma_f32 v[16:17], v[122:123], 0, v[16:17] op_sel_hi:[1,0,1]
	v_and_b32_e32 v123, 0xffff0000, v10
	v_pk_mul_f32 v[16:17], v[16:17], s[82:83] op_sel_hi:[1,0]
	v_lshlrev_b32_e32 v122, 16, v10
	v_cvt_pk_bf16_f32 v11, v16, v17
	v_mul_f32_e32 v10, v123, v123
	v_pk_fma_f32 v[124:125], v[122:123], v[122:123], v[10:11] op_sel_hi:[1,1,0]
	v_mul_f32_e32 v10, v25, v25
	v_pk_fma_f32 v[124:125], v[24:25], v[24:25], v[124:125]
	v_pk_mul_f32 v[16:17], v[58:59], v[120:121]
	v_pk_add_f32 v[124:125], v[10:11], v[124:125] op_sel_hi:[0,1]
	v_pk_fma_f32 v[124:125], v[140:141], v[140:141], v[124:125]
	v_mul_f32_e32 v10, v141, v141
	v_pk_add_f32 v[124:125], v[10:11], v[124:125] op_sel_hi:[0,1]
	v_pk_fma_f32 v[124:125], v[138:139], v[138:139], v[124:125]
	v_mul_f32_e32 v10, v139, v139
	v_pk_add_f32 v[124:125], v[10:11], v[124:125] op_sel_hi:[0,1]
	v_mov_b32_e32 v10, v124
	s_nop 1
	v_permlane16_swap_b32_e32 v124, v10
	v_add_f32_e32 v128, v124, v10
	v_mov_b32_e32 v130, v128
	s_nop 1
	v_permlane32_swap_b32_e32 v128, v130
	v_pk_add_f32 v[124:125], v[128:129], v[130:131]
	v_mov_b32_e32 v23, v16
	v_pk_fma_f32 v[124:125], v[124:125], s[6:7], v[106:107] op_sel_hi:[1,1,0]
	v_mov_b32_e32 v35, v16
	v_mul_f32_e32 v10, 0x4b800000, v125
	v_cmp_gt_f32_e64 s[4:5], s95, v125
	v_permlane16_swap_b32_e32 v23, v35
	v_mov_b32_e32 v94, v17
	v_mov_b32_e32 v96, v17
	v_cndmask_b32_e64 v10, v125, v10, s[4:5]
	s_nop 0
	v_permlane16_swap_b32_e32 v94, v96
	v_cndmask_b32_e32 v120, v23, v35, vcc
	v_rsq_f32_e32 v23, v10
	v_cndmask_b32_e32 v121, v94, v96, vcc
	v_pk_fma_f32 v[16:17], v[120:121], 0, v[16:17] op_sel_hi:[1,0,1]
	v_permlane32_swap_b32_e32 v113, v115
	v_pk_mul_f32 v[16:17], v[16:17], s[82:83] op_sel_hi:[1,0]
	s_mov_b32 s26, 0
	v_cvt_pk_bf16_f32 v10, v16, v17
	v_mul_f32_e32 v16, 0x45800000, v23
	v_cndmask_b32_e64 v94, v23, v16, s[4:5]
	v_pk_mul_f32 v[16:17], v[40:41], v[94:95] op_sel_hi:[1,0]
	v_cmp_gt_f32_e64 s[4:5], s95, v124
	v_pk_mul_f32 v[14:15], v[16:17], v[14:15]
	s_nop 0
	v_pk_mul_f32 v[14:15], v[14:15], s[82:83] op_sel_hi:[1,0]
	s_nop 0
	v_cvt_pk_bf16_f32 v17, v14, v15
	v_pk_mul_f32 v[14:15], v[38:39], v[94:95] op_sel_hi:[1,0]
	s_nop 0
	v_pk_mul_f32 v[14:15], v[14:15], v[18:19]
	v_pk_mul_f32 v[18:19], v[42:43], v[94:95] op_sel_hi:[1,0]
	v_pk_mul_f32 v[14:15], v[14:15], s[82:83] op_sel_hi:[1,0]
	v_pk_mul_f32 v[18:19], v[18:19], v[28:29]
	v_cvt_pk_bf16_f32 v16, v14, v15
	v_pk_mul_f32 v[14:15], v[44:45], v[94:95] op_sel_hi:[1,0]
	v_pk_mul_f32 v[18:19], v[18:19], s[82:83] op_sel_hi:[1,0]
	v_pk_mul_f32 v[14:15], v[14:15], v[20:21]
	v_pk_mul_f32 v[28:29], v[50:51], v[94:95] op_sel_hi:[1,0]
	v_pk_mul_f32 v[14:15], v[14:15], s[82:83] op_sel_hi:[1,0]
	v_pk_mul_f32 v[28:29], v[28:29], v[118:119]
	v_cvt_pk_bf16_f32 v15, v14, v15
	v_cvt_pk_bf16_f32 v14, v18, v19
	v_pk_mul_f32 v[18:19], v[48:49], v[94:95] op_sel_hi:[1,0]
	v_pk_mul_f32 v[28:29], v[28:29], s[82:83] op_sel_hi:[1,0]
	v_pk_mul_f32 v[18:19], v[18:19], v[102:103]
	s_nop 0
	v_pk_mul_f32 v[18:19], v[18:19], s[82:83] op_sel_hi:[1,0]
	s_nop 0
	v_cvt_pk_bf16_f32 v21, v18, v19
	v_pk_mul_f32 v[18:19], v[46:47], v[94:95] op_sel_hi:[1,0]
	s_nop 0
	v_pk_mul_f32 v[18:19], v[18:19], v[104:105]
	s_nop 0
	v_pk_mul_f32 v[18:19], v[18:19], s[82:83] op_sel_hi:[1,0]
	s_nop 0
	v_cvt_pk_bf16_f32 v20, v18, v19
	v_pk_mul_f32 v[18:19], v[52:53], v[94:95] op_sel_hi:[1,0]
	s_nop 0
	v_pk_mul_f32 v[18:19], v[18:19], v[108:109]
	s_nop 0
	v_pk_mul_f32 v[18:19], v[18:19], s[82:83] op_sel_hi:[1,0]
	s_nop 0
	v_cvt_pk_bf16_f32 v19, v18, v19
	v_mul_f32_e32 v18, 0x4b800000, v124
	v_cndmask_b32_e64 v18, v124, v18, s[4:5]
	v_rsq_f32_e32 v23, v18
	v_cvt_pk_bf16_f32 v18, v28, v29
	v_mul_f32_e32 v28, 0x45800000, v23
	v_cndmask_b32_e64 v28, v23, v28, s[4:5]
	v_pk_mul_f32 v[104:105], v[28:29], v[24:25] op_sel_hi:[0,1]
	v_pk_mul_f32 v[24:25], v[28:29], v[138:139] op_sel_hi:[0,1]
	v_pk_mul_f32 v[24:25], v[56:57], v[24:25]
	v_pk_mul_f32 v[102:103], v[28:29], v[122:123] op_sel_hi:[0,1]
	v_pk_mul_f32 v[108:109], v[28:29], v[140:141] op_sel_hi:[0,1]
	v_mov_b32_e32 v23, v24
	v_mov_b32_e32 v28, v24
	v_mov_b32_e32 v29, v25
	v_mov_b32_e32 v35, v25
	v_permlane16_swap_b32_e32 v23, v28
	s_nop 0
	v_permlane16_swap_b32_e32 v29, v35
	v_cndmask_b32_e32 v29, v29, v35, vcc
	v_cndmask_b32_e32 v28, v23, v28, vcc
	v_pk_fma_f32 v[24:25], v[28:29], 0, v[24:25] op_sel_hi:[1,0,1]
	v_pk_mul_f32 v[28:29], v[54:55], v[108:109]
	v_pk_mul_f32 v[24:25], v[24:25], s[82:83] op_sel_hi:[1,0]
	v_mov_b32_e32 v23, v28
	v_cvt_pk_bf16_f32 v25, v24, v25
	v_mov_b32_e32 v24, v28
	v_mov_b32_e32 v35, v29
	v_mov_b32_e32 v94, v29
	v_permlane16_swap_b32_e32 v23, v24
	s_nop 0
	v_permlane16_swap_b32_e32 v35, v94
	v_cndmask_b32_e32 v109, v35, v94, vcc
	v_cndmask_b32_e32 v108, v23, v24, vcc
	v_pk_fma_f32 v[28:29], v[108:109], 0, v[28:29] op_sel_hi:[1,0,1]
	s_nop 0
	v_pk_mul_f32 v[28:29], v[28:29], s[82:83] op_sel_hi:[1,0]
	s_nop 0
	v_cvt_pk_bf16_f32 v24, v28, v29
	v_pk_mul_f32 v[28:29], v[60:61], v[104:105]
	s_nop 0
	v_mov_b32_e32 v23, v28
	v_mov_b32_e32 v35, v28
	v_mov_b32_e32 v94, v29
	v_mov_b32_e32 v96, v29
	v_permlane16_swap_b32_e32 v23, v35
	s_nop 0
	v_permlane16_swap_b32_e32 v94, v96
	v_cndmask_b32_e32 v105, v94, v96, vcc
	v_cndmask_b32_e32 v104, v23, v35, vcc
	v_pk_fma_f32 v[28:29], v[104:105], 0, v[28:29] op_sel_hi:[1,0,1]
	v_and_b32_e32 v105, 0xffff0000, v22
; __device__ __forceinline__ unsigned cvtpk(float lo, float hi) { f32x2 v = {lo, hi}; bf16x2_t b = __builtin_convertvector(v, bf16x2_t); return __builtin_bit_cast(unsigned, b); }
; template <int DQK, int DV, bool LEAD> ...
;     ...
;           const float rn = rsqrtf(sn * (1.f / 64.f) + EPS);
; #pragma unroll
;           for (int ds = 0; ds < 2; ++ds)
; #pragma unroll
;               for (int j = 0; j < 8; ++j) x[ds][j] *= rn * qgain[32 * ds + 8 * g4 + j];
;           if constexpr (DQK == 64) {
; #pragma unroll
;               for (int ds = 0; ds < 2; ++ds)
; #pragma unroll
;                   for (int j = 0; j < 8; ++j) {
;                       auto rr = __builtin_amdgcn_permlane32_swap(__float_as_uint(x[ds][j]), __float_as_uint(x[ds][j]), false, false);
;                       const float other = hi ? __uint_as_float(rr[0]) : __uint_as_float(rr[1]);
;                       float cc = 1.f, sg = 0.f;
;                       if (lat) { const f32x2 cs = rope[(ds ? pcol : prow) * 16 + 8 * (g4 & 1) + j]; cc = cs.x; sg = hi ? cs.y : -cs.y; }
;                       x[ds][j] = x[ds][j] * cc + other * sg; }
;           } else {
;               float sr = 0.f;
; #pragma unroll
;               for (int j = 0; j < 8; ++j) sr += x[2][j] * x[2][j];
;               sr = lanes4_sum(sr);
;               const float rq = rsqrtf(sr * (1.f / 32.f) + EPS);
; #pragma unroll
;               for (int j = 0; j < 8; ++j) { const float av = x[2][j] * rq * qgain[64 + 8 * g4 + j];
;                   auto rr = __builtin_amdgcn_permlane16_swap(__float_as_uint(av), __float_as_uint(av), false, false);
;                   const float other = (g4 & 1) ? __uint_as_float(rr[0]) : __uint_as_float(rr[1]);
;                   float cc = 1.f, sg = 0.f;
;                   if (lat) { const f32x2 cs = rope[((g4 & 2) ? pcol : prow) * 8 + j]; cc = cs.x; sg = (g4 & 1) ? cs.y : -cs.y; }
;                   x[2][j] = av * cc + other * sg; }
;           }
; #pragma unroll
;           for (int ds = 0; ds < NDS; ++ds) { u32x4 w;
; #pragma unroll
;               for (int i = 0; i < 4; ++i) w[i] = cvtpk(x[ds][2 * i] * c2, x[ds][2 * i + 1] * c2);
;               qf[qb * NDS + ds] = __builtin_bit_cast(bf16x8, w); }
	v_pk_mul_f32 v[28:29], v[28:29], s[82:83] op_sel_hi:[1,0]
	v_lshlrev_b32_e32 v104, 16, v22
	v_cvt_pk_bf16_f32 v23, v28, v29
	v_mul_f32_e32 v22, v105, v105
	v_pk_fma_f32 v[108:109], v[104:105], v[104:105], v[22:23] op_sel_hi:[1,1,0]
	v_mul_f32_e32 v22, v37, v37
	v_pk_fma_f32 v[108:109], v[36:37], v[36:37], v[108:109]
	v_pk_mul_f32 v[28:29], v[58:59], v[102:103]
	v_pk_add_f32 v[108:109], v[22:23], v[108:109] op_sel_hi:[0,1]
	v_pk_fma_f32 v[108:109], v[116:117], v[116:117], v[108:109]
	v_mul_f32_e32 v22, v117, v117
	v_pk_add_f32 v[108:109], v[22:23], v[108:109] op_sel_hi:[0,1]
	v_pk_fma_f32 v[108:109], v[110:111], v[110:111], v[108:109]
	v_mul_f32_e32 v22, v111, v111
	v_pk_add_f32 v[108:109], v[22:23], v[108:109] op_sel_hi:[0,1]
	v_mov_b32_e32 v22, v108
	s_nop 1
	v_permlane16_swap_b32_e32 v108, v22
	v_add_f32_e32 v112, v108, v22
	v_mov_b32_e32 v114, v112
	s_nop 1
	v_permlane32_swap_b32_e32 v112, v114
	v_pk_add_f32 v[108:109], v[112:113], v[114:115]
	v_mov_b32_e32 v35, v28
	v_pk_fma_f32 v[108:109], v[108:109], s[6:7], v[106:107] op_sel_hi:[1,1,0]
	v_mov_b32_e32 v94, v28
	v_mov_b32_e32 v96, v29
	v_mov_b32_e32 v102, v29
	v_mul_f32_e32 v22, 0x4b800000, v109
	v_cmp_gt_f32_e64 s[4:5], s95, v109
	v_permlane16_swap_b32_e32 v35, v94
	v_permlane16_swap_b32_e32 v96, v102
	v_cndmask_b32_e64 v22, v109, v22, s[4:5]
	v_cndmask_b32_e32 v103, v96, v102, vcc
	v_cndmask_b32_e32 v102, v35, v94, vcc
	v_rsq_f32_e32 v35, v22
	v_pk_fma_f32 v[28:29], v[102:103], 0, v[28:29] op_sel_hi:[1,0,1]
	s_nop 0
	v_pk_mul_f32 v[28:29], v[28:29], s[82:83] op_sel_hi:[1,0]
	s_nop 0
	v_cvt_pk_bf16_f32 v22, v28, v29
	v_mul_f32_e32 v28, 0x45800000, v35
	v_cndmask_b32_e64 v94, v35, v28, s[4:5]
	v_pk_mul_f32 v[28:29], v[40:41], v[94:95] op_sel_hi:[1,0]
	v_cmp_gt_f32_e64 s[4:5], s95, v108
	v_pk_mul_f32 v[26:27], v[28:29], v[26:27]
	s_nop 0
	v_pk_mul_f32 v[26:27], v[26:27], s[82:83] op_sel_hi:[1,0]
	s_nop 0
	v_cvt_pk_bf16_f32 v29, v26, v27
	v_pk_mul_f32 v[26:27], v[38:39], v[94:95] op_sel_hi:[1,0]
	s_nop 0
	v_pk_mul_f32 v[26:27], v[26:27], v[30:31]
	v_pk_mul_f32 v[30:31], v[42:43], v[94:95] op_sel_hi:[1,0]
	v_pk_mul_f32 v[26:27], v[26:27], s[82:83] op_sel_hi:[1,0]
	v_pk_mul_f32 v[30:31], v[30:31], v[80:81]
	v_cvt_pk_bf16_f32 v28, v26, v27
	v_pk_mul_f32 v[26:27], v[44:45], v[94:95] op_sel_hi:[1,0]
	v_pk_mul_f32 v[30:31], v[30:31], s[82:83] op_sel_hi:[1,0]
	v_pk_mul_f32 v[26:27], v[26:27], v[32:33]
	v_pk_mul_f32 v[80:81], v[50:51], v[94:95] op_sel_hi:[1,0]
	v_pk_mul_f32 v[26:27], v[26:27], s[82:83] op_sel_hi:[1,0]
	v_pk_mul_f32 v[80:81], v[80:81], v[100:101]
	v_cvt_pk_bf16_f32 v27, v26, v27
	v_cvt_pk_bf16_f32 v26, v30, v31
	v_pk_mul_f32 v[30:31], v[48:49], v[94:95] op_sel_hi:[1,0]
	v_pk_mul_f32 v[80:81], v[80:81], s[82:83] op_sel_hi:[1,0]
	v_pk_mul_f32 v[30:31], v[30:31], v[84:85]
	s_nop 0
	v_pk_mul_f32 v[30:31], v[30:31], s[82:83] op_sel_hi:[1,0]
	s_nop 0
	v_cvt_pk_bf16_f32 v33, v30, v31
	v_pk_mul_f32 v[30:31], v[46:47], v[94:95] op_sel_hi:[1,0]
	s_nop 0
	v_pk_mul_f32 v[30:31], v[30:31], v[86:87]
	s_nop 0
	v_pk_mul_f32 v[30:31], v[30:31], s[82:83] op_sel_hi:[1,0]
	s_nop 0
	v_cvt_pk_bf16_f32 v32, v30, v31
	v_pk_mul_f32 v[30:31], v[52:53], v[94:95] op_sel_hi:[1,0]
	s_nop 0
	v_pk_mul_f32 v[30:31], v[30:31], v[92:93]
	s_nop 0
	v_pk_mul_f32 v[30:31], v[30:31], s[82:83] op_sel_hi:[1,0]
	s_nop 0
	v_cvt_pk_bf16_f32 v31, v30, v31
	v_mul_f32_e32 v30, 0x4b800000, v108
	v_cndmask_b32_e64 v30, v108, v30, s[4:5]
	v_rsq_f32_e32 v35, v30
	v_cvt_pk_bf16_f32 v30, v80, v81
	v_mul_f32_e32 v80, 0x45800000, v35
	v_cndmask_b32_e64 v80, v35, v80, s[4:5]
	v_pk_mul_f32 v[86:87], v[80:81], v[36:37] op_sel_hi:[0,1]
	v_pk_mul_f32 v[36:37], v[80:81], v[110:111] op_sel_hi:[0,1]
	v_pk_mul_f32 v[36:37], v[56:57], v[36:37]
	v_pk_mul_f32 v[84:85], v[80:81], v[104:105] op_sel_hi:[0,1]
	v_pk_mul_f32 v[92:93], v[80:81], v[116:117] op_sel_hi:[0,1]
	v_mov_b32_e32 v35, v36
	v_mov_b32_e32 v80, v36
	v_mov_b32_e32 v81, v37
	v_mov_b32_e32 v94, v37
	v_permlane16_swap_b32_e32 v35, v80
	s_nop 0
	v_permlane16_swap_b32_e32 v81, v94
	v_cndmask_b32_e32 v81, v81, v94, vcc
	v_cndmask_b32_e32 v80, v35, v80, vcc
	v_pk_fma_f32 v[36:37], v[80:81], 0, v[36:37] op_sel_hi:[1,0,1]
	v_pk_mul_f32 v[80:81], v[54:55], v[92:93]
	v_pk_mul_f32 v[36:37], v[36:37], s[82:83] op_sel_hi:[1,0]
	v_mov_b32_e32 v35, v80
	v_cvt_pk_bf16_f32 v37, v36, v37
	v_mov_b32_e32 v36, v80
	v_mov_b32_e32 v92, v81
	v_mov_b32_e32 v93, v81
	v_permlane16_swap_b32_e32 v35, v36
	s_nop 0
	v_permlane16_swap_b32_e32 v92, v93
	v_cndmask_b32_e32 v93, v92, v93, vcc
	v_cndmask_b32_e32 v92, v35, v36, vcc
	v_pk_fma_f32 v[80:81], v[92:93], 0, v[80:81] op_sel_hi:[1,0,1]
	s_nop 0
	v_pk_mul_f32 v[80:81], v[80:81], s[82:83] op_sel_hi:[1,0]
	s_nop 0
	v_cvt_pk_bf16_f32 v36, v80, v81
	v_pk_mul_f32 v[80:81], v[60:61], v[86:87]
	s_nop 0
	v_mov_b32_e32 v35, v80
	v_mov_b32_e32 v86, v80
	v_mov_b32_e32 v87, v81
	v_mov_b32_e32 v92, v81
	v_permlane16_swap_b32_e32 v35, v86
	s_nop 0
	v_permlane16_swap_b32_e32 v87, v92
	v_cndmask_b32_e32 v87, v87, v92, vcc
	v_cndmask_b32_e32 v86, v35, v86, vcc
	v_pk_fma_f32 v[80:81], v[86:87], 0, v[80:81] op_sel_hi:[1,0,1]
	s_nop 0
	v_pk_mul_f32 v[80:81], v[80:81], s[82:83] op_sel_hi:[1,0]
	s_nop 0
	v_cvt_pk_bf16_f32 v35, v80, v81
	v_pk_mul_f32 v[80:81], v[58:59], v[84:85]
	s_nop 0
	v_mov_b32_e32 v85, v81
	v_mov_b32_e32 v87, v81
	v_mov_b32_e32 v84, v80
	v_mov_b32_e32 v86, v80
	v_permlane16_swap_b32_e32 v85, v87
	s_nop 0
	v_permlane16_swap_b32_e32 v84, v86
	v_cndmask_b32_e32 v85, v85, v87, vcc
	v_and_b32_e32 v87, 0xffff0000, v34
	v_cndmask_b32_e32 v84, v84, v86, vcc
	v_lshlrev_b32_e32 v86, 16, v34
	v_mul_f32_e32 v34, v87, v87
	v_pk_fma_f32 v[92:93], v[86:87], v[86:87], v[34:35] op_sel_hi:[1,1,0]
; __device__ __forceinline__ unsigned cvtpk(float lo, float hi) { f32x2 v = {lo, hi}; bf16x2_t b = __builtin_convertvector(v, bf16x2_t); return __builtin_bit_cast(unsigned, b); }
; template <int DQK, int DV, bool LEAD> ...
;     ...
;               float sr = 0.f;
; #pragma unroll
;               for (int j = 0; j < 8; ++j) sr += x[2][j] * x[2][j];
;               sr = lanes4_sum(sr);
;               const float rq = rsqrtf(sr * (1.f / 32.f) + EPS);
; #pragma unroll
;               for (int j = 0; j < 8; ++j) { const float av = x[2][j] * rq * qgain[64 + 8 * g4 + j];
;                   auto rr = __builtin_amdgcn_permlane16_swap(__float_as_uint(av), __float_as_uint(av), false, false);
;                   const float other = (g4 & 1) ? __uint_as_float(rr[0]) : __uint_as_float(rr[1]);
;                   float cc = 1.f, sg = 0.f;
;                   if (lat) { const f32x2 cs = rope[((g4 & 2) ? pcol : prow) * 8 + j]; cc = cs.x; sg = (g4 & 1) ? cs.y : -cs.y; }
;                   x[2][j] = av * cc + other * sg; }
;           }
; #pragma unroll
;           for (int ds = 0; ds < NDS; ++ds) { u32x4 w;
; #pragma unroll
;               for (int i = 0; i < 4; ++i) w[i] = cvtpk(x[ds][2 * i] * c2, x[ds][2 * i + 1] * c2);
;               qf[qb * NDS + ds] = __builtin_bit_cast(bf16x8, w); }
;       }
; #pragma unroll
;       for (int d0 = 0; d0 < NQB * NDS; ++d0) asm volatile("" : "+v"(qf[d0])); }
;     wait_bar<0>();
	v_mul_f32_e32 v34, v99, v99
	v_pk_fma_f32 v[92:93], v[98:99], v[98:99], v[92:93]
	v_pk_fma_f32 v[80:81], v[84:85], 0, v[80:81] op_sel_hi:[1,0,1]
	v_pk_add_f32 v[92:93], v[34:35], v[92:93] op_sel_hi:[0,1]
	v_pk_fma_f32 v[92:93], v[90:91], v[90:91], v[92:93]
	v_mul_f32_e32 v34, v91, v91
	v_pk_add_f32 v[92:93], v[34:35], v[92:93] op_sel_hi:[0,1]
	v_pk_fma_f32 v[92:93], v[82:83], v[82:83], v[92:93]
	v_mul_f32_e32 v34, v83, v83
	v_pk_add_f32 v[92:93], v[34:35], v[92:93] op_sel_hi:[0,1]
	v_mov_b32_e32 v34, v92
	s_nop 1
	v_permlane16_swap_b32_e32 v92, v34
	v_add_f32_e32 v94, v92, v34
	v_mov_b32_e32 v96, v94
	s_nop 1
	v_permlane32_swap_b32_e32 v94, v96
	v_pk_add_f32 v[92:93], v[94:95], v[96:97]
	v_pk_mul_f32 v[80:81], v[80:81], s[82:83] op_sel_hi:[1,0]
	v_pk_fma_f32 v[92:93], v[92:93], s[6:7], v[106:107] op_sel_hi:[1,1,0]
	s_lshl_b32 s6, s25, 6
	v_mul_f32_e32 v34, 0x4b800000, v93
	v_cmp_gt_f32_e64 s[4:5], s95, v93
	s_mov_b32 s25, 1
	s_mov_b32 s7, 2
	v_cndmask_b32_e64 v34, v93, v34, s[4:5]
	v_rsq_f32_e32 v93, v34
	v_cvt_pk_bf16_f32 v34, v80, v81
	v_lshrrev_b32_e32 v106, 1, v142
	v_mul_f32_e32 v80, 0x45800000, v93
	v_cndmask_b32_e64 v80, v93, v80, s[4:5]
	v_pk_mul_f32 v[50:51], v[50:51], v[80:81] op_sel_hi:[1,0]
	v_pk_mul_f32 v[52:53], v[52:53], v[80:81] op_sel_hi:[1,0]
	v_pk_mul_f32 v[38:39], v[38:39], v[80:81] op_sel_hi:[1,0]
	v_pk_mul_f32 v[50:51], v[50:51], v[88:89]
	v_pk_mul_f32 v[52:53], v[52:53], v[78:79]
	v_pk_mul_f32 v[46:47], v[46:47], v[80:81] op_sel_hi:[1,0]
	v_pk_mul_f32 v[48:49], v[48:49], v[80:81] op_sel_hi:[1,0]
	v_pk_mul_f32 v[68:69], v[38:39], v[68:69]
	v_pk_mul_f32 v[38:39], v[40:41], v[80:81] op_sel_hi:[1,0]
	v_pk_mul_f32 v[46:47], v[46:47], v[76:77]
	v_pk_mul_f32 v[48:49], v[48:49], v[74:75]
	v_pk_mul_f32 v[66:67], v[38:39], v[66:67]
	v_pk_mul_f32 v[38:39], v[50:51], s[82:83] op_sel_hi:[1,0]
	v_pk_mul_f32 v[40:41], v[52:53], s[82:83] op_sel_hi:[1,0]
	v_cvt_pk_bf16_f32 v38, v38, v39
	v_cvt_pk_bf16_f32 v39, v40, v41
	v_pk_mul_f32 v[40:41], v[46:47], s[82:83] op_sel_hi:[1,0]
	v_pk_mul_f32 v[46:47], v[48:49], s[82:83] op_sel_hi:[1,0]
	v_cvt_pk_bf16_f32 v40, v40, v41
	v_cvt_pk_bf16_f32 v41, v46, v47
	v_mul_f32_e32 v46, 0x4b800000, v92
	v_cmp_gt_f32_e64 s[4:5], s95, v92
	v_pk_mul_f32 v[42:43], v[42:43], v[80:81] op_sel_hi:[1,0]
	v_pk_mul_f32 v[44:45], v[44:45], v[80:81] op_sel_hi:[1,0]
	v_cndmask_b32_e64 v46, v92, v46, s[4:5]
	v_rsq_f32_e32 v48, v46
	v_pk_mul_f32 v[42:43], v[42:43], v[72:73]
	v_pk_mul_f32 v[44:45], v[44:45], v[70:71]
	v_pk_mul_f32 v[42:43], v[42:43], s[82:83] op_sel_hi:[1,0]
	v_pk_mul_f32 v[44:45], v[44:45], s[82:83] op_sel_hi:[1,0]
	v_cvt_pk_bf16_f32 v42, v42, v43
	v_cvt_pk_bf16_f32 v43, v44, v45
	v_pk_mul_f32 v[44:45], v[68:69], s[82:83] op_sel_hi:[1,0]
	v_pk_mul_f32 v[46:47], v[66:67], s[82:83] op_sel_hi:[1,0]
	v_cvt_pk_bf16_f32 v44, v44, v45
	v_cvt_pk_bf16_f32 v45, v46, v47
	v_mul_f32_e32 v46, 0x45800000, v48
	v_cndmask_b32_e64 v46, v48, v46, s[4:5]
	v_pk_mul_f32 v[48:49], v[46:47], v[86:87] op_sel_hi:[0,1]
	v_pk_mul_f32 v[48:49], v[58:59], v[48:49]
	v_bitop3_b32 v74, v148, v209, v147 bitop3:0x36
	v_mov_b32_e32 v47, v48
	v_mov_b32_e32 v50, v48
	v_mov_b32_e32 v51, v49
	v_mov_b32_e32 v52, v49
	v_permlane16_swap_b32_e32 v47, v50
	s_nop 0
	v_permlane16_swap_b32_e32 v51, v52
	v_cndmask_b32_e32 v51, v51, v52, vcc
	v_cndmask_b32_e32 v50, v47, v50, vcc
	v_pk_fma_f32 v[48:49], v[50:51], 0, v[48:49] op_sel_hi:[1,0,1]
	v_pk_mul_f32 v[50:51], v[46:47], v[98:99] op_sel_hi:[0,1]
	v_pk_mul_f32 v[50:51], v[60:61], v[50:51]
	v_lshl_add_u32 v212, v74, 4, v149
	v_mov_b32_e32 v47, v50
	v_mov_b32_e32 v52, v50
	v_mov_b32_e32 v53, v51
	v_mov_b32_e32 v58, v51
	v_permlane16_swap_b32_e32 v47, v52
	s_nop 0
	v_permlane16_swap_b32_e32 v53, v58
	v_cndmask_b32_e32 v53, v53, v58, vcc
	v_cndmask_b32_e32 v52, v47, v52, vcc
	v_pk_fma_f32 v[50:51], v[52:53], 0, v[50:51] op_sel_hi:[1,0,1]
	v_pk_mul_f32 v[52:53], v[46:47], v[90:91] op_sel_hi:[0,1]
	v_pk_mul_f32 v[52:53], v[54:55], v[52:53]
	s_lshl_b32 s4, s36, 11
	v_mov_b32_e32 v47, v52
	v_mov_b32_e32 v54, v52
	s_nop 1
	v_permlane16_swap_b32_e32 v47, v54
	v_mov_b32_e32 v55, v53
	v_mov_b32_e32 v58, v53
	s_nop 1
	v_permlane16_swap_b32_e32 v55, v58
	v_cndmask_b32_e32 v54, v47, v54, vcc
	v_pk_mul_f32 v[46:47], v[46:47], v[82:83] op_sel_hi:[0,1]
	v_cndmask_b32_e32 v55, v55, v58, vcc
	v_pk_mul_f32 v[46:47], v[56:57], v[46:47]
	v_pk_fma_f32 v[52:53], v[54:55], 0, v[52:53] op_sel_hi:[1,0,1]
	v_mov_b32_e32 v54, v46
	v_mov_b32_e32 v56, v46
	v_mov_b32_e32 v55, v47
	v_mov_b32_e32 v57, v47
	v_permlane16_swap_b32_e32 v54, v56
	s_nop 0
	v_permlane16_swap_b32_e32 v55, v57
	v_cndmask_b32_e32 v55, v55, v57, vcc
	v_cndmask_b32_e32 v54, v54, v56, vcc
	v_pk_fma_f32 v[54:55], v[54:55], 0, v[46:47] op_sel_hi:[1,0,1]
	v_pk_mul_f32 v[46:47], v[48:49], s[82:83] op_sel_hi:[1,0]
	v_pk_mul_f32 v[48:49], v[50:51], s[82:83] op_sel_hi:[1,0]
	v_cvt_pk_bf16_f32 v46, v46, v47
	v_cvt_pk_bf16_f32 v47, v48, v49
	v_pk_mul_f32 v[48:49], v[52:53], s[82:83] op_sel_hi:[1,0]
	v_pk_mul_f32 v[50:51], v[54:55], s[82:83] op_sel_hi:[1,0]
	v_cvt_pk_bf16_f32 v48, v48, v49
	v_cvt_pk_bf16_f32 v49, v50, v51
	s_waitcnt vmcnt(0) lgkmcnt(0)
	s_barrier
; #define ATT_SB() __builtin_amdgcn_sched_barrier(0)
; #define ATT_DMA_K(t, sl) do { glds16(ksrc + (size_t)(t) * 64 * kpitch, (unsigned)__builtin_amdgcn_readfirstlane(kdst + (sl) * KSLOT)); \
;         if constexpr (DQK == 96) glds16(krsrc + (size_t)(t) * 64 * 32, (unsigned)__builtin_amdgcn_readfirstlane(krdst + (sl) * KSLOT)); } while (0)
; #define ATT_DMA_V(t, sl) do { glds16(vsrc + (size_t)(t) * 64, (unsigned)__builtin_amdgcn_readfirstlane(vdst + (sl) * VSLOT)); \
;         if constexpr (DV == 128) glds16(vsrc + (size_t)64 * NR + (size_t)(t) * 64, (unsigned)__builtin_amdgcn_readfirstlane(vdst + (sl) * VSLOT + 8192)); } while (0)
; #define ATT_KLOAD(sl) do { _Pragma("unroll") for (int kb_ = 0; kb_ < NKW; ++kb_) _Pragma("unroll") for (int ds_ = 0; ds_ < NDS; ++ds_) { \
;         if (ds_ < 2) kf[kb_ * NDS + ds_] = *(const LAS bf16x8*)(kp[ds_ & 1] + (sl) * KSLOT + (kb_ & 1) * 512 + (kb_ >> 1) * 4096); \
;         else kf[kb_ * NDS + ds_] = *(const LAS bf16x8*)(krp + (sl) * KSLOT + (kb_ & 1) * 256 + (kb_ >> 1) * 2048); } } while (0)
; #define ATT_QK() do { _Pragma("unroll") for (int kb_ = 0; kb_ < NKW; ++kb_) _Pragma("unroll") for (int ds_ = 0; ds_ < NDS; ++ds_) _Pragma("unroll") for (int qb_ = 0; qb_ < NQB; ++qb_) \
;         c[kb_][qb_] = __builtin_amdgcn_mfma_f32_16x16x32_bf16(kf[kb_ * NDS + ds_], qf[qb_ * NDS + ds_], ds_ == 0 ? zero4 : c[kb_][qb_], 0, 0, 0); } while (0)
; #define ATT_EXP() do { _Pragma("unroll") for (int kb_ = 0; kb_ < NKW; ++kb_) _Pragma("unroll") for (int qb_ = 0; qb_ < NQB; ++qb_) _Pragma("unroll") for (int i_ = 0; i_ < 4; ++i_) \
;         c[kb_][qb_][i_] = __builtin_amdgcn_exp2f(c[kb_][qb_][i_]); } while (0)
; template <int DQK, int DV, bool LEAD> ...
;     ...
;     bf16x8 kf[NKW * NDS], vf[NVF];
;     ATT_KLOAD(0);
;     asm volatile("s_waitcnt lgkmcnt(0)\n\ts_barrier" ::: "memory");
;     float lsum[NQB];
; #pragma unroll
;     for (int qb = 0; qb < NQB; ++qb) lsum[qb] = 0.f;
;     const f32x4 zero4 = {0.f, 0.f, 0.f, 0.f};
;     f32x4 o[NDB][NQB], c[NKW][NQB]; u32x4 pw[4];
; #pragma unroll
;     for (int i = 0; i < NDB; ++i)
; #pragma unroll
;         for (int qb = 0; qb < NQB; ++qb) o[i][qb] = zero4;
;     ATT_DMA_K(3, 0); ATT_DMA_V(1, 1);
;     ATT_QK(); ATT_SB();
;     ATT_KLOAD(1); ATT_SB();
;     if constexpr (LEAD) { ATT_EXP(); ATT_SUMPACK(); }
;     wait_bar<NDMA>();
;     int s_prev = 0, s_cur = 1, s_next = 2;
	ds_read_b128 v[50:53], v208
	ds_read_b128 v[54:57], v208 offset:512
	s_waitcnt lgkmcnt(1)
	v_mfma_f32_16x16x32_bf16 v[58:61], v[50:53], v[6:9], 0
	ds_read_b128 v[74:77], v212
	ds_read_b128 v[78:81], v212 offset:512
	v_lshlrev_b32_e32 v82, 5, v146
	v_lshlrev_b32_e32 v83, 6, v144
	v_mfma_f32_16x16x32_bf16 v[66:69], v[50:53], v[18:21], 0
	v_bitop3_b32 v82, v82, v142, 48 bitop3:0x78
	v_sub_u32_e32 v83, v145, v83
	v_add3_u32 v213, v83, v82, s4
	v_mfma_f32_16x16x32_bf16 v[70:73], v[50:53], v[30:33], 0
	s_mov_b64 s[4:5], 0x60000
	v_lshl_add_u64 v[192:193], v[62:63], 0, s[4:5]
	s_cmpk_lt_u32 s16, 0x100
	v_mfma_f32_16x16x32_bf16 v[50:53], v[50:53], v[38:41], 0
	s_cselect_b64 vcc, -1, 0
	s_waitcnt lgkmcnt(1)
	v_mfma_f32_16x16x32_bf16 v[58:61], v[74:77], v[2:5], v[58:61]
	v_mfma_f32_16x16x32_bf16 v[66:69], v[74:77], v[14:17], v[66:69]
	v_mfma_f32_16x16x32_bf16 v[70:73], v[74:77], v[26:29], v[70:73]
	v_mfma_f32_16x16x32_bf16 v[50:53], v[74:77], v[42:45], v[50:53]
	ds_read_b128 v[74:77], v213 offset:8192
	ds_read_b128 v[82:85], v213 offset:8448
	s_waitcnt lgkmcnt(0)
	s_barrier
	s_mov_b32 s4, m0
	s_mov_b32 m0, s31
	s_nop 0
	global_load_lds_dwordx4 v[192:193], off
	s_mov_b32 m0, s4
	s_waitcnt lgkmcnt(1)
	v_mfma_f32_16x16x32_bf16 v[86:89], v[74:77], v[10:13], v[58:61]
	s_mov_b64 s[4:5], 0x3000
	v_lshl_add_u64 v[204:205], v[64:65], 0, s[4:5]
	s_mov_b32 s4, m0
	s_mov_b32 m0, s42
	s_nop 0
	global_load_lds_dwordx4 v[204:205], off
	s_mov_b32 m0, s4
	v_mfma_f32_16x16x32_bf16 v[90:93], v[74:77], v[22:25], v[66:69]
	s_add_i32 s4, s41, 0x2000
	v_mfma_f32_16x16x32_bf16 v[94:97], v[74:77], v[34:37], v[70:73]
	v_mfma_f32_16x16x32_bf16 v[74:77], v[74:77], v[46:49], v[50:53]
	v_mfma_f32_16x16x32_bf16 v[50:53], v[54:57], v[6:9], 0
	v_mfma_f32_16x16x32_bf16 v[58:61], v[54:57], v[18:21], 0
	v_mfma_f32_16x16x32_bf16 v[66:69], v[54:57], v[30:33], 0
	v_mfma_f32_16x16x32_bf16 v[54:57], v[54:57], v[38:41], 0
	v_mfma_f32_16x16x32_bf16 v[50:53], v[78:81], v[2:5], v[50:53]
	v_mfma_f32_16x16x32_bf16 v[58:61], v[78:81], v[14:17], v[58:61]
	v_mfma_f32_16x16x32_bf16 v[66:69], v[78:81], v[26:29], v[66:69]
	v_mfma_f32_16x16x32_bf16 v[54:57], v[78:81], v[42:45], v[54:57]
	s_waitcnt lgkmcnt(0)
	v_mfma_f32_16x16x32_bf16 v[78:81], v[82:85], v[10:13], v[50:53]
	v_mfma_f32_16x16x32_bf16 v[98:101], v[82:85], v[22:25], v[58:61]
	s_nop 1
	v_lshl_add_u64 v[50:51], v[186:187], 0, s[66:67]
	s_mov_b32 s5, m0
	s_mov_b32 m0, s4
	s_nop 0
	global_load_lds_dwordx4 v[50:51], off
	s_mov_b32 m0, s5
	v_mfma_f32_16x16x32_bf16 v[102:105], v[82:85], v[34:37], v[66:69]
	v_mfma_f32_16x16x32_bf16 v[82:85], v[82:85], v[46:49], v[54:57]
	ds_read_b128 v[50:53], v208 offset:12288
	s_nop 1
	ds_read_b128 v[54:57], v208 offset:12800
	ds_read_b128 v[58:61], v212 offset:12288
	ds_read_b128 v[62:65], v212 offset:12800
	ds_read_b128 v[66:69], v213 offset:20480
	ds_read_b128 v[70:73], v213 offset:20736
	v_exp_f32_e32 v86, v86
	v_exp_f32_e32 v87, v87
	v_exp_f32_e32 v88, v88
	v_exp_f32_e32 v89, v89
	v_exp_f32_e32 v90, v90
	v_exp_f32_e32 v91, v91
	v_exp_f32_e32 v92, v92
	v_exp_f32_e32 v93, v93
	v_exp_f32_e32 v94, v94
	v_exp_f32_e32 v95, v95
	v_exp_f32_e32 v96, v96
	v_exp_f32_e32 v97, v97
	v_exp_f32_e32 v107, v74
	v_exp_f32_e32 v108, v75
	v_exp_f32_e32 v109, v76
	v_exp_f32_e32 v110, v77
	v_add_f32_e32 v74, v86, v87
	v_add_f32_e32 v75, v88, v89
	v_exp_f32_e32 v78, v78
	v_exp_f32_e32 v98, v98
	v_exp_f32_e32 v102, v102
	v_exp_f32_e32 v82, v82
	v_add_f32_e32 v74, v74, v75
	v_add_f32_e32 v75, v90, v91
	v_add_f32_e32 v76, v92, v93
	v_add_f32_e32 v75, v75, v76
	v_add_f32_e32 v76, v94, v95
	v_add_f32_e32 v77, v96, v97
	v_exp_f32_e32 v79, v79
	v_exp_f32_e32 v99, v99
	v_exp_f32_e32 v103, v103
	v_exp_f32_e32 v83, v83
	v_add_f32_e32 v76, v76, v77
	v_add_f32_e32 v77, v107, v108
	v_add_f32_e32 v111, v109, v110
	v_add_f32_e32 v77, v77, v111
	v_exp_f32_e32 v80, v80
	v_exp_f32_e32 v100, v100
	v_exp_f32_e32 v104, v104
	v_exp_f32_e32 v84, v84
	v_add_f32_e32 v74, v74, v78
	v_add_f32_e32 v75, v75, v98
	v_add_f32_e32 v76, v76, v102
	v_add_f32_e32 v77, v77, v82
	v_exp_f32_e32 v81, v81
	v_exp_f32_e32 v101, v101
	v_exp_f32_e32 v105, v105
	v_exp_f32_e32 v85, v85
	v_add_f32_e32 v74, v79, v74
	v_add_f32_e32 v75, v99, v75
	v_add_f32_e32 v76, v103, v76
	v_add_f32_e32 v77, v83, v77
	s_mov_b32 s4, 1
	v_add_f32_e32 v74, v80, v74
	v_add_f32_e32 v111, v100, v75
	v_add_f32_e32 v76, v104, v76
	v_add_f32_e32 v112, v84, v77
	v_cvt_pk_bf16_f32 v134, v86, v87
	v_add_f32_e32 v75, v81, v74
	v_add_f32_e32 v74, v101, v111
	v_add_f32_e32 v77, v105, v76
	v_add_f32_e32 v76, v85, v112
	s_waitcnt vmcnt(3) lgkmcnt(0)
	s_barrier
	s_cmp_lg_u32 s4, 0
	v_pk_add_f32 v[190:191], v[74:75], 0 op_sel_hi:[1,0]
	v_cndmask_b32_e32 v74, v209, v194, vcc
	v_bitop3_b32 v74, v74, v106, 7 bitop3:0x78
	v_lshlrev_b32_e32 v74, 4, v74
	v_add3_u32 v214, 0, v211, v74
	v_mov_b32_e32 v74, 0
	v_pk_add_f32 v[188:189], v[76:77], 0 op_sel_hi:[1,0]
	v_cvt_pk_bf16_f32 v135, v88, v89
	v_cvt_pk_bf16_f32 v136, v78, v79
	v_cvt_pk_bf16_f32 v137, v80, v81
	v_cvt_pk_bf16_f32 v142, v90, v91
	v_cvt_pk_bf16_f32 v143, v92, v93
	v_cvt_pk_bf16_f32 v144, v98, v99
	v_cvt_pk_bf16_f32 v145, v100, v101
	v_cvt_pk_bf16_f32 v146, v94, v95
	v_cvt_pk_bf16_f32 v147, v96, v97
	v_cvt_pk_bf16_f32 v148, v102, v103
	v_cvt_pk_bf16_f32 v149, v104, v105
	v_cvt_pk_bf16_f32 v150, v107, v108
	v_cvt_pk_bf16_f32 v151, v109, v110
	v_cvt_pk_bf16_f32 v152, v82, v83
	v_cvt_pk_bf16_f32 v153, v84, v85
	s_cselect_b64 s[4:5], -1, 0
	s_mov_b32 s27, 2
	v_mov_b32_e32 v75, v74
	v_mov_b32_e32 v76, v74
	v_mov_b32_e32 v77, v74
	v_mov_b32_e32 v78, v74
	v_mov_b32_e32 v79, v74
	v_mov_b32_e32 v80, v74
	v_mov_b32_e32 v81, v74
	v_mov_b32_e32 v82, v74
	v_mov_b32_e32 v83, v74
	v_mov_b32_e32 v84, v74
	v_mov_b32_e32 v85, v74
	v_mov_b32_e32 v86, v74
	v_mov_b32_e32 v87, v74
	v_mov_b32_e32 v88, v74
	v_mov_b32_e32 v89, v74
	v_mov_b32_e32 v90, v74
	v_mov_b32_e32 v91, v74
	v_mov_b32_e32 v92, v74
	v_mov_b32_e32 v93, v74
	v_mov_b32_e32 v94, v74
	v_mov_b32_e32 v95, v74
	v_mov_b32_e32 v96, v74
	v_mov_b32_e32 v97, v74
	v_mov_b32_e32 v98, v74
	v_mov_b32_e32 v99, v74
	v_mov_b32_e32 v100, v74
	v_mov_b32_e32 v101, v74
	v_mov_b32_e32 v102, v74
	v_mov_b32_e32 v103, v74
	v_mov_b32_e32 v104, v74
	v_mov_b32_e32 v105, v74
	v_mov_b32_e32 v106, v74
	v_mov_b32_e32 v107, v74
	v_mov_b32_e32 v108, v74
	v_mov_b32_e32 v109, v74
	v_mov_b32_e32 v110, v74
	v_mov_b32_e32 v111, v74
	v_mov_b32_e32 v112, v74
	v_mov_b32_e32 v113, v74
	v_mov_b32_e32 v114, v74
	v_mov_b32_e32 v115, v74
	v_mov_b32_e32 v116, v74
	v_mov_b32_e32 v117, v74
	v_mov_b32_e32 v118, v74
	v_mov_b32_e32 v119, v74
	v_mov_b32_e32 v120, v74
	v_mov_b32_e32 v121, v74
	v_mov_b32_e32 v122, v74
	v_mov_b32_e32 v123, v74
	v_mov_b32_e32 v124, v74
	v_mov_b32_e32 v125, v74
	v_mov_b32_e32 v126, v74
	v_mov_b32_e32 v127, v74
	v_mov_b32_e32 v128, v74
	v_mov_b32_e32 v129, v74
	v_mov_b32_e32 v130, v74
	v_mov_b32_e32 v131, v74
	v_mov_b32_e32 v132, v74
	v_mov_b32_e32 v133, v74
	v_mov_b32_e32 v138, v74
	v_mov_b32_e32 v139, v74
	v_mov_b32_e32 v140, v74
	v_mov_b32_e32 v141, v74
	s_branch .LBB0_669

; #define LAS __attribute__((address_space(3)))
; template <int DQK, int DV, bool LEAD> ...
;     ...
;     const int tid = tid_, lane = tid & 63, q16 = lane & 15, g4 = lane >> 4, hi = lane >> 5; const int wid = __builtin_amdgcn_readfirstlane(tid >> 6);
;     const int kg = KS ? (wid >> 2) : 0, qoff = KS ? (wid & 3) * 64 : wid * 32;
;     const unsigned lds0 = (unsigned)(uintptr_t)shm;
;     const int krow_l = wid * 8 + (lane >> 3);
;     const int kc_l = (lane & 7) ^ (((krow_l >> 1) & 1) | (((krow_l >> 3) & 1) << 1) | (((krow_l >> 4) & 1) << 2));
;     const int vc_l = (lane & 7) ^ ((krow_l >> 1) & 7);
;     const bf16_t* ksrc = K + (size_t)(krow0 + krow_l) * kpitch + kc_l * 8;
;     const int rrow_l = (wid & 3) * 16 + (lane >> 2), rc_l = (lane & 3) ^ (((rrow_l >> 4) & 1) << 1);
;     const bf16_t* krsrc = (DQK == 96) ? KR + (size_t)(krow0 + rrow_l) * 32 + rc_l * 8 : nullptr;
;     const bf16_t* vsrc = Vt + (size_t)krow_l * NR + krow0 + vc_l * 8;
;     const unsigned kdst = lds0 + KOFF + wid * 1024, krdst = lds0 + KOFF + 8192 + (wid & 3) * 1024, vdst = lds0 + VOFF + wid * 1024;
;     ...
;     const int kr0 = 8 * (q16 >> 2) + (q16 & 3);
;     const int fk = ((kr0 >> 1) & 1) | (((kr0 >> 3) & 1) << 1) | (((kr0 >> 4) & 1) << 2);
;     const LAS unsigned char* kp[2]; const LAS unsigned char* vp[2];
; #pragma unroll
;     for (int ds = 0; ds < 2; ++ds) kp[ds] = shm + KOFF + kr0 * 128 + ((((ds << 2) | g4) ^ fk) << 4) + kg * 4096;
;     const LAS unsigned char* krp = shm + KOFF + 8192 + kr0 * 64 + ((g4 ^ (((kr0 >> 4) & 1) << 1)) << 4) + kg * 2048;
; #pragma unroll
;     for (int s_ = 0; s_ < 2; ++s_) vp[s_] = shm + VOFF + q16 * 128 + ((((s_ << 2) | g4) ^ ((q16 >> 1) & 7)) << 4);
;     const LAS unsigned char* vpk = kg ? vp[1] : vp[0];
;     ...
;     ATT_DMA_K(0, 0); ATT_DMA_V(0, 0); ATT_DMA_K(1, 1); ATT_DMA_K(2, 2);
;     bf16x8 qf[NQB * NDS];
;     {
; __global__ void __launch_bounds__(NWAVES * 64, 2) mega_fwd(Args args_) {
;     ...
;             for (int i = 0;; ++i) { const int u = i * F.G + F.vcu; if (u >= 2048) break; const int sid = u >> 5, qb = u & 31, b = sid >> 3, hc = sid & 7, h = hc >> 1, c = hc & 1;
;                 att::attn_unit<64, 128>(QK + h * 128 + c * 64, QKW, QK + 512 + h * 128 + c * 64, QKW, nullptr, VTE + (size_t)(h * 128) * NR, OB + hc * 128, 1024, b * TPS + qb * 256, b * TPS, 132, F.lds, IN(a, I_AQK) + j * 128, (const f32x2*)(ws + WS_ROPE64), qb * 256); }
.LBB0_939:
	s_lshl_b32 s6, s4, 1
	s_and_b32 s6, s6, 0x180
	s_lshr_b32 s5, s4, 8
	s_lshl_b32 s7, s6, 1
	s_add_u32 s16, s18, s7
	s_addc_u32 s22, s19, 0
	s_lshl_b32 s23, s4, 2
	s_and_b32 s23, s23, 0x80
	s_add_u32 s36, s16, s23
	s_addc_u32 s37, s22, 0
	s_add_u32 s7, s15, s7
	s_addc_u32 s16, s17, 0
	s_add_u32 s40, s7, s23
	s_addc_u32 s41, s16, 0
	s_mul_i32 s6, s6, 0x21000
	s_add_u32 s44, s10, s6
	s_addc_u32 s45, s11, 0
	s_lshl_b32 s6, s4, 3
	s_and_b32 s6, s6, 0x700
	s_add_u32 s26, s3, s6
	s_mov_b64 s[6:7], s[0:1]
	s_load_dwordx2 s[6:7], s[6:7], 0x48
	s_addc_u32 s27, s14, 0
	s_lshl_b32 s25, s4, 8
	s_mul_i32 s46, s5, 0x2100
	s_and_b32 s4, s25, 0x1f00
	s_add_i32 s30, s46, s4
	s_lshl_b64 s[22:23], s[20:21], 2
	s_waitcnt lgkmcnt(0)
	s_add_u32 s28, s6, s22
	s_addc_u32 s29, s7, s23
	v_readfirstlane_b32 s4, v0
	s_cmpk_gt_u32 s4, 0xff
	s_mov_b64 s[4:5], -1
	s_cbranch_scc0 .LBB0_946
	v_mov_b32_e32 v79, v0
	s_ashr_i32 s47, s46, 31
	v_readfirstlane_b32 s4, v79
	s_ashr_i32 s42, s4, 6
	v_bfe_u32 v1, v79, 3, 3
	v_lshl_or_b32 v6, s42, 3, v1
	s_lshl_b32 s5, s42, 1
	s_lshr_b32 s4, s4, 5
	v_ashrrev_i32_e32 v2, 1, v6
	s_and_b32 s5, s5, 2
	s_and_b32 s4, s4, 4
	v_and_b32_e32 v203, 7, v79
	v_and_b32_e32 v3, 1, v2
	s_or_b32 s4, s5, s4
	v_bitop3_b32 v7, s4, v203, v3 bitop3:0x36
	v_xor_b32_e32 v8, v2, v79
	v_add_u32_e32 v4, s46, v6
	v_mov_b64_e32 v[2:3], s[40:41]
	v_mad_i64_i32 v[2:3], s[4:5], v4, s92, v[2:3]
	v_mov_b64_e32 v[4:5], s[44:45]
	v_lshlrev_b32_e32 v194, 4, v7
	s_lshl_b32 s43, s42, 10
	v_mad_i64_i32 v[4:5], s[4:5], v6, s91, v[4:5]
	v_lshl_add_u64 v[204:205], v[2:3], 0, v[194:195]
	v_lshlrev_b32_e32 v2, 4, v8
	s_add_i32 s43, s43, 0
	v_lshl_add_u64 v[4:5], s[46:47], 1, v[4:5]
	v_and_b32_e32 v194, 0x70, v2
	s_mov_b32 s4, m0
	s_mov_b32 m0, s43
	s_nop 0
	global_load_lds_dwordx4 v[204:205], off
	s_mov_b32 m0, s4
	v_lshl_add_u64 v[206:207], v[4:5], 0, v[194:195]
	s_add_i32 s16, s43, 0x9000
	s_mov_b32 s4, m0
	s_mov_b32 m0, s16
	s_nop 0
	global_load_lds_dwordx4 v[206:207], off
	s_mov_b32 m0, s4
	s_mov_b64 s[4:5], 0x840000
	v_lshl_add_u64 v[208:209], v[206:207], 0, s[4:5]
	s_add_i32 s4, s16, 0x2000
	s_mov_b32 s5, m0
	s_mov_b32 m0, s4
	s_nop 0
	global_load_lds_dwordx4 v[208:209], off
	s_mov_b32 m0, s5
	s_mov_b64 s[4:5], 0x38000
	v_lshl_add_u64 v[2:3], v[204:205], 0, s[4:5]
	s_add_i32 s4, s43, 0x2000
	s_mov_b32 s5, m0
	s_mov_b32 m0, s4
	s_nop 0
	global_load_lds_dwordx4 v[2:3], off
	s_mov_b32 m0, s5
	s_lshl_b32 s6, s42, 5
	s_mov_b64 s[4:5], 0x70000
	v_and_b32_e32 v78, 15, v79
	v_lshl_add_u64 v[2:3], v[204:205], 0, s[4:5]
	s_add_i32 s31, s6, s30
	v_and_b32_e32 v194, 48, v79
	s_add_i32 s4, s43, 0x4000
	s_mov_b32 s5, m0
	s_mov_b32 m0, s4
	s_nop 0
	global_load_lds_dwordx4 v[2:3], off
	s_mov_b32 m0, s5
	v_or_b32_e32 v4, s31, v78
	v_lshl_add_u64 v[2:3], s[36:37], 0, v[194:195]
	v_lshrrev_b32_e32 v38, 1, v79
	v_or_b32_e32 v5, s6, v78
	v_mad_i64_i32 v[26:27], s[4:5], v4, s92, v[2:3]
	v_and_b32_e32 v28, 8, v38
	v_lshlrev_b32_e32 v5, 4, v5
	s_movk_i32 s4, 0x2f0
	v_or_b32_e32 v4, 16, v4
	v_and_or_b32 v5, v5, s4, v28
	v_mad_i64_i32 v[30:31], s[4:5], v4, s92, v[2:3]
	s_add_i32 s6, s6, s25
	s_lshr_b32 s4, s6, 2
	v_lshlrev_b32_e32 v22, 3, v5
	s_and_b32 s4, s4, 0x7f0
	global_load_dwordx4 v[50:53], v[26:27], off offset:64 nt
	global_load_dwordx4 v[60:63], v22, s[8:9] offset:48
	global_load_dwordx4 v[70:73], v[30:31], off offset:64 nt
	global_load_dwordx4 v[6:9], v22, s[8:9] offset:2096
	global_load_dwordx4 v[54:57], v22, s[8:9] offset:32
	global_load_dwordx4 v[14:17], v22, s[8:9] offset:2080
	global_load_dwordx4 v[2:5], v22, s[8:9] offset:16
	global_load_dwordx4 v[18:21], v22, s[8:9] offset:2064
	global_load_dwordx4 v[10:13], v22, s[8:9]
	s_nop 0
	global_load_dwordx4 v[22:25], v22, s[8:9] offset:2048
	s_nop 0
	global_load_dwordx4 v[82:85], v[26:27], off nt
	v_or_b32_e32 v26, s4, v28
	v_lshlrev_b32_e32 v39, 3, v26
	global_load_dwordx4 v[26:29], v39, s[8:9] offset:48
	global_load_dwordx4 v[86:89], v[30:31], off nt
	s_nop 0
	global_load_dwordx4 v[30:33], v39, s[8:9] offset:32
	global_load_dwordx4 v[34:37], v39, s[8:9] offset:16
	v_bfe_u32 v214, v79, 4, 2
	v_lshlrev_b32_e32 v215, 1, v79
	v_and_b32_e32 v40, 3, v79
	v_and_or_b32 v40, v215, 24, v40
	v_bitop3_b32 v38, v214, v38, 7 bitop3:0x78
	v_lshlrev_b32_e32 v59, 5, v214
	v_lshl_add_u32 v81, v40, 7, 0
	v_lshlrev_b32_e32 v80, 4, v38
	global_load_dwordx4 v[38:41], v39, s[8:9]
	s_nop 0
	global_load_dwordx4 v[42:45], v59, s[28:29] offset:144
	global_load_dwordx4 v[46:49], v59, s[28:29] offset:128
	v_and_b32_e32 v58, 63, v79
	v_cmp_gt_u32_e32 vcc, 32, v58
	s_mov_b32 s4, 0x3c800000
	v_add_u32_e32 v194, v81, v80
	v_lshlrev_b32_e32 v217, 7, v78
	s_mov_b32 s47, 1
	s_mov_b32 s48, 2
	v_or_b32_e32 v216, 4, v214
	s_waitcnt vmcnt(15)
	v_and_b32_e32 v65, 0xffff0000, v73
	v_lshlrev_b32_e32 v64, 16, v73
	v_and_b32_e32 v67, 0xffff0000, v72
	v_lshlrev_b32_e32 v66, 16, v72
	s_waitcnt vmcnt(13)
	v_cndmask_b32_e64 v95, v57, -v57, vcc
	v_cndmask_b32_e64 v94, v55, -v55, vcc
	v_and_b32_e32 v91, 0xffff0000, v53
	v_lshlrev_b32_e32 v90, 16, v53
	v_and_b32_e32 v93, 0xffff0000, v52
	s_waitcnt vmcnt(5)
; template <int DQK, int DV, bool LEAD> ...
;     ...
;           float sn = 0.f;
; #pragma unroll
;           for (int ds = 0; ds < 2; ++ds)
; #pragma unroll
;               for (int j = 0; j < 8; ++j) sn += x[ds][j] * x[ds][j];
;           sn = lanes4_sum(sn);
;           const float rn = rsqrtf(sn * (1.f / 64.f) + EPS);
; #pragma unroll
;           for (int ds = 0; ds < 2; ++ds)
; #pragma unroll
;               for (int j = 0; j < 8; ++j) x[ds][j] *= rn * qgain[32 * ds + 8 * g4 + j];
;           if constexpr (DQK == 64) {
; #pragma unroll
;               for (int ds = 0; ds < 2; ++ds)
; #pragma unroll
;                   for (int j = 0; j < 8; ++j) {
;                       auto rr = __builtin_amdgcn_permlane32_swap(__float_as_uint(x[ds][j]), __float_as_uint(x[ds][j]), false, false);
;                       const float other = hi ? __uint_as_float(rr[0]) : __uint_as_float(rr[1]);
;                       float cc = 1.f, sg = 0.f;
;                       if (lat) { const f32x2 cs = rope[(ds ? pcol : prow) * 16 + 8 * (g4 & 1) + j]; cc = cs.x; sg = hi ? cs.y : -cs.y; }
;                       x[ds][j] = x[ds][j] * cc + other * sg; }
	v_and_b32_e32 v73, 0xffff0000, v89
	v_lshlrev_b32_e32 v72, 16, v89
	v_and_b32_e32 v75, 0xffff0000, v88
	v_lshlrev_b32_e32 v74, 16, v88
	v_and_b32_e32 v89, 0xffff0000, v83
	v_lshlrev_b32_e32 v88, 16, v83
	v_and_b32_e32 v83, 0xffff0000, v82
	v_lshlrev_b32_e32 v92, 16, v52
	v_mov_b32_e32 v55, v56
	v_and_b32_e32 v97, 0xffff0000, v51
	v_lshlrev_b32_e32 v96, 16, v51
	v_cndmask_b32_e64 v98, v3, -v3, vcc
	v_mov_b32_e32 v3, v4
	v_and_b32_e32 v101, 0xffff0000, v50
	v_lshlrev_b32_e32 v100, 16, v50
	global_load_dwordx4 v[50:53], v59, s[28:29] offset:16
	s_nop 0
	global_load_dwordx4 v[56:59], v59, s[28:29]
	v_lshlrev_b32_e32 v82, 16, v82
	v_mul_f32_e32 v4, v83, v83
	v_cndmask_b32_e64 v99, v5, -v5, vcc
	v_pk_fma_f32 v[4:5], v[82:83], v[82:83], v[4:5] op_sel_hi:[1,1,0]
	v_mul_f32_e32 v104, v89, v89
	v_pk_fma_f32 v[4:5], v[88:89], v[88:89], v[4:5]
	v_cndmask_b32_e64 v103, v13, -v13, vcc
	v_cndmask_b32_e64 v102, v11, -v11, vcc
	v_mov_b32_e32 v11, v12
	v_and_b32_e32 v13, 0xffff0000, v85
	v_lshlrev_b32_e32 v12, 16, v85
	v_and_b32_e32 v85, 0xffff0000, v84
	v_lshlrev_b32_e32 v84, 16, v84
	v_pk_add_f32 v[4:5], v[104:105], v[4:5] op_sel_hi:[0,1]
	v_pk_fma_f32 v[4:5], v[84:85], v[84:85], v[4:5]
	v_mul_f32_e32 v104, v85, v85
	v_pk_add_f32 v[4:5], v[104:105], v[4:5] op_sel_hi:[0,1]
	v_pk_fma_f32 v[4:5], v[12:13], v[12:13], v[4:5]
	v_mul_f32_e32 v104, v13, v13
	v_pk_add_f32 v[4:5], v[104:105], v[4:5] op_sel_hi:[0,1]
	v_pk_fma_f32 v[4:5], v[100:101], v[100:101], v[4:5]
	v_mul_f32_e32 v104, v101, v101
	v_pk_add_f32 v[4:5], v[104:105], v[4:5] op_sel_hi:[0,1]
	v_pk_fma_f32 v[4:5], v[96:97], v[96:97], v[4:5]
	v_mul_f32_e32 v104, v97, v97
	v_pk_add_f32 v[4:5], v[104:105], v[4:5] op_sel_hi:[0,1]
	v_pk_fma_f32 v[4:5], v[92:93], v[92:93], v[4:5]
	v_mul_f32_e32 v104, v93, v93
	v_pk_add_f32 v[4:5], v[104:105], v[4:5] op_sel_hi:[0,1]
	v_pk_fma_f32 v[4:5], v[90:91], v[90:91], v[4:5]
	v_mul_f32_e32 v104, v91, v91
	v_pk_add_f32 v[4:5], v[104:105], v[4:5] op_sel_hi:[0,1]
	v_mov_b32_e32 v5, v4
	s_nop 1
	v_permlane16_swap_b32_e32 v4, v5
	v_add_f32_e32 v5, v4, v5
	v_cndmask_b32_e64 v77, v63, -v63, vcc
	v_cndmask_b32_e64 v76, v61, -v61, vcc
	v_mov_b32_e32 v61, v62
	v_cndmask_b32_e64 v63, v9, -v9, vcc
	v_cndmask_b32_e64 v62, v7, -v7, vcc
	v_mov_b32_e32 v7, v8
	v_cndmask_b32_e64 v9, v17, -v17, vcc
	v_cndmask_b32_e64 v8, v15, -v15, vcc
	v_mov_b32_e32 v15, v16
	v_cndmask_b32_e64 v17, v21, -v21, vcc
	v_cndmask_b32_e64 v16, v19, -v19, vcc
	v_mov_b32_e32 v19, v20
	v_cndmask_b32_e64 v21, v25, -v25, vcc
	v_cndmask_b32_e64 v20, v23, -v23, vcc
	v_mov_b32_e32 v23, v24
	v_cndmask_b32_e64 v25, v29, -v29, vcc
	v_cndmask_b32_e64 v24, v27, -v27, vcc
	v_mov_b32_e32 v27, v28
	s_waitcnt vmcnt(6)
	v_cndmask_b32_e64 v29, v33, -v33, vcc
	v_cndmask_b32_e64 v28, v31, -v31, vcc
	v_mov_b32_e32 v31, v32
	s_waitcnt vmcnt(5)
	v_cndmask_b32_e64 v33, v37, -v37, vcc
	v_cndmask_b32_e64 v32, v35, -v35, vcc
	v_mov_b32_e32 v35, v36
	v_and_b32_e32 v37, 0xffff0000, v87
	v_lshlrev_b32_e32 v36, 16, v87
	v_mov_b32_e32 v87, v5
	v_and_b32_e32 v105, 0xffff0000, v86
	s_nop 0
	v_permlane32_swap_b32_e32 v5, v87
	v_lshlrev_b32_e32 v104, 16, v86
	v_mul_f32_e32 v4, v105, v105
	v_pk_fma_f32 v[106:107], v[104:105], v[104:105], v[4:5] op_sel_hi:[1,1,0]
	v_mul_f32_e32 v4, v37, v37
	v_pk_fma_f32 v[106:107], v[36:37], v[36:37], v[106:107]
	v_and_b32_e32 v69, 0xffff0000, v71
	v_pk_add_f32 v[106:107], v[4:5], v[106:107] op_sel_hi:[0,1]
	v_pk_fma_f32 v[106:107], v[74:75], v[74:75], v[106:107]
	v_mul_f32_e32 v4, v75, v75
	v_pk_add_f32 v[106:107], v[4:5], v[106:107] op_sel_hi:[0,1]
	v_pk_fma_f32 v[106:107], v[72:73], v[72:73], v[106:107]
	v_mul_f32_e32 v4, v73, v73
	v_lshlrev_b32_e32 v68, 16, v71
	v_and_b32_e32 v71, 0xffff0000, v70
	v_lshlrev_b32_e32 v70, 16, v70
	v_pk_add_f32 v[106:107], v[4:5], v[106:107] op_sel_hi:[0,1]
	v_pk_fma_f32 v[106:107], v[70:71], v[70:71], v[106:107]
	v_mul_f32_e32 v4, v71, v71
	v_pk_add_f32 v[106:107], v[4:5], v[106:107] op_sel_hi:[0,1]
	v_pk_fma_f32 v[106:107], v[68:69], v[68:69], v[106:107]
	v_mul_f32_e32 v4, v69, v69
	v_pk_add_f32 v[106:107], v[4:5], v[106:107] op_sel_hi:[0,1]
	v_pk_fma_f32 v[106:107], v[66:67], v[66:67], v[106:107]
	v_mul_f32_e32 v4, v67, v67
	v_pk_add_f32 v[106:107], v[4:5], v[106:107] op_sel_hi:[0,1]
	v_pk_fma_f32 v[106:107], v[64:65], v[64:65], v[106:107]
	v_mul_f32_e32 v4, v65, v65
	v_pk_add_f32 v[106:107], v[4:5], v[106:107] op_sel_hi:[0,1]
	v_mov_b32_e32 v4, v106
	s_nop 1
	v_permlane16_swap_b32_e32 v106, v4
	v_add_f32_e32 v4, v106, v4
	v_mov_b32_e32 v86, v4
	s_nop 1
	v_permlane32_swap_b32_e32 v4, v86
	v_pk_add_f32 v[4:5], v[4:5], v[86:87]
	s_waitcnt vmcnt(4)
	v_cndmask_b32_e64 v106, v39, -v39, vcc
	v_pk_fma_f32 v[86:87], v[4:5], s[4:5], v[196:197] op_sel_hi:[1,0,0]
	v_mov_b32_e32 v39, v40
	v_mul_f32_e32 v4, 0x4b800000, v87
	v_cmp_gt_f32_e64 s[4:5], s95, v87
	v_cndmask_b32_e64 v107, v41, -v41, vcc
	s_nop 0
	v_cndmask_b32_e64 v4, v87, v4, s[4:5]
	v_rsq_f32_e32 v4, v4
	s_nop 0
	v_mul_f32_e32 v5, 0x45800000, v4
	v_cndmask_b32_e64 v40, v4, v5, s[4:5]
	s_waitcnt vmcnt(3)
	v_pk_mul_f32 v[4:5], v[40:41], v[44:45] op_sel_hi:[0,1]
	v_pk_mul_f32 v[4:5], v[4:5], v[90:91]
	v_cmp_gt_f32_e64 s[4:5], s95, v86
	v_mov_b32_e32 v41, v4
	v_mov_b32_e32 v87, v4
	v_mov_b32_e32 v90, v5
	v_mov_b32_e32 v91, v5
	v_permlane32_swap_b32_e32 v41, v87
	s_nop 0
	v_permlane32_swap_b32_e32 v90, v91
	v_cndmask_b32_e32 v91, v90, v91, vcc
	v_cndmask_b32_e32 v90, v41, v87, vcc
	v_pk_mul_f32 v[76:77], v[76:77], v[90:91]
	s_nop 0
	v_pk_fma_f32 v[4:5], v[4:5], v[60:61], v[76:77]
	v_pk_mul_f32 v[60:61], v[40:41], v[42:43] op_sel_hi:[0,1]
	v_pk_mul_f32 v[4:5], v[4:5], s[94:95] op_sel_hi:[1,0]
	v_pk_mul_f32 v[60:61], v[60:61], v[92:93]
	v_cvt_pk_bf16_f32 v5, v4, v5
	v_mov_b32_e32 v4, v60
	v_mov_b32_e32 v41, v60
	v_mov_b32_e32 v76, v61
	v_mov_b32_e32 v77, v61
	v_permlane32_swap_b32_e32 v4, v41
	s_nop 0
	v_permlane32_swap_b32_e32 v76, v77
	v_cndmask_b32_e32 v77, v76, v77, vcc
	v_cndmask_b32_e32 v76, v4, v41, vcc
	v_pk_mul_f32 v[76:77], v[94:95], v[76:77]
	s_nop 0
	v_pk_fma_f32 v[54:55], v[60:61], v[54:55], v[76:77]
	s_nop 0
	v_pk_mul_f32 v[54:55], v[54:55], s[94:95] op_sel_hi:[1,0]
	s_nop 0
	v_cvt_pk_bf16_f32 v4, v54, v55
	s_waitcnt vmcnt(2)
; __device__ __forceinline__ unsigned cvtpk(float lo, float hi) { f32x2 v = {lo, hi}; bf16x2_t b = __builtin_convertvector(v, bf16x2_t); return __builtin_bit_cast(unsigned, b); }
; template <int DQK, int DV, bool LEAD> ...
;     ...
;               for (int j = 0; j < 8; ++j) x[ds][j] *= rn * qgain[32 * ds + 8 * g4 + j];
;           if constexpr (DQK == 64) {
; #pragma unroll
;               for (int ds = 0; ds < 2; ++ds)
; #pragma unroll
;                   for (int j = 0; j < 8; ++j) {
;                       auto rr = __builtin_amdgcn_permlane32_swap(__float_as_uint(x[ds][j]), __float_as_uint(x[ds][j]), false, false);
;                       const float other = hi ? __uint_as_float(rr[0]) : __uint_as_float(rr[1]);
;                       float cc = 1.f, sg = 0.f;
;                       if (lat) { const f32x2 cs = rope[(ds ? pcol : prow) * 16 + 8 * (g4 & 1) + j]; cc = cs.x; sg = hi ? cs.y : -cs.y; }
;                       x[ds][j] = x[ds][j] * cc + other * sg; }
;           } else {
;               float sr = 0.f;
; #pragma unroll
;               for (int j = 0; j < 8; ++j) sr += x[2][j] * x[2][j];
;               sr = lanes4_sum(sr);
;               const float rq = rsqrtf(sr * (1.f / 32.f) + EPS);
; #pragma unroll
;               for (int j = 0; j < 8; ++j) { const float av = x[2][j] * rq * qgain[64 + 8 * g4 + j];
;                   auto rr = __builtin_amdgcn_permlane16_swap(__float_as_uint(av), __float_as_uint(av), false, false);
;                   const float other = (g4 & 1) ? __uint_as_float(rr[0]) : __uint_as_float(rr[1]);
;                   float cc = 1.f, sg = 0.f;
;                   if (lat) { const f32x2 cs = rope[((g4 & 2) ? pcol : prow) * 8 + j]; cc = cs.x; sg = (g4 & 1) ? cs.y : -cs.y; }
;                   x[2][j] = av * cc + other * sg; }
;           }
; #pragma unroll
;           for (int ds = 0; ds < NDS; ++ds) { u32x4 w;
; #pragma unroll
;               for (int i = 0; i < 4; ++i) w[i] = cvtpk(x[ds][2 * i] * c2, x[ds][2 * i + 1] * c2);
;               qf[qb * NDS + ds] = __builtin_bit_cast(bf16x8, w); }
	v_pk_mul_f32 v[54:55], v[40:41], v[48:49] op_sel_hi:[0,1]
	v_pk_mul_f32 v[54:55], v[54:55], v[96:97]
	s_nop 0
	v_mov_b32_e32 v41, v54
	v_mov_b32_e32 v60, v54
	v_mov_b32_e32 v61, v55
	v_mov_b32_e32 v76, v55
	v_permlane32_swap_b32_e32 v41, v60
	s_nop 0
	v_permlane32_swap_b32_e32 v61, v76
	v_cndmask_b32_e32 v61, v61, v76, vcc
	v_cndmask_b32_e32 v60, v41, v60, vcc
	v_pk_mul_f32 v[60:61], v[98:99], v[60:61]
	s_nop 0
	v_pk_fma_f32 v[2:3], v[54:55], v[2:3], v[60:61]
	v_pk_mul_f32 v[54:55], v[46:47], v[40:41] op_sel_hi:[1,0]
	v_pk_mul_f32 v[2:3], v[2:3], s[94:95] op_sel_hi:[1,0]
	v_pk_mul_f32 v[54:55], v[54:55], v[100:101]
	v_cvt_pk_bf16_f32 v3, v2, v3
	v_mov_b32_e32 v2, v54
	v_mov_b32_e32 v41, v54
	v_mov_b32_e32 v60, v55
	v_mov_b32_e32 v61, v55
	v_permlane32_swap_b32_e32 v2, v41
	s_nop 0
	v_permlane32_swap_b32_e32 v60, v61
	v_cndmask_b32_e32 v61, v60, v61, vcc
	v_cndmask_b32_e32 v60, v2, v41, vcc
	v_pk_mul_f32 v[60:61], v[102:103], v[60:61]
	s_nop 0
	v_pk_fma_f32 v[10:11], v[54:55], v[10:11], v[60:61]
	s_nop 0
	v_pk_mul_f32 v[10:11], v[10:11], s[94:95] op_sel_hi:[1,0]
	s_nop 0
	v_cvt_pk_bf16_f32 v2, v10, v11
	s_waitcnt vmcnt(1)
	v_pk_mul_f32 v[10:11], v[52:53], v[40:41] op_sel_hi:[1,0]
	s_nop 0
	v_pk_mul_f32 v[10:11], v[10:11], v[12:13]
	s_nop 0
	v_mov_b32_e32 v12, v10
	v_mov_b32_e32 v41, v10
	v_mov_b32_e32 v13, v11
	v_mov_b32_e32 v54, v11
	v_permlane32_swap_b32_e32 v12, v41
	s_nop 0
	v_permlane32_swap_b32_e32 v13, v54
	v_cndmask_b32_e32 v13, v13, v54, vcc
	v_cndmask_b32_e32 v12, v12, v41, vcc
	v_pk_mul_f32 v[12:13], v[24:25], v[12:13]
	s_nop 0
	v_pk_fma_f32 v[10:11], v[10:11], v[26:27], v[12:13]
	s_nop 0
	v_pk_mul_f32 v[10:11], v[10:11], s[94:95] op_sel_hi:[1,0]
	s_nop 0
	v_cvt_pk_bf16_f32 v13, v10, v11
	v_pk_mul_f32 v[10:11], v[50:51], v[40:41] op_sel_hi:[1,0]
	s_nop 0
	v_pk_mul_f32 v[10:11], v[10:11], v[84:85]
	s_nop 0
	v_mov_b32_e32 v12, v10
	v_mov_b32_e32 v41, v10
	v_mov_b32_e32 v54, v11
	v_mov_b32_e32 v55, v11
	v_permlane32_swap_b32_e32 v12, v41
	s_nop 0
	v_permlane32_swap_b32_e32 v54, v55
	v_cndmask_b32_e32 v55, v54, v55, vcc
	v_cndmask_b32_e32 v54, v12, v41, vcc
	v_pk_mul_f32 v[54:55], v[28:29], v[54:55]
	s_nop 0
	v_pk_fma_f32 v[10:11], v[10:11], v[30:31], v[54:55]
	s_nop 0
	v_pk_mul_f32 v[10:11], v[10:11], s[94:95] op_sel_hi:[1,0]
	s_nop 0
	v_cvt_pk_bf16_f32 v12, v10, v11
	s_waitcnt vmcnt(0)
	v_pk_mul_f32 v[10:11], v[58:59], v[40:41] op_sel_hi:[1,0]
	s_nop 0
	v_pk_mul_f32 v[10:11], v[10:11], v[88:89]
	s_nop 0
	v_mov_b32_e32 v41, v10
	v_mov_b32_e32 v54, v10
	v_mov_b32_e32 v55, v11
	v_mov_b32_e32 v60, v11
	v_permlane32_swap_b32_e32 v41, v54
	s_nop 0
	v_permlane32_swap_b32_e32 v55, v60
	v_cndmask_b32_e32 v55, v55, v60, vcc
	v_cndmask_b32_e32 v54, v41, v54, vcc
	v_pk_mul_f32 v[54:55], v[32:33], v[54:55]
	v_pk_mul_f32 v[40:41], v[56:57], v[40:41] op_sel_hi:[1,0]
	v_pk_fma_f32 v[10:11], v[10:11], v[34:35], v[54:55]
	v_pk_mul_f32 v[40:41], v[40:41], v[82:83]
	v_pk_mul_f32 v[10:11], v[10:11], s[94:95] op_sel_hi:[1,0]
	v_mov_b32_e32 v54, v40
	v_cvt_pk_bf16_f32 v11, v10, v11
	v_mov_b32_e32 v10, v40
	s_nop 1
	v_permlane32_swap_b32_e32 v10, v54
	v_mov_b32_e32 v55, v41
	v_mov_b32_e32 v60, v41
	v_cndmask_b32_e32 v54, v10, v54, vcc
	v_mul_f32_e32 v10, 0x4b800000, v86
	v_permlane32_swap_b32_e32 v55, v60
	v_cndmask_b32_e64 v10, v86, v10, s[4:5]
	v_cndmask_b32_e32 v55, v55, v60, vcc
	v_rsq_f32_e32 v60, v10
	v_pk_mul_f32 v[54:55], v[106:107], v[54:55]
	s_nop 0
	v_pk_fma_f32 v[40:41], v[40:41], v[38:39], v[54:55]
	s_nop 0
	v_pk_mul_f32 v[40:41], v[40:41], s[94:95] op_sel_hi:[1,0]
	s_nop 0
	v_cvt_pk_bf16_f32 v10, v40, v41
	v_mul_f32_e32 v40, 0x45800000, v60
	v_cndmask_b32_e64 v40, v60, v40, s[4:5]
	v_pk_mul_f32 v[54:55], v[56:57], v[40:41] op_sel_hi:[1,0]
	v_pk_mul_f32 v[56:57], v[58:59], v[40:41] op_sel_hi:[1,0]
	v_pk_mul_f32 v[54:55], v[54:55], v[104:105]
	v_pk_mul_f32 v[36:37], v[56:57], v[36:37]
	v_pk_mul_f32 v[50:51], v[50:51], v[40:41] op_sel_hi:[1,0]
	v_pk_mul_f32 v[52:53], v[52:53], v[40:41] op_sel_hi:[1,0]
	v_pk_mul_f32 v[46:47], v[46:47], v[40:41] op_sel_hi:[1,0]
	v_pk_mul_f32 v[48:49], v[48:49], v[40:41] op_sel_hi:[1,0]
	v_pk_mul_f32 v[42:43], v[42:43], v[40:41] op_sel_hi:[1,0]
	v_pk_mul_f32 v[40:41], v[44:45], v[40:41] op_sel_hi:[1,0]
	v_mov_b32_e32 v44, v54
	v_mov_b32_e32 v56, v54
	v_mov_b32_e32 v45, v55
	v_mov_b32_e32 v57, v55
	v_permlane32_swap_b32_e32 v44, v56
	s_nop 0
	v_permlane32_swap_b32_e32 v45, v57
	v_cndmask_b32_e32 v45, v45, v57, vcc
	v_cndmask_b32_e32 v44, v44, v56, vcc
	v_pk_mul_f32 v[38:39], v[38:39], v[54:55]
	v_mov_b32_e32 v54, v36
	v_pk_fma_f32 v[38:39], v[106:107], v[44:45], v[38:39]
	v_mov_b32_e32 v44, v36
	v_mov_b32_e32 v45, v37
	v_mov_b32_e32 v55, v37
	v_permlane32_swap_b32_e32 v44, v54
	s_nop 0
	v_permlane32_swap_b32_e32 v45, v55
	v_pk_mul_f32 v[50:51], v[50:51], v[74:75]
	v_cndmask_b32_e32 v45, v45, v55, vcc
	v_cndmask_b32_e32 v44, v44, v54, vcc
	v_pk_mul_f32 v[34:35], v[34:35], v[36:37]
	v_mov_b32_e32 v36, v50
	v_pk_fma_f32 v[32:33], v[32:33], v[44:45], v[34:35]
	v_mov_b32_e32 v34, v50
	v_mov_b32_e32 v35, v51
	v_mov_b32_e32 v37, v51
	v_permlane32_swap_b32_e32 v34, v36
	s_nop 0
	v_permlane32_swap_b32_e32 v35, v37
	v_cndmask_b32_e32 v35, v35, v37, vcc
	v_cndmask_b32_e32 v34, v34, v36, vcc
	v_pk_mul_f32 v[52:53], v[52:53], v[72:73]
	v_pk_mul_f32 v[28:29], v[28:29], v[34:35]
	v_mov_b32_e32 v34, v52
	v_pk_fma_f32 v[28:29], v[30:31], v[50:51], v[28:29]
	v_mov_b32_e32 v30, v52
	v_mov_b32_e32 v31, v53
	v_mov_b32_e32 v35, v53
	v_permlane32_swap_b32_e32 v30, v34
	s_nop 0
	v_permlane32_swap_b32_e32 v31, v35
	v_cndmask_b32_e32 v31, v31, v35, vcc
	v_cndmask_b32_e32 v30, v30, v34, vcc
	v_pk_mul_f32 v[46:47], v[46:47], v[70:71]
; template <int DQK, int DV, bool LEAD> ...
;     ...
;           if constexpr (DQK == 64) {
; #pragma unroll
;               for (int ds = 0; ds < 2; ++ds)
; #pragma unroll
;                   for (int j = 0; j < 8; ++j) {
;                       auto rr = __builtin_amdgcn_permlane32_swap(__float_as_uint(x[ds][j]), __float_as_uint(x[ds][j]), false, false);
;                       const float other = hi ? __uint_as_float(rr[0]) : __uint_as_float(rr[1]);
;                       float cc = 1.f, sg = 0.f;
;                       if (lat) { const f32x2 cs = rope[(ds ? pcol : prow) * 16 + 8 * (g4 & 1) + j]; cc = cs.x; sg = hi ? cs.y : -cs.y; }
;                       x[ds][j] = x[ds][j] * cc + other * sg; }
;           } else {
;               float sr = 0.f;
; #pragma unroll
;               for (int j = 0; j < 8; ++j) sr += x[2][j] * x[2][j];
;               sr = lanes4_sum(sr);
;               const float rq = rsqrtf(sr * (1.f / 32.f) + EPS);
; #pragma unroll
;               for (int j = 0; j < 8; ++j) { const float av = x[2][j] * rq * qgain[64 + 8 * g4 + j];
;                   auto rr = __builtin_amdgcn_permlane16_swap(__float_as_uint(av), __float_as_uint(av), false, false);
;                   const float other = (g4 & 1) ? __uint_as_float(rr[0]) : __uint_as_float(rr[1]);
;                   float cc = 1.f, sg = 0.f;
;                   if (lat) { const f32x2 cs = rope[((g4 & 2) ? pcol : prow) * 8 + j]; cc = cs.x; sg = (g4 & 1) ? cs.y : -cs.y; }
;                   x[2][j] = av * cc + other * sg; }
;           }
; #pragma unroll
;           for (int ds = 0; ds < NDS; ++ds) { u32x4 w;
; #pragma unroll
;               for (int i = 0; i < 4; ++i) w[i] = cvtpk(x[ds][2 * i] * c2, x[ds][2 * i + 1] * c2);
;               qf[qb * NDS + ds] = __builtin_bit_cast(bf16x8, w); }
;       }
; #pragma unroll
;       for (int d0 = 0; d0 < NQB * NDS; ++d0) asm volatile("" : "+v"(qf[d0])); }
;     wait_bar<0>();
;     bf16x8 kf[NKW * NDS], vf[NVF];
;     ATT_KLOAD(0);
;     asm volatile("s_waitcnt lgkmcnt(0)\n\ts_barrier" ::: "memory");
;     float lsum[NQB];
; #pragma unroll
;     for (int qb = 0; qb < NQB; ++qb) lsum[qb] = 0.f;
;     const f32x4 zero4 = {0.f, 0.f, 0.f, 0.f};
;     f32x4 o[NDB][NQB], c[NKW][NQB]; u32x4 pw[4];
; #pragma unroll
;     for (int i = 0; i < NDB; ++i)
; #pragma unroll
;         for (int qb = 0; qb < NQB; ++qb) o[i][qb] = zero4;
	v_pk_mul_f32 v[24:25], v[24:25], v[30:31]
	v_mov_b32_e32 v30, v46
	v_pk_fma_f32 v[24:25], v[52:53], v[26:27], v[24:25]
	v_mov_b32_e32 v26, v46
	v_mov_b32_e32 v27, v47
	v_mov_b32_e32 v31, v47
	v_permlane32_swap_b32_e32 v26, v30
	s_nop 0
	v_permlane32_swap_b32_e32 v27, v31
	v_cndmask_b32_e32 v27, v27, v31, vcc
	v_cndmask_b32_e32 v26, v26, v30, vcc
	v_pk_mul_f32 v[48:49], v[48:49], v[68:69]
	v_pk_mul_f32 v[20:21], v[20:21], v[26:27]
	v_mov_b32_e32 v26, v48
	v_pk_fma_f32 v[20:21], v[46:47], v[22:23], v[20:21]
	v_mov_b32_e32 v22, v48
	v_mov_b32_e32 v23, v49
	v_mov_b32_e32 v27, v49
	v_permlane32_swap_b32_e32 v22, v26
	s_nop 0
	v_permlane32_swap_b32_e32 v23, v27
	v_cndmask_b32_e32 v23, v23, v27, vcc
	v_cndmask_b32_e32 v22, v22, v26, vcc
	v_pk_mul_f32 v[42:43], v[42:43], v[66:67]
	v_pk_mul_f32 v[16:17], v[16:17], v[22:23]
	v_mov_b32_e32 v22, v42
	v_pk_fma_f32 v[16:17], v[48:49], v[18:19], v[16:17]
	v_mov_b32_e32 v18, v42
	v_mov_b32_e32 v19, v43
	v_mov_b32_e32 v23, v43
	v_permlane32_swap_b32_e32 v18, v22
	s_nop 0
	v_permlane32_swap_b32_e32 v19, v23
	v_cndmask_b32_e32 v19, v19, v23, vcc
	v_cndmask_b32_e32 v18, v18, v22, vcc
	v_pk_mul_f32 v[40:41], v[40:41], v[64:65]
	v_pk_mul_f32 v[8:9], v[8:9], v[18:19]
	v_mov_b32_e32 v18, v40
	v_pk_fma_f32 v[8:9], v[42:43], v[14:15], v[8:9]
	v_mov_b32_e32 v14, v40
	v_mov_b32_e32 v15, v41
	v_mov_b32_e32 v19, v41
	v_permlane32_swap_b32_e32 v14, v18
	s_nop 0
	v_permlane32_swap_b32_e32 v15, v19
	v_cndmask_b32_e32 v15, v15, v19, vcc
	v_cndmask_b32_e32 v14, v14, v18, vcc
	v_pk_mul_f32 v[14:15], v[62:63], v[14:15]
	v_pk_mul_f32 v[8:9], v[8:9], s[94:95] op_sel_hi:[1,0]
	v_pk_fma_f32 v[6:7], v[40:41], v[6:7], v[14:15]
	v_pk_mul_f32 v[14:15], v[38:39], s[94:95] op_sel_hi:[1,0]
	v_pk_mul_f32 v[6:7], v[6:7], s[94:95] op_sel_hi:[1,0]
	v_cvt_pk_bf16_f32 v58, v14, v15
	v_pk_mul_f32 v[14:15], v[32:33], s[94:95] op_sel_hi:[1,0]
	v_cvt_pk_bf16_f32 v68, v8, v9
	v_cvt_pk_bf16_f32 v59, v14, v15
	v_pk_mul_f32 v[14:15], v[28:29], s[94:95] op_sel_hi:[1,0]
	v_cvt_pk_bf16_f32 v69, v6, v7
	v_cvt_pk_bf16_f32 v60, v14, v15
	v_pk_mul_f32 v[14:15], v[24:25], s[94:95] op_sel_hi:[1,0]
	v_bfe_u32 v22, v79, 1, 3
	v_cvt_pk_bf16_f32 v61, v14, v15
	v_pk_mul_f32 v[14:15], v[20:21], s[94:95] op_sel_hi:[1,0]
	v_bitop3_b32 v22, v214, v22, 4 bitop3:0x36
	v_cvt_pk_bf16_f32 v66, v14, v15
	v_pk_mul_f32 v[14:15], v[16:17], s[94:95] op_sel_hi:[1,0]
	v_lshlrev_b32_e32 v30, 4, v22
	v_cvt_pk_bf16_f32 v67, v14, v15
	s_waitcnt vmcnt(0) lgkmcnt(0)
	s_barrier
	ds_read_b128 v[6:9], v194
	ds_read_b128 v[14:17], v194 offset:512
	v_add_u32_e32 v220, v81, v30
	s_waitcnt lgkmcnt(1)
	v_mfma_f32_16x16x32_bf16 v[18:21], v[6:9], v[10:13], 0
	ds_read_b128 v[22:25], v220
	ds_read_b128 v[26:29], v220 offset:512
	v_add_u32_e32 v31, 0, v217
	v_add_u32_e32 v218, v31, v80
	v_mfma_f32_16x16x32_bf16 v[6:9], v[6:9], v[58:61], 0
	v_add_u32_e32 v219, v31, v30
	s_waitcnt lgkmcnt(1)
	v_mfma_f32_16x16x32_bf16 v[126:129], v[22:25], v[66:69], v[6:9]
	v_mfma_f32_16x16x32_bf16 v[6:9], v[14:17], v[10:13], 0
	s_waitcnt lgkmcnt(0)
	v_mfma_f32_16x16x32_bf16 v[122:125], v[26:29], v[2:5], v[6:9]
	v_mfma_f32_16x16x32_bf16 v[14:17], v[14:17], v[58:61], 0
	s_nop 4
	ds_read_b128 v[6:9], v194 offset:4096
	v_mfma_f32_16x16x32_bf16 v[138:141], v[22:25], v[2:5], v[18:21]
	v_mfma_f32_16x16x32_bf16 v[114:117], v[26:29], v[66:69], v[14:17]
	s_nop 2
	ds_read_b128 v[14:17], v220 offset:4096
	ds_read_b128 v[18:21], v194 offset:4608
	ds_read_b128 v[26:29], v220 offset:4608
	s_waitcnt lgkmcnt(0)
	s_barrier
	s_waitcnt lgkmcnt(3)
	v_mfma_f32_16x16x32_bf16 v[22:25], v[6:9], v[10:13], 0
	v_mfma_f32_16x16x32_bf16 v[6:9], v[6:9], v[58:61], 0
	s_waitcnt lgkmcnt(2)
	v_mfma_f32_16x16x32_bf16 v[130:133], v[14:17], v[2:5], v[22:25]
	s_nop 4
	v_lshl_add_u64 v[22:23], v[204:205], 0, s[96:97]
	v_mfma_f32_16x16x32_bf16 v[118:121], v[14:17], v[66:69], v[6:9]
	s_mov_b32 s4, m0
	s_mov_b32 m0, s43
	s_nop 0
	global_load_lds_dwordx4 v[22:23], off
	s_mov_b32 m0, s4
	v_lshl_add_u64 v[14:15], v[206:207], 0, s[66:67]
	s_add_i32 s4, s16, 0x4000
	s_waitcnt lgkmcnt(1)
	v_mfma_f32_16x16x32_bf16 v[6:9], v[18:21], v[10:13], 0
	s_mov_b32 s5, m0
	s_mov_b32 m0, s4
	s_nop 0
	global_load_lds_dwordx4 v[14:15], off
	s_mov_b32 m0, s5
	s_mov_b64 s[4:5], 0x840080
	v_lshl_add_u64 v[22:23], v[206:207], 0, s[4:5]
	v_mfma_f32_16x16x32_bf16 v[14:17], v[18:21], v[58:61], 0
	s_add_i32 s4, s16, 0x6000
	s_mov_b32 s5, m0
	s_mov_b32 m0, s4
	s_nop 0
	global_load_lds_dwordx4 v[22:23], off
	s_mov_b32 m0, s5
	s_mov_b32 s4, 0
	s_waitcnt lgkmcnt(0)
	v_mfma_f32_16x16x32_bf16 v[142:145], v[26:29], v[2:5], v[6:9]
	s_mov_b32 s6, s4
	s_mov_b32 s7, s4
	s_mov_b32 s5, s4
	v_mfma_f32_16x16x32_bf16 v[134:137], v[26:29], v[66:69], v[14:17]
	v_mov_b64_e32 v[8:9], s[6:7]
	v_mov_b64_e32 v[6:7], s[4:5]
	ds_read_b128 v[82:85], v194 offset:8192
	ds_read_b128 v[86:89], v194 offset:8704
	ds_read_b128 v[90:93], v220 offset:8192
	ds_read_b128 v[94:97], v220 offset:8704
	ds_read_b128 v[98:101], v194 offset:12288
	ds_read_b128 v[102:105], v194 offset:12800
	ds_read_b128 v[106:109], v220 offset:12288
	ds_read_b128 v[110:113], v220 offset:12800
	s_waitcnt vmcnt(3) lgkmcnt(0)
	s_barrier
	s_mov_b32 s5, 1
	v_mov_b32_e32 v42, 0
	s_cmp_lg_u32 s5, 0
	v_mov_b64_e32 v[16:17], v[8:9]
	v_mov_b64_e32 v[20:21], v[8:9]
	v_mov_b64_e32 v[24:25], v[8:9]
	v_mov_b64_e32 v[28:29], v[8:9]
	v_mov_b64_e32 v[32:33], v[8:9]
	v_mov_b64_e32 v[36:37], v[8:9]
	v_mov_b64_e32 v[40:41], v[8:9]
	s_cselect_b64 s[6:7], -1, 0
	v_mov_b64_e32 v[14:15], v[6:7]
	v_mov_b64_e32 v[18:19], v[6:7]
	v_mov_b64_e32 v[22:23], v[6:7]
	v_mov_b64_e32 v[26:27], v[6:7]
	v_mov_b64_e32 v[30:31], v[6:7]
	v_mov_b64_e32 v[34:35], v[6:7]
	v_mov_b64_e32 v[38:39], v[6:7]
	s_mov_b32 s38, 2
	v_mov_b32_e32 v43, v42
	v_mov_b32_e32 v44, v42
	v_mov_b32_e32 v45, v42
	v_mov_b32_e32 v46, v42
	v_mov_b32_e32 v47, v42
	v_mov_b32_e32 v48, v42
	v_mov_b32_e32 v49, v42
	v_mov_b32_e32 v50, v42
	v_mov_b32_e32 v51, v42
	v_mov_b32_e32 v52, v42
	v_mov_b32_e32 v53, v42
	v_mov_b32_e32 v54, v42
	v_mov_b32_e32 v55, v42
	v_mov_b32_e32 v56, v42
	v_mov_b32_e32 v57, v42
	v_mov_b32_e32 v62, v42
	v_mov_b32_e32 v63, v42
	v_mov_b32_e32 v64, v42
	v_mov_b32_e32 v65, v42
	v_mov_b32_e32 v70, v42
	v_mov_b32_e32 v71, v42
	v_mov_b32_e32 v72, v42
	v_mov_b32_e32 v73, v42
	v_mov_b32_e32 v74, v42
	v_mov_b32_e32 v75, v42
	v_mov_b32_e32 v76, v42
	v_mov_b32_e32 v77, v42
	v_mov_b32_e32 v78, v42
	v_mov_b32_e32 v79, v42
	v_mov_b32_e32 v80, v42
	v_mov_b32_e32 v81, v42
	v_mov_b32_e32 v210, v42
	v_mov_b32_e32 v211, v42

; template <int DQK, int DV, bool LEAD> ...
;     ...
;     const int tid = tid_, lane = tid & 63, q16 = lane & 15, g4 = lane >> 4, hi = lane >> 5; const int wid = __builtin_amdgcn_readfirstlane(tid >> 6);
;     const int kg = KS ? (wid >> 2) : 0, qoff = KS ? (wid & 3) * 64 : wid * 32;
;     const unsigned lds0 = (unsigned)(uintptr_t)shm;
;     const int krow_l = wid * 8 + (lane >> 3);
;     const int kc_l = (lane & 7) ^ (((krow_l >> 1) & 1) | (((krow_l >> 3) & 1) << 1) | (((krow_l >> 4) & 1) << 2));
;     const int vc_l = (lane & 7) ^ ((krow_l >> 1) & 7);
;     const bf16_t* ksrc = K + (size_t)(krow0 + krow_l) * kpitch + kc_l * 8;
;     const int rrow_l = (wid & 3) * 16 + (lane >> 2), rc_l = (lane & 3) ^ (((rrow_l >> 4) & 1) << 1);
;     const bf16_t* krsrc = (DQK == 96) ? KR + (size_t)(krow0 + rrow_l) * 32 + rc_l * 8 : nullptr;
;     const bf16_t* vsrc = Vt + (size_t)krow_l * NR + krow0 + vc_l * 8;
;     const unsigned kdst = lds0 + KOFF + wid * 1024, krdst = lds0 + KOFF + 8192 + (wid & 3) * 1024, vdst = lds0 + VOFF + wid * 1024;
;     ...
;     const int kr0 = 8 * (q16 >> 2) + (q16 & 3);
;     const int fk = ((kr0 >> 1) & 1) | (((kr0 >> 3) & 1) << 1) | (((kr0 >> 4) & 1) << 2);
;     const LAS unsigned char* kp[2]; const LAS unsigned char* vp[2];
; #pragma unroll
;     for (int ds = 0; ds < 2; ++ds) kp[ds] = shm + KOFF + kr0 * 128 + ((((ds << 2) | g4) ^ fk) << 4) + kg * 4096;
;     const LAS unsigned char* krp = shm + KOFF + 8192 + kr0 * 64 + ((g4 ^ (((kr0 >> 4) & 1) << 1)) << 4) + kg * 2048;
; #pragma unroll
;     for (int s_ = 0; s_ < 2; ++s_) vp[s_] = shm + VOFF + q16 * 128 + ((((s_ << 2) | g4) ^ ((q16 >> 1) & 7)) << 4);
;     const LAS unsigned char* vpk = kg ? vp[1] : vp[0];
;     ...
;     ATT_DMA_K(0, 0); ATT_DMA_V(0, 0); ATT_DMA_K(1, 1); ATT_DMA_K(2, 2);
;     bf16x8 qf[NQB * NDS];
;     {
;       const float c2 = (DQK == 64) ? C2_EVEN : C2_ODD; const bool lat = tq0 >= 0;
; #pragma unroll
;       for (int qb = 0; qb < NQB; ++qb) {
;           const bf16_t* qp = Q + (size_t)(qrow0 + qoff + qb * 16 + q16) * qpitch + g4 * 8;
; __global__ void __launch_bounds__(NWAVES * 64, 2) mega_fwd(Args args_) {
;     ...
;                 att::attn_unit<64, 128>(QK + h * 128 + c * 64, QKW, QK + 512 + h * 128 + c * 64, QKW, nullptr, VTE + (size_t)(h * 128) * NR, OB + hc * 128, 1024, b * TPS + qb * 256, b * TPS, 132, F.lds, IN(a, I_AQK) + j * 128, (const f32x2*)(ws + WS_ROPE64), qb * 256); }
.LBB0_946:
	s_and_b64 vcc, exec, s[4:5]
	s_cbranch_vccz .LBB0_938
	v_mov_b32_e32 v79, v0
	s_ashr_i32 s47, s46, 31
	v_readfirstlane_b32 s4, v79
	s_ashr_i32 s7, s4, 6
	v_bfe_u32 v1, v79, 3, 3
	v_lshl_or_b32 v6, s7, 3, v1
	s_lshl_b32 s5, s7, 1
	s_lshr_b32 s4, s4, 5
	v_ashrrev_i32_e32 v2, 1, v6
	s_and_b32 s5, s5, 2
	s_and_b32 s4, s4, 4
	v_and_b32_e32 v170, 7, v79
	v_and_b32_e32 v3, 1, v2
	s_or_b32 s4, s5, s4
	v_bitop3_b32 v7, s4, v170, v3 bitop3:0x36
	v_xor_b32_e32 v8, v2, v79
	v_add_u32_e32 v4, s46, v6
	s_lshl_b32 s4, s7, 10
	v_mov_b64_e32 v[2:3], s[40:41]
	s_add_i32 s31, s4, 0
	v_mad_i64_i32 v[2:3], s[4:5], v4, s92, v[2:3]
	v_mov_b64_e32 v[4:5], s[44:45]
	v_lshlrev_b32_e32 v194, 4, v7
	v_mad_i64_i32 v[4:5], s[4:5], v6, s91, v[4:5]
	v_lshl_add_u64 v[162:163], v[2:3], 0, v[194:195]
	v_lshlrev_b32_e32 v2, 4, v8
	v_lshl_add_u64 v[4:5], s[46:47], 1, v[4:5]
	v_and_b32_e32 v194, 0x70, v2
	s_mov_b32 s4, m0
	s_mov_b32 m0, s31
	s_nop 0
	global_load_lds_dwordx4 v[162:163], off
	s_mov_b32 m0, s4
	v_lshl_add_u64 v[164:165], v[4:5], 0, v[194:195]
	s_add_i32 s40, s31, 0x9000
	s_mov_b32 s4, m0
	s_mov_b32 m0, s40
	s_nop 0
	global_load_lds_dwordx4 v[164:165], off
	s_mov_b32 m0, s4
	s_mov_b64 s[4:5], 0x840000
	v_lshl_add_u64 v[166:167], v[164:165], 0, s[4:5]
	s_add_i32 s4, s40, 0x2000
	s_mov_b32 s5, m0
	s_mov_b32 m0, s4
	s_nop 0
	global_load_lds_dwordx4 v[166:167], off
	s_mov_b32 m0, s5
	s_mov_b64 s[4:5], 0x38000
	v_lshl_add_u64 v[2:3], v[162:163], 0, s[4:5]
	s_add_i32 s4, s31, 0x2000
	s_mov_b32 s5, m0
	s_mov_b32 m0, s4
	s_nop 0
	global_load_lds_dwordx4 v[2:3], off
	s_mov_b32 m0, s5
	s_lshl_b32 s16, s7, 5
	s_mov_b64 s[4:5], 0x70000
	v_and_b32_e32 v78, 15, v79
	v_lshl_add_u64 v[2:3], v[162:163], 0, s[4:5]
	s_add_i32 s6, s16, s30
	v_and_b32_e32 v194, 48, v79
	s_add_i32 s4, s31, 0x4000
	s_mov_b32 s5, m0
	s_mov_b32 m0, s4
	s_nop 0
	global_load_lds_dwordx4 v[2:3], off
	s_mov_b32 m0, s5
	v_or_b32_e32 v4, s6, v78
	v_lshl_add_u64 v[2:3], s[36:37], 0, v[194:195]
	v_lshrrev_b32_e32 v38, 1, v79
	v_or_b32_e32 v5, s16, v78
	v_mad_i64_i32 v[26:27], s[4:5], v4, s92, v[2:3]
	v_and_b32_e32 v28, 8, v38
	v_lshlrev_b32_e32 v5, 4, v5
	s_movk_i32 s4, 0x2f0
	v_or_b32_e32 v4, 16, v4
	v_and_or_b32 v5, v5, s4, v28
	v_mad_i64_i32 v[30:31], s[4:5], v4, s92, v[2:3]
	s_add_i32 s16, s16, s25
	s_lshr_b32 s4, s16, 2
	v_lshlrev_b32_e32 v22, 3, v5
	s_and_b32 s4, s4, 0x7f0
	global_load_dwordx4 v[50:53], v[26:27], off offset:64 nt
	global_load_dwordx4 v[60:63], v22, s[8:9] offset:48
	global_load_dwordx4 v[70:73], v[30:31], off offset:64 nt
	global_load_dwordx4 v[10:13], v22, s[8:9] offset:2096
	global_load_dwordx4 v[54:57], v22, s[8:9] offset:32
	global_load_dwordx4 v[14:17], v22, s[8:9] offset:2080
	global_load_dwordx4 v[2:5], v22, s[8:9] offset:16
	global_load_dwordx4 v[18:21], v22, s[8:9] offset:2064
	global_load_dwordx4 v[6:9], v22, s[8:9]
	s_nop 0
	global_load_dwordx4 v[22:25], v22, s[8:9] offset:2048
	s_nop 0
	global_load_dwordx4 v[82:85], v[26:27], off nt
	v_or_b32_e32 v26, s4, v28
	v_lshlrev_b32_e32 v39, 3, v26
	global_load_dwordx4 v[26:29], v39, s[8:9] offset:48
	global_load_dwordx4 v[86:89], v[30:31], off nt
	s_nop 0
	global_load_dwordx4 v[30:33], v39, s[8:9] offset:32
	global_load_dwordx4 v[34:37], v39, s[8:9] offset:16
	v_bfe_u32 v171, v79, 4, 2
	v_lshlrev_b32_e32 v172, 1, v79
	v_and_b32_e32 v40, 3, v79
	v_and_or_b32 v40, v172, 24, v40
	v_bitop3_b32 v38, v171, v38, 7 bitop3:0x78
	v_lshlrev_b32_e32 v59, 5, v171
	v_lshl_add_u32 v81, v40, 7, 0
	v_lshlrev_b32_e32 v80, 4, v38
	global_load_dwordx4 v[38:41], v39, s[8:9]
	s_nop 0
	global_load_dwordx4 v[42:45], v59, s[28:29] offset:144
	global_load_dwordx4 v[46:49], v59, s[28:29] offset:128
	v_and_b32_e32 v58, 63, v79
	v_cmp_gt_u32_e32 vcc, 32, v58
	s_mov_b32 s4, 0x3c800000
	v_add_u32_e32 v173, v81, v80
	v_lshlrev_b32_e32 v175, 7, v78
	s_mov_b32 s25, 1
	s_mov_b32 s16, 2
	v_or_b32_e32 v174, 4, v171
	s_waitcnt vmcnt(15)
	v_and_b32_e32 v65, 0xffff0000, v73
	v_lshlrev_b32_e32 v64, 16, v73
	v_and_b32_e32 v67, 0xffff0000, v72
	v_lshlrev_b32_e32 v66, 16, v72
	s_waitcnt vmcnt(13)
	v_cndmask_b32_e64 v95, v57, -v57, vcc
	v_cndmask_b32_e64 v94, v55, -v55, vcc
	v_and_b32_e32 v91, 0xffff0000, v53
	v_lshlrev_b32_e32 v90, 16, v53
	v_and_b32_e32 v93, 0xffff0000, v52
	s_waitcnt vmcnt(5)
	v_and_b32_e32 v73, 0xffff0000, v89
	v_lshlrev_b32_e32 v72, 16, v89
	v_and_b32_e32 v75, 0xffff0000, v88
	v_lshlrev_b32_e32 v74, 16, v88
	v_and_b32_e32 v89, 0xffff0000, v83
	v_lshlrev_b32_e32 v88, 16, v83
	v_and_b32_e32 v83, 0xffff0000, v82
	v_lshlrev_b32_e32 v92, 16, v52
	v_mov_b32_e32 v55, v56
	v_and_b32_e32 v97, 0xffff0000, v51
	v_lshlrev_b32_e32 v96, 16, v51
	v_cndmask_b32_e64 v98, v3, -v3, vcc
	v_mov_b32_e32 v3, v4
	v_and_b32_e32 v101, 0xffff0000, v50
	v_lshlrev_b32_e32 v100, 16, v50
	global_load_dwordx4 v[50:53], v59, s[28:29] offset:16
	s_nop 0
	global_load_dwordx4 v[56:59], v59, s[28:29]
	v_lshlrev_b32_e32 v82, 16, v82
	v_mul_f32_e32 v4, v83, v83
	v_cndmask_b32_e64 v99, v5, -v5, vcc
	v_pk_fma_f32 v[4:5], v[82:83], v[82:83], v[4:5] op_sel_hi:[1,1,0]
	v_mul_f32_e32 v104, v89, v89
	v_pk_fma_f32 v[4:5], v[88:89], v[88:89], v[4:5]
	v_cndmask_b32_e64 v103, v9, -v9, vcc
	v_cndmask_b32_e64 v102, v7, -v7, vcc
	v_mov_b32_e32 v7, v8
	v_and_b32_e32 v9, 0xffff0000, v85
	v_lshlrev_b32_e32 v8, 16, v85
	v_and_b32_e32 v85, 0xffff0000, v84
	v_lshlrev_b32_e32 v84, 16, v84
	v_pk_add_f32 v[4:5], v[104:105], v[4:5] op_sel_hi:[0,1]
	v_pk_fma_f32 v[4:5], v[84:85], v[84:85], v[4:5]
	v_mul_f32_e32 v104, v85, v85
	v_pk_add_f32 v[4:5], v[104:105], v[4:5] op_sel_hi:[0,1]
	v_pk_fma_f32 v[4:5], v[8:9], v[8:9], v[4:5]
	v_mul_f32_e32 v104, v9, v9
	v_pk_add_f32 v[4:5], v[104:105], v[4:5] op_sel_hi:[0,1]
	v_pk_fma_f32 v[4:5], v[100:101], v[100:101], v[4:5]
	v_mul_f32_e32 v104, v101, v101
	v_pk_add_f32 v[4:5], v[104:105], v[4:5] op_sel_hi:[0,1]
	v_pk_fma_f32 v[4:5], v[96:97], v[96:97], v[4:5]
	v_mul_f32_e32 v104, v97, v97
	v_pk_add_f32 v[4:5], v[104:105], v[4:5] op_sel_hi:[0,1]
	v_pk_fma_f32 v[4:5], v[92:93], v[92:93], v[4:5]
	v_mul_f32_e32 v104, v93, v93
	v_pk_add_f32 v[4:5], v[104:105], v[4:5] op_sel_hi:[0,1]
	v_pk_fma_f32 v[4:5], v[90:91], v[90:91], v[4:5]
	v_mul_f32_e32 v104, v91, v91
	v_pk_add_f32 v[4:5], v[104:105], v[4:5] op_sel_hi:[0,1]
	v_mov_b32_e32 v5, v4
	s_nop 1
	v_permlane16_swap_b32_e32 v4, v5
	v_add_f32_e32 v5, v4, v5
	v_cndmask_b32_e64 v77, v63, -v63, vcc
	v_cndmask_b32_e64 v76, v61, -v61, vcc
	v_mov_b32_e32 v61, v62
	v_cndmask_b32_e64 v63, v13, -v13, vcc
	v_cndmask_b32_e64 v62, v11, -v11, vcc
	v_mov_b32_e32 v11, v12
	v_cndmask_b32_e64 v13, v17, -v17, vcc
	v_cndmask_b32_e64 v12, v15, -v15, vcc
	v_mov_b32_e32 v15, v16
	v_cndmask_b32_e64 v17, v21, -v21, vcc
	v_cndmask_b32_e64 v16, v19, -v19, vcc
	v_mov_b32_e32 v19, v20
	v_cndmask_b32_e64 v21, v25, -v25, vcc
	v_cndmask_b32_e64 v20, v23, -v23, vcc
	v_mov_b32_e32 v23, v24
	v_cndmask_b32_e64 v25, v29, -v29, vcc
	v_cndmask_b32_e64 v24, v27, -v27, vcc
	v_mov_b32_e32 v27, v28
	s_waitcnt vmcnt(6)
; template <int DQK, int DV, bool LEAD> ...
;     ...
;           sn = lanes4_sum(sn);
;           const float rn = rsqrtf(sn * (1.f / 64.f) + EPS);
; #pragma unroll
;           for (int ds = 0; ds < 2; ++ds)
; #pragma unroll
;               for (int j = 0; j < 8; ++j) x[ds][j] *= rn * qgain[32 * ds + 8 * g4 + j];
;           if constexpr (DQK == 64) {
; #pragma unroll
;               for (int ds = 0; ds < 2; ++ds)
; #pragma unroll
;                   for (int j = 0; j < 8; ++j) {
;                       auto rr = __builtin_amdgcn_permlane32_swap(__float_as_uint(x[ds][j]), __float_as_uint(x[ds][j]), false, false);
;                       const float other = hi ? __uint_as_float(rr[0]) : __uint_as_float(rr[1]);
;                       float cc = 1.f, sg = 0.f;
;                       if (lat) { const f32x2 cs = rope[(ds ? pcol : prow) * 16 + 8 * (g4 & 1) + j]; cc = cs.x; sg = hi ? cs.y : -cs.y; }
;                       x[ds][j] = x[ds][j] * cc + other * sg; }
	v_cndmask_b32_e64 v29, v33, -v33, vcc
	v_cndmask_b32_e64 v28, v31, -v31, vcc
	v_mov_b32_e32 v31, v32
	s_waitcnt vmcnt(5)
	v_cndmask_b32_e64 v33, v37, -v37, vcc
	v_cndmask_b32_e64 v32, v35, -v35, vcc
	v_mov_b32_e32 v35, v36
	v_and_b32_e32 v37, 0xffff0000, v87
	v_lshlrev_b32_e32 v36, 16, v87
	v_mov_b32_e32 v87, v5
	v_and_b32_e32 v105, 0xffff0000, v86
	s_nop 0
	v_permlane32_swap_b32_e32 v5, v87
	v_lshlrev_b32_e32 v104, 16, v86
	v_mul_f32_e32 v4, v105, v105
	v_pk_fma_f32 v[106:107], v[104:105], v[104:105], v[4:5] op_sel_hi:[1,1,0]
	v_mul_f32_e32 v4, v37, v37
	v_pk_fma_f32 v[106:107], v[36:37], v[36:37], v[106:107]
	v_and_b32_e32 v69, 0xffff0000, v71
	v_pk_add_f32 v[106:107], v[4:5], v[106:107] op_sel_hi:[0,1]
	v_pk_fma_f32 v[106:107], v[74:75], v[74:75], v[106:107]
	v_mul_f32_e32 v4, v75, v75
	v_pk_add_f32 v[106:107], v[4:5], v[106:107] op_sel_hi:[0,1]
	v_pk_fma_f32 v[106:107], v[72:73], v[72:73], v[106:107]
	v_mul_f32_e32 v4, v73, v73
	v_lshlrev_b32_e32 v68, 16, v71
	v_and_b32_e32 v71, 0xffff0000, v70
	v_lshlrev_b32_e32 v70, 16, v70
	v_pk_add_f32 v[106:107], v[4:5], v[106:107] op_sel_hi:[0,1]
	v_pk_fma_f32 v[106:107], v[70:71], v[70:71], v[106:107]
	v_mul_f32_e32 v4, v71, v71
	v_pk_add_f32 v[106:107], v[4:5], v[106:107] op_sel_hi:[0,1]
	v_pk_fma_f32 v[106:107], v[68:69], v[68:69], v[106:107]
	v_mul_f32_e32 v4, v69, v69
	v_pk_add_f32 v[106:107], v[4:5], v[106:107] op_sel_hi:[0,1]
	v_pk_fma_f32 v[106:107], v[66:67], v[66:67], v[106:107]
	v_mul_f32_e32 v4, v67, v67
	v_pk_add_f32 v[106:107], v[4:5], v[106:107] op_sel_hi:[0,1]
	v_pk_fma_f32 v[106:107], v[64:65], v[64:65], v[106:107]
	v_mul_f32_e32 v4, v65, v65
	v_pk_add_f32 v[106:107], v[4:5], v[106:107] op_sel_hi:[0,1]
	v_mov_b32_e32 v4, v106
	s_nop 1
	v_permlane16_swap_b32_e32 v106, v4
	v_add_f32_e32 v4, v106, v4
	v_mov_b32_e32 v86, v4
	s_nop 1
	v_permlane32_swap_b32_e32 v4, v86
	v_pk_add_f32 v[4:5], v[4:5], v[86:87]
	s_waitcnt vmcnt(4)
	v_cndmask_b32_e64 v106, v39, -v39, vcc
	v_pk_fma_f32 v[86:87], v[4:5], s[4:5], v[196:197] op_sel_hi:[1,0,0]
	v_mov_b32_e32 v39, v40
	v_mul_f32_e32 v4, 0x4b800000, v87
	v_cmp_gt_f32_e64 s[4:5], s95, v87
	v_cndmask_b32_e64 v107, v41, -v41, vcc
	s_mov_b32 s28, 0
	v_cndmask_b32_e64 v4, v87, v4, s[4:5]
	v_rsq_f32_e32 v4, v4
	s_nop 0
	v_mul_f32_e32 v5, 0x45800000, v4
	v_cndmask_b32_e64 v40, v4, v5, s[4:5]
	s_waitcnt vmcnt(3)
	v_pk_mul_f32 v[4:5], v[40:41], v[44:45] op_sel_hi:[0,1]
	v_pk_mul_f32 v[4:5], v[4:5], v[90:91]
	v_cmp_gt_f32_e64 s[4:5], s95, v86
	v_mov_b32_e32 v41, v4
	v_mov_b32_e32 v87, v4
	v_mov_b32_e32 v90, v5
	v_mov_b32_e32 v91, v5
	v_permlane32_swap_b32_e32 v41, v87
	s_nop 0
	v_permlane32_swap_b32_e32 v90, v91
	v_cndmask_b32_e32 v91, v90, v91, vcc
	v_cndmask_b32_e32 v90, v41, v87, vcc
	v_pk_mul_f32 v[76:77], v[76:77], v[90:91]
	s_nop 0
	v_pk_fma_f32 v[4:5], v[4:5], v[60:61], v[76:77]
	v_pk_mul_f32 v[60:61], v[40:41], v[42:43] op_sel_hi:[0,1]
	v_pk_mul_f32 v[4:5], v[4:5], s[94:95] op_sel_hi:[1,0]
	v_pk_mul_f32 v[60:61], v[60:61], v[92:93]
	v_cvt_pk_bf16_f32 v5, v4, v5
	v_mov_b32_e32 v4, v60
	v_mov_b32_e32 v41, v60
	v_mov_b32_e32 v76, v61
	v_mov_b32_e32 v77, v61
	v_permlane32_swap_b32_e32 v4, v41
	s_nop 0
	v_permlane32_swap_b32_e32 v76, v77
	v_cndmask_b32_e32 v77, v76, v77, vcc
	v_cndmask_b32_e32 v76, v4, v41, vcc
	v_pk_mul_f32 v[76:77], v[94:95], v[76:77]
	s_nop 0
	v_pk_fma_f32 v[54:55], v[60:61], v[54:55], v[76:77]
	s_nop 0
	v_pk_mul_f32 v[54:55], v[54:55], s[94:95] op_sel_hi:[1,0]
	s_nop 0
	v_cvt_pk_bf16_f32 v4, v54, v55
	s_waitcnt vmcnt(2)
	v_pk_mul_f32 v[54:55], v[40:41], v[48:49] op_sel_hi:[0,1]
	v_pk_mul_f32 v[54:55], v[54:55], v[96:97]
	s_nop 0
	v_mov_b32_e32 v41, v54
	v_mov_b32_e32 v60, v54
	v_mov_b32_e32 v61, v55
	v_mov_b32_e32 v76, v55
	v_permlane32_swap_b32_e32 v41, v60
	s_nop 0
	v_permlane32_swap_b32_e32 v61, v76
	v_cndmask_b32_e32 v61, v61, v76, vcc
	v_cndmask_b32_e32 v60, v41, v60, vcc
	v_pk_mul_f32 v[60:61], v[98:99], v[60:61]
	s_nop 0
	v_pk_fma_f32 v[2:3], v[54:55], v[2:3], v[60:61]
	v_pk_mul_f32 v[54:55], v[46:47], v[40:41] op_sel_hi:[1,0]
	v_pk_mul_f32 v[2:3], v[2:3], s[94:95] op_sel_hi:[1,0]
	v_pk_mul_f32 v[54:55], v[54:55], v[100:101]
	v_cvt_pk_bf16_f32 v3, v2, v3
	v_mov_b32_e32 v2, v54
	v_mov_b32_e32 v41, v54
	v_mov_b32_e32 v60, v55
	v_mov_b32_e32 v61, v55
	v_permlane32_swap_b32_e32 v2, v41
	s_nop 0
	v_permlane32_swap_b32_e32 v60, v61
	v_cndmask_b32_e32 v61, v60, v61, vcc
	v_cndmask_b32_e32 v60, v2, v41, vcc
	v_pk_mul_f32 v[60:61], v[102:103], v[60:61]
	s_nop 0
	v_pk_fma_f32 v[6:7], v[54:55], v[6:7], v[60:61]
	s_nop 0
	v_pk_mul_f32 v[6:7], v[6:7], s[94:95] op_sel_hi:[1,0]
	s_nop 0
	v_cvt_pk_bf16_f32 v2, v6, v7
	s_waitcnt vmcnt(1)
	v_pk_mul_f32 v[6:7], v[52:53], v[40:41] op_sel_hi:[1,0]
	s_nop 0
	v_pk_mul_f32 v[6:7], v[6:7], v[8:9]
	s_nop 0
	v_mov_b32_e32 v8, v6
	v_mov_b32_e32 v41, v6
	v_mov_b32_e32 v9, v7
	v_mov_b32_e32 v54, v7
	v_permlane32_swap_b32_e32 v8, v41
	s_nop 0
	v_permlane32_swap_b32_e32 v9, v54
	v_cndmask_b32_e32 v9, v9, v54, vcc
	v_cndmask_b32_e32 v8, v8, v41, vcc
	v_pk_mul_f32 v[8:9], v[24:25], v[8:9]
	s_nop 0
	v_pk_fma_f32 v[6:7], v[6:7], v[26:27], v[8:9]
	s_nop 0
	v_pk_mul_f32 v[6:7], v[6:7], s[94:95] op_sel_hi:[1,0]
	s_nop 0
	v_cvt_pk_bf16_f32 v9, v6, v7
	v_pk_mul_f32 v[6:7], v[50:51], v[40:41] op_sel_hi:[1,0]
	s_nop 0
	v_pk_mul_f32 v[6:7], v[6:7], v[84:85]
	s_nop 0
	v_mov_b32_e32 v8, v6
	v_mov_b32_e32 v41, v6
	v_mov_b32_e32 v54, v7
	v_mov_b32_e32 v55, v7
	v_permlane32_swap_b32_e32 v8, v41
	s_nop 0
	v_permlane32_swap_b32_e32 v54, v55
	v_cndmask_b32_e32 v55, v54, v55, vcc
	v_cndmask_b32_e32 v54, v8, v41, vcc
	v_pk_mul_f32 v[54:55], v[28:29], v[54:55]
	s_nop 0
	v_pk_fma_f32 v[6:7], v[6:7], v[30:31], v[54:55]
	s_nop 0
	v_pk_mul_f32 v[6:7], v[6:7], s[94:95] op_sel_hi:[1,0]
	s_nop 0
	v_cvt_pk_bf16_f32 v8, v6, v7
	s_waitcnt vmcnt(0)
; __device__ __forceinline__ unsigned cvtpk(float lo, float hi) { f32x2 v = {lo, hi}; bf16x2_t b = __builtin_convertvector(v, bf16x2_t); return __builtin_bit_cast(unsigned, b); }
; template <int DQK, int DV, bool LEAD> ...
;     ...
;               for (int j = 0; j < 8; ++j) x[ds][j] *= rn * qgain[32 * ds + 8 * g4 + j];
;           if constexpr (DQK == 64) {
; #pragma unroll
;               for (int ds = 0; ds < 2; ++ds)
; #pragma unroll
;                   for (int j = 0; j < 8; ++j) {
;                       auto rr = __builtin_amdgcn_permlane32_swap(__float_as_uint(x[ds][j]), __float_as_uint(x[ds][j]), false, false);
;                       const float other = hi ? __uint_as_float(rr[0]) : __uint_as_float(rr[1]);
;                       float cc = 1.f, sg = 0.f;
;                       if (lat) { const f32x2 cs = rope[(ds ? pcol : prow) * 16 + 8 * (g4 & 1) + j]; cc = cs.x; sg = hi ? cs.y : -cs.y; }
;                       x[ds][j] = x[ds][j] * cc + other * sg; }
;           } else {
;               float sr = 0.f;
; #pragma unroll
;               for (int j = 0; j < 8; ++j) sr += x[2][j] * x[2][j];
;               sr = lanes4_sum(sr);
;               const float rq = rsqrtf(sr * (1.f / 32.f) + EPS);
; #pragma unroll
;               for (int j = 0; j < 8; ++j) { const float av = x[2][j] * rq * qgain[64 + 8 * g4 + j];
;                   auto rr = __builtin_amdgcn_permlane16_swap(__float_as_uint(av), __float_as_uint(av), false, false);
;                   const float other = (g4 & 1) ? __uint_as_float(rr[0]) : __uint_as_float(rr[1]);
;                   float cc = 1.f, sg = 0.f;
;                   if (lat) { const f32x2 cs = rope[((g4 & 2) ? pcol : prow) * 8 + j]; cc = cs.x; sg = (g4 & 1) ? cs.y : -cs.y; }
;                   x[2][j] = av * cc + other * sg; }
;           }
; #pragma unroll
;           for (int ds = 0; ds < NDS; ++ds) { u32x4 w;
; #pragma unroll
;               for (int i = 0; i < 4; ++i) w[i] = cvtpk(x[ds][2 * i] * c2, x[ds][2 * i + 1] * c2);
;               qf[qb * NDS + ds] = __builtin_bit_cast(bf16x8, w); }
;       }
; #pragma unroll
;       for (int d0 = 0; d0 < NQB * NDS; ++d0) asm volatile("" : "+v"(qf[d0])); }
;     wait_bar<0>();
	v_pk_mul_f32 v[6:7], v[58:59], v[40:41] op_sel_hi:[1,0]
	s_nop 0
	v_pk_mul_f32 v[6:7], v[6:7], v[88:89]
	s_nop 0
	v_mov_b32_e32 v41, v6
	v_mov_b32_e32 v54, v6
	v_mov_b32_e32 v55, v7
	v_mov_b32_e32 v60, v7
	v_permlane32_swap_b32_e32 v41, v54
	s_nop 0
	v_permlane32_swap_b32_e32 v55, v60
	v_cndmask_b32_e32 v55, v55, v60, vcc
	v_cndmask_b32_e32 v54, v41, v54, vcc
	v_pk_mul_f32 v[54:55], v[32:33], v[54:55]
	v_pk_mul_f32 v[40:41], v[56:57], v[40:41] op_sel_hi:[1,0]
	v_pk_fma_f32 v[6:7], v[6:7], v[34:35], v[54:55]
	v_pk_mul_f32 v[40:41], v[40:41], v[82:83]
	v_pk_mul_f32 v[6:7], v[6:7], s[94:95] op_sel_hi:[1,0]
	v_mov_b32_e32 v54, v40
	v_cvt_pk_bf16_f32 v7, v6, v7
	v_mov_b32_e32 v6, v40
	s_nop 1
	v_permlane32_swap_b32_e32 v6, v54
	v_mov_b32_e32 v55, v41
	v_mov_b32_e32 v60, v41
	v_cndmask_b32_e32 v54, v6, v54, vcc
	v_mul_f32_e32 v6, 0x4b800000, v86
	v_permlane32_swap_b32_e32 v55, v60
	v_cndmask_b32_e64 v6, v86, v6, s[4:5]
	v_cndmask_b32_e32 v55, v55, v60, vcc
	v_rsq_f32_e32 v60, v6
	v_pk_mul_f32 v[54:55], v[106:107], v[54:55]
	s_nop 0
	v_pk_fma_f32 v[40:41], v[40:41], v[38:39], v[54:55]
	s_nop 0
	v_pk_mul_f32 v[40:41], v[40:41], s[94:95] op_sel_hi:[1,0]
	s_nop 0
	v_cvt_pk_bf16_f32 v6, v40, v41
	v_mul_f32_e32 v40, 0x45800000, v60
	v_cndmask_b32_e64 v40, v60, v40, s[4:5]
	v_pk_mul_f32 v[54:55], v[56:57], v[40:41] op_sel_hi:[1,0]
	v_pk_mul_f32 v[56:57], v[58:59], v[40:41] op_sel_hi:[1,0]
	v_pk_mul_f32 v[54:55], v[54:55], v[104:105]
	v_pk_mul_f32 v[36:37], v[56:57], v[36:37]
	v_pk_mul_f32 v[50:51], v[50:51], v[40:41] op_sel_hi:[1,0]
	v_pk_mul_f32 v[52:53], v[52:53], v[40:41] op_sel_hi:[1,0]
	v_pk_mul_f32 v[46:47], v[46:47], v[40:41] op_sel_hi:[1,0]
	v_pk_mul_f32 v[48:49], v[48:49], v[40:41] op_sel_hi:[1,0]
	v_pk_mul_f32 v[42:43], v[42:43], v[40:41] op_sel_hi:[1,0]
	v_pk_mul_f32 v[40:41], v[44:45], v[40:41] op_sel_hi:[1,0]
	v_mov_b32_e32 v44, v54
	v_mov_b32_e32 v56, v54
	v_mov_b32_e32 v45, v55
	v_mov_b32_e32 v57, v55
	v_permlane32_swap_b32_e32 v44, v56
	s_nop 0
	v_permlane32_swap_b32_e32 v45, v57
	v_cndmask_b32_e32 v45, v45, v57, vcc
	v_cndmask_b32_e32 v44, v44, v56, vcc
	v_pk_mul_f32 v[38:39], v[38:39], v[54:55]
	v_mov_b32_e32 v54, v36
	v_pk_fma_f32 v[38:39], v[106:107], v[44:45], v[38:39]
	v_mov_b32_e32 v44, v36
	v_mov_b32_e32 v45, v37
	v_mov_b32_e32 v55, v37
	v_permlane32_swap_b32_e32 v44, v54
	s_nop 0
	v_permlane32_swap_b32_e32 v45, v55
	v_pk_mul_f32 v[50:51], v[50:51], v[74:75]
	v_cndmask_b32_e32 v45, v45, v55, vcc
	v_cndmask_b32_e32 v44, v44, v54, vcc
	v_pk_mul_f32 v[34:35], v[34:35], v[36:37]
	v_mov_b32_e32 v36, v50
	v_pk_fma_f32 v[32:33], v[32:33], v[44:45], v[34:35]
	v_mov_b32_e32 v34, v50
	v_mov_b32_e32 v35, v51
	v_mov_b32_e32 v37, v51
	v_permlane32_swap_b32_e32 v34, v36
	s_nop 0
	v_permlane32_swap_b32_e32 v35, v37
	v_cndmask_b32_e32 v35, v35, v37, vcc
	v_cndmask_b32_e32 v34, v34, v36, vcc
	v_pk_mul_f32 v[52:53], v[52:53], v[72:73]
	v_pk_mul_f32 v[28:29], v[28:29], v[34:35]
	v_mov_b32_e32 v34, v52
	v_pk_fma_f32 v[28:29], v[30:31], v[50:51], v[28:29]
	v_mov_b32_e32 v30, v52
	v_mov_b32_e32 v31, v53
	v_mov_b32_e32 v35, v53
	v_permlane32_swap_b32_e32 v30, v34
	s_nop 0
	v_permlane32_swap_b32_e32 v31, v35
	v_cndmask_b32_e32 v31, v31, v35, vcc
	v_cndmask_b32_e32 v30, v30, v34, vcc
	v_pk_mul_f32 v[46:47], v[46:47], v[70:71]
	v_pk_mul_f32 v[24:25], v[24:25], v[30:31]
	v_mov_b32_e32 v30, v46
	v_pk_fma_f32 v[24:25], v[52:53], v[26:27], v[24:25]
	v_mov_b32_e32 v26, v46
	v_mov_b32_e32 v27, v47
	v_mov_b32_e32 v31, v47
	v_permlane32_swap_b32_e32 v26, v30
	s_nop 0
	v_permlane32_swap_b32_e32 v27, v31
	v_cndmask_b32_e32 v27, v27, v31, vcc
	v_cndmask_b32_e32 v26, v26, v30, vcc
	v_pk_mul_f32 v[48:49], v[48:49], v[68:69]
	v_pk_mul_f32 v[20:21], v[20:21], v[26:27]
	v_mov_b32_e32 v26, v48
	v_pk_fma_f32 v[20:21], v[46:47], v[22:23], v[20:21]
	v_mov_b32_e32 v22, v48
	v_mov_b32_e32 v23, v49
	v_mov_b32_e32 v27, v49
	v_permlane32_swap_b32_e32 v22, v26
	s_nop 0
	v_permlane32_swap_b32_e32 v23, v27
	v_cndmask_b32_e32 v23, v23, v27, vcc
	v_cndmask_b32_e32 v22, v22, v26, vcc
	v_pk_mul_f32 v[42:43], v[42:43], v[66:67]
	v_pk_mul_f32 v[16:17], v[16:17], v[22:23]
	v_mov_b32_e32 v22, v42
	v_pk_fma_f32 v[16:17], v[48:49], v[18:19], v[16:17]
	v_mov_b32_e32 v18, v42
	v_mov_b32_e32 v19, v43
	v_mov_b32_e32 v23, v43
	v_permlane32_swap_b32_e32 v18, v22
	s_nop 0
	v_permlane32_swap_b32_e32 v19, v23
	v_cndmask_b32_e32 v19, v19, v23, vcc
	v_cndmask_b32_e32 v18, v18, v22, vcc
	v_pk_mul_f32 v[40:41], v[40:41], v[64:65]
	v_pk_mul_f32 v[12:13], v[12:13], v[18:19]
	v_pk_mul_f32 v[16:17], v[16:17], s[94:95] op_sel_hi:[1,0]
	v_pk_fma_f32 v[18:19], v[42:43], v[14:15], v[12:13]
	v_mov_b32_e32 v12, v40
	v_mov_b32_e32 v14, v40
	v_mov_b32_e32 v13, v41
	v_mov_b32_e32 v15, v41
	v_permlane32_swap_b32_e32 v12, v14
	s_nop 0
	v_permlane32_swap_b32_e32 v13, v15
	v_cndmask_b32_e32 v13, v13, v15, vcc
	v_cndmask_b32_e32 v12, v12, v14, vcc
	v_pk_mul_f32 v[12:13], v[62:63], v[12:13]
	v_pk_mul_f32 v[14:15], v[24:25], s[94:95] op_sel_hi:[1,0]
	v_pk_fma_f32 v[22:23], v[40:41], v[10:11], v[12:13]
	v_pk_mul_f32 v[10:11], v[38:39], s[94:95] op_sel_hi:[1,0]
	v_pk_mul_f32 v[12:13], v[32:33], s[94:95] op_sel_hi:[1,0]
	v_cvt_pk_bf16_f32 v10, v10, v11
	v_cvt_pk_bf16_f32 v11, v12, v13
	v_pk_mul_f32 v[12:13], v[28:29], s[94:95] op_sel_hi:[1,0]
	v_bfe_u32 v30, v79, 1, 3
	v_cvt_pk_bf16_f32 v12, v12, v13
	v_cvt_pk_bf16_f32 v13, v14, v15
	v_pk_mul_f32 v[14:15], v[20:21], s[94:95] op_sel_hi:[1,0]
	v_bitop3_b32 v30, v171, v30, 4 bitop3:0x36
	v_cvt_pk_bf16_f32 v14, v14, v15
	v_cvt_pk_bf16_f32 v15, v16, v17
	v_pk_mul_f32 v[16:17], v[18:19], s[94:95] op_sel_hi:[1,0]
	v_pk_mul_f32 v[18:19], v[22:23], s[94:95] op_sel_hi:[1,0]
	v_cvt_pk_bf16_f32 v16, v16, v17
	v_cvt_pk_bf16_f32 v17, v18, v19
	s_waitcnt vmcnt(0) lgkmcnt(0)
	s_barrier
; #define ATT_SB() __builtin_amdgcn_sched_barrier(0)
; #define ATT_DMA_K(t, sl) do { glds16(ksrc + (size_t)(t) * 64 * kpitch, (unsigned)__builtin_amdgcn_readfirstlane(kdst + (sl) * KSLOT)); \
;         if constexpr (DQK == 96) glds16(krsrc + (size_t)(t) * 64 * 32, (unsigned)__builtin_amdgcn_readfirstlane(krdst + (sl) * KSLOT)); } while (0)
; #define ATT_DMA_V(t, sl) do { glds16(vsrc + (size_t)(t) * 64, (unsigned)__builtin_amdgcn_readfirstlane(vdst + (sl) * VSLOT)); \
;         if constexpr (DV == 128) glds16(vsrc + (size_t)64 * NR + (size_t)(t) * 64, (unsigned)__builtin_amdgcn_readfirstlane(vdst + (sl) * VSLOT + 8192)); } while (0)
; #define ATT_KLOAD(sl) do { _Pragma("unroll") for (int kb_ = 0; kb_ < NKW; ++kb_) _Pragma("unroll") for (int ds_ = 0; ds_ < NDS; ++ds_) { \
;         if (ds_ < 2) kf[kb_ * NDS + ds_] = *(const LAS bf16x8*)(kp[ds_ & 1] + (sl) * KSLOT + (kb_ & 1) * 512 + (kb_ >> 1) * 4096); \
;         else kf[kb_ * NDS + ds_] = *(const LAS bf16x8*)(krp + (sl) * KSLOT + (kb_ & 1) * 256 + (kb_ >> 1) * 2048); } } while (0)
; #define ATT_QK() do { _Pragma("unroll") for (int kb_ = 0; kb_ < NKW; ++kb_) _Pragma("unroll") for (int ds_ = 0; ds_ < NDS; ++ds_) _Pragma("unroll") for (int qb_ = 0; qb_ < NQB; ++qb_) \
;         c[kb_][qb_] = __builtin_amdgcn_mfma_f32_16x16x32_bf16(kf[kb_ * NDS + ds_], qf[qb_ * NDS + ds_], ds_ == 0 ? zero4 : c[kb_][qb_], 0, 0, 0); } while (0)
; #define ATT_EXP() do { _Pragma("unroll") for (int kb_ = 0; kb_ < NKW; ++kb_) _Pragma("unroll") for (int qb_ = 0; qb_ < NQB; ++qb_) _Pragma("unroll") for (int i_ = 0; i_ < 4; ++i_) \
;         c[kb_][qb_][i_] = __builtin_amdgcn_exp2f(c[kb_][qb_][i_]); } while (0)
; template <int DQK, int DV, bool LEAD> ...
;     ...
;     bf16x8 kf[NKW * NDS], vf[NVF];
;     ATT_KLOAD(0);
;     asm volatile("s_waitcnt lgkmcnt(0)\n\ts_barrier" ::: "memory");
;     float lsum[NQB];
; #pragma unroll
;     for (int qb = 0; qb < NQB; ++qb) lsum[qb] = 0.f;
;     const f32x4 zero4 = {0.f, 0.f, 0.f, 0.f};
;     f32x4 o[NDB][NQB], c[NKW][NQB]; u32x4 pw[4];
; #pragma unroll
;     for (int i = 0; i < NDB; ++i)
; #pragma unroll
;         for (int qb = 0; qb < NQB; ++qb) o[i][qb] = zero4;
;     ATT_DMA_K(3, 0); ATT_DMA_V(1, 1);
;     ATT_QK(); ATT_SB();
;     ATT_KLOAD(1); ATT_SB();
;     if constexpr (LEAD) { ATT_EXP(); ATT_SUMPACK(); }
;     wait_bar<NDMA>();
;     int s_prev = 0, s_cur = 1, s_next = 2;
	ds_read_b128 v[18:21], v173
	ds_read_b128 v[22:25], v173 offset:512
	v_lshlrev_b32_e32 v54, 4, v30
	v_add_u32_e32 v176, v81, v54
	s_waitcnt lgkmcnt(1)
	v_mfma_f32_16x16x32_bf16 v[26:29], v[18:21], v[6:9], 0
	ds_read_b128 v[30:33], v176
	ds_read_b128 v[34:37], v176 offset:512
	v_add_u32_e32 v55, 0, v175
	v_add_u32_e32 v178, v55, v80
	v_mfma_f32_16x16x32_bf16 v[18:21], v[18:21], v[10:13], 0
	v_add_u32_e32 v177, v55, v54
	s_waitcnt lgkmcnt(1)
	v_mfma_f32_16x16x32_bf16 v[26:29], v[30:33], v[2:5], v[26:29]
	v_mfma_f32_16x16x32_bf16 v[18:21], v[30:33], v[14:17], v[18:21]
	v_mfma_f32_16x16x32_bf16 v[30:33], v[22:25], v[6:9], 0
	v_mfma_f32_16x16x32_bf16 v[22:25], v[22:25], v[10:13], 0
	s_waitcnt lgkmcnt(0)
	v_mfma_f32_16x16x32_bf16 v[30:33], v[34:37], v[2:5], v[30:33]
	v_mfma_f32_16x16x32_bf16 v[22:25], v[34:37], v[14:17], v[22:25]
	ds_read_b128 v[34:37], v173 offset:4096
	ds_read_b128 v[38:41], v173 offset:4608
	ds_read_b128 v[46:49], v176 offset:4096
	ds_read_b128 v[50:53], v176 offset:4608
	s_waitcnt lgkmcnt(3)
	v_mfma_f32_16x16x32_bf16 v[42:45], v[34:37], v[6:9], 0
	s_waitcnt lgkmcnt(0)
	s_barrier
	v_mfma_f32_16x16x32_bf16 v[34:37], v[34:37], v[10:13], 0
	s_waitcnt lgkmcnt(1)
	v_mfma_f32_16x16x32_bf16 v[58:61], v[46:49], v[14:17], v[34:37]
	v_mfma_f32_16x16x32_bf16 v[34:37], v[38:41], v[6:9], 0
	v_mfma_f32_16x16x32_bf16 v[38:41], v[38:41], v[10:13], 0
	v_mfma_f32_16x16x32_bf16 v[42:45], v[46:49], v[2:5], v[42:45]
	v_lshl_add_u64 v[46:47], v[162:163], 0, s[96:97]
	s_mov_b32 s4, m0
	s_mov_b32 m0, s31
	s_nop 0
	global_load_lds_dwordx4 v[46:47], off
	s_mov_b32 m0, s4
	v_lshl_add_u64 v[46:47], v[164:165], 0, s[66:67]
	s_add_i32 s4, s40, 0x4000
	s_mov_b32 s5, m0
	s_mov_b32 m0, s4
	s_nop 0
	global_load_lds_dwordx4 v[46:47], off
	s_mov_b32 m0, s5
	s_mov_b64 s[4:5], 0x840080
	s_waitcnt lgkmcnt(0)
	v_mfma_f32_16x16x32_bf16 v[74:77], v[50:53], v[2:5], v[34:37]
	v_lshl_add_u64 v[46:47], v[164:165], 0, s[4:5]
	s_add_i32 s4, s40, 0x6000
	s_mov_b32 s5, m0
	s_mov_b32 m0, s4
	s_nop 0
	global_load_lds_dwordx4 v[46:47], off
	s_mov_b32 m0, s5
	v_mfma_f32_16x16x32_bf16 v[78:81], v[50:53], v[14:17], v[38:41]
	ds_read_b128 v[34:37], v173 offset:8192
	s_nop 1
	ds_read_b128 v[38:41], v173 offset:8704
	ds_read_b128 v[46:49], v176 offset:8192
	ds_read_b128 v[50:53], v176 offset:8704
	ds_read_b128 v[54:57], v173 offset:12288
	ds_read_b128 v[62:65], v173 offset:12800
	ds_read_b128 v[66:69], v176 offset:12288
	ds_read_b128 v[70:73], v176 offset:12800
	v_exp_f32_e32 v26, v26
	v_exp_f32_e32 v27, v27
	v_exp_f32_e32 v28, v28
	v_exp_f32_e32 v29, v29
	v_exp_f32_e32 v86, v18
	v_exp_f32_e32 v87, v19
	v_exp_f32_e32 v20, v20
	v_exp_f32_e32 v21, v21
	v_exp_f32_e32 v30, v30
	v_exp_f32_e32 v22, v22
	v_add_f32_e32 v18, v26, v27
	v_add_f32_e32 v19, v28, v29
	v_exp_f32_e32 v31, v31
	v_exp_f32_e32 v23, v23
	v_add_f32_e32 v18, v18, v19
	v_add_f32_e32 v19, v86, v87
	v_add_f32_e32 v82, v20, v21
	v_add_f32_e32 v19, v19, v82
	v_exp_f32_e32 v32, v32
	v_exp_f32_e32 v24, v24
	v_add_f32_e32 v18, v18, v30
	v_add_f32_e32 v19, v19, v22
	v_exp_f32_e32 v33, v33
	v_exp_f32_e32 v25, v25
	v_add_f32_e32 v18, v31, v18
	v_add_f32_e32 v19, v23, v19
	v_exp_f32_e32 v42, v42
	v_exp_f32_e32 v58, v58
	v_add_f32_e32 v18, v32, v18
	v_add_f32_e32 v19, v24, v19
	v_exp_f32_e32 v43, v43
	v_exp_f32_e32 v59, v59
	v_add_f32_e32 v18, v33, v18
	v_add_f32_e32 v19, v25, v19
	v_exp_f32_e32 v44, v44
	v_exp_f32_e32 v60, v60
	v_add_f32_e32 v18, v42, v18
	v_add_f32_e32 v19, v58, v19
	v_exp_f32_e32 v45, v45
	v_exp_f32_e32 v61, v61
	v_add_f32_e32 v18, v43, v18
	v_add_f32_e32 v19, v59, v19
	v_exp_f32_e32 v74, v74
	v_exp_f32_e32 v78, v78
	v_add_f32_e32 v18, v44, v18
	v_add_f32_e32 v19, v60, v19
	v_exp_f32_e32 v75, v75
	v_exp_f32_e32 v79, v79
	v_add_f32_e32 v18, v45, v18
	v_add_f32_e32 v19, v61, v19
	v_exp_f32_e32 v76, v76
	v_exp_f32_e32 v80, v80
	v_add_f32_e32 v18, v74, v18
	v_add_f32_e32 v19, v78, v19
	v_exp_f32_e32 v77, v77
	v_exp_f32_e32 v81, v81
	v_add_f32_e32 v18, v75, v18
	v_add_f32_e32 v19, v79, v19
	s_mov_b32 s4, 1
	v_add_f32_e32 v18, v76, v18
	v_add_f32_e32 v82, v80, v19
	v_cvt_pk_bf16_f32 v83, v28, v29
	v_add_f32_e32 v19, v77, v18
	v_add_f32_e32 v18, v81, v82
	s_waitcnt vmcnt(3) lgkmcnt(0)
	s_barrier
	s_cmp_lg_u32 s4, 0
	v_pk_add_f32 v[168:169], v[18:19], 0 op_sel_hi:[1,0]
	v_mov_b32_e32 v18, 0
	v_cvt_pk_bf16_f32 v82, v26, v27
	v_cvt_pk_bf16_f32 v84, v30, v31
	v_cvt_pk_bf16_f32 v85, v32, v33
	v_cvt_pk_bf16_f32 v94, v86, v87
	v_cvt_pk_bf16_f32 v95, v20, v21
	v_cvt_pk_bf16_f32 v96, v22, v23
	v_cvt_pk_bf16_f32 v97, v24, v25
	v_cvt_pk_bf16_f32 v98, v42, v43
	v_cvt_pk_bf16_f32 v99, v44, v45
	v_cvt_pk_bf16_f32 v100, v74, v75
	v_cvt_pk_bf16_f32 v101, v76, v77
	v_cvt_pk_bf16_f32 v102, v58, v59
	v_cvt_pk_bf16_f32 v103, v60, v61
	v_cvt_pk_bf16_f32 v104, v78, v79
	v_cvt_pk_bf16_f32 v105, v80, v81
	s_cselect_b64 s[4:5], -1, 0
	s_mov_b32 s30, 2
	v_mov_b32_e32 v19, v18
	v_mov_b32_e32 v20, v18
	v_mov_b32_e32 v21, v18
	v_mov_b32_e32 v22, v18
	v_mov_b32_e32 v23, v18
	v_mov_b32_e32 v24, v18
	v_mov_b32_e32 v25, v18
	v_mov_b32_e32 v26, v18
	v_mov_b32_e32 v27, v18
	v_mov_b32_e32 v28, v18
	v_mov_b32_e32 v29, v18
	v_mov_b32_e32 v30, v18
	v_mov_b32_e32 v31, v18
	v_mov_b32_e32 v32, v18
	v_mov_b32_e32 v33, v18
	v_mov_b32_e32 v42, v18
	v_mov_b32_e32 v43, v18
	v_mov_b32_e32 v44, v18
	v_mov_b32_e32 v45, v18
	v_mov_b32_e32 v58, v18
	v_mov_b32_e32 v59, v18
	v_mov_b32_e32 v60, v18
	v_mov_b32_e32 v61, v18
	v_mov_b32_e32 v74, v18
	v_mov_b32_e32 v75, v18
	v_mov_b32_e32 v76, v18
	v_mov_b32_e32 v77, v18
	v_mov_b32_e32 v78, v18
	v_mov_b32_e32 v79, v18
	v_mov_b32_e32 v80, v18
	v_mov_b32_e32 v81, v18
	v_mov_b32_e32 v86, v18
	v_mov_b32_e32 v87, v18
	v_mov_b32_e32 v88, v18
	v_mov_b32_e32 v89, v18
	v_mov_b32_e32 v90, v18
	v_mov_b32_e32 v91, v18
	v_mov_b32_e32 v92, v18
	v_mov_b32_e32 v93, v18
	v_mov_b32_e32 v106, v18
	v_mov_b32_e32 v107, v18
	v_mov_b32_e32 v108, v18
	v_mov_b32_e32 v109, v18
	v_mov_b32_e32 v110, v18
	v_mov_b32_e32 v111, v18
	v_mov_b32_e32 v112, v18
	v_mov_b32_e32 v113, v18
	v_mov_b32_e32 v114, v18
	v_mov_b32_e32 v115, v18
	v_mov_b32_e32 v116, v18
	v_mov_b32_e32 v117, v18
	v_mov_b32_e32 v118, v18
	v_mov_b32_e32 v119, v18
	v_mov_b32_e32 v120, v18
	v_mov_b32_e32 v121, v18
	v_mov_b32_e32 v122, v18
	v_mov_b32_e32 v123, v18
	v_mov_b32_e32 v124, v18
	v_mov_b32_e32 v125, v18
	v_mov_b32_e32 v126, v18
	v_mov_b32_e32 v127, v18
	v_mov_b32_e32 v128, v18
	v_mov_b32_e32 v129, v18

; #define LAS __attribute__((address_space(3)))
; template <int DQK, int DV, bool LEAD> ...
;     ...
;     const int tid = tid_, lane = tid & 63, q16 = lane & 15, g4 = lane >> 4, hi = lane >> 5; const int wid = __builtin_amdgcn_readfirstlane(tid >> 6);
;     const int kg = KS ? (wid >> 2) : 0, qoff = KS ? (wid & 3) * 64 : wid * 32;
;     const unsigned lds0 = (unsigned)(uintptr_t)shm;
;     const int krow_l = wid * 8 + (lane >> 3);
;     const int kc_l = (lane & 7) ^ (((krow_l >> 1) & 1) | (((krow_l >> 3) & 1) << 1) | (((krow_l >> 4) & 1) << 2));
;     const int vc_l = (lane & 7) ^ ((krow_l >> 1) & 7);
;     const bf16_t* ksrc = K + (size_t)(krow0 + krow_l) * kpitch + kc_l * 8;
;     const int rrow_l = (wid & 3) * 16 + (lane >> 2), rc_l = (lane & 3) ^ (((rrow_l >> 4) & 1) << 1);
;     const bf16_t* krsrc = (DQK == 96) ? KR + (size_t)(krow0 + rrow_l) * 32 + rc_l * 8 : nullptr;
;     const bf16_t* vsrc = Vt + (size_t)krow_l * NR + krow0 + vc_l * 8;
;     const unsigned kdst = lds0 + KOFF + wid * 1024, krdst = lds0 + KOFF + 8192 + (wid & 3) * 1024, vdst = lds0 + VOFF + wid * 1024;
;     ...
;     const int kr0 = 8 * (q16 >> 2) + (q16 & 3);
;     const int fk = ((kr0 >> 1) & 1) | (((kr0 >> 3) & 1) << 1) | (((kr0 >> 4) & 1) << 2);
;     const LAS unsigned char* kp[2]; const LAS unsigned char* vp[2];
; #pragma unroll
;     for (int ds = 0; ds < 2; ++ds) kp[ds] = shm + KOFF + kr0 * 128 + ((((ds << 2) | g4) ^ fk) << 4) + kg * 4096;
;     const LAS unsigned char* krp = shm + KOFF + 8192 + kr0 * 64 + ((g4 ^ (((kr0 >> 4) & 1) << 1)) << 4) + kg * 2048;
; #pragma unroll
;     for (int s_ = 0; s_ < 2; ++s_) vp[s_] = shm + VOFF + q16 * 128 + ((((s_ << 2) | g4) ^ ((q16 >> 1) & 7)) << 4);
;     const LAS unsigned char* vpk = kg ? vp[1] : vp[0];
;     ...
;     ATT_DMA_K(0, 0); ATT_DMA_V(0, 0); ATT_DMA_K(1, 1); ATT_DMA_K(2, 2);
;     bf16x8 qf[NQB * NDS];
;     {
; __global__ void __launch_bounds__(NWAVES * 64, 2) mega_fwd(Args args_) {
;     ...
;             for (int i = 0;; ++i) { const int u = i * F.G + F.vcu; if (u >= 2048) break; const int sid = u >> 5, qb = u & 31, b = sid >> 3, kvh = (sid >> 2) & 1, g = sid & 3;
;                 att::attn_unit<64, 64>(QK + 1024 + kvh * 256 + g * 64, QKW, QK + 1536 + kvh * 64, QKW, nullptr, VTE + (size_t)(512 + kvh * 64) * NR, H + 512 + kvh * 256 + g * 64, 1024, b * TPS + qb * 256, b * TPS, 132, F.lds, IN(a, I_BQK) + j * 128, (const f32x2*)(ws + WS_ROPE64), qb * 256); }
.LBB0_955:
	s_bfe_u32 s46, s4, 0x10007
	s_lshr_b32 s5, s4, 8
	s_lshl_b32 s6, s46, 9
	s_add_u32 s6, s15, s6
	s_addc_u32 s7, s17, 0
	s_lshl_b32 s16, s4, 1
	s_and_b32 s16, s16, 0xc0
	s_lshl_b32 s43, s16, 1
	s_add_u32 s28, s6, s43
	s_addc_u32 s29, s7, 0
	s_lshl_b32 s6, s46, 7
	s_add_u32 s36, s24, s6
	s_addc_u32 s37, s25, 0
	s_mul_i32 s6, s46, 0x840000
	s_add_u32 s6, s10, s6
	s_addc_u32 s7, s11, 0
	s_add_u32 s40, s6, 0x4200000
	s_addc_u32 s41, s7, 0
	s_mov_b64 s[6:7], s[0:1]
	s_load_dwordx2 s[6:7], s[6:7], 0x60
	s_lshl_b32 s47, s4, 8
	s_mul_i32 s44, s5, 0x2100
	s_and_b32 s4, s47, 0x1f00
	s_add_i32 s48, s44, s4
	s_waitcnt lgkmcnt(0)
	s_add_u32 s26, s6, s22
	s_addc_u32 s27, s7, s23
	v_readfirstlane_b32 s4, v0
	s_cmpk_gt_u32 s4, 0xff
	s_mov_b64 s[4:5], -1
	s_cbranch_scc0 .LBB0_962
	v_mov_b32_e32 v162, v0
	s_ashr_i32 s45, s44, 31
	v_readfirstlane_b32 s6, v162
	s_ashr_i32 s4, s6, 6
	v_bfe_u32 v2, v162, 3, 3
	v_lshl_or_b32 v6, s4, 3, v2
	s_lshl_b32 s5, s4, 1
	s_lshr_b32 s7, s6, 5
	v_ashrrev_i32_e32 v3, 1, v6
	s_and_b32 s5, s5, 2
	s_and_b32 s7, s7, 4
	v_and_b32_e32 v2, 7, v162
	v_and_b32_e32 v4, 1, v3
	s_or_b32 s5, s5, s7
	v_bitop3_b32 v7, s5, v2, v4 bitop3:0x36
	v_xor_b32_e32 v8, v3, v162
	v_add_u32_e32 v4, s44, v6
	v_mov_b64_e32 v[2:3], s[36:37]
	s_and_b32 s49, s4, 3
	s_lshl_b32 s50, s4, 10
	v_mad_i64_i32 v[2:3], s[4:5], v4, s92, v[2:3]
	v_mov_b64_e32 v[4:5], s[40:41]
	v_lshlrev_b32_e32 v194, 4, v7
	v_mad_i64_i32 v[4:5], s[4:5], v6, s91, v[4:5]
	v_lshl_add_u64 v[164:165], v[2:3], 0, v[194:195]
	v_lshlrev_b32_e32 v2, 4, v8
	s_add_i32 s50, s50, 0
	v_lshl_add_u64 v[4:5], s[44:45], 1, v[4:5]
	v_and_b32_e32 v194, 0x70, v2
	s_mov_b32 s4, m0
	s_mov_b32 m0, s50
	s_nop 0
	global_load_lds_dwordx4 v[164:165], off
	s_mov_b32 m0, s4
	v_lshl_add_u64 v[166:167], v[4:5], 0, v[194:195]
	s_add_i32 s45, s50, 0x9000
	s_mov_b32 s4, m0
	s_mov_b32 m0, s45
	s_nop 0
	global_load_lds_dwordx4 v[166:167], off
	s_mov_b32 m0, s4
	s_mov_b64 s[4:5], 0x38000
	v_and_b32_e32 v1, 15, v162
	s_lshl_b32 s7, s49, 6
	v_lshl_add_u64 v[2:3], v[164:165], 0, s[4:5]
	s_add_i32 s4, s50, 0x2000
	s_mov_b32 s5, m0
	s_mov_b32 m0, s4
	s_nop 0
	global_load_lds_dwordx4 v[2:3], off
	s_mov_b32 m0, s5
	v_lshlrev_b32_e32 v163, 7, v1
	s_mov_b64 s[4:5], 0x70000
	v_or_b32_e32 v1, s7, v1
	v_and_b32_e32 v194, 48, v162
	v_lshrrev_b32_e32 v34, 1, v162
	v_lshl_add_u64 v[2:3], v[164:165], 0, s[4:5]
	s_add_i32 s4, s50, 0x4000
	v_or_b32_e32 v1, s48, v1
	v_lshl_add_u64 v[6:7], s[28:29], 0, v[194:195]
	s_mov_b32 s5, m0
	s_mov_b32 m0, s4
	s_nop 0
	global_load_lds_dwordx4 v[2:3], off
	s_mov_b32 m0, s5
	v_and_b32_e32 v35, 8, v34
	v_mad_i64_i32 v[8:9], s[4:5], v1, s92, v[6:7]
	v_or_b32_e32 v10, 16, v1
	v_or_b32_e32 v14, 32, v1
	v_or_b32_e32 v1, 48, v1
	v_lshl_or_b32 v194, v35, 3, v163
	v_mad_i64_i32 v[24:25], s[4:5], v10, s92, v[6:7]
	v_mad_i64_i32 v[26:27], s[4:5], v14, s92, v[6:7]
	v_mad_i64_i32 v[30:31], s[4:5], v1, s92, v[6:7]
	v_lshl_add_u64 v[22:23], s[8:9], 0, v[194:195]
	s_mov_b64 s[4:5], 0x1800
	v_lshl_add_u64 v[28:29], v[22:23], 0, s[60:61]
	v_lshl_add_u64 v[32:33], v[22:23], 0, s[4:5]
	s_movk_i32 s4, 0x1000
	global_load_dwordx4 v[72:75], v[8:9], off offset:64 nt
	global_load_dwordx4 v[2:5], v194, s[8:9] offset:48
	global_load_dwordx4 v[128:131], v[24:25], off offset:64 nt
	global_load_dwordx4 v[10:13], v194, s[8:9] offset:2096
	global_load_dwordx4 v[152:155], v[26:27], off offset:64 nt
	global_load_dwordx4 v[68:71], v[28:29], off offset:48
	global_load_dwordx4 v[176:179], v[30:31], off offset:64 nt
	global_load_dwordx4 v[14:17], v[32:33], off offset:48
	global_load_dwordx4 v[102:105], v194, s[8:9] offset:32
	global_load_dwordx4 v[94:97], v194, s[8:9] offset:2080
	global_load_dwordx4 v[64:67], v[28:29], off offset:32
	global_load_dwordx4 v[18:21], v[32:33], off offset:32
	global_load_dwordx4 v[110:113], v[8:9], off
	s_nop 0
	global_load_dwordx4 v[6:9], v194, s[8:9]
	global_load_dwordx4 v[106:109], v[24:25], off
	global_load_dwordx4 v[98:101], v194, s[8:9] offset:16
	global_load_dwordx4 v[82:85], v[26:27], off
	global_load_dwordx4 v[86:89], v194, s[8:9] offset:2064
	v_add_co_u32_e32 v26, vcc, s4, v22
	v_lshlrev_b32_e32 v22, 1, v162
	s_nop 0
	v_addc_co_u32_e32 v27, vcc, 0, v23, vcc
	v_and_b32_e32 v23, 3, v162
	global_load_dwordx4 v[56:59], v[26:27], off
	global_load_dwordx4 v[78:81], v[30:31], off
	global_load_dwordx4 v[60:63], v[28:29], off offset:16
	global_load_dwordx4 v[90:93], v194, s[8:9] offset:2048
	v_and_or_b32 v28, v22, 24, v23
	global_load_dwordx4 v[22:25], v[32:33], off offset:16
	s_lshl_b32 s4, s6, 4
	s_and_b32 s4, s4, 0xfffff000
	s_add_i32 s4, s4, 0
	v_lshl_add_u32 v170, v28, 7, s4
	s_or_b32 s4, s7, s47
	v_bfe_u32 v169, v162, 4, 2
	s_lshr_b32 s4, s4, 2
	v_bitop3_b32 v28, v169, v34, 7 bitop3:0x78
	s_and_b32 s4, s4, 0x7f0
	v_lshlrev_b32_e32 v168, 4, v28
	v_or_b32_e32 v28, s4, v35
	v_lshlrev_b32_e32 v28, 3, v28
	v_lshlrev_b32_e32 v76, 5, v169
	global_load_dwordx4 v[32:35], v28, s[8:9] offset:48
	global_load_dwordx4 v[36:39], v28, s[8:9] offset:32
	global_load_dwordx4 v[40:43], v28, s[8:9] offset:16
	global_load_dwordx4 v[44:47], v28, s[8:9]
	s_nop 0
	global_load_dwordx4 v[28:31], v[26:27], off offset:2048
	global_load_dwordx4 v[48:51], v76, s[26:27] offset:144
	global_load_dwordx4 v[52:55], v76, s[26:27] offset:128
	v_and_b32_e32 v1, 63, v162
	v_cmp_gt_u32_e32 vcc, 32, v1
	s_mov_b32 s4, 0x358637bd
	s_mov_b32 s12, 0x3c800000
	v_add_u32_e32 v174, v170, v168
	s_cmpk_lt_u32 s6, 0x100
	s_mov_b32 s51, 1
	s_mov_b32 s16, 2
	s_waitcnt vmcnt(22)
	v_cndmask_b32_e64 v115, v17, -v17, vcc
	v_cndmask_b32_e64 v114, v15, -v15, vcc
	v_mov_b32_e32 v15, v16
	s_waitcnt vmcnt(20)
; template <int DQK, int DV, bool LEAD> ...
;     ...
;           float x[NDS][8];
; #pragma unroll
;           for (int ds = 0; ds < NDS; ++ds)
; #pragma unroll
;               for (int j = 0; j < 8; ++j) x[ds][j] = __uint_as_float(((unsigned)(unsigned short)raw[ds][j]) << 16);
;           const int tq = tq0 + qoff + qb * 16 + q16, prow = (tq >> 6) & 127, pcol = tq & 63;
;           float sn = 0.f;
; #pragma unroll
;           for (int ds = 0; ds < 2; ++ds)
; #pragma unroll
;               for (int j = 0; j < 8; ++j) sn += x[ds][j] * x[ds][j];
;           sn = lanes4_sum(sn);
	v_cndmask_b32_e64 v135, v97, -v97, vcc
	v_cndmask_b32_e64 v134, v95, -v95, vcc
	v_cndmask_b32_e64 v144, v3, -v3, vcc
	v_mov_b32_e32 v3, v4
	v_cndmask_b32_e64 v27, v13, -v13, vcc
	v_cndmask_b32_e64 v26, v11, -v11, vcc
	v_and_b32_e32 v117, 0xffff0000, v179
	v_lshlrev_b32_e32 v116, 16, v179
	s_waitcnt vmcnt(17)
	v_and_b32_e32 v179, 0xffff0000, v110
	v_mov_b32_e32 v11, v12
	v_cndmask_b32_e64 v13, v105, -v105, vcc
	v_cndmask_b32_e64 v12, v103, -v103, vcc
	v_mov_b32_e32 v103, v104
	v_cndmask_b32_e64 v105, v67, -v67, vcc
	v_cndmask_b32_e64 v104, v65, -v65, vcc
	v_mov_b32_e32 v65, v66
	v_and_b32_e32 v67, 0xffff0000, v178
	v_lshlrev_b32_e32 v66, 16, v178
	v_lshlrev_b32_e32 v178, 16, v110
	v_mul_f32_e32 v4, v179, v179
	v_cndmask_b32_e64 v145, v5, -v5, vcc
	v_mov_b32_e32 v95, v96
	v_cndmask_b32_e64 v17, v21, -v21, vcc
	v_cndmask_b32_e64 v16, v19, -v19, vcc
	v_mov_b32_e32 v19, v20
	v_and_b32_e32 v97, 0xffff0000, v177
	v_lshlrev_b32_e32 v96, 16, v177
	s_waitcnt vmcnt(7)
	v_cndmask_b32_e64 v21, v25, -v25, vcc
	v_cndmask_b32_e64 v20, v23, -v23, vcc
	v_mov_b32_e32 v23, v24
	v_cndmask_b32_e64 v25, v93, -v93, vcc
	v_cndmask_b32_e64 v24, v91, -v91, vcc
	v_mov_b32_e32 v91, v92
	v_and_b32_e32 v93, 0xffff0000, v176
	v_lshlrev_b32_e32 v92, 16, v176
	v_and_b32_e32 v177, 0xffff0000, v111
	v_lshlrev_b32_e32 v176, 16, v111
	v_pk_fma_f32 v[4:5], v[178:179], v[178:179], v[4:5] op_sel_hi:[1,1,0]
	v_and_b32_e32 v149, 0xffff0000, v75
	v_lshlrev_b32_e32 v148, 16, v75
	v_cndmask_b32_e64 v119, v71, -v71, vcc
	v_cndmask_b32_e64 v118, v69, -v69, vcc
	v_mov_b32_e32 v69, v70
	v_and_b32_e32 v151, 0xffff0000, v74
	v_lshlrev_b32_e32 v150, 16, v74
	v_and_b32_e32 v157, 0xffff0000, v73
	v_lshlrev_b32_e32 v156, 16, v73
	v_and_b32_e32 v161, 0xffff0000, v72
	v_lshlrev_b32_e32 v160, 16, v72
	global_load_dwordx4 v[70:73], v76, s[26:27] offset:16
	s_nop 0
	global_load_dwordx4 v[74:77], v76, s[26:27]
	v_pk_fma_f32 v[4:5], v[176:177], v[176:177], v[4:5]
	v_mul_f32_e32 v110, v177, v177
	v_and_b32_e32 v173, 0xffff0000, v112
	v_lshlrev_b32_e32 v172, 16, v112
	v_pk_add_f32 v[4:5], v[110:111], v[4:5] op_sel_hi:[0,1]
	v_pk_fma_f32 v[4:5], v[172:173], v[172:173], v[4:5]
	v_mul_f32_e32 v110, v173, v173
	v_cndmask_b32_e64 v159, v9, -v9, vcc
	v_cndmask_b32_e64 v158, v7, -v7, vcc
	v_mov_b32_e32 v7, v8
	v_and_b32_e32 v9, 0xffff0000, v113
	v_lshlrev_b32_e32 v8, 16, v113
	v_pk_add_f32 v[4:5], v[110:111], v[4:5] op_sel_hi:[0,1]
	v_pk_fma_f32 v[4:5], v[8:9], v[8:9], v[4:5]
	v_mul_f32_e32 v110, v9, v9
	v_pk_add_f32 v[4:5], v[110:111], v[4:5] op_sel_hi:[0,1]
	v_pk_fma_f32 v[4:5], v[160:161], v[160:161], v[4:5]
	v_mul_f32_e32 v110, v161, v161
	v_pk_add_f32 v[4:5], v[110:111], v[4:5] op_sel_hi:[0,1]
	v_pk_fma_f32 v[4:5], v[156:157], v[156:157], v[4:5]
	v_mul_f32_e32 v110, v157, v157
	v_pk_add_f32 v[4:5], v[110:111], v[4:5] op_sel_hi:[0,1]
	v_pk_fma_f32 v[4:5], v[150:151], v[150:151], v[4:5]
	v_mul_f32_e32 v110, v151, v151
	v_pk_add_f32 v[4:5], v[110:111], v[4:5] op_sel_hi:[0,1]
	v_pk_fma_f32 v[4:5], v[148:149], v[148:149], v[4:5]
	v_mul_f32_e32 v110, v149, v149
	v_pk_add_f32 v[4:5], v[110:111], v[4:5] op_sel_hi:[0,1]
	v_mov_b32_e32 v5, v4
	s_nop 1
	v_permlane16_swap_b32_e32 v4, v5
	v_add_f32_e32 v5, v4, v5
	v_and_b32_e32 v127, 0xffff0000, v153
	v_lshlrev_b32_e32 v126, 16, v153
	v_and_b32_e32 v147, 0xffff0000, v107
	v_lshlrev_b32_e32 v146, 16, v107
	v_mov_b32_e32 v107, v5
	v_and_b32_e32 v153, 0xffff0000, v106
	v_and_b32_e32 v133, 0xffff0000, v131
	v_lshlrev_b32_e32 v132, 16, v131
	v_and_b32_e32 v137, 0xffff0000, v130
	v_lshlrev_b32_e32 v136, 16, v130
	v_and_b32_e32 v131, 0xffff0000, v152
	v_lshlrev_b32_e32 v130, 16, v152
	v_permlane32_swap_b32_e32 v5, v107
	v_lshlrev_b32_e32 v152, 16, v106
	v_mul_f32_e32 v4, v153, v153
	v_pk_fma_f32 v[110:111], v[152:153], v[152:153], v[4:5] op_sel_hi:[1,1,0]
	v_mul_f32_e32 v4, v147, v147
	v_pk_fma_f32 v[110:111], v[146:147], v[146:147], v[110:111]
	v_and_b32_e32 v113, 0xffff0000, v108
	v_lshlrev_b32_e32 v112, 16, v108
	v_pk_add_f32 v[110:111], v[4:5], v[110:111] op_sel_hi:[0,1]
	v_pk_fma_f32 v[110:111], v[112:113], v[112:113], v[110:111]
	v_mul_f32_e32 v4, v113, v113
	v_and_b32_e32 v143, 0xffff0000, v109
	v_lshlrev_b32_e32 v142, 16, v109
	v_pk_add_f32 v[110:111], v[4:5], v[110:111] op_sel_hi:[0,1]
	v_pk_fma_f32 v[110:111], v[142:143], v[142:143], v[110:111]
	v_mul_f32_e32 v4, v143, v143
	v_cndmask_b32_e64 v125, v63, -v63, vcc
	v_cndmask_b32_e64 v124, v61, -v61, vcc
	v_mov_b32_e32 v61, v62
	v_and_b32_e32 v63, 0xffff0000, v128
	v_lshlrev_b32_e32 v62, 16, v128
	v_pk_add_f32 v[110:111], v[4:5], v[110:111] op_sel_hi:[0,1]
	v_pk_fma_f32 v[110:111], v[62:63], v[62:63], v[110:111]
	v_mul_f32_e32 v4, v63, v63
	v_and_b32_e32 v141, 0xffff0000, v129
	v_lshlrev_b32_e32 v140, 16, v129
	v_pk_add_f32 v[110:111], v[4:5], v[110:111] op_sel_hi:[0,1]
	v_pk_fma_f32 v[110:111], v[140:141], v[140:141], v[110:111]
	v_mul_f32_e32 v4, v141, v141
	v_pk_add_f32 v[110:111], v[4:5], v[110:111] op_sel_hi:[0,1]
	v_pk_fma_f32 v[110:111], v[136:137], v[136:137], v[110:111]
	v_mul_f32_e32 v4, v137, v137
	v_pk_add_f32 v[110:111], v[4:5], v[110:111] op_sel_hi:[0,1]
	v_pk_fma_f32 v[110:111], v[132:133], v[132:133], v[110:111]
	v_mul_f32_e32 v4, v133, v133
	v_pk_add_f32 v[110:111], v[4:5], v[110:111] op_sel_hi:[0,1]
	v_mov_b32_e32 v4, v110
	s_nop 1
	v_permlane16_swap_b32_e32 v110, v4
	v_add_f32_e32 v4, v110, v4
	v_mov_b32_e32 v106, v4
	s_nop 1
	v_permlane32_swap_b32_e32 v4, v106
	v_pk_add_f32 v[4:5], v[4:5], v[106:107]
	v_mov_b64_e32 v[110:111], s[4:5]
	v_pk_fma_f32 v[180:181], v[4:5], s[12:13], v[110:111] op_sel_hi:[1,0,0]
	s_waitcnt vmcnt(5)
; template <int DQK, int DV, bool LEAD> ...
;     ...
;           const float rn = rsqrtf(sn * (1.f / 64.f) + EPS);
; #pragma unroll
;           for (int ds = 0; ds < 2; ++ds)
; #pragma unroll
;               for (int j = 0; j < 8; ++j) x[ds][j] *= rn * qgain[32 * ds + 8 * g4 + j];
;           if constexpr (DQK == 64) {
; #pragma unroll
;               for (int ds = 0; ds < 2; ++ds)
; #pragma unroll
;                   for (int j = 0; j < 8; ++j) {
;                       auto rr = __builtin_amdgcn_permlane32_swap(__float_as_uint(x[ds][j]), __float_as_uint(x[ds][j]), false, false);
;                       const float other = hi ? __uint_as_float(rr[0]) : __uint_as_float(rr[1]);
;                       float cc = 1.f, sg = 0.f;
;                       if (lat) { const f32x2 cs = rope[(ds ? pcol : prow) * 16 + 8 * (g4 & 1) + j]; cc = cs.x; sg = hi ? cs.y : -cs.y; }
;                       x[ds][j] = x[ds][j] * cc + other * sg; }
	v_cndmask_b32_e64 v106, v45, -v45, vcc
	v_mul_f32_e32 v4, 0x4b800000, v181
	v_cmp_gt_f32_e64 s[4:5], s95, v181
	v_mov_b32_e32 v45, v46
	v_cndmask_b32_e64 v139, v89, -v89, vcc
	v_cndmask_b32_e64 v4, v181, v4, s[4:5]
	v_rsq_f32_e32 v4, v4
	v_cndmask_b32_e64 v138, v87, -v87, vcc
	v_mov_b32_e32 v87, v88
	s_waitcnt vmcnt(4)
	v_cndmask_b32_e64 v89, v31, -v31, vcc
	v_mul_f32_e32 v5, 0x45800000, v4
	v_cndmask_b32_e64 v46, v4, v5, s[4:5]
	s_waitcnt vmcnt(3)
	v_pk_mul_f32 v[4:5], v[46:47], v[50:51] op_sel_hi:[0,1]
	v_pk_mul_f32 v[4:5], v[4:5], v[148:149]
	v_cndmask_b32_e64 v88, v29, -v29, vcc
	v_mov_b32_e32 v29, v30
	v_cndmask_b32_e64 v31, v35, -v35, vcc
	v_cndmask_b32_e64 v30, v33, -v33, vcc
	v_mov_b32_e32 v33, v34
	v_cndmask_b32_e64 v35, v39, -v39, vcc
	v_cndmask_b32_e64 v34, v37, -v37, vcc
	v_mov_b32_e32 v37, v38
	v_cndmask_b32_e64 v39, v43, -v43, vcc
	v_cndmask_b32_e64 v38, v41, -v41, vcc
	v_mov_b32_e32 v41, v42
	v_and_b32_e32 v109, 0xffff0000, v83
	v_lshlrev_b32_e32 v108, 16, v83
	v_and_b32_e32 v43, 0xffff0000, v79
	v_lshlrev_b32_e32 v42, 16, v79
	v_cndmask_b32_e64 v107, v47, -v47, vcc
	v_mov_b32_e32 v47, v4
	v_mov_b32_e32 v79, v4
	v_mov_b32_e32 v83, v5
	v_mov_b32_e32 v148, v5
	v_permlane32_swap_b32_e32 v47, v79
	s_nop 0
	v_permlane32_swap_b32_e32 v83, v148
	v_cndmask_b32_e32 v149, v83, v148, vcc
	v_cndmask_b32_e32 v148, v47, v79, vcc
	v_pk_mul_f32 v[144:145], v[144:145], v[148:149]
	v_and_b32_e32 v121, 0xffff0000, v155
	v_pk_fma_f32 v[2:3], v[4:5], v[2:3], v[144:145]
	v_lshlrev_b32_e32 v120, 16, v155
	v_pk_mul_f32 v[2:3], v[2:3], s[94:95] op_sel_hi:[1,0]
	v_and_b32_e32 v123, 0xffff0000, v154
	v_cvt_pk_bf16_f32 v5, v2, v3
	v_pk_mul_f32 v[2:3], v[46:47], v[48:49] op_sel_hi:[0,1]
	v_pk_mul_f32 v[2:3], v[2:3], v[150:151]
	v_lshlrev_b32_e32 v122, 16, v154
	v_mov_b32_e32 v4, v2
	v_mov_b32_e32 v47, v2
	v_mov_b32_e32 v79, v3
	v_mov_b32_e32 v83, v3
	v_permlane32_swap_b32_e32 v4, v47
	s_nop 0
	v_permlane32_swap_b32_e32 v79, v83
	v_cndmask_b32_e32 v145, v79, v83, vcc
	v_cndmask_b32_e32 v144, v4, v47, vcc
	v_pk_mul_f32 v[12:13], v[12:13], v[144:145]
	v_cndmask_b32_e64 v155, v101, -v101, vcc
	v_pk_fma_f32 v[2:3], v[2:3], v[102:103], v[12:13]
	v_cndmask_b32_e64 v154, v99, -v99, vcc
	v_pk_mul_f32 v[2:3], v[2:3], s[94:95] op_sel_hi:[1,0]
	v_mov_b32_e32 v99, v100
	v_cvt_pk_bf16_f32 v4, v2, v3
	s_waitcnt vmcnt(2)
	v_pk_mul_f32 v[2:3], v[46:47], v[54:55] op_sel_hi:[0,1]
	v_pk_mul_f32 v[2:3], v[2:3], v[156:157]
	v_cmp_gt_f32_e64 s[4:5], s95, v180
	v_mov_b32_e32 v12, v2
	v_mov_b32_e32 v47, v2
	v_mov_b32_e32 v13, v3
	v_mov_b32_e32 v79, v3
	v_permlane32_swap_b32_e32 v12, v47
	s_nop 0
	v_permlane32_swap_b32_e32 v13, v79
	v_cndmask_b32_e32 v13, v13, v79, vcc
	v_cndmask_b32_e32 v12, v12, v47, vcc
	v_pk_mul_f32 v[12:13], v[154:155], v[12:13]
	v_cndmask_b32_e64 v129, v59, -v59, vcc
	v_pk_fma_f32 v[2:3], v[2:3], v[98:99], v[12:13]
	v_pk_mul_f32 v[12:13], v[52:53], v[46:47] op_sel_hi:[1,0]
	v_pk_mul_f32 v[2:3], v[2:3], s[94:95] op_sel_hi:[1,0]
	v_pk_mul_f32 v[12:13], v[12:13], v[160:161]
	v_cvt_pk_bf16_f32 v3, v2, v3
	v_mov_b32_e32 v2, v12
	v_mov_b32_e32 v47, v12
	v_mov_b32_e32 v79, v13
	v_mov_b32_e32 v83, v13
	v_permlane32_swap_b32_e32 v2, v47
	s_nop 0
	v_permlane32_swap_b32_e32 v79, v83
	v_cndmask_b32_e32 v99, v79, v83, vcc
	v_cndmask_b32_e32 v98, v2, v47, vcc
	v_pk_mul_f32 v[98:99], v[158:159], v[98:99]
	v_cndmask_b32_e64 v128, v57, -v57, vcc
	v_pk_fma_f32 v[6:7], v[12:13], v[6:7], v[98:99]
	v_mov_b32_e32 v57, v58
	v_pk_mul_f32 v[6:7], v[6:7], s[94:95] op_sel_hi:[1,0]
	v_and_b32_e32 v59, 0xffff0000, v85
	v_cvt_pk_bf16_f32 v2, v6, v7
	s_waitcnt vmcnt(1)
	v_pk_mul_f32 v[6:7], v[72:73], v[46:47] op_sel_hi:[1,0]
	v_lshlrev_b32_e32 v58, 16, v85
	v_pk_mul_f32 v[6:7], v[6:7], v[8:9]
	v_and_b32_e32 v85, 0xffff0000, v84
	v_mov_b32_e32 v8, v6
	v_mov_b32_e32 v12, v6
	v_mov_b32_e32 v9, v7
	v_mov_b32_e32 v13, v7
	v_permlane32_swap_b32_e32 v8, v12
	s_nop 0
	v_permlane32_swap_b32_e32 v9, v13
	v_cndmask_b32_e32 v9, v9, v13, vcc
	v_cndmask_b32_e32 v8, v8, v12, vcc
	v_pk_mul_f32 v[8:9], v[30:31], v[8:9]
	v_lshlrev_b32_e32 v84, 16, v84
	v_pk_fma_f32 v[6:7], v[6:7], v[32:33], v[8:9]
	v_and_b32_e32 v101, 0xffff0000, v81
	v_pk_mul_f32 v[6:7], v[6:7], s[94:95] op_sel_hi:[1,0]
	v_lshlrev_b32_e32 v100, 16, v81
	v_cvt_pk_bf16_f32 v9, v6, v7
	v_pk_mul_f32 v[6:7], v[70:71], v[46:47] op_sel_hi:[1,0]
	v_and_b32_e32 v81, 0xffff0000, v80
	v_pk_mul_f32 v[6:7], v[6:7], v[172:173]
	v_lshlrev_b32_e32 v80, 16, v80
	v_mov_b32_e32 v8, v6
	v_mov_b32_e32 v12, v6
	v_mov_b32_e32 v13, v7
	v_mov_b32_e32 v47, v7
	v_permlane32_swap_b32_e32 v8, v12
	s_nop 0
	v_permlane32_swap_b32_e32 v13, v47
	v_cndmask_b32_e32 v13, v13, v47, vcc
	v_cndmask_b32_e32 v12, v8, v12, vcc
	v_pk_mul_f32 v[12:13], v[34:35], v[12:13]
	s_nop 0
	v_pk_fma_f32 v[6:7], v[6:7], v[36:37], v[12:13]
	s_nop 0
	v_pk_mul_f32 v[6:7], v[6:7], s[94:95] op_sel_hi:[1,0]
	s_nop 0
	v_cvt_pk_bf16_f32 v8, v6, v7
	s_waitcnt vmcnt(0)
; __device__ __forceinline__ unsigned cvtpk(float lo, float hi) { f32x2 v = {lo, hi}; bf16x2_t b = __builtin_convertvector(v, bf16x2_t); return __builtin_bit_cast(unsigned, b); }
; template <int DQK, int DV, bool LEAD> ...
;     ...
;               for (int j = 0; j < 8; ++j) x[ds][j] *= rn * qgain[32 * ds + 8 * g4 + j];
;           if constexpr (DQK == 64) {
; #pragma unroll
;               for (int ds = 0; ds < 2; ++ds)
; #pragma unroll
;                   for (int j = 0; j < 8; ++j) {
;                       auto rr = __builtin_amdgcn_permlane32_swap(__float_as_uint(x[ds][j]), __float_as_uint(x[ds][j]), false, false);
;                       const float other = hi ? __uint_as_float(rr[0]) : __uint_as_float(rr[1]);
;                       float cc = 1.f, sg = 0.f;
;                       if (lat) { const f32x2 cs = rope[(ds ? pcol : prow) * 16 + 8 * (g4 & 1) + j]; cc = cs.x; sg = hi ? cs.y : -cs.y; }
;                       x[ds][j] = x[ds][j] * cc + other * sg; }
;           } else {
;               float sr = 0.f;
; #pragma unroll
;               for (int j = 0; j < 8; ++j) sr += x[2][j] * x[2][j];
;               sr = lanes4_sum(sr);
;               const float rq = rsqrtf(sr * (1.f / 32.f) + EPS);
; #pragma unroll
;               for (int j = 0; j < 8; ++j) { const float av = x[2][j] * rq * qgain[64 + 8 * g4 + j];
;                   auto rr = __builtin_amdgcn_permlane16_swap(__float_as_uint(av), __float_as_uint(av), false, false);
;                   const float other = (g4 & 1) ? __uint_as_float(rr[0]) : __uint_as_float(rr[1]);
;                   float cc = 1.f, sg = 0.f;
;                   if (lat) { const f32x2 cs = rope[((g4 & 2) ? pcol : prow) * 8 + j]; cc = cs.x; sg = (g4 & 1) ? cs.y : -cs.y; }
;                   x[2][j] = av * cc + other * sg; }
;           }
; #pragma unroll
;           for (int ds = 0; ds < NDS; ++ds) { u32x4 w;
; #pragma unroll
;               for (int i = 0; i < 4; ++i) w[i] = cvtpk(x[ds][2 * i] * c2, x[ds][2 * i + 1] * c2);
;               qf[qb * NDS + ds] = __builtin_bit_cast(bf16x8, w); }
	v_pk_mul_f32 v[6:7], v[76:77], v[46:47] op_sel_hi:[1,0]
	s_nop 0
	v_pk_mul_f32 v[6:7], v[6:7], v[176:177]
	s_nop 0
	v_mov_b32_e32 v12, v6
	v_mov_b32_e32 v47, v6
	v_mov_b32_e32 v13, v7
	v_mov_b32_e32 v79, v7
	v_permlane32_swap_b32_e32 v12, v47
	s_nop 0
	v_permlane32_swap_b32_e32 v13, v79
	v_cndmask_b32_e32 v13, v13, v79, vcc
	v_cndmask_b32_e32 v12, v12, v47, vcc
	v_pk_mul_f32 v[12:13], v[38:39], v[12:13]
	s_nop 0
	v_pk_fma_f32 v[6:7], v[6:7], v[40:41], v[12:13]
	v_pk_mul_f32 v[12:13], v[74:75], v[46:47] op_sel_hi:[1,0]
	v_pk_mul_f32 v[6:7], v[6:7], s[94:95] op_sel_hi:[1,0]
	v_pk_mul_f32 v[12:13], v[12:13], v[178:179]
	v_cvt_pk_bf16_f32 v7, v6, v7
	v_mov_b32_e32 v6, v12
	v_mov_b32_e32 v46, v12
	s_nop 1
	v_permlane32_swap_b32_e32 v6, v46
	v_mov_b32_e32 v47, v13
	v_mov_b32_e32 v79, v13
	v_cndmask_b32_e32 v46, v6, v46, vcc
	v_mul_f32_e32 v6, 0x4b800000, v180
	v_permlane32_swap_b32_e32 v47, v79
	v_cndmask_b32_e64 v6, v180, v6, s[4:5]
	v_cndmask_b32_e32 v47, v47, v79, vcc
	v_rsq_f32_e32 v79, v6
	v_pk_mul_f32 v[46:47], v[106:107], v[46:47]
	s_nop 0
	v_pk_fma_f32 v[12:13], v[12:13], v[44:45], v[46:47]
	s_nop 0
	v_pk_mul_f32 v[12:13], v[12:13], s[94:95] op_sel_hi:[1,0]
	s_nop 0
	v_cvt_pk_bf16_f32 v6, v12, v13
	v_mul_f32_e32 v12, 0x45800000, v79
	v_cndmask_b32_e64 v46, v79, v12, s[4:5]
	v_pk_mul_f32 v[12:13], v[50:51], v[46:47] op_sel_hi:[1,0]
	s_nop 0
	v_pk_mul_f32 v[12:13], v[12:13], v[132:133]
	s_nop 0
	v_mov_b32_e32 v47, v12
	v_mov_b32_e32 v79, v12
	v_mov_b32_e32 v83, v13
	v_mov_b32_e32 v98, v13
	v_permlane32_swap_b32_e32 v47, v79
	s_nop 0
	v_permlane32_swap_b32_e32 v83, v98
	v_cndmask_b32_e32 v99, v83, v98, vcc
	v_cndmask_b32_e32 v98, v47, v79, vcc
	v_pk_mul_f32 v[26:27], v[26:27], v[98:99]
	v_and_b32_e32 v83, 0xffff0000, v82
	v_pk_fma_f32 v[10:11], v[12:13], v[10:11], v[26:27]
	v_lshlrev_b32_e32 v82, 16, v82
	v_pk_mul_f32 v[10:11], v[10:11], s[94:95] op_sel_hi:[1,0]
	s_nop 0
	v_cvt_pk_bf16_f32 v13, v10, v11
	v_pk_mul_f32 v[10:11], v[48:49], v[46:47] op_sel_hi:[1,0]
	s_nop 0
	v_pk_mul_f32 v[10:11], v[10:11], v[136:137]
	s_nop 0
	v_mov_b32_e32 v12, v10
	v_mov_b32_e32 v26, v10
	v_mov_b32_e32 v27, v11
	v_mov_b32_e32 v47, v11
	v_permlane32_swap_b32_e32 v12, v26
	s_nop 0
	v_permlane32_swap_b32_e32 v27, v47
	v_cndmask_b32_e32 v27, v27, v47, vcc
	v_cndmask_b32_e32 v26, v12, v26, vcc
	v_pk_mul_f32 v[26:27], v[134:135], v[26:27]
	s_nop 0
	v_pk_fma_f32 v[10:11], v[10:11], v[94:95], v[26:27]
	s_nop 0
	v_pk_mul_f32 v[10:11], v[10:11], s[94:95] op_sel_hi:[1,0]
	s_nop 0
	v_cvt_pk_bf16_f32 v12, v10, v11
	v_pk_mul_f32 v[10:11], v[54:55], v[46:47] op_sel_hi:[1,0]
	s_nop 0
	v_pk_mul_f32 v[10:11], v[10:11], v[140:141]
	s_nop 0
	v_mov_b32_e32 v26, v10
	v_mov_b32_e32 v47, v10
	v_mov_b32_e32 v27, v11
	v_mov_b32_e32 v79, v11
	v_permlane32_swap_b32_e32 v26, v47
	s_nop 0
	v_permlane32_swap_b32_e32 v27, v79
	v_cndmask_b32_e32 v27, v27, v79, vcc
	v_cndmask_b32_e32 v26, v26, v47, vcc
	v_pk_mul_f32 v[26:27], v[138:139], v[26:27]
	s_nop 0
	v_pk_fma_f32 v[10:11], v[10:11], v[86:87], v[26:27]
	v_pk_mul_f32 v[26:27], v[52:53], v[46:47] op_sel_hi:[1,0]
	v_pk_mul_f32 v[10:11], v[10:11], s[94:95] op_sel_hi:[1,0]
	v_pk_mul_f32 v[26:27], v[26:27], v[62:63]
	v_cvt_pk_bf16_f32 v11, v10, v11
	v_mov_b32_e32 v10, v26
	v_mov_b32_e32 v47, v26
	v_mov_b32_e32 v62, v27
	v_mov_b32_e32 v63, v27
	v_permlane32_swap_b32_e32 v10, v47
	s_nop 0
	v_permlane32_swap_b32_e32 v62, v63
	v_cndmask_b32_e32 v63, v62, v63, vcc
	v_cndmask_b32_e32 v62, v10, v47, vcc
	v_pk_mul_f32 v[24:25], v[24:25], v[62:63]
	s_nop 0
	v_pk_fma_f32 v[24:25], v[26:27], v[90:91], v[24:25]
	v_and_b32_e32 v91, 0xffff0000, v78
	v_pk_mul_f32 v[24:25], v[24:25], s[94:95] op_sel_hi:[1,0]
	v_lshlrev_b32_e32 v90, 16, v78
	v_cvt_pk_bf16_f32 v10, v24, v25
	v_pk_mul_f32 v[24:25], v[72:73], v[46:47] op_sel_hi:[1,0]
	s_nop 0
	v_pk_mul_f32 v[24:25], v[24:25], v[142:143]
	s_nop 0
	v_mov_b32_e32 v26, v24
	v_mov_b32_e32 v47, v24
	v_mov_b32_e32 v27, v25
	v_mov_b32_e32 v62, v25
	v_permlane32_swap_b32_e32 v26, v47
	s_nop 0
	v_permlane32_swap_b32_e32 v27, v62
	v_cndmask_b32_e32 v27, v27, v62, vcc
	v_cndmask_b32_e32 v26, v26, v47, vcc
	v_pk_mul_f32 v[26:27], v[30:31], v[26:27]
	s_nop 0
	v_pk_fma_f32 v[24:25], v[24:25], v[32:33], v[26:27]
	s_nop 0
	v_pk_mul_f32 v[24:25], v[24:25], s[94:95] op_sel_hi:[1,0]
	s_nop 0
	v_cvt_pk_bf16_f32 v27, v24, v25
	v_pk_mul_f32 v[24:25], v[70:71], v[46:47] op_sel_hi:[1,0]
	s_nop 0
	v_pk_mul_f32 v[24:25], v[24:25], v[112:113]
	s_nop 0
	v_mov_b32_e32 v26, v24
	v_mov_b32_e32 v47, v24
	v_mov_b32_e32 v62, v25
	v_mov_b32_e32 v63, v25
	v_permlane32_swap_b32_e32 v26, v47
	s_nop 0
	v_permlane32_swap_b32_e32 v62, v63
	v_cndmask_b32_e32 v63, v62, v63, vcc
	v_cndmask_b32_e32 v62, v26, v47, vcc
	v_pk_mul_f32 v[62:63], v[34:35], v[62:63]
	s_nop 0
	v_pk_fma_f32 v[24:25], v[36:37], v[24:25], v[62:63]
	s_nop 0
	v_pk_mul_f32 v[24:25], v[24:25], s[94:95] op_sel_hi:[1,0]
	s_nop 0
	v_cvt_pk_bf16_f32 v26, v24, v25
	v_pk_mul_f32 v[24:25], v[76:77], v[46:47] op_sel_hi:[1,0]
	s_nop 0
	v_pk_mul_f32 v[24:25], v[24:25], v[146:147]
	s_nop 0
	v_mov_b32_e32 v47, v24
	v_mov_b32_e32 v62, v24
	v_mov_b32_e32 v63, v25
	v_mov_b32_e32 v79, v25
	v_permlane32_swap_b32_e32 v47, v62
	s_nop 0
	v_permlane32_swap_b32_e32 v63, v79
	v_cndmask_b32_e32 v63, v63, v79, vcc
	v_cndmask_b32_e32 v62, v47, v62, vcc
	v_pk_mul_f32 v[24:25], v[40:41], v[24:25]
	v_pk_mul_f32 v[46:47], v[74:75], v[46:47] op_sel_hi:[1,0]
	v_pk_fma_f32 v[24:25], v[38:39], v[62:63], v[24:25]
	v_pk_mul_f32 v[46:47], v[46:47], v[152:153]
	v_pk_mul_f32 v[24:25], v[24:25], s[94:95] op_sel_hi:[1,0]
	v_mov_b32_e32 v62, v46
	v_cvt_pk_bf16_f32 v25, v24, v25
	v_mov_b32_e32 v24, v46
	s_nop 1
; template <int DQK, int DV, bool LEAD> ...
;     ...
;           float sn = 0.f;
; #pragma unroll
;           for (int ds = 0; ds < 2; ++ds)
; #pragma unroll
;               for (int j = 0; j < 8; ++j) sn += x[ds][j] * x[ds][j];
;           sn = lanes4_sum(sn);
;           const float rn = rsqrtf(sn * (1.f / 64.f) + EPS);
; #pragma unroll
;           for (int ds = 0; ds < 2; ++ds)
; #pragma unroll
;               for (int j = 0; j < 8; ++j) x[ds][j] *= rn * qgain[32 * ds + 8 * g4 + j];
;           if constexpr (DQK == 64) {
; #pragma unroll
;               for (int ds = 0; ds < 2; ++ds)
; #pragma unroll
;                   for (int j = 0; j < 8; ++j) {
;                       auto rr = __builtin_amdgcn_permlane32_swap(__float_as_uint(x[ds][j]), __float_as_uint(x[ds][j]), false, false);
;                       const float other = hi ? __uint_as_float(rr[0]) : __uint_as_float(rr[1]);
;                       float cc = 1.f, sg = 0.f;
;                       if (lat) { const f32x2 cs = rope[(ds ? pcol : prow) * 16 + 8 * (g4 & 1) + j]; cc = cs.x; sg = hi ? cs.y : -cs.y; }
;                       x[ds][j] = x[ds][j] * cc + other * sg; }
;           } else {
;               float sr = 0.f;
; #pragma unroll
;               for (int j = 0; j < 8; ++j) sr += x[2][j] * x[2][j];
;               sr = lanes4_sum(sr);
;               const float rq = rsqrtf(sr * (1.f / 32.f) + EPS);
; #pragma unroll
;               for (int j = 0; j < 8; ++j) { const float av = x[2][j] * rq * qgain[64 + 8 * g4 + j];
;                   auto rr = __builtin_amdgcn_permlane16_swap(__float_as_uint(av), __float_as_uint(av), false, false);
;                   const float other = (g4 & 1) ? __uint_as_float(rr[0]) : __uint_as_float(rr[1]);
;                   float cc = 1.f, sg = 0.f;
;                   if (lat) { const f32x2 cs = rope[((g4 & 2) ? pcol : prow) * 8 + j]; cc = cs.x; sg = (g4 & 1) ? cs.y : -cs.y; }
;                   x[2][j] = av * cc + other * sg; }
;           }
; #pragma unroll
;           for (int ds = 0; ds < NDS; ++ds) { u32x4 w;
; #pragma unroll
;               for (int i = 0; i < 4; ++i) w[i] = cvtpk(x[ds][2 * i] * c2, x[ds][2 * i + 1] * c2);
;               qf[qb * NDS + ds] = __builtin_bit_cast(bf16x8, w); }
	v_permlane32_swap_b32_e32 v24, v62
	v_cndmask_b32_e32 v62, v24, v62, vcc
	v_mul_f32_e32 v24, v83, v83
	v_pk_fma_f32 v[86:87], v[82:83], v[82:83], v[24:25] op_sel_hi:[1,1,0]
	v_mul_f32_e32 v24, v109, v109
	v_pk_fma_f32 v[86:87], v[108:109], v[108:109], v[86:87]
	v_mov_b32_e32 v63, v47
	v_pk_add_f32 v[86:87], v[24:25], v[86:87] op_sel_hi:[0,1]
	v_pk_fma_f32 v[86:87], v[84:85], v[84:85], v[86:87]
	v_mul_f32_e32 v24, v85, v85
	v_pk_add_f32 v[86:87], v[24:25], v[86:87] op_sel_hi:[0,1]
	v_pk_fma_f32 v[86:87], v[58:59], v[58:59], v[86:87]
	v_mul_f32_e32 v24, v59, v59
	v_pk_add_f32 v[86:87], v[24:25], v[86:87] op_sel_hi:[0,1]
	v_pk_fma_f32 v[86:87], v[130:131], v[130:131], v[86:87]
	v_mul_f32_e32 v24, v131, v131
	v_pk_add_f32 v[86:87], v[24:25], v[86:87] op_sel_hi:[0,1]
	v_pk_fma_f32 v[86:87], v[126:127], v[126:127], v[86:87]
	v_mul_f32_e32 v24, v127, v127
	v_pk_add_f32 v[86:87], v[24:25], v[86:87] op_sel_hi:[0,1]
	v_pk_fma_f32 v[86:87], v[122:123], v[122:123], v[86:87]
	v_mul_f32_e32 v24, v123, v123
	v_pk_add_f32 v[86:87], v[24:25], v[86:87] op_sel_hi:[0,1]
	v_pk_fma_f32 v[86:87], v[120:121], v[120:121], v[86:87]
	v_mul_f32_e32 v24, v121, v121
	v_pk_add_f32 v[86:87], v[24:25], v[86:87] op_sel_hi:[0,1]
	v_mov_b32_e32 v79, v47
	v_mov_b32_e32 v24, v86
	s_nop 0
	v_permlane32_swap_b32_e32 v63, v79
	v_permlane16_swap_b32_e32 v86, v24
	v_cndmask_b32_e32 v63, v63, v79, vcc
	v_add_f32_e32 v79, v86, v24
	v_mul_f32_e32 v24, v91, v91
	v_pk_fma_f32 v[94:95], v[90:91], v[90:91], v[24:25] op_sel_hi:[1,1,0]
	v_mul_f32_e32 v24, v43, v43
	v_pk_fma_f32 v[94:95], v[42:43], v[42:43], v[94:95]
	v_mov_b32_e32 v87, v79
	v_pk_add_f32 v[94:95], v[24:25], v[94:95] op_sel_hi:[0,1]
	v_pk_fma_f32 v[94:95], v[80:81], v[80:81], v[94:95]
	v_mul_f32_e32 v24, v81, v81
	v_pk_add_f32 v[94:95], v[24:25], v[94:95] op_sel_hi:[0,1]
	v_pk_fma_f32 v[94:95], v[100:101], v[100:101], v[94:95]
	v_mul_f32_e32 v24, v101, v101
	v_pk_add_f32 v[94:95], v[24:25], v[94:95] op_sel_hi:[0,1]
	v_pk_fma_f32 v[94:95], v[92:93], v[92:93], v[94:95]
	v_mul_f32_e32 v24, v93, v93
	v_pk_add_f32 v[94:95], v[24:25], v[94:95] op_sel_hi:[0,1]
	v_pk_fma_f32 v[94:95], v[96:97], v[96:97], v[94:95]
	v_mul_f32_e32 v24, v97, v97
	v_pk_add_f32 v[94:95], v[24:25], v[94:95] op_sel_hi:[0,1]
	v_pk_fma_f32 v[94:95], v[66:67], v[66:67], v[94:95]
	v_mul_f32_e32 v24, v67, v67
	v_pk_add_f32 v[94:95], v[24:25], v[94:95] op_sel_hi:[0,1]
	v_pk_fma_f32 v[94:95], v[116:117], v[116:117], v[94:95]
	v_mul_f32_e32 v24, v117, v117
	v_pk_add_f32 v[94:95], v[24:25], v[94:95] op_sel_hi:[0,1]
	v_mov_b32_e32 v24, v94
	s_nop 1
	v_permlane16_swap_b32_e32 v94, v24
	v_add_f32_e32 v78, v94, v24
	v_mov_b32_e32 v86, v78
	v_permlane32_swap_b32_e32 v79, v87
	s_nop 0
	v_permlane32_swap_b32_e32 v78, v86
	v_pk_add_f32 v[78:79], v[78:79], v[86:87]
	v_pk_mul_f32 v[46:47], v[44:45], v[46:47]
	v_pk_fma_f32 v[78:79], v[78:79], s[12:13], v[110:111] op_sel_hi:[1,0,0]
	v_pk_fma_f32 v[46:47], v[106:107], v[62:63], v[46:47]
	v_mul_f32_e32 v24, 0x4b800000, v79
	v_cmp_gt_f32_e64 s[4:5], s95, v79
	v_pk_mul_f32 v[46:47], v[46:47], s[94:95] op_sel_hi:[1,0]
	s_nop 0
	v_cndmask_b32_e64 v24, v79, v24, s[4:5]
	v_rsq_f32_e32 v79, v24
	v_cvt_pk_bf16_f32 v24, v46, v47
	v_mul_f32_e32 v46, 0x45800000, v79
	v_cndmask_b32_e64 v46, v79, v46, s[4:5]
	v_pk_mul_f32 v[62:63], v[50:51], v[46:47] op_sel_hi:[1,0]
	v_cmp_gt_f32_e64 s[4:5], s95, v78
	v_pk_mul_f32 v[62:63], v[62:63], v[120:121]
	s_nop 0
	v_mov_b32_e32 v47, v62
	v_mov_b32_e32 v79, v62
	v_mov_b32_e32 v86, v63
	v_mov_b32_e32 v87, v63
	v_permlane32_swap_b32_e32 v47, v79
	s_nop 0
	v_permlane32_swap_b32_e32 v86, v87
	v_cndmask_b32_e32 v87, v86, v87, vcc
	v_cndmask_b32_e32 v86, v47, v79, vcc
	v_pk_mul_f32 v[86:87], v[118:119], v[86:87]
	s_nop 0
	v_pk_fma_f32 v[62:63], v[62:63], v[68:69], v[86:87]
	v_pk_mul_f32 v[68:69], v[48:49], v[46:47] op_sel_hi:[1,0]
	v_pk_mul_f32 v[62:63], v[62:63], s[94:95] op_sel_hi:[1,0]
	v_pk_mul_f32 v[68:69], v[68:69], v[122:123]
	v_cvt_pk_bf16_f32 v63, v62, v63
	v_mov_b32_e32 v47, v68
	v_mov_b32_e32 v62, v68
	v_mov_b32_e32 v79, v69
	v_mov_b32_e32 v86, v69
	v_permlane32_swap_b32_e32 v47, v62
	s_nop 0
	v_permlane32_swap_b32_e32 v79, v86
	v_cndmask_b32_e32 v87, v79, v86, vcc
	v_cndmask_b32_e32 v86, v47, v62, vcc
	v_pk_mul_f32 v[86:87], v[104:105], v[86:87]
	s_nop 0
	v_pk_fma_f32 v[64:65], v[68:69], v[64:65], v[86:87]
	s_nop 0
	v_pk_mul_f32 v[64:65], v[64:65], s[94:95] op_sel_hi:[1,0]
	s_nop 0
	v_cvt_pk_bf16_f32 v62, v64, v65
	v_pk_mul_f32 v[64:65], v[54:55], v[46:47] op_sel_hi:[1,0]
	s_nop 0
	v_pk_mul_f32 v[64:65], v[64:65], v[126:127]
	s_nop 0
	v_mov_b32_e32 v47, v64
	v_mov_b32_e32 v68, v64
	v_mov_b32_e32 v69, v65
	v_mov_b32_e32 v79, v65
	v_permlane32_swap_b32_e32 v47, v68
	s_nop 0
	v_permlane32_swap_b32_e32 v69, v79
	v_cndmask_b32_e32 v69, v69, v79, vcc
	v_cndmask_b32_e32 v68, v47, v68, vcc
	v_pk_mul_f32 v[68:69], v[124:125], v[68:69]
	s_nop 0
	v_pk_fma_f32 v[60:61], v[64:65], v[60:61], v[68:69]
	v_pk_mul_f32 v[64:65], v[52:53], v[46:47] op_sel_hi:[1,0]
	v_pk_mul_f32 v[60:61], v[60:61], s[94:95] op_sel_hi:[1,0]
	v_pk_mul_f32 v[64:65], v[64:65], v[130:131]
	v_cvt_pk_bf16_f32 v61, v60, v61
	v_mov_b32_e32 v47, v64
	v_mov_b32_e32 v60, v64
	v_mov_b32_e32 v68, v65
	v_mov_b32_e32 v69, v65
	v_permlane32_swap_b32_e32 v47, v60
	s_nop 0
	v_permlane32_swap_b32_e32 v68, v69
	v_cndmask_b32_e32 v69, v68, v69, vcc
	v_cndmask_b32_e32 v68, v47, v60, vcc
	v_pk_mul_f32 v[68:69], v[128:129], v[68:69]
	s_nop 0
	v_pk_fma_f32 v[56:57], v[64:65], v[56:57], v[68:69]
	s_nop 0
	v_pk_mul_f32 v[56:57], v[56:57], s[94:95] op_sel_hi:[1,0]
	s_nop 0
	v_cvt_pk_bf16_f32 v60, v56, v57
	v_pk_mul_f32 v[56:57], v[72:73], v[46:47] op_sel_hi:[1,0]
; __device__ __forceinline__ unsigned cvtpk(float lo, float hi) { f32x2 v = {lo, hi}; bf16x2_t b = __builtin_convertvector(v, bf16x2_t); return __builtin_bit_cast(unsigned, b); }
; template <int DQK, int DV, bool LEAD> ...
;     ...
;           const float rn = rsqrtf(sn * (1.f / 64.f) + EPS);
; #pragma unroll
;           for (int ds = 0; ds < 2; ++ds)
; #pragma unroll
;               for (int j = 0; j < 8; ++j) x[ds][j] *= rn * qgain[32 * ds + 8 * g4 + j];
;           if constexpr (DQK == 64) {
; #pragma unroll
;               for (int ds = 0; ds < 2; ++ds)
; #pragma unroll
;                   for (int j = 0; j < 8; ++j) {
;                       auto rr = __builtin_amdgcn_permlane32_swap(__float_as_uint(x[ds][j]), __float_as_uint(x[ds][j]), false, false);
;                       const float other = hi ? __uint_as_float(rr[0]) : __uint_as_float(rr[1]);
;                       float cc = 1.f, sg = 0.f;
;                       if (lat) { const f32x2 cs = rope[(ds ? pcol : prow) * 16 + 8 * (g4 & 1) + j]; cc = cs.x; sg = hi ? cs.y : -cs.y; }
;                       x[ds][j] = x[ds][j] * cc + other * sg; }
;           } else {
;               float sr = 0.f;
; #pragma unroll
;               for (int j = 0; j < 8; ++j) sr += x[2][j] * x[2][j];
;               sr = lanes4_sum(sr);
;               const float rq = rsqrtf(sr * (1.f / 32.f) + EPS);
; #pragma unroll
;               for (int j = 0; j < 8; ++j) { const float av = x[2][j] * rq * qgain[64 + 8 * g4 + j];
;                   auto rr = __builtin_amdgcn_permlane16_swap(__float_as_uint(av), __float_as_uint(av), false, false);
;                   const float other = (g4 & 1) ? __uint_as_float(rr[0]) : __uint_as_float(rr[1]);
;                   float cc = 1.f, sg = 0.f;
;                   if (lat) { const f32x2 cs = rope[((g4 & 2) ? pcol : prow) * 8 + j]; cc = cs.x; sg = (g4 & 1) ? cs.y : -cs.y; }
;                   x[2][j] = av * cc + other * sg; }
;           }
; #pragma unroll
;           for (int ds = 0; ds < NDS; ++ds) { u32x4 w;
; #pragma unroll
;               for (int i = 0; i < 4; ++i) w[i] = cvtpk(x[ds][2 * i] * c2, x[ds][2 * i + 1] * c2);
;               qf[qb * NDS + ds] = __builtin_bit_cast(bf16x8, w); }
;       }
; #pragma unroll
;       for (int d0 = 0; d0 < NQB * NDS; ++d0) asm volatile("" : "+v"(qf[d0])); }
;     wait_bar<0>();
	s_nop 0
	v_pk_mul_f32 v[56:57], v[56:57], v[58:59]
	s_nop 0
	v_mov_b32_e32 v47, v56
	v_mov_b32_e32 v58, v56
	v_mov_b32_e32 v59, v57
	v_mov_b32_e32 v64, v57
	v_permlane32_swap_b32_e32 v47, v58
	s_nop 0
	v_permlane32_swap_b32_e32 v59, v64
	v_cndmask_b32_e32 v59, v59, v64, vcc
	v_cndmask_b32_e32 v58, v47, v58, vcc
	v_pk_mul_f32 v[58:59], v[30:31], v[58:59]
	s_nop 0
	v_pk_fma_f32 v[56:57], v[56:57], v[32:33], v[58:59]
	s_nop 0
	v_pk_mul_f32 v[56:57], v[56:57], s[94:95] op_sel_hi:[1,0]
	s_nop 0
	v_cvt_pk_bf16_f32 v59, v56, v57
	v_pk_mul_f32 v[56:57], v[70:71], v[46:47] op_sel_hi:[1,0]
	s_nop 0
	v_pk_mul_f32 v[56:57], v[56:57], v[84:85]
	s_nop 0
	v_mov_b32_e32 v47, v56
	v_mov_b32_e32 v58, v56
	v_mov_b32_e32 v64, v57
	v_mov_b32_e32 v65, v57
	v_permlane32_swap_b32_e32 v47, v58
	s_nop 0
	v_permlane32_swap_b32_e32 v64, v65
	v_cndmask_b32_e32 v65, v64, v65, vcc
	v_cndmask_b32_e32 v64, v47, v58, vcc
	v_pk_mul_f32 v[64:65], v[34:35], v[64:65]
	s_nop 0
	v_pk_fma_f32 v[56:57], v[36:37], v[56:57], v[64:65]
	s_nop 0
	v_pk_mul_f32 v[56:57], v[56:57], s[94:95] op_sel_hi:[1,0]
	s_nop 0
	v_cvt_pk_bf16_f32 v58, v56, v57
	v_pk_mul_f32 v[56:57], v[76:77], v[46:47] op_sel_hi:[1,0]
	s_nop 0
	v_pk_mul_f32 v[56:57], v[56:57], v[108:109]
	s_nop 0
	v_mov_b32_e32 v47, v56
	v_mov_b32_e32 v64, v56
	v_mov_b32_e32 v65, v57
	v_mov_b32_e32 v68, v57
	v_permlane32_swap_b32_e32 v47, v64
	s_nop 0
	v_permlane32_swap_b32_e32 v65, v68
	v_cndmask_b32_e32 v65, v65, v68, vcc
	v_cndmask_b32_e32 v64, v47, v64, vcc
	v_pk_mul_f32 v[56:57], v[40:41], v[56:57]
	v_pk_mul_f32 v[46:47], v[74:75], v[46:47] op_sel_hi:[1,0]
	v_pk_fma_f32 v[56:57], v[38:39], v[64:65], v[56:57]
	v_pk_mul_f32 v[46:47], v[46:47], v[82:83]
	v_pk_mul_f32 v[56:57], v[56:57], s[94:95] op_sel_hi:[1,0]
	v_mov_b32_e32 v64, v46
	v_cvt_pk_bf16_f32 v57, v56, v57
	v_mov_b32_e32 v56, v46
	s_nop 1
	v_permlane32_swap_b32_e32 v56, v64
	v_mov_b32_e32 v65, v47
	v_mov_b32_e32 v68, v47
	v_cndmask_b32_e32 v64, v56, v64, vcc
	v_mul_f32_e32 v56, 0x4b800000, v78
	v_permlane32_swap_b32_e32 v65, v68
	v_cndmask_b32_e64 v56, v78, v56, s[4:5]
	v_cndmask_b32_e32 v65, v65, v68, vcc
	v_rsq_f32_e32 v68, v56
	v_pk_mul_f32 v[46:47], v[44:45], v[46:47]
	s_nop 0
	v_pk_fma_f32 v[46:47], v[106:107], v[64:65], v[46:47]
	s_nop 0
	v_pk_mul_f32 v[46:47], v[46:47], s[94:95] op_sel_hi:[1,0]
	s_nop 0
	v_cvt_pk_bf16_f32 v56, v46, v47
	v_mul_f32_e32 v46, 0x45800000, v68
	v_cndmask_b32_e64 v46, v68, v46, s[4:5]
	v_pk_mul_f32 v[64:65], v[74:75], v[46:47] op_sel_hi:[1,0]
	v_pk_mul_f32 v[68:69], v[76:77], v[46:47] op_sel_hi:[1,0]
	v_pk_mul_f32 v[64:65], v[64:65], v[90:91]
	v_pk_mul_f32 v[48:49], v[48:49], v[46:47] op_sel_hi:[1,0]
	v_pk_mul_f32 v[42:43], v[68:69], v[42:43]
	v_pk_mul_f32 v[68:69], v[70:71], v[46:47] op_sel_hi:[1,0]
	v_pk_mul_f32 v[70:71], v[72:73], v[46:47] op_sel_hi:[1,0]
	v_pk_mul_f32 v[52:53], v[52:53], v[46:47] op_sel_hi:[1,0]
	v_pk_mul_f32 v[54:55], v[54:55], v[46:47] op_sel_hi:[1,0]
	v_pk_mul_f32 v[48:49], v[48:49], v[66:67]
	v_pk_mul_f32 v[46:47], v[50:51], v[46:47] op_sel_hi:[1,0]
	v_mov_b32_e32 v50, v64
	v_mov_b32_e32 v66, v64
	v_mov_b32_e32 v51, v65
	v_mov_b32_e32 v67, v65
	v_permlane32_swap_b32_e32 v50, v66
	s_nop 0
	v_permlane32_swap_b32_e32 v51, v67
	v_cndmask_b32_e32 v51, v51, v67, vcc
	v_cndmask_b32_e32 v50, v50, v66, vcc
	v_pk_mul_f32 v[44:45], v[44:45], v[64:65]
	v_mov_b32_e32 v64, v42
	v_pk_fma_f32 v[44:45], v[106:107], v[50:51], v[44:45]
	v_mov_b32_e32 v50, v42
	v_mov_b32_e32 v51, v43
	v_mov_b32_e32 v65, v43
	v_permlane32_swap_b32_e32 v50, v64
	s_nop 0
	v_permlane32_swap_b32_e32 v51, v65
	v_pk_mul_f32 v[68:69], v[68:69], v[80:81]
	v_cndmask_b32_e32 v51, v51, v65, vcc
	v_cndmask_b32_e32 v50, v50, v64, vcc
	v_pk_mul_f32 v[40:41], v[40:41], v[42:43]
	v_mov_b32_e32 v42, v68
	v_pk_fma_f32 v[38:39], v[38:39], v[50:51], v[40:41]
	v_mov_b32_e32 v40, v68
	v_mov_b32_e32 v41, v69
	v_mov_b32_e32 v43, v69
	v_permlane32_swap_b32_e32 v40, v42
	s_nop 0
	v_permlane32_swap_b32_e32 v41, v43
	v_cndmask_b32_e32 v41, v41, v43, vcc
	v_cndmask_b32_e32 v40, v40, v42, vcc
	v_pk_mul_f32 v[70:71], v[70:71], v[100:101]
	v_pk_mul_f32 v[34:35], v[34:35], v[40:41]
	v_mov_b32_e32 v40, v70
	v_pk_fma_f32 v[34:35], v[36:37], v[68:69], v[34:35]
	v_mov_b32_e32 v36, v70
	v_mov_b32_e32 v37, v71
	v_mov_b32_e32 v41, v71
	v_permlane32_swap_b32_e32 v36, v40
	s_nop 0
	v_permlane32_swap_b32_e32 v37, v41
	v_cndmask_b32_e32 v37, v37, v41, vcc
	v_cndmask_b32_e32 v36, v36, v40, vcc
	v_pk_mul_f32 v[52:53], v[52:53], v[92:93]
	v_pk_mul_f32 v[30:31], v[30:31], v[36:37]
	v_mov_b32_e32 v36, v52
	v_pk_fma_f32 v[30:31], v[70:71], v[32:33], v[30:31]
	v_mov_b32_e32 v32, v52
	v_mov_b32_e32 v33, v53
	v_mov_b32_e32 v37, v53
	v_permlane32_swap_b32_e32 v32, v36
	s_nop 0
	v_permlane32_swap_b32_e32 v33, v37
	v_cndmask_b32_e32 v33, v33, v37, vcc
	v_cndmask_b32_e32 v32, v32, v36, vcc
	v_pk_mul_f32 v[54:55], v[54:55], v[96:97]
	v_pk_mul_f32 v[32:33], v[88:89], v[32:33]
	v_mov_b32_e32 v36, v54
	v_pk_fma_f32 v[28:29], v[52:53], v[28:29], v[32:33]
	v_mov_b32_e32 v32, v54
	v_mov_b32_e32 v33, v55
	v_mov_b32_e32 v37, v55
	v_permlane32_swap_b32_e32 v32, v36
	s_nop 0
	v_permlane32_swap_b32_e32 v33, v37
	v_cndmask_b32_e32 v33, v33, v37, vcc
	v_cndmask_b32_e32 v32, v32, v36, vcc
	v_pk_mul_f32 v[20:21], v[20:21], v[32:33]
	v_mov_b32_e32 v32, v48
	v_pk_fma_f32 v[20:21], v[54:55], v[22:23], v[20:21]
	v_mov_b32_e32 v22, v48
	v_mov_b32_e32 v23, v49
	v_mov_b32_e32 v33, v49
	v_permlane32_swap_b32_e32 v22, v32
	s_nop 0
	v_permlane32_swap_b32_e32 v23, v33
	v_cndmask_b32_e32 v23, v23, v33, vcc
	v_cndmask_b32_e32 v22, v22, v32, vcc
	v_pk_mul_f32 v[46:47], v[46:47], v[116:117]
	v_pk_mul_f32 v[16:17], v[16:17], v[22:23]
	v_mov_b32_e32 v22, v46
	v_pk_fma_f32 v[16:17], v[48:49], v[18:19], v[16:17]
	v_mov_b32_e32 v18, v46
	v_mov_b32_e32 v19, v47
	v_mov_b32_e32 v23, v47
	v_permlane32_swap_b32_e32 v18, v22
	s_nop 0
	v_permlane32_swap_b32_e32 v19, v23
	v_cndmask_b32_e32 v19, v19, v23, vcc
	v_cndmask_b32_e32 v18, v18, v22, vcc
	v_pk_mul_f32 v[18:19], v[114:115], v[18:19]
	v_pk_mul_f32 v[16:17], v[16:17], s[94:95] op_sel_hi:[1,0]
	v_pk_fma_f32 v[14:15], v[46:47], v[14:15], v[18:19]
	v_pk_mul_f32 v[18:19], v[44:45], s[94:95] op_sel_hi:[1,0]
	v_pk_mul_f32 v[14:15], v[14:15], s[94:95] op_sel_hi:[1,0]
	v_cvt_pk_bf16_f32 v76, v18, v19
	v_pk_mul_f32 v[18:19], v[38:39], s[94:95] op_sel_hi:[1,0]
	v_cvt_pk_bf16_f32 v86, v16, v17
	v_cvt_pk_bf16_f32 v77, v18, v19
	v_pk_mul_f32 v[18:19], v[34:35], s[94:95] op_sel_hi:[1,0]
	v_cvt_pk_bf16_f32 v87, v14, v15
	v_cvt_pk_bf16_f32 v78, v18, v19
	v_pk_mul_f32 v[18:19], v[30:31], s[94:95] op_sel_hi:[1,0]
	v_bfe_u32 v22, v162, 1, 3
	v_cvt_pk_bf16_f32 v79, v18, v19
	v_pk_mul_f32 v[18:19], v[28:29], s[94:95] op_sel_hi:[1,0]
	v_bitop3_b32 v22, v169, v22, 4 bitop3:0x36
	v_cvt_pk_bf16_f32 v84, v18, v19
	v_pk_mul_f32 v[18:19], v[20:21], s[94:95] op_sel_hi:[1,0]
	v_lshlrev_b32_e32 v22, 4, v22
	v_cvt_pk_bf16_f32 v85, v18, v19
	s_waitcnt vmcnt(0) lgkmcnt(0)
	s_barrier
; #define ATT_SB() __builtin_amdgcn_sched_barrier(0)
; #define ATT_DMA_K(t, sl) do { glds16(ksrc + (size_t)(t) * 64 * kpitch, (unsigned)__builtin_amdgcn_readfirstlane(kdst + (sl) * KSLOT)); \
;         if constexpr (DQK == 96) glds16(krsrc + (size_t)(t) * 64 * 32, (unsigned)__builtin_amdgcn_readfirstlane(krdst + (sl) * KSLOT)); } while (0)
; #define ATT_DMA_V(t, sl) do { glds16(vsrc + (size_t)(t) * 64, (unsigned)__builtin_amdgcn_readfirstlane(vdst + (sl) * VSLOT)); \
;         if constexpr (DV == 128) glds16(vsrc + (size_t)64 * NR + (size_t)(t) * 64, (unsigned)__builtin_amdgcn_readfirstlane(vdst + (sl) * VSLOT + 8192)); } while (0)
; #define ATT_KLOAD(sl) do { _Pragma("unroll") for (int kb_ = 0; kb_ < NKW; ++kb_) _Pragma("unroll") for (int ds_ = 0; ds_ < NDS; ++ds_) { \
;         if (ds_ < 2) kf[kb_ * NDS + ds_] = *(const LAS bf16x8*)(kp[ds_ & 1] + (sl) * KSLOT + (kb_ & 1) * 512 + (kb_ >> 1) * 4096); \
;         else kf[kb_ * NDS + ds_] = *(const LAS bf16x8*)(krp + (sl) * KSLOT + (kb_ & 1) * 256 + (kb_ >> 1) * 2048); } } while (0)
; #define ATT_QK() do { _Pragma("unroll") for (int kb_ = 0; kb_ < NKW; ++kb_) _Pragma("unroll") for (int ds_ = 0; ds_ < NDS; ++ds_) _Pragma("unroll") for (int qb_ = 0; qb_ < NQB; ++qb_) \
;         c[kb_][qb_] = __builtin_amdgcn_mfma_f32_16x16x32_bf16(kf[kb_ * NDS + ds_], qf[qb_ * NDS + ds_], ds_ == 0 ? zero4 : c[kb_][qb_], 0, 0, 0); } while (0)
; template <int DQK, int DV, bool LEAD> ...
;     ...
;     wait_bar<0>();
;     bf16x8 kf[NKW * NDS], vf[NVF];
;     ATT_KLOAD(0);
;     asm volatile("s_waitcnt lgkmcnt(0)\n\ts_barrier" ::: "memory");
;     float lsum[NQB];
; #pragma unroll
;     for (int qb = 0; qb < NQB; ++qb) lsum[qb] = 0.f;
;     const f32x4 zero4 = {0.f, 0.f, 0.f, 0.f};
;     f32x4 o[NDB][NQB], c[NKW][NQB]; u32x4 pw[4];
; #pragma unroll
;     for (int i = 0; i < NDB; ++i)
; #pragma unroll
;         for (int qb = 0; qb < NQB; ++qb) o[i][qb] = zero4;
;     ATT_DMA_K(3, 0); ATT_DMA_V(1, 1);
;     ATT_QK(); ATT_SB();
;     ATT_KLOAD(1); ATT_SB();
;     if constexpr (LEAD) { ATT_EXP(); ATT_SUMPACK(); }
;     wait_bar<NDMA>();
;     int s_prev = 0, s_cur = 1, s_next = 2;
;     int one_ = 1; asm volatile("" : "+s"(one_));
	ds_read_b128 v[14:17], v174
	ds_read_b128 v[18:21], v174 offset:512
	v_add_u32_e32 v176, v170, v22
	s_waitcnt lgkmcnt(1)
	v_mfma_f32_16x16x32_bf16 v[28:31], v[14:17], v[6:9], 0
	ds_read_b128 v[40:43], v176
	ds_read_b128 v[44:47], v176 offset:512
	s_waitcnt lgkmcnt(0)
	s_barrier
	s_mov_b32 s4, 0
	v_mfma_f32_16x16x32_bf16 v[32:35], v[14:17], v[24:27], 0
	s_cselect_b64 vcc, -1, 0
	s_mov_b32 s7, s4
	v_mfma_f32_16x16x32_bf16 v[36:39], v[14:17], v[56:59], 0
	v_mfma_f32_16x16x32_bf16 v[14:17], v[14:17], v[76:79], 0
	s_waitcnt lgkmcnt(1)
	v_mfma_f32_16x16x32_bf16 v[116:119], v[40:43], v[84:87], v[14:17]
	v_mfma_f32_16x16x32_bf16 v[14:17], v[18:21], v[6:9], 0
	v_mfma_f32_16x16x32_bf16 v[144:147], v[40:43], v[2:5], v[28:31]
	v_mfma_f32_16x16x32_bf16 v[140:143], v[40:43], v[10:13], v[32:35]
	v_mfma_f32_16x16x32_bf16 v[28:31], v[18:21], v[24:27], 0
	v_mfma_f32_16x16x32_bf16 v[32:35], v[18:21], v[56:59], 0
	v_mfma_f32_16x16x32_bf16 v[18:21], v[18:21], v[76:79], 0
	s_waitcnt lgkmcnt(0)
	v_mfma_f32_16x16x32_bf16 v[136:139], v[44:47], v[2:5], v[14:17]
	s_nop 2
	v_lshl_add_u64 v[14:15], v[164:165], 0, s[96:97]
	s_mov_b32 s5, m0
	s_mov_b32 m0, s50
	s_nop 0
	global_load_lds_dwordx4 v[14:15], off
	s_mov_b32 m0, s5
	v_mfma_f32_16x16x32_bf16 v[128:131], v[40:43], v[60:63], v[36:39]
	v_lshl_add_u64 v[14:15], v[166:167], 0, s[66:67]
	s_add_i32 s5, s45, 0x2000
	s_mov_b32 s6, m0
	s_mov_b32 m0, s5
	s_nop 0
	global_load_lds_dwordx4 v[14:15], off
	s_mov_b32 m0, s6
	v_mfma_f32_16x16x32_bf16 v[132:135], v[44:47], v[10:13], v[28:31]
	s_mov_b32 s6, s4
	s_mov_b32 s5, s4
	v_mov_b64_e32 v[16:17], s[6:7]
	v_mfma_f32_16x16x32_bf16 v[124:127], v[44:47], v[60:63], v[32:35]
	v_mov_b64_e32 v[14:15], s[4:5]
	v_mfma_f32_16x16x32_bf16 v[120:123], v[44:47], v[84:87], v[18:21]
	ds_read_b128 v[100:103], v174 offset:8192
	ds_read_b128 v[108:111], v174 offset:8704
	ds_read_b128 v[104:107], v176 offset:8192
	ds_read_b128 v[112:115], v176 offset:8704
	v_cndmask_b32_e32 v18, v22, v168, vcc
	v_add3_u32 v175, 0, v163, v18
	s_waitcnt vmcnt(2) lgkmcnt(0)
	s_barrier
	s_mov_b32 s5, 1
	v_mov_b32_e32 v22, 0
	s_cmp_lg_u32 s5, 0
	v_mov_b64_e32 v[20:21], v[16:17]
	v_mov_b64_e32 v[30:31], v[16:17]
	v_mov_b64_e32 v[34:35], v[16:17]
	v_mov_b64_e32 v[38:39], v[16:17]
	v_mov_b64_e32 v[42:43], v[16:17]
	v_mov_b64_e32 v[46:47], v[16:17]
	v_mov_b64_e32 v[50:51], v[16:17]
	v_mov_b64_e32 v[54:55], v[16:17]
	v_mov_b64_e32 v[66:67], v[16:17]
	v_mov_b64_e32 v[70:71], v[16:17]
	v_mov_b64_e32 v[74:75], v[16:17]
	v_mov_b64_e32 v[82:83], v[16:17]
	v_mov_b64_e32 v[90:91], v[16:17]
	v_mov_b64_e32 v[94:95], v[16:17]
	v_mov_b64_e32 v[98:99], v[16:17]
	s_cselect_b64 s[6:7], -1, 0
	v_mov_b64_e32 v[18:19], v[14:15]
	v_mov_b64_e32 v[28:29], v[14:15]
	v_mov_b64_e32 v[32:33], v[14:15]
	v_mov_b64_e32 v[36:37], v[14:15]
	v_mov_b64_e32 v[40:41], v[14:15]
	v_mov_b64_e32 v[44:45], v[14:15]
	v_mov_b64_e32 v[48:49], v[14:15]
	v_mov_b64_e32 v[52:53], v[14:15]
	v_mov_b64_e32 v[64:65], v[14:15]
	v_mov_b64_e32 v[68:69], v[14:15]
	v_mov_b64_e32 v[72:73], v[14:15]
	v_mov_b64_e32 v[80:81], v[14:15]
	v_mov_b64_e32 v[88:89], v[14:15]
	v_mov_b64_e32 v[92:93], v[14:15]
	v_mov_b64_e32 v[96:97], v[14:15]
	s_mov_b32 s38, 2
	v_mov_b32_e32 v23, v22
	v_mov_b32_e32 v168, v22
	v_mov_b32_e32 v169, v22

; #define LAS __attribute__((address_space(3)))
; #define ATT_DMA_K(t, sl) do { glds16(ksrc + (size_t)(t) * 64 * kpitch, (unsigned)__builtin_amdgcn_readfirstlane(kdst + (sl) * KSLOT)); \
;         if constexpr (DQK == 96) glds16(krsrc + (size_t)(t) * 64 * 32, (unsigned)__builtin_amdgcn_readfirstlane(krdst + (sl) * KSLOT)); } while (0)
; template <int DQK, int DV, bool LEAD> ...
;     ...
;     const int kr0 = 8 * (q16 >> 2) + (q16 & 3);
;     const int fk = ((kr0 >> 1) & 1) | (((kr0 >> 3) & 1) << 1) | (((kr0 >> 4) & 1) << 2);
;     const LAS unsigned char* kp[2]; const LAS unsigned char* vp[2];
; #pragma unroll
;     for (int ds = 0; ds < 2; ++ds) kp[ds] = shm + KOFF + kr0 * 128 + ((((ds << 2) | g4) ^ fk) << 4) + kg * 4096;
;     const LAS unsigned char* krp = shm + KOFF + 8192 + kr0 * 64 + ((g4 ^ (((kr0 >> 4) & 1) << 1)) << 4) + kg * 2048;
; #pragma unroll
;     for (int s_ = 0; s_ < 2; ++s_) vp[s_] = shm + VOFF + q16 * 128 + ((((s_ << 2) | g4) ^ ((q16 >> 1) & 7)) << 4);
;     const LAS unsigned char* vpk = kg ? vp[1] : vp[0];
;     ...
;     ATT_DMA_K(0, 0); ATT_DMA_V(0, 0); ATT_DMA_K(1, 1); ATT_DMA_K(2, 2);
;     bf16x8 qf[NQB * NDS];
;     {
;       const float c2 = (DQK == 64) ? C2_EVEN : C2_ODD; const bool lat = tq0 >= 0;
; #pragma unroll
;       for (int qb = 0; qb < NQB; ++qb) {
;           const bf16_t* qp = Q + (size_t)(qrow0 + qoff + qb * 16 + q16) * qpitch + g4 * 8;
;           bf16x8 raw[NDS];
; #pragma unroll
;           for (int ds = 0; ds < NDS; ++ds) raw[ds] = *(const bf16x8*)(qp + ds * 32);
;           float x[NDS][8];
; #pragma unroll
;           for (int ds = 0; ds < NDS; ++ds)
; #pragma unroll
;               for (int j = 0; j < 8; ++j) x[ds][j] = __uint_as_float(((unsigned)(unsigned short)raw[ds][j]) << 16);
;           const int tq = tq0 + qoff + qb * 16 + q16, prow = (tq >> 6) & 127, pcol = tq & 63;
;           float sn = 0.f;
; #pragma unroll
;           for (int ds = 0; ds < 2; ++ds)
; #pragma unroll
;               for (int j = 0; j < 8; ++j) sn += x[ds][j] * x[ds][j];
;           sn = lanes4_sum(sn);
;           const float rn = rsqrtf(sn * (1.f / 64.f) + EPS);
; #pragma unroll
;           for (int ds = 0; ds < 2; ++ds)
; #pragma unroll
;               for (int j = 0; j < 8; ++j) x[ds][j] *= rn * qgain[32 * ds + 8 * g4 + j];
.LBB0_962:
	s_and_b64 vcc, exec, s[4:5]
	s_cbranch_vccz .LBB0_954
	v_mov_b32_e32 v168, v0
	s_ashr_i32 s45, s44, 31
	v_readfirstlane_b32 s16, v168
	s_ashr_i32 s4, s16, 6
	v_bfe_u32 v1, v168, 3, 3
	v_lshl_or_b32 v7, s4, 3, v1
	s_lshl_b32 s5, s4, 1
	s_lshr_b32 s6, s16, 5
	v_ashrrev_i32_e32 v2, 1, v7
	s_and_b32 s5, s5, 2
	s_and_b32 s6, s6, 4
	v_and_b32_e32 v170, 7, v168
	v_and_b32_e32 v3, 1, v2
	s_or_b32 s5, s5, s6
	s_and_b32 s7, s4, 3
	v_bitop3_b32 v8, s5, v170, v3 bitop3:0x36
	v_xor_b32_e32 v9, v2, v168
	v_add_u32_e32 v4, s44, v7
	s_lshl_b32 s4, s4, 10
	v_mov_b64_e32 v[2:3], s[36:37]
	s_add_i32 s49, s4, 0
	v_mad_i64_i32 v[2:3], s[4:5], v4, s92, v[2:3]
	v_mov_b64_e32 v[4:5], s[40:41]
	v_lshlrev_b32_e32 v194, 4, v8
	v_mad_i64_i32 v[4:5], s[4:5], v7, s91, v[4:5]
	v_lshl_add_u64 v[162:163], v[2:3], 0, v[194:195]
	v_lshlrev_b32_e32 v2, 4, v9
	v_lshl_add_u64 v[4:5], s[44:45], 1, v[4:5]
	v_and_b32_e32 v194, 0x70, v2
	s_mov_b32 s4, m0
	s_mov_b32 m0, s49
	s_nop 0
	global_load_lds_dwordx4 v[162:163], off
	s_mov_b32 m0, s4
	v_lshl_add_u64 v[164:165], v[4:5], 0, v[194:195]
	s_add_i32 s36, s49, 0x9000
	s_mov_b32 s4, m0
	s_mov_b32 m0, s36
	s_nop 0
	global_load_lds_dwordx4 v[164:165], off
	s_mov_b32 m0, s4
	s_mov_b64 s[4:5], 0x38000
	s_lshl_b32 s37, s7, 6
	v_lshl_add_u64 v[2:3], v[162:163], 0, s[4:5]
	s_add_i32 s4, s49, 0x2000
	s_mov_b32 s5, m0
	s_mov_b32 m0, s4
	s_nop 0
	global_load_lds_dwordx4 v[2:3], off
	s_mov_b32 m0, s5
	v_and_b32_e32 v6, 15, v168
	s_mov_b64 s[4:5], 0x70000
	s_or_b32 s6, s37, s48
	v_and_b32_e32 v194, 48, v168
	s_waitcnt vmcnt(0)
	v_lshrrev_b32_e32 v40, 1, v168
	v_lshlrev_b32_e32 v173, 7, v6
	v_lshl_add_u64 v[2:3], v[162:163], 0, s[4:5]
	s_add_i32 s4, s49, 0x4000
	v_or_b32_e32 v22, s6, v6
	v_lshl_add_u64 v[6:7], s[28:29], 0, v[194:195]
	s_mov_b32 s5, m0
	s_mov_b32 m0, s4
	s_nop 0
	global_load_lds_dwordx4 v[2:3], off
	s_mov_b32 m0, s5
	v_and_b32_e32 v41, 8, v40
	v_mad_i64_i32 v[8:9], s[4:5], v22, s92, v[6:7]
	v_or_b32_e32 v10, 16, v22
	v_or_b32_e32 v18, 32, v22
	v_or_b32_e32 v22, 48, v22
	v_lshl_or_b32 v194, v41, 3, v173
	v_mad_i64_i32 v[16:17], s[4:5], v10, s92, v[6:7]
	v_mad_i64_i32 v[18:19], s[4:5], v18, s92, v[6:7]
	v_mad_i64_i32 v[34:35], s[4:5], v22, s92, v[6:7]
	v_lshl_add_u64 v[14:15], s[8:9], 0, v[194:195]
	s_mov_b64 s[4:5], 0x1800
	v_lshl_add_u64 v[36:37], v[14:15], 0, s[4:5]
	s_movk_i32 s4, 0x1000
	v_add_co_u32_e32 v38, vcc, s4, v14
	global_load_dwordx4 v[2:5], v194, s[8:9] offset:48
	v_lshl_add_u64 v[20:21], v[14:15], 0, s[60:61]
	v_addc_co_u32_e32 v39, vcc, 0, v15, vcc
	global_load_dwordx4 v[74:77], v[8:9], off offset:64 nt
	global_load_dwordx4 v[124:127], v[16:17], off offset:64 nt
	global_load_dwordx4 v[10:13], v194, s[8:9] offset:2096
	global_load_dwordx4 v[142:145], v[18:19], off offset:64 nt
	global_load_dwordx4 v[70:73], v[20:21], off offset:48
	global_load_dwordx4 v[154:157], v[34:35], off offset:64 nt
	global_load_dwordx4 v[26:29], v[36:37], off offset:48
	global_load_dwordx4 v[100:103], v194, s[8:9] offset:32
	global_load_dwordx4 v[92:95], v194, s[8:9] offset:2080
	global_load_dwordx4 v[66:69], v[20:21], off offset:32
	global_load_dwordx4 v[30:33], v[36:37], off offset:32
	global_load_dwordx4 v[108:111], v[8:9], off
	s_nop 0
	global_load_dwordx4 v[6:9], v194, s[8:9]
	global_load_dwordx4 v[104:107], v[16:17], off
	global_load_dwordx4 v[96:99], v194, s[8:9] offset:16
	global_load_dwordx4 v[80:83], v[18:19], off
	global_load_dwordx4 v[84:87], v194, s[8:9] offset:2064
	global_load_dwordx4 v[22:25], v[38:39], off
	s_nop 0
	global_load_dwordx4 v[14:17], v[34:35], off
	global_load_dwordx4 v[88:91], v194, s[8:9] offset:2048
	s_lshl_b32 s4, s16, 4
	global_load_dwordx4 v[18:21], v[20:21], off offset:16
	v_lshlrev_b32_e32 v172, 1, v168
	v_and_b32_e32 v34, 3, v168
	s_and_b32 s4, s4, 0xfffff000
	v_and_or_b32 v42, v172, 24, v34
	s_add_i32 s4, s4, 0
	v_lshl_add_u32 v169, v42, 7, s4
	s_or_b32 s4, s47, s37
	v_bfe_u32 v171, v168, 4, 2
	s_lshr_b32 s4, s4, 2
	v_bitop3_b32 v40, v171, v40, 7 bitop3:0x78
	s_and_b32 s4, s4, 0x7f0
	v_lshlrev_b32_e32 v177, 4, v40
	v_or_b32_e32 v40, s4, v41
	v_lshlrev_b32_e32 v40, 3, v40
	global_load_dwordx4 v[34:37], v[36:37], off offset:16
	v_lshlrev_b32_e32 v78, 5, v171
	global_load_dwordx4 v[42:45], v40, s[8:9] offset:48
	global_load_dwordx4 v[46:49], v40, s[8:9] offset:32
	global_load_dwordx4 v[50:53], v40, s[8:9] offset:16
	global_load_dwordx4 v[54:57], v40, s[8:9]
	s_nop 0
	global_load_dwordx4 v[38:41], v[38:39], off offset:2048
	s_nop 0
	global_load_dwordx4 v[58:61], v78, s[26:27] offset:144
	global_load_dwordx4 v[62:65], v78, s[26:27] offset:128
	v_and_b32_e32 v174, 63, v168
	v_cmp_gt_u32_e32 vcc, 32, v174
	s_mov_b32 s4, 0x358637bd
	s_mov_b32 s12, 0x3c800000
	v_add_u32_e32 v175, v169, v177
	s_mov_b32 s28, 1
	v_or_b32_e32 v176, 4, v171
	s_mov_b32 s29, 0
	s_waitcnt vmcnt(22)
	v_cndmask_b32_e64 v113, v29, -v29, vcc
	v_cndmask_b32_e64 v146, v3, -v3, vcc
	v_mov_b32_e32 v3, v4
	v_cndmask_b32_e64 v147, v5, -v5, vcc
	s_waitcnt vmcnt(20)
	v_cndmask_b32_e64 v133, v95, -v95, vcc
	s_waitcnt vmcnt(17)
	v_and_b32_e32 v181, 0xffff0000, v108
	v_lshlrev_b32_e32 v180, 16, v108
	v_mul_f32_e32 v4, v181, v181
	v_and_b32_e32 v131, 0xffff0000, v127
	v_lshlrev_b32_e32 v130, 16, v127
	v_cndmask_b32_e64 v129, v13, -v13, vcc
	v_cndmask_b32_e64 v128, v11, -v11, vcc
	v_mov_b32_e32 v11, v12
	v_and_b32_e32 v119, 0xffff0000, v145
	v_lshlrev_b32_e32 v118, 16, v145
	v_and_b32_e32 v115, 0xffff0000, v157
	v_lshlrev_b32_e32 v114, 16, v157
	v_cndmask_b32_e64 v13, v103, -v103, vcc
	v_cndmask_b32_e64 v12, v101, -v101, vcc
	v_mov_b32_e32 v101, v102
	v_and_b32_e32 v135, 0xffff0000, v126
	v_lshlrev_b32_e32 v134, 16, v126
	v_cndmask_b32_e64 v132, v93, -v93, vcc
	v_mov_b32_e32 v93, v94
	v_and_b32_e32 v103, 0xffff0000, v144
	v_lshlrev_b32_e32 v102, 16, v144
	v_cndmask_b32_e64 v95, v69, -v69, vcc
	v_cndmask_b32_e64 v94, v67, -v67, vcc
	v_mov_b32_e32 v67, v68
	v_and_b32_e32 v69, 0xffff0000, v156
	v_lshlrev_b32_e32 v68, 16, v156
	s_waitcnt vmcnt(14)
; template <int DQK, int DV, bool LEAD> ...
;     ...
;           float x[NDS][8];
; #pragma unroll
;           for (int ds = 0; ds < NDS; ++ds)
; #pragma unroll
;               for (int j = 0; j < 8; ++j) x[ds][j] = __uint_as_float(((unsigned)(unsigned short)raw[ds][j]) << 16);
;           const int tq = tq0 + qoff + qb * 16 + q16, prow = (tq >> 6) & 127, pcol = tq & 63;
;           float sn = 0.f;
; #pragma unroll
;           for (int ds = 0; ds < 2; ++ds)
; #pragma unroll
;               for (int j = 0; j < 8; ++j) sn += x[ds][j] * x[ds][j];
;           sn = lanes4_sum(sn);
;           const float rn = rsqrtf(sn * (1.f / 64.f) + EPS);
; #pragma unroll
;           for (int ds = 0; ds < 2; ++ds)
; #pragma unroll
;               for (int j = 0; j < 8; ++j) x[ds][j] *= rn * qgain[32 * ds + 8 * g4 + j];
;           if constexpr (DQK == 64) {
; #pragma unroll
;               for (int ds = 0; ds < 2; ++ds)
; #pragma unroll
;                   for (int j = 0; j < 8; ++j) {
;                       auto rr = __builtin_amdgcn_permlane32_swap(__float_as_uint(x[ds][j]), __float_as_uint(x[ds][j]), false, false);
;                       const float other = hi ? __uint_as_float(rr[0]) : __uint_as_float(rr[1]);
;                       float cc = 1.f, sg = 0.f;
;                       if (lat) { const f32x2 cs = rope[(ds ? pcol : prow) * 16 + 8 * (g4 & 1) + j]; cc = cs.x; sg = hi ? cs.y : -cs.y; }
;                       x[ds][j] = x[ds][j] * cc + other * sg; }
	v_cndmask_b32_e64 v157, v99, -v99, vcc
	v_cndmask_b32_e64 v156, v97, -v97, vcc
	v_mov_b32_e32 v97, v98
	v_and_b32_e32 v139, 0xffff0000, v125
	v_lshlrev_b32_e32 v138, 16, v125
	v_and_b32_e32 v123, 0xffff0000, v143
	v_lshlrev_b32_e32 v122, 16, v143
	v_and_b32_e32 v141, 0xffff0000, v124
	v_lshlrev_b32_e32 v140, 16, v124
	v_and_b32_e32 v127, 0xffff0000, v142
	v_lshlrev_b32_e32 v126, 16, v142
	s_waitcnt vmcnt(11)
	v_cndmask_b32_e64 v125, v25, -v25, vcc
	v_cndmask_b32_e64 v124, v23, -v23, vcc
	v_mov_b32_e32 v23, v24
	v_and_b32_e32 v143, 0xffff0000, v107
	v_lshlrev_b32_e32 v142, 16, v107
	v_and_b32_e32 v25, 0xffff0000, v83
	v_lshlrev_b32_e32 v24, 16, v83
	s_waitcnt vmcnt(10)
	v_and_b32_e32 v99, 0xffff0000, v17
	v_lshlrev_b32_e32 v98, 16, v17
	v_and_b32_e32 v145, 0xffff0000, v106
	v_lshlrev_b32_e32 v144, 16, v106
	v_and_b32_e32 v107, 0xffff0000, v82
	v_lshlrev_b32_e32 v106, 16, v82
	v_and_b32_e32 v83, 0xffff0000, v16
	v_lshlrev_b32_e32 v82, 16, v16
	v_and_b32_e32 v17, 0xffff0000, v109
	v_lshlrev_b32_e32 v16, 16, v109
	v_pk_fma_f32 v[4:5], v[180:181], v[180:181], v[4:5] op_sel_hi:[1,1,0]
	v_and_b32_e32 v151, 0xffff0000, v77
	v_lshlrev_b32_e32 v150, 16, v77
	v_cndmask_b32_e64 v117, v73, -v73, vcc
	v_cndmask_b32_e64 v116, v71, -v71, vcc
	v_mov_b32_e32 v71, v72
	v_and_b32_e32 v153, 0xffff0000, v76
	v_lshlrev_b32_e32 v152, 16, v76
	v_and_b32_e32 v159, 0xffff0000, v75
	v_lshlrev_b32_e32 v158, 16, v75
	v_and_b32_e32 v167, 0xffff0000, v74
	v_lshlrev_b32_e32 v166, 16, v74
	global_load_dwordx4 v[72:75], v78, s[26:27] offset:16
	s_nop 0
	global_load_dwordx4 v[76:79], v78, s[26:27]
	v_pk_fma_f32 v[4:5], v[16:17], v[16:17], v[4:5]
	v_mul_f32_e32 v108, v17, v17
	v_and_b32_e32 v179, 0xffff0000, v110
	v_lshlrev_b32_e32 v178, 16, v110
	v_pk_add_f32 v[4:5], v[108:109], v[4:5] op_sel_hi:[0,1]
	v_pk_fma_f32 v[4:5], v[178:179], v[178:179], v[4:5]
	v_mul_f32_e32 v108, v179, v179
	v_cndmask_b32_e64 v161, v9, -v9, vcc
	v_cndmask_b32_e64 v160, v7, -v7, vcc
	v_mov_b32_e32 v7, v8
	v_and_b32_e32 v9, 0xffff0000, v111
	v_lshlrev_b32_e32 v8, 16, v111
	v_pk_add_f32 v[4:5], v[108:109], v[4:5] op_sel_hi:[0,1]
	v_pk_fma_f32 v[4:5], v[8:9], v[8:9], v[4:5]
	v_mul_f32_e32 v108, v9, v9
	v_pk_add_f32 v[4:5], v[108:109], v[4:5] op_sel_hi:[0,1]
	v_pk_fma_f32 v[4:5], v[166:167], v[166:167], v[4:5]
	v_mul_f32_e32 v108, v167, v167
	v_pk_add_f32 v[4:5], v[108:109], v[4:5] op_sel_hi:[0,1]
	v_pk_fma_f32 v[4:5], v[158:159], v[158:159], v[4:5]
	v_mul_f32_e32 v108, v159, v159
	v_pk_add_f32 v[4:5], v[108:109], v[4:5] op_sel_hi:[0,1]
	v_pk_fma_f32 v[4:5], v[152:153], v[152:153], v[4:5]
	v_mul_f32_e32 v108, v153, v153
	v_pk_add_f32 v[4:5], v[108:109], v[4:5] op_sel_hi:[0,1]
	v_pk_fma_f32 v[4:5], v[150:151], v[150:151], v[4:5]
	v_mul_f32_e32 v108, v151, v151
	v_pk_add_f32 v[4:5], v[108:109], v[4:5] op_sel_hi:[0,1]
	v_mov_b32_e32 v5, v4
	s_nop 1
	v_permlane16_swap_b32_e32 v4, v5
	v_add_f32_e32 v5, v4, v5
	v_cndmask_b32_e64 v137, v87, -v87, vcc
	v_cndmask_b32_e64 v136, v85, -v85, vcc
	v_mov_b32_e32 v85, v86
	v_and_b32_e32 v87, 0xffff0000, v155
	v_lshlrev_b32_e32 v86, 16, v155
	v_and_b32_e32 v149, 0xffff0000, v105
	v_lshlrev_b32_e32 v148, 16, v105
	v_mov_b32_e32 v105, v5
	v_and_b32_e32 v155, 0xffff0000, v104
	s_waitcnt vmcnt(10)
	v_cndmask_b32_e64 v121, v21, -v21, vcc
	v_cndmask_b32_e64 v120, v19, -v19, vcc
	v_mov_b32_e32 v19, v20
	v_cndmask_b32_e64 v21, v91, -v91, vcc
	v_cndmask_b32_e64 v20, v89, -v89, vcc
	v_mov_b32_e32 v89, v90
	v_and_b32_e32 v91, 0xffff0000, v154
	v_lshlrev_b32_e32 v90, 16, v154
	v_permlane32_swap_b32_e32 v5, v105
	v_lshlrev_b32_e32 v154, 16, v104
	v_mul_f32_e32 v4, v155, v155
	v_pk_fma_f32 v[108:109], v[154:155], v[154:155], v[4:5] op_sel_hi:[1,1,0]
	v_mul_f32_e32 v4, v149, v149
	v_pk_fma_f32 v[108:109], v[148:149], v[148:149], v[108:109]
	v_cndmask_b32_e64 v112, v27, -v27, vcc
	v_pk_add_f32 v[108:109], v[4:5], v[108:109] op_sel_hi:[0,1]
	v_pk_fma_f32 v[108:109], v[144:145], v[144:145], v[108:109]
	v_mul_f32_e32 v4, v145, v145
	v_pk_add_f32 v[108:109], v[4:5], v[108:109] op_sel_hi:[0,1]
	v_pk_fma_f32 v[108:109], v[142:143], v[142:143], v[108:109]
	v_mul_f32_e32 v4, v143, v143
	v_pk_add_f32 v[108:109], v[4:5], v[108:109] op_sel_hi:[0,1]
	v_pk_fma_f32 v[108:109], v[140:141], v[140:141], v[108:109]
	v_mul_f32_e32 v4, v141, v141
	v_pk_add_f32 v[108:109], v[4:5], v[108:109] op_sel_hi:[0,1]
	v_pk_fma_f32 v[108:109], v[138:139], v[138:139], v[108:109]
	v_mul_f32_e32 v4, v139, v139
	v_pk_add_f32 v[108:109], v[4:5], v[108:109] op_sel_hi:[0,1]
	v_pk_fma_f32 v[108:109], v[134:135], v[134:135], v[108:109]
	v_mul_f32_e32 v4, v135, v135
	v_pk_add_f32 v[108:109], v[4:5], v[108:109] op_sel_hi:[0,1]
	v_pk_fma_f32 v[108:109], v[130:131], v[130:131], v[108:109]
	v_mul_f32_e32 v4, v131, v131
	v_pk_add_f32 v[108:109], v[4:5], v[108:109] op_sel_hi:[0,1]
	v_mov_b32_e32 v4, v108
	s_nop 1
	v_permlane16_swap_b32_e32 v108, v4
	v_add_f32_e32 v4, v108, v4
	v_mov_b32_e32 v104, v4
	s_nop 1
	v_permlane32_swap_b32_e32 v4, v104
	v_pk_add_f32 v[4:5], v[4:5], v[104:105]
	v_mov_b64_e32 v[108:109], s[4:5]
	v_pk_fma_f32 v[182:183], v[4:5], s[12:13], v[108:109] op_sel_hi:[1,0,0]
	s_waitcnt vmcnt(5)
	v_cndmask_b32_e64 v104, v55, -v55, vcc
	v_mul_f32_e32 v4, 0x4b800000, v183
	v_cmp_gt_f32_e64 s[4:5], s95, v183
	v_mov_b32_e32 v55, v56
	v_mov_b32_e32 v27, v28
	v_cndmask_b32_e64 v4, v183, v4, s[4:5]
	v_rsq_f32_e32 v4, v4
	v_cndmask_b32_e64 v29, v33, -v33, vcc
	v_cndmask_b32_e64 v28, v31, -v31, vcc
	v_mov_b32_e32 v31, v32
	v_mul_f32_e32 v5, 0x45800000, v4
	v_cndmask_b32_e64 v56, v4, v5, s[4:5]
	s_waitcnt vmcnt(3)
; __device__ __forceinline__ unsigned cvtpk(float lo, float hi) { f32x2 v = {lo, hi}; bf16x2_t b = __builtin_convertvector(v, bf16x2_t); return __builtin_bit_cast(unsigned, b); }
; template <int DQK, int DV, bool LEAD> ...
;     ...
; #pragma unroll
;           for (int ds = 0; ds < 2; ++ds)
; #pragma unroll
;               for (int j = 0; j < 8; ++j) x[ds][j] *= rn * qgain[32 * ds + 8 * g4 + j];
;           if constexpr (DQK == 64) {
; #pragma unroll
;               for (int ds = 0; ds < 2; ++ds)
; #pragma unroll
;                   for (int j = 0; j < 8; ++j) {
;                       auto rr = __builtin_amdgcn_permlane32_swap(__float_as_uint(x[ds][j]), __float_as_uint(x[ds][j]), false, false);
;                       const float other = hi ? __uint_as_float(rr[0]) : __uint_as_float(rr[1]);
;                       float cc = 1.f, sg = 0.f;
;                       if (lat) { const f32x2 cs = rope[(ds ? pcol : prow) * 16 + 8 * (g4 & 1) + j]; cc = cs.x; sg = hi ? cs.y : -cs.y; }
;                       x[ds][j] = x[ds][j] * cc + other * sg; }
;           } else {
;               float sr = 0.f;
; #pragma unroll
;               for (int j = 0; j < 8; ++j) sr += x[2][j] * x[2][j];
;               sr = lanes4_sum(sr);
;               const float rq = rsqrtf(sr * (1.f / 32.f) + EPS);
; #pragma unroll
;               for (int j = 0; j < 8; ++j) { const float av = x[2][j] * rq * qgain[64 + 8 * g4 + j];
;                   auto rr = __builtin_amdgcn_permlane16_swap(__float_as_uint(av), __float_as_uint(av), false, false);
;                   const float other = (g4 & 1) ? __uint_as_float(rr[0]) : __uint_as_float(rr[1]);
;                   float cc = 1.f, sg = 0.f;
;                   if (lat) { const f32x2 cs = rope[((g4 & 2) ? pcol : prow) * 8 + j]; cc = cs.x; sg = (g4 & 1) ? cs.y : -cs.y; }
;                   x[2][j] = av * cc + other * sg; }
;           }
; #pragma unroll
;           for (int ds = 0; ds < NDS; ++ds) { u32x4 w;
; #pragma unroll
;               for (int i = 0; i < 4; ++i) w[i] = cvtpk(x[ds][2 * i] * c2, x[ds][2 * i + 1] * c2);
;               qf[qb * NDS + ds] = __builtin_bit_cast(bf16x8, w); }
	v_pk_mul_f32 v[4:5], v[56:57], v[60:61] op_sel_hi:[0,1]
	v_pk_mul_f32 v[4:5], v[4:5], v[150:151]
	v_cndmask_b32_e64 v33, v37, -v37, vcc
	v_cndmask_b32_e64 v32, v35, -v35, vcc
	v_mov_b32_e32 v35, v36
	v_cndmask_b32_e64 v37, v41, -v41, vcc
	v_cndmask_b32_e64 v36, v39, -v39, vcc
	v_mov_b32_e32 v39, v40
	v_cndmask_b32_e64 v41, v45, -v45, vcc
	v_cndmask_b32_e64 v40, v43, -v43, vcc
	v_mov_b32_e32 v43, v44
	v_cndmask_b32_e64 v45, v49, -v49, vcc
	v_cndmask_b32_e64 v44, v47, -v47, vcc
	v_mov_b32_e32 v47, v48
	v_cndmask_b32_e64 v49, v53, -v53, vcc
	v_cndmask_b32_e64 v48, v51, -v51, vcc
	v_mov_b32_e32 v51, v52
	v_and_b32_e32 v111, 0xffff0000, v81
	v_lshlrev_b32_e32 v110, 16, v81
	v_and_b32_e32 v53, 0xffff0000, v15
	v_lshlrev_b32_e32 v52, 16, v15
	v_cndmask_b32_e64 v105, v57, -v57, vcc
	v_mov_b32_e32 v15, v4
	v_mov_b32_e32 v57, v4
	v_mov_b32_e32 v81, v5
	v_mov_b32_e32 v150, v5
	v_permlane32_swap_b32_e32 v15, v57
	s_nop 0
	v_permlane32_swap_b32_e32 v81, v150
	v_cndmask_b32_e32 v151, v81, v150, vcc
	v_cndmask_b32_e32 v150, v15, v57, vcc
	v_pk_mul_f32 v[146:147], v[146:147], v[150:151]
	v_cmp_gt_f32_e64 s[4:5], s95, v182
	v_pk_fma_f32 v[2:3], v[4:5], v[2:3], v[146:147]
	s_lshl_b32 s26, s46, 8
	v_pk_mul_f32 v[2:3], v[2:3], s[94:95] op_sel_hi:[1,0]
	s_cmpk_lt_u32 s16, 0x100
	v_cvt_pk_bf16_f32 v5, v2, v3
	v_pk_mul_f32 v[2:3], v[56:57], v[58:59] op_sel_hi:[0,1]
	v_pk_mul_f32 v[2:3], v[2:3], v[152:153]
	s_mov_b32 s27, 2
	v_mov_b32_e32 v4, v2
	v_mov_b32_e32 v15, v2
	v_mov_b32_e32 v57, v3
	v_mov_b32_e32 v81, v3
	v_permlane32_swap_b32_e32 v4, v15
	s_nop 0
	v_permlane32_swap_b32_e32 v57, v81
	v_cndmask_b32_e32 v147, v57, v81, vcc
	v_cndmask_b32_e32 v146, v4, v15, vcc
	v_pk_mul_f32 v[12:13], v[12:13], v[146:147]
	s_nop 0
	v_pk_fma_f32 v[2:3], v[2:3], v[100:101], v[12:13]
	s_nop 0
	v_pk_mul_f32 v[2:3], v[2:3], s[94:95] op_sel_hi:[1,0]
	s_nop 0
	v_cvt_pk_bf16_f32 v4, v2, v3
	s_waitcnt vmcnt(2)
	v_pk_mul_f32 v[2:3], v[56:57], v[64:65] op_sel_hi:[0,1]
	v_pk_mul_f32 v[2:3], v[2:3], v[158:159]
	s_nop 0
	v_mov_b32_e32 v12, v2
	v_mov_b32_e32 v15, v2
	v_mov_b32_e32 v13, v3
	v_mov_b32_e32 v57, v3
	v_permlane32_swap_b32_e32 v12, v15
	s_nop 0
	v_permlane32_swap_b32_e32 v13, v57
	v_cndmask_b32_e32 v13, v13, v57, vcc
	v_cndmask_b32_e32 v12, v12, v15, vcc
	v_pk_mul_f32 v[12:13], v[156:157], v[12:13]
	s_nop 0
	v_pk_fma_f32 v[2:3], v[2:3], v[96:97], v[12:13]
	v_pk_mul_f32 v[12:13], v[62:63], v[56:57] op_sel_hi:[1,0]
	v_pk_mul_f32 v[2:3], v[2:3], s[94:95] op_sel_hi:[1,0]
	v_pk_mul_f32 v[12:13], v[12:13], v[166:167]
	v_cvt_pk_bf16_f32 v3, v2, v3
	v_mov_b32_e32 v2, v12
	v_mov_b32_e32 v15, v12
	v_mov_b32_e32 v57, v13
	v_mov_b32_e32 v81, v13
	v_permlane32_swap_b32_e32 v2, v15
	s_nop 0
	v_permlane32_swap_b32_e32 v57, v81
	v_cndmask_b32_e32 v97, v57, v81, vcc
	v_cndmask_b32_e32 v96, v2, v15, vcc
	v_pk_mul_f32 v[96:97], v[160:161], v[96:97]
	s_nop 0
	v_pk_fma_f32 v[6:7], v[12:13], v[6:7], v[96:97]
	s_nop 0
	v_pk_mul_f32 v[6:7], v[6:7], s[94:95] op_sel_hi:[1,0]
	s_nop 0
	v_cvt_pk_bf16_f32 v2, v6, v7
	s_waitcnt vmcnt(1)
	v_pk_mul_f32 v[6:7], v[74:75], v[56:57] op_sel_hi:[1,0]
	s_nop 0
	v_pk_mul_f32 v[6:7], v[6:7], v[8:9]
	s_nop 0
	v_mov_b32_e32 v8, v6
	v_mov_b32_e32 v12, v6
	v_mov_b32_e32 v9, v7
	v_mov_b32_e32 v13, v7
	v_permlane32_swap_b32_e32 v8, v12
	s_nop 0
	v_permlane32_swap_b32_e32 v9, v13
	v_cndmask_b32_e32 v9, v9, v13, vcc
	v_cndmask_b32_e32 v8, v8, v12, vcc
	v_pk_mul_f32 v[8:9], v[40:41], v[8:9]
	s_nop 0
	v_pk_fma_f32 v[6:7], v[6:7], v[42:43], v[8:9]
	s_nop 0
	v_pk_mul_f32 v[6:7], v[6:7], s[94:95] op_sel_hi:[1,0]
	s_nop 0
	v_cvt_pk_bf16_f32 v9, v6, v7
	v_pk_mul_f32 v[6:7], v[72:73], v[56:57] op_sel_hi:[1,0]
	s_nop 0
	v_pk_mul_f32 v[6:7], v[6:7], v[178:179]
	s_nop 0
	v_mov_b32_e32 v8, v6
	v_mov_b32_e32 v12, v6
	v_mov_b32_e32 v13, v7
	v_mov_b32_e32 v15, v7
	v_permlane32_swap_b32_e32 v8, v12
	s_nop 0
	v_permlane32_swap_b32_e32 v13, v15
	v_cndmask_b32_e32 v13, v13, v15, vcc
	v_cndmask_b32_e32 v12, v8, v12, vcc
	v_pk_mul_f32 v[12:13], v[44:45], v[12:13]
	s_nop 0
	v_pk_fma_f32 v[6:7], v[6:7], v[46:47], v[12:13]
	s_nop 0
	v_pk_mul_f32 v[6:7], v[6:7], s[94:95] op_sel_hi:[1,0]
	s_nop 0
	v_cvt_pk_bf16_f32 v8, v6, v7
	s_waitcnt vmcnt(0)
	v_pk_mul_f32 v[6:7], v[78:79], v[56:57] op_sel_hi:[1,0]
	s_nop 0
	v_pk_mul_f32 v[6:7], v[6:7], v[16:17]
	s_nop 0
	v_mov_b32_e32 v12, v6
	v_mov_b32_e32 v15, v6
	v_mov_b32_e32 v13, v7
	v_mov_b32_e32 v16, v7
	v_permlane32_swap_b32_e32 v12, v15
	s_nop 0
	v_permlane32_swap_b32_e32 v13, v16
	v_cndmask_b32_e32 v13, v13, v16, vcc
	v_cndmask_b32_e32 v12, v12, v15, vcc
	v_pk_mul_f32 v[12:13], v[48:49], v[12:13]
	s_nop 0
	v_pk_fma_f32 v[6:7], v[6:7], v[50:51], v[12:13]
	v_pk_mul_f32 v[12:13], v[76:77], v[56:57] op_sel_hi:[1,0]
	v_pk_mul_f32 v[6:7], v[6:7], s[94:95] op_sel_hi:[1,0]
	v_pk_mul_f32 v[12:13], v[12:13], v[180:181]
	v_cvt_pk_bf16_f32 v7, v6, v7
	v_mov_b32_e32 v6, v12
	v_mov_b32_e32 v15, v12
	v_mov_b32_e32 v16, v13
	v_mov_b32_e32 v17, v13
	v_permlane32_swap_b32_e32 v6, v15
	s_nop 0
	v_permlane32_swap_b32_e32 v16, v17
	v_cndmask_b32_e32 v17, v16, v17, vcc
	v_cndmask_b32_e32 v16, v6, v15, vcc
	v_mul_f32_e32 v6, 0x4b800000, v182
	v_cndmask_b32_e64 v6, v182, v6, s[4:5]
	v_rsq_f32_e32 v15, v6
	v_pk_mul_f32 v[16:17], v[104:105], v[16:17]
	s_nop 0
	v_pk_fma_f32 v[12:13], v[12:13], v[54:55], v[16:17]
	s_nop 0
	v_pk_mul_f32 v[12:13], v[12:13], s[94:95] op_sel_hi:[1,0]
	s_nop 0
	v_cvt_pk_bf16_f32 v6, v12, v13
	v_mul_f32_e32 v12, 0x45800000, v15
	v_cndmask_b32_e64 v56, v15, v12, s[4:5]
	v_pk_mul_f32 v[12:13], v[60:61], v[56:57] op_sel_hi:[1,0]
	s_nop 0
	v_pk_mul_f32 v[12:13], v[12:13], v[130:131]
	s_nop 0
	v_mov_b32_e32 v15, v12
	v_mov_b32_e32 v16, v12
	v_mov_b32_e32 v17, v13
; template <int DQK, int DV, bool LEAD> ...
;     ...
;           float sn = 0.f;
; #pragma unroll
;           for (int ds = 0; ds < 2; ++ds)
; #pragma unroll
;               for (int j = 0; j < 8; ++j) sn += x[ds][j] * x[ds][j];
;           sn = lanes4_sum(sn);
;           const float rn = rsqrtf(sn * (1.f / 64.f) + EPS);
; #pragma unroll
;           for (int ds = 0; ds < 2; ++ds)
; #pragma unroll
;               for (int j = 0; j < 8; ++j) x[ds][j] *= rn * qgain[32 * ds + 8 * g4 + j];
;           if constexpr (DQK == 64) {
; #pragma unroll
;               for (int ds = 0; ds < 2; ++ds)
; #pragma unroll
;                   for (int j = 0; j < 8; ++j) {
;                       auto rr = __builtin_amdgcn_permlane32_swap(__float_as_uint(x[ds][j]), __float_as_uint(x[ds][j]), false, false);
;                       const float other = hi ? __uint_as_float(rr[0]) : __uint_as_float(rr[1]);
;                       float cc = 1.f, sg = 0.f;
;                       if (lat) { const f32x2 cs = rope[(ds ? pcol : prow) * 16 + 8 * (g4 & 1) + j]; cc = cs.x; sg = hi ? cs.y : -cs.y; }
;                       x[ds][j] = x[ds][j] * cc + other * sg; }
;           } else {
;               float sr = 0.f;
; #pragma unroll
;               for (int j = 0; j < 8; ++j) sr += x[2][j] * x[2][j];
;               sr = lanes4_sum(sr);
;               const float rq = rsqrtf(sr * (1.f / 32.f) + EPS);
; #pragma unroll
;               for (int j = 0; j < 8; ++j) { const float av = x[2][j] * rq * qgain[64 + 8 * g4 + j];
;                   auto rr = __builtin_amdgcn_permlane16_swap(__float_as_uint(av), __float_as_uint(av), false, false);
;                   const float other = (g4 & 1) ? __uint_as_float(rr[0]) : __uint_as_float(rr[1]);
;                   float cc = 1.f, sg = 0.f;
;                   if (lat) { const f32x2 cs = rope[((g4 & 2) ? pcol : prow) * 8 + j]; cc = cs.x; sg = (g4 & 1) ? cs.y : -cs.y; }
;                   x[2][j] = av * cc + other * sg; }
;           }
; #pragma unroll
;           for (int ds = 0; ds < NDS; ++ds) { u32x4 w;
; #pragma unroll
;               for (int i = 0; i < 4; ++i) w[i] = cvtpk(x[ds][2 * i] * c2, x[ds][2 * i + 1] * c2);
;               qf[qb * NDS + ds] = __builtin_bit_cast(bf16x8, w); }
	v_mov_b32_e32 v57, v13
	v_permlane32_swap_b32_e32 v15, v16
	s_nop 0
	v_permlane32_swap_b32_e32 v17, v57
	v_cndmask_b32_e32 v17, v17, v57, vcc
	v_cndmask_b32_e32 v16, v15, v16, vcc
	v_pk_mul_f32 v[16:17], v[128:129], v[16:17]
	s_nop 0
	v_pk_fma_f32 v[10:11], v[12:13], v[10:11], v[16:17]
	s_nop 0
	v_pk_mul_f32 v[10:11], v[10:11], s[94:95] op_sel_hi:[1,0]
	s_nop 0
	v_cvt_pk_bf16_f32 v13, v10, v11
	v_pk_mul_f32 v[10:11], v[58:59], v[56:57] op_sel_hi:[1,0]
	s_nop 0
	v_pk_mul_f32 v[10:11], v[10:11], v[134:135]
	s_nop 0
	v_mov_b32_e32 v12, v10
	v_mov_b32_e32 v15, v10
	v_mov_b32_e32 v16, v11
	v_mov_b32_e32 v17, v11
	v_permlane32_swap_b32_e32 v12, v15
	s_nop 0
	v_permlane32_swap_b32_e32 v16, v17
	v_cndmask_b32_e32 v17, v16, v17, vcc
	v_cndmask_b32_e32 v16, v12, v15, vcc
	v_pk_mul_f32 v[16:17], v[132:133], v[16:17]
	s_nop 0
	v_pk_fma_f32 v[10:11], v[10:11], v[92:93], v[16:17]
	v_and_b32_e32 v93, 0xffff0000, v14
	v_pk_mul_f32 v[10:11], v[10:11], s[94:95] op_sel_hi:[1,0]
	v_lshlrev_b32_e32 v92, 16, v14
	v_cvt_pk_bf16_f32 v12, v10, v11
	v_pk_mul_f32 v[10:11], v[64:65], v[56:57] op_sel_hi:[1,0]
	v_mul_f32_e32 v14, v93, v93
	v_pk_mul_f32 v[10:11], v[10:11], v[138:139]
	s_nop 0
	v_mov_b32_e32 v15, v10
	v_mov_b32_e32 v16, v10
	v_mov_b32_e32 v17, v11
	v_mov_b32_e32 v57, v11
	v_permlane32_swap_b32_e32 v15, v16
	s_nop 0
	v_permlane32_swap_b32_e32 v17, v57
	v_cndmask_b32_e32 v17, v17, v57, vcc
	v_cndmask_b32_e32 v16, v15, v16, vcc
	v_pk_mul_f32 v[16:17], v[136:137], v[16:17]
	s_nop 0
	v_pk_fma_f32 v[10:11], v[10:11], v[84:85], v[16:17]
	v_pk_mul_f32 v[16:17], v[62:63], v[56:57] op_sel_hi:[1,0]
	v_pk_mul_f32 v[10:11], v[10:11], s[94:95] op_sel_hi:[1,0]
	v_pk_mul_f32 v[16:17], v[16:17], v[140:141]
	v_cvt_pk_bf16_f32 v11, v10, v11
	v_mov_b32_e32 v10, v16
	v_mov_b32_e32 v15, v16
	v_mov_b32_e32 v57, v17
	v_mov_b32_e32 v81, v17
	v_permlane32_swap_b32_e32 v10, v15
	s_nop 0
	v_permlane32_swap_b32_e32 v57, v81
	v_cndmask_b32_e32 v85, v57, v81, vcc
	v_cndmask_b32_e32 v84, v10, v15, vcc
	v_pk_mul_f32 v[20:21], v[20:21], v[84:85]
	s_nop 0
	v_pk_fma_f32 v[16:17], v[16:17], v[88:89], v[20:21]
	v_mul_f32_e32 v88, v111, v111
	v_pk_mul_f32 v[16:17], v[16:17], s[94:95] op_sel_hi:[1,0]
	s_nop 0
	v_cvt_pk_bf16_f32 v10, v16, v17
	v_pk_mul_f32 v[16:17], v[74:75], v[56:57] op_sel_hi:[1,0]
	s_nop 0
	v_pk_mul_f32 v[16:17], v[16:17], v[142:143]
	s_nop 0
	v_mov_b32_e32 v15, v16
	v_mov_b32_e32 v20, v16
	v_mov_b32_e32 v21, v17
	v_mov_b32_e32 v57, v17
	v_permlane32_swap_b32_e32 v15, v20
	s_nop 0
	v_permlane32_swap_b32_e32 v21, v57
	v_cndmask_b32_e32 v21, v21, v57, vcc
	v_cndmask_b32_e32 v20, v15, v20, vcc
	v_pk_mul_f32 v[20:21], v[40:41], v[20:21]
	s_nop 0
	v_pk_fma_f32 v[16:17], v[16:17], v[42:43], v[20:21]
	v_pk_mul_f32 v[20:21], v[72:73], v[56:57] op_sel_hi:[1,0]
	v_pk_mul_f32 v[16:17], v[16:17], s[94:95] op_sel_hi:[1,0]
	v_pk_mul_f32 v[20:21], v[20:21], v[144:145]
	v_cvt_pk_bf16_f32 v17, v16, v17
	v_mov_b32_e32 v15, v20
	v_mov_b32_e32 v16, v20
	v_mov_b32_e32 v57, v21
	v_mov_b32_e32 v81, v21
	v_permlane32_swap_b32_e32 v15, v16
	s_nop 0
	v_permlane32_swap_b32_e32 v57, v81
	v_cndmask_b32_e32 v85, v57, v81, vcc
	v_cndmask_b32_e32 v84, v15, v16, vcc
	v_pk_mul_f32 v[84:85], v[44:45], v[84:85]
	s_nop 0
	v_pk_fma_f32 v[20:21], v[46:47], v[20:21], v[84:85]
	s_nop 0
	v_pk_mul_f32 v[20:21], v[20:21], s[94:95] op_sel_hi:[1,0]
	s_nop 0
	v_cvt_pk_bf16_f32 v16, v20, v21
	v_pk_mul_f32 v[20:21], v[78:79], v[56:57] op_sel_hi:[1,0]
	s_nop 0
	v_pk_mul_f32 v[20:21], v[20:21], v[148:149]
	s_nop 0
	v_mov_b32_e32 v15, v20
	v_mov_b32_e32 v57, v20
	v_mov_b32_e32 v81, v21
	v_mov_b32_e32 v84, v21
	v_permlane32_swap_b32_e32 v15, v57
	s_nop 0
	v_permlane32_swap_b32_e32 v81, v84
	v_cndmask_b32_e32 v85, v81, v84, vcc
	v_cndmask_b32_e32 v84, v15, v57, vcc
	v_pk_mul_f32 v[20:21], v[50:51], v[20:21]
	s_nop 0
	v_pk_fma_f32 v[20:21], v[48:49], v[84:85], v[20:21]
	s_nop 0
	v_pk_mul_f32 v[20:21], v[20:21], s[94:95] op_sel_hi:[1,0]
	s_nop 0
	v_cvt_pk_bf16_f32 v15, v20, v21
	v_pk_mul_f32 v[20:21], v[76:77], v[56:57] op_sel_hi:[1,0]
	v_pk_fma_f32 v[96:97], v[92:93], v[92:93], v[14:15] op_sel_hi:[1,1,0]
	v_pk_mul_f32 v[20:21], v[20:21], v[154:155]
	v_pk_fma_f32 v[96:97], v[52:53], v[52:53], v[96:97]
	v_mov_b32_e32 v56, v20
	v_mov_b32_e32 v81, v20
	s_nop 1
	v_permlane32_swap_b32_e32 v56, v81
	v_mov_b32_e32 v57, v21
	v_mov_b32_e32 v84, v21
	s_nop 1
	v_permlane32_swap_b32_e32 v57, v84
	v_cndmask_b32_e32 v56, v56, v81, vcc
	v_and_b32_e32 v81, 0xffff0000, v80
	v_cndmask_b32_e32 v57, v57, v84, vcc
	v_lshlrev_b32_e32 v80, 16, v80
	v_mul_f32_e32 v84, v81, v81
	v_pk_fma_f32 v[84:85], v[80:81], v[80:81], v[84:85] op_sel_hi:[1,1,0]
	v_mul_f32_e32 v14, v53, v53
	v_pk_fma_f32 v[84:85], v[110:111], v[110:111], v[84:85]
	v_pk_add_f32 v[96:97], v[14:15], v[96:97] op_sel_hi:[0,1]
	v_pk_add_f32 v[84:85], v[88:89], v[84:85] op_sel_hi:[0,1]
	v_pk_fma_f32 v[84:85], v[106:107], v[106:107], v[84:85]
	v_mul_f32_e32 v88, v107, v107
	v_pk_fma_f32 v[96:97], v[82:83], v[82:83], v[96:97]
	v_mul_f32_e32 v14, v83, v83
	v_pk_add_f32 v[84:85], v[88:89], v[84:85] op_sel_hi:[0,1]
	v_pk_add_f32 v[96:97], v[14:15], v[96:97] op_sel_hi:[0,1]
	v_pk_fma_f32 v[84:85], v[24:25], v[24:25], v[84:85]
	v_mul_f32_e32 v88, v25, v25
	v_pk_fma_f32 v[96:97], v[98:99], v[98:99], v[96:97]
	v_mul_f32_e32 v14, v99, v99
	v_pk_add_f32 v[84:85], v[88:89], v[84:85] op_sel_hi:[0,1]
	v_pk_add_f32 v[96:97], v[14:15], v[96:97] op_sel_hi:[0,1]
	v_pk_fma_f32 v[84:85], v[126:127], v[126:127], v[84:85]
	v_mul_f32_e32 v88, v127, v127
	v_pk_fma_f32 v[96:97], v[90:91], v[90:91], v[96:97]
	v_mul_f32_e32 v14, v91, v91
	v_pk_add_f32 v[84:85], v[88:89], v[84:85] op_sel_hi:[0,1]
; template <int DQK, int DV, bool LEAD> ...
;     ...
;           float sn = 0.f;
; #pragma unroll
;           for (int ds = 0; ds < 2; ++ds)
; #pragma unroll
;               for (int j = 0; j < 8; ++j) sn += x[ds][j] * x[ds][j];
;           sn = lanes4_sum(sn);
;           const float rn = rsqrtf(sn * (1.f / 64.f) + EPS);
; #pragma unroll
;           for (int ds = 0; ds < 2; ++ds)
; #pragma unroll
;               for (int j = 0; j < 8; ++j) x[ds][j] *= rn * qgain[32 * ds + 8 * g4 + j];
;           if constexpr (DQK == 64) {
; #pragma unroll
;               for (int ds = 0; ds < 2; ++ds)
; #pragma unroll
;                   for (int j = 0; j < 8; ++j) {
;                       auto rr = __builtin_amdgcn_permlane32_swap(__float_as_uint(x[ds][j]), __float_as_uint(x[ds][j]), false, false);
;                       const float other = hi ? __uint_as_float(rr[0]) : __uint_as_float(rr[1]);
;                       float cc = 1.f, sg = 0.f;
;                       if (lat) { const f32x2 cs = rope[(ds ? pcol : prow) * 16 + 8 * (g4 & 1) + j]; cc = cs.x; sg = hi ? cs.y : -cs.y; }
;                       x[ds][j] = x[ds][j] * cc + other * sg; }
;           } else {
;               float sr = 0.f;
; #pragma unroll
;               for (int j = 0; j < 8; ++j) sr += x[2][j] * x[2][j];
;               sr = lanes4_sum(sr);
;               const float rq = rsqrtf(sr * (1.f / 32.f) + EPS);
; #pragma unroll
;               for (int j = 0; j < 8; ++j) { const float av = x[2][j] * rq * qgain[64 + 8 * g4 + j];
;                   auto rr = __builtin_amdgcn_permlane16_swap(__float_as_uint(av), __float_as_uint(av), false, false);
;                   const float other = (g4 & 1) ? __uint_as_float(rr[0]) : __uint_as_float(rr[1]);
;                   float cc = 1.f, sg = 0.f;
;                   if (lat) { const f32x2 cs = rope[((g4 & 2) ? pcol : prow) * 8 + j]; cc = cs.x; sg = (g4 & 1) ? cs.y : -cs.y; }
;                   x[2][j] = av * cc + other * sg; }
;           }
; #pragma unroll
;           for (int ds = 0; ds < NDS; ++ds) { u32x4 w;
; #pragma unroll
;               for (int i = 0; i < 4; ++i) w[i] = cvtpk(x[ds][2 * i] * c2, x[ds][2 * i + 1] * c2);
;               qf[qb * NDS + ds] = __builtin_bit_cast(bf16x8, w); }
	v_pk_add_f32 v[96:97], v[14:15], v[96:97] op_sel_hi:[0,1]
	v_pk_fma_f32 v[84:85], v[122:123], v[122:123], v[84:85]
	v_mul_f32_e32 v88, v123, v123
	v_pk_fma_f32 v[96:97], v[86:87], v[86:87], v[96:97]
	v_mul_f32_e32 v14, v87, v87
	v_pk_add_f32 v[84:85], v[88:89], v[84:85] op_sel_hi:[0,1]
	v_pk_add_f32 v[96:97], v[14:15], v[96:97] op_sel_hi:[0,1]
	v_pk_fma_f32 v[84:85], v[102:103], v[102:103], v[84:85]
	v_mul_f32_e32 v88, v103, v103
	v_pk_fma_f32 v[96:97], v[68:69], v[68:69], v[96:97]
	v_mul_f32_e32 v14, v69, v69
	v_pk_add_f32 v[84:85], v[88:89], v[84:85] op_sel_hi:[0,1]
	v_pk_add_f32 v[96:97], v[14:15], v[96:97] op_sel_hi:[0,1]
	v_pk_fma_f32 v[84:85], v[118:119], v[118:119], v[84:85]
	v_mul_f32_e32 v88, v119, v119
	v_pk_fma_f32 v[96:97], v[114:115], v[114:115], v[96:97]
	v_mul_f32_e32 v14, v115, v115
	v_pk_add_f32 v[84:85], v[88:89], v[84:85] op_sel_hi:[0,1]
	v_pk_add_f32 v[96:97], v[14:15], v[96:97] op_sel_hi:[0,1]
	v_mov_b32_e32 v85, v84
	v_mov_b32_e32 v14, v96
	s_nop 0
	v_permlane16_swap_b32_e32 v84, v85
	v_permlane16_swap_b32_e32 v96, v14
	v_add_f32_e32 v85, v84, v85
	v_add_f32_e32 v84, v96, v14
	v_mov_b32_e32 v89, v85
	v_mov_b32_e32 v88, v84
	s_nop 0
	v_permlane32_swap_b32_e32 v85, v89
	v_permlane32_swap_b32_e32 v84, v88
	v_pk_add_f32 v[84:85], v[84:85], v[88:89]
	v_pk_mul_f32 v[20:21], v[54:55], v[20:21]
	v_pk_fma_f32 v[84:85], v[84:85], s[12:13], v[108:109] op_sel_hi:[1,0,0]
	v_pk_fma_f32 v[20:21], v[104:105], v[56:57], v[20:21]
	v_mul_f32_e32 v14, 0x4b800000, v85
	v_cmp_gt_f32_e64 s[4:5], s95, v85
	v_pk_mul_f32 v[20:21], v[20:21], s[94:95] op_sel_hi:[1,0]
	s_nop 0
	v_cndmask_b32_e64 v14, v85, v14, s[4:5]
	v_rsq_f32_e32 v85, v14
	v_cvt_pk_bf16_f32 v14, v20, v21
	v_mul_f32_e32 v20, 0x45800000, v85
	v_cndmask_b32_e64 v56, v85, v20, s[4:5]
	v_pk_mul_f32 v[20:21], v[60:61], v[56:57] op_sel_hi:[1,0]
	v_cmp_gt_f32_e64 s[4:5], s95, v84
	v_pk_mul_f32 v[20:21], v[20:21], v[118:119]
	s_nop 0
	v_mov_b32_e32 v57, v20
	v_mov_b32_e32 v85, v20
	v_mov_b32_e32 v88, v21
	v_mov_b32_e32 v89, v21
	v_permlane32_swap_b32_e32 v57, v85
	s_nop 0
	v_permlane32_swap_b32_e32 v88, v89
	v_cndmask_b32_e32 v89, v88, v89, vcc
	v_cndmask_b32_e32 v88, v57, v85, vcc
	v_pk_mul_f32 v[88:89], v[116:117], v[88:89]
	s_nop 0
	v_pk_fma_f32 v[20:21], v[20:21], v[70:71], v[88:89]
	v_pk_mul_f32 v[70:71], v[58:59], v[56:57] op_sel_hi:[1,0]
	v_pk_mul_f32 v[20:21], v[20:21], s[94:95] op_sel_hi:[1,0]
	v_pk_mul_f32 v[70:71], v[70:71], v[102:103]
	v_cvt_pk_bf16_f32 v21, v20, v21
	v_mov_b32_e32 v20, v70
	v_mov_b32_e32 v57, v70
	v_mov_b32_e32 v85, v71
	v_mov_b32_e32 v88, v71
	v_permlane32_swap_b32_e32 v20, v57
	s_nop 0
	v_permlane32_swap_b32_e32 v85, v88
	v_cndmask_b32_e32 v89, v85, v88, vcc
	v_cndmask_b32_e32 v88, v20, v57, vcc
	v_pk_mul_f32 v[88:89], v[94:95], v[88:89]
	s_nop 0
	v_pk_fma_f32 v[66:67], v[70:71], v[66:67], v[88:89]
	s_nop 0
	v_pk_mul_f32 v[66:67], v[66:67], s[94:95] op_sel_hi:[1,0]
	s_nop 0
	v_cvt_pk_bf16_f32 v20, v66, v67
	v_pk_mul_f32 v[66:67], v[64:65], v[56:57] op_sel_hi:[1,0]
	s_nop 0
	v_pk_mul_f32 v[66:67], v[66:67], v[122:123]
	s_nop 0
	v_mov_b32_e32 v57, v66
	v_mov_b32_e32 v70, v66
	v_mov_b32_e32 v71, v67
	v_mov_b32_e32 v85, v67
	v_permlane32_swap_b32_e32 v57, v70
	s_nop 0
	v_permlane32_swap_b32_e32 v71, v85
	v_cndmask_b32_e32 v71, v71, v85, vcc
	v_cndmask_b32_e32 v70, v57, v70, vcc
	v_pk_mul_f32 v[70:71], v[120:121], v[70:71]
	s_nop 0
	v_pk_fma_f32 v[18:19], v[66:67], v[18:19], v[70:71]
	v_pk_mul_f32 v[66:67], v[62:63], v[56:57] op_sel_hi:[1,0]
	v_pk_mul_f32 v[18:19], v[18:19], s[94:95] op_sel_hi:[1,0]
	v_pk_mul_f32 v[66:67], v[66:67], v[126:127]
	v_cvt_pk_bf16_f32 v19, v18, v19
	v_mov_b32_e32 v18, v66
	v_mov_b32_e32 v57, v66
	v_mov_b32_e32 v70, v67
	v_mov_b32_e32 v71, v67
	v_permlane32_swap_b32_e32 v18, v57
	s_nop 0
	v_permlane32_swap_b32_e32 v70, v71
	v_cndmask_b32_e32 v71, v70, v71, vcc
	v_cndmask_b32_e32 v70, v18, v57, vcc
	v_pk_mul_f32 v[70:71], v[124:125], v[70:71]
	s_nop 0
	v_pk_fma_f32 v[22:23], v[66:67], v[22:23], v[70:71]
	s_nop 0
	v_pk_mul_f32 v[22:23], v[22:23], s[94:95] op_sel_hi:[1,0]
	s_nop 0
	v_cvt_pk_bf16_f32 v18, v22, v23
	v_pk_mul_f32 v[22:23], v[74:75], v[56:57] op_sel_hi:[1,0]
	s_nop 0
	v_pk_mul_f32 v[22:23], v[22:23], v[24:25]
	s_nop 0
	v_mov_b32_e32 v24, v22
	v_mov_b32_e32 v57, v22
	v_mov_b32_e32 v25, v23
	v_mov_b32_e32 v66, v23
	v_permlane32_swap_b32_e32 v24, v57
	s_nop 0
	v_permlane32_swap_b32_e32 v25, v66
	v_cndmask_b32_e32 v25, v25, v66, vcc
	v_cndmask_b32_e32 v24, v24, v57, vcc
	v_pk_mul_f32 v[24:25], v[40:41], v[24:25]
	s_nop 0
	v_pk_fma_f32 v[22:23], v[22:23], v[42:43], v[24:25]
	s_nop 0
	v_pk_mul_f32 v[22:23], v[22:23], s[94:95] op_sel_hi:[1,0]
	s_nop 0
	v_cvt_pk_bf16_f32 v25, v22, v23
	v_pk_mul_f32 v[22:23], v[72:73], v[56:57] op_sel_hi:[1,0]
	s_nop 0
	v_pk_mul_f32 v[22:23], v[22:23], v[106:107]
	s_nop 0
	v_mov_b32_e32 v24, v22
	v_mov_b32_e32 v57, v22
	v_mov_b32_e32 v66, v23
	v_mov_b32_e32 v67, v23
	v_permlane32_swap_b32_e32 v24, v57
	s_nop 0
	v_permlane32_swap_b32_e32 v66, v67
	v_cndmask_b32_e32 v67, v66, v67, vcc
	v_cndmask_b32_e32 v66, v24, v57, vcc
	v_pk_mul_f32 v[66:67], v[44:45], v[66:67]
	s_nop 0
	v_pk_fma_f32 v[22:23], v[46:47], v[22:23], v[66:67]
	s_nop 0
	v_pk_mul_f32 v[22:23], v[22:23], s[94:95] op_sel_hi:[1,0]
	s_nop 0
	v_cvt_pk_bf16_f32 v24, v22, v23
	v_pk_mul_f32 v[22:23], v[78:79], v[56:57] op_sel_hi:[1,0]
	s_nop 0
	v_pk_mul_f32 v[22:23], v[22:23], v[110:111]
	s_nop 0
	v_mov_b32_e32 v57, v22
	v_mov_b32_e32 v66, v22
	v_mov_b32_e32 v67, v23
	v_mov_b32_e32 v70, v23
	v_permlane32_swap_b32_e32 v57, v66
	s_nop 0
	v_permlane32_swap_b32_e32 v67, v70
	v_cndmask_b32_e32 v67, v67, v70, vcc
	v_cndmask_b32_e32 v66, v57, v66, vcc
; __device__ __forceinline__ unsigned cvtpk(float lo, float hi) { f32x2 v = {lo, hi}; bf16x2_t b = __builtin_convertvector(v, bf16x2_t); return __builtin_bit_cast(unsigned, b); }
; template <int DQK, int DV, bool LEAD> ...
;     ...
; #pragma unroll
;           for (int ds = 0; ds < 2; ++ds)
; #pragma unroll
;               for (int j = 0; j < 8; ++j) x[ds][j] *= rn * qgain[32 * ds + 8 * g4 + j];
;           if constexpr (DQK == 64) {
; #pragma unroll
;               for (int ds = 0; ds < 2; ++ds)
; #pragma unroll
;                   for (int j = 0; j < 8; ++j) {
;                       auto rr = __builtin_amdgcn_permlane32_swap(__float_as_uint(x[ds][j]), __float_as_uint(x[ds][j]), false, false);
;                       const float other = hi ? __uint_as_float(rr[0]) : __uint_as_float(rr[1]);
;                       float cc = 1.f, sg = 0.f;
;                       if (lat) { const f32x2 cs = rope[(ds ? pcol : prow) * 16 + 8 * (g4 & 1) + j]; cc = cs.x; sg = hi ? cs.y : -cs.y; }
;                       x[ds][j] = x[ds][j] * cc + other * sg; }
;           } else {
;               float sr = 0.f;
; #pragma unroll
;               for (int j = 0; j < 8; ++j) sr += x[2][j] * x[2][j];
;               sr = lanes4_sum(sr);
;               const float rq = rsqrtf(sr * (1.f / 32.f) + EPS);
; #pragma unroll
;               for (int j = 0; j < 8; ++j) { const float av = x[2][j] * rq * qgain[64 + 8 * g4 + j];
;                   auto rr = __builtin_amdgcn_permlane16_swap(__float_as_uint(av), __float_as_uint(av), false, false);
;                   const float other = (g4 & 1) ? __uint_as_float(rr[0]) : __uint_as_float(rr[1]);
;                   float cc = 1.f, sg = 0.f;
;                   if (lat) { const f32x2 cs = rope[((g4 & 2) ? pcol : prow) * 8 + j]; cc = cs.x; sg = (g4 & 1) ? cs.y : -cs.y; }
;                   x[2][j] = av * cc + other * sg; }
;           }
; #pragma unroll
;           for (int ds = 0; ds < NDS; ++ds) { u32x4 w;
; #pragma unroll
;               for (int i = 0; i < 4; ++i) w[i] = cvtpk(x[ds][2 * i] * c2, x[ds][2 * i + 1] * c2);
;               qf[qb * NDS + ds] = __builtin_bit_cast(bf16x8, w); }
;       }
; #pragma unroll
;       for (int d0 = 0; d0 < NQB * NDS; ++d0) asm volatile("" : "+v"(qf[d0])); }
;     wait_bar<0>();
;     bf16x8 kf[NKW * NDS], vf[NVF];
;     ATT_KLOAD(0);
;     asm volatile("s_waitcnt lgkmcnt(0)\n\ts_barrier" ::: "memory");
	v_pk_mul_f32 v[22:23], v[50:51], v[22:23]
	v_pk_mul_f32 v[56:57], v[76:77], v[56:57] op_sel_hi:[1,0]
	v_pk_fma_f32 v[22:23], v[48:49], v[66:67], v[22:23]
	v_pk_mul_f32 v[56:57], v[56:57], v[80:81]
	v_pk_mul_f32 v[22:23], v[22:23], s[94:95] op_sel_hi:[1,0]
	v_mov_b32_e32 v66, v56
	v_cvt_pk_bf16_f32 v23, v22, v23
	v_mov_b32_e32 v22, v56
	s_nop 1
	v_permlane32_swap_b32_e32 v22, v66
	v_mov_b32_e32 v67, v57
	v_mov_b32_e32 v70, v57
	v_cndmask_b32_e32 v66, v22, v66, vcc
	v_mul_f32_e32 v22, 0x4b800000, v84
	v_permlane32_swap_b32_e32 v67, v70
	v_cndmask_b32_e64 v22, v84, v22, s[4:5]
	v_cndmask_b32_e32 v67, v67, v70, vcc
	v_rsq_f32_e32 v70, v22
	v_pk_mul_f32 v[56:57], v[54:55], v[56:57]
	s_nop 0
	v_pk_fma_f32 v[56:57], v[104:105], v[66:67], v[56:57]
	s_nop 0
	v_pk_mul_f32 v[56:57], v[56:57], s[94:95] op_sel_hi:[1,0]
	s_nop 0
	v_cvt_pk_bf16_f32 v22, v56, v57
	v_mul_f32_e32 v56, 0x45800000, v70
	v_cndmask_b32_e64 v56, v70, v56, s[4:5]
	v_pk_mul_f32 v[66:67], v[76:77], v[56:57] op_sel_hi:[1,0]
	v_pk_mul_f32 v[70:71], v[78:79], v[56:57] op_sel_hi:[1,0]
	v_pk_mul_f32 v[66:67], v[66:67], v[92:93]
	v_pk_mul_f32 v[58:59], v[58:59], v[56:57] op_sel_hi:[1,0]
	v_pk_mul_f32 v[52:53], v[70:71], v[52:53]
	v_pk_mul_f32 v[70:71], v[72:73], v[56:57] op_sel_hi:[1,0]
	v_pk_mul_f32 v[72:73], v[74:75], v[56:57] op_sel_hi:[1,0]
	v_pk_mul_f32 v[62:63], v[62:63], v[56:57] op_sel_hi:[1,0]
	v_pk_mul_f32 v[64:65], v[64:65], v[56:57] op_sel_hi:[1,0]
	v_pk_mul_f32 v[58:59], v[58:59], v[68:69]
	v_pk_mul_f32 v[56:57], v[60:61], v[56:57] op_sel_hi:[1,0]
	v_mov_b32_e32 v60, v66
	v_mov_b32_e32 v68, v66
	v_mov_b32_e32 v61, v67
	v_mov_b32_e32 v69, v67
	v_permlane32_swap_b32_e32 v60, v68
	s_nop 0
	v_permlane32_swap_b32_e32 v61, v69
	v_cndmask_b32_e32 v61, v61, v69, vcc
	v_cndmask_b32_e32 v60, v60, v68, vcc
	v_pk_mul_f32 v[54:55], v[54:55], v[66:67]
	v_mov_b32_e32 v66, v52
	v_pk_fma_f32 v[54:55], v[104:105], v[60:61], v[54:55]
	v_mov_b32_e32 v60, v52
	v_mov_b32_e32 v61, v53
	v_mov_b32_e32 v67, v53
	v_permlane32_swap_b32_e32 v60, v66
	s_nop 0
	v_permlane32_swap_b32_e32 v61, v67
	v_pk_mul_f32 v[70:71], v[70:71], v[82:83]
	v_cndmask_b32_e32 v61, v61, v67, vcc
	v_cndmask_b32_e32 v60, v60, v66, vcc
	v_pk_mul_f32 v[50:51], v[50:51], v[52:53]
	v_mov_b32_e32 v52, v70
	v_pk_fma_f32 v[48:49], v[48:49], v[60:61], v[50:51]
	v_mov_b32_e32 v50, v70
	v_mov_b32_e32 v51, v71
	v_mov_b32_e32 v53, v71
	v_permlane32_swap_b32_e32 v50, v52
	s_nop 0
	v_permlane32_swap_b32_e32 v51, v53
	v_cndmask_b32_e32 v51, v51, v53, vcc
	v_cndmask_b32_e32 v50, v50, v52, vcc
	v_pk_mul_f32 v[72:73], v[72:73], v[98:99]
	v_pk_mul_f32 v[44:45], v[44:45], v[50:51]
	v_mov_b32_e32 v50, v72
	v_pk_fma_f32 v[44:45], v[46:47], v[70:71], v[44:45]
	v_mov_b32_e32 v46, v72
	v_mov_b32_e32 v47, v73
	v_mov_b32_e32 v51, v73
	v_permlane32_swap_b32_e32 v46, v50
	s_nop 0
	v_permlane32_swap_b32_e32 v47, v51
	v_cndmask_b32_e32 v47, v47, v51, vcc
	v_cndmask_b32_e32 v46, v46, v50, vcc
	v_pk_mul_f32 v[62:63], v[62:63], v[90:91]
	v_pk_mul_f32 v[40:41], v[40:41], v[46:47]
	v_mov_b32_e32 v46, v62
	v_pk_fma_f32 v[40:41], v[72:73], v[42:43], v[40:41]
	v_mov_b32_e32 v42, v62
	v_mov_b32_e32 v43, v63
	v_mov_b32_e32 v47, v63
	v_permlane32_swap_b32_e32 v42, v46
	s_nop 0
	v_permlane32_swap_b32_e32 v43, v47
	v_cndmask_b32_e32 v43, v43, v47, vcc
	v_cndmask_b32_e32 v42, v42, v46, vcc
	v_pk_mul_f32 v[64:65], v[64:65], v[86:87]
	v_pk_mul_f32 v[36:37], v[36:37], v[42:43]
	v_mov_b32_e32 v42, v64
	v_pk_fma_f32 v[36:37], v[62:63], v[38:39], v[36:37]
	v_mov_b32_e32 v38, v64
	v_mov_b32_e32 v39, v65
	v_mov_b32_e32 v43, v65
	v_permlane32_swap_b32_e32 v38, v42
	s_nop 0
	v_permlane32_swap_b32_e32 v39, v43
	v_cndmask_b32_e32 v39, v39, v43, vcc
	v_cndmask_b32_e32 v38, v38, v42, vcc
	v_pk_mul_f32 v[32:33], v[32:33], v[38:39]
	v_mov_b32_e32 v38, v58
	v_pk_fma_f32 v[32:33], v[64:65], v[34:35], v[32:33]
	v_mov_b32_e32 v34, v58
	v_mov_b32_e32 v35, v59
	v_mov_b32_e32 v39, v59
	v_permlane32_swap_b32_e32 v34, v38
	s_nop 0
	v_permlane32_swap_b32_e32 v35, v39
	v_cndmask_b32_e32 v35, v35, v39, vcc
	v_cndmask_b32_e32 v34, v34, v38, vcc
	v_pk_mul_f32 v[56:57], v[56:57], v[114:115]
	v_pk_mul_f32 v[28:29], v[28:29], v[34:35]
	v_pk_mul_f32 v[32:33], v[32:33], s[94:95] op_sel_hi:[1,0]
	v_pk_fma_f32 v[34:35], v[58:59], v[30:31], v[28:29]
	v_mov_b32_e32 v28, v56
	v_mov_b32_e32 v30, v56
	v_mov_b32_e32 v29, v57
	v_mov_b32_e32 v31, v57
	v_permlane32_swap_b32_e32 v28, v30
	s_nop 0
	v_permlane32_swap_b32_e32 v29, v31
	v_cndmask_b32_e32 v29, v29, v31, vcc
	v_cndmask_b32_e32 v28, v28, v30, vcc
	v_pk_mul_f32 v[28:29], v[112:113], v[28:29]
	v_pk_mul_f32 v[30:31], v[40:41], s[94:95] op_sel_hi:[1,0]
	v_pk_fma_f32 v[38:39], v[56:57], v[26:27], v[28:29]
	v_pk_mul_f32 v[26:27], v[54:55], s[94:95] op_sel_hi:[1,0]
	v_pk_mul_f32 v[28:29], v[48:49], s[94:95] op_sel_hi:[1,0]
	v_cvt_pk_bf16_f32 v26, v26, v27
	v_cvt_pk_bf16_f32 v27, v28, v29
	v_pk_mul_f32 v[28:29], v[44:45], s[94:95] op_sel_hi:[1,0]
	v_bfe_u32 v54, v168, 1, 3
	v_cvt_pk_bf16_f32 v28, v28, v29
	v_cvt_pk_bf16_f32 v29, v30, v31
	v_pk_mul_f32 v[30:31], v[36:37], s[94:95] op_sel_hi:[1,0]
	v_bitop3_b32 v54, v171, v54, 4 bitop3:0x36
	v_cvt_pk_bf16_f32 v30, v30, v31
	v_cvt_pk_bf16_f32 v31, v32, v33
	v_pk_mul_f32 v[32:33], v[34:35], s[94:95] op_sel_hi:[1,0]
	v_pk_mul_f32 v[34:35], v[38:39], s[94:95] op_sel_hi:[1,0]
	v_cvt_pk_bf16_f32 v32, v32, v33
	v_cvt_pk_bf16_f32 v33, v34, v35
	s_waitcnt vmcnt(0) lgkmcnt(0)
	s_barrier
	ds_read_b128 v[34:37], v175
	ds_read_b128 v[38:41], v175 offset:512
	v_lshlrev_b32_e32 v82, 4, v54
	v_add_u32_e32 v178, v169, v82
	s_waitcnt lgkmcnt(1)
	v_mfma_f32_16x16x32_bf16 v[42:45], v[34:37], v[6:9], 0
	ds_read_b128 v[54:57], v178
	ds_read_b128 v[58:61], v178 offset:512
	s_waitcnt lgkmcnt(0)
	s_barrier
; #define ATT_SB() __builtin_amdgcn_sched_barrier(0)
; #define ATT_DMA_K(t, sl) do { glds16(ksrc + (size_t)(t) * 64 * kpitch, (unsigned)__builtin_amdgcn_readfirstlane(kdst + (sl) * KSLOT)); \
;         if constexpr (DQK == 96) glds16(krsrc + (size_t)(t) * 64 * 32, (unsigned)__builtin_amdgcn_readfirstlane(krdst + (sl) * KSLOT)); } while (0)
; #define ATT_DMA_V(t, sl) do { glds16(vsrc + (size_t)(t) * 64, (unsigned)__builtin_amdgcn_readfirstlane(vdst + (sl) * VSLOT)); \
;         if constexpr (DV == 128) glds16(vsrc + (size_t)64 * NR + (size_t)(t) * 64, (unsigned)__builtin_amdgcn_readfirstlane(vdst + (sl) * VSLOT + 8192)); } while (0)
; #define ATT_KLOAD(sl) do { _Pragma("unroll") for (int kb_ = 0; kb_ < NKW; ++kb_) _Pragma("unroll") for (int ds_ = 0; ds_ < NDS; ++ds_) { \
;         if (ds_ < 2) kf[kb_ * NDS + ds_] = *(const LAS bf16x8*)(kp[ds_ & 1] + (sl) * KSLOT + (kb_ & 1) * 512 + (kb_ >> 1) * 4096); \
;         else kf[kb_ * NDS + ds_] = *(const LAS bf16x8*)(krp + (sl) * KSLOT + (kb_ & 1) * 256 + (kb_ >> 1) * 2048); } } while (0)
; #define ATT_QK() do { _Pragma("unroll") for (int kb_ = 0; kb_ < NKW; ++kb_) _Pragma("unroll") for (int ds_ = 0; ds_ < NDS; ++ds_) _Pragma("unroll") for (int qb_ = 0; qb_ < NQB; ++qb_) \
;         c[kb_][qb_] = __builtin_amdgcn_mfma_f32_16x16x32_bf16(kf[kb_ * NDS + ds_], qf[qb_ * NDS + ds_], ds_ == 0 ? zero4 : c[kb_][qb_], 0, 0, 0); } while (0)
; #define ATT_EXP() do { _Pragma("unroll") for (int kb_ = 0; kb_ < NKW; ++kb_) _Pragma("unroll") for (int qb_ = 0; qb_ < NQB; ++qb_) _Pragma("unroll") for (int i_ = 0; i_ < 4; ++i_) \
;         c[kb_][qb_][i_] = __builtin_amdgcn_exp2f(c[kb_][qb_][i_]); } while (0)
; template <int DQK, int DV, bool LEAD> ...
;     ...
;     ATT_KLOAD(0);
;     asm volatile("s_waitcnt lgkmcnt(0)\n\ts_barrier" ::: "memory");
;     float lsum[NQB];
; #pragma unroll
;     for (int qb = 0; qb < NQB; ++qb) lsum[qb] = 0.f;
;     const f32x4 zero4 = {0.f, 0.f, 0.f, 0.f};
;     f32x4 o[NDB][NQB], c[NKW][NQB]; u32x4 pw[4];
; #pragma unroll
;     for (int i = 0; i < NDB; ++i)
; #pragma unroll
;         for (int qb = 0; qb < NQB; ++qb) o[i][qb] = zero4;
;     ATT_DMA_K(3, 0); ATT_DMA_V(1, 1);
;     ATT_QK(); ATT_SB();
;     ATT_KLOAD(1); ATT_SB();
;     if constexpr (LEAD) { ATT_EXP(); ATT_SUMPACK(); }
;     wait_bar<NDMA>();
;     int s_prev = 0, s_cur = 1, s_next = 2;
;     int one_ = 1; asm volatile("" : "+s"(one_));
	s_cselect_b64 vcc, -1, 0
	v_mfma_f32_16x16x32_bf16 v[46:49], v[34:37], v[14:17], 0
	v_mfma_f32_16x16x32_bf16 v[50:53], v[34:37], v[22:25], 0
	v_mfma_f32_16x16x32_bf16 v[34:37], v[34:37], v[26:29], 0
	s_waitcnt lgkmcnt(1)
	v_mfma_f32_16x16x32_bf16 v[62:65], v[54:57], v[2:5], v[42:45]
	v_mfma_f32_16x16x32_bf16 v[66:69], v[54:57], v[10:13], v[46:49]
	v_mfma_f32_16x16x32_bf16 v[50:53], v[54:57], v[18:21], v[50:53]
	v_mfma_f32_16x16x32_bf16 v[54:57], v[54:57], v[30:33], v[34:37]
	v_mfma_f32_16x16x32_bf16 v[34:37], v[38:41], v[6:9], 0
	v_mfma_f32_16x16x32_bf16 v[42:45], v[38:41], v[14:17], 0
	v_mfma_f32_16x16x32_bf16 v[46:49], v[38:41], v[22:25], 0
	v_mfma_f32_16x16x32_bf16 v[38:41], v[38:41], v[26:29], 0
	s_waitcnt lgkmcnt(0)
	v_mfma_f32_16x16x32_bf16 v[70:73], v[58:61], v[2:5], v[34:37]
	v_mfma_f32_16x16x32_bf16 v[74:77], v[58:61], v[10:13], v[42:45]
	s_nop 1
	v_lshl_add_u64 v[34:35], v[162:163], 0, s[96:97]
	s_mov_b32 s4, m0
	s_mov_b32 m0, s49
	s_nop 0
	global_load_lds_dwordx4 v[34:35], off
	s_mov_b32 m0, s4
	v_lshl_add_u64 v[34:35], v[164:165], 0, s[66:67]
	v_mfma_f32_16x16x32_bf16 v[78:81], v[58:61], v[18:21], v[46:49]
	s_add_i32 s4, s36, 0x2000
	s_mov_b32 s5, m0
	s_mov_b32 m0, s4
	s_nop 0
	global_load_lds_dwordx4 v[34:35], off
	s_mov_b32 m0, s5
	v_mfma_f32_16x16x32_bf16 v[58:61], v[58:61], v[30:33], v[38:41]
	ds_read_b128 v[34:37], v175 offset:8192
	s_nop 1
	ds_read_b128 v[38:41], v175 offset:8704
	ds_read_b128 v[42:45], v178 offset:8192
	ds_read_b128 v[46:49], v178 offset:8704
	v_exp_f32_e32 v62, v62
	v_exp_f32_e32 v63, v63
	v_exp_f32_e32 v64, v64
	v_exp_f32_e32 v65, v65
	v_exp_f32_e32 v66, v66
	v_exp_f32_e32 v67, v67
	v_exp_f32_e32 v68, v68
	v_exp_f32_e32 v69, v69
	v_exp_f32_e32 v83, v50
	v_exp_f32_e32 v84, v51
	v_exp_f32_e32 v85, v52
	v_exp_f32_e32 v86, v53
	v_exp_f32_e32 v54, v54
	v_exp_f32_e32 v55, v55
	v_exp_f32_e32 v56, v56
	v_exp_f32_e32 v57, v57
	v_add_f32_e32 v50, v62, v63
	v_add_f32_e32 v51, v64, v65
	v_exp_f32_e32 v70, v70
	v_exp_f32_e32 v74, v74
	v_exp_f32_e32 v78, v78
	v_exp_f32_e32 v58, v58
	v_add_f32_e32 v50, v50, v51
	v_add_f32_e32 v51, v66, v67
	v_add_f32_e32 v52, v68, v69
	v_add_f32_e32 v51, v51, v52
	v_add_f32_e32 v52, v83, v84
	v_add_f32_e32 v53, v85, v86
	v_exp_f32_e32 v71, v71
	v_exp_f32_e32 v75, v75
	v_exp_f32_e32 v79, v79
	v_exp_f32_e32 v59, v59
	v_add_f32_e32 v52, v52, v53
	v_add_f32_e32 v53, v54, v55
	v_add_f32_e32 v87, v56, v57
	v_add_f32_e32 v53, v53, v87
	v_exp_f32_e32 v72, v72
	v_exp_f32_e32 v76, v76
	v_exp_f32_e32 v80, v80
	v_exp_f32_e32 v60, v60
	v_add_f32_e32 v50, v50, v70
	v_add_f32_e32 v51, v51, v74
	v_add_f32_e32 v52, v52, v78
	v_add_f32_e32 v53, v53, v58
	v_exp_f32_e32 v73, v73
	v_exp_f32_e32 v77, v77
	v_exp_f32_e32 v81, v81
	v_exp_f32_e32 v61, v61
	v_add_f32_e32 v50, v71, v50
	v_add_f32_e32 v51, v75, v51
	v_add_f32_e32 v52, v79, v52
	v_add_f32_e32 v53, v59, v53
	s_mov_b32 s4, 1
	v_add_f32_e32 v50, v72, v50
	v_add_f32_e32 v87, v76, v51
	v_add_f32_e32 v52, v80, v52
	v_add_f32_e32 v88, v60, v53
	v_cvt_pk_bf16_f32 v102, v62, v63
	v_add_f32_e32 v51, v73, v50
	v_add_f32_e32 v50, v77, v87
	v_add_f32_e32 v53, v81, v52
	v_add_f32_e32 v52, v61, v88
	s_waitcnt vmcnt(2) lgkmcnt(0)
	s_barrier
	s_cmp_lg_u32 s4, 0
	v_pk_add_f32 v[168:169], v[50:51], 0 op_sel_hi:[1,0]
	v_cndmask_b32_e32 v50, v82, v177, vcc
	v_add3_u32 v177, 0, v173, v50
	v_mov_b32_e32 v50, 0
	v_pk_add_f32 v[166:167], v[52:53], 0 op_sel_hi:[1,0]
	v_cvt_pk_bf16_f32 v103, v64, v65
	v_cvt_pk_bf16_f32 v104, v70, v71
	v_cvt_pk_bf16_f32 v105, v72, v73
	v_cvt_pk_bf16_f32 v114, v66, v67
	v_cvt_pk_bf16_f32 v115, v68, v69
	v_cvt_pk_bf16_f32 v116, v74, v75
	v_cvt_pk_bf16_f32 v117, v76, v77
	v_cvt_pk_bf16_f32 v122, v83, v84
	v_cvt_pk_bf16_f32 v123, v85, v86
	v_cvt_pk_bf16_f32 v124, v78, v79
	v_cvt_pk_bf16_f32 v125, v80, v81
	v_cvt_pk_bf16_f32 v126, v54, v55
	v_cvt_pk_bf16_f32 v127, v56, v57
	v_cvt_pk_bf16_f32 v128, v58, v59
	v_cvt_pk_bf16_f32 v129, v60, v61
	s_cselect_b64 s[4:5], -1, 0
	s_mov_b32 s37, 2
	v_mov_b32_e32 v51, v50
	v_mov_b32_e32 v52, v50
	v_mov_b32_e32 v53, v50
	v_mov_b32_e32 v54, v50
	v_mov_b32_e32 v55, v50
	v_mov_b32_e32 v56, v50
	v_mov_b32_e32 v57, v50
	v_mov_b32_e32 v58, v50
	v_mov_b32_e32 v59, v50
	v_mov_b32_e32 v60, v50
	v_mov_b32_e32 v61, v50
	v_mov_b32_e32 v62, v50
	v_mov_b32_e32 v63, v50
	v_mov_b32_e32 v64, v50
	v_mov_b32_e32 v65, v50
	v_mov_b32_e32 v66, v50
	v_mov_b32_e32 v67, v50
	v_mov_b32_e32 v68, v50
	v_mov_b32_e32 v69, v50
	v_mov_b32_e32 v70, v50
	v_mov_b32_e32 v71, v50
	v_mov_b32_e32 v72, v50
	v_mov_b32_e32 v73, v50
	v_mov_b32_e32 v74, v50
	v_mov_b32_e32 v75, v50
	v_mov_b32_e32 v76, v50
	v_mov_b32_e32 v77, v50
	v_mov_b32_e32 v78, v50
	v_mov_b32_e32 v79, v50
	v_mov_b32_e32 v80, v50
	v_mov_b32_e32 v81, v50
	v_mov_b32_e32 v82, v50
	v_mov_b32_e32 v83, v50
	v_mov_b32_e32 v84, v50
	v_mov_b32_e32 v85, v50
	v_mov_b32_e32 v86, v50
	v_mov_b32_e32 v87, v50
	v_mov_b32_e32 v88, v50
	v_mov_b32_e32 v89, v50
	v_mov_b32_e32 v90, v50
	v_mov_b32_e32 v91, v50
	v_mov_b32_e32 v92, v50
	v_mov_b32_e32 v93, v50
	v_mov_b32_e32 v94, v50
	v_mov_b32_e32 v95, v50
	v_mov_b32_e32 v96, v50
	v_mov_b32_e32 v97, v50
	v_mov_b32_e32 v98, v50
	v_mov_b32_e32 v99, v50
	v_mov_b32_e32 v100, v50
	v_mov_b32_e32 v101, v50
	v_mov_b32_e32 v106, v50
	v_mov_b32_e32 v107, v50
	v_mov_b32_e32 v108, v50
	v_mov_b32_e32 v109, v50
	v_mov_b32_e32 v110, v50
	v_mov_b32_e32 v111, v50
	v_mov_b32_e32 v112, v50
	v_mov_b32_e32 v113, v50
	v_mov_b32_e32 v118, v50
	v_mov_b32_e32 v119, v50
	v_mov_b32_e32 v120, v50
	v_mov_b32_e32 v121, v50
	s_branch .LBB0_965

; #define LAS __attribute__((address_space(3)))
; #define ATT_DMA_K(t, sl) do { glds16(ksrc + (size_t)(t) * 64 * kpitch, (unsigned)__builtin_amdgcn_readfirstlane(kdst + (sl) * KSLOT)); \
;         if constexpr (DQK == 96) glds16(krsrc + (size_t)(t) * 64 * 32, (unsigned)__builtin_amdgcn_readfirstlane(krdst + (sl) * KSLOT)); } while (0)
; template <int DQK, int DV, bool LEAD> ...
;     ...
;     const int kr0 = 8 * (q16 >> 2) + (q16 & 3);
;     const int fk = ((kr0 >> 1) & 1) | (((kr0 >> 3) & 1) << 1) | (((kr0 >> 4) & 1) << 2);
;     const LAS unsigned char* kp[2]; const LAS unsigned char* vp[2];
; #pragma unroll
;     for (int ds = 0; ds < 2; ++ds) kp[ds] = shm + KOFF + kr0 * 128 + ((((ds << 2) | g4) ^ fk) << 4) + kg * 4096;
;     const LAS unsigned char* krp = shm + KOFF + 8192 + kr0 * 64 + ((g4 ^ (((kr0 >> 4) & 1) << 1)) << 4) + kg * 2048;
; #pragma unroll
;     for (int s_ = 0; s_ < 2; ++s_) vp[s_] = shm + VOFF + q16 * 128 + ((((s_ << 2) | g4) ^ ((q16 >> 1) & 7)) << 4);
;     const LAS unsigned char* vpk = kg ? vp[1] : vp[0];
;     ...
;     ATT_DMA_K(0, 0); ATT_DMA_V(0, 0); ATT_DMA_K(1, 1); ATT_DMA_K(2, 2);
;     bf16x8 qf[NQB * NDS];
;     {
;       const float c2 = (DQK == 64) ? C2_EVEN : C2_ODD; const bool lat = tq0 >= 0;
; #pragma unroll
;       for (int qb = 0; qb < NQB; ++qb) {
;           const bf16_t* qp = Q + (size_t)(qrow0 + qoff + qb * 16 + q16) * qpitch + g4 * 8;
;           bf16x8 raw[NDS];
; #pragma unroll
;           for (int ds = 0; ds < NDS; ++ds) raw[ds] = *(const bf16x8*)(qp + ds * 32);
;           float x[NDS][8];
; #pragma unroll
;           for (int ds = 0; ds < NDS; ++ds)
; #pragma unroll
;               for (int j = 0; j < 8; ++j) x[ds][j] = __uint_as_float(((unsigned)(unsigned short)raw[ds][j]) << 16);
;           const int tq = tq0 + qoff + qb * 16 + q16, prow = (tq >> 6) & 127, pcol = tq & 63;
;           float sn = 0.f;
; #pragma unroll
;           for (int ds = 0; ds < 2; ++ds)
; #pragma unroll
;               for (int j = 0; j < 8; ++j) sn += x[ds][j] * x[ds][j];
;           sn = lanes4_sum(sn);
;           const float rn = rsqrtf(sn * (1.f / 64.f) + EPS);
; #pragma unroll
;           for (int ds = 0; ds < 2; ++ds)
; #pragma unroll
;               for (int j = 0; j < 8; ++j) x[ds][j] *= rn * qgain[32 * ds + 8 * g4 + j];
.LBB0_973:
	v_mov_b32_e32 v37, v0
	s_ashr_i32 s29, s28, 31
	v_readfirstlane_b32 s4, v37
	s_ashr_i32 s30, s4, 6
	v_bfe_u32 v1, v37, 3, 3
	v_lshl_or_b32 v6, s30, 3, v1
	s_lshl_b32 s5, s30, 1
	s_lshr_b32 s4, s4, 5
	v_ashrrev_i32_e32 v2, 1, v6
	s_and_b32 s5, s5, 2
	s_and_b32 s4, s4, 4
	v_and_b32_e32 v203, 7, v37
	v_and_b32_e32 v3, 1, v2
	s_or_b32 s4, s5, s4
	v_bitop3_b32 v7, s4, v203, v3 bitop3:0x36
	v_xor_b32_e32 v8, v2, v37
	v_add_u32_e32 v4, s28, v6
	v_mov_b64_e32 v[2:3], s[36:37]
	v_mad_i64_i32 v[2:3], s[4:5], v4, s92, v[2:3]
	v_mov_b64_e32 v[4:5], s[40:41]
	v_lshlrev_b32_e32 v194, 4, v7
	s_lshl_b32 s16, s30, 10
	v_mad_i64_i32 v[4:5], s[4:5], v6, s91, v[4:5]
	v_lshl_add_u64 v[22:23], v[2:3], 0, v[194:195]
	v_lshlrev_b32_e32 v2, 4, v8
	s_add_i32 s16, s16, 0
	v_lshl_add_u64 v[4:5], s[28:29], 1, v[4:5]
	v_and_b32_e32 v194, 0x70, v2
	s_mov_b32 s4, m0
	s_mov_b32 m0, s16
	s_nop 0
	global_load_lds_dwordx4 v[22:23], off
	s_mov_b32 m0, s4
	v_lshl_add_u64 v[204:205], v[4:5], 0, v[194:195]
	s_add_i32 s29, s16, 0x9000
	s_mov_b32 s4, m0
	s_mov_b32 m0, s29
	s_nop 0
	global_load_lds_dwordx4 v[204:205], off
	s_mov_b32 m0, s4
	s_mov_b64 s[4:5], 0x840000
	v_lshl_add_u64 v[206:207], v[204:205], 0, s[4:5]
	s_add_i32 s4, s29, 0x2000
	s_mov_b32 s5, m0
	s_mov_b32 m0, s4
	s_nop 0
	global_load_lds_dwordx4 v[206:207], off
	s_mov_b32 m0, s5
	s_mov_b64 s[4:5], 0x38000
	s_lshl_b32 s25, s30, 5
	v_lshl_add_u64 v[2:3], v[22:23], 0, s[4:5]
	s_add_i32 s4, s16, 0x2000
	s_mov_b32 s5, m0
	s_mov_b32 m0, s4
	s_nop 0
	global_load_lds_dwordx4 v[2:3], off
	s_mov_b32 m0, s5
	v_and_b32_e32 v36, 15, v37
	s_mov_b64 s[4:5], 0x70000
	s_add_i32 s25, s25, s28
	v_and_b32_e32 v194, 48, v37
	v_lshl_add_u64 v[2:3], v[22:23], 0, s[4:5]
	s_add_i32 s4, s16, 0x4000
	v_or_b32_e32 v10, s25, v36
	v_lshl_add_u64 v[6:7], s[26:27], 0, v[194:195]
	s_mov_b32 s5, m0
	s_mov_b32 m0, s4
	s_nop 0
	global_load_lds_dwordx4 v[2:3], off
	s_mov_b32 m0, s5
	v_bfe_u32 v214, v37, 4, 2
	v_mad_i64_i32 v[8:9], s[4:5], v10, s92, v[6:7]
	v_or_b32_e32 v10, 16, v10
	v_mad_i64_i32 v[6:7], s[4:5], v10, s92, v[6:7]
	global_load_dwordx4 v[2:5], v[8:9], off offset:64 nt
	global_load_dwordx4 v[10:13], v[6:7], off offset:64 nt
	global_load_dwordx4 v[38:41], v[8:9], off nt
	global_load_dwordx4 v[42:45], v[6:7], off nt
	v_lshlrev_b32_e32 v215, 1, v37
	v_and_b32_e32 v6, 3, v37
	v_lshrrev_b32_e32 v7, 1, v37
	v_and_or_b32 v6, v215, 24, v6
	v_lshlrev_b32_e32 v62, 5, v214
	v_bitop3_b32 v60, v214, v7, 7 bitop3:0x78
	v_lshl_add_u32 v66, v6, 7, 0
	global_load_dwordx4 v[6:9], v62, s[22:23] offset:144
	global_load_dwordx4 v[14:17], v62, s[22:23] offset:128
	global_load_dwordx4 v[18:21], v62, s[22:23] offset:16
	s_mov_b32 s4, 0x3c800000
	v_and_b32_e32 v61, 63, v37
	v_lshlrev_b32_e32 v67, 4, v60
	v_add_u32_e32 v217, v66, v67
	v_lshl_add_u64 v[210:211], v[22:23], 0, s[96:97]
	v_lshlrev_b32_e32 v194, 7, v36
	s_mov_b32 s31, 1
	s_mov_b32 s42, 2
	v_or_b32_e32 v216, 4, v214
	s_waitcnt vmcnt(5)
	v_and_b32_e32 v25, 0xffff0000, v13
	s_waitcnt vmcnt(4)
	v_and_b32_e32 v57, 0xffff0000, v38
	v_and_b32_e32 v51, 0xffff0000, v2
	v_lshlrev_b32_e32 v50, 16, v2
	v_lshlrev_b32_e32 v56, 16, v38
	v_mul_f32_e32 v2, v57, v57
	v_lshlrev_b32_e32 v24, 16, v13
	v_and_b32_e32 v27, 0xffff0000, v12
	v_lshlrev_b32_e32 v26, 16, v12
	v_and_b32_e32 v13, 0xffff0000, v3
	v_lshlrev_b32_e32 v12, 16, v3
	s_waitcnt vmcnt(3)
	v_and_b32_e32 v33, 0xffff0000, v45
	v_lshlrev_b32_e32 v32, 16, v45
	v_and_b32_e32 v35, 0xffff0000, v44
	v_lshlrev_b32_e32 v34, 16, v44
	v_and_b32_e32 v45, 0xffff0000, v39
	v_lshlrev_b32_e32 v44, 16, v39
	v_pk_fma_f32 v[2:3], v[56:57], v[56:57], v[2:3] op_sel_hi:[1,1,0]
	v_and_b32_e32 v49, 0xffff0000, v4
	v_lshlrev_b32_e32 v48, 16, v4
	v_pk_fma_f32 v[2:3], v[44:45], v[44:45], v[2:3]
	v_mul_f32_e32 v4, v45, v45
	v_and_b32_e32 v53, 0xffff0000, v40
	v_lshlrev_b32_e32 v52, 16, v40
	v_pk_add_f32 v[2:3], v[4:5], v[2:3] op_sel_hi:[0,1]
	v_pk_fma_f32 v[2:3], v[52:53], v[52:53], v[2:3]
	v_mul_f32_e32 v4, v53, v53
	v_and_b32_e32 v29, 0xffff0000, v11
	v_lshlrev_b32_e32 v28, 16, v11
	v_and_b32_e32 v31, 0xffff0000, v10
	v_lshlrev_b32_e32 v30, 16, v10
	v_and_b32_e32 v11, 0xffff0000, v41
	v_lshlrev_b32_e32 v10, 16, v41
	v_pk_add_f32 v[2:3], v[4:5], v[2:3] op_sel_hi:[0,1]
	v_pk_fma_f32 v[2:3], v[10:11], v[10:11], v[2:3]
	v_mul_f32_e32 v4, v11, v11
	v_pk_add_f32 v[2:3], v[4:5], v[2:3] op_sel_hi:[0,1]
	v_pk_fma_f32 v[2:3], v[50:51], v[50:51], v[2:3]
	v_mul_f32_e32 v4, v51, v51
	v_pk_add_f32 v[2:3], v[4:5], v[2:3] op_sel_hi:[0,1]
	v_pk_fma_f32 v[2:3], v[12:13], v[12:13], v[2:3]
	v_mul_f32_e32 v4, v13, v13
	v_pk_add_f32 v[2:3], v[4:5], v[2:3] op_sel_hi:[0,1]
	v_pk_fma_f32 v[2:3], v[48:49], v[48:49], v[2:3]
	v_mul_f32_e32 v4, v49, v49
	v_and_b32_e32 v47, 0xffff0000, v5
	v_lshlrev_b32_e32 v46, 16, v5
	v_pk_add_f32 v[2:3], v[4:5], v[2:3] op_sel_hi:[0,1]
	v_pk_fma_f32 v[2:3], v[46:47], v[46:47], v[2:3]
	v_mul_f32_e32 v4, v47, v47
	v_pk_add_f32 v[2:3], v[4:5], v[2:3] op_sel_hi:[0,1]
	v_mov_b32_e32 v3, v2
	s_nop 1
	v_permlane16_swap_b32_e32 v2, v3
	v_add_f32_e32 v3, v2, v3
	v_and_b32_e32 v55, 0xffff0000, v43
	v_lshlrev_b32_e32 v54, 16, v43
	v_mov_b32_e32 v5, v3
	v_and_b32_e32 v43, 0xffff0000, v42
	s_nop 0
	v_permlane32_swap_b32_e32 v3, v5
	v_lshlrev_b32_e32 v42, 16, v42
	v_mul_f32_e32 v2, v43, v43
	v_pk_fma_f32 v[38:39], v[42:43], v[42:43], v[2:3] op_sel_hi:[1,1,0]
	v_mul_f32_e32 v2, v55, v55
	v_pk_fma_f32 v[38:39], v[54:55], v[54:55], v[38:39]
	s_nop 0
	v_pk_add_f32 v[38:39], v[2:3], v[38:39] op_sel_hi:[0,1]
	v_pk_fma_f32 v[38:39], v[34:35], v[34:35], v[38:39]
	v_mul_f32_e32 v2, v35, v35
	v_pk_add_f32 v[38:39], v[2:3], v[38:39] op_sel_hi:[0,1]
	v_pk_fma_f32 v[38:39], v[32:33], v[32:33], v[38:39]
	v_mul_f32_e32 v2, v33, v33
	v_pk_add_f32 v[38:39], v[2:3], v[38:39] op_sel_hi:[0,1]
	v_pk_fma_f32 v[38:39], v[30:31], v[30:31], v[38:39]
	v_mul_f32_e32 v2, v31, v31
	v_pk_add_f32 v[38:39], v[2:3], v[38:39] op_sel_hi:[0,1]
	v_pk_fma_f32 v[38:39], v[28:29], v[28:29], v[38:39]
	v_mul_f32_e32 v2, v29, v29
	v_pk_add_f32 v[38:39], v[2:3], v[38:39] op_sel_hi:[0,1]
	v_pk_fma_f32 v[38:39], v[26:27], v[26:27], v[38:39]
	v_mul_f32_e32 v2, v27, v27
	v_pk_add_f32 v[38:39], v[2:3], v[38:39] op_sel_hi:[0,1]
	v_pk_fma_f32 v[38:39], v[24:25], v[24:25], v[38:39]
	v_mul_f32_e32 v2, v25, v25
	v_pk_add_f32 v[38:39], v[2:3], v[38:39] op_sel_hi:[0,1]
	v_mov_b32_e32 v2, v38
	s_nop 1
	v_permlane16_swap_b32_e32 v38, v2
	v_add_f32_e32 v2, v38, v2
	global_load_dwordx4 v[38:41], v62, s[22:23]
	v_mov_b32_e32 v4, v2
	s_nop 1
	v_permlane32_swap_b32_e32 v2, v4
	v_pk_add_f32 v[2:3], v[2:3], v[4:5]
	s_nop 0
	v_pk_fma_f32 v[58:59], v[2:3], s[4:5], v[196:197] op_sel_hi:[1,0,0]
	s_nop 0
	v_mul_f32_e32 v2, 0x4b800000, v59
	v_cmp_gt_f32_e32 vcc, s95, v59
	v_cmp_gt_f32_e64 s[4:5], s95, v58
	s_nop 0
	v_cndmask_b32_e32 v2, v59, v2, vcc
	v_rsq_f32_e32 v2, v2
	s_nop 0
	v_mul_f32_e32 v3, 0x45800000, v2
	v_cndmask_b32_e32 v60, v2, v3, vcc
	s_waitcnt vmcnt(3)
; __device__ __forceinline__ unsigned cvtpk(float lo, float hi) { f32x2 v = {lo, hi}; bf16x2_t b = __builtin_convertvector(v, bf16x2_t); return __builtin_bit_cast(unsigned, b); }
; template <int DQK, int DV, bool LEAD> ...
;     ...
; #pragma unroll
;           for (int ds = 0; ds < 2; ++ds)
; #pragma unroll
;               for (int j = 0; j < 8; ++j) x[ds][j] *= rn * qgain[32 * ds + 8 * g4 + j];
;           if constexpr (DQK == 64) {
; #pragma unroll
;               for (int ds = 0; ds < 2; ++ds)
; #pragma unroll
;                   for (int j = 0; j < 8; ++j) {
;                       auto rr = __builtin_amdgcn_permlane32_swap(__float_as_uint(x[ds][j]), __float_as_uint(x[ds][j]), false, false);
;                       const float other = hi ? __uint_as_float(rr[0]) : __uint_as_float(rr[1]);
;                       float cc = 1.f, sg = 0.f;
;                       if (lat) { const f32x2 cs = rope[(ds ? pcol : prow) * 16 + 8 * (g4 & 1) + j]; cc = cs.x; sg = hi ? cs.y : -cs.y; }
;                       x[ds][j] = x[ds][j] * cc + other * sg; }
;           } else {
;               float sr = 0.f;
; #pragma unroll
;               for (int j = 0; j < 8; ++j) sr += x[2][j] * x[2][j];
;               sr = lanes4_sum(sr);
;               const float rq = rsqrtf(sr * (1.f / 32.f) + EPS);
; #pragma unroll
;               for (int j = 0; j < 8; ++j) { const float av = x[2][j] * rq * qgain[64 + 8 * g4 + j];
;                   auto rr = __builtin_amdgcn_permlane16_swap(__float_as_uint(av), __float_as_uint(av), false, false);
;                   const float other = (g4 & 1) ? __uint_as_float(rr[0]) : __uint_as_float(rr[1]);
;                   float cc = 1.f, sg = 0.f;
;                   if (lat) { const f32x2 cs = rope[((g4 & 2) ? pcol : prow) * 8 + j]; cc = cs.x; sg = (g4 & 1) ? cs.y : -cs.y; }
;                   x[2][j] = av * cc + other * sg; }
;           }
; #pragma unroll
;           for (int ds = 0; ds < NDS; ++ds) { u32x4 w;
; #pragma unroll
;               for (int i = 0; i < 4; ++i) w[i] = cvtpk(x[ds][2 * i] * c2, x[ds][2 * i + 1] * c2);
;               qf[qb * NDS + ds] = __builtin_bit_cast(bf16x8, w); }
	v_pk_mul_f32 v[2:3], v[60:61], v[8:9] op_sel_hi:[0,1]
	v_pk_mul_f32 v[2:3], v[2:3], v[46:47]
	v_cmp_gt_u32_e32 vcc, 32, v61
	v_mov_b32_e32 v4, v2
	v_mov_b32_e32 v46, v2
	v_mov_b32_e32 v5, v3
	v_mov_b32_e32 v47, v3
	v_permlane32_swap_b32_e32 v4, v46
	s_nop 0
	v_permlane32_swap_b32_e32 v5, v47
	v_cndmask_b32_e32 v5, v5, v47, vcc
	v_cndmask_b32_e32 v4, v4, v46, vcc
	v_pk_fma_f32 v[2:3], v[4:5], 0, v[2:3] op_sel_hi:[1,0,1]
	s_nop 0
	v_pk_mul_f32 v[2:3], v[2:3], s[94:95] op_sel_hi:[1,0]
	s_nop 0
	v_cvt_pk_bf16_f32 v5, v2, v3
	v_pk_mul_f32 v[2:3], v[60:61], v[6:7] op_sel_hi:[0,1]
	v_pk_mul_f32 v[2:3], v[2:3], v[48:49]
	s_nop 0
	v_mov_b32_e32 v4, v2
	v_mov_b32_e32 v46, v2
	v_mov_b32_e32 v47, v3
	v_mov_b32_e32 v48, v3
	v_permlane32_swap_b32_e32 v4, v46
	s_nop 0
	v_permlane32_swap_b32_e32 v47, v48
	v_cndmask_b32_e32 v47, v47, v48, vcc
	v_cndmask_b32_e32 v46, v4, v46, vcc
	v_pk_fma_f32 v[2:3], v[46:47], 0, v[2:3] op_sel_hi:[1,0,1]
	s_nop 0
	v_pk_mul_f32 v[2:3], v[2:3], s[94:95] op_sel_hi:[1,0]
	s_nop 0
	v_cvt_pk_bf16_f32 v4, v2, v3
	s_waitcnt vmcnt(2)
	v_pk_mul_f32 v[2:3], v[60:61], v[16:17] op_sel_hi:[0,1]
	v_pk_mul_f32 v[2:3], v[2:3], v[12:13]
	s_nop 0
	v_mov_b32_e32 v12, v2
	v_mov_b32_e32 v46, v2
	v_mov_b32_e32 v13, v3
	v_mov_b32_e32 v47, v3
	v_permlane32_swap_b32_e32 v12, v46
	s_nop 0
	v_permlane32_swap_b32_e32 v13, v47
	v_cndmask_b32_e32 v13, v13, v47, vcc
	v_cndmask_b32_e32 v12, v12, v46, vcc
	v_pk_fma_f32 v[2:3], v[12:13], 0, v[2:3] op_sel_hi:[1,0,1]
	v_pk_mul_f32 v[12:13], v[14:15], v[60:61] op_sel_hi:[1,0]
	v_pk_mul_f32 v[2:3], v[2:3], s[94:95] op_sel_hi:[1,0]
	v_pk_mul_f32 v[12:13], v[12:13], v[50:51]
	v_cvt_pk_bf16_f32 v3, v2, v3
	v_mov_b32_e32 v2, v12
	v_mov_b32_e32 v46, v12
	v_mov_b32_e32 v47, v13
	v_mov_b32_e32 v48, v13
	v_permlane32_swap_b32_e32 v2, v46
	s_nop 0
	v_permlane32_swap_b32_e32 v47, v48
	v_cndmask_b32_e32 v47, v47, v48, vcc
	v_cndmask_b32_e32 v46, v2, v46, vcc
	v_pk_fma_f32 v[12:13], v[46:47], 0, v[12:13] op_sel_hi:[1,0,1]
	s_nop 0
	v_pk_mul_f32 v[12:13], v[12:13], s[94:95] op_sel_hi:[1,0]
	s_nop 0
	v_cvt_pk_bf16_f32 v2, v12, v13
	s_waitcnt vmcnt(1)
	v_pk_mul_f32 v[12:13], v[20:21], v[60:61] op_sel_hi:[1,0]
	s_nop 0
	v_pk_mul_f32 v[10:11], v[12:13], v[10:11]
	s_nop 0
	v_mov_b32_e32 v12, v10
	v_mov_b32_e32 v46, v10
	v_mov_b32_e32 v13, v11
	v_mov_b32_e32 v47, v11
	v_permlane32_swap_b32_e32 v12, v46
	s_nop 0
	v_permlane32_swap_b32_e32 v13, v47
	v_cndmask_b32_e32 v13, v13, v47, vcc
	v_cndmask_b32_e32 v12, v12, v46, vcc
	v_pk_fma_f32 v[10:11], v[12:13], 0, v[10:11] op_sel_hi:[1,0,1]
	s_nop 0
	v_pk_mul_f32 v[10:11], v[10:11], s[94:95] op_sel_hi:[1,0]
	s_nop 0
	v_cvt_pk_bf16_f32 v13, v10, v11
	v_pk_mul_f32 v[10:11], v[18:19], v[60:61] op_sel_hi:[1,0]
	s_nop 0
	v_pk_mul_f32 v[10:11], v[10:11], v[52:53]
	s_nop 0
	v_mov_b32_e32 v12, v10
	v_mov_b32_e32 v46, v10
	v_mov_b32_e32 v47, v11
	v_mov_b32_e32 v48, v11
	v_permlane32_swap_b32_e32 v12, v46
	s_nop 0
	v_permlane32_swap_b32_e32 v47, v48
	v_cndmask_b32_e32 v47, v47, v48, vcc
	v_cndmask_b32_e32 v46, v12, v46, vcc
	v_pk_fma_f32 v[10:11], v[46:47], 0, v[10:11] op_sel_hi:[1,0,1]
	s_nop 0
	v_pk_mul_f32 v[10:11], v[10:11], s[94:95] op_sel_hi:[1,0]
	s_nop 0
	v_cvt_pk_bf16_f32 v12, v10, v11
	s_waitcnt vmcnt(0)
	v_pk_mul_f32 v[10:11], v[40:41], v[60:61] op_sel_hi:[1,0]
	s_nop 0
	v_pk_mul_f32 v[10:11], v[10:11], v[44:45]
	s_nop 0
	v_mov_b32_e32 v44, v10
	v_mov_b32_e32 v46, v10
	v_mov_b32_e32 v45, v11
	v_mov_b32_e32 v47, v11
	v_permlane32_swap_b32_e32 v44, v46
	s_nop 0
	v_permlane32_swap_b32_e32 v45, v47
	v_cndmask_b32_e32 v45, v45, v47, vcc
	v_cndmask_b32_e32 v44, v44, v46, vcc
	v_pk_fma_f32 v[10:11], v[44:45], 0, v[10:11] op_sel_hi:[1,0,1]
	v_pk_mul_f32 v[44:45], v[38:39], v[60:61] op_sel_hi:[1,0]
	v_pk_mul_f32 v[10:11], v[10:11], s[94:95] op_sel_hi:[1,0]
	v_pk_mul_f32 v[44:45], v[44:45], v[56:57]
	v_cvt_pk_bf16_f32 v11, v10, v11
	v_mov_b32_e32 v10, v44
	v_mov_b32_e32 v46, v44
	s_nop 1
	v_permlane32_swap_b32_e32 v10, v46
	v_mov_b32_e32 v47, v45
	v_mov_b32_e32 v48, v45
	v_cndmask_b32_e32 v46, v10, v46, vcc
	v_mul_f32_e32 v10, 0x4b800000, v58
	v_permlane32_swap_b32_e32 v47, v48
	v_cndmask_b32_e64 v10, v58, v10, s[4:5]
	v_cndmask_b32_e32 v47, v47, v48, vcc
	v_rsq_f32_e32 v48, v10
	v_pk_fma_f32 v[44:45], v[46:47], 0, v[44:45] op_sel_hi:[1,0,1]
	s_nop 0
	v_pk_mul_f32 v[44:45], v[44:45], s[94:95] op_sel_hi:[1,0]
	s_nop 0
	v_cvt_pk_bf16_f32 v10, v44, v45
	v_mul_f32_e32 v44, 0x45800000, v48
	v_cndmask_b32_e64 v44, v48, v44, s[4:5]
	v_pk_mul_f32 v[38:39], v[38:39], v[44:45] op_sel_hi:[1,0]
	v_pk_mul_f32 v[6:7], v[6:7], v[44:45] op_sel_hi:[1,0]
	v_pk_mul_f32 v[38:39], v[38:39], v[42:43]
	v_pk_mul_f32 v[8:9], v[8:9], v[44:45] op_sel_hi:[1,0]
	v_pk_mul_f32 v[40:41], v[40:41], v[44:45] op_sel_hi:[1,0]
	v_pk_mul_f32 v[6:7], v[6:7], v[26:27]
	v_pk_mul_f32 v[8:9], v[8:9], v[24:25]
	v_mov_b32_e32 v24, v38
	v_mov_b32_e32 v26, v38
	v_mov_b32_e32 v25, v39
	v_mov_b32_e32 v27, v39
	v_pk_mul_f32 v[40:41], v[40:41], v[54:55]
	v_pk_mul_f32 v[16:17], v[16:17], v[44:45] op_sel_hi:[1,0]
	v_permlane32_swap_b32_e32 v24, v26
	v_permlane32_swap_b32_e32 v25, v27
	v_pk_mul_f32 v[18:19], v[18:19], v[44:45] op_sel_hi:[1,0]
	v_pk_mul_f32 v[16:17], v[16:17], v[28:29]
	v_cndmask_b32_e32 v25, v25, v27, vcc
	v_cndmask_b32_e32 v24, v24, v26, vcc
	v_mov_b32_e32 v26, v40
	v_mov_b32_e32 v28, v40
	v_mov_b32_e32 v27, v41
	v_mov_b32_e32 v29, v41
	v_pk_mul_f32 v[18:19], v[18:19], v[34:35]
	v_pk_mul_f32 v[14:15], v[14:15], v[44:45] op_sel_hi:[1,0]
	v_permlane32_swap_b32_e32 v26, v28
	v_permlane32_swap_b32_e32 v27, v29
	v_pk_mul_f32 v[14:15], v[14:15], v[30:31]
	v_cndmask_b32_e32 v27, v27, v29, vcc
	v_cndmask_b32_e32 v26, v26, v28, vcc
; __device__ __forceinline__ unsigned cvtpk(float lo, float hi) { f32x2 v = {lo, hi}; bf16x2_t b = __builtin_convertvector(v, bf16x2_t); return __builtin_bit_cast(unsigned, b); }
; #define ATT_SB() __builtin_amdgcn_sched_barrier(0)
; #define ATT_DMA_K(t, sl) do { glds16(ksrc + (size_t)(t) * 64 * kpitch, (unsigned)__builtin_amdgcn_readfirstlane(kdst + (sl) * KSLOT)); \
;         if constexpr (DQK == 96) glds16(krsrc + (size_t)(t) * 64 * 32, (unsigned)__builtin_amdgcn_readfirstlane(krdst + (sl) * KSLOT)); } while (0)
; #define ATT_DMA_V(t, sl) do { glds16(vsrc + (size_t)(t) * 64, (unsigned)__builtin_amdgcn_readfirstlane(vdst + (sl) * VSLOT)); \
;         if constexpr (DV == 128) glds16(vsrc + (size_t)64 * NR + (size_t)(t) * 64, (unsigned)__builtin_amdgcn_readfirstlane(vdst + (sl) * VSLOT + 8192)); } while (0)
; #define ATT_KLOAD(sl) do { _Pragma("unroll") for (int kb_ = 0; kb_ < NKW; ++kb_) _Pragma("unroll") for (int ds_ = 0; ds_ < NDS; ++ds_) { \
;         if (ds_ < 2) kf[kb_ * NDS + ds_] = *(const LAS bf16x8*)(kp[ds_ & 1] + (sl) * KSLOT + (kb_ & 1) * 512 + (kb_ >> 1) * 4096); \
;         else kf[kb_ * NDS + ds_] = *(const LAS bf16x8*)(krp + (sl) * KSLOT + (kb_ & 1) * 256 + (kb_ >> 1) * 2048); } } while (0)
; template <int DQK, int DV, bool LEAD> ...
;     ...
;           for (int ds = 0; ds < NDS; ++ds) { u32x4 w;
; #pragma unroll
;               for (int i = 0; i < 4; ++i) w[i] = cvtpk(x[ds][2 * i] * c2, x[ds][2 * i + 1] * c2);
;               qf[qb * NDS + ds] = __builtin_bit_cast(bf16x8, w); }
;       }
; #pragma unroll
;       for (int d0 = 0; d0 < NQB * NDS; ++d0) asm volatile("" : "+v"(qf[d0])); }
;     wait_bar<0>();
;     bf16x8 kf[NKW * NDS], vf[NVF];
;     ATT_KLOAD(0);
;     asm volatile("s_waitcnt lgkmcnt(0)\n\ts_barrier" ::: "memory");
;     float lsum[NQB];
; #pragma unroll
;     for (int qb = 0; qb < NQB; ++qb) lsum[qb] = 0.f;
;     const f32x4 zero4 = {0.f, 0.f, 0.f, 0.f};
;     f32x4 o[NDB][NQB], c[NKW][NQB]; u32x4 pw[4];
; #pragma unroll
;     for (int i = 0; i < NDB; ++i)
; #pragma unroll
;         for (int qb = 0; qb < NQB; ++qb) o[i][qb] = zero4;
;     ATT_DMA_K(3, 0); ATT_DMA_V(1, 1);
;     ATT_QK(); ATT_SB();
;     ATT_KLOAD(1); ATT_SB();
;     if constexpr (LEAD) { ATT_EXP(); ATT_SUMPACK(); }
;     wait_bar<NDMA>();
;     int s_prev = 0, s_cur = 1, s_next = 2;
;     int one_ = 1; asm volatile("" : "+s"(one_));
	v_mov_b32_e32 v28, v18
	v_mov_b32_e32 v30, v18
	v_mov_b32_e32 v29, v19
	v_mov_b32_e32 v31, v19
	v_pk_mul_f32 v[20:21], v[20:21], v[44:45] op_sel_hi:[1,0]
	v_permlane32_swap_b32_e32 v28, v30
	v_permlane32_swap_b32_e32 v29, v31
	v_pk_mul_f32 v[20:21], v[20:21], v[32:33]
	v_cndmask_b32_e32 v29, v29, v31, vcc
	v_cndmask_b32_e32 v28, v28, v30, vcc
	v_pk_fma_f32 v[18:19], v[28:29], 0, v[18:19] op_sel_hi:[1,0,1]
	v_mov_b32_e32 v28, v20
	v_mov_b32_e32 v30, v20
	v_mov_b32_e32 v29, v21
	v_mov_b32_e32 v31, v21
	v_permlane32_swap_b32_e32 v28, v30
	s_nop 0
	v_permlane32_swap_b32_e32 v29, v31
	v_cndmask_b32_e32 v29, v29, v31, vcc
	v_cndmask_b32_e32 v28, v28, v30, vcc
	v_pk_fma_f32 v[20:21], v[28:29], 0, v[20:21] op_sel_hi:[1,0,1]
	v_mov_b32_e32 v28, v14
	v_mov_b32_e32 v30, v14
	v_mov_b32_e32 v29, v15
	v_mov_b32_e32 v31, v15
	v_permlane32_swap_b32_e32 v28, v30
	s_nop 0
	v_permlane32_swap_b32_e32 v29, v31
	v_cndmask_b32_e32 v29, v29, v31, vcc
	v_cndmask_b32_e32 v28, v28, v30, vcc
	v_pk_fma_f32 v[14:15], v[28:29], 0, v[14:15] op_sel_hi:[1,0,1]
	v_mov_b32_e32 v28, v16
	v_mov_b32_e32 v30, v16
	v_mov_b32_e32 v29, v17
	v_mov_b32_e32 v31, v17
	v_permlane32_swap_b32_e32 v28, v30
	s_nop 0
	v_permlane32_swap_b32_e32 v29, v31
	v_cndmask_b32_e32 v29, v29, v31, vcc
	v_cndmask_b32_e32 v28, v28, v30, vcc
	v_pk_fma_f32 v[16:17], v[28:29], 0, v[16:17] op_sel_hi:[1,0,1]
	v_mov_b32_e32 v28, v6
	v_mov_b32_e32 v30, v6
	v_mov_b32_e32 v29, v7
	v_mov_b32_e32 v31, v7
	v_permlane32_swap_b32_e32 v28, v30
	s_nop 0
	v_permlane32_swap_b32_e32 v29, v31
	v_cndmask_b32_e32 v29, v29, v31, vcc
	v_cndmask_b32_e32 v28, v28, v30, vcc
	v_pk_fma_f32 v[6:7], v[28:29], 0, v[6:7] op_sel_hi:[1,0,1]
	v_mov_b32_e32 v28, v8
	v_mov_b32_e32 v30, v8
	v_mov_b32_e32 v29, v9
	v_mov_b32_e32 v31, v9
	v_permlane32_swap_b32_e32 v28, v30
	s_nop 0
	v_permlane32_swap_b32_e32 v29, v31
	v_pk_fma_f32 v[24:25], v[24:25], 0, v[38:39] op_sel_hi:[1,0,1]
	v_cndmask_b32_e32 v29, v29, v31, vcc
	v_cndmask_b32_e32 v28, v28, v30, vcc
	v_pk_fma_f32 v[26:27], v[26:27], 0, v[40:41] op_sel_hi:[1,0,1]
	v_pk_fma_f32 v[8:9], v[28:29], 0, v[8:9] op_sel_hi:[1,0,1]
	v_pk_mul_f32 v[24:25], v[24:25], s[94:95] op_sel_hi:[1,0]
	v_pk_mul_f32 v[18:19], v[18:19], s[94:95] op_sel_hi:[1,0]
	v_pk_mul_f32 v[14:15], v[14:15], s[94:95] op_sel_hi:[1,0]
	v_pk_mul_f32 v[6:7], v[6:7], s[94:95] op_sel_hi:[1,0]
	v_cvt_pk_bf16_f32 v58, v24, v25
	v_pk_mul_f32 v[24:25], v[26:27], s[94:95] op_sel_hi:[1,0]
	v_cvt_pk_bf16_f32 v60, v18, v19
	v_pk_mul_f32 v[18:19], v[20:21], s[94:95] op_sel_hi:[1,0]
	v_cvt_pk_bf16_f32 v62, v14, v15
	v_pk_mul_f32 v[14:15], v[16:17], s[94:95] op_sel_hi:[1,0]
	v_cvt_pk_bf16_f32 v64, v6, v7
	v_pk_mul_f32 v[6:7], v[8:9], s[94:95] op_sel_hi:[1,0]
	v_cvt_pk_bf16_f32 v59, v24, v25
	v_cvt_pk_bf16_f32 v61, v18, v19
	v_cvt_pk_bf16_f32 v63, v14, v15
	v_cvt_pk_bf16_f32 v65, v6, v7
	s_waitcnt vmcnt(0) lgkmcnt(0)
	s_barrier
	ds_read_b128 v[6:9], v217
	ds_read_b128 v[14:17], v217 offset:512
	v_bfe_u32 v24, v37, 1, 3
	v_bitop3_b32 v24, v214, v24, 4 bitop3:0x36
	v_lshlrev_b32_e32 v32, 4, v24
	v_add_u32_e32 v220, v66, v32
	s_waitcnt lgkmcnt(1)
	v_mfma_f32_16x16x32_bf16 v[18:21], v[6:9], v[10:13], 0
	ds_read_b128 v[24:27], v220
	ds_read_b128 v[28:31], v220 offset:512
	v_add_u32_e32 v33, 0, v194
	v_add_u32_e32 v218, v33, v67
	v_mfma_f32_16x16x32_bf16 v[6:9], v[6:9], v[58:61], 0
	v_add_u32_e32 v219, v33, v32
	s_waitcnt lgkmcnt(1)
	v_mfma_f32_16x16x32_bf16 v[126:129], v[24:27], v[62:65], v[6:9]
	v_mfma_f32_16x16x32_bf16 v[6:9], v[14:17], v[10:13], 0
	s_waitcnt lgkmcnt(0)
	v_mfma_f32_16x16x32_bf16 v[122:125], v[28:31], v[2:5], v[6:9]
	v_mfma_f32_16x16x32_bf16 v[14:17], v[14:17], v[58:61], 0
	s_nop 4
	ds_read_b128 v[6:9], v217 offset:4096
	v_mfma_f32_16x16x32_bf16 v[138:141], v[24:27], v[2:5], v[18:21]
	v_mfma_f32_16x16x32_bf16 v[114:117], v[28:31], v[62:65], v[14:17]
	s_nop 2
	ds_read_b128 v[14:17], v220 offset:4096
	ds_read_b128 v[18:21], v217 offset:4608
	ds_read_b128 v[28:31], v220 offset:4608
	s_waitcnt lgkmcnt(0)
	s_barrier
	s_waitcnt lgkmcnt(3)
	v_mfma_f32_16x16x32_bf16 v[24:27], v[6:9], v[10:13], 0
	s_mov_b32 s4, m0
	s_mov_b32 m0, s16
	s_nop 0
	global_load_lds_dwordx4 v[210:211], off
	s_mov_b32 m0, s4
	s_add_i32 s4, s29, 0x4000
	v_mfma_f32_16x16x32_bf16 v[6:9], v[6:9], v[58:61], 0
	s_waitcnt lgkmcnt(2)
	v_mfma_f32_16x16x32_bf16 v[130:133], v[14:17], v[2:5], v[24:27]
	v_mfma_f32_16x16x32_bf16 v[118:121], v[14:17], v[62:65], v[6:9]
	v_lshl_add_u64 v[14:15], v[204:205], 0, s[66:67]
	s_mov_b32 s5, m0
	s_mov_b32 m0, s4
	s_nop 0
	global_load_lds_dwordx4 v[14:15], off
	s_mov_b32 m0, s5
	s_mov_b64 s[4:5], 0x840080
	s_waitcnt lgkmcnt(1)
	v_mfma_f32_16x16x32_bf16 v[6:9], v[18:21], v[10:13], 0
	v_lshl_add_u64 v[22:23], v[204:205], 0, s[4:5]
	s_add_i32 s4, s29, 0x6000
	s_mov_b32 s5, m0
	s_mov_b32 m0, s4
	s_nop 0
	global_load_lds_dwordx4 v[22:23], off
	s_mov_b32 m0, s5
	v_mfma_f32_16x16x32_bf16 v[14:17], v[18:21], v[58:61], 0
	s_mov_b32 s4, 0
	s_mov_b32 s6, s4
	s_mov_b32 s7, s4
	s_waitcnt lgkmcnt(0)
	v_mfma_f32_16x16x32_bf16 v[142:145], v[28:31], v[2:5], v[6:9]
	s_mov_b32 s5, s4
	v_mfma_f32_16x16x32_bf16 v[134:137], v[28:31], v[62:65], v[14:17]
	s_nop 0
	v_mov_b64_e32 v[8:9], s[6:7]
	v_mov_b64_e32 v[6:7], s[4:5]
	ds_read_b128 v[82:85], v217 offset:8192
	ds_read_b128 v[86:89], v217 offset:8704
	ds_read_b128 v[90:93], v220 offset:8192
	ds_read_b128 v[94:97], v220 offset:8704
	ds_read_b128 v[98:101], v217 offset:12288
	ds_read_b128 v[102:105], v217 offset:12800
	ds_read_b128 v[106:109], v220 offset:12288
	ds_read_b128 v[110:113], v220 offset:12800
	s_waitcnt vmcnt(3) lgkmcnt(0)
	s_barrier
	s_mov_b32 s5, 1
	v_mov_b32_e32 v42, 0
	s_cmp_lg_u32 s5, 0
	v_mov_b64_e32 v[16:17], v[8:9]
	v_mov_b64_e32 v[20:21], v[8:9]
	v_mov_b64_e32 v[24:25], v[8:9]
	v_mov_b64_e32 v[28:29], v[8:9]
	v_mov_b64_e32 v[32:33], v[8:9]
	v_mov_b64_e32 v[36:37], v[8:9]
	v_mov_b64_e32 v[40:41], v[8:9]
	s_cselect_b64 s[6:7], -1, 0
	v_mov_b64_e32 v[14:15], v[6:7]
	v_mov_b64_e32 v[18:19], v[6:7]
	v_mov_b64_e32 v[22:23], v[6:7]
	v_mov_b64_e32 v[26:27], v[6:7]
	v_mov_b64_e32 v[30:31], v[6:7]
	v_mov_b64_e32 v[34:35], v[6:7]
	v_mov_b64_e32 v[38:39], v[6:7]
	s_mov_b32 s38, 2
	v_mov_b32_e32 v43, v42
	v_mov_b32_e32 v44, v42
	v_mov_b32_e32 v45, v42
	v_mov_b32_e32 v46, v42
	v_mov_b32_e32 v47, v42
	v_mov_b32_e32 v48, v42
	v_mov_b32_e32 v49, v42
	v_mov_b32_e32 v50, v42
	v_mov_b32_e32 v51, v42
	v_mov_b32_e32 v52, v42
	v_mov_b32_e32 v53, v42
	v_mov_b32_e32 v54, v42
	v_mov_b32_e32 v55, v42
	v_mov_b32_e32 v56, v42
	v_mov_b32_e32 v57, v42
	v_mov_b32_e32 v66, v42
	v_mov_b32_e32 v67, v42
	v_mov_b32_e32 v68, v42
	v_mov_b32_e32 v69, v42
	v_mov_b32_e32 v70, v42
	v_mov_b32_e32 v71, v42
	v_mov_b32_e32 v72, v42
	v_mov_b32_e32 v73, v42
	v_mov_b32_e32 v74, v42
	v_mov_b32_e32 v75, v42
	v_mov_b32_e32 v76, v42
	v_mov_b32_e32 v77, v42
	v_mov_b32_e32 v78, v42
	v_mov_b32_e32 v79, v42
	v_mov_b32_e32 v80, v42
	v_mov_b32_e32 v81, v42
	v_mov_b32_e32 v208, v42
	v_mov_b32_e32 v209, v42

; #define LAS __attribute__((address_space(3)))
; #define ATT_DMA_K(t, sl) do { glds16(ksrc + (size_t)(t) * 64 * kpitch, (unsigned)__builtin_amdgcn_readfirstlane(kdst + (sl) * KSLOT)); \
;         if constexpr (DQK == 96) glds16(krsrc + (size_t)(t) * 64 * 32, (unsigned)__builtin_amdgcn_readfirstlane(krdst + (sl) * KSLOT)); } while (0)
; template <int DQK, int DV, bool LEAD> ...
;     ...
;     const int kr0 = 8 * (q16 >> 2) + (q16 & 3);
;     const int fk = ((kr0 >> 1) & 1) | (((kr0 >> 3) & 1) << 1) | (((kr0 >> 4) & 1) << 2);
;     const LAS unsigned char* kp[2]; const LAS unsigned char* vp[2];
; #pragma unroll
;     for (int ds = 0; ds < 2; ++ds) kp[ds] = shm + KOFF + kr0 * 128 + ((((ds << 2) | g4) ^ fk) << 4) + kg * 4096;
;     const LAS unsigned char* krp = shm + KOFF + 8192 + kr0 * 64 + ((g4 ^ (((kr0 >> 4) & 1) << 1)) << 4) + kg * 2048;
; #pragma unroll
;     for (int s_ = 0; s_ < 2; ++s_) vp[s_] = shm + VOFF + q16 * 128 + ((((s_ << 2) | g4) ^ ((q16 >> 1) & 7)) << 4);
;     const LAS unsigned char* vpk = kg ? vp[1] : vp[0];
;     ...
;     ATT_DMA_K(0, 0); ATT_DMA_V(0, 0); ATT_DMA_K(1, 1); ATT_DMA_K(2, 2);
;     bf16x8 qf[NQB * NDS];
;     {
;       const float c2 = (DQK == 64) ? C2_EVEN : C2_ODD; const bool lat = tq0 >= 0;
; #pragma unroll
;       for (int qb = 0; qb < NQB; ++qb) {
;           const bf16_t* qp = Q + (size_t)(qrow0 + qoff + qb * 16 + q16) * qpitch + g4 * 8;
;           bf16x8 raw[NDS];
; #pragma unroll
;           for (int ds = 0; ds < NDS; ++ds) raw[ds] = *(const bf16x8*)(qp + ds * 32);
;           float x[NDS][8];
; #pragma unroll
;           for (int ds = 0; ds < NDS; ++ds)
; #pragma unroll
;               for (int j = 0; j < 8; ++j) x[ds][j] = __uint_as_float(((unsigned)(unsigned short)raw[ds][j]) << 16);
;           const int tq = tq0 + qoff + qb * 16 + q16, prow = (tq >> 6) & 127, pcol = tq & 63;
;           float sn = 0.f;
; #pragma unroll
;           for (int ds = 0; ds < 2; ++ds)
; #pragma unroll
;               for (int j = 0; j < 8; ++j) sn += x[ds][j] * x[ds][j];
;           sn = lanes4_sum(sn);
;           const float rn = rsqrtf(sn * (1.f / 64.f) + EPS);
; #pragma unroll
;           for (int ds = 0; ds < 2; ++ds)
; #pragma unroll
;               for (int j = 0; j < 8; ++j) x[ds][j] *= rn * qgain[32 * ds + 8 * g4 + j];
.LBB0_979:
	v_mov_b32_e32 v37, v0
	s_ashr_i32 s29, s28, 31
	v_readfirstlane_b32 s4, v37
	s_ashr_i32 s7, s4, 6
	v_bfe_u32 v1, v37, 3, 3
	v_lshl_or_b32 v6, s7, 3, v1
	s_lshl_b32 s5, s7, 1
	s_lshr_b32 s4, s4, 5
	v_ashrrev_i32_e32 v2, 1, v6
	s_and_b32 s5, s5, 2
	s_and_b32 s4, s4, 4
	v_and_b32_e32 v170, 7, v37
	v_and_b32_e32 v3, 1, v2
	s_or_b32 s4, s5, s4
	v_bitop3_b32 v7, s4, v170, v3 bitop3:0x36
	v_xor_b32_e32 v8, v2, v37
	v_add_u32_e32 v4, s28, v6
	s_lshl_b32 s4, s7, 10
	v_mov_b64_e32 v[2:3], s[36:37]
	s_add_i32 s25, s4, 0
	v_mad_i64_i32 v[2:3], s[4:5], v4, s92, v[2:3]
	v_mov_b64_e32 v[4:5], s[40:41]
	v_lshlrev_b32_e32 v194, 4, v7
	v_mad_i64_i32 v[4:5], s[4:5], v6, s91, v[4:5]
	v_lshl_add_u64 v[22:23], v[2:3], 0, v[194:195]
	v_lshlrev_b32_e32 v2, 4, v8
	v_lshl_add_u64 v[4:5], s[28:29], 1, v[4:5]
	v_and_b32_e32 v194, 0x70, v2
	s_mov_b32 s4, m0
	s_mov_b32 m0, s25
	s_nop 0
	global_load_lds_dwordx4 v[22:23], off
	s_mov_b32 m0, s4
	v_lshl_add_u64 v[162:163], v[4:5], 0, v[194:195]
	s_add_i32 s29, s25, 0x9000
	s_mov_b32 s4, m0
	s_mov_b32 m0, s29
	s_nop 0
	global_load_lds_dwordx4 v[162:163], off
	s_mov_b32 m0, s4
	s_mov_b64 s[4:5], 0x840000
	v_lshl_add_u64 v[164:165], v[162:163], 0, s[4:5]
	s_add_i32 s4, s29, 0x2000
	s_mov_b32 s5, m0
	s_mov_b32 m0, s4
	s_nop 0
	global_load_lds_dwordx4 v[164:165], off
	s_mov_b32 m0, s5
	s_mov_b64 s[4:5], 0x38000
	s_lshl_b32 s6, s7, 5
	v_lshl_add_u64 v[2:3], v[22:23], 0, s[4:5]
	s_add_i32 s4, s25, 0x2000
	s_mov_b32 s5, m0
	s_mov_b32 m0, s4
	s_nop 0
	global_load_lds_dwordx4 v[2:3], off
	s_mov_b32 m0, s5
	v_and_b32_e32 v36, 15, v37
	s_mov_b64 s[4:5], 0x70000
	s_add_i32 s6, s6, s28
	v_and_b32_e32 v194, 48, v37
	v_lshl_add_u64 v[2:3], v[22:23], 0, s[4:5]
	s_add_i32 s4, s25, 0x4000
	v_or_b32_e32 v8, s6, v36
	v_lshl_add_u64 v[6:7], s[26:27], 0, v[194:195]
	s_mov_b32 s5, m0
	s_mov_b32 m0, s4
	s_nop 0
	global_load_lds_dwordx4 v[2:3], off
	s_mov_b32 m0, s5
	v_bfe_u32 v171, v37, 4, 2
	v_mad_i64_i32 v[10:11], s[4:5], v8, s92, v[6:7]
	v_or_b32_e32 v8, 16, v8
	v_mad_i64_i32 v[12:13], s[4:5], v8, s92, v[6:7]
	global_load_dwordx4 v[2:5], v[10:11], off offset:64 nt
	global_load_dwordx4 v[6:9], v[12:13], off offset:64 nt
	global_load_dwordx4 v[38:41], v[10:11], off nt
	global_load_dwordx4 v[42:45], v[12:13], off nt
	v_lshlrev_b32_e32 v172, 1, v37
	v_and_b32_e32 v10, 3, v37
	v_lshrrev_b32_e32 v11, 1, v37
	v_and_or_b32 v10, v172, 24, v10
	v_lshlrev_b32_e32 v62, 5, v171
	v_bitop3_b32 v60, v171, v11, 7 bitop3:0x78
	v_lshl_add_u32 v63, v10, 7, 0
	global_load_dwordx4 v[10:13], v62, s[22:23] offset:144
	global_load_dwordx4 v[14:17], v62, s[22:23] offset:128
	global_load_dwordx4 v[18:21], v62, s[22:23] offset:16
	s_mov_b32 s4, 0x3c800000
	v_and_b32_e32 v61, 63, v37
	v_lshlrev_b32_e32 v64, 4, v60
	v_add_u32_e32 v175, v63, v64
	v_lshlrev_b32_e32 v174, 7, v36
	v_lshl_add_u64 v[168:169], v[22:23], 0, s[96:97]
	v_lshl_add_u64 v[22:23], v[162:163], 0, s[66:67]
	s_mov_b32 s16, 2
	v_or_b32_e32 v173, 4, v171
	s_waitcnt vmcnt(5)
	v_and_b32_e32 v25, 0xffff0000, v9
	s_waitcnt vmcnt(4)
	v_and_b32_e32 v57, 0xffff0000, v38
	v_and_b32_e32 v51, 0xffff0000, v2
	v_lshlrev_b32_e32 v50, 16, v2
	v_lshlrev_b32_e32 v56, 16, v38
	v_mul_f32_e32 v2, v57, v57
	v_lshlrev_b32_e32 v24, 16, v9
	v_and_b32_e32 v27, 0xffff0000, v8
	v_lshlrev_b32_e32 v26, 16, v8
	v_and_b32_e32 v9, 0xffff0000, v3
	v_lshlrev_b32_e32 v8, 16, v3
	s_waitcnt vmcnt(3)
	v_and_b32_e32 v33, 0xffff0000, v45
	v_lshlrev_b32_e32 v32, 16, v45
	v_and_b32_e32 v35, 0xffff0000, v44
	v_lshlrev_b32_e32 v34, 16, v44
	v_and_b32_e32 v45, 0xffff0000, v39
	v_lshlrev_b32_e32 v44, 16, v39
	v_pk_fma_f32 v[2:3], v[56:57], v[56:57], v[2:3] op_sel_hi:[1,1,0]
	v_and_b32_e32 v49, 0xffff0000, v4
	v_lshlrev_b32_e32 v48, 16, v4
	v_pk_fma_f32 v[2:3], v[44:45], v[44:45], v[2:3]
	v_mul_f32_e32 v4, v45, v45
	v_and_b32_e32 v53, 0xffff0000, v40
	v_lshlrev_b32_e32 v52, 16, v40
	v_pk_add_f32 v[2:3], v[4:5], v[2:3] op_sel_hi:[0,1]
	v_pk_fma_f32 v[2:3], v[52:53], v[52:53], v[2:3]
	v_mul_f32_e32 v4, v53, v53
	v_and_b32_e32 v29, 0xffff0000, v7
	v_lshlrev_b32_e32 v28, 16, v7
	v_and_b32_e32 v31, 0xffff0000, v6
	v_lshlrev_b32_e32 v30, 16, v6
	v_and_b32_e32 v7, 0xffff0000, v41
	v_lshlrev_b32_e32 v6, 16, v41
	v_pk_add_f32 v[2:3], v[4:5], v[2:3] op_sel_hi:[0,1]
	v_pk_fma_f32 v[2:3], v[6:7], v[6:7], v[2:3]
	v_mul_f32_e32 v4, v7, v7
	v_pk_add_f32 v[2:3], v[4:5], v[2:3] op_sel_hi:[0,1]
	v_pk_fma_f32 v[2:3], v[50:51], v[50:51], v[2:3]
	v_mul_f32_e32 v4, v51, v51
	v_pk_add_f32 v[2:3], v[4:5], v[2:3] op_sel_hi:[0,1]
	v_pk_fma_f32 v[2:3], v[8:9], v[8:9], v[2:3]
	v_mul_f32_e32 v4, v9, v9
	v_pk_add_f32 v[2:3], v[4:5], v[2:3] op_sel_hi:[0,1]
	v_pk_fma_f32 v[2:3], v[48:49], v[48:49], v[2:3]
	v_mul_f32_e32 v4, v49, v49
	v_and_b32_e32 v47, 0xffff0000, v5
	v_lshlrev_b32_e32 v46, 16, v5
	v_pk_add_f32 v[2:3], v[4:5], v[2:3] op_sel_hi:[0,1]
	v_pk_fma_f32 v[2:3], v[46:47], v[46:47], v[2:3]
	v_mul_f32_e32 v4, v47, v47
	v_pk_add_f32 v[2:3], v[4:5], v[2:3] op_sel_hi:[0,1]
	v_mov_b32_e32 v3, v2
	s_nop 1
	v_permlane16_swap_b32_e32 v2, v3
	v_add_f32_e32 v3, v2, v3
	v_and_b32_e32 v55, 0xffff0000, v43
	v_lshlrev_b32_e32 v54, 16, v43
	v_mov_b32_e32 v5, v3
	v_and_b32_e32 v43, 0xffff0000, v42
	s_nop 0
	v_permlane32_swap_b32_e32 v3, v5
	v_lshlrev_b32_e32 v42, 16, v42
	v_mul_f32_e32 v2, v43, v43
	v_pk_fma_f32 v[38:39], v[42:43], v[42:43], v[2:3] op_sel_hi:[1,1,0]
	v_mul_f32_e32 v2, v55, v55
	v_pk_fma_f32 v[38:39], v[54:55], v[54:55], v[38:39]
	s_nop 0
	v_pk_add_f32 v[38:39], v[2:3], v[38:39] op_sel_hi:[0,1]
	v_pk_fma_f32 v[38:39], v[34:35], v[34:35], v[38:39]
	v_mul_f32_e32 v2, v35, v35
	v_pk_add_f32 v[38:39], v[2:3], v[38:39] op_sel_hi:[0,1]
	v_pk_fma_f32 v[38:39], v[32:33], v[32:33], v[38:39]
	v_mul_f32_e32 v2, v33, v33
	v_pk_add_f32 v[38:39], v[2:3], v[38:39] op_sel_hi:[0,1]
	v_pk_fma_f32 v[38:39], v[30:31], v[30:31], v[38:39]
	v_mul_f32_e32 v2, v31, v31
	v_pk_add_f32 v[38:39], v[2:3], v[38:39] op_sel_hi:[0,1]
	v_pk_fma_f32 v[38:39], v[28:29], v[28:29], v[38:39]
	v_mul_f32_e32 v2, v29, v29
	v_pk_add_f32 v[38:39], v[2:3], v[38:39] op_sel_hi:[0,1]
	v_pk_fma_f32 v[38:39], v[26:27], v[26:27], v[38:39]
	v_mul_f32_e32 v2, v27, v27
	v_pk_add_f32 v[38:39], v[2:3], v[38:39] op_sel_hi:[0,1]
	v_pk_fma_f32 v[38:39], v[24:25], v[24:25], v[38:39]
	v_mul_f32_e32 v2, v25, v25
	v_pk_add_f32 v[38:39], v[2:3], v[38:39] op_sel_hi:[0,1]
	v_mov_b32_e32 v2, v38
	s_nop 1
	v_permlane16_swap_b32_e32 v38, v2
	v_add_f32_e32 v2, v38, v2
	global_load_dwordx4 v[38:41], v62, s[22:23]
	v_mov_b32_e32 v4, v2
	s_nop 1
	v_permlane32_swap_b32_e32 v2, v4
	v_pk_add_f32 v[2:3], v[2:3], v[4:5]
	s_mov_b32 s22, 1
	v_pk_fma_f32 v[58:59], v[2:3], s[4:5], v[196:197] op_sel_hi:[1,0,0]
	s_mov_b32 s23, 0
	v_mul_f32_e32 v2, 0x4b800000, v59
	v_cmp_gt_f32_e32 vcc, s95, v59
	v_cmp_gt_f32_e64 s[4:5], s95, v58
	s_nop 0
	v_cndmask_b32_e32 v2, v59, v2, vcc
	v_rsq_f32_e32 v2, v2
	s_nop 0
	v_mul_f32_e32 v3, 0x45800000, v2
	v_cndmask_b32_e32 v60, v2, v3, vcc
	s_waitcnt vmcnt(3)
; __device__ __forceinline__ unsigned cvtpk(float lo, float hi) { f32x2 v = {lo, hi}; bf16x2_t b = __builtin_convertvector(v, bf16x2_t); return __builtin_bit_cast(unsigned, b); }
; template <int DQK, int DV, bool LEAD> ...
;     ...
; #pragma unroll
;           for (int ds = 0; ds < 2; ++ds)
; #pragma unroll
;               for (int j = 0; j < 8; ++j) x[ds][j] *= rn * qgain[32 * ds + 8 * g4 + j];
;           if constexpr (DQK == 64) {
; #pragma unroll
;               for (int ds = 0; ds < 2; ++ds)
; #pragma unroll
;                   for (int j = 0; j < 8; ++j) {
;                       auto rr = __builtin_amdgcn_permlane32_swap(__float_as_uint(x[ds][j]), __float_as_uint(x[ds][j]), false, false);
;                       const float other = hi ? __uint_as_float(rr[0]) : __uint_as_float(rr[1]);
;                       float cc = 1.f, sg = 0.f;
;                       if (lat) { const f32x2 cs = rope[(ds ? pcol : prow) * 16 + 8 * (g4 & 1) + j]; cc = cs.x; sg = hi ? cs.y : -cs.y; }
;                       x[ds][j] = x[ds][j] * cc + other * sg; }
;           } else {
;               float sr = 0.f;
; #pragma unroll
;               for (int j = 0; j < 8; ++j) sr += x[2][j] * x[2][j];
;               sr = lanes4_sum(sr);
;               const float rq = rsqrtf(sr * (1.f / 32.f) + EPS);
; #pragma unroll
;               for (int j = 0; j < 8; ++j) { const float av = x[2][j] * rq * qgain[64 + 8 * g4 + j];
;                   auto rr = __builtin_amdgcn_permlane16_swap(__float_as_uint(av), __float_as_uint(av), false, false);
;                   const float other = (g4 & 1) ? __uint_as_float(rr[0]) : __uint_as_float(rr[1]);
;                   float cc = 1.f, sg = 0.f;
;                   if (lat) { const f32x2 cs = rope[((g4 & 2) ? pcol : prow) * 8 + j]; cc = cs.x; sg = (g4 & 1) ? cs.y : -cs.y; }
;                   x[2][j] = av * cc + other * sg; }
;           }
; #pragma unroll
;           for (int ds = 0; ds < NDS; ++ds) { u32x4 w;
; #pragma unroll
;               for (int i = 0; i < 4; ++i) w[i] = cvtpk(x[ds][2 * i] * c2, x[ds][2 * i + 1] * c2);
;               qf[qb * NDS + ds] = __builtin_bit_cast(bf16x8, w); }
	v_pk_mul_f32 v[2:3], v[60:61], v[12:13] op_sel_hi:[0,1]
	v_pk_mul_f32 v[2:3], v[2:3], v[46:47]
	v_cmp_gt_u32_e32 vcc, 32, v61
	v_mov_b32_e32 v4, v2
	v_mov_b32_e32 v46, v2
	v_mov_b32_e32 v5, v3
	v_mov_b32_e32 v47, v3
	v_permlane32_swap_b32_e32 v4, v46
	s_nop 0
	v_permlane32_swap_b32_e32 v5, v47
	v_cndmask_b32_e32 v5, v5, v47, vcc
	v_cndmask_b32_e32 v4, v4, v46, vcc
	v_pk_fma_f32 v[2:3], v[4:5], 0, v[2:3] op_sel_hi:[1,0,1]
	s_nop 0
	v_pk_mul_f32 v[2:3], v[2:3], s[94:95] op_sel_hi:[1,0]
	s_nop 0
	v_cvt_pk_bf16_f32 v5, v2, v3
	v_pk_mul_f32 v[2:3], v[60:61], v[10:11] op_sel_hi:[0,1]
	v_pk_mul_f32 v[2:3], v[2:3], v[48:49]
	s_nop 0
	v_mov_b32_e32 v4, v2
	v_mov_b32_e32 v46, v2
	v_mov_b32_e32 v47, v3
	v_mov_b32_e32 v48, v3
	v_permlane32_swap_b32_e32 v4, v46
	s_nop 0
	v_permlane32_swap_b32_e32 v47, v48
	v_cndmask_b32_e32 v47, v47, v48, vcc
	v_cndmask_b32_e32 v46, v4, v46, vcc
	v_pk_fma_f32 v[2:3], v[46:47], 0, v[2:3] op_sel_hi:[1,0,1]
	s_nop 0
	v_pk_mul_f32 v[2:3], v[2:3], s[94:95] op_sel_hi:[1,0]
	s_nop 0
	v_cvt_pk_bf16_f32 v4, v2, v3
	s_waitcnt vmcnt(2)
	v_pk_mul_f32 v[2:3], v[60:61], v[16:17] op_sel_hi:[0,1]
	v_pk_mul_f32 v[2:3], v[2:3], v[8:9]
	s_nop 0
	v_mov_b32_e32 v8, v2
	v_mov_b32_e32 v46, v2
	v_mov_b32_e32 v9, v3
	v_mov_b32_e32 v47, v3
	v_permlane32_swap_b32_e32 v8, v46
	s_nop 0
	v_permlane32_swap_b32_e32 v9, v47
	v_cndmask_b32_e32 v9, v9, v47, vcc
	v_cndmask_b32_e32 v8, v8, v46, vcc
	v_pk_fma_f32 v[2:3], v[8:9], 0, v[2:3] op_sel_hi:[1,0,1]
	v_pk_mul_f32 v[8:9], v[14:15], v[60:61] op_sel_hi:[1,0]
	v_pk_mul_f32 v[2:3], v[2:3], s[94:95] op_sel_hi:[1,0]
	v_pk_mul_f32 v[8:9], v[8:9], v[50:51]
	v_cvt_pk_bf16_f32 v3, v2, v3
	v_mov_b32_e32 v2, v8
	v_mov_b32_e32 v46, v8
	v_mov_b32_e32 v47, v9
	v_mov_b32_e32 v48, v9
	v_permlane32_swap_b32_e32 v2, v46
	s_nop 0
	v_permlane32_swap_b32_e32 v47, v48
	v_cndmask_b32_e32 v47, v47, v48, vcc
	v_cndmask_b32_e32 v46, v2, v46, vcc
	v_pk_fma_f32 v[8:9], v[46:47], 0, v[8:9] op_sel_hi:[1,0,1]
	s_nop 0
	v_pk_mul_f32 v[8:9], v[8:9], s[94:95] op_sel_hi:[1,0]
	s_nop 0
	v_cvt_pk_bf16_f32 v2, v8, v9
	s_waitcnt vmcnt(1)
	v_pk_mul_f32 v[8:9], v[20:21], v[60:61] op_sel_hi:[1,0]
	s_nop 0
	v_pk_mul_f32 v[6:7], v[8:9], v[6:7]
	s_nop 0
	v_mov_b32_e32 v8, v6
	v_mov_b32_e32 v46, v6
	v_mov_b32_e32 v9, v7
	v_mov_b32_e32 v47, v7
	v_permlane32_swap_b32_e32 v8, v46
	s_nop 0
	v_permlane32_swap_b32_e32 v9, v47
	v_cndmask_b32_e32 v9, v9, v47, vcc
	v_cndmask_b32_e32 v8, v8, v46, vcc
	v_pk_fma_f32 v[6:7], v[8:9], 0, v[6:7] op_sel_hi:[1,0,1]
	s_nop 0
	v_pk_mul_f32 v[6:7], v[6:7], s[94:95] op_sel_hi:[1,0]
	s_nop 0
	v_cvt_pk_bf16_f32 v9, v6, v7
	v_pk_mul_f32 v[6:7], v[18:19], v[60:61] op_sel_hi:[1,0]
	s_nop 0
	v_pk_mul_f32 v[6:7], v[6:7], v[52:53]
	s_nop 0
	v_mov_b32_e32 v8, v6
	v_mov_b32_e32 v46, v6
	v_mov_b32_e32 v47, v7
	v_mov_b32_e32 v48, v7
	v_permlane32_swap_b32_e32 v8, v46
	s_nop 0
	v_permlane32_swap_b32_e32 v47, v48
	v_cndmask_b32_e32 v47, v47, v48, vcc
	v_cndmask_b32_e32 v46, v8, v46, vcc
	v_pk_fma_f32 v[6:7], v[46:47], 0, v[6:7] op_sel_hi:[1,0,1]
	s_nop 0
	v_pk_mul_f32 v[6:7], v[6:7], s[94:95] op_sel_hi:[1,0]
	s_nop 0
	v_cvt_pk_bf16_f32 v8, v6, v7
	s_waitcnt vmcnt(0)
	v_pk_mul_f32 v[6:7], v[40:41], v[60:61] op_sel_hi:[1,0]
	s_nop 0
	v_pk_mul_f32 v[6:7], v[6:7], v[44:45]
	s_nop 0
	v_mov_b32_e32 v44, v6
	v_mov_b32_e32 v46, v6
	v_mov_b32_e32 v45, v7
	v_mov_b32_e32 v47, v7
	v_permlane32_swap_b32_e32 v44, v46
	s_nop 0
	v_permlane32_swap_b32_e32 v45, v47
	v_cndmask_b32_e32 v45, v45, v47, vcc
	v_cndmask_b32_e32 v44, v44, v46, vcc
	v_pk_fma_f32 v[6:7], v[44:45], 0, v[6:7] op_sel_hi:[1,0,1]
	v_pk_mul_f32 v[44:45], v[38:39], v[60:61] op_sel_hi:[1,0]
	v_pk_mul_f32 v[6:7], v[6:7], s[94:95] op_sel_hi:[1,0]
	v_pk_mul_f32 v[44:45], v[44:45], v[56:57]
	v_cvt_pk_bf16_f32 v7, v6, v7
	v_mov_b32_e32 v6, v44
	v_mov_b32_e32 v46, v44
	s_nop 1
	v_permlane32_swap_b32_e32 v6, v46
	v_mov_b32_e32 v47, v45
	v_mov_b32_e32 v48, v45
	v_cndmask_b32_e32 v46, v6, v46, vcc
	v_mul_f32_e32 v6, 0x4b800000, v58
	v_permlane32_swap_b32_e32 v47, v48
	v_cndmask_b32_e64 v6, v58, v6, s[4:5]
	v_cndmask_b32_e32 v47, v47, v48, vcc
	v_rsq_f32_e32 v48, v6
	v_pk_fma_f32 v[44:45], v[46:47], 0, v[44:45] op_sel_hi:[1,0,1]
	s_nop 0
	v_pk_mul_f32 v[44:45], v[44:45], s[94:95] op_sel_hi:[1,0]
	s_nop 0
	v_cvt_pk_bf16_f32 v6, v44, v45
	v_mul_f32_e32 v44, 0x45800000, v48
	v_cndmask_b32_e64 v44, v48, v44, s[4:5]
	v_pk_mul_f32 v[38:39], v[38:39], v[44:45] op_sel_hi:[1,0]
	v_pk_mul_f32 v[10:11], v[10:11], v[44:45] op_sel_hi:[1,0]
	v_pk_mul_f32 v[38:39], v[38:39], v[42:43]
	v_pk_mul_f32 v[12:13], v[12:13], v[44:45] op_sel_hi:[1,0]
	v_pk_mul_f32 v[40:41], v[40:41], v[44:45] op_sel_hi:[1,0]
	v_pk_mul_f32 v[10:11], v[10:11], v[26:27]
	v_pk_mul_f32 v[12:13], v[12:13], v[24:25]
	v_mov_b32_e32 v24, v38
	v_mov_b32_e32 v26, v38
	v_mov_b32_e32 v25, v39
	v_mov_b32_e32 v27, v39
	v_pk_mul_f32 v[40:41], v[40:41], v[54:55]
	v_pk_mul_f32 v[16:17], v[16:17], v[44:45] op_sel_hi:[1,0]
	v_permlane32_swap_b32_e32 v24, v26
	v_permlane32_swap_b32_e32 v25, v27
	v_pk_mul_f32 v[18:19], v[18:19], v[44:45] op_sel_hi:[1,0]
	v_pk_mul_f32 v[16:17], v[16:17], v[28:29]
	v_cndmask_b32_e32 v25, v25, v27, vcc
	v_cndmask_b32_e32 v24, v24, v26, vcc
	v_mov_b32_e32 v26, v40
	v_mov_b32_e32 v28, v40
	v_mov_b32_e32 v27, v41
	v_mov_b32_e32 v29, v41
	v_pk_mul_f32 v[18:19], v[18:19], v[34:35]
	v_pk_mul_f32 v[14:15], v[14:15], v[44:45] op_sel_hi:[1,0]
	v_permlane32_swap_b32_e32 v26, v28
	v_permlane32_swap_b32_e32 v27, v29
	v_pk_mul_f32 v[14:15], v[14:15], v[30:31]
	v_cndmask_b32_e32 v27, v27, v29, vcc
	v_cndmask_b32_e32 v26, v26, v28, vcc
	v_mov_b32_e32 v28, v18
	v_mov_b32_e32 v30, v18
	v_mov_b32_e32 v29, v19
	v_mov_b32_e32 v31, v19
; __device__ __forceinline__ unsigned cvtpk(float lo, float hi) { f32x2 v = {lo, hi}; bf16x2_t b = __builtin_convertvector(v, bf16x2_t); return __builtin_bit_cast(unsigned, b); }
; #define ATT_SB() __builtin_amdgcn_sched_barrier(0)
; #define ATT_DMA_K(t, sl) do { glds16(ksrc + (size_t)(t) * 64 * kpitch, (unsigned)__builtin_amdgcn_readfirstlane(kdst + (sl) * KSLOT)); \
;         if constexpr (DQK == 96) glds16(krsrc + (size_t)(t) * 64 * 32, (unsigned)__builtin_amdgcn_readfirstlane(krdst + (sl) * KSLOT)); } while (0)
; #define ATT_DMA_V(t, sl) do { glds16(vsrc + (size_t)(t) * 64, (unsigned)__builtin_amdgcn_readfirstlane(vdst + (sl) * VSLOT)); \
;         if constexpr (DV == 128) glds16(vsrc + (size_t)64 * NR + (size_t)(t) * 64, (unsigned)__builtin_amdgcn_readfirstlane(vdst + (sl) * VSLOT + 8192)); } while (0)
; #define ATT_KLOAD(sl) do { _Pragma("unroll") for (int kb_ = 0; kb_ < NKW; ++kb_) _Pragma("unroll") for (int ds_ = 0; ds_ < NDS; ++ds_) { \
;         if (ds_ < 2) kf[kb_ * NDS + ds_] = *(const LAS bf16x8*)(kp[ds_ & 1] + (sl) * KSLOT + (kb_ & 1) * 512 + (kb_ >> 1) * 4096); \
;         else kf[kb_ * NDS + ds_] = *(const LAS bf16x8*)(krp + (sl) * KSLOT + (kb_ & 1) * 256 + (kb_ >> 1) * 2048); } } while (0)
; template <int DQK, int DV, bool LEAD> ...
;     ...
;           for (int ds = 0; ds < NDS; ++ds) { u32x4 w;
; #pragma unroll
;               for (int i = 0; i < 4; ++i) w[i] = cvtpk(x[ds][2 * i] * c2, x[ds][2 * i + 1] * c2);
;               qf[qb * NDS + ds] = __builtin_bit_cast(bf16x8, w); }
;       }
; #pragma unroll
;       for (int d0 = 0; d0 < NQB * NDS; ++d0) asm volatile("" : "+v"(qf[d0])); }
;     wait_bar<0>();
;     bf16x8 kf[NKW * NDS], vf[NVF];
;     ATT_KLOAD(0);
;     asm volatile("s_waitcnt lgkmcnt(0)\n\ts_barrier" ::: "memory");
;     float lsum[NQB];
; #pragma unroll
;     for (int qb = 0; qb < NQB; ++qb) lsum[qb] = 0.f;
;     const f32x4 zero4 = {0.f, 0.f, 0.f, 0.f};
;     f32x4 o[NDB][NQB], c[NKW][NQB]; u32x4 pw[4];
; #pragma unroll
;     for (int i = 0; i < NDB; ++i)
; #pragma unroll
;         for (int qb = 0; qb < NQB; ++qb) o[i][qb] = zero4;
;     ATT_DMA_K(3, 0); ATT_DMA_V(1, 1);
;     ATT_QK(); ATT_SB();
;     ATT_KLOAD(1); ATT_SB();
	v_pk_mul_f32 v[20:21], v[20:21], v[44:45] op_sel_hi:[1,0]
	v_permlane32_swap_b32_e32 v28, v30
	v_permlane32_swap_b32_e32 v29, v31
	v_pk_mul_f32 v[20:21], v[20:21], v[32:33]
	v_cndmask_b32_e32 v29, v29, v31, vcc
	v_cndmask_b32_e32 v28, v28, v30, vcc
	v_pk_fma_f32 v[18:19], v[28:29], 0, v[18:19] op_sel_hi:[1,0,1]
	v_mov_b32_e32 v28, v20
	v_mov_b32_e32 v30, v20
	v_mov_b32_e32 v29, v21
	v_mov_b32_e32 v31, v21
	v_permlane32_swap_b32_e32 v28, v30
	s_nop 0
	v_permlane32_swap_b32_e32 v29, v31
	v_cndmask_b32_e32 v29, v29, v31, vcc
	v_cndmask_b32_e32 v28, v28, v30, vcc
	v_pk_fma_f32 v[20:21], v[28:29], 0, v[20:21] op_sel_hi:[1,0,1]
	v_mov_b32_e32 v28, v14
	v_mov_b32_e32 v30, v14
	v_mov_b32_e32 v29, v15
	v_mov_b32_e32 v31, v15
	v_permlane32_swap_b32_e32 v28, v30
	s_nop 0
	v_permlane32_swap_b32_e32 v29, v31
	v_cndmask_b32_e32 v29, v29, v31, vcc
	v_cndmask_b32_e32 v28, v28, v30, vcc
	v_pk_fma_f32 v[14:15], v[28:29], 0, v[14:15] op_sel_hi:[1,0,1]
	v_mov_b32_e32 v28, v16
	v_mov_b32_e32 v30, v16
	v_mov_b32_e32 v29, v17
	v_mov_b32_e32 v31, v17
	v_permlane32_swap_b32_e32 v28, v30
	s_nop 0
	v_permlane32_swap_b32_e32 v29, v31
	v_cndmask_b32_e32 v29, v29, v31, vcc
	v_cndmask_b32_e32 v28, v28, v30, vcc
	v_pk_fma_f32 v[16:17], v[28:29], 0, v[16:17] op_sel_hi:[1,0,1]
	v_mov_b32_e32 v28, v10
	v_mov_b32_e32 v30, v10
	v_mov_b32_e32 v29, v11
	v_mov_b32_e32 v31, v11
	v_permlane32_swap_b32_e32 v28, v30
	s_nop 0
	v_permlane32_swap_b32_e32 v29, v31
	v_cndmask_b32_e32 v29, v29, v31, vcc
	v_cndmask_b32_e32 v28, v28, v30, vcc
	v_pk_fma_f32 v[28:29], v[28:29], 0, v[10:11] op_sel_hi:[1,0,1]
	v_mov_b32_e32 v10, v12
	v_mov_b32_e32 v30, v12
	v_mov_b32_e32 v11, v13
	v_mov_b32_e32 v31, v13
	v_permlane32_swap_b32_e32 v10, v30
	s_nop 0
	v_permlane32_swap_b32_e32 v11, v31
	v_pk_fma_f32 v[24:25], v[24:25], 0, v[38:39] op_sel_hi:[1,0,1]
	v_pk_fma_f32 v[26:27], v[26:27], 0, v[40:41] op_sel_hi:[1,0,1]
	v_cndmask_b32_e32 v11, v11, v31, vcc
	v_cndmask_b32_e32 v10, v10, v30, vcc
	v_pk_fma_f32 v[30:31], v[10:11], 0, v[12:13] op_sel_hi:[1,0,1]
	v_pk_mul_f32 v[10:11], v[24:25], s[94:95] op_sel_hi:[1,0]
	v_pk_mul_f32 v[12:13], v[26:27], s[94:95] op_sel_hi:[1,0]
	v_cvt_pk_bf16_f32 v10, v10, v11
	v_cvt_pk_bf16_f32 v11, v12, v13
	v_pk_mul_f32 v[12:13], v[18:19], s[94:95] op_sel_hi:[1,0]
	v_pk_mul_f32 v[18:19], v[20:21], s[94:95] op_sel_hi:[1,0]
	v_pk_mul_f32 v[14:15], v[14:15], s[94:95] op_sel_hi:[1,0]
	v_pk_mul_f32 v[16:17], v[16:17], s[94:95] op_sel_hi:[1,0]
	v_cvt_pk_bf16_f32 v12, v12, v13
	v_cvt_pk_bf16_f32 v13, v18, v19
	v_cvt_pk_bf16_f32 v14, v14, v15
	v_cvt_pk_bf16_f32 v15, v16, v17
	v_pk_mul_f32 v[16:17], v[28:29], s[94:95] op_sel_hi:[1,0]
	v_pk_mul_f32 v[18:19], v[30:31], s[94:95] op_sel_hi:[1,0]
	v_cvt_pk_bf16_f32 v16, v16, v17
	v_cvt_pk_bf16_f32 v17, v18, v19
	s_waitcnt vmcnt(0) lgkmcnt(0)
	s_barrier
	ds_read_b128 v[18:21], v175
	ds_read_b128 v[24:27], v175 offset:512
	v_bfe_u32 v32, v37, 1, 3
	v_bitop3_b32 v32, v171, v32, 4 bitop3:0x36
	v_lshlrev_b32_e32 v37, 4, v32
	v_add_u32_e32 v178, v63, v37
	s_waitcnt lgkmcnt(1)
	v_mfma_f32_16x16x32_bf16 v[28:31], v[18:21], v[6:9], 0
	ds_read_b128 v[32:35], v178
	ds_read_b128 v[38:41], v178 offset:512
	v_mfma_f32_16x16x32_bf16 v[18:21], v[18:21], v[10:13], 0
	s_waitcnt lgkmcnt(1)
	v_mfma_f32_16x16x32_bf16 v[42:45], v[32:35], v[2:5], v[28:31]
	v_mfma_f32_16x16x32_bf16 v[28:31], v[24:27], v[6:9], 0
	v_mfma_f32_16x16x32_bf16 v[24:27], v[24:27], v[10:13], 0
	v_mfma_f32_16x16x32_bf16 v[18:21], v[32:35], v[14:17], v[18:21]
	s_waitcnt lgkmcnt(0)
	v_mfma_f32_16x16x32_bf16 v[30:33], v[38:41], v[2:5], v[28:31]
	v_mfma_f32_16x16x32_bf16 v[58:61], v[38:41], v[14:17], v[24:27]
	s_nop 3
	ds_read_b128 v[24:27], v175 offset:4096
	ds_read_b128 v[38:41], v175 offset:4608
	ds_read_b128 v[50:53], v178 offset:4096
	ds_read_b128 v[54:57], v178 offset:4608
	s_waitcnt lgkmcnt(3)
	v_mfma_f32_16x16x32_bf16 v[46:49], v[24:27], v[6:9], 0
	v_add_u32_e32 v28, 0, v174
	v_add_u32_e32 v177, v28, v37
	s_waitcnt lgkmcnt(0)
	s_barrier
; #define ATT_SB() __builtin_amdgcn_sched_barrier(0)
; #define ATT_DMA_K(t, sl) do { glds16(ksrc + (size_t)(t) * 64 * kpitch, (unsigned)__builtin_amdgcn_readfirstlane(kdst + (sl) * KSLOT)); \
;         if constexpr (DQK == 96) glds16(krsrc + (size_t)(t) * 64 * 32, (unsigned)__builtin_amdgcn_readfirstlane(krdst + (sl) * KSLOT)); } while (0)
; #define ATT_DMA_V(t, sl) do { glds16(vsrc + (size_t)(t) * 64, (unsigned)__builtin_amdgcn_readfirstlane(vdst + (sl) * VSLOT)); \
;         if constexpr (DV == 128) glds16(vsrc + (size_t)64 * NR + (size_t)(t) * 64, (unsigned)__builtin_amdgcn_readfirstlane(vdst + (sl) * VSLOT + 8192)); } while (0)
; #define ATT_KLOAD(sl) do { _Pragma("unroll") for (int kb_ = 0; kb_ < NKW; ++kb_) _Pragma("unroll") for (int ds_ = 0; ds_ < NDS; ++ds_) { \
;         if (ds_ < 2) kf[kb_ * NDS + ds_] = *(const LAS bf16x8*)(kp[ds_ & 1] + (sl) * KSLOT + (kb_ & 1) * 512 + (kb_ >> 1) * 4096); \
;         else kf[kb_ * NDS + ds_] = *(const LAS bf16x8*)(krp + (sl) * KSLOT + (kb_ & 1) * 256 + (kb_ >> 1) * 2048); } } while (0)
; #define ATT_QK() do { _Pragma("unroll") for (int kb_ = 0; kb_ < NKW; ++kb_) _Pragma("unroll") for (int ds_ = 0; ds_ < NDS; ++ds_) _Pragma("unroll") for (int qb_ = 0; qb_ < NQB; ++qb_) \
;         c[kb_][qb_] = __builtin_amdgcn_mfma_f32_16x16x32_bf16(kf[kb_ * NDS + ds_], qf[qb_ * NDS + ds_], ds_ == 0 ? zero4 : c[kb_][qb_], 0, 0, 0); } while (0)
; #define ATT_EXP() do { _Pragma("unroll") for (int kb_ = 0; kb_ < NKW; ++kb_) _Pragma("unroll") for (int qb_ = 0; qb_ < NQB; ++qb_) _Pragma("unroll") for (int i_ = 0; i_ < 4; ++i_) \
;         c[kb_][qb_][i_] = __builtin_amdgcn_exp2f(c[kb_][qb_][i_]); } while (0)
; template <int DQK, int DV, bool LEAD> ...
;     ...
;     ATT_DMA_K(3, 0); ATT_DMA_V(1, 1);
;     ATT_QK(); ATT_SB();
;     ATT_KLOAD(1); ATT_SB();
;     if constexpr (LEAD) { ATT_EXP(); ATT_SUMPACK(); }
;     wait_bar<NDMA>();
;     int s_prev = 0, s_cur = 1, s_next = 2;
;     int one_ = 1; asm volatile("" : "+s"(one_));
	v_mfma_f32_16x16x32_bf16 v[24:27], v[24:27], v[10:13], 0
	s_mov_b32 s4, m0
	s_mov_b32 m0, s25
	s_nop 0
	global_load_lds_dwordx4 v[168:169], off
	s_mov_b32 m0, s4
	s_add_i32 s4, s29, 0x4000
	s_mov_b32 s5, m0
	s_mov_b32 m0, s4
	s_nop 0
	global_load_lds_dwordx4 v[22:23], off
	s_mov_b32 m0, s5
	s_waitcnt lgkmcnt(1)
	v_mfma_f32_16x16x32_bf16 v[74:77], v[50:53], v[14:17], v[24:27]
	s_mov_b64 s[4:5], 0x840080
	v_add_u32_e32 v176, v28, v64
	v_lshl_add_u64 v[28:29], v[162:163], 0, s[4:5]
	v_mfma_f32_16x16x32_bf16 v[24:27], v[38:41], v[6:9], 0
	s_add_i32 s4, s29, 0x6000
	s_mov_b32 s5, m0
	s_mov_b32 m0, s4
	s_nop 0
	global_load_lds_dwordx4 v[28:29], off
	s_mov_b32 m0, s5
	v_mfma_f32_16x16x32_bf16 v[34:37], v[38:41], v[10:13], 0
	v_mfma_f32_16x16x32_bf16 v[70:73], v[50:53], v[2:5], v[46:49]
	s_waitcnt lgkmcnt(0)
	v_mfma_f32_16x16x32_bf16 v[22:25], v[54:57], v[2:5], v[24:27]
	v_mfma_f32_16x16x32_bf16 v[78:81], v[54:57], v[14:17], v[34:37]
	s_nop 1
	ds_read_b128 v[26:29], v175 offset:8192
	s_nop 0
	ds_read_b128 v[34:37], v175 offset:8704
	ds_read_b128 v[38:41], v178 offset:8192
	ds_read_b128 v[46:49], v178 offset:8704
	ds_read_b128 v[50:53], v175 offset:12288
	ds_read_b128 v[54:57], v175 offset:12800
	ds_read_b128 v[62:65], v178 offset:12288
	ds_read_b128 v[66:69], v178 offset:12800
	v_exp_f32_e32 v42, v42
	v_exp_f32_e32 v43, v43
	v_exp_f32_e32 v44, v44
	v_exp_f32_e32 v45, v45
	v_exp_f32_e32 v86, v18
	v_exp_f32_e32 v87, v19
	v_exp_f32_e32 v20, v20
	v_exp_f32_e32 v21, v21
	v_exp_f32_e32 v30, v30
	v_exp_f32_e32 v58, v58
	v_add_f32_e32 v18, v42, v43
	v_add_f32_e32 v19, v44, v45
	v_exp_f32_e32 v31, v31
	v_exp_f32_e32 v59, v59
	v_add_f32_e32 v18, v18, v19
	v_add_f32_e32 v19, v86, v87
	v_add_f32_e32 v82, v20, v21
	v_add_f32_e32 v19, v19, v82
	v_exp_f32_e32 v32, v32
	v_exp_f32_e32 v60, v60
	v_add_f32_e32 v18, v18, v30
	v_add_f32_e32 v19, v19, v58
	v_exp_f32_e32 v33, v33
	v_exp_f32_e32 v61, v61
	v_add_f32_e32 v18, v31, v18
	v_add_f32_e32 v19, v59, v19
	v_exp_f32_e32 v70, v70
	v_exp_f32_e32 v74, v74
	v_add_f32_e32 v18, v32, v18
	v_add_f32_e32 v19, v60, v19
	v_exp_f32_e32 v71, v71
	v_exp_f32_e32 v75, v75
	v_add_f32_e32 v18, v33, v18
	v_add_f32_e32 v19, v61, v19
	v_exp_f32_e32 v72, v72
	v_exp_f32_e32 v76, v76
	v_add_f32_e32 v18, v70, v18
	v_add_f32_e32 v19, v74, v19
	v_exp_f32_e32 v73, v73
	v_exp_f32_e32 v77, v77
	v_add_f32_e32 v18, v71, v18
	v_add_f32_e32 v19, v75, v19
	v_exp_f32_e32 v22, v22
	v_exp_f32_e32 v78, v78
	v_add_f32_e32 v18, v72, v18
	v_add_f32_e32 v19, v76, v19
	v_exp_f32_e32 v23, v23
	v_exp_f32_e32 v79, v79
	v_add_f32_e32 v18, v73, v18
	v_add_f32_e32 v19, v77, v19
	v_exp_f32_e32 v24, v24
	v_exp_f32_e32 v80, v80
	v_add_f32_e32 v18, v22, v18
	v_add_f32_e32 v19, v78, v19
	v_exp_f32_e32 v25, v25
	v_exp_f32_e32 v81, v81
	v_add_f32_e32 v18, v23, v18
	v_add_f32_e32 v19, v79, v19
	s_mov_b32 s4, 1
	v_add_f32_e32 v18, v24, v18
	v_add_f32_e32 v82, v80, v19
	v_cvt_pk_bf16_f32 v83, v44, v45
	v_add_f32_e32 v19, v25, v18
	v_add_f32_e32 v18, v81, v82
	s_waitcnt vmcnt(3) lgkmcnt(0)
	s_barrier
	s_cmp_lg_u32 s4, 0
	v_pk_add_f32 v[166:167], v[18:19], 0 op_sel_hi:[1,0]
	v_mov_b32_e32 v18, 0
	v_cvt_pk_bf16_f32 v82, v42, v43
	v_cvt_pk_bf16_f32 v84, v30, v31
	v_cvt_pk_bf16_f32 v85, v32, v33
	v_cvt_pk_bf16_f32 v90, v86, v87
	v_cvt_pk_bf16_f32 v91, v20, v21
	v_cvt_pk_bf16_f32 v92, v58, v59
	v_cvt_pk_bf16_f32 v93, v60, v61
	v_cvt_pk_bf16_f32 v98, v70, v71
	v_cvt_pk_bf16_f32 v99, v72, v73
	v_cvt_pk_bf16_f32 v100, v22, v23
	v_cvt_pk_bf16_f32 v101, v24, v25
	v_cvt_pk_bf16_f32 v102, v74, v75
	v_cvt_pk_bf16_f32 v103, v76, v77
	v_cvt_pk_bf16_f32 v104, v78, v79
	v_cvt_pk_bf16_f32 v105, v80, v81
	s_cselect_b64 s[4:5], -1, 0
	s_mov_b32 s27, 2
	v_mov_b32_e32 v19, v18
	v_mov_b32_e32 v20, v18
	v_mov_b32_e32 v21, v18
	v_mov_b32_e32 v22, v18
	v_mov_b32_e32 v23, v18
	v_mov_b32_e32 v24, v18
	v_mov_b32_e32 v25, v18
	v_mov_b32_e32 v30, v18
	v_mov_b32_e32 v31, v18
	v_mov_b32_e32 v32, v18
	v_mov_b32_e32 v33, v18
	v_mov_b32_e32 v42, v18
	v_mov_b32_e32 v43, v18
	v_mov_b32_e32 v44, v18
	v_mov_b32_e32 v45, v18
	v_mov_b32_e32 v58, v18
	v_mov_b32_e32 v59, v18
	v_mov_b32_e32 v60, v18
	v_mov_b32_e32 v61, v18
	v_mov_b32_e32 v70, v18
	v_mov_b32_e32 v71, v18
	v_mov_b32_e32 v72, v18
	v_mov_b32_e32 v73, v18
	v_mov_b32_e32 v74, v18
	v_mov_b32_e32 v75, v18
	v_mov_b32_e32 v76, v18
	v_mov_b32_e32 v77, v18
	v_mov_b32_e32 v78, v18
	v_mov_b32_e32 v79, v18
	v_mov_b32_e32 v80, v18
	v_mov_b32_e32 v81, v18
	v_mov_b32_e32 v86, v18
	v_mov_b32_e32 v87, v18
	v_mov_b32_e32 v88, v18
	v_mov_b32_e32 v89, v18
	v_mov_b32_e32 v94, v18
	v_mov_b32_e32 v95, v18
	v_mov_b32_e32 v96, v18
	v_mov_b32_e32 v97, v18
	v_mov_b32_e32 v106, v18
	v_mov_b32_e32 v107, v18
	v_mov_b32_e32 v108, v18
	v_mov_b32_e32 v109, v18
	v_mov_b32_e32 v110, v18
	v_mov_b32_e32 v111, v18
	v_mov_b32_e32 v112, v18
	v_mov_b32_e32 v113, v18
	v_mov_b32_e32 v114, v18
	v_mov_b32_e32 v115, v18
	v_mov_b32_e32 v116, v18
	v_mov_b32_e32 v117, v18
	v_mov_b32_e32 v118, v18
	v_mov_b32_e32 v119, v18
	v_mov_b32_e32 v120, v18
	v_mov_b32_e32 v121, v18
	v_mov_b32_e32 v122, v18
	v_mov_b32_e32 v123, v18
	v_mov_b32_e32 v124, v18
	v_mov_b32_e32 v125, v18
	v_mov_b32_e32 v126, v18
	v_mov_b32_e32 v127, v18
	v_mov_b32_e32 v128, v18
	v_mov_b32_e32 v129, v18
	s_branch .LBB0_981

; #define a launder(kargs)
; template <int DQK, int DV, bool LEAD> ...
;     ...
;     const int kr0 = 8 * (q16 >> 2) + (q16 & 3);
;     const int fk = ((kr0 >> 1) & 1) | (((kr0 >> 3) & 1) << 1) | (((kr0 >> 4) & 1) << 2);
;     const LAS unsigned char* kp[2]; const LAS unsigned char* vp[2];
; #pragma unroll
;     for (int ds = 0; ds < 2; ++ds) kp[ds] = shm + KOFF + kr0 * 128 + ((((ds << 2) | g4) ^ fk) << 4) + kg * 4096;
;     const LAS unsigned char* krp = shm + KOFF + 8192 + kr0 * 64 + ((g4 ^ (((kr0 >> 4) & 1) << 1)) << 4) + kg * 2048;
; #pragma unroll
;     for (int s_ = 0; s_ < 2; ++s_) vp[s_] = shm + VOFF + q16 * 128 + ((((s_ << 2) | g4) ^ ((q16 >> 1) & 7)) << 4);
;     const LAS unsigned char* vpk = kg ? vp[1] : vp[0];
;     ...
;     ATT_DMA_K(0, 0); ATT_DMA_V(0, 0); ATT_DMA_K(1, 1); ATT_DMA_K(2, 2);
;     bf16x8 qf[NQB * NDS];
;     {
;       const float c2 = (DQK == 64) ? C2_EVEN : C2_ODD; const bool lat = tq0 >= 0;
; #pragma unroll
;       for (int qb = 0; qb < NQB; ++qb) {
;           const bf16_t* qp = Q + (size_t)(qrow0 + qoff + qb * 16 + q16) * qpitch + g4 * 8;
;           bf16x8 raw[NDS];
; #pragma unroll
;           for (int ds = 0; ds < NDS; ++ds) raw[ds] = *(const bf16x8*)(qp + ds * 32);
;           float x[NDS][8];
; #pragma unroll
;           for (int ds = 0; ds < NDS; ++ds)
; #pragma unroll
;               for (int j = 0; j < 8; ++j) x[ds][j] = __uint_as_float(((unsigned)(unsigned short)raw[ds][j]) << 16);
;           const int tq = tq0 + qoff + qb * 16 + q16, prow = (tq >> 6) & 127, pcol = tq & 63;
;           float sn = 0.f;
; #pragma unroll
;           for (int ds = 0; ds < 2; ++ds)
; #pragma unroll
;               for (int j = 0; j < 8; ++j) sn += x[ds][j] * x[ds][j];
;           sn = lanes4_sum(sn);
;           const float rn = rsqrtf(sn * (1.f / 64.f) + EPS);
; #pragma unroll
;           for (int ds = 0; ds < 2; ++ds)
; #pragma unroll
; __global__ void __launch_bounds__(NWAVES * 64, 2) mega_fwd(Args args_) {
;     ...
;                 for (int u = F.vcu - 64; u < 64; u += F.G) { if (u < 0) continue; const int b = u >> 3, kvh = (u >> 2) & 1, g = u & 3;
;                     att::attn_unit<64, 64>(QK + 1024 + kvh * 256 + g * 64, QKW, QK + 1536 + kvh * 64, QKW, nullptr, VTE + (size_t)(512 + kvh * 64) * NR, H + 512 + kvh * 256 + g * 64, 1024, b * TPS + SEQ, b * TPS + SEQ, 4, F.lds, IN(a, I_BQK) + j * 128, (const f32x2*)(ws + WS_ROPE64), -100000); }
.LBB0_987:
	s_cmp_lt_i32 s3, 0
	s_cbranch_scc1 .LBB0_986
	s_bfe_u32 s30, s3, 0x10002
	s_lshr_b32 s6, s3, 3
	s_lshl_b32 s4, s30, 9
	s_add_u32 s4, s14, s4
	s_addc_u32 s5, s15, 0
	s_lshl_b32 s7, s3, 6
	s_and_b32 s7, s7, 0xc0
	s_lshl_b32 s29, s7, 1
	s_add_u32 s12, s4, s29
	s_addc_u32 s13, s5, 0
	s_lshl_b32 s4, s30, 7
	s_add_u32 s22, s17, s4
	s_addc_u32 s23, s24, 0
	s_mul_i32 s4, s30, 0x840000
	s_add_u32 s4, s10, s4
	s_addc_u32 s7, s11, 0
	s_add_u32 s26, s4, 0x4200000
	s_mov_b64 s[4:5], s[0:1]
	s_load_dwordx2 s[4:5], s[4:5], 0x60
	s_mulk_i32 s6, 0x2100
	s_addc_u32 s27, s7, 0
	s_add_i32 s18, s6, 0x2000
	s_lshl_b64 s[6:7], s[20:21], 2
	s_waitcnt lgkmcnt(0)
	s_add_u32 s8, s4, s6
	s_addc_u32 s9, s5, s7
	v_readfirstlane_b32 s4, v0
	s_cmpk_gt_u32 s4, 0xff
	s_mov_b64 s[4:5], -1
	s_cbranch_scc0 .LBB0_995
	v_mov_b32_e32 v83, v0
	s_mov_b32 s19, s39
	v_readfirstlane_b32 s6, v83
	s_ashr_i32 s4, s6, 6
	v_bfe_u32 v1, v83, 3, 3
	v_lshl_or_b32 v1, s4, 3, v1
	s_lshl_b32 s5, s4, 1
	s_lshr_b32 s7, s6, 5
	v_ashrrev_i32_e32 v3, 1, v1
	s_and_b32 s5, s5, 2
	s_and_b32 s7, s7, 4
	v_and_b32_e32 v2, 7, v83
	v_and_b32_e32 v4, 1, v3
	s_or_b32 s5, s5, s7
	v_bitop3_b32 v6, s5, v2, v4 bitop3:0x36
	v_xor_b32_e32 v7, v3, v83
	v_add_u32_e32 v4, s18, v1
	v_mov_b64_e32 v[2:3], s[22:23]
	s_and_b32 s31, s4, 3
	s_lshl_b32 s36, s4, 10
	v_mad_i64_i32 v[2:3], s[4:5], v4, s92, v[2:3]
	v_mov_b64_e32 v[4:5], s[26:27]
	v_mad_i64_i32 v[4:5], s[4:5], v1, s91, v[4:5]
	v_lshlrev_b32_e32 v194, 4, v6
	v_lshlrev_b32_e32 v1, 4, v7
	s_add_i32 s36, s36, 0
	v_lshl_add_u64 v[4:5], s[18:19], 1, v[4:5]
	v_lshl_add_u64 v[42:43], v[2:3], 0, v[194:195]
	v_and_b32_e32 v194, 0x70, v1
	s_mov_b32 s4, m0
	s_mov_b32 m0, s36
	s_nop 0
	global_load_lds_dwordx4 v[42:43], off
	s_mov_b32 m0, s4
	v_lshl_add_u64 v[162:163], v[4:5], 0, v[194:195]
	s_add_i32 s19, s36, 0x9000
	s_mov_b32 s4, m0
	s_mov_b32 m0, s19
	s_nop 0
	global_load_lds_dwordx4 v[162:163], off
	s_mov_b32 m0, s4
	v_and_b32_e32 v82, 15, v83
	s_mov_b64 s[4:5], 0x38000
	v_lshl_add_u64 v[2:3], v[42:43], 0, s[4:5]
	s_add_i32 s4, s36, 0x2000
	s_mov_b32 s5, m0
	s_mov_b32 m0, s4
	s_nop 0
	global_load_lds_dwordx4 v[2:3], off
	s_mov_b32 m0, s5
	v_lshl_or_b32 v1, s31, 6, v82
	s_mov_b64 s[4:5], 0x70000
	v_or_b32_e32 v1, s18, v1
	v_and_b32_e32 v194, 48, v83
	v_lshl_add_u64 v[2:3], v[42:43], 0, s[4:5]
	s_add_i32 s4, s36, 0x4000
	v_lshl_add_u64 v[10:11], s[12:13], 0, v[194:195]
	v_or_b32_e32 v16, 32, v1
	s_mov_b32 s5, m0
	s_mov_b32 m0, s4
	s_nop 0
	global_load_lds_dwordx4 v[2:3], off
	s_mov_b32 m0, s5
	v_or_b32_e32 v6, 16, v1
	v_mad_u64_u32 v[16:17], s[4:5], v16, s92, v[10:11]
	global_load_dwordx4 v[34:37], v[16:17], off offset:64 nt
	v_mad_u64_u32 v[12:13], s[4:5], v1, s92, v[10:11]
	v_or_b32_e32 v1, 48, v1
	global_load_dwordx4 v[2:5], v[12:13], off offset:64 nt
	v_mad_u64_u32 v[14:15], s[4:5], v6, s92, v[10:11]
	v_mad_u64_u32 v[10:11], s[4:5], v1, s92, v[10:11]
	global_load_dwordx4 v[6:9], v[14:15], off offset:64 nt
	global_load_dwordx4 v[38:41], v[10:11], off offset:64 nt
	global_load_dwordx4 v[64:67], v[12:13], off nt
	global_load_dwordx4 v[86:89], v[14:15], off nt
	global_load_dwordx4 v[18:21], v[16:17], off nt
	s_nop 0
	global_load_dwordx4 v[14:17], v[10:11], off nt
	v_bfe_u32 v85, v83, 4, 2
	s_waitcnt vmcnt(8)
	v_lshlrev_b32_e32 v52, 5, v85
	global_load_dwordx4 v[22:25], v52, s[8:9] offset:144
	global_load_dwordx4 v[26:29], v52, s[8:9] offset:128
	s_lshl_b32 s4, s6, 4
	v_lshlrev_b32_e32 v10, 1, v83
	v_and_b32_e32 v11, 3, v83
	v_lshrrev_b32_e32 v12, 1, v83
	s_and_b32 s4, s4, 0xfffff000
	v_and_or_b32 v10, v10, 24, v11
	v_bitop3_b32 v11, v85, v12, 7 bitop3:0x78
	s_add_i32 s4, s4, 0
	v_lshlrev_b32_e32 v84, 4, v11
	v_lshl_add_u32 v90, v10, 7, s4
	s_mov_b32 s4, 0x358637bd
	s_mov_b32 s16, 0x3c800000
	v_and_b32_e32 v1, 63, v83
	v_add_u32_e32 v174, v90, v84
	s_cmpk_lt_u32 s6, 0x100
	v_lshl_add_u64 v[168:169], v[42:43], 0, s[96:97]
	s_mov_b32 s37, 2
	s_waitcnt vmcnt(9)
	v_and_b32_e32 v31, 0xffff0000, v37
	v_lshlrev_b32_e32 v30, 16, v37
	v_and_b32_e32 v33, 0xffff0000, v36
	v_lshlrev_b32_e32 v32, 16, v36
	v_and_b32_e32 v57, 0xffff0000, v35
	v_lshlrev_b32_e32 v56, 16, v35
	s_waitcnt vmcnt(6)
	v_and_b32_e32 v45, 0xffff0000, v41
	v_lshlrev_b32_e32 v44, 16, v41
	v_and_b32_e32 v47, 0xffff0000, v40
	v_lshlrev_b32_e32 v46, 16, v40
	v_and_b32_e32 v49, 0xffff0000, v39
	v_lshlrev_b32_e32 v48, 16, v39
	v_and_b32_e32 v59, 0xffff0000, v34
	v_lshlrev_b32_e32 v58, 16, v34
	v_and_b32_e32 v51, 0xffff0000, v38
	v_lshlrev_b32_e32 v50, 16, v38
	global_load_dwordx4 v[34:37], v52, s[8:9] offset:16
	global_load_dwordx4 v[38:41], v52, s[8:9]
	s_waitcnt vmcnt(6)
	v_and_b32_e32 v75, 0xffff0000, v89
	v_lshlrev_b32_e32 v74, 16, v89
	v_and_b32_e32 v89, 0xffff0000, v64
	v_and_b32_e32 v95, 0xffff0000, v2
	v_lshlrev_b32_e32 v94, 16, v2
	v_and_b32_e32 v77, 0xffff0000, v88
	v_lshlrev_b32_e32 v76, 16, v88
	v_lshlrev_b32_e32 v88, 16, v64
	v_mul_f32_e32 v2, v89, v89
	v_and_b32_e32 v11, 0xffff0000, v9
	v_lshlrev_b32_e32 v10, 16, v9
	v_and_b32_e32 v69, 0xffff0000, v8
	v_lshlrev_b32_e32 v68, 16, v8
	v_and_b32_e32 v9, 0xffff0000, v3
	v_lshlrev_b32_e32 v8, 16, v3
	s_waitcnt vmcnt(4)
; template <int DQK, int DV, bool LEAD> ...
;     ...
;           float sn = 0.f;
; #pragma unroll
;           for (int ds = 0; ds < 2; ++ds)
; #pragma unroll
;               for (int j = 0; j < 8; ++j) sn += x[ds][j] * x[ds][j];
;           sn = lanes4_sum(sn);
;           const float rn = rsqrtf(sn * (1.f / 64.f) + EPS);
; #pragma unroll
;           for (int ds = 0; ds < 2; ++ds)
; #pragma unroll
;               for (int j = 0; j < 8; ++j) x[ds][j] *= rn * qgain[32 * ds + 8 * g4 + j];
;           if constexpr (DQK == 64) {
; #pragma unroll
;               for (int ds = 0; ds < 2; ++ds)
; #pragma unroll
;                   for (int j = 0; j < 8; ++j) {
;                       auto rr = __builtin_amdgcn_permlane32_swap(__float_as_uint(x[ds][j]), __float_as_uint(x[ds][j]), false, false);
;                       const float other = hi ? __uint_as_float(rr[0]) : __uint_as_float(rr[1]);
;                       float cc = 1.f, sg = 0.f;
;                       if (lat) { const f32x2 cs = rope[(ds ? pcol : prow) * 16 + 8 * (g4 & 1) + j]; cc = cs.x; sg = hi ? cs.y : -cs.y; }
;                       x[ds][j] = x[ds][j] * cc + other * sg; }
;           } else {
;               float sr = 0.f;
; #pragma unroll
;               for (int j = 0; j < 8; ++j) sr += x[2][j] * x[2][j];
;               sr = lanes4_sum(sr);
;               const float rq = rsqrtf(sr * (1.f / 32.f) + EPS);
; #pragma unroll
;               for (int j = 0; j < 8; ++j) { const float av = x[2][j] * rq * qgain[64 + 8 * g4 + j];
;                   auto rr = __builtin_amdgcn_permlane16_swap(__float_as_uint(av), __float_as_uint(av), false, false);
;                   const float other = (g4 & 1) ? __uint_as_float(rr[0]) : __uint_as_float(rr[1]);
;                   float cc = 1.f, sg = 0.f;
;                   if (lat) { const f32x2 cs = rope[((g4 & 2) ? pcol : prow) * 8 + j]; cc = cs.x; sg = (g4 & 1) ? cs.y : -cs.y; }
;                   x[2][j] = av * cc + other * sg; }
;           }
; #pragma unroll
;           for (int ds = 0; ds < NDS; ++ds) { u32x4 w;
; #pragma unroll
;               for (int i = 0; i < 4; ++i) w[i] = cvtpk(x[ds][2 * i] * c2, x[ds][2 * i + 1] * c2);
;               qf[qb * NDS + ds] = __builtin_bit_cast(bf16x8, w); }
	v_and_b32_e32 v53, 0xffff0000, v17
	v_lshlrev_b32_e32 v52, 16, v17
	v_and_b32_e32 v55, 0xffff0000, v16
	v_lshlrev_b32_e32 v54, 16, v16
	v_and_b32_e32 v17, 0xffff0000, v65
	v_lshlrev_b32_e32 v16, 16, v65
	v_pk_fma_f32 v[2:3], v[88:89], v[88:89], v[2:3] op_sel_hi:[1,1,0]
	v_and_b32_e32 v93, 0xffff0000, v4
	v_lshlrev_b32_e32 v92, 16, v4
	v_pk_fma_f32 v[2:3], v[16:17], v[16:17], v[2:3]
	v_mul_f32_e32 v4, v17, v17
	v_and_b32_e32 v97, 0xffff0000, v66
	v_lshlrev_b32_e32 v96, 16, v66
	v_pk_add_f32 v[2:3], v[4:5], v[2:3] op_sel_hi:[0,1]
	v_pk_fma_f32 v[2:3], v[96:97], v[96:97], v[2:3]
	v_mul_f32_e32 v4, v97, v97
	v_and_b32_e32 v71, 0xffff0000, v7
	v_lshlrev_b32_e32 v70, 16, v7
	v_and_b32_e32 v73, 0xffff0000, v6
	v_lshlrev_b32_e32 v72, 16, v6
	v_and_b32_e32 v7, 0xffff0000, v67
	v_lshlrev_b32_e32 v6, 16, v67
	v_pk_add_f32 v[2:3], v[4:5], v[2:3] op_sel_hi:[0,1]
	v_pk_fma_f32 v[2:3], v[6:7], v[6:7], v[2:3]
	v_mul_f32_e32 v4, v7, v7
	v_pk_add_f32 v[2:3], v[4:5], v[2:3] op_sel_hi:[0,1]
	v_pk_fma_f32 v[2:3], v[94:95], v[94:95], v[2:3]
	v_mul_f32_e32 v4, v95, v95
	v_pk_add_f32 v[2:3], v[4:5], v[2:3] op_sel_hi:[0,1]
	v_pk_fma_f32 v[2:3], v[8:9], v[8:9], v[2:3]
	v_mul_f32_e32 v4, v9, v9
	v_pk_add_f32 v[2:3], v[4:5], v[2:3] op_sel_hi:[0,1]
	v_pk_fma_f32 v[2:3], v[92:93], v[92:93], v[2:3]
	v_mul_f32_e32 v4, v93, v93
	v_and_b32_e32 v13, 0xffff0000, v5
	v_lshlrev_b32_e32 v12, 16, v5
	v_pk_add_f32 v[2:3], v[4:5], v[2:3] op_sel_hi:[0,1]
	v_pk_fma_f32 v[2:3], v[12:13], v[12:13], v[2:3]
	v_mul_f32_e32 v4, v13, v13
	v_pk_add_f32 v[2:3], v[4:5], v[2:3] op_sel_hi:[0,1]
	v_mov_b32_e32 v3, v2
	s_nop 1
	v_permlane16_swap_b32_e32 v2, v3
	v_add_f32_e32 v3, v2, v3
	v_mov_b32_e32 v5, v3
	v_and_b32_e32 v81, 0xffff0000, v86
	s_nop 0
	v_permlane32_swap_b32_e32 v3, v5
	v_lshlrev_b32_e32 v80, 16, v86
	v_mul_f32_e32 v2, v81, v81
	v_and_b32_e32 v61, 0xffff0000, v21
	v_lshlrev_b32_e32 v60, 16, v21
	v_and_b32_e32 v63, 0xffff0000, v20
	v_lshlrev_b32_e32 v62, 16, v20
	v_and_b32_e32 v79, 0xffff0000, v87
	v_lshlrev_b32_e32 v78, 16, v87
	v_pk_fma_f32 v[20:21], v[80:81], v[80:81], v[2:3] op_sel_hi:[1,1,0]
	v_mul_f32_e32 v2, v79, v79
	v_pk_fma_f32 v[20:21], v[78:79], v[78:79], v[20:21]
	v_and_b32_e32 v67, 0xffff0000, v15
	v_pk_add_f32 v[20:21], v[2:3], v[20:21] op_sel_hi:[0,1]
	v_pk_fma_f32 v[20:21], v[76:77], v[76:77], v[20:21]
	v_mul_f32_e32 v2, v77, v77
	v_pk_add_f32 v[20:21], v[2:3], v[20:21] op_sel_hi:[0,1]
	v_pk_fma_f32 v[20:21], v[74:75], v[74:75], v[20:21]
	v_mul_f32_e32 v2, v75, v75
	v_pk_add_f32 v[20:21], v[2:3], v[20:21] op_sel_hi:[0,1]
	v_pk_fma_f32 v[20:21], v[72:73], v[72:73], v[20:21]
	v_mul_f32_e32 v2, v73, v73
	v_pk_add_f32 v[20:21], v[2:3], v[20:21] op_sel_hi:[0,1]
	v_pk_fma_f32 v[20:21], v[70:71], v[70:71], v[20:21]
	v_mul_f32_e32 v2, v71, v71
	v_pk_add_f32 v[20:21], v[2:3], v[20:21] op_sel_hi:[0,1]
	v_pk_fma_f32 v[20:21], v[68:69], v[68:69], v[20:21]
	v_mul_f32_e32 v2, v69, v69
	v_pk_add_f32 v[20:21], v[2:3], v[20:21] op_sel_hi:[0,1]
	v_pk_fma_f32 v[20:21], v[10:11], v[10:11], v[20:21]
	v_mul_f32_e32 v2, v11, v11
	v_pk_add_f32 v[20:21], v[2:3], v[20:21] op_sel_hi:[0,1]
	v_mov_b32_e32 v2, v20
	s_nop 1
	v_permlane16_swap_b32_e32 v20, v2
	v_add_f32_e32 v2, v20, v2
	v_mov_b32_e32 v4, v2
	s_nop 1
	v_permlane32_swap_b32_e32 v2, v4
	v_pk_add_f32 v[2:3], v[2:3], v[4:5]
	v_mov_b64_e32 v[20:21], s[4:5]
	v_pk_fma_f32 v[86:87], v[2:3], s[16:17], v[20:21] op_sel_hi:[1,0,0]
	v_lshlrev_b32_e32 v66, 16, v15
	v_mul_f32_e32 v2, 0x4b800000, v87
	v_cmp_gt_f32_e32 vcc, s95, v87
	v_cmp_gt_f32_e64 s[4:5], s95, v86
	v_and_b32_e32 v65, 0xffff0000, v19
	v_cndmask_b32_e32 v2, v87, v2, vcc
	v_rsq_f32_e32 v2, v2
	v_lshlrev_b32_e32 v64, 16, v19
	v_mul_f32_e32 v3, 0x45800000, v2
	v_cndmask_b32_e32 v98, v2, v3, vcc
	s_waitcnt vmcnt(3)
	v_pk_mul_f32 v[2:3], v[98:99], v[24:25] op_sel_hi:[0,1]
	v_pk_mul_f32 v[2:3], v[2:3], v[12:13]
	v_cmp_gt_u32_e32 vcc, 32, v1
	v_mov_b32_e32 v4, v2
	v_mov_b32_e32 v12, v2
	v_mov_b32_e32 v5, v3
	v_mov_b32_e32 v13, v3
	v_permlane32_swap_b32_e32 v4, v12
	s_nop 0
	v_permlane32_swap_b32_e32 v5, v13
	v_cndmask_b32_e32 v5, v5, v13, vcc
	v_cndmask_b32_e32 v4, v4, v12, vcc
	v_pk_fma_f32 v[2:3], v[4:5], 0, v[2:3] op_sel_hi:[1,0,1]
	s_nop 0
	v_pk_mul_f32 v[2:3], v[2:3], s[94:95] op_sel_hi:[1,0]
	s_nop 0
	v_cvt_pk_bf16_f32 v5, v2, v3
	v_pk_mul_f32 v[2:3], v[98:99], v[22:23] op_sel_hi:[0,1]
	v_pk_mul_f32 v[2:3], v[2:3], v[92:93]
	s_nop 0
	v_mov_b32_e32 v4, v2
	v_mov_b32_e32 v12, v2
	v_mov_b32_e32 v13, v3
	v_mov_b32_e32 v15, v3
	v_permlane32_swap_b32_e32 v4, v12
	s_nop 0
	v_permlane32_swap_b32_e32 v13, v15
	v_cndmask_b32_e32 v13, v13, v15, vcc
	v_cndmask_b32_e32 v12, v4, v12, vcc
	v_pk_fma_f32 v[2:3], v[12:13], 0, v[2:3] op_sel_hi:[1,0,1]
	s_nop 0
	v_pk_mul_f32 v[2:3], v[2:3], s[94:95] op_sel_hi:[1,0]
	s_nop 0
	v_cvt_pk_bf16_f32 v4, v2, v3
	s_waitcnt vmcnt(2)
	v_pk_mul_f32 v[2:3], v[98:99], v[28:29] op_sel_hi:[0,1]
	v_pk_mul_f32 v[2:3], v[2:3], v[8:9]
	s_nop 0
	v_mov_b32_e32 v8, v2
	v_mov_b32_e32 v12, v2
	v_mov_b32_e32 v9, v3
	v_mov_b32_e32 v13, v3
	v_permlane32_swap_b32_e32 v8, v12
	s_nop 0
	v_permlane32_swap_b32_e32 v9, v13
	v_cndmask_b32_e32 v9, v9, v13, vcc
	v_cndmask_b32_e32 v8, v8, v12, vcc
	v_pk_fma_f32 v[2:3], v[8:9], 0, v[2:3] op_sel_hi:[1,0,1]
	v_pk_mul_f32 v[8:9], v[26:27], v[98:99] op_sel_hi:[1,0]
	v_pk_mul_f32 v[2:3], v[2:3], s[94:95] op_sel_hi:[1,0]
	v_pk_mul_f32 v[8:9], v[8:9], v[94:95]
	v_cvt_pk_bf16_f32 v3, v2, v3
	v_mov_b32_e32 v2, v8
	v_mov_b32_e32 v12, v8
	v_mov_b32_e32 v13, v9
	v_mov_b32_e32 v15, v9
	v_permlane32_swap_b32_e32 v2, v12
	s_nop 0
	v_permlane32_swap_b32_e32 v13, v15
	v_cndmask_b32_e32 v13, v13, v15, vcc
	v_cndmask_b32_e32 v12, v2, v12, vcc
	v_pk_fma_f32 v[8:9], v[12:13], 0, v[8:9] op_sel_hi:[1,0,1]
	s_nop 0
	v_pk_mul_f32 v[8:9], v[8:9], s[94:95] op_sel_hi:[1,0]
	s_nop 0
	v_cvt_pk_bf16_f32 v2, v8, v9
	s_waitcnt vmcnt(1)
; __device__ __forceinline__ unsigned cvtpk(float lo, float hi) { f32x2 v = {lo, hi}; bf16x2_t b = __builtin_convertvector(v, bf16x2_t); return __builtin_bit_cast(unsigned, b); }
; template <int DQK, int DV, bool LEAD> ...
;     ...
; #pragma unroll
;           for (int ds = 0; ds < 2; ++ds)
; #pragma unroll
;               for (int j = 0; j < 8; ++j) x[ds][j] *= rn * qgain[32 * ds + 8 * g4 + j];
;           if constexpr (DQK == 64) {
; #pragma unroll
;               for (int ds = 0; ds < 2; ++ds)
; #pragma unroll
;                   for (int j = 0; j < 8; ++j) {
;                       auto rr = __builtin_amdgcn_permlane32_swap(__float_as_uint(x[ds][j]), __float_as_uint(x[ds][j]), false, false);
;                       const float other = hi ? __uint_as_float(rr[0]) : __uint_as_float(rr[1]);
;                       float cc = 1.f, sg = 0.f;
;                       if (lat) { const f32x2 cs = rope[(ds ? pcol : prow) * 16 + 8 * (g4 & 1) + j]; cc = cs.x; sg = hi ? cs.y : -cs.y; }
;                       x[ds][j] = x[ds][j] * cc + other * sg; }
;           } else {
;               float sr = 0.f;
; #pragma unroll
;               for (int j = 0; j < 8; ++j) sr += x[2][j] * x[2][j];
;               sr = lanes4_sum(sr);
;               const float rq = rsqrtf(sr * (1.f / 32.f) + EPS);
; #pragma unroll
;               for (int j = 0; j < 8; ++j) { const float av = x[2][j] * rq * qgain[64 + 8 * g4 + j];
;                   auto rr = __builtin_amdgcn_permlane16_swap(__float_as_uint(av), __float_as_uint(av), false, false);
;                   const float other = (g4 & 1) ? __uint_as_float(rr[0]) : __uint_as_float(rr[1]);
;                   float cc = 1.f, sg = 0.f;
;                   if (lat) { const f32x2 cs = rope[((g4 & 2) ? pcol : prow) * 8 + j]; cc = cs.x; sg = (g4 & 1) ? cs.y : -cs.y; }
;                   x[2][j] = av * cc + other * sg; }
;           }
; #pragma unroll
;           for (int ds = 0; ds < NDS; ++ds) { u32x4 w;
; #pragma unroll
;               for (int i = 0; i < 4; ++i) w[i] = cvtpk(x[ds][2 * i] * c2, x[ds][2 * i + 1] * c2);
;               qf[qb * NDS + ds] = __builtin_bit_cast(bf16x8, w); }
	v_pk_mul_f32 v[8:9], v[36:37], v[98:99] op_sel_hi:[1,0]
	s_nop 0
	v_pk_mul_f32 v[6:7], v[8:9], v[6:7]
	s_nop 0
	v_mov_b32_e32 v8, v6
	v_mov_b32_e32 v12, v6
	v_mov_b32_e32 v9, v7
	v_mov_b32_e32 v13, v7
	v_permlane32_swap_b32_e32 v8, v12
	s_nop 0
	v_permlane32_swap_b32_e32 v9, v13
	v_cndmask_b32_e32 v9, v9, v13, vcc
	v_cndmask_b32_e32 v8, v8, v12, vcc
	v_pk_fma_f32 v[6:7], v[8:9], 0, v[6:7] op_sel_hi:[1,0,1]
	s_nop 0
	v_pk_mul_f32 v[6:7], v[6:7], s[94:95] op_sel_hi:[1,0]
	s_nop 0
	v_cvt_pk_bf16_f32 v9, v6, v7
	v_pk_mul_f32 v[6:7], v[34:35], v[98:99] op_sel_hi:[1,0]
	s_nop 0
	v_pk_mul_f32 v[6:7], v[6:7], v[96:97]
	s_nop 0
	v_mov_b32_e32 v8, v6
	v_mov_b32_e32 v12, v6
	v_mov_b32_e32 v13, v7
	v_mov_b32_e32 v15, v7
	v_permlane32_swap_b32_e32 v8, v12
	s_nop 0
	v_permlane32_swap_b32_e32 v13, v15
	v_cndmask_b32_e32 v13, v13, v15, vcc
	v_cndmask_b32_e32 v12, v8, v12, vcc
	v_pk_fma_f32 v[6:7], v[12:13], 0, v[6:7] op_sel_hi:[1,0,1]
	s_nop 0
	v_pk_mul_f32 v[6:7], v[6:7], s[94:95] op_sel_hi:[1,0]
	s_nop 0
	v_cvt_pk_bf16_f32 v8, v6, v7
	s_waitcnt vmcnt(0)
	v_pk_mul_f32 v[6:7], v[40:41], v[98:99] op_sel_hi:[1,0]
	s_nop 0
	v_pk_mul_f32 v[6:7], v[6:7], v[16:17]
	s_nop 0
	v_mov_b32_e32 v12, v6
	v_mov_b32_e32 v15, v6
	v_mov_b32_e32 v13, v7
	v_mov_b32_e32 v16, v7
	v_permlane32_swap_b32_e32 v12, v15
	s_nop 0
	v_permlane32_swap_b32_e32 v13, v16
	v_cndmask_b32_e32 v13, v13, v16, vcc
	v_cndmask_b32_e32 v12, v12, v15, vcc
	v_pk_fma_f32 v[6:7], v[12:13], 0, v[6:7] op_sel_hi:[1,0,1]
	v_pk_mul_f32 v[12:13], v[38:39], v[98:99] op_sel_hi:[1,0]
	v_pk_mul_f32 v[6:7], v[6:7], s[94:95] op_sel_hi:[1,0]
	v_pk_mul_f32 v[12:13], v[12:13], v[88:89]
	v_cvt_pk_bf16_f32 v7, v6, v7
	v_mov_b32_e32 v6, v12
	v_mov_b32_e32 v15, v12
	v_mov_b32_e32 v16, v13
	v_mov_b32_e32 v17, v13
	v_permlane32_swap_b32_e32 v6, v15
	s_nop 0
	v_permlane32_swap_b32_e32 v16, v17
	v_cndmask_b32_e32 v17, v16, v17, vcc
	v_cndmask_b32_e32 v16, v6, v15, vcc
	v_mul_f32_e32 v6, 0x4b800000, v86
	v_cndmask_b32_e64 v6, v86, v6, s[4:5]
	v_rsq_f32_e32 v15, v6
	v_pk_fma_f32 v[12:13], v[16:17], 0, v[12:13] op_sel_hi:[1,0,1]
	s_nop 0
	v_pk_mul_f32 v[12:13], v[12:13], s[94:95] op_sel_hi:[1,0]
	s_nop 0
	v_cvt_pk_bf16_f32 v6, v12, v13
	v_mul_f32_e32 v12, 0x45800000, v15
	v_cndmask_b32_e64 v86, v15, v12, s[4:5]
	v_pk_mul_f32 v[12:13], v[24:25], v[86:87] op_sel_hi:[1,0]
	s_nop 0
	v_pk_mul_f32 v[10:11], v[12:13], v[10:11]
	s_nop 0
	v_mov_b32_e32 v12, v10
	v_mov_b32_e32 v15, v10
	v_mov_b32_e32 v13, v11
	v_mov_b32_e32 v16, v11
	v_permlane32_swap_b32_e32 v12, v15
	s_nop 0
	v_permlane32_swap_b32_e32 v13, v16
	v_cndmask_b32_e32 v13, v13, v16, vcc
	v_cndmask_b32_e32 v12, v12, v15, vcc
	v_pk_fma_f32 v[10:11], v[12:13], 0, v[10:11] op_sel_hi:[1,0,1]
	s_nop 0
	v_pk_mul_f32 v[10:11], v[10:11], s[94:95] op_sel_hi:[1,0]
	s_nop 0
	v_cvt_pk_bf16_f32 v13, v10, v11
	v_pk_mul_f32 v[10:11], v[22:23], v[86:87] op_sel_hi:[1,0]
	s_nop 0
	v_pk_mul_f32 v[10:11], v[10:11], v[68:69]
	s_nop 0
	v_mov_b32_e32 v12, v10
	v_mov_b32_e32 v15, v10
	v_mov_b32_e32 v16, v11
	v_mov_b32_e32 v17, v11
	v_permlane32_swap_b32_e32 v12, v15
	s_nop 0
	v_permlane32_swap_b32_e32 v16, v17
	v_cndmask_b32_e32 v17, v16, v17, vcc
	v_cndmask_b32_e32 v16, v12, v15, vcc
	v_pk_fma_f32 v[10:11], v[16:17], 0, v[10:11] op_sel_hi:[1,0,1]
	s_nop 0
	v_pk_mul_f32 v[10:11], v[10:11], s[94:95] op_sel_hi:[1,0]
	s_nop 0
	v_cvt_pk_bf16_f32 v12, v10, v11
	v_pk_mul_f32 v[10:11], v[28:29], v[86:87] op_sel_hi:[1,0]
	s_nop 0
	v_pk_mul_f32 v[10:11], v[10:11], v[70:71]
	s_nop 0
	v_mov_b32_e32 v15, v10
	v_mov_b32_e32 v16, v10
	v_mov_b32_e32 v17, v11
	v_mov_b32_e32 v19, v11
	v_permlane32_swap_b32_e32 v15, v16
	s_nop 0
	v_permlane32_swap_b32_e32 v17, v19
	v_cndmask_b32_e32 v17, v17, v19, vcc
	v_cndmask_b32_e32 v16, v15, v16, vcc
	v_pk_fma_f32 v[10:11], v[16:17], 0, v[10:11] op_sel_hi:[1,0,1]
	v_pk_mul_f32 v[16:17], v[26:27], v[86:87] op_sel_hi:[1,0]
	v_pk_mul_f32 v[10:11], v[10:11], s[94:95] op_sel_hi:[1,0]
	v_pk_mul_f32 v[16:17], v[16:17], v[72:73]
	v_cvt_pk_bf16_f32 v11, v10, v11
	v_mov_b32_e32 v10, v16
	v_mov_b32_e32 v15, v16
	v_mov_b32_e32 v19, v17
	v_mov_b32_e32 v68, v17
	v_permlane32_swap_b32_e32 v10, v15
	s_nop 0
	v_permlane32_swap_b32_e32 v19, v68
	v_cndmask_b32_e32 v69, v19, v68, vcc
	v_cndmask_b32_e32 v68, v10, v15, vcc
	v_pk_fma_f32 v[16:17], v[68:69], 0, v[16:17] op_sel_hi:[1,0,1]
	v_and_b32_e32 v73, 0xffff0000, v18
	v_pk_mul_f32 v[16:17], v[16:17], s[94:95] op_sel_hi:[1,0]
	s_nop 0
	v_cvt_pk_bf16_f32 v10, v16, v17
	v_pk_mul_f32 v[16:17], v[36:37], v[86:87] op_sel_hi:[1,0]
	s_nop 0
	v_pk_mul_f32 v[16:17], v[16:17], v[74:75]
	v_mul_f32_e32 v74, v65, v65
	v_mov_b32_e32 v15, v16
	v_mov_b32_e32 v19, v16
	v_mov_b32_e32 v68, v17
	v_mov_b32_e32 v69, v17
	v_permlane32_swap_b32_e32 v15, v19
	s_nop 0
	v_permlane32_swap_b32_e32 v68, v69
	v_cndmask_b32_e32 v69, v68, v69, vcc
	v_cndmask_b32_e32 v68, v15, v19, vcc
	v_pk_fma_f32 v[16:17], v[68:69], 0, v[16:17] op_sel_hi:[1,0,1]
	v_pk_mul_f32 v[68:69], v[34:35], v[86:87] op_sel_hi:[1,0]
	v_pk_mul_f32 v[16:17], v[16:17], s[94:95] op_sel_hi:[1,0]
	v_pk_mul_f32 v[68:69], v[68:69], v[76:77]
	v_cvt_pk_bf16_f32 v17, v16, v17
	v_mov_b32_e32 v15, v68
	v_mov_b32_e32 v16, v68
	v_mov_b32_e32 v19, v69
	v_mov_b32_e32 v70, v69
	v_permlane32_swap_b32_e32 v15, v16
	s_nop 0
	v_permlane32_swap_b32_e32 v19, v70
	v_cndmask_b32_e32 v71, v19, v70, vcc
	v_cndmask_b32_e32 v70, v15, v16, vcc
	v_pk_fma_f32 v[68:69], v[70:71], 0, v[68:69] op_sel_hi:[1,0,1]
	v_and_b32_e32 v77, 0xffff0000, v14
	v_pk_mul_f32 v[68:69], v[68:69], s[94:95] op_sel_hi:[1,0]
	v_lshlrev_b32_e32 v76, 16, v14
	v_cvt_pk_bf16_f32 v16, v68, v69
	v_pk_mul_f32 v[68:69], v[40:41], v[86:87] op_sel_hi:[1,0]
; template <int DQK, int DV, bool LEAD> ...
;     ...
;           float sn = 0.f;
; #pragma unroll
;           for (int ds = 0; ds < 2; ++ds)
; #pragma unroll
;               for (int j = 0; j < 8; ++j) sn += x[ds][j] * x[ds][j];
;           sn = lanes4_sum(sn);
;           const float rn = rsqrtf(sn * (1.f / 64.f) + EPS);
; #pragma unroll
;           for (int ds = 0; ds < 2; ++ds)
; #pragma unroll
;               for (int j = 0; j < 8; ++j) x[ds][j] *= rn * qgain[32 * ds + 8 * g4 + j];
;           if constexpr (DQK == 64) {
; #pragma unroll
;               for (int ds = 0; ds < 2; ++ds)
; #pragma unroll
;                   for (int j = 0; j < 8; ++j) {
;                       auto rr = __builtin_amdgcn_permlane32_swap(__float_as_uint(x[ds][j]), __float_as_uint(x[ds][j]), false, false);
;                       const float other = hi ? __uint_as_float(rr[0]) : __uint_as_float(rr[1]);
;                       float cc = 1.f, sg = 0.f;
;                       if (lat) { const f32x2 cs = rope[(ds ? pcol : prow) * 16 + 8 * (g4 & 1) + j]; cc = cs.x; sg = hi ? cs.y : -cs.y; }
;                       x[ds][j] = x[ds][j] * cc + other * sg; }
;           } else {
;               float sr = 0.f;
; #pragma unroll
;               for (int j = 0; j < 8; ++j) sr += x[2][j] * x[2][j];
;               sr = lanes4_sum(sr);
;               const float rq = rsqrtf(sr * (1.f / 32.f) + EPS);
; #pragma unroll
;               for (int j = 0; j < 8; ++j) { const float av = x[2][j] * rq * qgain[64 + 8 * g4 + j];
;                   auto rr = __builtin_amdgcn_permlane16_swap(__float_as_uint(av), __float_as_uint(av), false, false);
;                   const float other = (g4 & 1) ? __uint_as_float(rr[0]) : __uint_as_float(rr[1]);
;                   float cc = 1.f, sg = 0.f;
;                   if (lat) { const f32x2 cs = rope[((g4 & 2) ? pcol : prow) * 8 + j]; cc = cs.x; sg = (g4 & 1) ? cs.y : -cs.y; }
;                   x[2][j] = av * cc + other * sg; }
;           }
; #pragma unroll
;           for (int ds = 0; ds < NDS; ++ds) { u32x4 w;
; #pragma unroll
;               for (int i = 0; i < 4; ++i) w[i] = cvtpk(x[ds][2 * i] * c2, x[ds][2 * i + 1] * c2);
;               qf[qb * NDS + ds] = __builtin_bit_cast(bf16x8, w); }
	v_mul_f32_e32 v14, v77, v77
	v_pk_mul_f32 v[68:69], v[68:69], v[78:79]
	s_nop 0
	v_mov_b32_e32 v15, v68
	v_mov_b32_e32 v19, v68
	v_mov_b32_e32 v70, v69
	v_mov_b32_e32 v71, v69
	v_permlane32_swap_b32_e32 v15, v19
	s_nop 0
	v_permlane32_swap_b32_e32 v70, v71
	v_cndmask_b32_e32 v71, v70, v71, vcc
	v_cndmask_b32_e32 v70, v15, v19, vcc
	v_pk_fma_f32 v[68:69], v[70:71], 0, v[68:69] op_sel_hi:[1,0,1]
	s_nop 0
	v_pk_mul_f32 v[68:69], v[68:69], s[94:95] op_sel_hi:[1,0]
	s_nop 0
	v_cvt_pk_bf16_f32 v15, v68, v69
	v_pk_mul_f32 v[68:69], v[38:39], v[86:87] op_sel_hi:[1,0]
	v_pk_fma_f32 v[78:79], v[76:77], v[76:77], v[14:15] op_sel_hi:[1,1,0]
	v_pk_mul_f32 v[68:69], v[68:69], v[80:81]
	v_pk_fma_f32 v[78:79], v[66:67], v[66:67], v[78:79]
	v_mov_b32_e32 v71, v69
	v_mov_b32_e32 v72, v69
	v_mov_b32_e32 v19, v68
	v_mov_b32_e32 v70, v68
	v_permlane32_swap_b32_e32 v71, v72
	s_nop 0
	v_permlane32_swap_b32_e32 v19, v70
	v_cndmask_b32_e32 v71, v71, v72, vcc
	v_lshlrev_b32_e32 v72, 16, v18
	v_mul_f32_e32 v18, v73, v73
	v_cndmask_b32_e32 v70, v19, v70, vcc
	v_pk_fma_f32 v[18:19], v[72:73], v[72:73], v[18:19] op_sel_hi:[1,1,0]
	v_mul_f32_e32 v14, v67, v67
	v_pk_fma_f32 v[18:19], v[64:65], v[64:65], v[18:19]
	v_pk_add_f32 v[78:79], v[14:15], v[78:79] op_sel_hi:[0,1]
	v_pk_add_f32 v[18:19], v[74:75], v[18:19] op_sel_hi:[0,1]
	v_pk_fma_f32 v[18:19], v[62:63], v[62:63], v[18:19]
	v_mul_f32_e32 v74, v63, v63
	v_pk_fma_f32 v[78:79], v[54:55], v[54:55], v[78:79]
	v_mul_f32_e32 v14, v55, v55
	v_pk_add_f32 v[18:19], v[74:75], v[18:19] op_sel_hi:[0,1]
	v_pk_add_f32 v[78:79], v[14:15], v[78:79] op_sel_hi:[0,1]
	v_pk_fma_f32 v[18:19], v[60:61], v[60:61], v[18:19]
	v_mul_f32_e32 v74, v61, v61
	v_pk_fma_f32 v[78:79], v[52:53], v[52:53], v[78:79]
	v_mul_f32_e32 v14, v53, v53
	v_pk_add_f32 v[18:19], v[74:75], v[18:19] op_sel_hi:[0,1]
	v_pk_add_f32 v[78:79], v[14:15], v[78:79] op_sel_hi:[0,1]
	v_pk_fma_f32 v[18:19], v[58:59], v[58:59], v[18:19]
	v_mul_f32_e32 v74, v59, v59
	v_pk_fma_f32 v[78:79], v[50:51], v[50:51], v[78:79]
	v_mul_f32_e32 v14, v51, v51
	v_pk_add_f32 v[18:19], v[74:75], v[18:19] op_sel_hi:[0,1]
	v_pk_add_f32 v[78:79], v[14:15], v[78:79] op_sel_hi:[0,1]
	v_pk_fma_f32 v[18:19], v[56:57], v[56:57], v[18:19]
	v_mul_f32_e32 v74, v57, v57
	v_pk_fma_f32 v[78:79], v[48:49], v[48:49], v[78:79]
	v_mul_f32_e32 v14, v49, v49
	v_pk_add_f32 v[18:19], v[74:75], v[18:19] op_sel_hi:[0,1]
	v_pk_add_f32 v[78:79], v[14:15], v[78:79] op_sel_hi:[0,1]
	v_pk_fma_f32 v[18:19], v[32:33], v[32:33], v[18:19]
	v_mul_f32_e32 v74, v33, v33
	v_pk_fma_f32 v[78:79], v[46:47], v[46:47], v[78:79]
	v_mul_f32_e32 v14, v47, v47
	v_pk_add_f32 v[18:19], v[74:75], v[18:19] op_sel_hi:[0,1]
	v_pk_add_f32 v[78:79], v[14:15], v[78:79] op_sel_hi:[0,1]
	v_pk_fma_f32 v[18:19], v[30:31], v[30:31], v[18:19]
	v_mul_f32_e32 v74, v31, v31
	v_pk_fma_f32 v[78:79], v[44:45], v[44:45], v[78:79]
	v_mul_f32_e32 v14, v45, v45
	v_pk_add_f32 v[18:19], v[74:75], v[18:19] op_sel_hi:[0,1]
	v_pk_add_f32 v[78:79], v[14:15], v[78:79] op_sel_hi:[0,1]
	v_mov_b32_e32 v19, v18
	v_mov_b32_e32 v14, v78
	s_nop 0
	v_permlane16_swap_b32_e32 v18, v19
	v_permlane16_swap_b32_e32 v78, v14
	v_add_f32_e32 v19, v18, v19
	v_add_f32_e32 v18, v78, v14
	v_mov_b32_e32 v75, v19
	v_mov_b32_e32 v74, v18
	s_nop 0
	v_permlane32_swap_b32_e32 v19, v75
	v_permlane32_swap_b32_e32 v18, v74
	v_pk_add_f32 v[18:19], v[18:19], v[74:75]
	s_nop 0
	v_pk_fma_f32 v[74:75], v[18:19], s[16:17], v[20:21] op_sel_hi:[1,0,0]
	v_pk_fma_f32 v[18:19], v[70:71], 0, v[68:69] op_sel_hi:[1,0,1]
	v_mul_f32_e32 v14, 0x4b800000, v75
	v_cmp_gt_f32_e64 s[4:5], s95, v75
	v_pk_mul_f32 v[18:19], v[18:19], s[94:95] op_sel_hi:[1,0]
	s_mov_b32 s16, 1
	v_cndmask_b32_e64 v14, v75, v14, s[4:5]
	v_rsq_f32_e32 v20, v14
	v_cvt_pk_bf16_f32 v14, v18, v19
	v_mul_f32_e32 v18, 0x45800000, v20
	v_cndmask_b32_e64 v68, v20, v18, s[4:5]
	v_pk_mul_f32 v[18:19], v[24:25], v[68:69] op_sel_hi:[1,0]
	v_cmp_gt_f32_e64 s[4:5], s95, v74
	v_pk_mul_f32 v[18:19], v[18:19], v[30:31]
	s_nop 0
	v_mov_b32_e32 v20, v18
	v_mov_b32_e32 v30, v18
	v_mov_b32_e32 v21, v19
	v_mov_b32_e32 v31, v19
	v_permlane32_swap_b32_e32 v20, v30
	s_nop 0
	v_permlane32_swap_b32_e32 v21, v31
	v_cndmask_b32_e32 v21, v21, v31, vcc
	v_cndmask_b32_e32 v20, v20, v30, vcc
	v_pk_fma_f32 v[18:19], v[20:21], 0, v[18:19] op_sel_hi:[1,0,1]
	s_nop 0
	v_pk_mul_f32 v[18:19], v[18:19], s[94:95] op_sel_hi:[1,0]
	s_nop 0
	v_cvt_pk_bf16_f32 v21, v18, v19
	v_pk_mul_f32 v[18:19], v[22:23], v[68:69] op_sel_hi:[1,0]
	s_nop 0
	v_pk_mul_f32 v[18:19], v[18:19], v[32:33]
	s_nop 0
	v_mov_b32_e32 v20, v18
	v_mov_b32_e32 v30, v18
	v_mov_b32_e32 v31, v19
	v_mov_b32_e32 v32, v19
	v_permlane32_swap_b32_e32 v20, v30
	s_nop 0
	v_permlane32_swap_b32_e32 v31, v32
	v_cndmask_b32_e32 v31, v31, v32, vcc
	v_cndmask_b32_e32 v30, v20, v30, vcc
	v_pk_fma_f32 v[18:19], v[30:31], 0, v[18:19] op_sel_hi:[1,0,1]
	s_nop 0
	v_pk_mul_f32 v[18:19], v[18:19], s[94:95] op_sel_hi:[1,0]
	s_nop 0
	v_cvt_pk_bf16_f32 v20, v18, v19
	v_pk_mul_f32 v[18:19], v[28:29], v[68:69] op_sel_hi:[1,0]
	s_nop 0
	v_pk_mul_f32 v[18:19], v[18:19], v[56:57]
	s_nop 0
	v_mov_b32_e32 v30, v18
	v_mov_b32_e32 v32, v18
	v_mov_b32_e32 v31, v19
	v_mov_b32_e32 v33, v19
	v_permlane32_swap_b32_e32 v30, v32
	s_nop 0
	v_permlane32_swap_b32_e32 v31, v33
	v_cndmask_b32_e32 v31, v31, v33, vcc
	v_cndmask_b32_e32 v30, v30, v32, vcc
	v_pk_fma_f32 v[18:19], v[30:31], 0, v[18:19] op_sel_hi:[1,0,1]
	v_pk_mul_f32 v[30:31], v[26:27], v[68:69] op_sel_hi:[1,0]
	v_pk_mul_f32 v[18:19], v[18:19], s[94:95] op_sel_hi:[1,0]
	v_pk_mul_f32 v[30:31], v[30:31], v[58:59]
	v_cvt_pk_bf16_f32 v19, v18, v19
	v_mov_b32_e32 v18, v30
	v_mov_b32_e32 v32, v30
; __device__ __forceinline__ unsigned cvtpk(float lo, float hi) { f32x2 v = {lo, hi}; bf16x2_t b = __builtin_convertvector(v, bf16x2_t); return __builtin_bit_cast(unsigned, b); }
; template <int DQK, int DV, bool LEAD> ...
;     ...
;           const float rn = rsqrtf(sn * (1.f / 64.f) + EPS);
; #pragma unroll
;           for (int ds = 0; ds < 2; ++ds)
; #pragma unroll
;               for (int j = 0; j < 8; ++j) x[ds][j] *= rn * qgain[32 * ds + 8 * g4 + j];
;           if constexpr (DQK == 64) {
; #pragma unroll
;               for (int ds = 0; ds < 2; ++ds)
; #pragma unroll
;                   for (int j = 0; j < 8; ++j) {
;                       auto rr = __builtin_amdgcn_permlane32_swap(__float_as_uint(x[ds][j]), __float_as_uint(x[ds][j]), false, false);
;                       const float other = hi ? __uint_as_float(rr[0]) : __uint_as_float(rr[1]);
;                       float cc = 1.f, sg = 0.f;
;                       if (lat) { const f32x2 cs = rope[(ds ? pcol : prow) * 16 + 8 * (g4 & 1) + j]; cc = cs.x; sg = hi ? cs.y : -cs.y; }
;                       x[ds][j] = x[ds][j] * cc + other * sg; }
;           } else {
;               float sr = 0.f;
; #pragma unroll
;               for (int j = 0; j < 8; ++j) sr += x[2][j] * x[2][j];
;               sr = lanes4_sum(sr);
;               const float rq = rsqrtf(sr * (1.f / 32.f) + EPS);
; #pragma unroll
;               for (int j = 0; j < 8; ++j) { const float av = x[2][j] * rq * qgain[64 + 8 * g4 + j];
;                   auto rr = __builtin_amdgcn_permlane16_swap(__float_as_uint(av), __float_as_uint(av), false, false);
;                   const float other = (g4 & 1) ? __uint_as_float(rr[0]) : __uint_as_float(rr[1]);
;                   float cc = 1.f, sg = 0.f;
;                   if (lat) { const f32x2 cs = rope[((g4 & 2) ? pcol : prow) * 8 + j]; cc = cs.x; sg = (g4 & 1) ? cs.y : -cs.y; }
;                   x[2][j] = av * cc + other * sg; }
;           }
; #pragma unroll
;           for (int ds = 0; ds < NDS; ++ds) { u32x4 w;
; #pragma unroll
;               for (int i = 0; i < 4; ++i) w[i] = cvtpk(x[ds][2 * i] * c2, x[ds][2 * i + 1] * c2);
;               qf[qb * NDS + ds] = __builtin_bit_cast(bf16x8, w); }
;       }
; #pragma unroll
;       for (int d0 = 0; d0 < NQB * NDS; ++d0) asm volatile("" : "+v"(qf[d0])); }
;     wait_bar<0>();
	v_mov_b32_e32 v33, v31
	v_mov_b32_e32 v56, v31
	v_permlane32_swap_b32_e32 v18, v32
	s_nop 0
	v_permlane32_swap_b32_e32 v33, v56
	v_cndmask_b32_e32 v33, v33, v56, vcc
	v_cndmask_b32_e32 v32, v18, v32, vcc
	v_pk_fma_f32 v[30:31], v[32:33], 0, v[30:31] op_sel_hi:[1,0,1]
	s_nop 0
	v_pk_mul_f32 v[30:31], v[30:31], s[94:95] op_sel_hi:[1,0]
	s_nop 0
	v_cvt_pk_bf16_f32 v18, v30, v31
	v_pk_mul_f32 v[30:31], v[36:37], v[68:69] op_sel_hi:[1,0]
	s_nop 0
	v_pk_mul_f32 v[30:31], v[30:31], v[60:61]
	s_nop 0
	v_mov_b32_e32 v32, v30
	v_mov_b32_e32 v56, v30
	v_mov_b32_e32 v33, v31
	v_mov_b32_e32 v57, v31
	v_permlane32_swap_b32_e32 v32, v56
	s_nop 0
	v_permlane32_swap_b32_e32 v33, v57
	v_cndmask_b32_e32 v33, v33, v57, vcc
	v_cndmask_b32_e32 v32, v32, v56, vcc
	v_pk_fma_f32 v[30:31], v[32:33], 0, v[30:31] op_sel_hi:[1,0,1]
	s_nop 0
	v_pk_mul_f32 v[30:31], v[30:31], s[94:95] op_sel_hi:[1,0]
	s_nop 0
	v_cvt_pk_bf16_f32 v33, v30, v31
	v_pk_mul_f32 v[30:31], v[34:35], v[68:69] op_sel_hi:[1,0]
	s_nop 0
	v_pk_mul_f32 v[30:31], v[30:31], v[62:63]
	s_nop 0
	v_mov_b32_e32 v32, v30
	v_mov_b32_e32 v56, v30
	v_mov_b32_e32 v57, v31
	v_mov_b32_e32 v58, v31
	v_permlane32_swap_b32_e32 v32, v56
	s_nop 0
	v_permlane32_swap_b32_e32 v57, v58
	v_cndmask_b32_e32 v57, v57, v58, vcc
	v_cndmask_b32_e32 v56, v32, v56, vcc
	v_pk_fma_f32 v[30:31], v[56:57], 0, v[30:31] op_sel_hi:[1,0,1]
	s_nop 0
	v_pk_mul_f32 v[30:31], v[30:31], s[94:95] op_sel_hi:[1,0]
	s_nop 0
	v_cvt_pk_bf16_f32 v32, v30, v31
	v_pk_mul_f32 v[30:31], v[40:41], v[68:69] op_sel_hi:[1,0]
	s_nop 0
	v_pk_mul_f32 v[30:31], v[30:31], v[64:65]
	s_nop 0
	v_mov_b32_e32 v56, v30
	v_mov_b32_e32 v58, v30
	v_mov_b32_e32 v57, v31
	v_mov_b32_e32 v59, v31
	v_permlane32_swap_b32_e32 v56, v58
	s_nop 0
	v_permlane32_swap_b32_e32 v57, v59
	v_cndmask_b32_e32 v57, v57, v59, vcc
	v_cndmask_b32_e32 v56, v56, v58, vcc
	v_pk_fma_f32 v[30:31], v[56:57], 0, v[30:31] op_sel_hi:[1,0,1]
	v_pk_mul_f32 v[56:57], v[38:39], v[68:69] op_sel_hi:[1,0]
	v_pk_mul_f32 v[30:31], v[30:31], s[94:95] op_sel_hi:[1,0]
	v_pk_mul_f32 v[56:57], v[56:57], v[72:73]
	v_cvt_pk_bf16_f32 v31, v30, v31
	v_mov_b32_e32 v30, v56
	v_mov_b32_e32 v58, v56
	s_nop 1
	v_permlane32_swap_b32_e32 v30, v58
	v_mov_b32_e32 v59, v57
	v_mov_b32_e32 v60, v57
	v_cndmask_b32_e32 v58, v30, v58, vcc
	v_mul_f32_e32 v30, 0x4b800000, v74
	v_permlane32_swap_b32_e32 v59, v60
	v_cndmask_b32_e64 v30, v74, v30, s[4:5]
	v_cndmask_b32_e32 v59, v59, v60, vcc
	v_rsq_f32_e32 v60, v30
	v_pk_fma_f32 v[56:57], v[58:59], 0, v[56:57] op_sel_hi:[1,0,1]
	s_nop 0
	v_pk_mul_f32 v[56:57], v[56:57], s[94:95] op_sel_hi:[1,0]
	s_nop 0
	v_cvt_pk_bf16_f32 v30, v56, v57
	v_mul_f32_e32 v56, 0x45800000, v60
	v_cndmask_b32_e64 v56, v60, v56, s[4:5]
	v_pk_mul_f32 v[38:39], v[38:39], v[56:57] op_sel_hi:[1,0]
	v_pk_mul_f32 v[22:23], v[22:23], v[56:57] op_sel_hi:[1,0]
	v_pk_mul_f32 v[38:39], v[38:39], v[76:77]
	v_pk_mul_f32 v[24:25], v[24:25], v[56:57] op_sel_hi:[1,0]
	v_pk_mul_f32 v[22:23], v[22:23], v[46:47]
	v_pk_mul_f32 v[24:25], v[24:25], v[44:45]
	v_mov_b32_e32 v44, v38
	v_mov_b32_e32 v46, v38
	v_mov_b32_e32 v45, v39
	v_mov_b32_e32 v47, v39
	v_pk_mul_f32 v[40:41], v[40:41], v[56:57] op_sel_hi:[1,0]
	v_permlane32_swap_b32_e32 v44, v46
	v_permlane32_swap_b32_e32 v45, v47
	v_pk_mul_f32 v[40:41], v[40:41], v[66:67]
	v_cndmask_b32_e32 v45, v45, v47, vcc
	v_cndmask_b32_e32 v44, v44, v46, vcc
	v_pk_fma_f32 v[38:39], v[44:45], 0, v[38:39] op_sel_hi:[1,0,1]
	v_mov_b32_e32 v44, v40
	v_mov_b32_e32 v46, v40
	v_mov_b32_e32 v45, v41
	v_mov_b32_e32 v47, v41
	v_pk_mul_f32 v[34:35], v[34:35], v[56:57] op_sel_hi:[1,0]
	v_permlane32_swap_b32_e32 v44, v46
	v_permlane32_swap_b32_e32 v45, v47
	v_pk_mul_f32 v[34:35], v[34:35], v[54:55]
	v_cndmask_b32_e32 v45, v45, v47, vcc
	v_cndmask_b32_e32 v44, v44, v46, vcc
	v_pk_fma_f32 v[40:41], v[44:45], 0, v[40:41] op_sel_hi:[1,0,1]
	v_mov_b32_e32 v44, v34
	v_mov_b32_e32 v46, v34
	v_mov_b32_e32 v45, v35
	v_mov_b32_e32 v47, v35
	v_pk_mul_f32 v[36:37], v[36:37], v[56:57] op_sel_hi:[1,0]
	v_permlane32_swap_b32_e32 v44, v46
	v_permlane32_swap_b32_e32 v45, v47
	v_pk_mul_f32 v[36:37], v[36:37], v[52:53]
	v_cndmask_b32_e32 v45, v45, v47, vcc
	v_cndmask_b32_e32 v44, v44, v46, vcc
	v_pk_fma_f32 v[34:35], v[44:45], 0, v[34:35] op_sel_hi:[1,0,1]
	v_mov_b32_e32 v44, v36
	v_mov_b32_e32 v46, v36
	v_mov_b32_e32 v45, v37
	v_mov_b32_e32 v47, v37
	v_pk_mul_f32 v[26:27], v[26:27], v[56:57] op_sel_hi:[1,0]
	v_permlane32_swap_b32_e32 v44, v46
	v_permlane32_swap_b32_e32 v45, v47
	v_pk_mul_f32 v[26:27], v[26:27], v[50:51]
	v_cndmask_b32_e32 v45, v45, v47, vcc
	v_cndmask_b32_e32 v44, v44, v46, vcc
	v_pk_fma_f32 v[36:37], v[44:45], 0, v[36:37] op_sel_hi:[1,0,1]
	v_mov_b32_e32 v44, v26
	v_mov_b32_e32 v46, v26
	v_mov_b32_e32 v45, v27
	v_mov_b32_e32 v47, v27
	v_pk_mul_f32 v[28:29], v[28:29], v[56:57] op_sel_hi:[1,0]
	v_permlane32_swap_b32_e32 v44, v46
	v_permlane32_swap_b32_e32 v45, v47
	v_pk_mul_f32 v[28:29], v[28:29], v[48:49]
	v_cndmask_b32_e32 v45, v45, v47, vcc
	v_cndmask_b32_e32 v44, v44, v46, vcc
	v_pk_fma_f32 v[26:27], v[44:45], 0, v[26:27] op_sel_hi:[1,0,1]
	v_mov_b32_e32 v44, v28
	v_mov_b32_e32 v46, v28
	v_mov_b32_e32 v45, v29
	v_mov_b32_e32 v47, v29
	v_permlane32_swap_b32_e32 v44, v46
	s_nop 0
	v_permlane32_swap_b32_e32 v45, v47
	v_cndmask_b32_e32 v45, v45, v47, vcc
	v_cndmask_b32_e32 v44, v44, v46, vcc
	v_pk_fma_f32 v[28:29], v[44:45], 0, v[28:29] op_sel_hi:[1,0,1]
	v_mov_b32_e32 v44, v22
	v_mov_b32_e32 v46, v22
	v_mov_b32_e32 v45, v23
	v_mov_b32_e32 v47, v23
	v_permlane32_swap_b32_e32 v44, v46
	s_nop 0
	v_permlane32_swap_b32_e32 v45, v47
	v_cndmask_b32_e32 v45, v45, v47, vcc
	v_cndmask_b32_e32 v44, v44, v46, vcc
	v_pk_fma_f32 v[22:23], v[44:45], 0, v[22:23] op_sel_hi:[1,0,1]
	v_mov_b32_e32 v44, v24
	v_mov_b32_e32 v46, v24
	v_mov_b32_e32 v45, v25
	v_mov_b32_e32 v47, v25
	v_permlane32_swap_b32_e32 v44, v46
	s_nop 0
	v_permlane32_swap_b32_e32 v45, v47
	v_cndmask_b32_e32 v45, v45, v47, vcc
	v_cndmask_b32_e32 v44, v44, v46, vcc
	v_pk_fma_f32 v[24:25], v[44:45], 0, v[24:25] op_sel_hi:[1,0,1]
	v_pk_mul_f32 v[38:39], v[38:39], s[94:95] op_sel_hi:[1,0]
	v_pk_mul_f32 v[34:35], v[34:35], s[94:95] op_sel_hi:[1,0]
	v_pk_mul_f32 v[26:27], v[26:27], s[94:95] op_sel_hi:[1,0]
	v_pk_mul_f32 v[22:23], v[22:23], s[94:95] op_sel_hi:[1,0]
	v_cvt_pk_bf16_f32 v58, v38, v39
	v_pk_mul_f32 v[38:39], v[40:41], s[94:95] op_sel_hi:[1,0]
	v_cvt_pk_bf16_f32 v60, v34, v35
	v_pk_mul_f32 v[34:35], v[36:37], s[94:95] op_sel_hi:[1,0]
	v_cvt_pk_bf16_f32 v86, v26, v27
	v_pk_mul_f32 v[26:27], v[28:29], s[94:95] op_sel_hi:[1,0]
	v_cvt_pk_bf16_f32 v88, v22, v23
	v_pk_mul_f32 v[22:23], v[24:25], s[94:95] op_sel_hi:[1,0]
	v_cvt_pk_bf16_f32 v59, v38, v39
	v_cvt_pk_bf16_f32 v61, v34, v35
	v_cvt_pk_bf16_f32 v87, v26, v27
	v_cvt_pk_bf16_f32 v89, v22, v23
	s_waitcnt vmcnt(0) lgkmcnt(0)
	s_barrier
; #define ATT_SB() __builtin_amdgcn_sched_barrier(0)
; #define ATT_DMA_K(t, sl) do { glds16(ksrc + (size_t)(t) * 64 * kpitch, (unsigned)__builtin_amdgcn_readfirstlane(kdst + (sl) * KSLOT)); \
;         if constexpr (DQK == 96) glds16(krsrc + (size_t)(t) * 64 * 32, (unsigned)__builtin_amdgcn_readfirstlane(krdst + (sl) * KSLOT)); } while (0)
; #define ATT_DMA_V(t, sl) do { glds16(vsrc + (size_t)(t) * 64, (unsigned)__builtin_amdgcn_readfirstlane(vdst + (sl) * VSLOT)); \
;         if constexpr (DV == 128) glds16(vsrc + (size_t)64 * NR + (size_t)(t) * 64, (unsigned)__builtin_amdgcn_readfirstlane(vdst + (sl) * VSLOT + 8192)); } while (0)
; #define ATT_KLOAD(sl) do { _Pragma("unroll") for (int kb_ = 0; kb_ < NKW; ++kb_) _Pragma("unroll") for (int ds_ = 0; ds_ < NDS; ++ds_) { \
;         if (ds_ < 2) kf[kb_ * NDS + ds_] = *(const LAS bf16x8*)(kp[ds_ & 1] + (sl) * KSLOT + (kb_ & 1) * 512 + (kb_ >> 1) * 4096); \
;         else kf[kb_ * NDS + ds_] = *(const LAS bf16x8*)(krp + (sl) * KSLOT + (kb_ & 1) * 256 + (kb_ >> 1) * 2048); } } while (0)
; #define ATT_QK() do { _Pragma("unroll") for (int kb_ = 0; kb_ < NKW; ++kb_) _Pragma("unroll") for (int ds_ = 0; ds_ < NDS; ++ds_) _Pragma("unroll") for (int qb_ = 0; qb_ < NQB; ++qb_) \
;         c[kb_][qb_] = __builtin_amdgcn_mfma_f32_16x16x32_bf16(kf[kb_ * NDS + ds_], qf[qb_ * NDS + ds_], ds_ == 0 ? zero4 : c[kb_][qb_], 0, 0, 0); } while (0)
; template <int DQK, int DV, bool LEAD> ...
;     ...
;     bf16x8 kf[NKW * NDS], vf[NVF];
;     ATT_KLOAD(0);
;     asm volatile("s_waitcnt lgkmcnt(0)\n\ts_barrier" ::: "memory");
;     float lsum[NQB];
; #pragma unroll
;     for (int qb = 0; qb < NQB; ++qb) lsum[qb] = 0.f;
;     const f32x4 zero4 = {0.f, 0.f, 0.f, 0.f};
;     f32x4 o[NDB][NQB], c[NKW][NQB]; u32x4 pw[4];
; #pragma unroll
;     for (int i = 0; i < NDB; ++i)
; #pragma unroll
;         for (int qb = 0; qb < NQB; ++qb) o[i][qb] = zero4;
;     ATT_DMA_K(3, 0); ATT_DMA_V(1, 1);
;     ATT_QK(); ATT_SB();
;     ATT_KLOAD(1); ATT_SB();
;     if constexpr (LEAD) { ATT_EXP(); ATT_SUMPACK(); }
;     wait_bar<NDMA>();
;     int s_prev = 0, s_cur = 1, s_next = 2;
;     int one_ = 1; asm volatile("" : "+s"(one_));
	ds_read_b128 v[22:25], v174
	ds_read_b128 v[26:29], v174 offset:512
	v_bfe_u32 v48, v83, 1, 3
	v_bitop3_b32 v48, v85, v48, 4 bitop3:0x36
	v_lshlrev_b32_e32 v56, 4, v48
	v_add_u32_e32 v176, v90, v56
	s_waitcnt lgkmcnt(1)
	v_mfma_f32_16x16x32_bf16 v[34:37], v[22:25], v[6:9], 0
	ds_read_b128 v[48:51], v176
	ds_read_b128 v[52:55], v176 offset:512
	s_waitcnt lgkmcnt(0)
	s_barrier
	s_mov_b32 s4, m0
	s_mov_b32 m0, s36
	s_nop 0
	global_load_lds_dwordx4 v[168:169], off
	s_mov_b32 m0, s4
	v_mfma_f32_16x16x32_bf16 v[38:41], v[22:25], v[14:17], 0
	s_cselect_b64 vcc, -1, 0
	s_add_i32 s4, s19, 0x2000
	v_mfma_f32_16x16x32_bf16 v[44:47], v[22:25], v[30:33], 0
	v_mfma_f32_16x16x32_bf16 v[22:25], v[22:25], v[58:61], 0
	s_waitcnt lgkmcnt(1)
	v_mfma_f32_16x16x32_bf16 v[142:145], v[48:51], v[2:5], v[34:37]
	v_mfma_f32_16x16x32_bf16 v[138:141], v[48:51], v[10:13], v[38:41]
	v_mfma_f32_16x16x32_bf16 v[110:113], v[48:51], v[86:89], v[22:25]
	v_mfma_f32_16x16x32_bf16 v[22:25], v[26:29], v[6:9], 0
	v_mfma_f32_16x16x32_bf16 v[34:37], v[26:29], v[14:17], 0
	v_mfma_f32_16x16x32_bf16 v[38:41], v[26:29], v[30:33], 0
	v_mfma_f32_16x16x32_bf16 v[26:29], v[26:29], v[58:61], 0
	v_mfma_f32_16x16x32_bf16 v[126:129], v[48:51], v[18:21], v[44:47]
	s_waitcnt lgkmcnt(0)
	v_mfma_f32_16x16x32_bf16 v[134:137], v[52:55], v[2:5], v[22:25]
	s_nop 0
	v_lshlrev_b32_e32 v44, 7, v82
	s_nop 0
	v_lshl_add_u64 v[22:23], v[162:163], 0, s[66:67]
	v_mfma_f32_16x16x32_bf16 v[130:133], v[52:55], v[10:13], v[34:37]
	s_mov_b32 s5, m0
	s_mov_b32 m0, s4
	s_nop 0
	global_load_lds_dwordx4 v[22:23], off
	s_mov_b32 m0, s5
	s_mov_b32 s4, 0
	s_mov_b32 s6, s4
	v_mfma_f32_16x16x32_bf16 v[122:125], v[52:55], v[18:21], v[38:41]
	s_mov_b32 s7, s4
	s_mov_b32 s5, s4
	v_mov_b64_e32 v[24:25], s[6:7]
	v_mfma_f32_16x16x32_bf16 v[114:117], v[52:55], v[86:89], v[26:29]
	v_mov_b64_e32 v[22:23], s[4:5]
	ds_read_b128 v[98:101], v174 offset:8192
	ds_read_b128 v[106:109], v174 offset:8704
	ds_read_b128 v[102:105], v176 offset:8192
	ds_read_b128 v[118:121], v176 offset:8704
	v_cndmask_b32_e32 v26, v56, v84, vcc
	v_add3_u32 v175, 0, v44, v26
	s_waitcnt vmcnt(2) lgkmcnt(0)
	s_barrier
	s_mov_b32 s5, 1
	v_mov_b32_e32 v164, 0
	s_cmp_lg_u32 s5, 0
	v_mov_b64_e32 v[28:29], v[24:25]
	v_mov_b64_e32 v[36:37], v[24:25]
	v_mov_b64_e32 v[40:41], v[24:25]
	v_mov_b64_e32 v[44:45], v[24:25]
	v_mov_b64_e32 v[48:49], v[24:25]
	v_mov_b64_e32 v[52:53], v[24:25]
	v_mov_b64_e32 v[56:57], v[24:25]
	v_mov_b64_e32 v[64:65], v[24:25]
	v_mov_b64_e32 v[68:69], v[24:25]
	v_mov_b64_e32 v[72:73], v[24:25]
	v_mov_b64_e32 v[76:77], v[24:25]
	v_mov_b64_e32 v[80:81], v[24:25]
	v_mov_b64_e32 v[84:85], v[24:25]
	v_mov_b64_e32 v[92:93], v[24:25]
	v_mov_b64_e32 v[96:97], v[24:25]
	s_cselect_b64 s[6:7], -1, 0
	v_mov_b64_e32 v[26:27], v[22:23]
	v_mov_b64_e32 v[34:35], v[22:23]
	v_mov_b64_e32 v[38:39], v[22:23]
	v_mov_b64_e32 v[42:43], v[22:23]
	v_mov_b64_e32 v[46:47], v[22:23]
	v_mov_b64_e32 v[50:51], v[22:23]
	v_mov_b64_e32 v[54:55], v[22:23]
	v_mov_b64_e32 v[62:63], v[22:23]
	v_mov_b64_e32 v[66:67], v[22:23]
	v_mov_b64_e32 v[70:71], v[22:23]
	v_mov_b64_e32 v[74:75], v[22:23]
	v_mov_b64_e32 v[78:79], v[22:23]
	v_mov_b64_e32 v[82:83], v[22:23]
	v_mov_b64_e32 v[90:91], v[22:23]
	v_mov_b64_e32 v[94:95], v[22:23]
	s_mov_b32 s38, 2
	v_mov_b32_e32 v165, v164
	v_mov_b32_e32 v166, v164
	v_mov_b32_e32 v167, v164

; #define LAS __attribute__((address_space(3)))
; template <int DQK, int DV, bool LEAD> ...
;     ...
;     const bf16_t* ksrc = K + (size_t)(krow0 + krow_l) * kpitch + kc_l * 8;
;     const int rrow_l = (wid & 3) * 16 + (lane >> 2), rc_l = (lane & 3) ^ (((rrow_l >> 4) & 1) << 1);
;     const bf16_t* krsrc = (DQK == 96) ? KR + (size_t)(krow0 + rrow_l) * 32 + rc_l * 8 : nullptr;
;     const bf16_t* vsrc = Vt + (size_t)krow_l * NR + krow0 + vc_l * 8;
;     const unsigned kdst = lds0 + KOFF + wid * 1024, krdst = lds0 + KOFF + 8192 + (wid & 3) * 1024, vdst = lds0 + VOFF + wid * 1024;
;     ...
;     const int kr0 = 8 * (q16 >> 2) + (q16 & 3);
;     const int fk = ((kr0 >> 1) & 1) | (((kr0 >> 3) & 1) << 1) | (((kr0 >> 4) & 1) << 2);
;     const LAS unsigned char* kp[2]; const LAS unsigned char* vp[2];
; #pragma unroll
;     for (int ds = 0; ds < 2; ++ds) kp[ds] = shm + KOFF + kr0 * 128 + ((((ds << 2) | g4) ^ fk) << 4) + kg * 4096;
;     const LAS unsigned char* krp = shm + KOFF + 8192 + kr0 * 64 + ((g4 ^ (((kr0 >> 4) & 1) << 1)) << 4) + kg * 2048;
; #pragma unroll
;     for (int s_ = 0; s_ < 2; ++s_) vp[s_] = shm + VOFF + q16 * 128 + ((((s_ << 2) | g4) ^ ((q16 >> 1) & 7)) << 4);
;     const LAS unsigned char* vpk = kg ? vp[1] : vp[0];
;     ...
;     ATT_DMA_K(0, 0); ATT_DMA_V(0, 0); ATT_DMA_K(1, 1); ATT_DMA_K(2, 2);
;     bf16x8 qf[NQB * NDS];
;     {
;       const float c2 = (DQK == 64) ? C2_EVEN : C2_ODD; const bool lat = tq0 >= 0;
; #pragma unroll
;       for (int qb = 0; qb < NQB; ++qb) {
;           const bf16_t* qp = Q + (size_t)(qrow0 + qoff + qb * 16 + q16) * qpitch + g4 * 8;
;           bf16x8 raw[NDS];
; #pragma unroll
;           for (int ds = 0; ds < NDS; ++ds) raw[ds] = *(const bf16x8*)(qp + ds * 32);
;           float x[NDS][8];
; #pragma unroll
;           for (int ds = 0; ds < NDS; ++ds)
; #pragma unroll
;               for (int j = 0; j < 8; ++j) x[ds][j] = __uint_as_float(((unsigned)(unsigned short)raw[ds][j]) << 16);
;           const int tq = tq0 + qoff + qb * 16 + q16, prow = (tq >> 6) & 127, pcol = tq & 63;
;           float sn = 0.f;
; #pragma unroll
;           for (int ds = 0; ds < 2; ++ds)
; #pragma unroll
;               for (int j = 0; j < 8; ++j) sn += x[ds][j] * x[ds][j];
;           sn = lanes4_sum(sn);
.LBB0_995:
	s_and_b64 vcc, exec, s[4:5]
	s_cbranch_vccz .LBB0_986
	v_mov_b32_e32 v84, v0
	s_mov_b32 s19, s39
	v_readfirstlane_b32 s16, v84
	s_ashr_i32 s4, s16, 6
	v_bfe_u32 v1, v84, 3, 3
	v_lshl_or_b32 v6, s4, 3, v1
	s_lshl_b32 s5, s4, 1
	s_lshr_b32 s6, s16, 5
	v_ashrrev_i32_e32 v2, 1, v6
	s_and_b32 s5, s5, 2
	s_and_b32 s6, s6, 4
	v_and_b32_e32 v170, 7, v84
	v_and_b32_e32 v3, 1, v2
	s_or_b32 s5, s5, s6
	s_and_b32 s7, s4, 3
	v_bitop3_b32 v7, s5, v170, v3 bitop3:0x36
	v_xor_b32_e32 v8, v2, v84
	v_add_u32_e32 v4, s18, v6
	s_lshl_b32 s4, s4, 10
	v_mov_b64_e32 v[2:3], s[22:23]
	s_add_i32 s31, s4, 0
	v_mad_i64_i32 v[2:3], s[4:5], v4, s92, v[2:3]
	v_mov_b64_e32 v[4:5], s[26:27]
	v_lshlrev_b32_e32 v194, 4, v7
	v_mad_i64_i32 v[4:5], s[4:5], v6, s91, v[4:5]
	v_lshl_add_u64 v[42:43], v[2:3], 0, v[194:195]
	v_lshlrev_b32_e32 v2, 4, v8
	v_lshl_add_u64 v[4:5], s[18:19], 1, v[4:5]
	v_and_b32_e32 v194, 0x70, v2
	s_mov_b32 s5, m0
	s_mov_b32 m0, s31
	s_nop 0
	global_load_lds_dwordx4 v[42:43], off
	s_mov_b32 m0, s5
	v_lshl_add_u64 v[162:163], v[4:5], 0, v[194:195]
	s_add_i32 s19, s31, 0x9000
	s_mov_b32 s5, m0
	s_mov_b32 m0, s19
	s_nop 0
	global_load_lds_dwordx4 v[162:163], off
	s_mov_b32 m0, s5
	s_mov_b64 s[22:23], 0x38000
	v_lshl_add_u64 v[2:3], v[42:43], 0, s[22:23]
	s_add_i32 s5, s31, 0x2000
	s_mov_b32 s6, m0
	s_mov_b32 m0, s5
	s_nop 0
	global_load_lds_dwordx4 v[2:3], off
	s_mov_b32 m0, s6
	s_mov_b64 s[22:23], 0x70000
	s_lshl_b32 s4, s7, 6
	v_lshl_add_u64 v[2:3], v[42:43], 0, s[22:23]
	s_add_i32 s5, s31, 0x4000
	s_mov_b32 s6, m0
	s_mov_b32 m0, s5
	s_nop 0
	global_load_lds_dwordx4 v[2:3], off
	s_mov_b32 m0, s6
	v_and_b32_e32 v83, 15, v84
	s_or_b32 s6, s4, s18
	v_or_b32_e32 v18, s6, v83
	v_and_b32_e32 v194, 48, v84
	v_lshl_add_u64 v[10:11], s[12:13], 0, v[194:195]
	v_or_b32_e32 v16, 32, v18
	v_mad_u64_u32 v[16:17], s[4:5], v16, s92, v[10:11]
	global_load_dwordx4 v[34:37], v[16:17], off offset:64 nt
	v_mad_u64_u32 v[12:13], s[4:5], v18, s92, v[10:11]
	v_or_b32_e32 v6, 16, v18
	v_or_b32_e32 v18, 48, v18
	global_load_dwordx4 v[2:5], v[12:13], off offset:64 nt
	v_mad_u64_u32 v[14:15], s[4:5], v6, s92, v[10:11]
	v_mad_u64_u32 v[10:11], s[4:5], v18, s92, v[10:11]
	global_load_dwordx4 v[6:9], v[14:15], off offset:64 nt
	global_load_dwordx4 v[38:41], v[10:11], off offset:64 nt
	global_load_dwordx4 v[64:67], v[12:13], off nt
	global_load_dwordx4 v[86:89], v[14:15], off nt
	global_load_dwordx4 v[18:21], v[16:17], off nt
	s_nop 0
	global_load_dwordx4 v[14:17], v[10:11], off nt
	v_bfe_u32 v171, v84, 4, 2
	s_waitcnt vmcnt(8)
	v_lshlrev_b32_e32 v52, 5, v171
	global_load_dwordx4 v[26:29], v52, s[8:9] offset:144
	global_load_dwordx4 v[30:33], v52, s[8:9] offset:128
	s_lshl_b32 s4, s16, 4
	v_lshlrev_b32_e32 v172, 1, v84
	v_and_b32_e32 v10, 3, v84
	v_lshrrev_b32_e32 v11, 1, v84
	s_and_b32 s4, s4, 0xfffff000
	v_and_or_b32 v10, v172, 24, v10
	v_bitop3_b32 v11, v171, v11, 7 bitop3:0x78
	s_add_i32 s4, s4, 0
	v_lshlrev_b32_e32 v82, 4, v11
	v_lshl_add_u32 v85, v10, 7, s4
	s_mov_b32 s4, 0x358637bd
	v_and_b32_e32 v173, 63, v84
	v_add_u32_e32 v174, v85, v82
	v_lshl_add_u64 v[168:169], v[42:43], 0, s[96:97]
	s_mov_b32 s12, 2
	v_or_b32_e32 v175, 4, v171
	v_lshlrev_b32_e32 v176, 7, v83
	s_mov_b32 s13, 0
	s_waitcnt vmcnt(9)
	v_and_b32_e32 v23, 0xffff0000, v37
	v_lshlrev_b32_e32 v22, 16, v37
	v_and_b32_e32 v25, 0xffff0000, v36
	v_lshlrev_b32_e32 v24, 16, v36
	v_and_b32_e32 v57, 0xffff0000, v35
	v_lshlrev_b32_e32 v56, 16, v35
	v_and_b32_e32 v59, 0xffff0000, v34
	s_waitcnt vmcnt(6)
	v_and_b32_e32 v45, 0xffff0000, v41
	v_lshlrev_b32_e32 v44, 16, v41
	v_and_b32_e32 v47, 0xffff0000, v40
	v_lshlrev_b32_e32 v46, 16, v40
	v_and_b32_e32 v49, 0xffff0000, v39
	v_lshlrev_b32_e32 v48, 16, v39
	v_lshlrev_b32_e32 v58, 16, v34
	v_and_b32_e32 v51, 0xffff0000, v38
	v_lshlrev_b32_e32 v50, 16, v38
	global_load_dwordx4 v[34:37], v52, s[8:9] offset:16
	global_load_dwordx4 v[38:41], v52, s[8:9]
	s_waitcnt vmcnt(6)
	v_and_b32_e32 v75, 0xffff0000, v89
	v_lshlrev_b32_e32 v74, 16, v89
	v_and_b32_e32 v89, 0xffff0000, v64
	v_and_b32_e32 v93, 0xffff0000, v2
	v_lshlrev_b32_e32 v92, 16, v2
	v_and_b32_e32 v77, 0xffff0000, v88
	v_lshlrev_b32_e32 v76, 16, v88
	v_lshlrev_b32_e32 v88, 16, v64
	v_mul_f32_e32 v2, v89, v89
	v_and_b32_e32 v11, 0xffff0000, v9
	v_lshlrev_b32_e32 v10, 16, v9
	v_and_b32_e32 v69, 0xffff0000, v8
	v_lshlrev_b32_e32 v68, 16, v8
	v_and_b32_e32 v9, 0xffff0000, v3
	v_lshlrev_b32_e32 v8, 16, v3
	s_waitcnt vmcnt(4)
; template <int DQK, int DV, bool LEAD> ...
;     ...
;           float sn = 0.f;
; #pragma unroll
;           for (int ds = 0; ds < 2; ++ds)
; #pragma unroll
;               for (int j = 0; j < 8; ++j) sn += x[ds][j] * x[ds][j];
;           sn = lanes4_sum(sn);
;           const float rn = rsqrtf(sn * (1.f / 64.f) + EPS);
; #pragma unroll
;           for (int ds = 0; ds < 2; ++ds)
; #pragma unroll
;               for (int j = 0; j < 8; ++j) x[ds][j] *= rn * qgain[32 * ds + 8 * g4 + j];
;           if constexpr (DQK == 64) {
; #pragma unroll
;               for (int ds = 0; ds < 2; ++ds)
; #pragma unroll
;                   for (int j = 0; j < 8; ++j) {
;                       auto rr = __builtin_amdgcn_permlane32_swap(__float_as_uint(x[ds][j]), __float_as_uint(x[ds][j]), false, false);
;                       const float other = hi ? __uint_as_float(rr[0]) : __uint_as_float(rr[1]);
;                       float cc = 1.f, sg = 0.f;
;                       if (lat) { const f32x2 cs = rope[(ds ? pcol : prow) * 16 + 8 * (g4 & 1) + j]; cc = cs.x; sg = hi ? cs.y : -cs.y; }
;                       x[ds][j] = x[ds][j] * cc + other * sg; }
;           } else {
;               float sr = 0.f;
; #pragma unroll
;               for (int j = 0; j < 8; ++j) sr += x[2][j] * x[2][j];
;               sr = lanes4_sum(sr);
;               const float rq = rsqrtf(sr * (1.f / 32.f) + EPS);
; #pragma unroll
;               for (int j = 0; j < 8; ++j) { const float av = x[2][j] * rq * qgain[64 + 8 * g4 + j];
;                   auto rr = __builtin_amdgcn_permlane16_swap(__float_as_uint(av), __float_as_uint(av), false, false);
;                   const float other = (g4 & 1) ? __uint_as_float(rr[0]) : __uint_as_float(rr[1]);
;                   float cc = 1.f, sg = 0.f;
;                   if (lat) { const f32x2 cs = rope[((g4 & 2) ? pcol : prow) * 8 + j]; cc = cs.x; sg = (g4 & 1) ? cs.y : -cs.y; }
;                   x[2][j] = av * cc + other * sg; }
;           }
; #pragma unroll
;           for (int ds = 0; ds < NDS; ++ds) { u32x4 w;
; #pragma unroll
;               for (int i = 0; i < 4; ++i) w[i] = cvtpk(x[ds][2 * i] * c2, x[ds][2 * i + 1] * c2);
;               qf[qb * NDS + ds] = __builtin_bit_cast(bf16x8, w); }
	v_and_b32_e32 v53, 0xffff0000, v17
	v_lshlrev_b32_e32 v52, 16, v17
	v_and_b32_e32 v55, 0xffff0000, v16
	v_lshlrev_b32_e32 v54, 16, v16
	v_and_b32_e32 v17, 0xffff0000, v65
	v_lshlrev_b32_e32 v16, 16, v65
	v_pk_fma_f32 v[2:3], v[88:89], v[88:89], v[2:3] op_sel_hi:[1,1,0]
	v_and_b32_e32 v91, 0xffff0000, v4
	v_lshlrev_b32_e32 v90, 16, v4
	v_pk_fma_f32 v[2:3], v[16:17], v[16:17], v[2:3]
	v_mul_f32_e32 v4, v17, v17
	v_and_b32_e32 v95, 0xffff0000, v66
	v_lshlrev_b32_e32 v94, 16, v66
	v_pk_add_f32 v[2:3], v[4:5], v[2:3] op_sel_hi:[0,1]
	v_pk_fma_f32 v[2:3], v[94:95], v[94:95], v[2:3]
	v_mul_f32_e32 v4, v95, v95
	v_and_b32_e32 v71, 0xffff0000, v7
	v_lshlrev_b32_e32 v70, 16, v7
	v_and_b32_e32 v73, 0xffff0000, v6
	v_lshlrev_b32_e32 v72, 16, v6
	v_and_b32_e32 v7, 0xffff0000, v67
	v_lshlrev_b32_e32 v6, 16, v67
	v_pk_add_f32 v[2:3], v[4:5], v[2:3] op_sel_hi:[0,1]
	v_pk_fma_f32 v[2:3], v[6:7], v[6:7], v[2:3]
	v_mul_f32_e32 v4, v7, v7
	v_pk_add_f32 v[2:3], v[4:5], v[2:3] op_sel_hi:[0,1]
	v_pk_fma_f32 v[2:3], v[92:93], v[92:93], v[2:3]
	v_mul_f32_e32 v4, v93, v93
	v_pk_add_f32 v[2:3], v[4:5], v[2:3] op_sel_hi:[0,1]
	v_pk_fma_f32 v[2:3], v[8:9], v[8:9], v[2:3]
	v_mul_f32_e32 v4, v9, v9
	v_pk_add_f32 v[2:3], v[4:5], v[2:3] op_sel_hi:[0,1]
	v_pk_fma_f32 v[2:3], v[90:91], v[90:91], v[2:3]
	v_mul_f32_e32 v4, v91, v91
	v_and_b32_e32 v13, 0xffff0000, v5
	v_lshlrev_b32_e32 v12, 16, v5
	v_pk_add_f32 v[2:3], v[4:5], v[2:3] op_sel_hi:[0,1]
	v_pk_fma_f32 v[2:3], v[12:13], v[12:13], v[2:3]
	v_mul_f32_e32 v4, v13, v13
	v_pk_add_f32 v[2:3], v[4:5], v[2:3] op_sel_hi:[0,1]
	v_mov_b32_e32 v3, v2
	s_nop 1
	v_permlane16_swap_b32_e32 v2, v3
	v_add_f32_e32 v3, v2, v3
	v_mov_b32_e32 v5, v3
	v_and_b32_e32 v81, 0xffff0000, v86
	s_nop 0
	v_permlane32_swap_b32_e32 v3, v5
	v_lshlrev_b32_e32 v80, 16, v86
	v_mul_f32_e32 v2, v81, v81
	v_and_b32_e32 v61, 0xffff0000, v21
	v_lshlrev_b32_e32 v60, 16, v21
	v_and_b32_e32 v63, 0xffff0000, v20
	v_lshlrev_b32_e32 v62, 16, v20
	v_and_b32_e32 v79, 0xffff0000, v87
	v_lshlrev_b32_e32 v78, 16, v87
	v_pk_fma_f32 v[20:21], v[80:81], v[80:81], v[2:3] op_sel_hi:[1,1,0]
	v_mul_f32_e32 v2, v79, v79
	v_pk_fma_f32 v[20:21], v[78:79], v[78:79], v[20:21]
	s_mov_b32 s8, 0x3c800000
	v_pk_add_f32 v[20:21], v[2:3], v[20:21] op_sel_hi:[0,1]
	v_pk_fma_f32 v[20:21], v[76:77], v[76:77], v[20:21]
	v_mul_f32_e32 v2, v77, v77
	v_pk_add_f32 v[20:21], v[2:3], v[20:21] op_sel_hi:[0,1]
	v_pk_fma_f32 v[20:21], v[74:75], v[74:75], v[20:21]
	v_mul_f32_e32 v2, v75, v75
	v_pk_add_f32 v[20:21], v[2:3], v[20:21] op_sel_hi:[0,1]
	v_pk_fma_f32 v[20:21], v[72:73], v[72:73], v[20:21]
	v_mul_f32_e32 v2, v73, v73
	v_pk_add_f32 v[20:21], v[2:3], v[20:21] op_sel_hi:[0,1]
	v_pk_fma_f32 v[20:21], v[70:71], v[70:71], v[20:21]
	v_mul_f32_e32 v2, v71, v71
	v_pk_add_f32 v[20:21], v[2:3], v[20:21] op_sel_hi:[0,1]
	v_pk_fma_f32 v[20:21], v[68:69], v[68:69], v[20:21]
	v_mul_f32_e32 v2, v69, v69
	v_pk_add_f32 v[20:21], v[2:3], v[20:21] op_sel_hi:[0,1]
	v_pk_fma_f32 v[20:21], v[10:11], v[10:11], v[20:21]
	v_mul_f32_e32 v2, v11, v11
	v_pk_add_f32 v[20:21], v[2:3], v[20:21] op_sel_hi:[0,1]
	v_mov_b32_e32 v2, v20
	s_nop 1
	v_permlane16_swap_b32_e32 v20, v2
	v_add_f32_e32 v2, v20, v2
	v_mov_b32_e32 v4, v2
	s_nop 1
	v_permlane32_swap_b32_e32 v2, v4
	v_pk_add_f32 v[2:3], v[2:3], v[4:5]
	v_mov_b64_e32 v[20:21], s[4:5]
	v_pk_fma_f32 v[86:87], v[2:3], s[8:9], v[20:21] op_sel_hi:[1,0,0]
	v_and_b32_e32 v67, 0xffff0000, v15
	v_mul_f32_e32 v2, 0x4b800000, v87
	v_cmp_gt_f32_e32 vcc, s95, v87
	v_lshlrev_b32_e32 v66, 16, v15
	v_cmp_gt_f32_e64 s[4:5], s95, v86
	v_cndmask_b32_e32 v2, v87, v2, vcc
	v_rsq_f32_e32 v2, v2
	v_and_b32_e32 v65, 0xffff0000, v19
	v_lshlrev_b32_e32 v64, 16, v19
	v_mul_f32_e32 v3, 0x45800000, v2
	v_cndmask_b32_e32 v96, v2, v3, vcc
	s_waitcnt vmcnt(3)
	v_pk_mul_f32 v[2:3], v[96:97], v[28:29] op_sel_hi:[0,1]
	v_pk_mul_f32 v[2:3], v[2:3], v[12:13]
	v_cmp_gt_u32_e32 vcc, 32, v173
	v_mov_b32_e32 v4, v2
	v_mov_b32_e32 v12, v2
	v_mov_b32_e32 v5, v3
	v_mov_b32_e32 v13, v3
	v_permlane32_swap_b32_e32 v4, v12
	s_nop 0
	v_permlane32_swap_b32_e32 v5, v13
	v_cndmask_b32_e32 v5, v5, v13, vcc
	v_cndmask_b32_e32 v4, v4, v12, vcc
	v_pk_fma_f32 v[2:3], v[4:5], 0, v[2:3] op_sel_hi:[1,0,1]
	s_nop 0
	v_pk_mul_f32 v[2:3], v[2:3], s[94:95] op_sel_hi:[1,0]
	s_nop 0
	v_cvt_pk_bf16_f32 v5, v2, v3
	v_pk_mul_f32 v[2:3], v[96:97], v[26:27] op_sel_hi:[0,1]
	v_pk_mul_f32 v[2:3], v[2:3], v[90:91]
	s_nop 0
	v_mov_b32_e32 v4, v2
	v_mov_b32_e32 v12, v2
	v_mov_b32_e32 v13, v3
	v_mov_b32_e32 v15, v3
	v_permlane32_swap_b32_e32 v4, v12
	s_nop 0
	v_permlane32_swap_b32_e32 v13, v15
	v_cndmask_b32_e32 v13, v13, v15, vcc
	v_cndmask_b32_e32 v12, v4, v12, vcc
	v_pk_fma_f32 v[2:3], v[12:13], 0, v[2:3] op_sel_hi:[1,0,1]
	s_nop 0
	v_pk_mul_f32 v[2:3], v[2:3], s[94:95] op_sel_hi:[1,0]
	s_nop 0
	v_cvt_pk_bf16_f32 v4, v2, v3
	s_waitcnt vmcnt(2)
	v_pk_mul_f32 v[2:3], v[96:97], v[32:33] op_sel_hi:[0,1]
	v_pk_mul_f32 v[2:3], v[2:3], v[8:9]
	s_nop 0
	v_mov_b32_e32 v8, v2
	v_mov_b32_e32 v12, v2
	v_mov_b32_e32 v9, v3
	v_mov_b32_e32 v13, v3
	v_permlane32_swap_b32_e32 v8, v12
	s_nop 0
	v_permlane32_swap_b32_e32 v9, v13
	v_cndmask_b32_e32 v9, v9, v13, vcc
	v_cndmask_b32_e32 v8, v8, v12, vcc
	v_pk_fma_f32 v[2:3], v[8:9], 0, v[2:3] op_sel_hi:[1,0,1]
	v_pk_mul_f32 v[8:9], v[30:31], v[96:97] op_sel_hi:[1,0]
	v_pk_mul_f32 v[2:3], v[2:3], s[94:95] op_sel_hi:[1,0]
	v_pk_mul_f32 v[8:9], v[8:9], v[92:93]
	v_cvt_pk_bf16_f32 v3, v2, v3
	v_mov_b32_e32 v2, v8
	v_mov_b32_e32 v12, v8
	v_mov_b32_e32 v13, v9
	v_mov_b32_e32 v15, v9
	v_permlane32_swap_b32_e32 v2, v12
	s_nop 0
	v_permlane32_swap_b32_e32 v13, v15
	v_cndmask_b32_e32 v13, v13, v15, vcc
	v_cndmask_b32_e32 v12, v2, v12, vcc
	v_pk_fma_f32 v[8:9], v[12:13], 0, v[8:9] op_sel_hi:[1,0,1]
	s_nop 0
	v_pk_mul_f32 v[8:9], v[8:9], s[94:95] op_sel_hi:[1,0]
	s_nop 0
	v_cvt_pk_bf16_f32 v2, v8, v9
	s_waitcnt vmcnt(1)
; __device__ __forceinline__ unsigned cvtpk(float lo, float hi) { f32x2 v = {lo, hi}; bf16x2_t b = __builtin_convertvector(v, bf16x2_t); return __builtin_bit_cast(unsigned, b); }
; template <int DQK, int DV, bool LEAD> ...
;     ...
;           const float rn = rsqrtf(sn * (1.f / 64.f) + EPS);
; #pragma unroll
;           for (int ds = 0; ds < 2; ++ds)
; #pragma unroll
;               for (int j = 0; j < 8; ++j) x[ds][j] *= rn * qgain[32 * ds + 8 * g4 + j];
;           if constexpr (DQK == 64) {
; #pragma unroll
;               for (int ds = 0; ds < 2; ++ds)
; #pragma unroll
;                   for (int j = 0; j < 8; ++j) {
;                       auto rr = __builtin_amdgcn_permlane32_swap(__float_as_uint(x[ds][j]), __float_as_uint(x[ds][j]), false, false);
;                       const float other = hi ? __uint_as_float(rr[0]) : __uint_as_float(rr[1]);
;                       float cc = 1.f, sg = 0.f;
;                       if (lat) { const f32x2 cs = rope[(ds ? pcol : prow) * 16 + 8 * (g4 & 1) + j]; cc = cs.x; sg = hi ? cs.y : -cs.y; }
;                       x[ds][j] = x[ds][j] * cc + other * sg; }
;           } else {
;               float sr = 0.f;
; #pragma unroll
;               for (int j = 0; j < 8; ++j) sr += x[2][j] * x[2][j];
;               sr = lanes4_sum(sr);
;               const float rq = rsqrtf(sr * (1.f / 32.f) + EPS);
; #pragma unroll
;               for (int j = 0; j < 8; ++j) { const float av = x[2][j] * rq * qgain[64 + 8 * g4 + j];
;                   auto rr = __builtin_amdgcn_permlane16_swap(__float_as_uint(av), __float_as_uint(av), false, false);
;                   const float other = (g4 & 1) ? __uint_as_float(rr[0]) : __uint_as_float(rr[1]);
;                   float cc = 1.f, sg = 0.f;
;                   if (lat) { const f32x2 cs = rope[((g4 & 2) ? pcol : prow) * 8 + j]; cc = cs.x; sg = (g4 & 1) ? cs.y : -cs.y; }
;                   x[2][j] = av * cc + other * sg; }
;           }
; #pragma unroll
;           for (int ds = 0; ds < NDS; ++ds) { u32x4 w;
; #pragma unroll
;               for (int i = 0; i < 4; ++i) w[i] = cvtpk(x[ds][2 * i] * c2, x[ds][2 * i + 1] * c2);
;               qf[qb * NDS + ds] = __builtin_bit_cast(bf16x8, w); }
	v_pk_mul_f32 v[8:9], v[36:37], v[96:97] op_sel_hi:[1,0]
	s_nop 0
	v_pk_mul_f32 v[6:7], v[8:9], v[6:7]
	s_nop 0
	v_mov_b32_e32 v8, v6
	v_mov_b32_e32 v12, v6
	v_mov_b32_e32 v9, v7
	v_mov_b32_e32 v13, v7
	v_permlane32_swap_b32_e32 v8, v12
	s_nop 0
	v_permlane32_swap_b32_e32 v9, v13
	v_cndmask_b32_e32 v9, v9, v13, vcc
	v_cndmask_b32_e32 v8, v8, v12, vcc
	v_pk_fma_f32 v[6:7], v[8:9], 0, v[6:7] op_sel_hi:[1,0,1]
	s_nop 0
	v_pk_mul_f32 v[6:7], v[6:7], s[94:95] op_sel_hi:[1,0]
	s_nop 0
	v_cvt_pk_bf16_f32 v9, v6, v7
	v_pk_mul_f32 v[6:7], v[34:35], v[96:97] op_sel_hi:[1,0]
	s_nop 0
	v_pk_mul_f32 v[6:7], v[6:7], v[94:95]
	s_nop 0
	v_mov_b32_e32 v8, v6
	v_mov_b32_e32 v12, v6
	v_mov_b32_e32 v13, v7
	v_mov_b32_e32 v15, v7
	v_permlane32_swap_b32_e32 v8, v12
	s_nop 0
	v_permlane32_swap_b32_e32 v13, v15
	v_cndmask_b32_e32 v13, v13, v15, vcc
	v_cndmask_b32_e32 v12, v8, v12, vcc
	v_pk_fma_f32 v[6:7], v[12:13], 0, v[6:7] op_sel_hi:[1,0,1]
	s_nop 0
	v_pk_mul_f32 v[6:7], v[6:7], s[94:95] op_sel_hi:[1,0]
	s_nop 0
	v_cvt_pk_bf16_f32 v8, v6, v7
	s_waitcnt vmcnt(0)
	v_pk_mul_f32 v[6:7], v[40:41], v[96:97] op_sel_hi:[1,0]
	s_nop 0
	v_pk_mul_f32 v[6:7], v[6:7], v[16:17]
	s_nop 0
	v_mov_b32_e32 v12, v6
	v_mov_b32_e32 v15, v6
	v_mov_b32_e32 v13, v7
	v_mov_b32_e32 v16, v7
	v_permlane32_swap_b32_e32 v12, v15
	s_nop 0
	v_permlane32_swap_b32_e32 v13, v16
	v_cndmask_b32_e32 v13, v13, v16, vcc
	v_cndmask_b32_e32 v12, v12, v15, vcc
	v_pk_fma_f32 v[6:7], v[12:13], 0, v[6:7] op_sel_hi:[1,0,1]
	v_pk_mul_f32 v[12:13], v[38:39], v[96:97] op_sel_hi:[1,0]
	v_pk_mul_f32 v[6:7], v[6:7], s[94:95] op_sel_hi:[1,0]
	v_pk_mul_f32 v[12:13], v[12:13], v[88:89]
	v_cvt_pk_bf16_f32 v7, v6, v7
	v_mov_b32_e32 v6, v12
	v_mov_b32_e32 v15, v12
	v_mov_b32_e32 v16, v13
	v_mov_b32_e32 v17, v13
	v_permlane32_swap_b32_e32 v6, v15
	s_nop 0
	v_permlane32_swap_b32_e32 v16, v17
	v_cndmask_b32_e32 v17, v16, v17, vcc
	v_cndmask_b32_e32 v16, v6, v15, vcc
	v_mul_f32_e32 v6, 0x4b800000, v86
	v_cndmask_b32_e64 v6, v86, v6, s[4:5]
	v_rsq_f32_e32 v15, v6
	v_pk_fma_f32 v[12:13], v[16:17], 0, v[12:13] op_sel_hi:[1,0,1]
	s_nop 0
	v_pk_mul_f32 v[12:13], v[12:13], s[94:95] op_sel_hi:[1,0]
	s_nop 0
	v_cvt_pk_bf16_f32 v6, v12, v13
	v_mul_f32_e32 v12, 0x45800000, v15
	v_cndmask_b32_e64 v86, v15, v12, s[4:5]
	v_pk_mul_f32 v[12:13], v[28:29], v[86:87] op_sel_hi:[1,0]
	s_nop 0
	v_pk_mul_f32 v[10:11], v[12:13], v[10:11]
	s_nop 0
	v_mov_b32_e32 v12, v10
	v_mov_b32_e32 v15, v10
	v_mov_b32_e32 v13, v11
	v_mov_b32_e32 v16, v11
	v_permlane32_swap_b32_e32 v12, v15
	s_nop 0
	v_permlane32_swap_b32_e32 v13, v16
	v_cndmask_b32_e32 v13, v13, v16, vcc
	v_cndmask_b32_e32 v12, v12, v15, vcc
	v_pk_fma_f32 v[10:11], v[12:13], 0, v[10:11] op_sel_hi:[1,0,1]
	s_nop 0
	v_pk_mul_f32 v[10:11], v[10:11], s[94:95] op_sel_hi:[1,0]
	s_nop 0
	v_cvt_pk_bf16_f32 v13, v10, v11
	v_pk_mul_f32 v[10:11], v[26:27], v[86:87] op_sel_hi:[1,0]
	s_nop 0
	v_pk_mul_f32 v[10:11], v[10:11], v[68:69]
	s_nop 0
	v_mov_b32_e32 v12, v10
	v_mov_b32_e32 v15, v10
	v_mov_b32_e32 v16, v11
	v_mov_b32_e32 v17, v11
	v_permlane32_swap_b32_e32 v12, v15
	s_nop 0
	v_permlane32_swap_b32_e32 v16, v17
	v_cndmask_b32_e32 v17, v16, v17, vcc
	v_cndmask_b32_e32 v16, v12, v15, vcc
	v_pk_fma_f32 v[10:11], v[16:17], 0, v[10:11] op_sel_hi:[1,0,1]
	s_nop 0
	v_pk_mul_f32 v[10:11], v[10:11], s[94:95] op_sel_hi:[1,0]
	s_nop 0
	v_cvt_pk_bf16_f32 v12, v10, v11
	v_pk_mul_f32 v[10:11], v[32:33], v[86:87] op_sel_hi:[1,0]
	s_nop 0
	v_pk_mul_f32 v[10:11], v[10:11], v[70:71]
	s_nop 0
	v_mov_b32_e32 v15, v10
	v_mov_b32_e32 v16, v10
	v_mov_b32_e32 v17, v11
	v_mov_b32_e32 v19, v11
	v_permlane32_swap_b32_e32 v15, v16
	s_nop 0
	v_permlane32_swap_b32_e32 v17, v19
	v_cndmask_b32_e32 v17, v17, v19, vcc
	v_cndmask_b32_e32 v16, v15, v16, vcc
	v_pk_fma_f32 v[10:11], v[16:17], 0, v[10:11] op_sel_hi:[1,0,1]
	v_pk_mul_f32 v[16:17], v[30:31], v[86:87] op_sel_hi:[1,0]
	v_pk_mul_f32 v[10:11], v[10:11], s[94:95] op_sel_hi:[1,0]
	v_pk_mul_f32 v[16:17], v[16:17], v[72:73]
	v_cvt_pk_bf16_f32 v11, v10, v11
	v_mov_b32_e32 v10, v16
	v_mov_b32_e32 v15, v16
	v_mov_b32_e32 v19, v17
	v_mov_b32_e32 v68, v17
	v_permlane32_swap_b32_e32 v10, v15
	s_nop 0
	v_permlane32_swap_b32_e32 v19, v68
	v_cndmask_b32_e32 v69, v19, v68, vcc
	v_cndmask_b32_e32 v68, v10, v15, vcc
	v_pk_fma_f32 v[16:17], v[68:69], 0, v[16:17] op_sel_hi:[1,0,1]
	v_and_b32_e32 v73, 0xffff0000, v18
	v_pk_mul_f32 v[16:17], v[16:17], s[94:95] op_sel_hi:[1,0]
	s_nop 0
	v_cvt_pk_bf16_f32 v10, v16, v17
	v_pk_mul_f32 v[16:17], v[36:37], v[86:87] op_sel_hi:[1,0]
	s_nop 0
	v_pk_mul_f32 v[16:17], v[16:17], v[74:75]
	v_mul_f32_e32 v74, v65, v65
	v_mov_b32_e32 v15, v16
	v_mov_b32_e32 v19, v16
	v_mov_b32_e32 v68, v17
	v_mov_b32_e32 v69, v17
	v_permlane32_swap_b32_e32 v15, v19
	s_nop 0
	v_permlane32_swap_b32_e32 v68, v69
	v_cndmask_b32_e32 v69, v68, v69, vcc
	v_cndmask_b32_e32 v68, v15, v19, vcc
	v_pk_fma_f32 v[16:17], v[68:69], 0, v[16:17] op_sel_hi:[1,0,1]
	v_pk_mul_f32 v[68:69], v[34:35], v[86:87] op_sel_hi:[1,0]
	v_pk_mul_f32 v[16:17], v[16:17], s[94:95] op_sel_hi:[1,0]
	v_pk_mul_f32 v[68:69], v[68:69], v[76:77]
	v_cvt_pk_bf16_f32 v17, v16, v17
	v_mov_b32_e32 v15, v68
	v_mov_b32_e32 v16, v68
	v_mov_b32_e32 v19, v69
	v_mov_b32_e32 v70, v69
	v_permlane32_swap_b32_e32 v15, v16
	s_nop 0
	v_permlane32_swap_b32_e32 v19, v70
	v_cndmask_b32_e32 v71, v19, v70, vcc
	v_cndmask_b32_e32 v70, v15, v16, vcc
	v_pk_fma_f32 v[68:69], v[70:71], 0, v[68:69] op_sel_hi:[1,0,1]
	v_and_b32_e32 v77, 0xffff0000, v14
	v_pk_mul_f32 v[68:69], v[68:69], s[94:95] op_sel_hi:[1,0]
	v_lshlrev_b32_e32 v76, 16, v14
	v_cvt_pk_bf16_f32 v16, v68, v69
	v_pk_mul_f32 v[68:69], v[40:41], v[86:87] op_sel_hi:[1,0]
; template <int DQK, int DV, bool LEAD> ...
;     ...
;           float sn = 0.f;
; #pragma unroll
;           for (int ds = 0; ds < 2; ++ds)
; #pragma unroll
;               for (int j = 0; j < 8; ++j) sn += x[ds][j] * x[ds][j];
;           sn = lanes4_sum(sn);
;           const float rn = rsqrtf(sn * (1.f / 64.f) + EPS);
; #pragma unroll
;           for (int ds = 0; ds < 2; ++ds)
; #pragma unroll
;               for (int j = 0; j < 8; ++j) x[ds][j] *= rn * qgain[32 * ds + 8 * g4 + j];
;           if constexpr (DQK == 64) {
; #pragma unroll
;               for (int ds = 0; ds < 2; ++ds)
; #pragma unroll
;                   for (int j = 0; j < 8; ++j) {
;                       auto rr = __builtin_amdgcn_permlane32_swap(__float_as_uint(x[ds][j]), __float_as_uint(x[ds][j]), false, false);
;                       const float other = hi ? __uint_as_float(rr[0]) : __uint_as_float(rr[1]);
;                       float cc = 1.f, sg = 0.f;
;                       if (lat) { const f32x2 cs = rope[(ds ? pcol : prow) * 16 + 8 * (g4 & 1) + j]; cc = cs.x; sg = hi ? cs.y : -cs.y; }
;                       x[ds][j] = x[ds][j] * cc + other * sg; }
;           } else {
;               float sr = 0.f;
; #pragma unroll
;               for (int j = 0; j < 8; ++j) sr += x[2][j] * x[2][j];
;               sr = lanes4_sum(sr);
;               const float rq = rsqrtf(sr * (1.f / 32.f) + EPS);
; #pragma unroll
;               for (int j = 0; j < 8; ++j) { const float av = x[2][j] * rq * qgain[64 + 8 * g4 + j];
;                   auto rr = __builtin_amdgcn_permlane16_swap(__float_as_uint(av), __float_as_uint(av), false, false);
;                   const float other = (g4 & 1) ? __uint_as_float(rr[0]) : __uint_as_float(rr[1]);
;                   float cc = 1.f, sg = 0.f;
;                   if (lat) { const f32x2 cs = rope[((g4 & 2) ? pcol : prow) * 8 + j]; cc = cs.x; sg = (g4 & 1) ? cs.y : -cs.y; }
;                   x[2][j] = av * cc + other * sg; }
;           }
; #pragma unroll
;           for (int ds = 0; ds < NDS; ++ds) { u32x4 w;
; #pragma unroll
;               for (int i = 0; i < 4; ++i) w[i] = cvtpk(x[ds][2 * i] * c2, x[ds][2 * i + 1] * c2);
;               qf[qb * NDS + ds] = __builtin_bit_cast(bf16x8, w); }
	v_mul_f32_e32 v14, v77, v77
	v_pk_mul_f32 v[68:69], v[68:69], v[78:79]
	s_nop 0
	v_mov_b32_e32 v15, v68
	v_mov_b32_e32 v19, v68
	v_mov_b32_e32 v70, v69
	v_mov_b32_e32 v71, v69
	v_permlane32_swap_b32_e32 v15, v19
	s_nop 0
	v_permlane32_swap_b32_e32 v70, v71
	v_cndmask_b32_e32 v71, v70, v71, vcc
	v_cndmask_b32_e32 v70, v15, v19, vcc
	v_pk_fma_f32 v[68:69], v[70:71], 0, v[68:69] op_sel_hi:[1,0,1]
	s_nop 0
	v_pk_mul_f32 v[68:69], v[68:69], s[94:95] op_sel_hi:[1,0]
	s_nop 0
	v_cvt_pk_bf16_f32 v15, v68, v69
	v_pk_mul_f32 v[68:69], v[38:39], v[86:87] op_sel_hi:[1,0]
	v_pk_fma_f32 v[78:79], v[76:77], v[76:77], v[14:15] op_sel_hi:[1,1,0]
	v_pk_mul_f32 v[68:69], v[68:69], v[80:81]
	v_pk_fma_f32 v[78:79], v[66:67], v[66:67], v[78:79]
	v_mov_b32_e32 v71, v69
	v_mov_b32_e32 v72, v69
	v_mov_b32_e32 v19, v68
	v_mov_b32_e32 v70, v68
	v_permlane32_swap_b32_e32 v71, v72
	s_nop 0
	v_permlane32_swap_b32_e32 v19, v70
	v_cndmask_b32_e32 v71, v71, v72, vcc
	v_lshlrev_b32_e32 v72, 16, v18
	v_mul_f32_e32 v18, v73, v73
	v_cndmask_b32_e32 v70, v19, v70, vcc
	v_pk_fma_f32 v[18:19], v[72:73], v[72:73], v[18:19] op_sel_hi:[1,1,0]
	v_mul_f32_e32 v14, v67, v67
	v_pk_fma_f32 v[18:19], v[64:65], v[64:65], v[18:19]
	v_pk_add_f32 v[78:79], v[14:15], v[78:79] op_sel_hi:[0,1]
	v_pk_add_f32 v[18:19], v[74:75], v[18:19] op_sel_hi:[0,1]
	v_pk_fma_f32 v[18:19], v[62:63], v[62:63], v[18:19]
	v_mul_f32_e32 v74, v63, v63
	v_pk_fma_f32 v[78:79], v[54:55], v[54:55], v[78:79]
	v_mul_f32_e32 v14, v55, v55
	v_pk_add_f32 v[18:19], v[74:75], v[18:19] op_sel_hi:[0,1]
	v_pk_add_f32 v[78:79], v[14:15], v[78:79] op_sel_hi:[0,1]
	v_pk_fma_f32 v[18:19], v[60:61], v[60:61], v[18:19]
	v_mul_f32_e32 v74, v61, v61
	v_pk_fma_f32 v[78:79], v[52:53], v[52:53], v[78:79]
	v_mul_f32_e32 v14, v53, v53
	v_pk_add_f32 v[18:19], v[74:75], v[18:19] op_sel_hi:[0,1]
	v_pk_add_f32 v[78:79], v[14:15], v[78:79] op_sel_hi:[0,1]
	v_pk_fma_f32 v[18:19], v[58:59], v[58:59], v[18:19]
	v_mul_f32_e32 v74, v59, v59
	v_pk_fma_f32 v[78:79], v[50:51], v[50:51], v[78:79]
	v_mul_f32_e32 v14, v51, v51
	v_pk_add_f32 v[18:19], v[74:75], v[18:19] op_sel_hi:[0,1]
	v_pk_add_f32 v[78:79], v[14:15], v[78:79] op_sel_hi:[0,1]
	v_pk_fma_f32 v[18:19], v[56:57], v[56:57], v[18:19]
	v_mul_f32_e32 v74, v57, v57
	v_pk_fma_f32 v[78:79], v[48:49], v[48:49], v[78:79]
	v_mul_f32_e32 v14, v49, v49
	v_pk_add_f32 v[18:19], v[74:75], v[18:19] op_sel_hi:[0,1]
	v_pk_add_f32 v[78:79], v[14:15], v[78:79] op_sel_hi:[0,1]
	v_pk_fma_f32 v[18:19], v[24:25], v[24:25], v[18:19]
	v_mul_f32_e32 v74, v25, v25
	v_pk_fma_f32 v[78:79], v[46:47], v[46:47], v[78:79]
	v_mul_f32_e32 v14, v47, v47
	v_pk_add_f32 v[18:19], v[74:75], v[18:19] op_sel_hi:[0,1]
	v_pk_add_f32 v[78:79], v[14:15], v[78:79] op_sel_hi:[0,1]
	v_pk_fma_f32 v[18:19], v[22:23], v[22:23], v[18:19]
	v_mul_f32_e32 v74, v23, v23
	v_pk_fma_f32 v[78:79], v[44:45], v[44:45], v[78:79]
	v_mul_f32_e32 v14, v45, v45
	v_pk_add_f32 v[18:19], v[74:75], v[18:19] op_sel_hi:[0,1]
	v_pk_add_f32 v[78:79], v[14:15], v[78:79] op_sel_hi:[0,1]
	v_mov_b32_e32 v19, v18
	v_mov_b32_e32 v14, v78
	s_nop 0
	v_permlane16_swap_b32_e32 v18, v19
	v_permlane16_swap_b32_e32 v78, v14
	v_add_f32_e32 v19, v18, v19
	v_add_f32_e32 v18, v78, v14
	v_mov_b32_e32 v75, v19
	v_mov_b32_e32 v74, v18
	s_nop 0
	v_permlane32_swap_b32_e32 v19, v75
	v_permlane32_swap_b32_e32 v18, v74
	v_pk_add_f32 v[18:19], v[18:19], v[74:75]
	s_nop 0
	v_pk_fma_f32 v[74:75], v[18:19], s[8:9], v[20:21] op_sel_hi:[1,0,0]
	v_pk_fma_f32 v[18:19], v[70:71], 0, v[68:69] op_sel_hi:[1,0,1]
	v_mul_f32_e32 v14, 0x4b800000, v75
	v_cmp_gt_f32_e64 s[4:5], s95, v75
	v_pk_mul_f32 v[18:19], v[18:19], s[94:95] op_sel_hi:[1,0]
	s_lshl_b32 s8, s30, 8
	v_cndmask_b32_e64 v14, v75, v14, s[4:5]
	v_rsq_f32_e32 v20, v14
	v_cvt_pk_bf16_f32 v14, v18, v19
	v_mul_f32_e32 v18, 0x45800000, v20
	v_cndmask_b32_e64 v68, v20, v18, s[4:5]
	v_pk_mul_f32 v[18:19], v[28:29], v[68:69] op_sel_hi:[1,0]
	v_cmp_gt_f32_e64 s[4:5], s95, v74
	v_pk_mul_f32 v[18:19], v[18:19], v[22:23]
	s_cmpk_lt_u32 s16, 0x100
	v_mov_b32_e32 v20, v18
	v_mov_b32_e32 v22, v18
	v_mov_b32_e32 v21, v19
	v_mov_b32_e32 v23, v19
	v_permlane32_swap_b32_e32 v20, v22
	s_nop 0
	v_permlane32_swap_b32_e32 v21, v23
	v_cndmask_b32_e32 v21, v21, v23, vcc
	v_cndmask_b32_e32 v20, v20, v22, vcc
	v_pk_fma_f32 v[18:19], v[20:21], 0, v[18:19] op_sel_hi:[1,0,1]
	s_mov_b32 s9, 1
	v_pk_mul_f32 v[18:19], v[18:19], s[94:95] op_sel_hi:[1,0]
	s_nop 0
	v_cvt_pk_bf16_f32 v21, v18, v19
	v_pk_mul_f32 v[18:19], v[26:27], v[68:69] op_sel_hi:[1,0]
	s_nop 0
	v_pk_mul_f32 v[18:19], v[18:19], v[24:25]
	s_nop 0
	v_mov_b32_e32 v20, v18
	v_mov_b32_e32 v22, v18
	v_mov_b32_e32 v23, v19
	v_mov_b32_e32 v24, v19
	v_permlane32_swap_b32_e32 v20, v22
	s_nop 0
	v_permlane32_swap_b32_e32 v23, v24
	v_cndmask_b32_e32 v23, v23, v24, vcc
	v_cndmask_b32_e32 v22, v20, v22, vcc
	v_pk_fma_f32 v[18:19], v[22:23], 0, v[18:19] op_sel_hi:[1,0,1]
	s_nop 0
	v_pk_mul_f32 v[18:19], v[18:19], s[94:95] op_sel_hi:[1,0]
	s_nop 0
	v_cvt_pk_bf16_f32 v20, v18, v19
	v_pk_mul_f32 v[18:19], v[32:33], v[68:69] op_sel_hi:[1,0]
	s_nop 0
	v_pk_mul_f32 v[18:19], v[18:19], v[56:57]
	s_nop 0
	v_mov_b32_e32 v22, v18
	v_mov_b32_e32 v24, v18
	v_mov_b32_e32 v23, v19
	v_mov_b32_e32 v25, v19
	v_permlane32_swap_b32_e32 v22, v24
	s_nop 0
	v_permlane32_swap_b32_e32 v23, v25
	v_cndmask_b32_e32 v23, v23, v25, vcc
	v_cndmask_b32_e32 v22, v22, v24, vcc
	v_pk_fma_f32 v[18:19], v[22:23], 0, v[18:19] op_sel_hi:[1,0,1]
	v_pk_mul_f32 v[22:23], v[30:31], v[68:69] op_sel_hi:[1,0]
	v_pk_mul_f32 v[18:19], v[18:19], s[94:95] op_sel_hi:[1,0]
	v_pk_mul_f32 v[22:23], v[22:23], v[58:59]
	v_cvt_pk_bf16_f32 v19, v18, v19
	v_mov_b32_e32 v18, v22
; __device__ __forceinline__ unsigned cvtpk(float lo, float hi) { f32x2 v = {lo, hi}; bf16x2_t b = __builtin_convertvector(v, bf16x2_t); return __builtin_bit_cast(unsigned, b); }
; template <int DQK, int DV, bool LEAD> ...
;     ...
;           const float rn = rsqrtf(sn * (1.f / 64.f) + EPS);
; #pragma unroll
;           for (int ds = 0; ds < 2; ++ds)
; #pragma unroll
;               for (int j = 0; j < 8; ++j) x[ds][j] *= rn * qgain[32 * ds + 8 * g4 + j];
;           if constexpr (DQK == 64) {
; #pragma unroll
;               for (int ds = 0; ds < 2; ++ds)
; #pragma unroll
;                   for (int j = 0; j < 8; ++j) {
;                       auto rr = __builtin_amdgcn_permlane32_swap(__float_as_uint(x[ds][j]), __float_as_uint(x[ds][j]), false, false);
;                       const float other = hi ? __uint_as_float(rr[0]) : __uint_as_float(rr[1]);
;                       float cc = 1.f, sg = 0.f;
;                       if (lat) { const f32x2 cs = rope[(ds ? pcol : prow) * 16 + 8 * (g4 & 1) + j]; cc = cs.x; sg = hi ? cs.y : -cs.y; }
;                       x[ds][j] = x[ds][j] * cc + other * sg; }
;           } else {
;               float sr = 0.f;
; #pragma unroll
;               for (int j = 0; j < 8; ++j) sr += x[2][j] * x[2][j];
;               sr = lanes4_sum(sr);
;               const float rq = rsqrtf(sr * (1.f / 32.f) + EPS);
; #pragma unroll
;               for (int j = 0; j < 8; ++j) { const float av = x[2][j] * rq * qgain[64 + 8 * g4 + j];
;                   auto rr = __builtin_amdgcn_permlane16_swap(__float_as_uint(av), __float_as_uint(av), false, false);
;                   const float other = (g4 & 1) ? __uint_as_float(rr[0]) : __uint_as_float(rr[1]);
;                   float cc = 1.f, sg = 0.f;
;                   if (lat) { const f32x2 cs = rope[((g4 & 2) ? pcol : prow) * 8 + j]; cc = cs.x; sg = (g4 & 1) ? cs.y : -cs.y; }
;                   x[2][j] = av * cc + other * sg; }
;           }
; #pragma unroll
;           for (int ds = 0; ds < NDS; ++ds) { u32x4 w;
; #pragma unroll
;               for (int i = 0; i < 4; ++i) w[i] = cvtpk(x[ds][2 * i] * c2, x[ds][2 * i + 1] * c2);
;               qf[qb * NDS + ds] = __builtin_bit_cast(bf16x8, w); }
;       }
; #pragma unroll
;       for (int d0 = 0; d0 < NQB * NDS; ++d0) asm volatile("" : "+v"(qf[d0])); }
;     wait_bar<0>();
	v_mov_b32_e32 v24, v22
	v_mov_b32_e32 v25, v23
	v_mov_b32_e32 v56, v23
	v_permlane32_swap_b32_e32 v18, v24
	s_nop 0
	v_permlane32_swap_b32_e32 v25, v56
	v_cndmask_b32_e32 v25, v25, v56, vcc
	v_cndmask_b32_e32 v24, v18, v24, vcc
	v_pk_fma_f32 v[22:23], v[24:25], 0, v[22:23] op_sel_hi:[1,0,1]
	s_nop 0
	v_pk_mul_f32 v[22:23], v[22:23], s[94:95] op_sel_hi:[1,0]
	s_nop 0
	v_cvt_pk_bf16_f32 v18, v22, v23
	v_pk_mul_f32 v[22:23], v[36:37], v[68:69] op_sel_hi:[1,0]
	s_nop 0
	v_pk_mul_f32 v[22:23], v[22:23], v[60:61]
	s_nop 0
	v_mov_b32_e32 v24, v22
	v_mov_b32_e32 v56, v22
	v_mov_b32_e32 v25, v23
	v_mov_b32_e32 v57, v23
	v_permlane32_swap_b32_e32 v24, v56
	s_nop 0
	v_permlane32_swap_b32_e32 v25, v57
	v_cndmask_b32_e32 v25, v25, v57, vcc
	v_cndmask_b32_e32 v24, v24, v56, vcc
	v_pk_fma_f32 v[22:23], v[24:25], 0, v[22:23] op_sel_hi:[1,0,1]
	s_nop 0
	v_pk_mul_f32 v[22:23], v[22:23], s[94:95] op_sel_hi:[1,0]
	s_nop 0
	v_cvt_pk_bf16_f32 v25, v22, v23
	v_pk_mul_f32 v[22:23], v[34:35], v[68:69] op_sel_hi:[1,0]
	s_nop 0
	v_pk_mul_f32 v[22:23], v[22:23], v[62:63]
	s_nop 0
	v_mov_b32_e32 v24, v22
	v_mov_b32_e32 v56, v22
	v_mov_b32_e32 v57, v23
	v_mov_b32_e32 v58, v23
	v_permlane32_swap_b32_e32 v24, v56
	s_nop 0
	v_permlane32_swap_b32_e32 v57, v58
	v_cndmask_b32_e32 v57, v57, v58, vcc
	v_cndmask_b32_e32 v56, v24, v56, vcc
	v_pk_fma_f32 v[22:23], v[56:57], 0, v[22:23] op_sel_hi:[1,0,1]
	s_nop 0
	v_pk_mul_f32 v[22:23], v[22:23], s[94:95] op_sel_hi:[1,0]
	s_nop 0
	v_cvt_pk_bf16_f32 v24, v22, v23
	v_pk_mul_f32 v[22:23], v[40:41], v[68:69] op_sel_hi:[1,0]
	s_nop 0
	v_pk_mul_f32 v[22:23], v[22:23], v[64:65]
	s_nop 0
	v_mov_b32_e32 v56, v22
	v_mov_b32_e32 v58, v22
	v_mov_b32_e32 v57, v23
	v_mov_b32_e32 v59, v23
	v_permlane32_swap_b32_e32 v56, v58
	s_nop 0
	v_permlane32_swap_b32_e32 v57, v59
	v_cndmask_b32_e32 v57, v57, v59, vcc
	v_cndmask_b32_e32 v56, v56, v58, vcc
	v_pk_fma_f32 v[22:23], v[56:57], 0, v[22:23] op_sel_hi:[1,0,1]
	v_pk_mul_f32 v[56:57], v[38:39], v[68:69] op_sel_hi:[1,0]
	v_pk_mul_f32 v[22:23], v[22:23], s[94:95] op_sel_hi:[1,0]
	v_pk_mul_f32 v[56:57], v[56:57], v[72:73]
	v_cvt_pk_bf16_f32 v23, v22, v23
	v_mov_b32_e32 v22, v56
	v_mov_b32_e32 v58, v56
	s_nop 1
	v_permlane32_swap_b32_e32 v22, v58
	v_mov_b32_e32 v59, v57
	v_mov_b32_e32 v60, v57
	v_cndmask_b32_e32 v58, v22, v58, vcc
	v_mul_f32_e32 v22, 0x4b800000, v74
	v_permlane32_swap_b32_e32 v59, v60
	v_cndmask_b32_e64 v22, v74, v22, s[4:5]
	v_cndmask_b32_e32 v59, v59, v60, vcc
	v_rsq_f32_e32 v60, v22
	v_pk_fma_f32 v[56:57], v[58:59], 0, v[56:57] op_sel_hi:[1,0,1]
	s_nop 0
	v_pk_mul_f32 v[56:57], v[56:57], s[94:95] op_sel_hi:[1,0]
	s_nop 0
	v_cvt_pk_bf16_f32 v22, v56, v57
	v_mul_f32_e32 v56, 0x45800000, v60
	v_cndmask_b32_e64 v56, v60, v56, s[4:5]
	v_pk_mul_f32 v[38:39], v[38:39], v[56:57] op_sel_hi:[1,0]
	v_pk_mul_f32 v[26:27], v[26:27], v[56:57] op_sel_hi:[1,0]
	v_pk_mul_f32 v[38:39], v[38:39], v[76:77]
	v_pk_mul_f32 v[28:29], v[28:29], v[56:57] op_sel_hi:[1,0]
	v_pk_mul_f32 v[26:27], v[26:27], v[46:47]
	v_pk_mul_f32 v[28:29], v[28:29], v[44:45]
	v_mov_b32_e32 v44, v38
	v_mov_b32_e32 v46, v38
	v_mov_b32_e32 v45, v39
	v_mov_b32_e32 v47, v39
	v_pk_mul_f32 v[40:41], v[40:41], v[56:57] op_sel_hi:[1,0]
	v_permlane32_swap_b32_e32 v44, v46
	v_permlane32_swap_b32_e32 v45, v47
	v_pk_mul_f32 v[40:41], v[40:41], v[66:67]
	v_cndmask_b32_e32 v45, v45, v47, vcc
	v_cndmask_b32_e32 v44, v44, v46, vcc
	v_pk_fma_f32 v[38:39], v[44:45], 0, v[38:39] op_sel_hi:[1,0,1]
	v_mov_b32_e32 v44, v40
	v_mov_b32_e32 v46, v40
	v_mov_b32_e32 v45, v41
	v_mov_b32_e32 v47, v41
	v_pk_mul_f32 v[34:35], v[34:35], v[56:57] op_sel_hi:[1,0]
	v_permlane32_swap_b32_e32 v44, v46
	v_permlane32_swap_b32_e32 v45, v47
	v_pk_mul_f32 v[34:35], v[34:35], v[54:55]
	v_cndmask_b32_e32 v45, v45, v47, vcc
	v_cndmask_b32_e32 v44, v44, v46, vcc
	v_pk_fma_f32 v[40:41], v[44:45], 0, v[40:41] op_sel_hi:[1,0,1]
	v_mov_b32_e32 v44, v34
	v_mov_b32_e32 v46, v34
	v_mov_b32_e32 v45, v35
	v_mov_b32_e32 v47, v35
	v_pk_mul_f32 v[36:37], v[36:37], v[56:57] op_sel_hi:[1,0]
	v_permlane32_swap_b32_e32 v44, v46
	v_permlane32_swap_b32_e32 v45, v47
	v_pk_mul_f32 v[36:37], v[36:37], v[52:53]
	v_cndmask_b32_e32 v45, v45, v47, vcc
	v_cndmask_b32_e32 v44, v44, v46, vcc
	v_pk_fma_f32 v[34:35], v[44:45], 0, v[34:35] op_sel_hi:[1,0,1]
	v_mov_b32_e32 v44, v36
	v_mov_b32_e32 v46, v36
	v_mov_b32_e32 v45, v37
	v_mov_b32_e32 v47, v37
	v_pk_mul_f32 v[30:31], v[30:31], v[56:57] op_sel_hi:[1,0]
	v_permlane32_swap_b32_e32 v44, v46
	v_permlane32_swap_b32_e32 v45, v47
	v_pk_mul_f32 v[30:31], v[30:31], v[50:51]
	v_cndmask_b32_e32 v45, v45, v47, vcc
	v_cndmask_b32_e32 v44, v44, v46, vcc
	v_pk_fma_f32 v[36:37], v[44:45], 0, v[36:37] op_sel_hi:[1,0,1]
	v_mov_b32_e32 v44, v30
	v_mov_b32_e32 v46, v30
	v_mov_b32_e32 v45, v31
	v_mov_b32_e32 v47, v31
	v_pk_mul_f32 v[32:33], v[32:33], v[56:57] op_sel_hi:[1,0]
	v_permlane32_swap_b32_e32 v44, v46
	v_permlane32_swap_b32_e32 v45, v47
	v_pk_mul_f32 v[32:33], v[32:33], v[48:49]
	v_cndmask_b32_e32 v45, v45, v47, vcc
	v_cndmask_b32_e32 v44, v44, v46, vcc
	v_pk_fma_f32 v[30:31], v[44:45], 0, v[30:31] op_sel_hi:[1,0,1]
	v_mov_b32_e32 v44, v32
	v_mov_b32_e32 v46, v32
	v_mov_b32_e32 v45, v33
	v_mov_b32_e32 v47, v33
	v_permlane32_swap_b32_e32 v44, v46
	s_nop 0
	v_permlane32_swap_b32_e32 v45, v47
	v_cndmask_b32_e32 v45, v45, v47, vcc
	v_cndmask_b32_e32 v44, v44, v46, vcc
	v_pk_fma_f32 v[32:33], v[44:45], 0, v[32:33] op_sel_hi:[1,0,1]
	v_mov_b32_e32 v44, v26
	v_mov_b32_e32 v46, v26
	v_mov_b32_e32 v45, v27
	v_mov_b32_e32 v47, v27
	v_permlane32_swap_b32_e32 v44, v46
	s_nop 0
	v_permlane32_swap_b32_e32 v45, v47
	v_cndmask_b32_e32 v45, v45, v47, vcc
	v_cndmask_b32_e32 v44, v44, v46, vcc
	v_pk_fma_f32 v[44:45], v[44:45], 0, v[26:27] op_sel_hi:[1,0,1]
	v_mov_b32_e32 v26, v28
	v_mov_b32_e32 v46, v28
	v_mov_b32_e32 v27, v29
	v_mov_b32_e32 v47, v29
	v_permlane32_swap_b32_e32 v26, v46
	s_nop 0
	v_permlane32_swap_b32_e32 v27, v47
	v_cndmask_b32_e32 v27, v27, v47, vcc
	v_cndmask_b32_e32 v26, v26, v46, vcc
	v_pk_fma_f32 v[46:47], v[26:27], 0, v[28:29] op_sel_hi:[1,0,1]
	v_pk_mul_f32 v[26:27], v[38:39], s[94:95] op_sel_hi:[1,0]
	v_pk_mul_f32 v[28:29], v[40:41], s[94:95] op_sel_hi:[1,0]
	v_cvt_pk_bf16_f32 v26, v26, v27
	v_cvt_pk_bf16_f32 v27, v28, v29
	v_pk_mul_f32 v[28:29], v[34:35], s[94:95] op_sel_hi:[1,0]
	v_pk_mul_f32 v[34:35], v[36:37], s[94:95] op_sel_hi:[1,0]
	v_pk_mul_f32 v[30:31], v[30:31], s[94:95] op_sel_hi:[1,0]
	v_pk_mul_f32 v[32:33], v[32:33], s[94:95] op_sel_hi:[1,0]
	v_cvt_pk_bf16_f32 v28, v28, v29
	v_cvt_pk_bf16_f32 v29, v34, v35
	v_cvt_pk_bf16_f32 v30, v30, v31
	v_cvt_pk_bf16_f32 v31, v32, v33
	v_pk_mul_f32 v[32:33], v[44:45], s[94:95] op_sel_hi:[1,0]
	v_pk_mul_f32 v[34:35], v[46:47], s[94:95] op_sel_hi:[1,0]
	v_cvt_pk_bf16_f32 v32, v32, v33
	v_cvt_pk_bf16_f32 v33, v34, v35
	s_waitcnt vmcnt(0) lgkmcnt(0)
	s_barrier
; #define ATT_SB() __builtin_amdgcn_sched_barrier(0)
; #define ATT_DMA_K(t, sl) do { glds16(ksrc + (size_t)(t) * 64 * kpitch, (unsigned)__builtin_amdgcn_readfirstlane(kdst + (sl) * KSLOT)); \
;         if constexpr (DQK == 96) glds16(krsrc + (size_t)(t) * 64 * 32, (unsigned)__builtin_amdgcn_readfirstlane(krdst + (sl) * KSLOT)); } while (0)
; #define ATT_DMA_V(t, sl) do { glds16(vsrc + (size_t)(t) * 64, (unsigned)__builtin_amdgcn_readfirstlane(vdst + (sl) * VSLOT)); \
;         if constexpr (DV == 128) glds16(vsrc + (size_t)64 * NR + (size_t)(t) * 64, (unsigned)__builtin_amdgcn_readfirstlane(vdst + (sl) * VSLOT + 8192)); } while (0)
; #define ATT_KLOAD(sl) do { _Pragma("unroll") for (int kb_ = 0; kb_ < NKW; ++kb_) _Pragma("unroll") for (int ds_ = 0; ds_ < NDS; ++ds_) { \
;         if (ds_ < 2) kf[kb_ * NDS + ds_] = *(const LAS bf16x8*)(kp[ds_ & 1] + (sl) * KSLOT + (kb_ & 1) * 512 + (kb_ >> 1) * 4096); \
;         else kf[kb_ * NDS + ds_] = *(const LAS bf16x8*)(krp + (sl) * KSLOT + (kb_ & 1) * 256 + (kb_ >> 1) * 2048); } } while (0)
; #define ATT_QK() do { _Pragma("unroll") for (int kb_ = 0; kb_ < NKW; ++kb_) _Pragma("unroll") for (int ds_ = 0; ds_ < NDS; ++ds_) _Pragma("unroll") for (int qb_ = 0; qb_ < NQB; ++qb_) \
;         c[kb_][qb_] = __builtin_amdgcn_mfma_f32_16x16x32_bf16(kf[kb_ * NDS + ds_], qf[qb_ * NDS + ds_], ds_ == 0 ? zero4 : c[kb_][qb_], 0, 0, 0); } while (0)
; template <int DQK, int DV, bool LEAD> ...
;     ...
;     bf16x8 kf[NKW * NDS], vf[NVF];
;     ATT_KLOAD(0);
;     asm volatile("s_waitcnt lgkmcnt(0)\n\ts_barrier" ::: "memory");
;     float lsum[NQB];
; #pragma unroll
;     for (int qb = 0; qb < NQB; ++qb) lsum[qb] = 0.f;
;     const f32x4 zero4 = {0.f, 0.f, 0.f, 0.f};
;     f32x4 o[NDB][NQB], c[NKW][NQB]; u32x4 pw[4];
; #pragma unroll
;     for (int i = 0; i < NDB; ++i)
; #pragma unroll
;         for (int qb = 0; qb < NQB; ++qb) o[i][qb] = zero4;
;     ATT_DMA_K(3, 0); ATT_DMA_V(1, 1);
;     ATT_QK(); ATT_SB();
;     ATT_KLOAD(1); ATT_SB();
;     if constexpr (LEAD) { ATT_EXP(); ATT_SUMPACK(); }
;     wait_bar<NDMA>();
;     int s_prev = 0, s_cur = 1, s_next = 2;
;     int one_ = 1; asm volatile("" : "+s"(one_));
	ds_read_b128 v[34:37], v174
	ds_read_b128 v[38:41], v174 offset:512
	v_bfe_u32 v56, v84, 1, 3
	v_bitop3_b32 v56, v171, v56, 4 bitop3:0x36
	v_lshlrev_b32_e32 v80, 4, v56
	v_add_u32_e32 v177, v85, v80
	s_waitcnt lgkmcnt(1)
	v_mfma_f32_16x16x32_bf16 v[44:47], v[34:37], v[6:9], 0
	ds_read_b128 v[56:59], v177
	ds_read_b128 v[60:63], v177 offset:512
	s_waitcnt lgkmcnt(0)
	s_barrier
	s_mov_b32 s4, m0
	s_mov_b32 m0, s31
	s_nop 0
	global_load_lds_dwordx4 v[168:169], off
	s_mov_b32 m0, s4
	v_mfma_f32_16x16x32_bf16 v[48:51], v[34:37], v[14:17], 0
	s_cselect_b64 vcc, -1, 0
	s_add_i32 s4, s19, 0x2000
	v_mfma_f32_16x16x32_bf16 v[52:55], v[34:37], v[22:25], 0
	v_mfma_f32_16x16x32_bf16 v[34:37], v[34:37], v[26:29], 0
	s_waitcnt lgkmcnt(1)
	v_mfma_f32_16x16x32_bf16 v[64:67], v[56:59], v[2:5], v[44:47]
	v_mfma_f32_16x16x32_bf16 v[68:71], v[56:59], v[10:13], v[48:51]
	v_mfma_f32_16x16x32_bf16 v[50:53], v[56:59], v[18:21], v[52:55]
	v_mfma_f32_16x16x32_bf16 v[54:57], v[56:59], v[30:33], v[34:37]
	v_mfma_f32_16x16x32_bf16 v[34:37], v[38:41], v[6:9], 0
	v_mfma_f32_16x16x32_bf16 v[44:47], v[38:41], v[14:17], 0
	v_mfma_f32_16x16x32_bf16 v[72:75], v[38:41], v[22:25], 0
	v_mfma_f32_16x16x32_bf16 v[38:41], v[38:41], v[26:29], 0
	s_waitcnt lgkmcnt(0)
	v_mfma_f32_16x16x32_bf16 v[76:79], v[60:63], v[2:5], v[34:37]
	v_mfma_f32_16x16x32_bf16 v[84:87], v[60:63], v[10:13], v[44:47]
	s_nop 1
	v_lshl_add_u64 v[34:35], v[162:163], 0, s[66:67]
	s_mov_b32 s5, m0
	s_mov_b32 m0, s4
	s_nop 0
	global_load_lds_dwordx4 v[34:35], off
	s_mov_b32 m0, s5
	v_mfma_f32_16x16x32_bf16 v[72:75], v[60:63], v[18:21], v[72:75]
	v_mfma_f32_16x16x32_bf16 v[58:61], v[60:63], v[30:33], v[38:41]
	ds_read_b128 v[34:37], v174 offset:8192
	s_nop 1
	ds_read_b128 v[38:41], v174 offset:8704
	ds_read_b128 v[42:45], v177 offset:8192
	ds_read_b128 v[46:49], v177 offset:8704
	v_exp_f32_e32 v62, v64
	v_exp_f32_e32 v63, v65
	v_exp_f32_e32 v64, v66
	v_exp_f32_e32 v65, v67
	v_exp_f32_e32 v66, v68
	v_exp_f32_e32 v67, v69
	v_exp_f32_e32 v68, v70
	v_exp_f32_e32 v69, v71
	v_exp_f32_e32 v70, v50
	v_exp_f32_e32 v71, v51
	v_exp_f32_e32 v81, v52
	v_exp_f32_e32 v83, v53
	v_exp_f32_e32 v54, v54
	v_exp_f32_e32 v55, v55
	v_exp_f32_e32 v56, v56
	v_exp_f32_e32 v57, v57
	v_add_f32_e32 v50, v62, v63
	v_add_f32_e32 v51, v64, v65
	v_exp_f32_e32 v76, v76
	v_exp_f32_e32 v84, v84
	v_exp_f32_e32 v72, v72
	v_exp_f32_e32 v58, v58
	v_add_f32_e32 v50, v50, v51
	v_add_f32_e32 v51, v66, v67
	v_add_f32_e32 v52, v68, v69
	v_add_f32_e32 v51, v51, v52
	v_add_f32_e32 v52, v70, v71
	v_add_f32_e32 v53, v81, v83
	v_exp_f32_e32 v77, v77
	v_exp_f32_e32 v85, v85
	v_exp_f32_e32 v73, v73
	v_exp_f32_e32 v59, v59
	v_add_f32_e32 v52, v52, v53
	v_add_f32_e32 v53, v54, v55
	v_add_f32_e32 v88, v56, v57
	v_add_f32_e32 v53, v53, v88
	v_exp_f32_e32 v78, v78
	v_exp_f32_e32 v86, v86
	v_exp_f32_e32 v74, v74
	v_exp_f32_e32 v60, v60
	v_add_f32_e32 v50, v50, v76
	v_add_f32_e32 v51, v51, v84
	v_add_f32_e32 v52, v52, v72
	v_add_f32_e32 v53, v53, v58
	v_exp_f32_e32 v79, v79
	v_exp_f32_e32 v87, v87
	v_exp_f32_e32 v75, v75
	v_exp_f32_e32 v61, v61
	v_add_f32_e32 v50, v77, v50
	v_add_f32_e32 v51, v85, v51
	v_add_f32_e32 v52, v73, v52
	v_add_f32_e32 v53, v59, v53
	s_mov_b32 s4, 1
	v_add_f32_e32 v50, v78, v50
	v_add_f32_e32 v88, v86, v51
	v_add_f32_e32 v52, v74, v52
	v_add_f32_e32 v89, v60, v53
	v_cvt_pk_bf16_f32 v102, v62, v63
	v_add_f32_e32 v51, v79, v50
	v_add_f32_e32 v50, v87, v88
	v_add_f32_e32 v53, v75, v52
	v_add_f32_e32 v52, v61, v89
	s_waitcnt vmcnt(2) lgkmcnt(0)
	s_barrier
	s_cmp_lg_u32 s4, 0
	v_pk_add_f32 v[166:167], v[50:51], 0 op_sel_hi:[1,0]
	v_cndmask_b32_e32 v50, v80, v82, vcc
	v_add3_u32 v178, 0, v176, v50
	v_mov_b32_e32 v50, 0
	v_pk_add_f32 v[164:165], v[52:53], 0 op_sel_hi:[1,0]
	v_cvt_pk_bf16_f32 v103, v64, v65
	v_cvt_pk_bf16_f32 v104, v76, v77
	v_cvt_pk_bf16_f32 v105, v78, v79
	v_cvt_pk_bf16_f32 v110, v66, v67
	v_cvt_pk_bf16_f32 v111, v68, v69
	v_cvt_pk_bf16_f32 v112, v84, v85
	v_cvt_pk_bf16_f32 v113, v86, v87
	v_cvt_pk_bf16_f32 v122, v70, v71
	v_cvt_pk_bf16_f32 v123, v81, v83
	v_cvt_pk_bf16_f32 v124, v72, v73
	v_cvt_pk_bf16_f32 v125, v74, v75
	v_cvt_pk_bf16_f32 v126, v54, v55
	v_cvt_pk_bf16_f32 v127, v56, v57
	v_cvt_pk_bf16_f32 v128, v58, v59
	v_cvt_pk_bf16_f32 v129, v60, v61
	s_cselect_b64 s[4:5], -1, 0
	s_mov_b32 s16, 2
	v_mov_b32_e32 v51, v50
	v_mov_b32_e32 v52, v50
	v_mov_b32_e32 v53, v50
	v_mov_b32_e32 v54, v50
	v_mov_b32_e32 v55, v50
	v_mov_b32_e32 v56, v50
	v_mov_b32_e32 v57, v50
	v_mov_b32_e32 v58, v50
	v_mov_b32_e32 v59, v50
	v_mov_b32_e32 v60, v50
	v_mov_b32_e32 v61, v50
	v_mov_b32_e32 v62, v50
	v_mov_b32_e32 v63, v50
	v_mov_b32_e32 v64, v50
	v_mov_b32_e32 v65, v50
	v_mov_b32_e32 v66, v50
	v_mov_b32_e32 v67, v50
	v_mov_b32_e32 v68, v50
	v_mov_b32_e32 v69, v50
	v_mov_b32_e32 v70, v50
	v_mov_b32_e32 v71, v50
	v_mov_b32_e32 v72, v50
	v_mov_b32_e32 v73, v50
	v_mov_b32_e32 v74, v50
	v_mov_b32_e32 v75, v50
	v_mov_b32_e32 v76, v50
	v_mov_b32_e32 v77, v50
	v_mov_b32_e32 v78, v50
	v_mov_b32_e32 v79, v50
	v_mov_b32_e32 v80, v50
	v_mov_b32_e32 v81, v50
	v_mov_b32_e32 v82, v50
	v_mov_b32_e32 v83, v50
	v_mov_b32_e32 v84, v50
	v_mov_b32_e32 v85, v50
	v_mov_b32_e32 v86, v50
	v_mov_b32_e32 v87, v50
	v_mov_b32_e32 v88, v50
	v_mov_b32_e32 v89, v50
	v_mov_b32_e32 v90, v50
	v_mov_b32_e32 v91, v50
	v_mov_b32_e32 v92, v50
	v_mov_b32_e32 v93, v50
	v_mov_b32_e32 v94, v50
	v_mov_b32_e32 v95, v50
	v_mov_b32_e32 v96, v50
	v_mov_b32_e32 v97, v50
	v_mov_b32_e32 v98, v50
	v_mov_b32_e32 v99, v50
	v_mov_b32_e32 v100, v50
	v_mov_b32_e32 v101, v50
	v_mov_b32_e32 v106, v50
	v_mov_b32_e32 v107, v50
	v_mov_b32_e32 v108, v50
	v_mov_b32_e32 v109, v50
	v_mov_b32_e32 v114, v50
	v_mov_b32_e32 v115, v50
	v_mov_b32_e32 v116, v50
	v_mov_b32_e32 v117, v50
	v_mov_b32_e32 v118, v50
	v_mov_b32_e32 v119, v50
	v_mov_b32_e32 v120, v50
	v_mov_b32_e32 v121, v50
	s_branch .LBB0_998
